# speedup vs baseline: 1.0093x; 1.0045x over previous
.LBB3_5:
	s_waitcnt lgkmcnt(0)
	v_cvt_f16_f32_e32 v180, s7
	v_cvt_f16_f32_e32 v182, s6
	v_cvt_f16_f32_e32 v181, s28
	s_waitcnt vmcnt(3)
	v_pk_mul_f16 v183, v182, v184 op_sel_hi:[0,1]
	v_pk_mul_f16 v190, v182, v187 op_sel_hi:[0,1]
	v_pk_mul_f16 v194, v180, v187 op_sel_hi:[0,1]
	v_pk_mul_f16 v198, v181, v187 op_sel_hi:[0,1]
	v_pk_mul_f16 v188, v182, v185 op_sel_hi:[0,1]
	v_pk_mul_f16 v189, v182, v186 op_sel_hi:[0,1]
	v_pk_mul_f16 v191, v180, v184 op_sel_hi:[0,1]
	s_mov_b64 exec, s[64:65]
	buffer_load_dwordx4 v[18:21], v249, s[16:19], 0 offen
	buffer_load_dwordx4 v[6:9], v249, s[16:19], 0 offen offset:512
	s_mov_b64 exec, -1
	v_pk_mul_f16 v192, v180, v185 op_sel_hi:[0,1]
	v_pk_mul_f16 v193, v180, v186 op_sel_hi:[0,1]
	v_pk_mul_f16 v195, v181, v184 op_sel_hi:[0,1]
	v_pk_mul_f16 v196, v181, v185 op_sel_hi:[0,1]
	v_pk_mul_f16 v197, v181, v186 op_sel_hi:[0,1]
	v_pk_fma_f16 v113, v113, v187, v190
	v_pk_fma_f16 v110, v110, v184, v183
	v_pk_fma_f16 v129, v129, v187, v190
	v_pk_fma_f16 v126, v126, v184, v183
	v_pk_fma_f16 v141, v141, v187, v190
	v_pk_fma_f16 v138, v138, v184, v183
	v_pk_fma_f16 v183, v89, v187, v194
	v_pk_fma_f16 v199, v109, v187, v194
	buffer_load_dwordx4 v[30:33], v250, s[16:19], 0 offen offset:512
	buffer_load_dwordx4 v[10:13], v250, s[16:19], 0 offen offset:1024
	v_pk_fma_f16 v194, v125, v187, v194
	v_pk_fma_f16 v203, v53, v187, v198
	v_pk_fma_f16 v207, v69, v187, v198
	v_pk_fma_f16 v187, v97, v187, v198
	v_pk_maximum3_f16 v198, v113, v129, v141
	v_pk_fma_f16 v112, v112, v186, v189
	v_pk_fma_f16 v111, v111, v185, v188
	v_pk_fma_f16 v128, v128, v186, v189
	v_pk_fma_f16 v127, v127, v185, v188
	v_pk_fma_f16 v140, v140, v186, v189
	v_pk_fma_f16 v139, v139, v185, v188
	v_pk_fma_f16 v188, v88, v186, v193
	v_pk_fma_f16 v189, v87, v185, v192
	v_pk_fma_f16 v190, v86, v184, v191
	v_pk_fma_f16 v200, v108, v186, v193
	v_pk_fma_f16 v201, v107, v185, v192
	s_mov_b64 exec, s[66:67]
	buffer_load_dwordx4 v[54:57], v250, s[16:19], 0 offen offset:2048
	buffer_load_dwordx4 v[14:17], v250, s[16:19], 0 offen offset:2560
	s_mov_b64 exec, -1
	v_pk_fma_f16 v202, v106, v184, v191
	v_pk_fma_f16 v193, v124, v186, v193
	v_pk_fma_f16 v192, v123, v185, v192
	v_pk_fma_f16 v191, v122, v184, v191
	v_pk_fma_f16 v204, v52, v186, v197
	v_pk_fma_f16 v205, v51, v185, v196
	v_pk_fma_f16 v206, v50, v184, v195
	v_pk_fma_f16 v208, v68, v186, v197
	v_pk_fma_f16 v209, v67, v185, v196
	v_pk_fma_f16 v210, v66, v184, v195
	v_pk_fma_f16 v186, v96, v186, v197
	v_pk_fma_f16 v185, v95, v185, v196
	v_pk_fma_f16 v184, v94, v184, v195
	v_pk_maximum3_f16 v195, v110, v126, v138
	v_pk_maximum3_f16 v196, v111, v127, v139
	v_pk_maximum3_f16 v197, v112, v128, v140
	v_pk_maximum3_f16 v214, v183, v199, v194
	v_pk_maximum3_f16 v218, v203, v207, v187
	v_pk_maximum3_f16 v211, v190, v202, v191
	v_pk_maximum3_f16 v212, v189, v201, v192
	v_pk_maximum3_f16 v213, v188, v200, v193
	v_pk_maximum3_f16 v215, v206, v210, v184
	v_pk_maximum3_f16 v216, v205, v209, v185
	v_pk_maximum3_f16 v198, v198, v214, v218
	v_pk_maximum3_f16 v217, v204, v208, v186
	v_pk_maximum3_f16 v195, v195, v211, v215
	v_pk_maximum3_f16 v196, v196, v212, v216
	v_pk_maximum3_f16 v197, v197, v213, v217
	v_pk_add_f16 v113, v113, v198 neg_lo:[0,1] neg_hi:[0,1]
	s_mov_b64 exec, s[64:65]
	buffer_load_dwordx4 v[74:77], v251, s[16:19], 0 offen
	buffer_load_dwordx4 v[26:29], v251, s[16:19], 0 offen offset:512
	s_mov_b64 exec, -1
	v_pk_add_f16 v110, v110, v195 neg_lo:[0,1] neg_hi:[0,1]
	v_pk_add_f16 v111, v111, v196 neg_lo:[0,1] neg_hi:[0,1]
	v_pk_add_f16 v112, v112, v197 neg_lo:[0,1] neg_hi:[0,1]
	v_pk_add_f16 v126, v126, v195 neg_lo:[0,1] neg_hi:[0,1]
	v_exp_f16_sdwa v211, v110 dst_sel:WORD_0 dst_unused:UNUSED_PAD src0_sel:WORD_0
	v_exp_f16_sdwa v212, v111 dst_sel:WORD_0 dst_unused:UNUSED_PAD src0_sel:WORD_0
	v_exp_f16_sdwa v213, v112 dst_sel:WORD_0 dst_unused:UNUSED_PAD src0_sel:WORD_0
	v_exp_f16_sdwa v214, v113 dst_sel:WORD_0 dst_unused:UNUSED_PAD src0_sel:WORD_0
	v_exp_f16_sdwa v211, v110 dst_sel:WORD_1 dst_unused:UNUSED_PRESERVE src0_sel:WORD_1
	v_exp_f16_sdwa v212, v111 dst_sel:WORD_1 dst_unused:UNUSED_PRESERVE src0_sel:WORD_1
	v_exp_f16_sdwa v213, v112 dst_sel:WORD_1 dst_unused:UNUSED_PRESERVE src0_sel:WORD_1
	v_exp_f16_sdwa v214, v113 dst_sel:WORD_1 dst_unused:UNUSED_PRESERVE src0_sel:WORD_1
	v_pk_add_f16 v127, v127, v196 neg_lo:[0,1] neg_hi:[0,1]
	v_pk_add_f16 v113, v211, 0
	v_pk_fma_f16 v81, v81, v214, 0
	v_pk_add_f16 v110, v214, 0
	v_pk_add_f16 v111, v213, 0
	v_pk_add_f16 v112, v212, 0
	v_pk_fma_f16 v80, v80, v213, 0
	v_pk_fma_f16 v79, v79, v212, 0
	v_pk_fma_f16 v78, v78, v211, 0
	v_pk_add_f16 v128, v128, v197 neg_lo:[0,1] neg_hi:[0,1]
	buffer_load_dwordx4 v[98:101], v252, s[16:19], 0 offen offset:512
	buffer_load_dwordx4 v[38:41], v252, s[16:19], 0 offen offset:1024
	v_pk_add_f16 v129, v129, v198 neg_lo:[0,1] neg_hi:[0,1]
	v_exp_f16_sdwa v211, v126 dst_sel:WORD_0 dst_unused:UNUSED_PAD src0_sel:WORD_0
	v_exp_f16_sdwa v212, v127 dst_sel:WORD_0 dst_unused:UNUSED_PAD src0_sel:WORD_0
	v_exp_f16_sdwa v213, v128 dst_sel:WORD_0 dst_unused:UNUSED_PAD src0_sel:WORD_0
	v_exp_f16_sdwa v214, v129 dst_sel:WORD_0 dst_unused:UNUSED_PAD src0_sel:WORD_0
	v_exp_f16_sdwa v211, v126 dst_sel:WORD_1 dst_unused:UNUSED_PRESERVE src0_sel:WORD_1
	v_exp_f16_sdwa v212, v127 dst_sel:WORD_1 dst_unused:UNUSED_PRESERVE src0_sel:WORD_1
	v_exp_f16_sdwa v213, v128 dst_sel:WORD_1 dst_unused:UNUSED_PRESERVE src0_sel:WORD_1
	v_exp_f16_sdwa v214, v129 dst_sel:WORD_1 dst_unused:UNUSED_PRESERVE src0_sel:WORD_1
	v_pk_add_f16 v113, v113, v211
	v_pk_fma_f16 v81, v105, v214, v81
	v_pk_add_f16 v105, v141, v198 neg_lo:[0,1] neg_hi:[0,1]
	v_pk_add_f16 v112, v112, v212
	v_pk_add_f16 v111, v111, v213
	v_pk_add_f16 v110, v110, v214
	v_pk_fma_f16 v78, v102, v211, v78
	v_pk_fma_f16 v79, v103, v212, v79
	v_pk_fma_f16 v80, v104, v213, v80
	v_pk_add_f16 v102, v138, v195 neg_lo:[0,1] neg_hi:[0,1]
	v_pk_add_f16 v103, v139, v196 neg_lo:[0,1] neg_hi:[0,1]
	v_pk_add_f16 v104, v140, v197 neg_lo:[0,1] neg_hi:[0,1]
	v_exp_f16_sdwa v126, v102 dst_sel:WORD_0 dst_unused:UNUSED_PAD src0_sel:WORD_0
	v_exp_f16_sdwa v127, v103 dst_sel:WORD_0 dst_unused:UNUSED_PAD src0_sel:WORD_0
	v_exp_f16_sdwa v128, v104 dst_sel:WORD_0 dst_unused:UNUSED_PAD src0_sel:WORD_0
	v_exp_f16_sdwa v129, v105 dst_sel:WORD_0 dst_unused:UNUSED_PAD src0_sel:WORD_0
	v_exp_f16_sdwa v126, v102 dst_sel:WORD_1 dst_unused:UNUSED_PRESERVE src0_sel:WORD_1
	v_exp_f16_sdwa v127, v103 dst_sel:WORD_1 dst_unused:UNUSED_PRESERVE src0_sel:WORD_1
	v_exp_f16_sdwa v128, v104 dst_sel:WORD_1 dst_unused:UNUSED_PRESERVE src0_sel:WORD_1
	v_exp_f16_sdwa v129, v105 dst_sel:WORD_1 dst_unused:UNUSED_PRESERVE src0_sel:WORD_1
	v_pk_add_f16 v105, v113, v126
	v_pk_add_f16 v102, v110, v129
	s_mov_b64 exec, s[66:67]
	buffer_load_dwordx4 v[114:117], v252, s[16:19], 0 offen offset:2048
	buffer_load_dwordx4 v[58:61], v252, s[16:19], 0 offen offset:2560
	s_mov_b64 exec, -1
	v_pk_add_f16 v103, v111, v128
	v_pk_add_f16 v104, v112, v127
	v_pk_fma_f16 v81, v121, v129, v81
	v_pk_fma_f16 v80, v120, v128, v80
	v_pk_fma_f16 v79, v119, v127, v79
	v_pk_fma_f16 v78, v118, v126, v78
	v_pk_add_f16 v110, v190, v195 neg_lo:[0,1] neg_hi:[0,1]
	v_pk_add_f16 v111, v189, v196 neg_lo:[0,1] neg_hi:[0,1]
	v_pk_add_f16 v112, v188, v197 neg_lo:[0,1] neg_hi:[0,1]
	v_pk_add_f16 v113, v183, v198 neg_lo:[0,1] neg_hi:[0,1]
	v_exp_f16_sdwa v118, v110 dst_sel:WORD_0 dst_unused:UNUSED_PAD src0_sel:WORD_0
	v_exp_f16_sdwa v119, v111 dst_sel:WORD_0 dst_unused:UNUSED_PAD src0_sel:WORD_0
	v_exp_f16_sdwa v120, v112 dst_sel:WORD_0 dst_unused:UNUSED_PAD src0_sel:WORD_0
	v_exp_f16_sdwa v121, v113 dst_sel:WORD_0 dst_unused:UNUSED_PAD src0_sel:WORD_0
	v_exp_f16_sdwa v118, v110 dst_sel:WORD_1 dst_unused:UNUSED_PRESERVE src0_sel:WORD_1
	v_exp_f16_sdwa v119, v111 dst_sel:WORD_1 dst_unused:UNUSED_PRESERVE src0_sel:WORD_1
	v_exp_f16_sdwa v120, v112 dst_sel:WORD_1 dst_unused:UNUSED_PRESERVE src0_sel:WORD_1
	v_exp_f16_sdwa v121, v113 dst_sel:WORD_1 dst_unused:UNUSED_PRESERVE src0_sel:WORD_1
	v_pk_add_f16 v110, v202, v195 neg_lo:[0,1] neg_hi:[0,1]
	v_pk_add_f16 v105, v105, v118
	v_pk_add_f16 v104, v104, v119
	v_pk_add_f16 v103, v103, v120
	s_mov_b64 exec, s[76:77]
	buffer_load_dwordx4 v[130:133], v253, s[16:19], 0 offen
	buffer_load_dwordx4 v[70:73], v253, s[16:19], 0 offen offset:512
	s_mov_b64 exec, -1
	v_pk_add_f16 v102, v102, v121
	v_pk_fma_f16 v78, v46, v118, v78
	v_pk_fma_f16 v79, v47, v119, v79
	v_pk_fma_f16 v80, v48, v120, v80
	v_pk_fma_f16 v81, v49, v121, v81
	v_pk_add_f16 v111, v201, v196 neg_lo:[0,1] neg_hi:[0,1]
	v_pk_add_f16 v112, v200, v197 neg_lo:[0,1] neg_hi:[0,1]
	v_pk_add_f16 v113, v199, v198 neg_lo:[0,1] neg_hi:[0,1]
	v_exp_f16_sdwa v118, v110 dst_sel:WORD_0 dst_unused:UNUSED_PAD src0_sel:WORD_0
	v_exp_f16_sdwa v119, v111 dst_sel:WORD_0 dst_unused:UNUSED_PAD src0_sel:WORD_0
	v_exp_f16_sdwa v120, v112 dst_sel:WORD_0 dst_unused:UNUSED_PAD src0_sel:WORD_0
	v_exp_f16_sdwa v121, v113 dst_sel:WORD_0 dst_unused:UNUSED_PAD src0_sel:WORD_0
	v_exp_f16_sdwa v118, v110 dst_sel:WORD_1 dst_unused:UNUSED_PRESERVE src0_sel:WORD_1
	v_exp_f16_sdwa v119, v111 dst_sel:WORD_1 dst_unused:UNUSED_PRESERVE src0_sel:WORD_1
	v_exp_f16_sdwa v120, v112 dst_sel:WORD_1 dst_unused:UNUSED_PRESERVE src0_sel:WORD_1
	v_exp_f16_sdwa v121, v113 dst_sel:WORD_1 dst_unused:UNUSED_PRESERVE src0_sel:WORD_1
	v_pk_add_f16 v110, v191, v195 neg_lo:[0,1] neg_hi:[0,1]
	v_pk_add_f16 v105, v105, v118
	v_pk_add_f16 v102, v102, v121
	v_pk_add_f16 v103, v103, v120
	v_pk_add_f16 v104, v104, v119
	v_pk_fma_f16 v81, v65, v121, v81
	v_pk_fma_f16 v80, v64, v120, v80
	s_mov_b64 exec, s[70:71]
	buffer_load_dwordx4 v[134:137], v254, s[16:19], 0 offen offset:512
	buffer_load_dwordx4 v[90:93], v254, s[16:19], 0 offen offset:1024
	s_mov_b64 exec, -1
	v_pk_fma_f16 v79, v63, v119, v79
	v_pk_fma_f16 v78, v62, v118, v78
	v_pk_add_f16 v111, v192, v196 neg_lo:[0,1] neg_hi:[0,1]
	v_pk_add_f16 v112, v193, v197 neg_lo:[0,1] neg_hi:[0,1]
	v_pk_add_f16 v113, v194, v198 neg_lo:[0,1] neg_hi:[0,1]
	v_exp_f16_sdwa v118, v110 dst_sel:WORD_0 dst_unused:UNUSED_PAD src0_sel:WORD_0
	v_exp_f16_sdwa v119, v111 dst_sel:WORD_0 dst_unused:UNUSED_PAD src0_sel:WORD_0
	v_exp_f16_sdwa v120, v112 dst_sel:WORD_0 dst_unused:UNUSED_PAD src0_sel:WORD_0
	v_exp_f16_sdwa v121, v113 dst_sel:WORD_0 dst_unused:UNUSED_PAD src0_sel:WORD_0
	v_exp_f16_sdwa v118, v110 dst_sel:WORD_1 dst_unused:UNUSED_PRESERVE src0_sel:WORD_1
	v_exp_f16_sdwa v119, v111 dst_sel:WORD_1 dst_unused:UNUSED_PRESERVE src0_sel:WORD_1
	v_exp_f16_sdwa v120, v112 dst_sel:WORD_1 dst_unused:UNUSED_PRESERVE src0_sel:WORD_1
	v_exp_f16_sdwa v121, v113 dst_sel:WORD_1 dst_unused:UNUSED_PRESERVE src0_sel:WORD_1
	v_pk_add_f16 v110, v206, v195 neg_lo:[0,1] neg_hi:[0,1]
	v_pk_add_f16 v105, v105, v118
	v_pk_add_f16 v104, v104, v119
	v_pk_add_f16 v103, v103, v120
	v_pk_add_f16 v102, v102, v121
	v_pk_fma_f16 v78, v82, v118, v78
	v_pk_fma_f16 v79, v83, v119, v79
	v_pk_fma_f16 v80, v84, v120, v80
	v_pk_fma_f16 v81, v85, v121, v81
	s_mov_b64 exec, s[78:79]
	buffer_load_dwordx4 v[142:145], v254, s[16:19], 0 offen offset:2048
	buffer_load_dwordx4 v[2:5], v254, s[16:19], 0 offen offset:2560
	s_mov_b64 exec, -1
	v_pk_add_f16 v111, v205, v196 neg_lo:[0,1] neg_hi:[0,1]
	v_pk_add_f16 v112, v204, v197 neg_lo:[0,1] neg_hi:[0,1]
	v_pk_add_f16 v113, v203, v198 neg_lo:[0,1] neg_hi:[0,1]
	v_exp_f16_sdwa v118, v110 dst_sel:WORD_0 dst_unused:UNUSED_PAD src0_sel:WORD_0
	v_exp_f16_sdwa v119, v111 dst_sel:WORD_0 dst_unused:UNUSED_PAD src0_sel:WORD_0
	v_exp_f16_sdwa v120, v112 dst_sel:WORD_0 dst_unused:UNUSED_PAD src0_sel:WORD_0
	v_exp_f16_sdwa v121, v113 dst_sel:WORD_0 dst_unused:UNUSED_PAD src0_sel:WORD_0
	v_exp_f16_sdwa v118, v110 dst_sel:WORD_1 dst_unused:UNUSED_PRESERVE src0_sel:WORD_1
	v_exp_f16_sdwa v119, v111 dst_sel:WORD_1 dst_unused:UNUSED_PRESERVE src0_sel:WORD_1
	v_exp_f16_sdwa v120, v112 dst_sel:WORD_1 dst_unused:UNUSED_PRESERVE src0_sel:WORD_1
	v_exp_f16_sdwa v121, v113 dst_sel:WORD_1 dst_unused:UNUSED_PRESERVE src0_sel:WORD_1
	v_pk_add_f16 v110, v210, v195 neg_lo:[0,1] neg_hi:[0,1]
	v_pk_add_f16 v105, v105, v118
	v_pk_add_f16 v102, v102, v121
	v_pk_add_f16 v103, v103, v120
	v_pk_add_f16 v104, v104, v119
	v_pk_fma_f16 v81, v25, v121, v81
	v_pk_fma_f16 v80, v24, v120, v80
	v_pk_fma_f16 v79, v23, v119, v79
	v_pk_fma_f16 v78, v22, v118, v78
	v_pk_add_f16 v111, v209, v196 neg_lo:[0,1] neg_hi:[0,1]
	v_pk_add_f16 v112, v208, v197 neg_lo:[0,1] neg_hi:[0,1]
	v_pk_add_f16 v113, v207, v198 neg_lo:[0,1] neg_hi:[0,1]
	v_exp_f16_sdwa v118, v110 dst_sel:WORD_0 dst_unused:UNUSED_PAD src0_sel:WORD_0
	v_exp_f16_sdwa v119, v111 dst_sel:WORD_0 dst_unused:UNUSED_PAD src0_sel:WORD_0
	v_exp_f16_sdwa v120, v112 dst_sel:WORD_0 dst_unused:UNUSED_PAD src0_sel:WORD_0
	v_exp_f16_sdwa v121, v113 dst_sel:WORD_0 dst_unused:UNUSED_PAD src0_sel:WORD_0
	v_exp_f16_sdwa v118, v110 dst_sel:WORD_1 dst_unused:UNUSED_PRESERVE src0_sel:WORD_1
	v_exp_f16_sdwa v119, v111 dst_sel:WORD_1 dst_unused:UNUSED_PRESERVE src0_sel:WORD_1
	v_exp_f16_sdwa v120, v112 dst_sel:WORD_1 dst_unused:UNUSED_PRESERVE src0_sel:WORD_1
	v_exp_f16_sdwa v121, v113 dst_sel:WORD_1 dst_unused:UNUSED_PRESERVE src0_sel:WORD_1
	v_pk_add_f16 v110, v184, v195 neg_lo:[0,1] neg_hi:[0,1]
	v_pk_add_f16 v105, v105, v118
	v_pk_add_f16 v104, v104, v119
	v_pk_add_f16 v103, v103, v120
	v_pk_add_f16 v102, v102, v121
	v_pk_fma_f16 v78, v34, v118, v78
	v_pk_fma_f16 v79, v35, v119, v79
	v_pk_fma_f16 v80, v36, v120, v80
	v_pk_fma_f16 v81, v37, v121, v81
	v_pk_add_f16 v111, v185, v196 neg_lo:[0,1] neg_hi:[0,1]
	v_pk_add_f16 v112, v186, v197 neg_lo:[0,1] neg_hi:[0,1]
	v_pk_add_f16 v113, v187, v198 neg_lo:[0,1] neg_hi:[0,1]
	v_exp_f16_sdwa v118, v110 dst_sel:WORD_0 dst_unused:UNUSED_PAD src0_sel:WORD_0
	v_exp_f16_sdwa v119, v111 dst_sel:WORD_0 dst_unused:UNUSED_PAD src0_sel:WORD_0
	v_exp_f16_sdwa v120, v112 dst_sel:WORD_0 dst_unused:UNUSED_PAD src0_sel:WORD_0
	v_exp_f16_sdwa v121, v113 dst_sel:WORD_0 dst_unused:UNUSED_PAD src0_sel:WORD_0
	v_exp_f16_sdwa v118, v110 dst_sel:WORD_1 dst_unused:UNUSED_PRESERVE src0_sel:WORD_1
	v_exp_f16_sdwa v119, v111 dst_sel:WORD_1 dst_unused:UNUSED_PRESERVE src0_sel:WORD_1
	v_exp_f16_sdwa v120, v112 dst_sel:WORD_1 dst_unused:UNUSED_PRESERVE src0_sel:WORD_1
	v_exp_f16_sdwa v121, v113 dst_sel:WORD_1 dst_unused:UNUSED_PRESERVE src0_sel:WORD_1
	v_pk_add_f16 v105, v105, v118
	v_pk_add_f16 v104, v104, v119
	v_rcp_f16_e32 v110, v105
	v_rcp_f16_sdwa v105, v105 dst_sel:DWORD dst_unused:UNUSED_PAD src0_sel:WORD_1
	v_pk_add_f16 v103, v103, v120
	v_rcp_f16_e32 v111, v104
	v_rcp_f16_sdwa v104, v104 dst_sel:DWORD dst_unused:UNUSED_PAD src0_sel:WORD_1
	v_pk_add_f16 v102, v102, v121
	v_rcp_f16_e32 v112, v103
	v_rcp_f16_sdwa v103, v103 dst_sel:DWORD dst_unused:UNUSED_PAD src0_sel:WORD_1
	v_rcp_f16_e32 v113, v102
	v_rcp_f16_sdwa v102, v102 dst_sel:DWORD dst_unused:UNUSED_PAD src0_sel:WORD_1
	v_pk_fma_f16 v78, v42, v118, v78
	v_pack_b32_f16 v105, v110, v105
	v_pk_fma_f16 v79, v43, v119, v79
	v_pk_mul_f16 v110, v78, v105
	v_pack_b32_f16 v78, v111, v104
	v_pk_fma_f16 v80, v44, v120, v80
	v_pk_mul_f16 v111, v79, v78
	v_pack_b32_f16 v78, v112, v103
	v_pk_fma_f16 v81, v45, v121, v81
	v_pk_mul_f16 v112, v80, v78
	v_pack_b32_f16 v78, v113, v102
	v_pk_mul_f16 v113, v81, v78
	s_waitcnt vmcnt(12)
	v_pk_mul_f16 v78, v182, v154 op_sel_hi:[0,1]
	v_pk_mul_f16 v81, v182, v157 op_sel_hi:[0,1]
	v_pk_mul_f16 v105, v180, v157 op_sel_hi:[0,1]
	v_pk_mul_f16 v121, v181, v157 op_sel_hi:[0,1]
	v_pk_mul_f16 v79, v182, v155 op_sel_hi:[0,1]
	v_pk_mul_f16 v80, v182, v156 op_sel_hi:[0,1]
	v_pk_mul_f16 v102, v180, v154 op_sel_hi:[0,1]
	v_pk_mul_f16 v103, v180, v155 op_sel_hi:[0,1]
	v_pk_mul_f16 v104, v180, v156 op_sel_hi:[0,1]
	v_pk_mul_f16 v118, v181, v154 op_sel_hi:[0,1]
	v_pk_mul_f16 v119, v181, v155 op_sel_hi:[0,1]
	v_pk_mul_f16 v120, v181, v156 op_sel_hi:[0,1]
	v_pk_fma_f16 v89, v89, v157, v81
	v_pk_fma_f16 v86, v86, v154, v78
	v_pk_fma_f16 v109, v109, v157, v81
	v_pk_fma_f16 v106, v106, v154, v78
	v_pk_fma_f16 v81, v125, v157, v81
	v_pk_fma_f16 v78, v122, v154, v78
	v_pk_fma_f16 v122, v53, v157, v105
	v_pk_fma_f16 v126, v69, v157, v105
	v_pk_fma_f16 v105, v97, v157, v105
	v_pk_fma_f16 v138, v21, v157, v121
	v_pk_fma_f16 v183, v33, v157, v121
	v_pk_fma_f16 v121, v57, v157, v121
	v_pk_maximum3_f16 v157, v89, v109, v81
	v_pk_fma_f16 v88, v88, v156, v80
	v_pk_fma_f16 v87, v87, v155, v79
	v_pk_fma_f16 v108, v108, v156, v80
	v_pk_fma_f16 v107, v107, v155, v79
	v_pk_fma_f16 v80, v124, v156, v80
	v_pk_fma_f16 v79, v123, v155, v79
	v_pk_fma_f16 v123, v52, v156, v104
	v_pk_fma_f16 v124, v51, v155, v103
	v_pk_fma_f16 v125, v50, v154, v102
	v_pk_fma_f16 v127, v68, v156, v104
	v_pk_fma_f16 v128, v67, v155, v103
	v_pk_fma_f16 v129, v66, v154, v102
	v_pk_fma_f16 v104, v96, v156, v104
	v_pk_fma_f16 v103, v95, v155, v103
	v_pk_fma_f16 v102, v94, v154, v102
	v_pk_fma_f16 v139, v20, v156, v120
	v_pk_fma_f16 v140, v19, v155, v119
	v_pk_fma_f16 v141, v18, v154, v118
	v_pk_fma_f16 v184, v32, v156, v120
	v_pk_fma_f16 v185, v31, v155, v119
	v_pk_fma_f16 v186, v30, v154, v118
	v_pk_fma_f16 v120, v56, v156, v120
	v_pk_fma_f16 v119, v55, v155, v119
	v_pk_fma_f16 v118, v54, v154, v118
	v_pk_maximum3_f16 v154, v86, v106, v78
	v_pk_maximum3_f16 v155, v87, v107, v79
	v_pk_maximum3_f16 v156, v88, v108, v80
	v_pk_maximum3_f16 v190, v122, v126, v105
	v_pk_maximum3_f16 v194, v138, v183, v121
	v_pk_maximum3_f16 v187, v125, v129, v102
	v_pk_maximum3_f16 v188, v124, v128, v103
	v_pk_maximum3_f16 v189, v123, v127, v104
	v_pk_maximum3_f16 v191, v141, v186, v118
	v_pk_maximum3_f16 v192, v140, v185, v119
	v_pk_maximum3_f16 v157, v157, v190, v194
	v_pk_maximum3_f16 v193, v139, v184, v120
	v_pk_maximum3_f16 v154, v154, v187, v191
	v_pk_maximum3_f16 v155, v155, v188, v192
	v_pk_maximum3_f16 v156, v156, v189, v193
	v_pk_add_f16 v89, v89, v157 neg_lo:[0,1] neg_hi:[0,1]
	v_pk_add_f16 v86, v86, v154 neg_lo:[0,1] neg_hi:[0,1]
	v_pk_add_f16 v87, v87, v155 neg_lo:[0,1] neg_hi:[0,1]
	v_pk_add_f16 v88, v88, v156 neg_lo:[0,1] neg_hi:[0,1]
	v_pk_add_f16 v106, v106, v154 neg_lo:[0,1] neg_hi:[0,1]
	v_exp_f16_sdwa v187, v86 dst_sel:WORD_0 dst_unused:UNUSED_PAD src0_sel:WORD_0
	v_exp_f16_sdwa v188, v87 dst_sel:WORD_0 dst_unused:UNUSED_PAD src0_sel:WORD_0
	v_exp_f16_sdwa v189, v88 dst_sel:WORD_0 dst_unused:UNUSED_PAD src0_sel:WORD_0
	v_exp_f16_sdwa v190, v89 dst_sel:WORD_0 dst_unused:UNUSED_PAD src0_sel:WORD_0
	v_exp_f16_sdwa v187, v86 dst_sel:WORD_1 dst_unused:UNUSED_PRESERVE src0_sel:WORD_1
	v_exp_f16_sdwa v188, v87 dst_sel:WORD_1 dst_unused:UNUSED_PRESERVE src0_sel:WORD_1
	v_exp_f16_sdwa v189, v88 dst_sel:WORD_1 dst_unused:UNUSED_PRESERVE src0_sel:WORD_1
	v_exp_f16_sdwa v190, v89 dst_sel:WORD_1 dst_unused:UNUSED_PRESERVE src0_sel:WORD_1
	v_pk_add_f16 v107, v107, v155 neg_lo:[0,1] neg_hi:[0,1]
	v_pk_add_f16 v89, v187, 0
	v_pk_fma_f16 v49, v49, v190, 0
	v_pk_add_f16 v86, v190, 0
	v_pk_add_f16 v87, v189, 0
	v_pk_add_f16 v88, v188, 0
	v_pk_fma_f16 v48, v48, v189, 0
	v_pk_fma_f16 v47, v47, v188, 0
	v_pk_fma_f16 v46, v46, v187, 0
	v_pk_add_f16 v108, v108, v156 neg_lo:[0,1] neg_hi:[0,1]
	v_pk_add_f16 v109, v109, v157 neg_lo:[0,1] neg_hi:[0,1]
	v_exp_f16_sdwa v187, v106 dst_sel:WORD_0 dst_unused:UNUSED_PAD src0_sel:WORD_0
	v_exp_f16_sdwa v188, v107 dst_sel:WORD_0 dst_unused:UNUSED_PAD src0_sel:WORD_0
	v_exp_f16_sdwa v189, v108 dst_sel:WORD_0 dst_unused:UNUSED_PAD src0_sel:WORD_0
	v_exp_f16_sdwa v190, v109 dst_sel:WORD_0 dst_unused:UNUSED_PAD src0_sel:WORD_0
	v_exp_f16_sdwa v187, v106 dst_sel:WORD_1 dst_unused:UNUSED_PRESERVE src0_sel:WORD_1
	v_exp_f16_sdwa v188, v107 dst_sel:WORD_1 dst_unused:UNUSED_PRESERVE src0_sel:WORD_1
	v_exp_f16_sdwa v189, v108 dst_sel:WORD_1 dst_unused:UNUSED_PRESERVE src0_sel:WORD_1
	v_exp_f16_sdwa v190, v109 dst_sel:WORD_1 dst_unused:UNUSED_PRESERVE src0_sel:WORD_1
	v_pk_add_f16 v89, v89, v187
	v_pk_fma_f16 v49, v65, v190, v49
	v_pk_add_f16 v65, v81, v157 neg_lo:[0,1] neg_hi:[0,1]
	v_pk_add_f16 v88, v88, v188
	v_pk_add_f16 v87, v87, v189
	v_pk_add_f16 v86, v86, v190
	v_pk_fma_f16 v46, v62, v187, v46
	v_pk_fma_f16 v47, v63, v188, v47
	v_pk_fma_f16 v48, v64, v189, v48
	v_pk_add_f16 v62, v78, v154 neg_lo:[0,1] neg_hi:[0,1]
	v_pk_add_f16 v63, v79, v155 neg_lo:[0,1] neg_hi:[0,1]
	v_pk_add_f16 v64, v80, v156 neg_lo:[0,1] neg_hi:[0,1]
	v_exp_f16_sdwa v78, v62 dst_sel:WORD_0 dst_unused:UNUSED_PAD src0_sel:WORD_0
	v_exp_f16_sdwa v79, v63 dst_sel:WORD_0 dst_unused:UNUSED_PAD src0_sel:WORD_0
	v_exp_f16_sdwa v80, v64 dst_sel:WORD_0 dst_unused:UNUSED_PAD src0_sel:WORD_0
	v_exp_f16_sdwa v81, v65 dst_sel:WORD_0 dst_unused:UNUSED_PAD src0_sel:WORD_0
	v_exp_f16_sdwa v78, v62 dst_sel:WORD_1 dst_unused:UNUSED_PRESERVE src0_sel:WORD_1
	v_exp_f16_sdwa v79, v63 dst_sel:WORD_1 dst_unused:UNUSED_PRESERVE src0_sel:WORD_1
	v_exp_f16_sdwa v80, v64 dst_sel:WORD_1 dst_unused:UNUSED_PRESERVE src0_sel:WORD_1
	v_exp_f16_sdwa v81, v65 dst_sel:WORD_1 dst_unused:UNUSED_PRESERVE src0_sel:WORD_1
	v_pk_add_f16 v65, v89, v78
	v_pk_add_f16 v62, v86, v81
	v_pk_add_f16 v63, v87, v80
	v_pk_add_f16 v64, v88, v79
	v_pk_fma_f16 v49, v85, v81, v49
	v_pk_fma_f16 v48, v84, v80, v48
	v_pk_fma_f16 v47, v83, v79, v47
	v_pk_fma_f16 v46, v82, v78, v46
	v_pk_add_f16 v78, v125, v154 neg_lo:[0,1] neg_hi:[0,1]
	v_pk_add_f16 v79, v124, v155 neg_lo:[0,1] neg_hi:[0,1]
	v_pk_add_f16 v80, v123, v156 neg_lo:[0,1] neg_hi:[0,1]
	v_pk_add_f16 v81, v122, v157 neg_lo:[0,1] neg_hi:[0,1]
	v_exp_f16_sdwa v82, v78 dst_sel:WORD_0 dst_unused:UNUSED_PAD src0_sel:WORD_0
	v_exp_f16_sdwa v83, v79 dst_sel:WORD_0 dst_unused:UNUSED_PAD src0_sel:WORD_0
	v_exp_f16_sdwa v84, v80 dst_sel:WORD_0 dst_unused:UNUSED_PAD src0_sel:WORD_0
	v_exp_f16_sdwa v85, v81 dst_sel:WORD_0 dst_unused:UNUSED_PAD src0_sel:WORD_0
	v_exp_f16_sdwa v82, v78 dst_sel:WORD_1 dst_unused:UNUSED_PRESERVE src0_sel:WORD_1
	v_exp_f16_sdwa v83, v79 dst_sel:WORD_1 dst_unused:UNUSED_PRESERVE src0_sel:WORD_1
	v_exp_f16_sdwa v84, v80 dst_sel:WORD_1 dst_unused:UNUSED_PRESERVE src0_sel:WORD_1
	v_exp_f16_sdwa v85, v81 dst_sel:WORD_1 dst_unused:UNUSED_PRESERVE src0_sel:WORD_1
	v_pk_add_f16 v78, v129, v154 neg_lo:[0,1] neg_hi:[0,1]
	v_pk_add_f16 v65, v65, v82
	v_pk_add_f16 v64, v64, v83
	v_pk_add_f16 v63, v63, v84
	v_pk_add_f16 v62, v62, v85
	v_pk_fma_f16 v46, v22, v82, v46
	v_pk_fma_f16 v47, v23, v83, v47
	v_pk_fma_f16 v48, v24, v84, v48
	v_pk_fma_f16 v49, v25, v85, v49
	v_pk_add_f16 v79, v128, v155 neg_lo:[0,1] neg_hi:[0,1]
	v_pk_add_f16 v80, v127, v156 neg_lo:[0,1] neg_hi:[0,1]
	v_pk_add_f16 v81, v126, v157 neg_lo:[0,1] neg_hi:[0,1]
	v_exp_f16_sdwa v82, v78 dst_sel:WORD_0 dst_unused:UNUSED_PAD src0_sel:WORD_0
	v_exp_f16_sdwa v83, v79 dst_sel:WORD_0 dst_unused:UNUSED_PAD src0_sel:WORD_0
	v_exp_f16_sdwa v84, v80 dst_sel:WORD_0 dst_unused:UNUSED_PAD src0_sel:WORD_0
	v_exp_f16_sdwa v85, v81 dst_sel:WORD_0 dst_unused:UNUSED_PAD src0_sel:WORD_0
	v_exp_f16_sdwa v82, v78 dst_sel:WORD_1 dst_unused:UNUSED_PRESERVE src0_sel:WORD_1
	v_exp_f16_sdwa v83, v79 dst_sel:WORD_1 dst_unused:UNUSED_PRESERVE src0_sel:WORD_1
	v_exp_f16_sdwa v84, v80 dst_sel:WORD_1 dst_unused:UNUSED_PRESERVE src0_sel:WORD_1
	v_exp_f16_sdwa v85, v81 dst_sel:WORD_1 dst_unused:UNUSED_PRESERVE src0_sel:WORD_1
	v_pk_add_f16 v78, v102, v154 neg_lo:[0,1] neg_hi:[0,1]
	v_pk_add_f16 v65, v65, v82
	v_pk_add_f16 v62, v62, v85
	v_pk_add_f16 v63, v63, v84
	v_pk_add_f16 v64, v64, v83
	v_pk_fma_f16 v49, v37, v85, v49
	v_pk_fma_f16 v48, v36, v84, v48
	v_pk_fma_f16 v47, v35, v83, v47
	v_pk_fma_f16 v46, v34, v82, v46
	v_pk_add_f16 v79, v103, v155 neg_lo:[0,1] neg_hi:[0,1]
	v_pk_add_f16 v80, v104, v156 neg_lo:[0,1] neg_hi:[0,1]
	v_pk_add_f16 v81, v105, v157 neg_lo:[0,1] neg_hi:[0,1]
	v_exp_f16_sdwa v82, v78 dst_sel:WORD_0 dst_unused:UNUSED_PAD src0_sel:WORD_0
	v_exp_f16_sdwa v83, v79 dst_sel:WORD_0 dst_unused:UNUSED_PAD src0_sel:WORD_0
	v_exp_f16_sdwa v84, v80 dst_sel:WORD_0 dst_unused:UNUSED_PAD src0_sel:WORD_0
	v_exp_f16_sdwa v85, v81 dst_sel:WORD_0 dst_unused:UNUSED_PAD src0_sel:WORD_0
	v_exp_f16_sdwa v82, v78 dst_sel:WORD_1 dst_unused:UNUSED_PRESERVE src0_sel:WORD_1
	v_exp_f16_sdwa v83, v79 dst_sel:WORD_1 dst_unused:UNUSED_PRESERVE src0_sel:WORD_1
	v_exp_f16_sdwa v84, v80 dst_sel:WORD_1 dst_unused:UNUSED_PRESERVE src0_sel:WORD_1
	v_exp_f16_sdwa v85, v81 dst_sel:WORD_1 dst_unused:UNUSED_PRESERVE src0_sel:WORD_1
	v_pk_add_f16 v78, v141, v154 neg_lo:[0,1] neg_hi:[0,1]
	v_pk_add_f16 v65, v65, v82
	v_pk_add_f16 v64, v64, v83
	v_pk_add_f16 v63, v63, v84
	v_pk_add_f16 v62, v62, v85
	v_pk_fma_f16 v46, v42, v82, v46
	v_pk_fma_f16 v47, v43, v83, v47
	v_pk_fma_f16 v48, v44, v84, v48
	v_pk_fma_f16 v49, v45, v85, v49
	v_pk_add_f16 v79, v140, v155 neg_lo:[0,1] neg_hi:[0,1]
	v_pk_add_f16 v80, v139, v156 neg_lo:[0,1] neg_hi:[0,1]
	v_pk_add_f16 v81, v138, v157 neg_lo:[0,1] neg_hi:[0,1]
	v_exp_f16_sdwa v82, v78 dst_sel:WORD_0 dst_unused:UNUSED_PAD src0_sel:WORD_0
	v_exp_f16_sdwa v83, v79 dst_sel:WORD_0 dst_unused:UNUSED_PAD src0_sel:WORD_0
	v_exp_f16_sdwa v84, v80 dst_sel:WORD_0 dst_unused:UNUSED_PAD src0_sel:WORD_0
	v_exp_f16_sdwa v85, v81 dst_sel:WORD_0 dst_unused:UNUSED_PAD src0_sel:WORD_0
	v_exp_f16_sdwa v82, v78 dst_sel:WORD_1 dst_unused:UNUSED_PRESERVE src0_sel:WORD_1
	v_exp_f16_sdwa v83, v79 dst_sel:WORD_1 dst_unused:UNUSED_PRESERVE src0_sel:WORD_1
	v_exp_f16_sdwa v84, v80 dst_sel:WORD_1 dst_unused:UNUSED_PRESERVE src0_sel:WORD_1
	v_exp_f16_sdwa v85, v81 dst_sel:WORD_1 dst_unused:UNUSED_PRESERVE src0_sel:WORD_1
	v_pk_add_f16 v78, v186, v154 neg_lo:[0,1] neg_hi:[0,1]
	v_pk_add_f16 v65, v65, v82
	v_pk_add_f16 v62, v62, v85
	v_pk_add_f16 v63, v63, v84
	v_pk_add_f16 v64, v64, v83
	v_pk_fma_f16 v49, v9, v85, v49
	v_pk_fma_f16 v48, v8, v84, v48
	v_pk_fma_f16 v47, v7, v83, v47
	v_pk_fma_f16 v46, v6, v82, v46
	v_pk_add_f16 v79, v185, v155 neg_lo:[0,1] neg_hi:[0,1]
	v_pk_add_f16 v80, v184, v156 neg_lo:[0,1] neg_hi:[0,1]
	v_pk_add_f16 v81, v183, v157 neg_lo:[0,1] neg_hi:[0,1]
	v_exp_f16_sdwa v82, v78 dst_sel:WORD_0 dst_unused:UNUSED_PAD src0_sel:WORD_0
	v_exp_f16_sdwa v83, v79 dst_sel:WORD_0 dst_unused:UNUSED_PAD src0_sel:WORD_0
	v_exp_f16_sdwa v84, v80 dst_sel:WORD_0 dst_unused:UNUSED_PAD src0_sel:WORD_0
	v_exp_f16_sdwa v85, v81 dst_sel:WORD_0 dst_unused:UNUSED_PAD src0_sel:WORD_0
	v_exp_f16_sdwa v82, v78 dst_sel:WORD_1 dst_unused:UNUSED_PRESERVE src0_sel:WORD_1
	v_exp_f16_sdwa v83, v79 dst_sel:WORD_1 dst_unused:UNUSED_PRESERVE src0_sel:WORD_1
	v_exp_f16_sdwa v84, v80 dst_sel:WORD_1 dst_unused:UNUSED_PRESERVE src0_sel:WORD_1
	v_exp_f16_sdwa v85, v81 dst_sel:WORD_1 dst_unused:UNUSED_PRESERVE src0_sel:WORD_1
	v_pk_add_f16 v78, v118, v154 neg_lo:[0,1] neg_hi:[0,1]
	v_pk_add_f16 v65, v65, v82
	v_pk_add_f16 v64, v64, v83
	v_pk_add_f16 v63, v63, v84
	v_pk_add_f16 v62, v62, v85
	v_pk_fma_f16 v46, v10, v82, v46
	v_pk_fma_f16 v47, v11, v83, v47
	v_pk_fma_f16 v48, v12, v84, v48
	v_pk_fma_f16 v49, v13, v85, v49
	v_pk_add_f16 v79, v119, v155 neg_lo:[0,1] neg_hi:[0,1]
	v_pk_add_f16 v80, v120, v156 neg_lo:[0,1] neg_hi:[0,1]
	v_pk_add_f16 v81, v121, v157 neg_lo:[0,1] neg_hi:[0,1]
	v_exp_f16_sdwa v82, v78 dst_sel:WORD_0 dst_unused:UNUSED_PAD src0_sel:WORD_0
	v_exp_f16_sdwa v83, v79 dst_sel:WORD_0 dst_unused:UNUSED_PAD src0_sel:WORD_0
	v_exp_f16_sdwa v84, v80 dst_sel:WORD_0 dst_unused:UNUSED_PAD src0_sel:WORD_0
	v_exp_f16_sdwa v85, v81 dst_sel:WORD_0 dst_unused:UNUSED_PAD src0_sel:WORD_0
	v_exp_f16_sdwa v82, v78 dst_sel:WORD_1 dst_unused:UNUSED_PRESERVE src0_sel:WORD_1
	v_exp_f16_sdwa v83, v79 dst_sel:WORD_1 dst_unused:UNUSED_PRESERVE src0_sel:WORD_1
	v_exp_f16_sdwa v84, v80 dst_sel:WORD_1 dst_unused:UNUSED_PRESERVE src0_sel:WORD_1
	v_exp_f16_sdwa v85, v81 dst_sel:WORD_1 dst_unused:UNUSED_PRESERVE src0_sel:WORD_1
	v_pk_add_f16 v65, v65, v82
	v_pk_add_f16 v64, v64, v83
	v_rcp_f16_e32 v78, v65
	v_rcp_f16_sdwa v65, v65 dst_sel:DWORD dst_unused:UNUSED_PAD src0_sel:WORD_1
	v_pk_add_f16 v63, v63, v84
	v_rcp_f16_e32 v79, v64
	v_rcp_f16_sdwa v64, v64 dst_sel:DWORD dst_unused:UNUSED_PAD src0_sel:WORD_1
	v_pk_add_f16 v62, v62, v85
	v_rcp_f16_e32 v80, v63
	v_rcp_f16_sdwa v81, v63 dst_sel:DWORD dst_unused:UNUSED_PAD src0_sel:WORD_1
	v_pk_fma_f16 v47, v15, v83, v47
	v_pk_fma_f16 v46, v14, v82, v46
	v_rcp_f16_e32 v82, v62
	v_rcp_f16_sdwa v83, v62 dst_sel:DWORD dst_unused:UNUSED_PAD src0_sel:WORD_1
	v_pack_b32_f16 v62, v78, v65
	v_pk_mul_f16 v62, v46, v62
	v_pack_b32_f16 v46, v79, v64
	v_pk_fma_f16 v48, v16, v84, v48
	v_pk_mul_f16 v63, v47, v46
	v_pack_b32_f16 v46, v80, v81
	v_pk_fma_f16 v49, v17, v85, v49
	v_pk_mul_f16 v64, v48, v46
	v_pack_b32_f16 v46, v82, v83
	v_pk_mul_f16 v65, v49, v46
	s_waitcnt vmcnt(6)
	v_pk_mul_f16 v46, v182, v150 op_sel_hi:[0,1]
	v_pk_mul_f16 v47, v182, v151 op_sel_hi:[0,1]
	v_pk_mul_f16 v48, v182, v152 op_sel_hi:[0,1]
	v_pk_mul_f16 v49, v182, v153 op_sel_hi:[0,1]
	v_pk_mul_f16 v78, v180, v150 op_sel_hi:[0,1]
	v_pk_mul_f16 v82, v181, v150 op_sel_hi:[0,1]
	v_pk_fma_f16 v50, v50, v150, v46
	v_pk_fma_f16 v66, v66, v150, v46
	v_pk_fma_f16 v46, v94, v150, v46
	v_pk_mul_f16 v79, v180, v151 op_sel_hi:[0,1]
	v_pk_maximum3_f16 v118, v50, v66, v46
	v_pk_mul_f16 v80, v180, v152 op_sel_hi:[0,1]
	v_pk_mul_f16 v81, v180, v153 op_sel_hi:[0,1]
	v_pk_mul_f16 v83, v181, v151 op_sel_hi:[0,1]
	v_pk_mul_f16 v84, v181, v152 op_sel_hi:[0,1]
	v_pk_mul_f16 v85, v181, v153 op_sel_hi:[0,1]
	v_pk_fma_f16 v53, v53, v153, v49
	v_pk_fma_f16 v52, v52, v152, v48
	v_pk_fma_f16 v51, v51, v151, v47
	v_pk_fma_f16 v69, v69, v153, v49
	v_pk_fma_f16 v68, v68, v152, v48
	v_pk_fma_f16 v67, v67, v151, v47
	v_pk_fma_f16 v49, v97, v153, v49
	v_pk_fma_f16 v48, v96, v152, v48
	v_pk_fma_f16 v47, v95, v151, v47
	v_pk_fma_f16 v89, v18, v150, v78
	v_pk_fma_f16 v97, v30, v150, v78
	v_pk_fma_f16 v78, v54, v150, v78
	v_pk_fma_f16 v105, v74, v150, v82
	v_pk_fma_f16 v109, v98, v150, v82
	v_pk_fma_f16 v82, v114, v150, v82
	v_pk_maximum3_f16 v119, v51, v67, v47
	v_pk_maximum3_f16 v120, v52, v68, v48
	v_pk_maximum3_f16 v121, v53, v69, v49
	v_pk_maximum3_f16 v122, v89, v97, v78
	v_pk_fma_f16 v86, v21, v153, v81
	v_pk_maximum3_f16 v126, v105, v109, v82
	v_pk_fma_f16 v87, v20, v152, v80
	v_pk_maximum3_f16 v118, v118, v122, v126
	v_pk_fma_f16 v88, v19, v151, v79
	v_pk_fma_f16 v94, v33, v153, v81
	v_pk_fma_f16 v95, v32, v152, v80
	v_pk_fma_f16 v96, v31, v151, v79
	v_pk_fma_f16 v81, v57, v153, v81
	v_pk_fma_f16 v80, v56, v152, v80
	v_pk_fma_f16 v79, v55, v151, v79
	v_pk_fma_f16 v102, v77, v153, v85
	v_pk_fma_f16 v103, v76, v152, v84
	v_pk_fma_f16 v104, v75, v151, v83
	v_pk_fma_f16 v106, v101, v153, v85
	v_pk_fma_f16 v107, v100, v152, v84
	v_pk_fma_f16 v108, v99, v151, v83
	v_pk_fma_f16 v85, v117, v153, v85
	v_pk_fma_f16 v84, v116, v152, v84
	v_pk_fma_f16 v83, v115, v151, v83
	v_pk_maximum3_f16 v123, v88, v96, v79
	v_pk_maximum3_f16 v124, v87, v95, v80
	v_pk_maximum3_f16 v125, v86, v94, v81
	v_pk_maximum3_f16 v128, v103, v107, v84
	v_pk_maximum3_f16 v129, v102, v106, v85
	v_pk_maximum3_f16 v127, v104, v108, v83
	v_pk_maximum3_f16 v119, v119, v123, v127
	v_pk_maximum3_f16 v120, v120, v124, v128
	v_pk_maximum3_f16 v121, v121, v125, v129
	v_pk_add_f16 v50, v50, v118 neg_lo:[0,1] neg_hi:[0,1]
	v_pk_add_f16 v51, v51, v119 neg_lo:[0,1] neg_hi:[0,1]
	v_pk_add_f16 v52, v52, v120 neg_lo:[0,1] neg_hi:[0,1]
	v_pk_add_f16 v53, v53, v121 neg_lo:[0,1] neg_hi:[0,1]
	v_pk_add_f16 v66, v66, v118 neg_lo:[0,1] neg_hi:[0,1]
	v_exp_f16_sdwa v122, v50 dst_sel:WORD_0 dst_unused:UNUSED_PAD src0_sel:WORD_0
	v_exp_f16_sdwa v123, v51 dst_sel:WORD_0 dst_unused:UNUSED_PAD src0_sel:WORD_0
	v_exp_f16_sdwa v124, v52 dst_sel:WORD_0 dst_unused:UNUSED_PAD src0_sel:WORD_0
	v_exp_f16_sdwa v125, v53 dst_sel:WORD_0 dst_unused:UNUSED_PAD src0_sel:WORD_0
	v_exp_f16_sdwa v122, v50 dst_sel:WORD_1 dst_unused:UNUSED_PRESERVE src0_sel:WORD_1
	v_exp_f16_sdwa v123, v51 dst_sel:WORD_1 dst_unused:UNUSED_PRESERVE src0_sel:WORD_1
	v_exp_f16_sdwa v124, v52 dst_sel:WORD_1 dst_unused:UNUSED_PRESERVE src0_sel:WORD_1
	v_exp_f16_sdwa v125, v53 dst_sel:WORD_1 dst_unused:UNUSED_PRESERVE src0_sel:WORD_1
	v_pk_add_f16 v67, v67, v119 neg_lo:[0,1] neg_hi:[0,1]
	v_pk_add_f16 v50, v125, 0
	v_pk_fma_f16 v22, v22, v122, 0
	v_pk_add_f16 v51, v124, 0
	v_pk_add_f16 v52, v123, 0
	v_pk_add_f16 v53, v122, 0
	v_pk_fma_f16 v23, v23, v123, 0
	v_pk_fma_f16 v24, v24, v124, 0
	v_pk_fma_f16 v25, v25, v125, 0
	v_pk_add_f16 v68, v68, v120 neg_lo:[0,1] neg_hi:[0,1]
	v_pk_add_f16 v69, v69, v121 neg_lo:[0,1] neg_hi:[0,1]
	v_exp_f16_sdwa v122, v66 dst_sel:WORD_0 dst_unused:UNUSED_PAD src0_sel:WORD_0
	v_exp_f16_sdwa v123, v67 dst_sel:WORD_0 dst_unused:UNUSED_PAD src0_sel:WORD_0
	v_exp_f16_sdwa v124, v68 dst_sel:WORD_0 dst_unused:UNUSED_PAD src0_sel:WORD_0
	v_exp_f16_sdwa v125, v69 dst_sel:WORD_0 dst_unused:UNUSED_PAD src0_sel:WORD_0
	v_exp_f16_sdwa v122, v66 dst_sel:WORD_1 dst_unused:UNUSED_PRESERVE src0_sel:WORD_1
	v_exp_f16_sdwa v123, v67 dst_sel:WORD_1 dst_unused:UNUSED_PRESERVE src0_sel:WORD_1
	v_exp_f16_sdwa v124, v68 dst_sel:WORD_1 dst_unused:UNUSED_PRESERVE src0_sel:WORD_1
	v_exp_f16_sdwa v125, v69 dst_sel:WORD_1 dst_unused:UNUSED_PRESERVE src0_sel:WORD_1
	s_nop 0
	v_pk_add_f16 v50, v50, v125
	v_pk_fma_f16 v22, v34, v122, v22
	v_pk_add_f16 v34, v46, v118 neg_lo:[0,1] neg_hi:[0,1]
	v_pk_add_f16 v53, v53, v122
	v_pk_add_f16 v52, v52, v123
	v_pk_add_f16 v51, v51, v124
	v_pk_fma_f16 v25, v37, v125, v25
	v_pk_fma_f16 v24, v36, v124, v24
	v_pk_fma_f16 v23, v35, v123, v23
	v_pk_add_f16 v35, v47, v119 neg_lo:[0,1] neg_hi:[0,1]
	v_pk_add_f16 v36, v48, v120 neg_lo:[0,1] neg_hi:[0,1]
	v_pk_add_f16 v37, v49, v121 neg_lo:[0,1] neg_hi:[0,1]
	v_exp_f16_sdwa v46, v34 dst_sel:WORD_0 dst_unused:UNUSED_PAD src0_sel:WORD_0
	v_exp_f16_sdwa v47, v35 dst_sel:WORD_0 dst_unused:UNUSED_PAD src0_sel:WORD_0
	v_exp_f16_sdwa v48, v36 dst_sel:WORD_0 dst_unused:UNUSED_PAD src0_sel:WORD_0
	v_exp_f16_sdwa v49, v37 dst_sel:WORD_0 dst_unused:UNUSED_PAD src0_sel:WORD_0
	v_exp_f16_sdwa v46, v34 dst_sel:WORD_1 dst_unused:UNUSED_PRESERVE src0_sel:WORD_1
	v_exp_f16_sdwa v47, v35 dst_sel:WORD_1 dst_unused:UNUSED_PRESERVE src0_sel:WORD_1
	v_exp_f16_sdwa v48, v36 dst_sel:WORD_1 dst_unused:UNUSED_PRESERVE src0_sel:WORD_1
	v_exp_f16_sdwa v49, v37 dst_sel:WORD_1 dst_unused:UNUSED_PRESERVE src0_sel:WORD_1
	s_nop 0
	v_pk_add_f16 v34, v50, v49
	v_pk_add_f16 v35, v51, v48
	v_pk_add_f16 v36, v52, v47
	v_pk_add_f16 v37, v53, v46
	v_pk_fma_f16 v22, v42, v46, v22
	v_pk_fma_f16 v23, v43, v47, v23
	v_pk_fma_f16 v24, v44, v48, v24
	v_pk_fma_f16 v25, v45, v49, v25
	v_pk_add_f16 v42, v89, v118 neg_lo:[0,1] neg_hi:[0,1]
	v_pk_add_f16 v43, v88, v119 neg_lo:[0,1] neg_hi:[0,1]
	v_pk_add_f16 v44, v87, v120 neg_lo:[0,1] neg_hi:[0,1]
	v_pk_add_f16 v45, v86, v121 neg_lo:[0,1] neg_hi:[0,1]
	v_exp_f16_sdwa v46, v42 dst_sel:WORD_0 dst_unused:UNUSED_PAD src0_sel:WORD_0
	v_exp_f16_sdwa v47, v43 dst_sel:WORD_0 dst_unused:UNUSED_PAD src0_sel:WORD_0
	v_exp_f16_sdwa v48, v44 dst_sel:WORD_0 dst_unused:UNUSED_PAD src0_sel:WORD_0
	v_exp_f16_sdwa v49, v45 dst_sel:WORD_0 dst_unused:UNUSED_PAD src0_sel:WORD_0
	v_exp_f16_sdwa v46, v42 dst_sel:WORD_1 dst_unused:UNUSED_PRESERVE src0_sel:WORD_1
	v_exp_f16_sdwa v47, v43 dst_sel:WORD_1 dst_unused:UNUSED_PRESERVE src0_sel:WORD_1
	v_exp_f16_sdwa v48, v44 dst_sel:WORD_1 dst_unused:UNUSED_PRESERVE src0_sel:WORD_1
	v_exp_f16_sdwa v49, v45 dst_sel:WORD_1 dst_unused:UNUSED_PRESERVE src0_sel:WORD_1
	v_pk_add_f16 v42, v97, v118 neg_lo:[0,1] neg_hi:[0,1]
	v_pk_add_f16 v34, v34, v49
	v_pk_add_f16 v37, v37, v46
	v_pk_add_f16 v36, v36, v47
	v_pk_add_f16 v35, v35, v48
	v_pk_fma_f16 v25, v9, v49, v25
	v_pk_fma_f16 v24, v8, v48, v24
	v_pk_fma_f16 v23, v7, v47, v23
	v_pk_fma_f16 v22, v6, v46, v22
	v_pk_add_f16 v43, v96, v119 neg_lo:[0,1] neg_hi:[0,1]
	v_pk_add_f16 v44, v95, v120 neg_lo:[0,1] neg_hi:[0,1]
	v_pk_add_f16 v45, v94, v121 neg_lo:[0,1] neg_hi:[0,1]
	v_exp_f16_sdwa v46, v42 dst_sel:WORD_0 dst_unused:UNUSED_PAD src0_sel:WORD_0
	v_exp_f16_sdwa v47, v43 dst_sel:WORD_0 dst_unused:UNUSED_PAD src0_sel:WORD_0
	v_exp_f16_sdwa v48, v44 dst_sel:WORD_0 dst_unused:UNUSED_PAD src0_sel:WORD_0
	v_exp_f16_sdwa v49, v45 dst_sel:WORD_0 dst_unused:UNUSED_PAD src0_sel:WORD_0
	v_exp_f16_sdwa v46, v42 dst_sel:WORD_1 dst_unused:UNUSED_PRESERVE src0_sel:WORD_1
	v_exp_f16_sdwa v47, v43 dst_sel:WORD_1 dst_unused:UNUSED_PRESERVE src0_sel:WORD_1
	v_exp_f16_sdwa v48, v44 dst_sel:WORD_1 dst_unused:UNUSED_PRESERVE src0_sel:WORD_1
	v_exp_f16_sdwa v49, v45 dst_sel:WORD_1 dst_unused:UNUSED_PRESERVE src0_sel:WORD_1
	v_pk_add_f16 v42, v78, v118 neg_lo:[0,1] neg_hi:[0,1]
	v_pk_add_f16 v34, v34, v49
	v_pk_add_f16 v35, v35, v48
	v_pk_add_f16 v36, v36, v47
	v_pk_add_f16 v37, v37, v46
	v_pk_fma_f16 v22, v10, v46, v22
	v_pk_fma_f16 v23, v11, v47, v23
	v_pk_fma_f16 v24, v12, v48, v24
	v_pk_fma_f16 v25, v13, v49, v25
	v_pk_add_f16 v43, v79, v119 neg_lo:[0,1] neg_hi:[0,1]
	v_pk_add_f16 v44, v80, v120 neg_lo:[0,1] neg_hi:[0,1]
	v_pk_add_f16 v45, v81, v121 neg_lo:[0,1] neg_hi:[0,1]
	v_exp_f16_sdwa v46, v42 dst_sel:WORD_0 dst_unused:UNUSED_PAD src0_sel:WORD_0
	v_exp_f16_sdwa v47, v43 dst_sel:WORD_0 dst_unused:UNUSED_PAD src0_sel:WORD_0
	v_exp_f16_sdwa v48, v44 dst_sel:WORD_0 dst_unused:UNUSED_PAD src0_sel:WORD_0
	v_exp_f16_sdwa v49, v45 dst_sel:WORD_0 dst_unused:UNUSED_PAD src0_sel:WORD_0
	v_exp_f16_sdwa v46, v42 dst_sel:WORD_1 dst_unused:UNUSED_PRESERVE src0_sel:WORD_1
	v_exp_f16_sdwa v47, v43 dst_sel:WORD_1 dst_unused:UNUSED_PRESERVE src0_sel:WORD_1
	v_exp_f16_sdwa v48, v44 dst_sel:WORD_1 dst_unused:UNUSED_PRESERVE src0_sel:WORD_1
	v_exp_f16_sdwa v49, v45 dst_sel:WORD_1 dst_unused:UNUSED_PRESERVE src0_sel:WORD_1
	v_pk_add_f16 v42, v105, v118 neg_lo:[0,1] neg_hi:[0,1]
	v_pk_add_f16 v34, v34, v49
	v_pk_add_f16 v37, v37, v46
	v_pk_add_f16 v36, v36, v47
	v_pk_add_f16 v35, v35, v48
	v_pk_fma_f16 v25, v17, v49, v25
	v_pk_fma_f16 v24, v16, v48, v24
	v_pk_fma_f16 v23, v15, v47, v23
	v_pk_fma_f16 v22, v14, v46, v22
	v_pk_add_f16 v43, v104, v119 neg_lo:[0,1] neg_hi:[0,1]
	v_pk_add_f16 v44, v103, v120 neg_lo:[0,1] neg_hi:[0,1]
	v_pk_add_f16 v45, v102, v121 neg_lo:[0,1] neg_hi:[0,1]
	v_exp_f16_sdwa v46, v42 dst_sel:WORD_0 dst_unused:UNUSED_PAD src0_sel:WORD_0
	v_exp_f16_sdwa v47, v43 dst_sel:WORD_0 dst_unused:UNUSED_PAD src0_sel:WORD_0
	v_exp_f16_sdwa v48, v44 dst_sel:WORD_0 dst_unused:UNUSED_PAD src0_sel:WORD_0
	v_exp_f16_sdwa v49, v45 dst_sel:WORD_0 dst_unused:UNUSED_PAD src0_sel:WORD_0
	v_exp_f16_sdwa v46, v42 dst_sel:WORD_1 dst_unused:UNUSED_PRESERVE src0_sel:WORD_1
	v_exp_f16_sdwa v47, v43 dst_sel:WORD_1 dst_unused:UNUSED_PRESERVE src0_sel:WORD_1
	v_exp_f16_sdwa v48, v44 dst_sel:WORD_1 dst_unused:UNUSED_PRESERVE src0_sel:WORD_1
	v_exp_f16_sdwa v49, v45 dst_sel:WORD_1 dst_unused:UNUSED_PRESERVE src0_sel:WORD_1
	v_pk_add_f16 v42, v109, v118 neg_lo:[0,1] neg_hi:[0,1]
	v_pk_add_f16 v34, v34, v49
	v_pk_add_f16 v35, v35, v48
	v_pk_add_f16 v36, v36, v47
	v_pk_add_f16 v37, v37, v46
	v_pk_fma_f16 v22, v26, v46, v22
	v_pk_fma_f16 v23, v27, v47, v23
	v_pk_fma_f16 v24, v28, v48, v24
	v_pk_fma_f16 v25, v29, v49, v25
	v_pk_add_f16 v43, v108, v119 neg_lo:[0,1] neg_hi:[0,1]
	v_pk_add_f16 v44, v107, v120 neg_lo:[0,1] neg_hi:[0,1]
	v_pk_add_f16 v45, v106, v121 neg_lo:[0,1] neg_hi:[0,1]
	v_exp_f16_sdwa v46, v42 dst_sel:WORD_0 dst_unused:UNUSED_PAD src0_sel:WORD_0
	v_exp_f16_sdwa v47, v43 dst_sel:WORD_0 dst_unused:UNUSED_PAD src0_sel:WORD_0
	v_exp_f16_sdwa v48, v44 dst_sel:WORD_0 dst_unused:UNUSED_PAD src0_sel:WORD_0
	v_exp_f16_sdwa v49, v45 dst_sel:WORD_0 dst_unused:UNUSED_PAD src0_sel:WORD_0
	v_exp_f16_sdwa v46, v42 dst_sel:WORD_1 dst_unused:UNUSED_PRESERVE src0_sel:WORD_1
	v_exp_f16_sdwa v47, v43 dst_sel:WORD_1 dst_unused:UNUSED_PRESERVE src0_sel:WORD_1
	v_exp_f16_sdwa v48, v44 dst_sel:WORD_1 dst_unused:UNUSED_PRESERVE src0_sel:WORD_1
	v_exp_f16_sdwa v49, v45 dst_sel:WORD_1 dst_unused:UNUSED_PRESERVE src0_sel:WORD_1
	v_pk_add_f16 v42, v82, v118 neg_lo:[0,1] neg_hi:[0,1]
	v_pk_add_f16 v34, v34, v49
	v_pk_add_f16 v37, v37, v46
	v_pk_add_f16 v36, v36, v47
	v_pk_add_f16 v35, v35, v48
	v_pk_fma_f16 v25, v41, v49, v25
	v_pk_fma_f16 v24, v40, v48, v24
	v_pk_fma_f16 v23, v39, v47, v23
	v_pk_fma_f16 v22, v38, v46, v22
	v_pk_add_f16 v43, v83, v119 neg_lo:[0,1] neg_hi:[0,1]
	v_pk_add_f16 v44, v84, v120 neg_lo:[0,1] neg_hi:[0,1]
	v_pk_add_f16 v45, v85, v121 neg_lo:[0,1] neg_hi:[0,1]
	v_exp_f16_sdwa v46, v42 dst_sel:WORD_0 dst_unused:UNUSED_PAD src0_sel:WORD_0
	v_exp_f16_sdwa v47, v43 dst_sel:WORD_0 dst_unused:UNUSED_PAD src0_sel:WORD_0
	v_exp_f16_sdwa v48, v44 dst_sel:WORD_0 dst_unused:UNUSED_PAD src0_sel:WORD_0
	v_exp_f16_sdwa v49, v45 dst_sel:WORD_0 dst_unused:UNUSED_PAD src0_sel:WORD_0
	v_exp_f16_sdwa v46, v42 dst_sel:WORD_1 dst_unused:UNUSED_PRESERVE src0_sel:WORD_1
	v_exp_f16_sdwa v47, v43 dst_sel:WORD_1 dst_unused:UNUSED_PRESERVE src0_sel:WORD_1
	v_exp_f16_sdwa v48, v44 dst_sel:WORD_1 dst_unused:UNUSED_PRESERVE src0_sel:WORD_1
	v_exp_f16_sdwa v49, v45 dst_sel:WORD_1 dst_unused:UNUSED_PRESERVE src0_sel:WORD_1
	s_nop 0
	v_pk_add_f16 v34, v34, v49
	v_pk_add_f16 v35, v35, v48
	v_rcp_f16_e32 v44, v34
	v_rcp_f16_sdwa v34, v34 dst_sel:DWORD dst_unused:UNUSED_PAD src0_sel:WORD_1
	v_pk_add_f16 v36, v36, v47
	v_rcp_f16_e32 v45, v35
	v_rcp_f16_sdwa v35, v35 dst_sel:DWORD dst_unused:UNUSED_PAD src0_sel:WORD_1
	v_pk_add_f16 v37, v37, v46
	v_rcp_f16_e32 v43, v36
	v_rcp_f16_sdwa v36, v36 dst_sel:DWORD dst_unused:UNUSED_PAD src0_sel:WORD_1
	v_rcp_f16_e32 v42, v37
	v_rcp_f16_sdwa v37, v37 dst_sel:DWORD dst_unused:UNUSED_PAD src0_sel:WORD_1
	v_pk_fma_f16 v25, v61, v49, v25
	v_pack_b32_f16 v34, v44, v34
	v_pk_fma_f16 v24, v60, v48, v24
	v_pk_mul_f16 v25, v25, v34
	v_pack_b32_f16 v34, v45, v35
	v_pk_fma_f16 v23, v59, v47, v23
	v_pk_mul_f16 v24, v24, v34
	v_pack_b32_f16 v34, v43, v36
	v_pk_fma_f16 v22, v58, v46, v22
	v_pk_mul_f16 v23, v23, v34
	v_pack_b32_f16 v34, v42, v37
	v_pk_mul_f16 v22, v22, v34
	s_waitcnt vmcnt(0)
	v_pk_mul_f16 v34, v182, v146 op_sel_hi:[0,1]
	v_pk_mul_f16 v35, v182, v147 op_sel_hi:[0,1]
	v_pk_mul_f16 v36, v182, v148 op_sel_hi:[0,1]
	v_pk_mul_f16 v37, v182, v149 op_sel_hi:[0,1]
	v_pk_mul_f16 v42, v180, v146 op_sel_hi:[0,1]
	v_pk_mul_f16 v43, v180, v147 op_sel_hi:[0,1]
	v_pk_mul_f16 v44, v180, v148 op_sel_hi:[0,1]
	v_pk_mul_f16 v45, v180, v149 op_sel_hi:[0,1]
	v_pk_mul_f16 v46, v181, v146 op_sel_hi:[0,1]
	v_pk_mul_f16 v47, v181, v147 op_sel_hi:[0,1]
	v_pk_mul_f16 v48, v181, v148 op_sel_hi:[0,1]
	v_pk_mul_f16 v49, v181, v149 op_sel_hi:[0,1]
	v_pk_fma_f16 v21, v21, v149, v37
	v_pk_fma_f16 v20, v20, v148, v36
	v_pk_fma_f16 v19, v19, v147, v35
	v_pk_fma_f16 v18, v18, v146, v34
	v_pk_fma_f16 v33, v33, v149, v37
	v_pk_fma_f16 v32, v32, v148, v36
	v_pk_fma_f16 v31, v31, v147, v35
	v_pk_fma_f16 v30, v30, v146, v34
	v_pk_fma_f16 v37, v57, v149, v37
	v_pk_fma_f16 v36, v56, v148, v36
	v_pk_fma_f16 v35, v55, v147, v35
	v_pk_fma_f16 v34, v54, v146, v34
	v_pk_maximum3_f16 v79, v19, v31, v35
	v_pk_maximum3_f16 v80, v20, v32, v36
	v_pk_maximum3_f16 v81, v21, v33, v37
	v_pk_fma_f16 v50, v77, v149, v45
	v_pk_maximum3_f16 v78, v18, v30, v34
	v_pk_fma_f16 v51, v76, v148, v44
	v_pk_fma_f16 v52, v75, v147, v43
	v_pk_fma_f16 v53, v74, v146, v42
	v_pk_fma_f16 v54, v101, v149, v45
	v_pk_fma_f16 v55, v100, v148, v44
	v_pk_fma_f16 v56, v99, v147, v43
	v_pk_fma_f16 v57, v98, v146, v42
	v_pk_fma_f16 v45, v117, v149, v45
	v_pk_fma_f16 v44, v116, v148, v44
	v_pk_fma_f16 v43, v115, v147, v43
	v_pk_fma_f16 v42, v114, v146, v42
	v_pk_fma_f16 v66, v133, v149, v49
	v_pk_fma_f16 v67, v132, v148, v48
	v_pk_fma_f16 v68, v131, v147, v47
	v_pk_fma_f16 v69, v130, v146, v46
	v_pk_fma_f16 v74, v137, v149, v49
	v_pk_fma_f16 v75, v136, v148, v48
	v_pk_fma_f16 v76, v135, v147, v47
	v_pk_fma_f16 v77, v134, v146, v46
	v_pk_fma_f16 v49, v145, v149, v49
	v_pk_fma_f16 v48, v144, v148, v48
	v_pk_fma_f16 v47, v143, v147, v47
	v_pk_fma_f16 v46, v142, v146, v46
	v_pk_maximum3_f16 v82, v53, v57, v42
	v_pk_maximum3_f16 v83, v52, v56, v43
	v_pk_maximum3_f16 v84, v51, v55, v44
	v_pk_maximum3_f16 v85, v50, v54, v45
	v_pk_maximum3_f16 v87, v68, v76, v47
	v_pk_maximum3_f16 v86, v69, v77, v46
	v_pk_maximum3_f16 v88, v67, v75, v48
	v_pk_maximum3_f16 v89, v66, v74, v49
	v_pk_maximum3_f16 v78, v78, v82, v86
	v_pk_maximum3_f16 v79, v79, v83, v87
	v_pk_maximum3_f16 v80, v80, v84, v88
	v_pk_maximum3_f16 v81, v81, v85, v89
	s_nop 0
	v_pk_add_f16 v18, v18, v78 neg_lo:[0,1] neg_hi:[0,1]
	v_pk_add_f16 v19, v19, v79 neg_lo:[0,1] neg_hi:[0,1]
	v_pk_add_f16 v20, v20, v80 neg_lo:[0,1] neg_hi:[0,1]
	v_pk_add_f16 v21, v21, v81 neg_lo:[0,1] neg_hi:[0,1]
	v_pk_add_f16 v30, v30, v78 neg_lo:[0,1] neg_hi:[0,1]
	v_exp_f16_sdwa v82, v18 dst_sel:WORD_0 dst_unused:UNUSED_PAD src0_sel:WORD_0
	v_exp_f16_sdwa v83, v19 dst_sel:WORD_0 dst_unused:UNUSED_PAD src0_sel:WORD_0
	v_exp_f16_sdwa v84, v20 dst_sel:WORD_0 dst_unused:UNUSED_PAD src0_sel:WORD_0
	v_exp_f16_sdwa v85, v21 dst_sel:WORD_0 dst_unused:UNUSED_PAD src0_sel:WORD_0
	v_exp_f16_sdwa v82, v18 dst_sel:WORD_1 dst_unused:UNUSED_PRESERVE src0_sel:WORD_1
	v_exp_f16_sdwa v83, v19 dst_sel:WORD_1 dst_unused:UNUSED_PRESERVE src0_sel:WORD_1
	v_exp_f16_sdwa v84, v20 dst_sel:WORD_1 dst_unused:UNUSED_PRESERVE src0_sel:WORD_1
	v_exp_f16_sdwa v85, v21 dst_sel:WORD_1 dst_unused:UNUSED_PRESERVE src0_sel:WORD_1
	v_pk_add_f16 v31, v31, v79 neg_lo:[0,1] neg_hi:[0,1]
	v_pk_add_f16 v18, v82, 0
	v_pk_add_f16 v19, v83, 0
	v_pk_add_f16 v20, v84, 0
	v_pk_add_f16 v21, v85, 0
	v_pk_fma_f16 v6, v6, v82, 0
	v_pk_fma_f16 v7, v7, v83, 0
	v_pk_fma_f16 v8, v8, v84, 0
	v_pk_fma_f16 v9, v9, v85, 0
	v_pk_add_f16 v32, v32, v80 neg_lo:[0,1] neg_hi:[0,1]
	v_pk_add_f16 v33, v33, v81 neg_lo:[0,1] neg_hi:[0,1]
	v_exp_f16_sdwa v82, v30 dst_sel:WORD_0 dst_unused:UNUSED_PAD src0_sel:WORD_0
	v_exp_f16_sdwa v83, v31 dst_sel:WORD_0 dst_unused:UNUSED_PAD src0_sel:WORD_0
	v_exp_f16_sdwa v84, v32 dst_sel:WORD_0 dst_unused:UNUSED_PAD src0_sel:WORD_0
	v_exp_f16_sdwa v85, v33 dst_sel:WORD_0 dst_unused:UNUSED_PAD src0_sel:WORD_0
	v_exp_f16_sdwa v82, v30 dst_sel:WORD_1 dst_unused:UNUSED_PRESERVE src0_sel:WORD_1
	v_exp_f16_sdwa v83, v31 dst_sel:WORD_1 dst_unused:UNUSED_PRESERVE src0_sel:WORD_1
	v_exp_f16_sdwa v84, v32 dst_sel:WORD_1 dst_unused:UNUSED_PRESERVE src0_sel:WORD_1
	v_exp_f16_sdwa v85, v33 dst_sel:WORD_1 dst_unused:UNUSED_PRESERVE src0_sel:WORD_1
	s_nop 0
	v_pk_add_f16 v21, v21, v85
	v_pk_add_f16 v20, v20, v84
	v_pk_add_f16 v19, v19, v83
	v_pk_add_f16 v18, v18, v82
	v_pk_fma_f16 v9, v13, v85, v9
	v_pk_fma_f16 v8, v12, v84, v8
	v_pk_fma_f16 v7, v11, v83, v7
	v_pk_fma_f16 v6, v10, v82, v6
	v_pk_add_f16 v10, v34, v78 neg_lo:[0,1] neg_hi:[0,1]
	v_pk_add_f16 v11, v35, v79 neg_lo:[0,1] neg_hi:[0,1]
	v_pk_add_f16 v12, v36, v80 neg_lo:[0,1] neg_hi:[0,1]
	v_pk_add_f16 v13, v37, v81 neg_lo:[0,1] neg_hi:[0,1]
	v_exp_f16_sdwa v30, v10 dst_sel:WORD_0 dst_unused:UNUSED_PAD src0_sel:WORD_0
	v_exp_f16_sdwa v31, v11 dst_sel:WORD_0 dst_unused:UNUSED_PAD src0_sel:WORD_0
	v_exp_f16_sdwa v32, v12 dst_sel:WORD_0 dst_unused:UNUSED_PAD src0_sel:WORD_0
	v_exp_f16_sdwa v33, v13 dst_sel:WORD_0 dst_unused:UNUSED_PAD src0_sel:WORD_0
	v_exp_f16_sdwa v30, v10 dst_sel:WORD_1 dst_unused:UNUSED_PRESERVE src0_sel:WORD_1
	v_exp_f16_sdwa v31, v11 dst_sel:WORD_1 dst_unused:UNUSED_PRESERVE src0_sel:WORD_1
	v_exp_f16_sdwa v32, v12 dst_sel:WORD_1 dst_unused:UNUSED_PRESERVE src0_sel:WORD_1
	v_exp_f16_sdwa v33, v13 dst_sel:WORD_1 dst_unused:UNUSED_PRESERVE src0_sel:WORD_1
	v_pk_add_f16 v10, v18, v30
	v_pk_add_f16 v11, v19, v31
	v_pk_add_f16 v12, v20, v32
	v_pk_add_f16 v13, v21, v33
	v_pk_fma_f16 v6, v14, v30, v6
	v_pk_fma_f16 v7, v15, v31, v7
	v_pk_fma_f16 v8, v16, v32, v8
	v_pk_fma_f16 v9, v17, v33, v9
	v_pk_add_f16 v14, v53, v78 neg_lo:[0,1] neg_hi:[0,1]
	v_pk_add_f16 v15, v52, v79 neg_lo:[0,1] neg_hi:[0,1]
	v_pk_add_f16 v16, v51, v80 neg_lo:[0,1] neg_hi:[0,1]
	v_pk_add_f16 v17, v50, v81 neg_lo:[0,1] neg_hi:[0,1]
	v_exp_f16_sdwa v18, v14 dst_sel:WORD_0 dst_unused:UNUSED_PAD src0_sel:WORD_0
	v_exp_f16_sdwa v19, v15 dst_sel:WORD_0 dst_unused:UNUSED_PAD src0_sel:WORD_0
	v_exp_f16_sdwa v20, v16 dst_sel:WORD_0 dst_unused:UNUSED_PAD src0_sel:WORD_0
	v_exp_f16_sdwa v21, v17 dst_sel:WORD_0 dst_unused:UNUSED_PAD src0_sel:WORD_0
	v_exp_f16_sdwa v18, v14 dst_sel:WORD_1 dst_unused:UNUSED_PRESERVE src0_sel:WORD_1
	v_exp_f16_sdwa v19, v15 dst_sel:WORD_1 dst_unused:UNUSED_PRESERVE src0_sel:WORD_1
	v_exp_f16_sdwa v20, v16 dst_sel:WORD_1 dst_unused:UNUSED_PRESERVE src0_sel:WORD_1
	v_exp_f16_sdwa v21, v17 dst_sel:WORD_1 dst_unused:UNUSED_PRESERVE src0_sel:WORD_1
	v_pk_add_f16 v14, v57, v78 neg_lo:[0,1] neg_hi:[0,1]
	v_pk_add_f16 v13, v13, v21
	v_pk_add_f16 v12, v12, v20
	v_pk_add_f16 v11, v11, v19
	v_pk_add_f16 v10, v10, v18
	v_pk_fma_f16 v9, v29, v21, v9
	v_pk_fma_f16 v8, v28, v20, v8
	v_pk_fma_f16 v7, v27, v19, v7
	v_pk_fma_f16 v6, v26, v18, v6
	v_pk_add_f16 v15, v56, v79 neg_lo:[0,1] neg_hi:[0,1]
	v_pk_add_f16 v16, v55, v80 neg_lo:[0,1] neg_hi:[0,1]
	v_pk_add_f16 v17, v54, v81 neg_lo:[0,1] neg_hi:[0,1]
	v_exp_f16_sdwa v18, v14 dst_sel:WORD_0 dst_unused:UNUSED_PAD src0_sel:WORD_0
	v_exp_f16_sdwa v19, v15 dst_sel:WORD_0 dst_unused:UNUSED_PAD src0_sel:WORD_0
	v_exp_f16_sdwa v20, v16 dst_sel:WORD_0 dst_unused:UNUSED_PAD src0_sel:WORD_0
	v_exp_f16_sdwa v21, v17 dst_sel:WORD_0 dst_unused:UNUSED_PAD src0_sel:WORD_0
	v_exp_f16_sdwa v18, v14 dst_sel:WORD_1 dst_unused:UNUSED_PRESERVE src0_sel:WORD_1
	v_exp_f16_sdwa v19, v15 dst_sel:WORD_1 dst_unused:UNUSED_PRESERVE src0_sel:WORD_1
	v_exp_f16_sdwa v20, v16 dst_sel:WORD_1 dst_unused:UNUSED_PRESERVE src0_sel:WORD_1
	v_exp_f16_sdwa v21, v17 dst_sel:WORD_1 dst_unused:UNUSED_PRESERVE src0_sel:WORD_1
	v_pk_add_f16 v14, v42, v78 neg_lo:[0,1] neg_hi:[0,1]
	v_pk_add_f16 v10, v10, v18
	v_pk_add_f16 v11, v11, v19
	v_pk_add_f16 v12, v12, v20
	v_pk_add_f16 v13, v13, v21
	v_pk_fma_f16 v6, v38, v18, v6
	v_pk_fma_f16 v7, v39, v19, v7
	v_pk_fma_f16 v8, v40, v20, v8
	v_pk_fma_f16 v9, v41, v21, v9
	v_pk_add_f16 v15, v43, v79 neg_lo:[0,1] neg_hi:[0,1]
	v_pk_add_f16 v16, v44, v80 neg_lo:[0,1] neg_hi:[0,1]
	v_pk_add_f16 v17, v45, v81 neg_lo:[0,1] neg_hi:[0,1]
	v_exp_f16_sdwa v18, v14 dst_sel:WORD_0 dst_unused:UNUSED_PAD src0_sel:WORD_0
	v_exp_f16_sdwa v19, v15 dst_sel:WORD_0 dst_unused:UNUSED_PAD src0_sel:WORD_0
	v_exp_f16_sdwa v20, v16 dst_sel:WORD_0 dst_unused:UNUSED_PAD src0_sel:WORD_0
	v_exp_f16_sdwa v21, v17 dst_sel:WORD_0 dst_unused:UNUSED_PAD src0_sel:WORD_0
	v_exp_f16_sdwa v18, v14 dst_sel:WORD_1 dst_unused:UNUSED_PRESERVE src0_sel:WORD_1
	v_exp_f16_sdwa v19, v15 dst_sel:WORD_1 dst_unused:UNUSED_PRESERVE src0_sel:WORD_1
	v_exp_f16_sdwa v20, v16 dst_sel:WORD_1 dst_unused:UNUSED_PRESERVE src0_sel:WORD_1
	v_exp_f16_sdwa v21, v17 dst_sel:WORD_1 dst_unused:UNUSED_PRESERVE src0_sel:WORD_1
	v_pk_add_f16 v14, v69, v78 neg_lo:[0,1] neg_hi:[0,1]
	v_pk_add_f16 v13, v13, v21
	v_pk_add_f16 v12, v12, v20
	v_pk_add_f16 v11, v11, v19
	v_pk_add_f16 v10, v10, v18
	v_pk_fma_f16 v9, v61, v21, v9
	v_pk_fma_f16 v8, v60, v20, v8
	v_pk_fma_f16 v7, v59, v19, v7
	v_pk_fma_f16 v6, v58, v18, v6
	v_pk_add_f16 v15, v68, v79 neg_lo:[0,1] neg_hi:[0,1]
	v_pk_add_f16 v16, v67, v80 neg_lo:[0,1] neg_hi:[0,1]
	v_pk_add_f16 v17, v66, v81 neg_lo:[0,1] neg_hi:[0,1]
	v_exp_f16_sdwa v18, v14 dst_sel:WORD_0 dst_unused:UNUSED_PAD src0_sel:WORD_0
	v_exp_f16_sdwa v19, v15 dst_sel:WORD_0 dst_unused:UNUSED_PAD src0_sel:WORD_0
	v_exp_f16_sdwa v20, v16 dst_sel:WORD_0 dst_unused:UNUSED_PAD src0_sel:WORD_0
	v_exp_f16_sdwa v21, v17 dst_sel:WORD_0 dst_unused:UNUSED_PAD src0_sel:WORD_0
	v_exp_f16_sdwa v18, v14 dst_sel:WORD_1 dst_unused:UNUSED_PRESERVE src0_sel:WORD_1
	v_exp_f16_sdwa v19, v15 dst_sel:WORD_1 dst_unused:UNUSED_PRESERVE src0_sel:WORD_1
	v_exp_f16_sdwa v20, v16 dst_sel:WORD_1 dst_unused:UNUSED_PRESERVE src0_sel:WORD_1
	v_exp_f16_sdwa v21, v17 dst_sel:WORD_1 dst_unused:UNUSED_PRESERVE src0_sel:WORD_1
	v_pk_add_f16 v10, v10, v18
	v_pk_add_f16 v11, v11, v19
	v_pk_add_f16 v12, v12, v20
	v_pk_add_f16 v13, v13, v21
	v_pk_fma_f16 v14, v70, v18, v6
	v_pk_fma_f16 v15, v71, v19, v7
	v_pk_fma_f16 v16, v72, v20, v8
	v_pk_fma_f16 v17, v73, v21, v9
	v_pk_add_f16 v6, v77, v78 neg_lo:[0,1] neg_hi:[0,1]
	v_pk_add_f16 v7, v76, v79 neg_lo:[0,1] neg_hi:[0,1]
	v_pk_add_f16 v8, v75, v80 neg_lo:[0,1] neg_hi:[0,1]
	v_pk_add_f16 v9, v74, v81 neg_lo:[0,1] neg_hi:[0,1]
	v_exp_f16_sdwa v18, v6 dst_sel:WORD_0 dst_unused:UNUSED_PAD src0_sel:WORD_0
	v_exp_f16_sdwa v19, v7 dst_sel:WORD_0 dst_unused:UNUSED_PAD src0_sel:WORD_0
	v_exp_f16_sdwa v20, v8 dst_sel:WORD_0 dst_unused:UNUSED_PAD src0_sel:WORD_0
	v_exp_f16_sdwa v21, v9 dst_sel:WORD_0 dst_unused:UNUSED_PAD src0_sel:WORD_0
	v_exp_f16_sdwa v18, v6 dst_sel:WORD_1 dst_unused:UNUSED_PRESERVE src0_sel:WORD_1
	v_exp_f16_sdwa v19, v7 dst_sel:WORD_1 dst_unused:UNUSED_PRESERVE src0_sel:WORD_1
	v_exp_f16_sdwa v20, v8 dst_sel:WORD_1 dst_unused:UNUSED_PRESERVE src0_sel:WORD_1
	v_exp_f16_sdwa v21, v9 dst_sel:WORD_1 dst_unused:UNUSED_PRESERVE src0_sel:WORD_1
	s_nop 0
	v_pk_add_f16 v9, v13, v21
	v_pk_add_f16 v8, v12, v20
	v_pk_add_f16 v7, v11, v19
	v_pk_add_f16 v6, v10, v18
	v_pk_fma_f16 v13, v93, v21, v17
	v_pk_fma_f16 v12, v92, v20, v16
	v_pk_fma_f16 v11, v91, v19, v15
	v_pk_fma_f16 v10, v90, v18, v14
	v_pk_add_f16 v18, v46, v78 neg_lo:[0,1] neg_hi:[0,1]
	v_pk_add_f16 v19, v47, v79 neg_lo:[0,1] neg_hi:[0,1]
	v_pk_add_f16 v20, v48, v80 neg_lo:[0,1] neg_hi:[0,1]
	v_pk_add_f16 v21, v49, v81 neg_lo:[0,1] neg_hi:[0,1]
	v_exp_f16_sdwa v14, v18 dst_sel:WORD_0 dst_unused:UNUSED_PAD src0_sel:WORD_0
	v_exp_f16_sdwa v17, v19 dst_sel:WORD_0 dst_unused:UNUSED_PAD src0_sel:WORD_0
	v_exp_f16_sdwa v15, v20 dst_sel:WORD_0 dst_unused:UNUSED_PAD src0_sel:WORD_0
	v_exp_f16_sdwa v16, v21 dst_sel:WORD_0 dst_unused:UNUSED_PAD src0_sel:WORD_0
	v_exp_f16_sdwa v14, v18 dst_sel:WORD_1 dst_unused:UNUSED_PRESERVE src0_sel:WORD_1
	v_exp_f16_sdwa v17, v19 dst_sel:WORD_1 dst_unused:UNUSED_PRESERVE src0_sel:WORD_1
	v_exp_f16_sdwa v15, v20 dst_sel:WORD_1 dst_unused:UNUSED_PRESERVE src0_sel:WORD_1
	v_exp_f16_sdwa v16, v21 dst_sel:WORD_1 dst_unused:UNUSED_PRESERVE src0_sel:WORD_1
	s_nop 0
.LBB3_6:
	v_pk_add_f16 v9, v9, v16
	v_pk_add_f16 v8, v8, v15
	v_pk_fma_f16 v4, v4, v15, v12
	v_rcp_f16_e32 v12, v9
	v_rcp_f16_sdwa v9, v9 dst_sel:DWORD dst_unused:UNUSED_PAD src0_sel:WORD_1
	v_pk_add_f16 v6, v6, v14
	v_pk_fma_f16 v5, v5, v16, v13
	v_rcp_f16_e32 v13, v8
	v_rcp_f16_sdwa v8, v8 dst_sel:DWORD dst_unused:UNUSED_PAD src0_sel:WORD_1
	v_pk_add_f16 v7, v7, v17
	v_pk_fma_f16 v2, v2, v14, v10
	v_rcp_f16_e32 v10, v6
	v_rcp_f16_sdwa v6, v6 dst_sel:DWORD dst_unused:UNUSED_PAD src0_sel:WORD_1
	v_pk_fma_f16 v3, v3, v17, v11
	v_rcp_f16_e32 v11, v7
	v_rcp_f16_sdwa v7, v7 dst_sel:DWORD dst_unused:UNUSED_PAD src0_sel:WORD_1
	v_pack_b32_f16 v9, v12, v9
	v_pk_mul_f16 v9, v5, v9
	v_pack_b32_f16 v5, v13, v8
	v_pk_mul_f16 v8, v4, v5
	v_pack_b32_f16 v4, v10, v6
	v_pk_mul_f16 v6, v2, v4
	v_pack_b32_f16 v2, v11, v7
	v_pk_mul_f16 v7, v3, v2
	v_pk_max_f16 v2, v113, v113
	v_add_u32_e32 v10, v168, v160
	v_pk_max_f16 v5, v2, 0
	v_pk_max_f16 v2, v112, v112
	s_add_i32 s10, s10, -1
	v_pk_max_f16 v4, v2, 0
	v_pk_max_f16 v2, v111, v111
	s_add_i32 s33, s33, 8
	v_pk_max_f16 v3, v2, 0
	v_pk_max_f16 v2, v110, v110
	v_add_u32_e32 v168, 0x8000, v168
	v_pk_max_f16 v2, v2, 0
	ds_write_b128 v10, v[2:5]
	v_pk_max_f16 v2, v65, v65
	v_bitop3_b32 v10, v166, v159, 15 bitop3:0x6c
	v_pk_max_f16 v5, v2, 0
	v_pk_max_f16 v2, v64, v64
	v_lshlrev_b32_e32 v10, 4, v10
	v_pk_max_f16 v4, v2, 0
	v_pk_max_f16 v2, v63, v63
	v_add3_u32 v10, v160, v10, v167
	v_pk_max_f16 v3, v2, 0
	v_pk_max_f16 v2, v62, v62
	v_add_u32_e32 v166, 64, v166
	v_pk_max_f16 v2, v2, 0
	ds_write_b128 v10, v[2:5]
	v_pk_max_f16 v2, v25, v25
	v_add_u32_e32 v10, v170, v160
	v_pk_max_f16 v5, v2, 0
	v_pk_max_f16 v2, v24, v24
	v_add_u32_e32 v170, 0x8000, v170
	v_pk_max_f16 v4, v2, 0
	v_pk_max_f16 v2, v23, v23
	v_add_u32_e32 v167, 0x8000, v167
	v_pk_max_f16 v3, v2, 0
	v_pk_max_f16 v2, v22, v22
	s_cmp_eq_u32 s10, 0
	v_pk_max_f16 v2, v2, 0
	ds_write_b128 v10, v[2:5]
	v_pk_max_f16 v3, v7, 0
	v_pk_max_f16 v2, v6, 0
	v_pk_max_f16 v4, v8, 0
	v_pk_max_f16 v5, v9, 0
	v_add_u32_e32 v6, v169, v163
	v_add_u32_e32 v163, 0x8000, v163
	v_add_u32_e32 v171, 0x3000, v171
	ds_write_b128 v6, v[2:5]
	s_cbranch_scc1 .LBB3_82
.LBB3_7:
	v_add_u32_e32 v182, s33, v161
	v_add_u32_e32 v181, -1, v182
	v_or_b32_e32 v2, v181, v164
	v_add_u32_e32 v180, 0x18400, v171
	v_cmp_gt_u32_e64 s[0:1], 64, v2
	s_mov_b64 s[4:5], -1
	s_and_b64 vcc, exec, s[24:25]
	s_cbranch_vccz .LBB3_45
	s_load_dwordx2 s[4:5], s[22:23], 0x20
	s_waitcnt lgkmcnt(0)
	s_load_dwordx2 s[26:27], s[4:5], 0x0
	s_load_dword s34, s[4:5], 0x8
	v_cmp_lt_u32_e64 s[64:65], 0, v182
	v_cmp_gt_u32_e64 s[66:67], 63, v182
	v_cmp_lt_u32_e64 s[68:69], 0, v162
	v_cmp_gt_u32_e64 s[70:71], 60, v162
	buffer_load_dwordx4 v[186:189], v180, s[16:19], 0 offen
	s_and_b64 s[72:73], s[68:69], s[64:65]
	s_and_b64 s[74:75], s[68:69], s[66:67]
	s_and_b64 s[76:77], s[70:71], s[64:65]
	s_and_b64 s[78:79], s[70:71], s[66:67]
	v_mov_b32_e32 v110, v172
	v_mov_b32_e32 v111, v174
	v_mov_b32_e32 v112, v176
	v_mov_b32_e32 v113, v178
	v_mov_b32_e32 v70, v173
	v_mov_b32_e32 v71, v175
	v_mov_b32_e32 v72, v177
	v_mov_b32_e32 v73, v179
	v_mov_b32_e32 v126, v172
	v_mov_b32_e32 v127, v174
	v_mov_b32_e32 v128, v176
	v_mov_b32_e32 v129, v178
	v_mov_b32_e32 v98, v173
	v_mov_b32_e32 v99, v175
	v_mov_b32_e32 v100, v177
	v_mov_b32_e32 v101, v179
	v_mov_b32_e32 v134, v172
	v_mov_b32_e32 v135, v174
	v_mov_b32_e32 v136, v176
	v_mov_b32_e32 v137, v178
	v_mov_b32_e32 v114, v173
	v_mov_b32_e32 v115, v175
	v_mov_b32_e32 v116, v177
	v_mov_b32_e32 v117, v179
	v_mov_b32_e32 v82, v172
	v_mov_b32_e32 v83, v174
	v_mov_b32_e32 v84, v176
	v_mov_b32_e32 v85, v178
	v_mov_b32_e32 v42, v173
	v_mov_b32_e32 v43, v175
	v_mov_b32_e32 v44, v177
	v_mov_b32_e32 v45, v179
	v_mov_b32_e32 v122, v172
	v_mov_b32_e32 v123, v174
	v_mov_b32_e32 v124, v176
	v_mov_b32_e32 v125, v178
	v_mov_b32_e32 v86, v173
	v_mov_b32_e32 v87, v175
	v_mov_b32_e32 v88, v177
	v_mov_b32_e32 v89, v179
	v_mov_b32_e32 v50, v172
	v_mov_b32_e32 v51, v174
	v_mov_b32_e32 v52, v176
	v_mov_b32_e32 v53, v178
	v_mov_b32_e32 v22, v173
	v_mov_b32_e32 v23, v175
	v_mov_b32_e32 v24, v177
	v_mov_b32_e32 v25, v179
	v_mov_b32_e32 v94, v172
	v_mov_b32_e32 v95, v174
	v_mov_b32_e32 v96, v176
	v_mov_b32_e32 v97, v178
	v_mov_b32_e32 v46, v173
	v_mov_b32_e32 v47, v175
	v_mov_b32_e32 v48, v177
	v_mov_b32_e32 v49, v179
	v_mov_b32_e32 v18, v172
	v_mov_b32_e32 v19, v174
	v_mov_b32_e32 v20, v176
	v_mov_b32_e32 v21, v178
	v_mov_b32_e32 v6, v173
	v_mov_b32_e32 v7, v175
	v_mov_b32_e32 v8, v177
	v_mov_b32_e32 v9, v179
	v_mov_b32_e32 v54, v172
	v_mov_b32_e32 v55, v174
	v_mov_b32_e32 v56, v176
	v_mov_b32_e32 v57, v178
	v_mov_b32_e32 v14, v173
	v_mov_b32_e32 v15, v175
	v_mov_b32_e32 v16, v177
	v_mov_b32_e32 v17, v179
	v_mov_b32_e32 v74, v172
	v_mov_b32_e32 v75, v174
	v_mov_b32_e32 v76, v176
	v_mov_b32_e32 v77, v178
	v_mov_b32_e32 v26, v173
	v_mov_b32_e32 v27, v175
	v_mov_b32_e32 v28, v177
	v_mov_b32_e32 v29, v179
	v_mov_b32_e32 v118, v172
	v_mov_b32_e32 v119, v174
	v_mov_b32_e32 v120, v176
	v_mov_b32_e32 v121, v178
	v_mov_b32_e32 v58, v173
	v_mov_b32_e32 v59, v175
	v_mov_b32_e32 v60, v177
	v_mov_b32_e32 v61, v179
	v_mov_b32_e32 v130, v172
	v_mov_b32_e32 v131, v174
	v_mov_b32_e32 v132, v176
	v_mov_b32_e32 v133, v178
	v_mov_b32_e32 v78, v173
	v_mov_b32_e32 v79, v175
	v_mov_b32_e32 v80, v177
	v_mov_b32_e32 v81, v179
	v_mov_b32_e32 v138, v172
	v_mov_b32_e32 v139, v174
	v_mov_b32_e32 v140, v176
	v_mov_b32_e32 v141, v178
	v_mov_b32_e32 v90, v173
	v_mov_b32_e32 v91, v175
	v_mov_b32_e32 v92, v177
	v_mov_b32_e32 v93, v179
	v_mov_b32_e32 v142, v172
	v_mov_b32_e32 v143, v174
	v_mov_b32_e32 v144, v176
	v_mov_b32_e32 v145, v178
	v_mov_b32_e32 v2, v173
	v_mov_b32_e32 v3, v175
	v_mov_b32_e32 v4, v177
	v_mov_b32_e32 v5, v179
	v_add_u32_e32 v249, 0xfffe7c00, v180
	v_add_u32_e32 v250, 0xfffe8000, v180
	s_mov_b64 exec, s[72:73]
	buffer_load_dwordx4 v[110:113], v249, s[16:19], 0 offen
	buffer_load_dwordx4 v[70:73], v249, s[16:19], 0 offen offset:512
	s_mov_b64 exec, -1
	s_mov_b64 exec, s[68:69]
	buffer_load_dwordx4 v[126:129], v250, s[16:19], 0 offen offset:512
	buffer_load_dwordx4 v[98:101], v250, s[16:19], 0 offen offset:1024
	s_mov_b64 exec, -1
	s_mov_b64 exec, s[74:75]
	buffer_load_dwordx4 v[134:137], v250, s[16:19], 0 offen offset:2048
	buffer_load_dwordx4 v[114:117], v250, s[16:19], 0 offen offset:2560
	s_mov_b64 exec, -1
	v_add_u32_e32 v249, 0xfffffc00, v180
	s_mov_b64 exec, s[64:65]
	buffer_load_dwordx4 v[82:85], v249, s[16:19], 0 offen
	buffer_load_dwordx4 v[42:45], v249, s[16:19], 0 offen offset:512
	s_mov_b64 exec, -1
	buffer_load_dwordx4 v[106:109], v180, s[16:19], 0 offen offset:512
	buffer_load_dwordx4 v[62:65], v180, s[16:19], 0 offen offset:1024
	s_mov_b64 exec, s[66:67]
	buffer_load_dwordx4 v[122:125], v180, s[16:19], 0 offen offset:2048
	buffer_load_dwordx4 v[86:89], v180, s[16:19], 0 offen offset:2560
	s_mov_b64 exec, -1
	v_add_u32_e32 v249, 0x17c00, v180
	v_add_u32_e32 v250, 0x18000, v180
	s_mov_b64 exec, s[64:65]
	buffer_load_dwordx4 v[50:53], v249, s[16:19], 0 offen
	buffer_load_dwordx4 v[22:25], v249, s[16:19], 0 offen offset:512
	s_mov_b64 exec, -1
	buffer_load_dwordx4 v[66:69], v250, s[16:19], 0 offen offset:512
	buffer_load_dwordx4 v[30:33], v250, s[16:19], 0 offen offset:1024
	s_mov_b64 exec, s[66:67]
	buffer_load_dwordx4 v[94:97], v250, s[16:19], 0 offen offset:2048
	buffer_load_dwordx4 v[46:49], v250, s[16:19], 0 offen offset:2560
	s_mov_b64 exec, -1
	v_add_u32_e32 v249, 0x18000, v180
	buffer_load_dwordx4 v[154:157], v249, s[16:19], 0 offen
	v_add_u32_e32 v250, 0x30000, v180
	buffer_load_dwordx4 v[150:153], v250, s[16:19], 0 offen
	v_add_u32_e32 v249, 0x48000, v180
	buffer_load_dwordx4 v[146:149], v249, s[16:19], 0 offen
	v_add_u32_e32 v249, 0x2fc00, v180
	v_add_u32_e32 v250, 0x30000, v180
	v_add_u32_e32 v251, 0x47c00, v180
	v_add_u32_e32 v252, 0x48000, v180
	v_add_u32_e32 v253, 0x5fc00, v180
	v_add_u32_e32 v254, 0x60000, v180
	s_waitcnt lgkmcnt(0)
	v_cvt_f16_f32_e32 v183, s27
	v_cvt_f16_f32_e32 v185, s26
	v_cvt_f16_f32_e32 v184, s34
	s_mov_b64 s[4:5], 0
	s_waitcnt vmcnt(3)
	v_pk_mul_f16 v193, v185, v189 op_sel_hi:[0,1]
	v_pk_mul_f16 v197, v183, v189 op_sel_hi:[0,1]
	v_pk_mul_f16 v201, v184, v189 op_sel_hi:[0,1]
	v_pk_mul_f16 v190, v185, v186 op_sel_hi:[0,1]
	v_pk_mul_f16 v191, v185, v187 op_sel_hi:[0,1]
	v_pk_mul_f16 v192, v185, v188 op_sel_hi:[0,1]
	v_pk_mul_f16 v194, v183, v186 op_sel_hi:[0,1]
	s_mov_b64 exec, s[64:65]
	buffer_load_dwordx4 v[18:21], v249, s[16:19], 0 offen
	buffer_load_dwordx4 v[6:9], v249, s[16:19], 0 offen offset:512
	s_mov_b64 exec, -1
	v_pk_mul_f16 v195, v183, v187 op_sel_hi:[0,1]
	v_pk_mul_f16 v196, v183, v188 op_sel_hi:[0,1]
	v_pk_mul_f16 v198, v184, v186 op_sel_hi:[0,1]
	v_pk_mul_f16 v199, v184, v187 op_sel_hi:[0,1]
	v_pk_mul_f16 v200, v184, v188 op_sel_hi:[0,1]
	v_pk_fma_f16 v113, v113, v189, v193
	v_pk_fma_f16 v129, v129, v189, v197
	v_pk_fma_f16 v137, v137, v189, v201
	v_pk_fma_f16 v202, v85, v189, v193
	v_pk_fma_f16 v206, v109, v189, v197
	v_pk_fma_f16 v210, v125, v189, v201
	v_pk_fma_f16 v193, v53, v189, v193
	v_pk_fma_f16 v197, v69, v189, v197
	buffer_load_dwordx4 v[34:37], v250, s[16:19], 0 offen offset:512
	buffer_load_dwordx4 v[10:13], v250, s[16:19], 0 offen offset:1024
	v_pk_fma_f16 v189, v97, v189, v201
	v_pk_maximum3_f16 v201, v113, v129, v137
	v_pk_fma_f16 v112, v112, v188, v192
	v_pk_fma_f16 v111, v111, v187, v191
	v_pk_fma_f16 v110, v110, v186, v190
	v_pk_fma_f16 v128, v128, v188, v196
	v_pk_fma_f16 v127, v127, v187, v195
	v_pk_fma_f16 v126, v126, v186, v194
	v_pk_fma_f16 v136, v136, v188, v200
	v_pk_fma_f16 v135, v135, v187, v199
	v_pk_fma_f16 v134, v134, v186, v198
	v_pk_fma_f16 v203, v84, v188, v192
	v_pk_fma_f16 v204, v83, v187, v191
	v_pk_fma_f16 v205, v82, v186, v190
	v_pk_fma_f16 v207, v108, v188, v196
	v_pk_fma_f16 v208, v107, v187, v195
	s_mov_b64 exec, s[66:67]
	buffer_load_dwordx4 v[54:57], v250, s[16:19], 0 offen offset:2048
	buffer_load_dwordx4 v[14:17], v250, s[16:19], 0 offen offset:2560
	s_mov_b64 exec, -1
	v_pk_fma_f16 v209, v106, v186, v194
	v_pk_fma_f16 v211, v124, v188, v200
	v_pk_fma_f16 v212, v123, v187, v199
	v_pk_fma_f16 v213, v122, v186, v198
	v_pk_fma_f16 v192, v52, v188, v192
	v_pk_fma_f16 v191, v51, v187, v191
	v_pk_fma_f16 v190, v50, v186, v190
	v_pk_fma_f16 v196, v68, v188, v196
	v_pk_fma_f16 v195, v67, v187, v195
	v_pk_fma_f16 v194, v66, v186, v194
	v_pk_fma_f16 v188, v96, v188, v200
	v_pk_fma_f16 v187, v95, v187, v199
	v_pk_fma_f16 v186, v94, v186, v198
	v_pk_maximum3_f16 v198, v110, v126, v134
	v_pk_maximum3_f16 v199, v111, v127, v135
	v_pk_maximum3_f16 v200, v112, v128, v136
	v_pk_maximum3_f16 v217, v202, v206, v210
	v_pk_maximum3_f16 v221, v193, v197, v189
	v_pk_maximum3_f16 v214, v205, v209, v213
	v_pk_maximum3_f16 v215, v204, v208, v212
	v_pk_maximum3_f16 v216, v203, v207, v211
	v_pk_maximum3_f16 v218, v190, v194, v186
	v_pk_maximum3_f16 v219, v191, v195, v187
	v_pk_maximum3_f16 v201, v201, v217, v221
	v_pk_maximum3_f16 v220, v192, v196, v188
	v_pk_maximum3_f16 v198, v198, v214, v218
	v_pk_maximum3_f16 v199, v199, v215, v219
	v_pk_maximum3_f16 v200, v200, v216, v220
	v_pk_add_f16 v113, v113, v201 neg_lo:[0,1] neg_hi:[0,1]
	s_mov_b64 exec, s[64:65]
	buffer_load_dwordx4 v[74:77], v251, s[16:19], 0 offen
	buffer_load_dwordx4 v[26:29], v251, s[16:19], 0 offen offset:512
	s_mov_b64 exec, -1
	v_pk_add_f16 v110, v110, v198 neg_lo:[0,1] neg_hi:[0,1]
	v_pk_add_f16 v111, v111, v199 neg_lo:[0,1] neg_hi:[0,1]
	v_pk_add_f16 v112, v112, v200 neg_lo:[0,1] neg_hi:[0,1]
	v_pk_add_f16 v126, v126, v198 neg_lo:[0,1] neg_hi:[0,1]
	v_exp_f16_sdwa v214, v110 dst_sel:WORD_0 dst_unused:UNUSED_PAD src0_sel:WORD_0
	v_exp_f16_sdwa v215, v111 dst_sel:WORD_0 dst_unused:UNUSED_PAD src0_sel:WORD_0
	v_exp_f16_sdwa v216, v112 dst_sel:WORD_0 dst_unused:UNUSED_PAD src0_sel:WORD_0
	v_exp_f16_sdwa v217, v113 dst_sel:WORD_0 dst_unused:UNUSED_PAD src0_sel:WORD_0
	v_exp_f16_sdwa v214, v110 dst_sel:WORD_1 dst_unused:UNUSED_PRESERVE src0_sel:WORD_1
	v_exp_f16_sdwa v215, v111 dst_sel:WORD_1 dst_unused:UNUSED_PRESERVE src0_sel:WORD_1
	v_exp_f16_sdwa v216, v112 dst_sel:WORD_1 dst_unused:UNUSED_PRESERVE src0_sel:WORD_1
	v_exp_f16_sdwa v217, v113 dst_sel:WORD_1 dst_unused:UNUSED_PRESERVE src0_sel:WORD_1
	v_pk_add_f16 v127, v127, v199 neg_lo:[0,1] neg_hi:[0,1]
	v_pk_add_f16 v113, v214, 0
	v_pk_fma_f16 v73, v73, v217, 0
	v_pk_add_f16 v110, v217, 0
	v_pk_add_f16 v111, v216, 0
	v_pk_add_f16 v112, v215, 0
	v_pk_fma_f16 v72, v72, v216, 0
	v_pk_fma_f16 v71, v71, v215, 0
	v_pk_fma_f16 v70, v70, v214, 0
	v_pk_add_f16 v128, v128, v200 neg_lo:[0,1] neg_hi:[0,1]
	buffer_load_dwordx4 v[102:105], v252, s[16:19], 0 offen offset:512
	buffer_load_dwordx4 v[38:41], v252, s[16:19], 0 offen offset:1024
	v_pk_add_f16 v129, v129, v201 neg_lo:[0,1] neg_hi:[0,1]
	v_exp_f16_sdwa v214, v126 dst_sel:WORD_0 dst_unused:UNUSED_PAD src0_sel:WORD_0
	v_exp_f16_sdwa v215, v127 dst_sel:WORD_0 dst_unused:UNUSED_PAD src0_sel:WORD_0
	v_exp_f16_sdwa v216, v128 dst_sel:WORD_0 dst_unused:UNUSED_PAD src0_sel:WORD_0
	v_exp_f16_sdwa v217, v129 dst_sel:WORD_0 dst_unused:UNUSED_PAD src0_sel:WORD_0
	v_exp_f16_sdwa v214, v126 dst_sel:WORD_1 dst_unused:UNUSED_PRESERVE src0_sel:WORD_1
	v_exp_f16_sdwa v215, v127 dst_sel:WORD_1 dst_unused:UNUSED_PRESERVE src0_sel:WORD_1
	v_exp_f16_sdwa v216, v128 dst_sel:WORD_1 dst_unused:UNUSED_PRESERVE src0_sel:WORD_1
	v_exp_f16_sdwa v217, v129 dst_sel:WORD_1 dst_unused:UNUSED_PRESERVE src0_sel:WORD_1
	v_pk_add_f16 v113, v113, v214
	v_pk_fma_f16 v73, v101, v217, v73
	v_pk_add_f16 v101, v137, v201 neg_lo:[0,1] neg_hi:[0,1]
	v_pk_add_f16 v112, v112, v215
	v_pk_add_f16 v111, v111, v216
	v_pk_add_f16 v110, v110, v217
	v_pk_fma_f16 v70, v98, v214, v70
	v_pk_fma_f16 v71, v99, v215, v71
	v_pk_fma_f16 v72, v100, v216, v72
	v_pk_add_f16 v98, v134, v198 neg_lo:[0,1] neg_hi:[0,1]
	v_pk_add_f16 v99, v135, v199 neg_lo:[0,1] neg_hi:[0,1]
	v_pk_add_f16 v100, v136, v200 neg_lo:[0,1] neg_hi:[0,1]
	v_exp_f16_sdwa v126, v98 dst_sel:WORD_0 dst_unused:UNUSED_PAD src0_sel:WORD_0
	v_exp_f16_sdwa v127, v99 dst_sel:WORD_0 dst_unused:UNUSED_PAD src0_sel:WORD_0
	v_exp_f16_sdwa v128, v100 dst_sel:WORD_0 dst_unused:UNUSED_PAD src0_sel:WORD_0
	v_exp_f16_sdwa v129, v101 dst_sel:WORD_0 dst_unused:UNUSED_PAD src0_sel:WORD_0
	v_exp_f16_sdwa v126, v98 dst_sel:WORD_1 dst_unused:UNUSED_PRESERVE src0_sel:WORD_1
	v_exp_f16_sdwa v127, v99 dst_sel:WORD_1 dst_unused:UNUSED_PRESERVE src0_sel:WORD_1
	v_exp_f16_sdwa v128, v100 dst_sel:WORD_1 dst_unused:UNUSED_PRESERVE src0_sel:WORD_1
	v_exp_f16_sdwa v129, v101 dst_sel:WORD_1 dst_unused:UNUSED_PRESERVE src0_sel:WORD_1
	v_pk_add_f16 v101, v113, v126
	v_pk_add_f16 v98, v110, v129
	s_mov_b64 exec, s[66:67]
	buffer_load_dwordx4 v[118:121], v252, s[16:19], 0 offen offset:2048
	buffer_load_dwordx4 v[58:61], v252, s[16:19], 0 offen offset:2560
	s_mov_b64 exec, -1
	v_pk_add_f16 v99, v111, v128
	v_pk_add_f16 v100, v112, v127
	v_pk_fma_f16 v73, v117, v129, v73
	v_pk_fma_f16 v72, v116, v128, v72
	v_pk_fma_f16 v71, v115, v127, v71
	v_pk_fma_f16 v70, v114, v126, v70
	v_pk_add_f16 v110, v205, v198 neg_lo:[0,1] neg_hi:[0,1]
	v_pk_add_f16 v111, v204, v199 neg_lo:[0,1] neg_hi:[0,1]
	v_pk_add_f16 v112, v203, v200 neg_lo:[0,1] neg_hi:[0,1]
	v_pk_add_f16 v113, v202, v201 neg_lo:[0,1] neg_hi:[0,1]
	v_exp_f16_sdwa v114, v110 dst_sel:WORD_0 dst_unused:UNUSED_PAD src0_sel:WORD_0
	v_exp_f16_sdwa v115, v111 dst_sel:WORD_0 dst_unused:UNUSED_PAD src0_sel:WORD_0
	v_exp_f16_sdwa v116, v112 dst_sel:WORD_0 dst_unused:UNUSED_PAD src0_sel:WORD_0
	v_exp_f16_sdwa v117, v113 dst_sel:WORD_0 dst_unused:UNUSED_PAD src0_sel:WORD_0
	v_exp_f16_sdwa v114, v110 dst_sel:WORD_1 dst_unused:UNUSED_PRESERVE src0_sel:WORD_1
	v_exp_f16_sdwa v115, v111 dst_sel:WORD_1 dst_unused:UNUSED_PRESERVE src0_sel:WORD_1
	v_exp_f16_sdwa v116, v112 dst_sel:WORD_1 dst_unused:UNUSED_PRESERVE src0_sel:WORD_1
	v_exp_f16_sdwa v117, v113 dst_sel:WORD_1 dst_unused:UNUSED_PRESERVE src0_sel:WORD_1
	v_pk_add_f16 v110, v209, v198 neg_lo:[0,1] neg_hi:[0,1]
	v_pk_add_f16 v101, v101, v114
	v_pk_add_f16 v100, v100, v115
	v_pk_add_f16 v99, v99, v116
	s_mov_b64 exec, s[76:77]
	buffer_load_dwordx4 v[130:133], v253, s[16:19], 0 offen
	buffer_load_dwordx4 v[78:81], v253, s[16:19], 0 offen offset:512
	s_mov_b64 exec, -1
	v_pk_add_f16 v98, v98, v117
	v_pk_fma_f16 v70, v42, v114, v70
	v_pk_fma_f16 v71, v43, v115, v71
	v_pk_fma_f16 v72, v44, v116, v72
	v_pk_fma_f16 v73, v45, v117, v73
	v_pk_add_f16 v111, v208, v199 neg_lo:[0,1] neg_hi:[0,1]
	v_pk_add_f16 v112, v207, v200 neg_lo:[0,1] neg_hi:[0,1]
	v_pk_add_f16 v113, v206, v201 neg_lo:[0,1] neg_hi:[0,1]
	v_exp_f16_sdwa v114, v110 dst_sel:WORD_0 dst_unused:UNUSED_PAD src0_sel:WORD_0
	v_exp_f16_sdwa v115, v111 dst_sel:WORD_0 dst_unused:UNUSED_PAD src0_sel:WORD_0
	v_exp_f16_sdwa v116, v112 dst_sel:WORD_0 dst_unused:UNUSED_PAD src0_sel:WORD_0
	v_exp_f16_sdwa v117, v113 dst_sel:WORD_0 dst_unused:UNUSED_PAD src0_sel:WORD_0
	v_exp_f16_sdwa v114, v110 dst_sel:WORD_1 dst_unused:UNUSED_PRESERVE src0_sel:WORD_1
	v_exp_f16_sdwa v115, v111 dst_sel:WORD_1 dst_unused:UNUSED_PRESERVE src0_sel:WORD_1
	v_exp_f16_sdwa v116, v112 dst_sel:WORD_1 dst_unused:UNUSED_PRESERVE src0_sel:WORD_1
	v_exp_f16_sdwa v117, v113 dst_sel:WORD_1 dst_unused:UNUSED_PRESERVE src0_sel:WORD_1
	v_pk_add_f16 v110, v213, v198 neg_lo:[0,1] neg_hi:[0,1]
	v_pk_add_f16 v101, v101, v114
	v_pk_add_f16 v98, v98, v117
	v_pk_add_f16 v99, v99, v116
	v_pk_add_f16 v100, v100, v115
	v_pk_fma_f16 v73, v65, v117, v73
	v_pk_fma_f16 v72, v64, v116, v72
	s_mov_b64 exec, s[70:71]
	buffer_load_dwordx4 v[138:141], v254, s[16:19], 0 offen offset:512
	buffer_load_dwordx4 v[90:93], v254, s[16:19], 0 offen offset:1024
	s_mov_b64 exec, -1
	v_pk_fma_f16 v71, v63, v115, v71
	v_pk_fma_f16 v70, v62, v114, v70
	v_pk_add_f16 v111, v212, v199 neg_lo:[0,1] neg_hi:[0,1]
	v_pk_add_f16 v112, v211, v200 neg_lo:[0,1] neg_hi:[0,1]
	v_pk_add_f16 v113, v210, v201 neg_lo:[0,1] neg_hi:[0,1]
	v_exp_f16_sdwa v114, v110 dst_sel:WORD_0 dst_unused:UNUSED_PAD src0_sel:WORD_0
	v_exp_f16_sdwa v115, v111 dst_sel:WORD_0 dst_unused:UNUSED_PAD src0_sel:WORD_0
	v_exp_f16_sdwa v116, v112 dst_sel:WORD_0 dst_unused:UNUSED_PAD src0_sel:WORD_0
	v_exp_f16_sdwa v117, v113 dst_sel:WORD_0 dst_unused:UNUSED_PAD src0_sel:WORD_0
	v_exp_f16_sdwa v114, v110 dst_sel:WORD_1 dst_unused:UNUSED_PRESERVE src0_sel:WORD_1
	v_exp_f16_sdwa v115, v111 dst_sel:WORD_1 dst_unused:UNUSED_PRESERVE src0_sel:WORD_1
	v_exp_f16_sdwa v116, v112 dst_sel:WORD_1 dst_unused:UNUSED_PRESERVE src0_sel:WORD_1
	v_exp_f16_sdwa v117, v113 dst_sel:WORD_1 dst_unused:UNUSED_PRESERVE src0_sel:WORD_1
	v_pk_add_f16 v110, v190, v198 neg_lo:[0,1] neg_hi:[0,1]
	v_pk_add_f16 v101, v101, v114
	v_pk_add_f16 v100, v100, v115
	v_pk_add_f16 v99, v99, v116
	v_pk_add_f16 v98, v98, v117
	v_pk_fma_f16 v70, v86, v114, v70
	v_pk_fma_f16 v71, v87, v115, v71
	v_pk_fma_f16 v72, v88, v116, v72
	v_pk_fma_f16 v73, v89, v117, v73
	s_mov_b64 exec, s[78:79]
	buffer_load_dwordx4 v[142:145], v254, s[16:19], 0 offen offset:2048
	buffer_load_dwordx4 v[2:5], v254, s[16:19], 0 offen offset:2560
	s_mov_b64 exec, -1
	v_pk_add_f16 v111, v191, v199 neg_lo:[0,1] neg_hi:[0,1]
	v_pk_add_f16 v112, v192, v200 neg_lo:[0,1] neg_hi:[0,1]
	v_pk_add_f16 v113, v193, v201 neg_lo:[0,1] neg_hi:[0,1]
	v_exp_f16_sdwa v114, v110 dst_sel:WORD_0 dst_unused:UNUSED_PAD src0_sel:WORD_0
	v_exp_f16_sdwa v115, v111 dst_sel:WORD_0 dst_unused:UNUSED_PAD src0_sel:WORD_0
	v_exp_f16_sdwa v116, v112 dst_sel:WORD_0 dst_unused:UNUSED_PAD src0_sel:WORD_0
	v_exp_f16_sdwa v117, v113 dst_sel:WORD_0 dst_unused:UNUSED_PAD src0_sel:WORD_0
	v_exp_f16_sdwa v114, v110 dst_sel:WORD_1 dst_unused:UNUSED_PRESERVE src0_sel:WORD_1
	v_exp_f16_sdwa v115, v111 dst_sel:WORD_1 dst_unused:UNUSED_PRESERVE src0_sel:WORD_1
	v_exp_f16_sdwa v116, v112 dst_sel:WORD_1 dst_unused:UNUSED_PRESERVE src0_sel:WORD_1
	v_exp_f16_sdwa v117, v113 dst_sel:WORD_1 dst_unused:UNUSED_PRESERVE src0_sel:WORD_1
	v_pk_add_f16 v110, v194, v198 neg_lo:[0,1] neg_hi:[0,1]
	v_pk_add_f16 v101, v101, v114
	v_pk_add_f16 v98, v98, v117
	v_pk_add_f16 v99, v99, v116
	v_pk_add_f16 v100, v100, v115
	v_pk_fma_f16 v73, v25, v117, v73
	v_pk_fma_f16 v72, v24, v116, v72
	v_pk_fma_f16 v71, v23, v115, v71
	v_pk_fma_f16 v70, v22, v114, v70
	v_pk_add_f16 v111, v195, v199 neg_lo:[0,1] neg_hi:[0,1]
	v_pk_add_f16 v112, v196, v200 neg_lo:[0,1] neg_hi:[0,1]
	v_pk_add_f16 v113, v197, v201 neg_lo:[0,1] neg_hi:[0,1]
	v_exp_f16_sdwa v114, v110 dst_sel:WORD_0 dst_unused:UNUSED_PAD src0_sel:WORD_0
	v_exp_f16_sdwa v115, v111 dst_sel:WORD_0 dst_unused:UNUSED_PAD src0_sel:WORD_0
	v_exp_f16_sdwa v116, v112 dst_sel:WORD_0 dst_unused:UNUSED_PAD src0_sel:WORD_0
	v_exp_f16_sdwa v117, v113 dst_sel:WORD_0 dst_unused:UNUSED_PAD src0_sel:WORD_0
	v_exp_f16_sdwa v114, v110 dst_sel:WORD_1 dst_unused:UNUSED_PRESERVE src0_sel:WORD_1
	v_exp_f16_sdwa v115, v111 dst_sel:WORD_1 dst_unused:UNUSED_PRESERVE src0_sel:WORD_1
	v_exp_f16_sdwa v116, v112 dst_sel:WORD_1 dst_unused:UNUSED_PRESERVE src0_sel:WORD_1
	v_exp_f16_sdwa v117, v113 dst_sel:WORD_1 dst_unused:UNUSED_PRESERVE src0_sel:WORD_1
	v_pk_add_f16 v110, v186, v198 neg_lo:[0,1] neg_hi:[0,1]
	v_pk_add_f16 v101, v101, v114
	v_pk_add_f16 v100, v100, v115
	v_pk_add_f16 v99, v99, v116
	v_pk_add_f16 v98, v98, v117
	v_pk_fma_f16 v70, v30, v114, v70
	v_pk_fma_f16 v71, v31, v115, v71
	v_pk_fma_f16 v72, v32, v116, v72
	v_pk_fma_f16 v73, v33, v117, v73
	v_pk_add_f16 v111, v187, v199 neg_lo:[0,1] neg_hi:[0,1]
	v_pk_add_f16 v112, v188, v200 neg_lo:[0,1] neg_hi:[0,1]
	v_pk_add_f16 v113, v189, v201 neg_lo:[0,1] neg_hi:[0,1]
	v_exp_f16_sdwa v114, v110 dst_sel:WORD_0 dst_unused:UNUSED_PAD src0_sel:WORD_0
	v_exp_f16_sdwa v115, v111 dst_sel:WORD_0 dst_unused:UNUSED_PAD src0_sel:WORD_0
	v_exp_f16_sdwa v116, v112 dst_sel:WORD_0 dst_unused:UNUSED_PAD src0_sel:WORD_0
	v_exp_f16_sdwa v117, v113 dst_sel:WORD_0 dst_unused:UNUSED_PAD src0_sel:WORD_0
	v_exp_f16_sdwa v114, v110 dst_sel:WORD_1 dst_unused:UNUSED_PRESERVE src0_sel:WORD_1
	v_exp_f16_sdwa v115, v111 dst_sel:WORD_1 dst_unused:UNUSED_PRESERVE src0_sel:WORD_1
	v_exp_f16_sdwa v116, v112 dst_sel:WORD_1 dst_unused:UNUSED_PRESERVE src0_sel:WORD_1
	v_exp_f16_sdwa v117, v113 dst_sel:WORD_1 dst_unused:UNUSED_PRESERVE src0_sel:WORD_1
	v_pk_add_f16 v101, v101, v114
	v_pk_add_f16 v100, v100, v115
	v_rcp_f16_e32 v110, v101
	v_rcp_f16_sdwa v101, v101 dst_sel:DWORD dst_unused:UNUSED_PAD src0_sel:WORD_1
	v_pk_add_f16 v99, v99, v116
	v_rcp_f16_e32 v111, v100
	v_rcp_f16_sdwa v100, v100 dst_sel:DWORD dst_unused:UNUSED_PAD src0_sel:WORD_1
	v_pk_add_f16 v98, v98, v117
	v_rcp_f16_e32 v112, v99
	v_rcp_f16_sdwa v99, v99 dst_sel:DWORD dst_unused:UNUSED_PAD src0_sel:WORD_1
	v_rcp_f16_e32 v113, v98
	v_rcp_f16_sdwa v98, v98 dst_sel:DWORD dst_unused:UNUSED_PAD src0_sel:WORD_1
	v_pk_fma_f16 v70, v46, v114, v70
	v_pack_b32_f16 v101, v110, v101
	v_pk_fma_f16 v71, v47, v115, v71
	v_pk_mul_f16 v110, v70, v101
	v_pack_b32_f16 v70, v111, v100
	v_pk_fma_f16 v72, v48, v116, v72
	v_pk_mul_f16 v111, v71, v70
	v_pack_b32_f16 v70, v112, v99
	v_pk_fma_f16 v73, v49, v117, v73
	v_pk_mul_f16 v112, v72, v70
	v_pack_b32_f16 v70, v113, v98
	v_pk_mul_f16 v113, v73, v70
	s_waitcnt vmcnt(12)
	v_pk_mul_f16 v73, v185, v157 op_sel_hi:[0,1]
	v_pk_mul_f16 v101, v183, v157 op_sel_hi:[0,1]
	v_pk_mul_f16 v117, v184, v157 op_sel_hi:[0,1]
	v_pk_mul_f16 v70, v185, v154 op_sel_hi:[0,1]
	v_pk_mul_f16 v71, v185, v155 op_sel_hi:[0,1]
	v_pk_mul_f16 v72, v185, v156 op_sel_hi:[0,1]
	v_pk_mul_f16 v98, v183, v154 op_sel_hi:[0,1]
	v_pk_mul_f16 v99, v183, v155 op_sel_hi:[0,1]
	v_pk_mul_f16 v100, v183, v156 op_sel_hi:[0,1]
	v_pk_mul_f16 v114, v184, v154 op_sel_hi:[0,1]
	v_pk_mul_f16 v115, v184, v155 op_sel_hi:[0,1]
	v_pk_mul_f16 v116, v184, v156 op_sel_hi:[0,1]
	v_pk_fma_f16 v85, v85, v157, v73
	v_pk_fma_f16 v109, v109, v157, v101
	v_pk_fma_f16 v125, v125, v157, v117
	v_pk_fma_f16 v126, v53, v157, v73
	v_pk_fma_f16 v134, v69, v157, v101
	v_pk_fma_f16 v186, v97, v157, v117
	v_pk_fma_f16 v73, v21, v157, v73
	v_pk_fma_f16 v101, v37, v157, v101
	v_pk_fma_f16 v117, v57, v157, v117
	v_pk_maximum3_f16 v157, v85, v109, v125
	v_pk_fma_f16 v84, v84, v156, v72
	v_pk_fma_f16 v83, v83, v155, v71
	v_pk_fma_f16 v82, v82, v154, v70
	v_pk_fma_f16 v108, v108, v156, v100
	v_pk_fma_f16 v107, v107, v155, v99
	v_pk_fma_f16 v106, v106, v154, v98
	v_pk_fma_f16 v124, v124, v156, v116
	v_pk_fma_f16 v123, v123, v155, v115
	v_pk_fma_f16 v122, v122, v154, v114
	v_pk_fma_f16 v127, v52, v156, v72
	v_pk_fma_f16 v128, v51, v155, v71
	v_pk_fma_f16 v129, v50, v154, v70
	v_pk_fma_f16 v135, v68, v156, v100
	v_pk_fma_f16 v136, v67, v155, v99
	v_pk_fma_f16 v137, v66, v154, v98
	v_pk_fma_f16 v187, v96, v156, v116
	v_pk_fma_f16 v188, v95, v155, v115
	v_pk_fma_f16 v189, v94, v154, v114
	v_pk_fma_f16 v72, v20, v156, v72
	v_pk_fma_f16 v71, v19, v155, v71
	v_pk_fma_f16 v70, v18, v154, v70
	v_pk_fma_f16 v100, v36, v156, v100
	v_pk_fma_f16 v99, v35, v155, v99
	v_pk_fma_f16 v98, v34, v154, v98
	v_pk_fma_f16 v116, v56, v156, v116
	v_pk_fma_f16 v115, v55, v155, v115
	v_pk_fma_f16 v114, v54, v154, v114
	v_pk_maximum3_f16 v154, v82, v106, v122
	v_pk_maximum3_f16 v155, v83, v107, v123
	v_pk_maximum3_f16 v156, v84, v108, v124
	v_pk_maximum3_f16 v193, v126, v134, v186
	v_pk_maximum3_f16 v197, v73, v101, v117
	v_pk_maximum3_f16 v190, v129, v137, v189
	v_pk_maximum3_f16 v191, v128, v136, v188
	v_pk_maximum3_f16 v192, v127, v135, v187
	v_pk_maximum3_f16 v194, v70, v98, v114
	v_pk_maximum3_f16 v195, v71, v99, v115
	v_pk_maximum3_f16 v157, v157, v193, v197
	v_pk_maximum3_f16 v196, v72, v100, v116
	v_pk_maximum3_f16 v154, v154, v190, v194
	v_pk_maximum3_f16 v155, v155, v191, v195
	v_pk_maximum3_f16 v156, v156, v192, v196
	v_pk_add_f16 v85, v85, v157 neg_lo:[0,1] neg_hi:[0,1]
	v_pk_add_f16 v82, v82, v154 neg_lo:[0,1] neg_hi:[0,1]
	v_pk_add_f16 v83, v83, v155 neg_lo:[0,1] neg_hi:[0,1]
	v_pk_add_f16 v84, v84, v156 neg_lo:[0,1] neg_hi:[0,1]
	v_pk_add_f16 v106, v106, v154 neg_lo:[0,1] neg_hi:[0,1]
	v_exp_f16_sdwa v190, v82 dst_sel:WORD_0 dst_unused:UNUSED_PAD src0_sel:WORD_0
	v_exp_f16_sdwa v191, v83 dst_sel:WORD_0 dst_unused:UNUSED_PAD src0_sel:WORD_0
	v_exp_f16_sdwa v192, v84 dst_sel:WORD_0 dst_unused:UNUSED_PAD src0_sel:WORD_0
	v_exp_f16_sdwa v193, v85 dst_sel:WORD_0 dst_unused:UNUSED_PAD src0_sel:WORD_0
	v_exp_f16_sdwa v190, v82 dst_sel:WORD_1 dst_unused:UNUSED_PRESERVE src0_sel:WORD_1
	v_exp_f16_sdwa v191, v83 dst_sel:WORD_1 dst_unused:UNUSED_PRESERVE src0_sel:WORD_1
	v_exp_f16_sdwa v192, v84 dst_sel:WORD_1 dst_unused:UNUSED_PRESERVE src0_sel:WORD_1
	v_exp_f16_sdwa v193, v85 dst_sel:WORD_1 dst_unused:UNUSED_PRESERVE src0_sel:WORD_1
	v_pk_add_f16 v107, v107, v155 neg_lo:[0,1] neg_hi:[0,1]
	v_pk_add_f16 v85, v190, 0
	v_pk_fma_f16 v45, v45, v193, 0
	v_pk_add_f16 v82, v193, 0
	v_pk_add_f16 v83, v192, 0
	v_pk_add_f16 v84, v191, 0
	v_pk_fma_f16 v44, v44, v192, 0
	v_pk_fma_f16 v43, v43, v191, 0
	v_pk_fma_f16 v42, v42, v190, 0
	v_pk_add_f16 v108, v108, v156 neg_lo:[0,1] neg_hi:[0,1]
	v_pk_add_f16 v109, v109, v157 neg_lo:[0,1] neg_hi:[0,1]
	v_pk_add_f16 v70, v70, v154 neg_lo:[0,1] neg_hi:[0,1]
	v_exp_f16_sdwa v190, v106 dst_sel:WORD_0 dst_unused:UNUSED_PAD src0_sel:WORD_0
	v_exp_f16_sdwa v191, v107 dst_sel:WORD_0 dst_unused:UNUSED_PAD src0_sel:WORD_0
	v_exp_f16_sdwa v192, v108 dst_sel:WORD_0 dst_unused:UNUSED_PAD src0_sel:WORD_0
	v_exp_f16_sdwa v193, v109 dst_sel:WORD_0 dst_unused:UNUSED_PAD src0_sel:WORD_0
	v_exp_f16_sdwa v190, v106 dst_sel:WORD_1 dst_unused:UNUSED_PRESERVE src0_sel:WORD_1
	v_exp_f16_sdwa v191, v107 dst_sel:WORD_1 dst_unused:UNUSED_PRESERVE src0_sel:WORD_1
	v_exp_f16_sdwa v192, v108 dst_sel:WORD_1 dst_unused:UNUSED_PRESERVE src0_sel:WORD_1
	v_exp_f16_sdwa v193, v109 dst_sel:WORD_1 dst_unused:UNUSED_PRESERVE src0_sel:WORD_1
	v_pk_add_f16 v71, v71, v155 neg_lo:[0,1] neg_hi:[0,1]
	v_pk_add_f16 v85, v85, v190
	v_pk_fma_f16 v45, v65, v193, v45
	v_pk_add_f16 v65, v125, v157 neg_lo:[0,1] neg_hi:[0,1]
	v_pk_add_f16 v84, v84, v191
	v_pk_add_f16 v83, v83, v192
	v_pk_add_f16 v82, v82, v193
	v_pk_fma_f16 v42, v62, v190, v42
	v_pk_fma_f16 v43, v63, v191, v43
	v_pk_fma_f16 v44, v64, v192, v44
	v_pk_add_f16 v62, v122, v154 neg_lo:[0,1] neg_hi:[0,1]
	v_pk_add_f16 v63, v123, v155 neg_lo:[0,1] neg_hi:[0,1]
	v_pk_add_f16 v64, v124, v156 neg_lo:[0,1] neg_hi:[0,1]
	v_pk_add_f16 v72, v72, v156 neg_lo:[0,1] neg_hi:[0,1]
	v_exp_f16_sdwa v106, v62 dst_sel:WORD_0 dst_unused:UNUSED_PAD src0_sel:WORD_0
	v_exp_f16_sdwa v107, v63 dst_sel:WORD_0 dst_unused:UNUSED_PAD src0_sel:WORD_0
	v_exp_f16_sdwa v108, v64 dst_sel:WORD_0 dst_unused:UNUSED_PAD src0_sel:WORD_0
	v_exp_f16_sdwa v109, v65 dst_sel:WORD_0 dst_unused:UNUSED_PAD src0_sel:WORD_0
	v_exp_f16_sdwa v106, v62 dst_sel:WORD_1 dst_unused:UNUSED_PRESERVE src0_sel:WORD_1
	v_exp_f16_sdwa v107, v63 dst_sel:WORD_1 dst_unused:UNUSED_PRESERVE src0_sel:WORD_1
	v_exp_f16_sdwa v108, v64 dst_sel:WORD_1 dst_unused:UNUSED_PRESERVE src0_sel:WORD_1
	v_exp_f16_sdwa v109, v65 dst_sel:WORD_1 dst_unused:UNUSED_PRESERVE src0_sel:WORD_1
	v_pk_add_f16 v73, v73, v157 neg_lo:[0,1] neg_hi:[0,1]
	v_pk_add_f16 v65, v85, v106
	v_pk_add_f16 v62, v82, v109
	v_pk_add_f16 v63, v83, v108
	v_pk_add_f16 v64, v84, v107
	v_pk_fma_f16 v45, v89, v109, v45
	v_pk_fma_f16 v44, v88, v108, v44
	v_pk_fma_f16 v43, v87, v107, v43
	v_pk_fma_f16 v42, v86, v106, v42
	v_pk_add_f16 v82, v129, v154 neg_lo:[0,1] neg_hi:[0,1]
	v_pk_add_f16 v83, v128, v155 neg_lo:[0,1] neg_hi:[0,1]
	v_pk_add_f16 v84, v127, v156 neg_lo:[0,1] neg_hi:[0,1]
	v_pk_add_f16 v85, v126, v157 neg_lo:[0,1] neg_hi:[0,1]
	v_exp_f16_sdwa v86, v82 dst_sel:WORD_0 dst_unused:UNUSED_PAD src0_sel:WORD_0
	v_exp_f16_sdwa v87, v83 dst_sel:WORD_0 dst_unused:UNUSED_PAD src0_sel:WORD_0
	v_exp_f16_sdwa v88, v84 dst_sel:WORD_0 dst_unused:UNUSED_PAD src0_sel:WORD_0
	v_exp_f16_sdwa v89, v85 dst_sel:WORD_0 dst_unused:UNUSED_PAD src0_sel:WORD_0
	v_exp_f16_sdwa v86, v82 dst_sel:WORD_1 dst_unused:UNUSED_PRESERVE src0_sel:WORD_1
	v_exp_f16_sdwa v87, v83 dst_sel:WORD_1 dst_unused:UNUSED_PRESERVE src0_sel:WORD_1
	v_exp_f16_sdwa v88, v84 dst_sel:WORD_1 dst_unused:UNUSED_PRESERVE src0_sel:WORD_1
	v_exp_f16_sdwa v89, v85 dst_sel:WORD_1 dst_unused:UNUSED_PRESERVE src0_sel:WORD_1
	v_pk_add_f16 v82, v137, v154 neg_lo:[0,1] neg_hi:[0,1]
	v_pk_add_f16 v65, v65, v86
	v_pk_add_f16 v64, v64, v87
	v_pk_add_f16 v63, v63, v88
	v_pk_add_f16 v62, v62, v89
	v_pk_fma_f16 v42, v22, v86, v42
	v_pk_fma_f16 v43, v23, v87, v43
	v_pk_fma_f16 v44, v24, v88, v44
	v_pk_fma_f16 v45, v25, v89, v45
	v_pk_add_f16 v83, v136, v155 neg_lo:[0,1] neg_hi:[0,1]
	v_pk_add_f16 v84, v135, v156 neg_lo:[0,1] neg_hi:[0,1]
	v_pk_add_f16 v85, v134, v157 neg_lo:[0,1] neg_hi:[0,1]
	v_exp_f16_sdwa v86, v82 dst_sel:WORD_0 dst_unused:UNUSED_PAD src0_sel:WORD_0
	v_exp_f16_sdwa v87, v83 dst_sel:WORD_0 dst_unused:UNUSED_PAD src0_sel:WORD_0
	v_exp_f16_sdwa v88, v84 dst_sel:WORD_0 dst_unused:UNUSED_PAD src0_sel:WORD_0
	v_exp_f16_sdwa v89, v85 dst_sel:WORD_0 dst_unused:UNUSED_PAD src0_sel:WORD_0
	v_exp_f16_sdwa v86, v82 dst_sel:WORD_1 dst_unused:UNUSED_PRESERVE src0_sel:WORD_1
	v_exp_f16_sdwa v87, v83 dst_sel:WORD_1 dst_unused:UNUSED_PRESERVE src0_sel:WORD_1
	v_exp_f16_sdwa v88, v84 dst_sel:WORD_1 dst_unused:UNUSED_PRESERVE src0_sel:WORD_1
	v_exp_f16_sdwa v89, v85 dst_sel:WORD_1 dst_unused:UNUSED_PRESERVE src0_sel:WORD_1
	v_pk_add_f16 v82, v189, v154 neg_lo:[0,1] neg_hi:[0,1]
	v_pk_add_f16 v65, v65, v86
	v_pk_add_f16 v62, v62, v89
	v_pk_add_f16 v63, v63, v88
	v_pk_add_f16 v64, v64, v87
	v_pk_fma_f16 v45, v33, v89, v45
	v_pk_fma_f16 v44, v32, v88, v44
	v_pk_fma_f16 v43, v31, v87, v43
	v_pk_fma_f16 v42, v30, v86, v42
	v_pk_add_f16 v83, v188, v155 neg_lo:[0,1] neg_hi:[0,1]
	v_pk_add_f16 v84, v187, v156 neg_lo:[0,1] neg_hi:[0,1]
	v_pk_add_f16 v85, v186, v157 neg_lo:[0,1] neg_hi:[0,1]
	v_exp_f16_sdwa v86, v82 dst_sel:WORD_0 dst_unused:UNUSED_PAD src0_sel:WORD_0
	v_exp_f16_sdwa v87, v83 dst_sel:WORD_0 dst_unused:UNUSED_PAD src0_sel:WORD_0
	v_exp_f16_sdwa v88, v84 dst_sel:WORD_0 dst_unused:UNUSED_PAD src0_sel:WORD_0
	v_exp_f16_sdwa v89, v85 dst_sel:WORD_0 dst_unused:UNUSED_PAD src0_sel:WORD_0
	v_exp_f16_sdwa v86, v82 dst_sel:WORD_1 dst_unused:UNUSED_PRESERVE src0_sel:WORD_1
	v_exp_f16_sdwa v87, v83 dst_sel:WORD_1 dst_unused:UNUSED_PRESERVE src0_sel:WORD_1
	v_exp_f16_sdwa v88, v84 dst_sel:WORD_1 dst_unused:UNUSED_PRESERVE src0_sel:WORD_1
	v_exp_f16_sdwa v89, v85 dst_sel:WORD_1 dst_unused:UNUSED_PRESERVE src0_sel:WORD_1
	v_exp_f16_sdwa v82, v70 dst_sel:WORD_0 dst_unused:UNUSED_PAD src0_sel:WORD_0
	v_exp_f16_sdwa v83, v71 dst_sel:WORD_0 dst_unused:UNUSED_PAD src0_sel:WORD_0
	v_exp_f16_sdwa v84, v72 dst_sel:WORD_0 dst_unused:UNUSED_PAD src0_sel:WORD_0
	v_exp_f16_sdwa v85, v73 dst_sel:WORD_0 dst_unused:UNUSED_PAD src0_sel:WORD_0
	v_exp_f16_sdwa v82, v70 dst_sel:WORD_1 dst_unused:UNUSED_PRESERVE src0_sel:WORD_1
	v_exp_f16_sdwa v83, v71 dst_sel:WORD_1 dst_unused:UNUSED_PRESERVE src0_sel:WORD_1
	v_exp_f16_sdwa v84, v72 dst_sel:WORD_1 dst_unused:UNUSED_PRESERVE src0_sel:WORD_1
	v_exp_f16_sdwa v85, v73 dst_sel:WORD_1 dst_unused:UNUSED_PRESERVE src0_sel:WORD_1
	v_pk_add_f16 v70, v98, v154 neg_lo:[0,1] neg_hi:[0,1]
	v_pk_add_f16 v65, v65, v86
	v_pk_add_f16 v64, v64, v87
	v_pk_add_f16 v63, v63, v88
	v_pk_add_f16 v62, v62, v89
	v_pk_fma_f16 v42, v46, v86, v42
	v_pk_fma_f16 v43, v47, v87, v43
	v_pk_fma_f16 v44, v48, v88, v44
	v_pk_fma_f16 v45, v49, v89, v45
	v_pk_add_f16 v65, v65, v82
	v_pk_add_f16 v62, v62, v85
	v_pk_add_f16 v63, v63, v84
	v_pk_add_f16 v64, v64, v83
	v_pk_fma_f16 v45, v9, v85, v45
	v_pk_fma_f16 v44, v8, v84, v44
	v_pk_fma_f16 v43, v7, v83, v43
	v_pk_fma_f16 v42, v6, v82, v42
	v_pk_add_f16 v71, v99, v155 neg_lo:[0,1] neg_hi:[0,1]
	v_pk_add_f16 v72, v100, v156 neg_lo:[0,1] neg_hi:[0,1]
	v_pk_add_f16 v73, v101, v157 neg_lo:[0,1] neg_hi:[0,1]
	v_exp_f16_sdwa v82, v70 dst_sel:WORD_0 dst_unused:UNUSED_PAD src0_sel:WORD_0
	v_exp_f16_sdwa v83, v71 dst_sel:WORD_0 dst_unused:UNUSED_PAD src0_sel:WORD_0
	v_exp_f16_sdwa v84, v72 dst_sel:WORD_0 dst_unused:UNUSED_PAD src0_sel:WORD_0
	v_exp_f16_sdwa v85, v73 dst_sel:WORD_0 dst_unused:UNUSED_PAD src0_sel:WORD_0
	v_exp_f16_sdwa v82, v70 dst_sel:WORD_1 dst_unused:UNUSED_PRESERVE src0_sel:WORD_1
	v_exp_f16_sdwa v83, v71 dst_sel:WORD_1 dst_unused:UNUSED_PRESERVE src0_sel:WORD_1
	v_exp_f16_sdwa v84, v72 dst_sel:WORD_1 dst_unused:UNUSED_PRESERVE src0_sel:WORD_1
	v_exp_f16_sdwa v85, v73 dst_sel:WORD_1 dst_unused:UNUSED_PRESERVE src0_sel:WORD_1
	v_pk_add_f16 v70, v114, v154 neg_lo:[0,1] neg_hi:[0,1]
	v_pk_add_f16 v65, v65, v82
	v_pk_add_f16 v64, v64, v83
	v_pk_add_f16 v63, v63, v84
	v_pk_add_f16 v62, v62, v85
	v_pk_fma_f16 v42, v10, v82, v42
	v_pk_fma_f16 v43, v11, v83, v43
	v_pk_fma_f16 v44, v12, v84, v44
	v_pk_fma_f16 v45, v13, v85, v45
	v_pk_add_f16 v71, v115, v155 neg_lo:[0,1] neg_hi:[0,1]
	v_pk_add_f16 v72, v116, v156 neg_lo:[0,1] neg_hi:[0,1]
	v_pk_add_f16 v73, v117, v157 neg_lo:[0,1] neg_hi:[0,1]
	v_exp_f16_sdwa v82, v70 dst_sel:WORD_0 dst_unused:UNUSED_PAD src0_sel:WORD_0
	v_exp_f16_sdwa v83, v71 dst_sel:WORD_0 dst_unused:UNUSED_PAD src0_sel:WORD_0
	v_exp_f16_sdwa v84, v72 dst_sel:WORD_0 dst_unused:UNUSED_PAD src0_sel:WORD_0
	v_exp_f16_sdwa v85, v73 dst_sel:WORD_0 dst_unused:UNUSED_PAD src0_sel:WORD_0
	v_exp_f16_sdwa v82, v70 dst_sel:WORD_1 dst_unused:UNUSED_PRESERVE src0_sel:WORD_1
	v_exp_f16_sdwa v83, v71 dst_sel:WORD_1 dst_unused:UNUSED_PRESERVE src0_sel:WORD_1
	v_exp_f16_sdwa v84, v72 dst_sel:WORD_1 dst_unused:UNUSED_PRESERVE src0_sel:WORD_1
	v_exp_f16_sdwa v85, v73 dst_sel:WORD_1 dst_unused:UNUSED_PRESERVE src0_sel:WORD_1
	v_pk_add_f16 v65, v65, v82
	v_pk_add_f16 v64, v64, v83
	v_rcp_f16_e32 v70, v65
	v_rcp_f16_sdwa v65, v65 dst_sel:DWORD dst_unused:UNUSED_PAD src0_sel:WORD_1
	v_pk_add_f16 v63, v63, v84
	v_rcp_f16_e32 v71, v64
	v_rcp_f16_sdwa v64, v64 dst_sel:DWORD dst_unused:UNUSED_PAD src0_sel:WORD_1
	v_pk_add_f16 v62, v62, v85
	v_rcp_f16_e32 v72, v63
	v_rcp_f16_sdwa v73, v63 dst_sel:DWORD dst_unused:UNUSED_PAD src0_sel:WORD_1
	v_pk_fma_f16 v43, v15, v83, v43
	v_pk_fma_f16 v42, v14, v82, v42
	v_rcp_f16_e32 v82, v62
	v_rcp_f16_sdwa v83, v62 dst_sel:DWORD dst_unused:UNUSED_PAD src0_sel:WORD_1
	v_pack_b32_f16 v62, v70, v65
	v_pk_mul_f16 v62, v42, v62
	v_pack_b32_f16 v42, v71, v64
	v_pk_fma_f16 v44, v16, v84, v44
	v_pk_mul_f16 v63, v43, v42
	v_pack_b32_f16 v42, v72, v73
	v_pk_fma_f16 v45, v17, v85, v45
	v_pk_mul_f16 v64, v44, v42
	v_pack_b32_f16 v42, v82, v83
	v_pk_mul_f16 v65, v45, v42
	s_waitcnt vmcnt(6)
	v_pk_mul_f16 v42, v185, v150 op_sel_hi:[0,1]
	v_pk_mul_f16 v70, v183, v150 op_sel_hi:[0,1]
	v_pk_mul_f16 v82, v184, v150 op_sel_hi:[0,1]
	v_pk_mul_f16 v43, v185, v151 op_sel_hi:[0,1]
	v_pk_mul_f16 v44, v185, v152 op_sel_hi:[0,1]
	v_pk_mul_f16 v45, v185, v153 op_sel_hi:[0,1]
	v_pk_mul_f16 v71, v183, v151 op_sel_hi:[0,1]
	v_pk_mul_f16 v72, v183, v152 op_sel_hi:[0,1]
	v_pk_mul_f16 v73, v183, v153 op_sel_hi:[0,1]
	v_pk_mul_f16 v83, v184, v151 op_sel_hi:[0,1]
	v_pk_mul_f16 v84, v184, v152 op_sel_hi:[0,1]
	v_pk_mul_f16 v85, v184, v153 op_sel_hi:[0,1]
	v_pk_fma_f16 v50, v50, v150, v42
	v_pk_fma_f16 v66, v66, v150, v70
	v_pk_fma_f16 v89, v94, v150, v82
	v_pk_fma_f16 v53, v53, v153, v45
	v_pk_maximum3_f16 v114, v50, v66, v89
	v_pk_fma_f16 v52, v52, v152, v44
	v_pk_fma_f16 v51, v51, v151, v43
	v_pk_fma_f16 v69, v69, v153, v73
	v_pk_fma_f16 v68, v68, v152, v72
	v_pk_fma_f16 v67, v67, v151, v71
	v_pk_fma_f16 v86, v97, v153, v85
	v_pk_fma_f16 v87, v96, v152, v84
	v_pk_fma_f16 v88, v95, v151, v83
	v_pk_fma_f16 v97, v18, v150, v42
	v_pk_fma_f16 v101, v34, v150, v70
	v_pk_fma_f16 v109, v54, v150, v82
	v_pk_fma_f16 v42, v74, v150, v42
	v_pk_fma_f16 v70, v102, v150, v70
	v_pk_fma_f16 v82, v118, v150, v82
	v_pk_maximum3_f16 v115, v51, v67, v88
	v_pk_maximum3_f16 v116, v52, v68, v87
	v_pk_maximum3_f16 v117, v53, v69, v86
	v_pk_maximum3_f16 v122, v97, v101, v109
	v_pk_fma_f16 v94, v21, v153, v45
	v_pk_maximum3_f16 v126, v42, v70, v82
	v_pk_fma_f16 v95, v20, v152, v44
	v_pk_maximum3_f16 v114, v114, v122, v126
	v_pk_fma_f16 v96, v19, v151, v43
	v_pk_fma_f16 v98, v37, v153, v73
	v_pk_fma_f16 v99, v36, v152, v72
	v_pk_fma_f16 v100, v35, v151, v71
	v_pk_fma_f16 v106, v57, v153, v85
	v_pk_fma_f16 v107, v56, v152, v84
	v_pk_fma_f16 v108, v55, v151, v83
	v_pk_fma_f16 v45, v77, v153, v45
	v_pk_fma_f16 v44, v76, v152, v44
	v_pk_fma_f16 v43, v75, v151, v43
	v_pk_fma_f16 v73, v105, v153, v73
	v_pk_fma_f16 v72, v104, v152, v72
	v_pk_fma_f16 v71, v103, v151, v71
	v_pk_fma_f16 v85, v121, v153, v85
	v_pk_fma_f16 v84, v120, v152, v84
	v_pk_fma_f16 v83, v119, v151, v83
	v_pk_maximum3_f16 v123, v96, v100, v108
	v_pk_maximum3_f16 v124, v95, v99, v107
	v_pk_maximum3_f16 v125, v94, v98, v106
	v_pk_maximum3_f16 v128, v44, v72, v84
	v_pk_maximum3_f16 v129, v45, v73, v85
	v_pk_maximum3_f16 v127, v43, v71, v83
	v_pk_maximum3_f16 v115, v115, v123, v127
	v_pk_maximum3_f16 v116, v116, v124, v128
	v_pk_maximum3_f16 v117, v117, v125, v129
	v_pk_add_f16 v50, v50, v114 neg_lo:[0,1] neg_hi:[0,1]
	v_pk_add_f16 v51, v51, v115 neg_lo:[0,1] neg_hi:[0,1]
	v_pk_add_f16 v52, v52, v116 neg_lo:[0,1] neg_hi:[0,1]
	v_pk_add_f16 v53, v53, v117 neg_lo:[0,1] neg_hi:[0,1]
	v_pk_add_f16 v66, v66, v114 neg_lo:[0,1] neg_hi:[0,1]
	v_exp_f16_sdwa v122, v50 dst_sel:WORD_0 dst_unused:UNUSED_PAD src0_sel:WORD_0
	v_exp_f16_sdwa v123, v51 dst_sel:WORD_0 dst_unused:UNUSED_PAD src0_sel:WORD_0
	v_exp_f16_sdwa v124, v52 dst_sel:WORD_0 dst_unused:UNUSED_PAD src0_sel:WORD_0
	v_exp_f16_sdwa v125, v53 dst_sel:WORD_0 dst_unused:UNUSED_PAD src0_sel:WORD_0
	v_exp_f16_sdwa v122, v50 dst_sel:WORD_1 dst_unused:UNUSED_PRESERVE src0_sel:WORD_1
	v_exp_f16_sdwa v123, v51 dst_sel:WORD_1 dst_unused:UNUSED_PRESERVE src0_sel:WORD_1
	v_exp_f16_sdwa v124, v52 dst_sel:WORD_1 dst_unused:UNUSED_PRESERVE src0_sel:WORD_1
	v_exp_f16_sdwa v125, v53 dst_sel:WORD_1 dst_unused:UNUSED_PRESERVE src0_sel:WORD_1
	v_pk_add_f16 v67, v67, v115 neg_lo:[0,1] neg_hi:[0,1]
	v_pk_add_f16 v50, v125, 0
	v_pk_fma_f16 v22, v22, v122, 0
	v_pk_add_f16 v51, v124, 0
	v_pk_add_f16 v52, v123, 0
	v_pk_add_f16 v53, v122, 0
	v_pk_fma_f16 v23, v23, v123, 0
	v_pk_fma_f16 v24, v24, v124, 0
	v_pk_fma_f16 v25, v25, v125, 0
	v_pk_add_f16 v68, v68, v116 neg_lo:[0,1] neg_hi:[0,1]
	v_pk_add_f16 v69, v69, v117 neg_lo:[0,1] neg_hi:[0,1]
	v_pk_add_f16 v42, v42, v114 neg_lo:[0,1] neg_hi:[0,1]
	v_exp_f16_sdwa v122, v66 dst_sel:WORD_0 dst_unused:UNUSED_PAD src0_sel:WORD_0
	v_exp_f16_sdwa v123, v67 dst_sel:WORD_0 dst_unused:UNUSED_PAD src0_sel:WORD_0
	v_exp_f16_sdwa v124, v68 dst_sel:WORD_0 dst_unused:UNUSED_PAD src0_sel:WORD_0
	v_exp_f16_sdwa v125, v69 dst_sel:WORD_0 dst_unused:UNUSED_PAD src0_sel:WORD_0
	v_exp_f16_sdwa v122, v66 dst_sel:WORD_1 dst_unused:UNUSED_PRESERVE src0_sel:WORD_1
	v_exp_f16_sdwa v123, v67 dst_sel:WORD_1 dst_unused:UNUSED_PRESERVE src0_sel:WORD_1
	v_exp_f16_sdwa v124, v68 dst_sel:WORD_1 dst_unused:UNUSED_PRESERVE src0_sel:WORD_1
	v_exp_f16_sdwa v125, v69 dst_sel:WORD_1 dst_unused:UNUSED_PRESERVE src0_sel:WORD_1
	v_pk_add_f16 v43, v43, v115 neg_lo:[0,1] neg_hi:[0,1]
	v_pk_add_f16 v50, v50, v125
	v_pk_fma_f16 v22, v30, v122, v22
	v_pk_add_f16 v30, v89, v114 neg_lo:[0,1] neg_hi:[0,1]
	v_pk_add_f16 v53, v53, v122
	v_pk_add_f16 v52, v52, v123
	v_pk_add_f16 v51, v51, v124
	v_pk_fma_f16 v25, v33, v125, v25
	v_pk_fma_f16 v24, v32, v124, v24
	v_pk_fma_f16 v23, v31, v123, v23
	v_pk_add_f16 v31, v88, v115 neg_lo:[0,1] neg_hi:[0,1]
	v_pk_add_f16 v32, v87, v116 neg_lo:[0,1] neg_hi:[0,1]
	v_pk_add_f16 v33, v86, v117 neg_lo:[0,1] neg_hi:[0,1]
	v_pk_add_f16 v44, v44, v116 neg_lo:[0,1] neg_hi:[0,1]
	v_exp_f16_sdwa v66, v30 dst_sel:WORD_0 dst_unused:UNUSED_PAD src0_sel:WORD_0
	v_exp_f16_sdwa v67, v31 dst_sel:WORD_0 dst_unused:UNUSED_PAD src0_sel:WORD_0
	v_exp_f16_sdwa v68, v32 dst_sel:WORD_0 dst_unused:UNUSED_PAD src0_sel:WORD_0
	v_exp_f16_sdwa v69, v33 dst_sel:WORD_0 dst_unused:UNUSED_PAD src0_sel:WORD_0
	v_exp_f16_sdwa v66, v30 dst_sel:WORD_1 dst_unused:UNUSED_PRESERVE src0_sel:WORD_1
	v_exp_f16_sdwa v67, v31 dst_sel:WORD_1 dst_unused:UNUSED_PRESERVE src0_sel:WORD_1
	v_exp_f16_sdwa v68, v32 dst_sel:WORD_1 dst_unused:UNUSED_PRESERVE src0_sel:WORD_1
	v_exp_f16_sdwa v69, v33 dst_sel:WORD_1 dst_unused:UNUSED_PRESERVE src0_sel:WORD_1
	v_pk_add_f16 v45, v45, v117 neg_lo:[0,1] neg_hi:[0,1]
	v_pk_add_f16 v30, v50, v69
	v_pk_add_f16 v31, v51, v68
	v_pk_add_f16 v32, v52, v67
	v_pk_add_f16 v33, v53, v66
	v_pk_fma_f16 v22, v46, v66, v22
	v_pk_fma_f16 v23, v47, v67, v23
	v_pk_fma_f16 v24, v48, v68, v24
	v_pk_fma_f16 v25, v49, v69, v25
	v_pk_add_f16 v46, v97, v114 neg_lo:[0,1] neg_hi:[0,1]
	v_pk_add_f16 v47, v96, v115 neg_lo:[0,1] neg_hi:[0,1]
	v_pk_add_f16 v48, v95, v116 neg_lo:[0,1] neg_hi:[0,1]
	v_pk_add_f16 v49, v94, v117 neg_lo:[0,1] neg_hi:[0,1]
	v_exp_f16_sdwa v50, v46 dst_sel:WORD_0 dst_unused:UNUSED_PAD src0_sel:WORD_0
	v_exp_f16_sdwa v51, v47 dst_sel:WORD_0 dst_unused:UNUSED_PAD src0_sel:WORD_0
	v_exp_f16_sdwa v52, v48 dst_sel:WORD_0 dst_unused:UNUSED_PAD src0_sel:WORD_0
	v_exp_f16_sdwa v53, v49 dst_sel:WORD_0 dst_unused:UNUSED_PAD src0_sel:WORD_0
	v_exp_f16_sdwa v50, v46 dst_sel:WORD_1 dst_unused:UNUSED_PRESERVE src0_sel:WORD_1
	v_exp_f16_sdwa v51, v47 dst_sel:WORD_1 dst_unused:UNUSED_PRESERVE src0_sel:WORD_1
	v_exp_f16_sdwa v52, v48 dst_sel:WORD_1 dst_unused:UNUSED_PRESERVE src0_sel:WORD_1
	v_exp_f16_sdwa v53, v49 dst_sel:WORD_1 dst_unused:UNUSED_PRESERVE src0_sel:WORD_1
	v_pk_add_f16 v46, v101, v114 neg_lo:[0,1] neg_hi:[0,1]
	v_pk_add_f16 v30, v30, v53
	v_pk_add_f16 v33, v33, v50
	v_pk_add_f16 v32, v32, v51
	v_pk_add_f16 v31, v31, v52
	v_pk_fma_f16 v25, v9, v53, v25
	v_pk_fma_f16 v24, v8, v52, v24
	v_pk_fma_f16 v23, v7, v51, v23
	v_pk_fma_f16 v22, v6, v50, v22
	v_pk_add_f16 v47, v100, v115 neg_lo:[0,1] neg_hi:[0,1]
	v_pk_add_f16 v48, v99, v116 neg_lo:[0,1] neg_hi:[0,1]
	v_pk_add_f16 v49, v98, v117 neg_lo:[0,1] neg_hi:[0,1]
	v_exp_f16_sdwa v50, v46 dst_sel:WORD_0 dst_unused:UNUSED_PAD src0_sel:WORD_0
	v_exp_f16_sdwa v51, v47 dst_sel:WORD_0 dst_unused:UNUSED_PAD src0_sel:WORD_0
	v_exp_f16_sdwa v52, v48 dst_sel:WORD_0 dst_unused:UNUSED_PAD src0_sel:WORD_0
	v_exp_f16_sdwa v53, v49 dst_sel:WORD_0 dst_unused:UNUSED_PAD src0_sel:WORD_0
	v_exp_f16_sdwa v50, v46 dst_sel:WORD_1 dst_unused:UNUSED_PRESERVE src0_sel:WORD_1
	v_exp_f16_sdwa v51, v47 dst_sel:WORD_1 dst_unused:UNUSED_PRESERVE src0_sel:WORD_1
	v_exp_f16_sdwa v52, v48 dst_sel:WORD_1 dst_unused:UNUSED_PRESERVE src0_sel:WORD_1
	v_exp_f16_sdwa v53, v49 dst_sel:WORD_1 dst_unused:UNUSED_PRESERVE src0_sel:WORD_1
	v_pk_add_f16 v46, v109, v114 neg_lo:[0,1] neg_hi:[0,1]
	v_pk_add_f16 v30, v30, v53
	v_pk_add_f16 v31, v31, v52
	v_pk_add_f16 v32, v32, v51
	v_pk_add_f16 v33, v33, v50
	v_pk_fma_f16 v22, v10, v50, v22
	v_pk_fma_f16 v23, v11, v51, v23
	v_pk_fma_f16 v24, v12, v52, v24
	v_pk_fma_f16 v25, v13, v53, v25
	v_pk_add_f16 v47, v108, v115 neg_lo:[0,1] neg_hi:[0,1]
	v_pk_add_f16 v48, v107, v116 neg_lo:[0,1] neg_hi:[0,1]
	v_pk_add_f16 v49, v106, v117 neg_lo:[0,1] neg_hi:[0,1]
	v_exp_f16_sdwa v50, v46 dst_sel:WORD_0 dst_unused:UNUSED_PAD src0_sel:WORD_0
	v_exp_f16_sdwa v51, v47 dst_sel:WORD_0 dst_unused:UNUSED_PAD src0_sel:WORD_0
	v_exp_f16_sdwa v52, v48 dst_sel:WORD_0 dst_unused:UNUSED_PAD src0_sel:WORD_0
	v_exp_f16_sdwa v53, v49 dst_sel:WORD_0 dst_unused:UNUSED_PAD src0_sel:WORD_0
	v_exp_f16_sdwa v50, v46 dst_sel:WORD_1 dst_unused:UNUSED_PRESERVE src0_sel:WORD_1
	v_exp_f16_sdwa v51, v47 dst_sel:WORD_1 dst_unused:UNUSED_PRESERVE src0_sel:WORD_1
	v_exp_f16_sdwa v52, v48 dst_sel:WORD_1 dst_unused:UNUSED_PRESERVE src0_sel:WORD_1
	v_exp_f16_sdwa v53, v49 dst_sel:WORD_1 dst_unused:UNUSED_PRESERVE src0_sel:WORD_1
	v_exp_f16_sdwa v46, v42 dst_sel:WORD_0 dst_unused:UNUSED_PAD src0_sel:WORD_0
	v_exp_f16_sdwa v47, v43 dst_sel:WORD_0 dst_unused:UNUSED_PAD src0_sel:WORD_0
	v_exp_f16_sdwa v48, v44 dst_sel:WORD_0 dst_unused:UNUSED_PAD src0_sel:WORD_0
	v_exp_f16_sdwa v49, v45 dst_sel:WORD_0 dst_unused:UNUSED_PAD src0_sel:WORD_0
	v_exp_f16_sdwa v46, v42 dst_sel:WORD_1 dst_unused:UNUSED_PRESERVE src0_sel:WORD_1
	v_exp_f16_sdwa v47, v43 dst_sel:WORD_1 dst_unused:UNUSED_PRESERVE src0_sel:WORD_1
	v_exp_f16_sdwa v48, v44 dst_sel:WORD_1 dst_unused:UNUSED_PRESERVE src0_sel:WORD_1
	v_exp_f16_sdwa v49, v45 dst_sel:WORD_1 dst_unused:UNUSED_PRESERVE src0_sel:WORD_1
	v_pk_add_f16 v42, v70, v114 neg_lo:[0,1] neg_hi:[0,1]
	v_pk_add_f16 v30, v30, v53
	v_pk_add_f16 v33, v33, v50
	v_pk_add_f16 v32, v32, v51
	v_pk_add_f16 v31, v31, v52
	v_pk_fma_f16 v25, v17, v53, v25
	v_pk_fma_f16 v24, v16, v52, v24
	v_pk_fma_f16 v23, v15, v51, v23
	v_pk_fma_f16 v22, v14, v50, v22
	v_pk_add_f16 v30, v30, v49
	v_pk_add_f16 v31, v31, v48
	v_pk_add_f16 v32, v32, v47
	v_pk_add_f16 v33, v33, v46
	v_pk_fma_f16 v22, v26, v46, v22
	v_pk_fma_f16 v23, v27, v47, v23
	v_pk_fma_f16 v24, v28, v48, v24
	v_pk_fma_f16 v25, v29, v49, v25
	v_pk_add_f16 v43, v71, v115 neg_lo:[0,1] neg_hi:[0,1]
	v_pk_add_f16 v44, v72, v116 neg_lo:[0,1] neg_hi:[0,1]
	v_pk_add_f16 v45, v73, v117 neg_lo:[0,1] neg_hi:[0,1]
	v_exp_f16_sdwa v46, v42 dst_sel:WORD_0 dst_unused:UNUSED_PAD src0_sel:WORD_0
	v_exp_f16_sdwa v47, v43 dst_sel:WORD_0 dst_unused:UNUSED_PAD src0_sel:WORD_0
	v_exp_f16_sdwa v48, v44 dst_sel:WORD_0 dst_unused:UNUSED_PAD src0_sel:WORD_0
	v_exp_f16_sdwa v49, v45 dst_sel:WORD_0 dst_unused:UNUSED_PAD src0_sel:WORD_0
	v_exp_f16_sdwa v46, v42 dst_sel:WORD_1 dst_unused:UNUSED_PRESERVE src0_sel:WORD_1
	v_exp_f16_sdwa v47, v43 dst_sel:WORD_1 dst_unused:UNUSED_PRESERVE src0_sel:WORD_1
	v_exp_f16_sdwa v48, v44 dst_sel:WORD_1 dst_unused:UNUSED_PRESERVE src0_sel:WORD_1
	v_exp_f16_sdwa v49, v45 dst_sel:WORD_1 dst_unused:UNUSED_PRESERVE src0_sel:WORD_1
	v_pk_add_f16 v42, v82, v114 neg_lo:[0,1] neg_hi:[0,1]
	v_pk_add_f16 v30, v30, v49
	v_pk_add_f16 v33, v33, v46
	v_pk_add_f16 v32, v32, v47
	v_pk_add_f16 v31, v31, v48
	v_pk_fma_f16 v25, v41, v49, v25
	v_pk_fma_f16 v24, v40, v48, v24
	v_pk_fma_f16 v23, v39, v47, v23
	v_pk_fma_f16 v22, v38, v46, v22
	v_pk_add_f16 v43, v83, v115 neg_lo:[0,1] neg_hi:[0,1]
	v_pk_add_f16 v44, v84, v116 neg_lo:[0,1] neg_hi:[0,1]
	v_pk_add_f16 v45, v85, v117 neg_lo:[0,1] neg_hi:[0,1]
	v_exp_f16_sdwa v46, v42 dst_sel:WORD_0 dst_unused:UNUSED_PAD src0_sel:WORD_0
	v_exp_f16_sdwa v47, v43 dst_sel:WORD_0 dst_unused:UNUSED_PAD src0_sel:WORD_0
	v_exp_f16_sdwa v48, v44 dst_sel:WORD_0 dst_unused:UNUSED_PAD src0_sel:WORD_0
	v_exp_f16_sdwa v49, v45 dst_sel:WORD_0 dst_unused:UNUSED_PAD src0_sel:WORD_0
	v_exp_f16_sdwa v46, v42 dst_sel:WORD_1 dst_unused:UNUSED_PRESERVE src0_sel:WORD_1
	v_exp_f16_sdwa v47, v43 dst_sel:WORD_1 dst_unused:UNUSED_PRESERVE src0_sel:WORD_1
	v_exp_f16_sdwa v48, v44 dst_sel:WORD_1 dst_unused:UNUSED_PRESERVE src0_sel:WORD_1
	v_exp_f16_sdwa v49, v45 dst_sel:WORD_1 dst_unused:UNUSED_PRESERVE src0_sel:WORD_1
	s_nop 0
	v_pk_add_f16 v30, v30, v49
	v_pk_add_f16 v31, v31, v48
	v_rcp_f16_e32 v44, v30
	v_rcp_f16_sdwa v30, v30 dst_sel:DWORD dst_unused:UNUSED_PAD src0_sel:WORD_1
	v_pk_add_f16 v32, v32, v47
	v_rcp_f16_e32 v45, v31
	v_rcp_f16_sdwa v31, v31 dst_sel:DWORD dst_unused:UNUSED_PAD src0_sel:WORD_1
	v_pk_add_f16 v33, v33, v46
	v_rcp_f16_e32 v43, v32
	v_rcp_f16_sdwa v32, v32 dst_sel:DWORD dst_unused:UNUSED_PAD src0_sel:WORD_1
	v_rcp_f16_e32 v42, v33
	v_rcp_f16_sdwa v33, v33 dst_sel:DWORD dst_unused:UNUSED_PAD src0_sel:WORD_1
	v_pk_fma_f16 v25, v61, v49, v25
	v_pack_b32_f16 v30, v44, v30
	v_pk_fma_f16 v24, v60, v48, v24
	v_pk_mul_f16 v25, v25, v30
	v_pack_b32_f16 v30, v45, v31
	v_pk_fma_f16 v23, v59, v47, v23
	v_pk_mul_f16 v24, v24, v30
	v_pack_b32_f16 v30, v43, v32
	v_pk_fma_f16 v22, v58, v46, v22
	v_pk_mul_f16 v23, v23, v30
	v_pack_b32_f16 v30, v42, v33
	v_pk_mul_f16 v22, v22, v30
	s_waitcnt vmcnt(0)
	v_pk_mul_f16 v30, v185, v146 op_sel_hi:[0,1]
	v_pk_mul_f16 v31, v185, v147 op_sel_hi:[0,1]
	v_pk_mul_f16 v32, v185, v148 op_sel_hi:[0,1]
	v_pk_mul_f16 v33, v185, v149 op_sel_hi:[0,1]
	v_pk_mul_f16 v42, v183, v146 op_sel_hi:[0,1]
	v_pk_mul_f16 v43, v183, v147 op_sel_hi:[0,1]
	v_pk_mul_f16 v44, v183, v148 op_sel_hi:[0,1]
	v_pk_mul_f16 v45, v183, v149 op_sel_hi:[0,1]
	v_pk_mul_f16 v46, v184, v146 op_sel_hi:[0,1]
	v_pk_mul_f16 v47, v184, v147 op_sel_hi:[0,1]
	v_pk_mul_f16 v48, v184, v148 op_sel_hi:[0,1]
	v_pk_mul_f16 v49, v184, v149 op_sel_hi:[0,1]
	v_pk_fma_f16 v21, v21, v149, v33
	v_pk_fma_f16 v20, v20, v148, v32
	v_pk_fma_f16 v19, v19, v147, v31
	v_pk_fma_f16 v18, v18, v146, v30
	v_pk_fma_f16 v37, v37, v149, v45
	v_pk_fma_f16 v36, v36, v148, v44
	v_pk_fma_f16 v35, v35, v147, v43
	v_pk_fma_f16 v34, v34, v146, v42
	v_pk_fma_f16 v50, v57, v149, v49
	v_pk_fma_f16 v51, v56, v148, v48
	v_pk_fma_f16 v52, v55, v147, v47
	v_pk_fma_f16 v53, v54, v146, v46
	v_pk_fma_f16 v54, v77, v149, v33
	v_pk_fma_f16 v55, v76, v148, v32
	v_pk_fma_f16 v56, v75, v147, v31
	v_pk_fma_f16 v57, v74, v146, v30
	v_pk_maximum3_f16 v74, v18, v34, v53
	v_pk_maximum3_f16 v75, v19, v35, v52
	v_pk_maximum3_f16 v76, v20, v36, v51
	v_pk_maximum3_f16 v77, v21, v37, v50
	v_pk_fma_f16 v66, v105, v149, v45
	v_pk_fma_f16 v67, v104, v148, v44
	v_pk_fma_f16 v68, v103, v147, v43
	v_pk_fma_f16 v69, v102, v146, v42
	v_pk_fma_f16 v70, v121, v149, v49
	v_pk_fma_f16 v71, v120, v148, v48
	v_pk_fma_f16 v72, v119, v147, v47
	v_pk_fma_f16 v73, v118, v146, v46
	v_pk_fma_f16 v33, v133, v149, v33
	v_pk_fma_f16 v32, v132, v148, v32
	v_pk_fma_f16 v31, v131, v147, v31
	v_pk_fma_f16 v30, v130, v146, v30
	v_pk_fma_f16 v45, v141, v149, v45
	v_pk_fma_f16 v44, v140, v148, v44
	v_pk_fma_f16 v43, v139, v147, v43
	v_pk_fma_f16 v42, v138, v146, v42
	v_pk_fma_f16 v49, v145, v149, v49
	v_pk_fma_f16 v48, v144, v148, v48
	v_pk_fma_f16 v47, v143, v147, v47
	v_pk_fma_f16 v46, v142, v146, v46
	v_pk_maximum3_f16 v82, v57, v69, v73
	v_pk_maximum3_f16 v83, v56, v68, v72
	v_pk_maximum3_f16 v84, v55, v67, v71
	v_pk_maximum3_f16 v85, v54, v66, v70
	v_pk_maximum3_f16 v87, v31, v43, v47
	v_pk_maximum3_f16 v86, v30, v42, v46
	v_pk_maximum3_f16 v88, v32, v44, v48
	v_pk_maximum3_f16 v89, v33, v45, v49
	v_pk_maximum3_f16 v74, v74, v82, v86
	v_pk_maximum3_f16 v75, v75, v83, v87
	v_pk_maximum3_f16 v76, v76, v84, v88
	v_pk_maximum3_f16 v77, v77, v85, v89
	s_nop 0
	v_pk_add_f16 v18, v18, v74 neg_lo:[0,1] neg_hi:[0,1]
	v_pk_add_f16 v19, v19, v75 neg_lo:[0,1] neg_hi:[0,1]
	v_pk_add_f16 v20, v20, v76 neg_lo:[0,1] neg_hi:[0,1]
	v_pk_add_f16 v21, v21, v77 neg_lo:[0,1] neg_hi:[0,1]
	v_pk_add_f16 v34, v34, v74 neg_lo:[0,1] neg_hi:[0,1]
	v_exp_f16_sdwa v82, v18 dst_sel:WORD_0 dst_unused:UNUSED_PAD src0_sel:WORD_0
	v_exp_f16_sdwa v83, v19 dst_sel:WORD_0 dst_unused:UNUSED_PAD src0_sel:WORD_0
	v_exp_f16_sdwa v84, v20 dst_sel:WORD_0 dst_unused:UNUSED_PAD src0_sel:WORD_0
	v_exp_f16_sdwa v85, v21 dst_sel:WORD_0 dst_unused:UNUSED_PAD src0_sel:WORD_0
	v_exp_f16_sdwa v82, v18 dst_sel:WORD_1 dst_unused:UNUSED_PRESERVE src0_sel:WORD_1
	v_exp_f16_sdwa v83, v19 dst_sel:WORD_1 dst_unused:UNUSED_PRESERVE src0_sel:WORD_1
	v_exp_f16_sdwa v84, v20 dst_sel:WORD_1 dst_unused:UNUSED_PRESERVE src0_sel:WORD_1
	v_exp_f16_sdwa v85, v21 dst_sel:WORD_1 dst_unused:UNUSED_PRESERVE src0_sel:WORD_1
	v_pk_add_f16 v35, v35, v75 neg_lo:[0,1] neg_hi:[0,1]
	v_pk_add_f16 v18, v82, 0
	v_pk_add_f16 v19, v83, 0
	v_pk_add_f16 v20, v84, 0
	v_pk_add_f16 v21, v85, 0
	v_pk_fma_f16 v6, v6, v82, 0
	v_pk_fma_f16 v7, v7, v83, 0
	v_pk_fma_f16 v8, v8, v84, 0
	v_pk_fma_f16 v9, v9, v85, 0
	v_pk_add_f16 v36, v36, v76 neg_lo:[0,1] neg_hi:[0,1]
	v_pk_add_f16 v37, v37, v77 neg_lo:[0,1] neg_hi:[0,1]
	v_exp_f16_sdwa v82, v34 dst_sel:WORD_0 dst_unused:UNUSED_PAD src0_sel:WORD_0
	v_exp_f16_sdwa v83, v35 dst_sel:WORD_0 dst_unused:UNUSED_PAD src0_sel:WORD_0
	v_exp_f16_sdwa v84, v36 dst_sel:WORD_0 dst_unused:UNUSED_PAD src0_sel:WORD_0
	v_exp_f16_sdwa v85, v37 dst_sel:WORD_0 dst_unused:UNUSED_PAD src0_sel:WORD_0
	v_exp_f16_sdwa v82, v34 dst_sel:WORD_1 dst_unused:UNUSED_PRESERVE src0_sel:WORD_1
	v_exp_f16_sdwa v83, v35 dst_sel:WORD_1 dst_unused:UNUSED_PRESERVE src0_sel:WORD_1
	v_exp_f16_sdwa v84, v36 dst_sel:WORD_1 dst_unused:UNUSED_PRESERVE src0_sel:WORD_1
	v_exp_f16_sdwa v85, v37 dst_sel:WORD_1 dst_unused:UNUSED_PRESERVE src0_sel:WORD_1
	s_nop 0
	v_pk_add_f16 v21, v21, v85
	v_pk_add_f16 v20, v20, v84
	v_pk_add_f16 v19, v19, v83
	v_pk_add_f16 v18, v18, v82
	v_pk_fma_f16 v9, v13, v85, v9
	v_pk_fma_f16 v8, v12, v84, v8
	v_pk_fma_f16 v7, v11, v83, v7
	v_pk_fma_f16 v6, v10, v82, v6
	v_pk_add_f16 v10, v53, v74 neg_lo:[0,1] neg_hi:[0,1]
	v_pk_add_f16 v11, v52, v75 neg_lo:[0,1] neg_hi:[0,1]
	v_pk_add_f16 v12, v51, v76 neg_lo:[0,1] neg_hi:[0,1]
	v_pk_add_f16 v13, v50, v77 neg_lo:[0,1] neg_hi:[0,1]
	v_exp_f16_sdwa v34, v10 dst_sel:WORD_0 dst_unused:UNUSED_PAD src0_sel:WORD_0
	v_exp_f16_sdwa v35, v11 dst_sel:WORD_0 dst_unused:UNUSED_PAD src0_sel:WORD_0
	v_exp_f16_sdwa v36, v12 dst_sel:WORD_0 dst_unused:UNUSED_PAD src0_sel:WORD_0
	v_exp_f16_sdwa v37, v13 dst_sel:WORD_0 dst_unused:UNUSED_PAD src0_sel:WORD_0
	v_exp_f16_sdwa v34, v10 dst_sel:WORD_1 dst_unused:UNUSED_PRESERVE src0_sel:WORD_1
	v_exp_f16_sdwa v35, v11 dst_sel:WORD_1 dst_unused:UNUSED_PRESERVE src0_sel:WORD_1
	v_exp_f16_sdwa v36, v12 dst_sel:WORD_1 dst_unused:UNUSED_PRESERVE src0_sel:WORD_1
	v_exp_f16_sdwa v37, v13 dst_sel:WORD_1 dst_unused:UNUSED_PRESERVE src0_sel:WORD_1
	v_pk_add_f16 v10, v18, v34
	v_pk_add_f16 v11, v19, v35
	v_pk_add_f16 v12, v20, v36
	v_pk_add_f16 v13, v21, v37
	v_pk_fma_f16 v6, v14, v34, v6
	v_pk_fma_f16 v7, v15, v35, v7
	v_pk_fma_f16 v8, v16, v36, v8
	v_pk_fma_f16 v9, v17, v37, v9
	v_pk_add_f16 v14, v57, v74 neg_lo:[0,1] neg_hi:[0,1]
	v_pk_add_f16 v15, v56, v75 neg_lo:[0,1] neg_hi:[0,1]
	v_pk_add_f16 v16, v55, v76 neg_lo:[0,1] neg_hi:[0,1]
	v_pk_add_f16 v17, v54, v77 neg_lo:[0,1] neg_hi:[0,1]
	v_exp_f16_sdwa v18, v14 dst_sel:WORD_0 dst_unused:UNUSED_PAD src0_sel:WORD_0
	v_exp_f16_sdwa v19, v15 dst_sel:WORD_0 dst_unused:UNUSED_PAD src0_sel:WORD_0
	v_exp_f16_sdwa v20, v16 dst_sel:WORD_0 dst_unused:UNUSED_PAD src0_sel:WORD_0
	v_exp_f16_sdwa v21, v17 dst_sel:WORD_0 dst_unused:UNUSED_PAD src0_sel:WORD_0
	v_exp_f16_sdwa v18, v14 dst_sel:WORD_1 dst_unused:UNUSED_PRESERVE src0_sel:WORD_1
	v_exp_f16_sdwa v19, v15 dst_sel:WORD_1 dst_unused:UNUSED_PRESERVE src0_sel:WORD_1
	v_exp_f16_sdwa v20, v16 dst_sel:WORD_1 dst_unused:UNUSED_PRESERVE src0_sel:WORD_1
	v_exp_f16_sdwa v21, v17 dst_sel:WORD_1 dst_unused:UNUSED_PRESERVE src0_sel:WORD_1
	v_pk_add_f16 v14, v69, v74 neg_lo:[0,1] neg_hi:[0,1]
	v_pk_add_f16 v13, v13, v21
	v_pk_add_f16 v12, v12, v20
	v_pk_add_f16 v11, v11, v19
	v_pk_add_f16 v10, v10, v18
	v_pk_fma_f16 v9, v29, v21, v9
	v_pk_fma_f16 v8, v28, v20, v8
	v_pk_fma_f16 v7, v27, v19, v7
	v_pk_fma_f16 v6, v26, v18, v6
	v_pk_add_f16 v15, v68, v75 neg_lo:[0,1] neg_hi:[0,1]
	v_pk_add_f16 v16, v67, v76 neg_lo:[0,1] neg_hi:[0,1]
	v_pk_add_f16 v17, v66, v77 neg_lo:[0,1] neg_hi:[0,1]
	v_exp_f16_sdwa v18, v14 dst_sel:WORD_0 dst_unused:UNUSED_PAD src0_sel:WORD_0
	v_exp_f16_sdwa v19, v15 dst_sel:WORD_0 dst_unused:UNUSED_PAD src0_sel:WORD_0
	v_exp_f16_sdwa v20, v16 dst_sel:WORD_0 dst_unused:UNUSED_PAD src0_sel:WORD_0
	v_exp_f16_sdwa v21, v17 dst_sel:WORD_0 dst_unused:UNUSED_PAD src0_sel:WORD_0
	v_exp_f16_sdwa v18, v14 dst_sel:WORD_1 dst_unused:UNUSED_PRESERVE src0_sel:WORD_1
	v_exp_f16_sdwa v19, v15 dst_sel:WORD_1 dst_unused:UNUSED_PRESERVE src0_sel:WORD_1
	v_exp_f16_sdwa v20, v16 dst_sel:WORD_1 dst_unused:UNUSED_PRESERVE src0_sel:WORD_1
	v_exp_f16_sdwa v21, v17 dst_sel:WORD_1 dst_unused:UNUSED_PRESERVE src0_sel:WORD_1
	v_pk_add_f16 v14, v73, v74 neg_lo:[0,1] neg_hi:[0,1]
	v_pk_add_f16 v10, v10, v18
	v_pk_add_f16 v11, v11, v19
	v_pk_add_f16 v12, v12, v20
	v_pk_add_f16 v13, v13, v21
	v_pk_fma_f16 v6, v38, v18, v6
	v_pk_fma_f16 v7, v39, v19, v7
	v_pk_fma_f16 v8, v40, v20, v8
	v_pk_fma_f16 v9, v41, v21, v9
	v_pk_add_f16 v15, v72, v75 neg_lo:[0,1] neg_hi:[0,1]
	v_pk_add_f16 v16, v71, v76 neg_lo:[0,1] neg_hi:[0,1]
	v_pk_add_f16 v17, v70, v77 neg_lo:[0,1] neg_hi:[0,1]
	v_exp_f16_sdwa v18, v14 dst_sel:WORD_0 dst_unused:UNUSED_PAD src0_sel:WORD_0
	v_exp_f16_sdwa v19, v15 dst_sel:WORD_0 dst_unused:UNUSED_PAD src0_sel:WORD_0
	v_exp_f16_sdwa v20, v16 dst_sel:WORD_0 dst_unused:UNUSED_PAD src0_sel:WORD_0
	v_exp_f16_sdwa v21, v17 dst_sel:WORD_0 dst_unused:UNUSED_PAD src0_sel:WORD_0
	v_exp_f16_sdwa v18, v14 dst_sel:WORD_1 dst_unused:UNUSED_PRESERVE src0_sel:WORD_1
	v_exp_f16_sdwa v19, v15 dst_sel:WORD_1 dst_unused:UNUSED_PRESERVE src0_sel:WORD_1
	v_exp_f16_sdwa v20, v16 dst_sel:WORD_1 dst_unused:UNUSED_PRESERVE src0_sel:WORD_1
	v_exp_f16_sdwa v21, v17 dst_sel:WORD_1 dst_unused:UNUSED_PRESERVE src0_sel:WORD_1
	v_pk_add_f16 v14, v30, v74 neg_lo:[0,1] neg_hi:[0,1]
	v_pk_add_f16 v13, v13, v21
	v_pk_add_f16 v12, v12, v20
	v_pk_add_f16 v11, v11, v19
	v_pk_add_f16 v10, v10, v18
	v_pk_fma_f16 v9, v61, v21, v9
	v_pk_fma_f16 v8, v60, v20, v8
	v_pk_fma_f16 v7, v59, v19, v7
	v_pk_fma_f16 v6, v58, v18, v6
	v_pk_add_f16 v15, v31, v75 neg_lo:[0,1] neg_hi:[0,1]
	v_pk_add_f16 v16, v32, v76 neg_lo:[0,1] neg_hi:[0,1]
	v_pk_add_f16 v17, v33, v77 neg_lo:[0,1] neg_hi:[0,1]
	v_exp_f16_sdwa v18, v14 dst_sel:WORD_0 dst_unused:UNUSED_PAD src0_sel:WORD_0
	v_exp_f16_sdwa v19, v15 dst_sel:WORD_0 dst_unused:UNUSED_PAD src0_sel:WORD_0
	v_exp_f16_sdwa v20, v16 dst_sel:WORD_0 dst_unused:UNUSED_PAD src0_sel:WORD_0
	v_exp_f16_sdwa v21, v17 dst_sel:WORD_0 dst_unused:UNUSED_PAD src0_sel:WORD_0
	v_exp_f16_sdwa v18, v14 dst_sel:WORD_1 dst_unused:UNUSED_PRESERVE src0_sel:WORD_1
	v_exp_f16_sdwa v19, v15 dst_sel:WORD_1 dst_unused:UNUSED_PRESERVE src0_sel:WORD_1
	v_exp_f16_sdwa v20, v16 dst_sel:WORD_1 dst_unused:UNUSED_PRESERVE src0_sel:WORD_1
	v_exp_f16_sdwa v21, v17 dst_sel:WORD_1 dst_unused:UNUSED_PRESERVE src0_sel:WORD_1
	v_pk_add_f16 v10, v10, v18
	v_pk_add_f16 v11, v11, v19
	v_pk_add_f16 v12, v12, v20
	v_pk_add_f16 v13, v13, v21
	v_pk_fma_f16 v14, v78, v18, v6
	v_pk_fma_f16 v15, v79, v19, v7
	v_pk_fma_f16 v16, v80, v20, v8
	v_pk_fma_f16 v17, v81, v21, v9
	v_pk_add_f16 v6, v42, v74 neg_lo:[0,1] neg_hi:[0,1]
	v_pk_add_f16 v7, v43, v75 neg_lo:[0,1] neg_hi:[0,1]
	v_pk_add_f16 v8, v44, v76 neg_lo:[0,1] neg_hi:[0,1]
	v_pk_add_f16 v9, v45, v77 neg_lo:[0,1] neg_hi:[0,1]
	v_exp_f16_sdwa v18, v6 dst_sel:WORD_0 dst_unused:UNUSED_PAD src0_sel:WORD_0
	v_exp_f16_sdwa v19, v7 dst_sel:WORD_0 dst_unused:UNUSED_PAD src0_sel:WORD_0
	v_exp_f16_sdwa v20, v8 dst_sel:WORD_0 dst_unused:UNUSED_PAD src0_sel:WORD_0
	v_exp_f16_sdwa v21, v9 dst_sel:WORD_0 dst_unused:UNUSED_PAD src0_sel:WORD_0
	v_exp_f16_sdwa v18, v6 dst_sel:WORD_1 dst_unused:UNUSED_PRESERVE src0_sel:WORD_1
	v_exp_f16_sdwa v19, v7 dst_sel:WORD_1 dst_unused:UNUSED_PRESERVE src0_sel:WORD_1
	v_exp_f16_sdwa v20, v8 dst_sel:WORD_1 dst_unused:UNUSED_PRESERVE src0_sel:WORD_1
	v_exp_f16_sdwa v21, v9 dst_sel:WORD_1 dst_unused:UNUSED_PRESERVE src0_sel:WORD_1
	s_nop 0
	v_pk_add_f16 v9, v13, v21
	v_pk_add_f16 v8, v12, v20
	v_pk_add_f16 v7, v11, v19
	v_pk_add_f16 v6, v10, v18
	v_pk_fma_f16 v13, v93, v21, v17
	v_pk_fma_f16 v12, v92, v20, v16
	v_pk_fma_f16 v11, v91, v19, v15
	v_pk_fma_f16 v10, v90, v18, v14
	v_pk_add_f16 v18, v46, v74 neg_lo:[0,1] neg_hi:[0,1]
	v_pk_add_f16 v19, v47, v75 neg_lo:[0,1] neg_hi:[0,1]
	v_pk_add_f16 v20, v48, v76 neg_lo:[0,1] neg_hi:[0,1]
	v_pk_add_f16 v21, v49, v77 neg_lo:[0,1] neg_hi:[0,1]
	v_exp_f16_sdwa v14, v18 dst_sel:WORD_0 dst_unused:UNUSED_PAD src0_sel:WORD_0
	v_exp_f16_sdwa v17, v19 dst_sel:WORD_0 dst_unused:UNUSED_PAD src0_sel:WORD_0
	v_exp_f16_sdwa v15, v20 dst_sel:WORD_0 dst_unused:UNUSED_PAD src0_sel:WORD_0
	v_exp_f16_sdwa v16, v21 dst_sel:WORD_0 dst_unused:UNUSED_PAD src0_sel:WORD_0
	v_exp_f16_sdwa v14, v18 dst_sel:WORD_1 dst_unused:UNUSED_PRESERVE src0_sel:WORD_1
	v_exp_f16_sdwa v17, v19 dst_sel:WORD_1 dst_unused:UNUSED_PRESERVE src0_sel:WORD_1
	v_exp_f16_sdwa v15, v20 dst_sel:WORD_1 dst_unused:UNUSED_PRESERVE src0_sel:WORD_1
	v_exp_f16_sdwa v16, v21 dst_sel:WORD_1 dst_unused:UNUSED_PRESERVE src0_sel:WORD_1
	s_nop 0
.LBB3_45:
	s_and_b64 vcc, exec, s[4:5]
	s_cbranch_vccz .LBB3_6
	s_load_dwordx2 s[0:1], s[22:23], 0x18
	s_waitcnt lgkmcnt(0)
	s_load_dwordx2 s[6:7], s[0:1], 0x0
	s_load_dword s28, s[0:1], 0x8
	v_cmp_lt_u32_e64 s[64:65], 0, v182
	v_cmp_gt_u32_e64 s[66:67], 63, v182
	v_cmp_lt_u32_e64 s[68:69], 0, v162
	v_cmp_gt_u32_e64 s[70:71], 60, v162
	buffer_load_dwordx4 v[184:187], v180, s[16:19], 0 offen
	s_and_b64 s[72:73], s[68:69], s[64:65]
	s_and_b64 s[74:75], s[68:69], s[66:67]
	s_and_b64 s[76:77], s[70:71], s[64:65]
	s_and_b64 s[78:79], s[70:71], s[66:67]
	v_mov_b32_e32 v110, v172
	v_mov_b32_e32 v111, v174
	v_mov_b32_e32 v112, v176
	v_mov_b32_e32 v113, v178
	v_mov_b32_e32 v78, v173
	v_mov_b32_e32 v79, v175
	v_mov_b32_e32 v80, v177
	v_mov_b32_e32 v81, v179
	v_mov_b32_e32 v126, v172
	v_mov_b32_e32 v127, v174
	v_mov_b32_e32 v128, v176
	v_mov_b32_e32 v129, v178
	v_mov_b32_e32 v102, v173
	v_mov_b32_e32 v103, v175
	v_mov_b32_e32 v104, v177
	v_mov_b32_e32 v105, v179
	v_mov_b32_e32 v138, v172
	v_mov_b32_e32 v139, v174
	v_mov_b32_e32 v140, v176
	v_mov_b32_e32 v141, v178
	v_mov_b32_e32 v118, v173
	v_mov_b32_e32 v119, v175
	v_mov_b32_e32 v120, v177
	v_mov_b32_e32 v121, v179
	v_mov_b32_e32 v86, v172
	v_mov_b32_e32 v87, v174
	v_mov_b32_e32 v88, v176
	v_mov_b32_e32 v89, v178
	v_mov_b32_e32 v46, v173
	v_mov_b32_e32 v47, v175
	v_mov_b32_e32 v48, v177
	v_mov_b32_e32 v49, v179
	v_mov_b32_e32 v122, v172
	v_mov_b32_e32 v123, v174
	v_mov_b32_e32 v124, v176
	v_mov_b32_e32 v125, v178
	v_mov_b32_e32 v82, v173
	v_mov_b32_e32 v83, v175
	v_mov_b32_e32 v84, v177
	v_mov_b32_e32 v85, v179
	v_mov_b32_e32 v50, v172
	v_mov_b32_e32 v51, v174
	v_mov_b32_e32 v52, v176
	v_mov_b32_e32 v53, v178
	v_mov_b32_e32 v22, v173
	v_mov_b32_e32 v23, v175
	v_mov_b32_e32 v24, v177
	v_mov_b32_e32 v25, v179
	v_mov_b32_e32 v94, v172
	v_mov_b32_e32 v95, v174
	v_mov_b32_e32 v96, v176
	v_mov_b32_e32 v97, v178
	v_mov_b32_e32 v42, v173
	v_mov_b32_e32 v43, v175
	v_mov_b32_e32 v44, v177
	v_mov_b32_e32 v45, v179
	v_mov_b32_e32 v18, v172
	v_mov_b32_e32 v19, v174
	v_mov_b32_e32 v20, v176
	v_mov_b32_e32 v21, v178
	v_mov_b32_e32 v6, v173
	v_mov_b32_e32 v7, v175
	v_mov_b32_e32 v8, v177
	v_mov_b32_e32 v9, v179
	v_mov_b32_e32 v54, v172
	v_mov_b32_e32 v55, v174
	v_mov_b32_e32 v56, v176
	v_mov_b32_e32 v57, v178
	v_mov_b32_e32 v14, v173
	v_mov_b32_e32 v15, v175
	v_mov_b32_e32 v16, v177
	v_mov_b32_e32 v17, v179
	v_mov_b32_e32 v74, v172
	v_mov_b32_e32 v75, v174
	v_mov_b32_e32 v76, v176
	v_mov_b32_e32 v77, v178
	v_mov_b32_e32 v26, v173
	v_mov_b32_e32 v27, v175
	v_mov_b32_e32 v28, v177
	v_mov_b32_e32 v29, v179
	v_mov_b32_e32 v114, v172
	v_mov_b32_e32 v115, v174
	v_mov_b32_e32 v116, v176
	v_mov_b32_e32 v117, v178
	v_mov_b32_e32 v58, v173
	v_mov_b32_e32 v59, v175
	v_mov_b32_e32 v60, v177
	v_mov_b32_e32 v61, v179
	v_mov_b32_e32 v130, v172
	v_mov_b32_e32 v131, v174
	v_mov_b32_e32 v132, v176
	v_mov_b32_e32 v133, v178
	v_mov_b32_e32 v70, v173
	v_mov_b32_e32 v71, v175
	v_mov_b32_e32 v72, v177
	v_mov_b32_e32 v73, v179
	v_mov_b32_e32 v134, v172
	v_mov_b32_e32 v135, v174
	v_mov_b32_e32 v136, v176
	v_mov_b32_e32 v137, v178
	v_mov_b32_e32 v90, v173
	v_mov_b32_e32 v91, v175
	v_mov_b32_e32 v92, v177
	v_mov_b32_e32 v93, v179
	v_mov_b32_e32 v142, v172
	v_mov_b32_e32 v143, v174
	v_mov_b32_e32 v144, v176
	v_mov_b32_e32 v145, v178
	v_mov_b32_e32 v2, v173
	v_mov_b32_e32 v3, v175
	v_mov_b32_e32 v4, v177
	v_mov_b32_e32 v5, v179
	v_add_u32_e32 v249, 0xfffe7c00, v180
	v_add_u32_e32 v250, 0xfffe8000, v180
	s_mov_b64 exec, s[72:73]
	buffer_load_dwordx4 v[110:113], v249, s[16:19], 0 offen
	buffer_load_dwordx4 v[78:81], v249, s[16:19], 0 offen offset:512
	s_mov_b64 exec, -1
	s_mov_b64 exec, s[68:69]
	buffer_load_dwordx4 v[126:129], v250, s[16:19], 0 offen offset:512
	buffer_load_dwordx4 v[102:105], v250, s[16:19], 0 offen offset:1024
	s_mov_b64 exec, -1
	s_mov_b64 exec, s[74:75]
	buffer_load_dwordx4 v[138:141], v250, s[16:19], 0 offen offset:2048
	buffer_load_dwordx4 v[118:121], v250, s[16:19], 0 offen offset:2560
	s_mov_b64 exec, -1
	v_add_u32_e32 v249, 0xfffffc00, v180
	s_mov_b64 exec, s[64:65]
	buffer_load_dwordx4 v[86:89], v249, s[16:19], 0 offen
	buffer_load_dwordx4 v[46:49], v249, s[16:19], 0 offen offset:512
	s_mov_b64 exec, -1
	buffer_load_dwordx4 v[106:109], v180, s[16:19], 0 offen offset:512
	buffer_load_dwordx4 v[62:65], v180, s[16:19], 0 offen offset:1024
	s_mov_b64 exec, s[66:67]
	buffer_load_dwordx4 v[122:125], v180, s[16:19], 0 offen offset:2048
	buffer_load_dwordx4 v[82:85], v180, s[16:19], 0 offen offset:2560
	s_mov_b64 exec, -1
	v_add_u32_e32 v249, 0x17c00, v180
	v_add_u32_e32 v250, 0x18000, v180
	s_mov_b64 exec, s[64:65]
	buffer_load_dwordx4 v[50:53], v249, s[16:19], 0 offen
	buffer_load_dwordx4 v[22:25], v249, s[16:19], 0 offen offset:512
	s_mov_b64 exec, -1
	buffer_load_dwordx4 v[66:69], v250, s[16:19], 0 offen offset:512
	buffer_load_dwordx4 v[34:37], v250, s[16:19], 0 offen offset:1024
	s_mov_b64 exec, s[66:67]
	buffer_load_dwordx4 v[94:97], v250, s[16:19], 0 offen offset:2048
	buffer_load_dwordx4 v[42:45], v250, s[16:19], 0 offen offset:2560
	s_mov_b64 exec, -1
	v_add_u32_e32 v249, 0x18000, v180
	buffer_load_dwordx4 v[154:157], v249, s[16:19], 0 offen
	v_add_u32_e32 v250, 0x30000, v180
	buffer_load_dwordx4 v[150:153], v250, s[16:19], 0 offen
	v_add_u32_e32 v249, 0x48000, v180
	buffer_load_dwordx4 v[146:149], v249, s[16:19], 0 offen
	v_add_u32_e32 v249, 0x2fc00, v180
	v_add_u32_e32 v250, 0x30000, v180
	v_add_u32_e32 v251, 0x47c00, v180
	v_add_u32_e32 v252, 0x48000, v180
	v_add_u32_e32 v253, 0x5fc00, v180
	v_add_u32_e32 v254, 0x60000, v180
	s_branch .LBB3_5

	.amdhsa_kernel _Z7k_stageILi0ELi8EEv8AttnArgsPKDF16_PKfPDF16_iii
		.amdhsa_group_segment_fixed_size 115712
		.amdhsa_private_segment_fixed_size 0
		.amdhsa_kernarg_size 148
		.amdhsa_user_sgpr_count 2
		.amdhsa_user_sgpr_dispatch_ptr 0
		.amdhsa_user_sgpr_queue_ptr 0
		.amdhsa_user_sgpr_kernarg_segment_ptr 1
		.amdhsa_user_sgpr_dispatch_id 0
		.amdhsa_user_sgpr_kernarg_preload_length 0
		.amdhsa_user_sgpr_kernarg_preload_offset 0
		.amdhsa_user_sgpr_private_segment_size 0
		.amdhsa_uses_dynamic_stack 0
		.amdhsa_enable_private_segment 0
		.amdhsa_system_sgpr_workgroup_id_x 1
		.amdhsa_system_sgpr_workgroup_id_y 1
		.amdhsa_system_sgpr_workgroup_id_z 0
		.amdhsa_system_sgpr_workgroup_info 0
		.amdhsa_system_vgpr_workitem_id 0
		.amdhsa_next_free_vgpr 255
		.amdhsa_next_free_sgpr 96
		.amdhsa_accum_offset 256
		.amdhsa_reserve_vcc 1
		.amdhsa_float_round_mode_32 0
		.amdhsa_float_round_mode_16_64 0
		.amdhsa_float_denorm_mode_32 3
		.amdhsa_float_denorm_mode_16_64 3
		.amdhsa_dx10_clamp 1
		.amdhsa_ieee_mode 1
		.amdhsa_fp16_overflow 0
		.amdhsa_tg_split 0
		.amdhsa_exception_fp_ieee_invalid_op 0
		.amdhsa_exception_fp_denorm_src 0
		.amdhsa_exception_fp_ieee_div_zero 0
		.amdhsa_exception_fp_ieee_overflow 0
		.amdhsa_exception_fp_ieee_underflow 0
		.amdhsa_exception_fp_ieee_inexact 0
		.amdhsa_exception_int_div_zero 0
	.end_amdhsa_kernel

.LBB4_2:
	s_waitcnt vmcnt(3)
	v_pk_mul_f16 v161, v160, v162 op_sel_hi:[0,1]
	v_pk_mul_f16 v206, v160, v165 op_sel_hi:[0,1]
	v_pk_mul_f16 v210, v158, v165 op_sel_hi:[0,1]
	v_pk_mul_f16 v214, v159, v165 op_sel_hi:[0,1]
	v_pk_mul_f16 v200, v160, v163 op_sel_hi:[0,1]
	v_pk_mul_f16 v201, v160, v164 op_sel_hi:[0,1]
	v_pk_mul_f16 v207, v158, v162 op_sel_hi:[0,1]
	s_mov_b64 exec, s[64:65]
	buffer_load_dwordx4 v[26:29], v245, s[12:15], 0 offen
	buffer_load_dwordx4 v[10:13], v245, s[12:15], 0 offen offset:512
	s_mov_b64 exec, -1
	v_pk_mul_f16 v208, v158, v163 op_sel_hi:[0,1]
	v_pk_mul_f16 v209, v158, v164 op_sel_hi:[0,1]
	v_pk_mul_f16 v211, v159, v162 op_sel_hi:[0,1]
	v_pk_mul_f16 v212, v159, v163 op_sel_hi:[0,1]
	v_pk_mul_f16 v213, v159, v164 op_sel_hi:[0,1]
	v_pk_fma_f16 v117, v117, v165, v206
	v_pk_fma_f16 v114, v114, v162, v161
	v_pk_fma_f16 v133, v133, v165, v206
	v_pk_fma_f16 v130, v130, v162, v161
	v_pk_fma_f16 v141, v141, v165, v206
	v_pk_fma_f16 v138, v138, v162, v161
	v_pk_fma_f16 v161, v89, v165, v210
	v_pk_fma_f16 v215, v113, v165, v210
	buffer_load_dwordx4 v[38:41], v246, s[12:15], 0 offen offset:512
	buffer_load_dwordx4 v[14:17], v246, s[12:15], 0 offen offset:1024
	v_pk_fma_f16 v210, v129, v165, v210
	v_pk_fma_f16 v219, v57, v165, v214
	v_pk_fma_f16 v223, v77, v165, v214
	v_pk_fma_f16 v165, v101, v165, v214
	v_pk_maximum3_f16 v214, v117, v133, v141
	v_pk_fma_f16 v116, v116, v164, v201
	v_pk_fma_f16 v115, v115, v163, v200
	v_pk_fma_f16 v132, v132, v164, v201
	v_pk_fma_f16 v131, v131, v163, v200
	v_pk_fma_f16 v140, v140, v164, v201
	v_pk_fma_f16 v139, v139, v163, v200
	v_pk_fma_f16 v200, v88, v164, v209
	v_pk_fma_f16 v201, v87, v163, v208
	v_pk_fma_f16 v206, v86, v162, v207
	v_pk_fma_f16 v216, v112, v164, v209
	v_pk_fma_f16 v217, v111, v163, v208
	s_mov_b64 exec, s[66:67]
	buffer_load_dwordx4 v[58:61], v246, s[12:15], 0 offen offset:2048
	buffer_load_dwordx4 v[18:21], v246, s[12:15], 0 offen offset:2560
	s_mov_b64 exec, -1
	v_pk_fma_f16 v218, v110, v162, v207
	v_pk_fma_f16 v209, v128, v164, v209
	v_pk_fma_f16 v208, v127, v163, v208
	v_pk_fma_f16 v207, v126, v162, v207
	v_pk_fma_f16 v220, v56, v164, v213
	v_pk_fma_f16 v221, v55, v163, v212
	v_pk_fma_f16 v222, v54, v162, v211
	v_pk_fma_f16 v224, v76, v164, v213
	v_pk_fma_f16 v225, v75, v163, v212
	v_pk_fma_f16 v226, v74, v162, v211
	v_pk_fma_f16 v164, v100, v164, v213
	v_pk_fma_f16 v163, v99, v163, v212
	v_pk_fma_f16 v162, v98, v162, v211
	v_pk_maximum3_f16 v211, v114, v130, v138
	v_pk_maximum3_f16 v212, v115, v131, v139
	v_pk_maximum3_f16 v213, v116, v132, v140
	v_pk_maximum3_f16 v230, v161, v215, v210
	v_pk_maximum3_f16 v234, v219, v223, v165
	v_pk_maximum3_f16 v227, v206, v218, v207
	v_pk_maximum3_f16 v228, v201, v217, v208
	v_pk_maximum3_f16 v229, v200, v216, v209
	v_pk_maximum3_f16 v231, v222, v226, v162
	v_pk_maximum3_f16 v232, v221, v225, v163
	v_pk_maximum3_f16 v214, v214, v230, v234
	v_pk_maximum3_f16 v233, v220, v224, v164
	v_pk_maximum3_f16 v211, v211, v227, v231
	v_pk_maximum3_f16 v212, v212, v228, v232
	v_pk_maximum3_f16 v213, v213, v229, v233
	v_pk_add_f16 v117, v117, v214 neg_lo:[0,1] neg_hi:[0,1]
	s_mov_b64 exec, s[64:65]
	buffer_load_dwordx4 v[78:81], v247, s[12:15], 0 offen
	buffer_load_dwordx4 v[30:33], v247, s[12:15], 0 offen offset:512
	s_mov_b64 exec, -1
	v_pk_add_f16 v114, v114, v211 neg_lo:[0,1] neg_hi:[0,1]
	v_pk_add_f16 v115, v115, v212 neg_lo:[0,1] neg_hi:[0,1]
	v_pk_add_f16 v116, v116, v213 neg_lo:[0,1] neg_hi:[0,1]
	v_pk_add_f16 v130, v130, v211 neg_lo:[0,1] neg_hi:[0,1]
	v_exp_f16_sdwa v227, v114 dst_sel:WORD_0 dst_unused:UNUSED_PAD src0_sel:WORD_0
	v_exp_f16_sdwa v228, v115 dst_sel:WORD_0 dst_unused:UNUSED_PAD src0_sel:WORD_0
	v_exp_f16_sdwa v229, v116 dst_sel:WORD_0 dst_unused:UNUSED_PAD src0_sel:WORD_0
	v_exp_f16_sdwa v230, v117 dst_sel:WORD_0 dst_unused:UNUSED_PAD src0_sel:WORD_0
	v_exp_f16_sdwa v227, v114 dst_sel:WORD_1 dst_unused:UNUSED_PRESERVE src0_sel:WORD_1
	v_exp_f16_sdwa v228, v115 dst_sel:WORD_1 dst_unused:UNUSED_PRESERVE src0_sel:WORD_1
	v_exp_f16_sdwa v229, v116 dst_sel:WORD_1 dst_unused:UNUSED_PRESERVE src0_sel:WORD_1
	v_exp_f16_sdwa v230, v117 dst_sel:WORD_1 dst_unused:UNUSED_PRESERVE src0_sel:WORD_1
	v_pk_add_f16 v131, v131, v212 neg_lo:[0,1] neg_hi:[0,1]
	v_pk_add_f16 v117, v227, 0
	v_pk_fma_f16 v73, v73, v230, 0
	v_pk_add_f16 v114, v230, 0
	v_pk_add_f16 v115, v229, 0
	v_pk_add_f16 v116, v228, 0
	v_pk_fma_f16 v72, v72, v229, 0
	v_pk_fma_f16 v71, v71, v228, 0
	v_pk_fma_f16 v70, v70, v227, 0
	v_pk_add_f16 v132, v132, v213 neg_lo:[0,1] neg_hi:[0,1]
	buffer_load_dwordx4 v[106:109], v248, s[12:15], 0 offen offset:512
	buffer_load_dwordx4 v[46:49], v248, s[12:15], 0 offen offset:1024
	v_pk_add_f16 v133, v133, v214 neg_lo:[0,1] neg_hi:[0,1]
	v_exp_f16_sdwa v227, v130 dst_sel:WORD_0 dst_unused:UNUSED_PAD src0_sel:WORD_0
	v_exp_f16_sdwa v228, v131 dst_sel:WORD_0 dst_unused:UNUSED_PAD src0_sel:WORD_0
	v_exp_f16_sdwa v229, v132 dst_sel:WORD_0 dst_unused:UNUSED_PAD src0_sel:WORD_0
	v_exp_f16_sdwa v230, v133 dst_sel:WORD_0 dst_unused:UNUSED_PAD src0_sel:WORD_0
	v_exp_f16_sdwa v227, v130 dst_sel:WORD_1 dst_unused:UNUSED_PRESERVE src0_sel:WORD_1
	v_exp_f16_sdwa v228, v131 dst_sel:WORD_1 dst_unused:UNUSED_PRESERVE src0_sel:WORD_1
	v_exp_f16_sdwa v229, v132 dst_sel:WORD_1 dst_unused:UNUSED_PRESERVE src0_sel:WORD_1
	v_exp_f16_sdwa v230, v133 dst_sel:WORD_1 dst_unused:UNUSED_PRESERVE src0_sel:WORD_1
	v_pk_add_f16 v117, v117, v227
	v_pk_fma_f16 v73, v97, v230, v73
	v_pk_add_f16 v97, v141, v214 neg_lo:[0,1] neg_hi:[0,1]
	v_pk_add_f16 v116, v116, v228
	v_pk_add_f16 v115, v115, v229
	v_pk_add_f16 v114, v114, v230
	v_pk_fma_f16 v70, v94, v227, v70
	v_pk_fma_f16 v71, v95, v228, v71
	v_pk_fma_f16 v72, v96, v229, v72
	v_pk_add_f16 v94, v138, v211 neg_lo:[0,1] neg_hi:[0,1]
	v_pk_add_f16 v95, v139, v212 neg_lo:[0,1] neg_hi:[0,1]
	v_pk_add_f16 v96, v140, v213 neg_lo:[0,1] neg_hi:[0,1]
	v_exp_f16_sdwa v130, v94 dst_sel:WORD_0 dst_unused:UNUSED_PAD src0_sel:WORD_0
	v_exp_f16_sdwa v131, v95 dst_sel:WORD_0 dst_unused:UNUSED_PAD src0_sel:WORD_0
	v_exp_f16_sdwa v132, v96 dst_sel:WORD_0 dst_unused:UNUSED_PAD src0_sel:WORD_0
	v_exp_f16_sdwa v133, v97 dst_sel:WORD_0 dst_unused:UNUSED_PAD src0_sel:WORD_0
	v_exp_f16_sdwa v130, v94 dst_sel:WORD_1 dst_unused:UNUSED_PRESERVE src0_sel:WORD_1
	v_exp_f16_sdwa v131, v95 dst_sel:WORD_1 dst_unused:UNUSED_PRESERVE src0_sel:WORD_1
	v_exp_f16_sdwa v132, v96 dst_sel:WORD_1 dst_unused:UNUSED_PRESERVE src0_sel:WORD_1
	v_exp_f16_sdwa v133, v97 dst_sel:WORD_1 dst_unused:UNUSED_PRESERVE src0_sel:WORD_1
	v_pk_add_f16 v97, v117, v130
	v_pk_add_f16 v94, v114, v133
	s_mov_b64 exec, s[66:67]
	buffer_load_dwordx4 v[122:125], v248, s[12:15], 0 offen offset:2048
	buffer_load_dwordx4 v[62:65], v248, s[12:15], 0 offen offset:2560
	s_mov_b64 exec, -1
	v_pk_add_f16 v95, v115, v132
	v_pk_add_f16 v96, v116, v131
	v_pk_fma_f16 v73, v121, v133, v73
	v_pk_fma_f16 v72, v120, v132, v72
	v_pk_fma_f16 v71, v119, v131, v71
	v_pk_fma_f16 v70, v118, v130, v70
	v_pk_add_f16 v114, v206, v211 neg_lo:[0,1] neg_hi:[0,1]
	v_pk_add_f16 v115, v201, v212 neg_lo:[0,1] neg_hi:[0,1]
	v_pk_add_f16 v116, v200, v213 neg_lo:[0,1] neg_hi:[0,1]
	v_pk_add_f16 v117, v161, v214 neg_lo:[0,1] neg_hi:[0,1]
	v_exp_f16_sdwa v118, v114 dst_sel:WORD_0 dst_unused:UNUSED_PAD src0_sel:WORD_0
	v_exp_f16_sdwa v119, v115 dst_sel:WORD_0 dst_unused:UNUSED_PAD src0_sel:WORD_0
	v_exp_f16_sdwa v120, v116 dst_sel:WORD_0 dst_unused:UNUSED_PAD src0_sel:WORD_0
	v_exp_f16_sdwa v121, v117 dst_sel:WORD_0 dst_unused:UNUSED_PAD src0_sel:WORD_0
	v_exp_f16_sdwa v118, v114 dst_sel:WORD_1 dst_unused:UNUSED_PRESERVE src0_sel:WORD_1
	v_exp_f16_sdwa v119, v115 dst_sel:WORD_1 dst_unused:UNUSED_PRESERVE src0_sel:WORD_1
	v_exp_f16_sdwa v120, v116 dst_sel:WORD_1 dst_unused:UNUSED_PRESERVE src0_sel:WORD_1
	v_exp_f16_sdwa v121, v117 dst_sel:WORD_1 dst_unused:UNUSED_PRESERVE src0_sel:WORD_1
	v_pk_add_f16 v114, v218, v211 neg_lo:[0,1] neg_hi:[0,1]
	v_pk_add_f16 v97, v97, v118
	v_pk_add_f16 v96, v96, v119
	v_pk_add_f16 v95, v95, v120
	s_mov_b64 exec, s[76:77]
	buffer_load_dwordx4 v[134:137], v249, s[12:15], 0 offen
	buffer_load_dwordx4 v[82:85], v249, s[12:15], 0 offen offset:512
	s_mov_b64 exec, -1
	v_pk_add_f16 v94, v94, v121
	v_pk_fma_f16 v70, v42, v118, v70
	v_pk_fma_f16 v71, v43, v119, v71
	v_pk_fma_f16 v72, v44, v120, v72
	v_pk_fma_f16 v73, v45, v121, v73
	v_pk_add_f16 v115, v217, v212 neg_lo:[0,1] neg_hi:[0,1]
	v_pk_add_f16 v116, v216, v213 neg_lo:[0,1] neg_hi:[0,1]
	v_pk_add_f16 v117, v215, v214 neg_lo:[0,1] neg_hi:[0,1]
	v_exp_f16_sdwa v118, v114 dst_sel:WORD_0 dst_unused:UNUSED_PAD src0_sel:WORD_0
	v_exp_f16_sdwa v119, v115 dst_sel:WORD_0 dst_unused:UNUSED_PAD src0_sel:WORD_0
	v_exp_f16_sdwa v120, v116 dst_sel:WORD_0 dst_unused:UNUSED_PAD src0_sel:WORD_0
	v_exp_f16_sdwa v121, v117 dst_sel:WORD_0 dst_unused:UNUSED_PAD src0_sel:WORD_0
	v_exp_f16_sdwa v118, v114 dst_sel:WORD_1 dst_unused:UNUSED_PRESERVE src0_sel:WORD_1
	v_exp_f16_sdwa v119, v115 dst_sel:WORD_1 dst_unused:UNUSED_PRESERVE src0_sel:WORD_1
	v_exp_f16_sdwa v120, v116 dst_sel:WORD_1 dst_unused:UNUSED_PRESERVE src0_sel:WORD_1
	v_exp_f16_sdwa v121, v117 dst_sel:WORD_1 dst_unused:UNUSED_PRESERVE src0_sel:WORD_1
	v_pk_add_f16 v114, v207, v211 neg_lo:[0,1] neg_hi:[0,1]
	v_pk_add_f16 v97, v97, v118
	v_pk_add_f16 v94, v94, v121
	v_pk_add_f16 v95, v95, v120
	v_pk_add_f16 v96, v96, v119
	v_pk_fma_f16 v73, v69, v121, v73
	v_pk_fma_f16 v72, v68, v120, v72
	s_mov_b64 exec, s[70:71]
	buffer_load_dwordx4 v[142:145], v250, s[12:15], 0 offen offset:512
	buffer_load_dwordx4 v[102:105], v250, s[12:15], 0 offen offset:1024
	s_mov_b64 exec, -1
	v_pk_fma_f16 v71, v67, v119, v71
	v_pk_fma_f16 v70, v66, v118, v70
	v_pk_add_f16 v115, v208, v212 neg_lo:[0,1] neg_hi:[0,1]
	v_pk_add_f16 v116, v209, v213 neg_lo:[0,1] neg_hi:[0,1]
	v_pk_add_f16 v117, v210, v214 neg_lo:[0,1] neg_hi:[0,1]
	v_exp_f16_sdwa v118, v114 dst_sel:WORD_0 dst_unused:UNUSED_PAD src0_sel:WORD_0
	v_exp_f16_sdwa v119, v115 dst_sel:WORD_0 dst_unused:UNUSED_PAD src0_sel:WORD_0
	v_exp_f16_sdwa v120, v116 dst_sel:WORD_0 dst_unused:UNUSED_PAD src0_sel:WORD_0
	v_exp_f16_sdwa v121, v117 dst_sel:WORD_0 dst_unused:UNUSED_PAD src0_sel:WORD_0
	v_exp_f16_sdwa v118, v114 dst_sel:WORD_1 dst_unused:UNUSED_PRESERVE src0_sel:WORD_1
	v_exp_f16_sdwa v119, v115 dst_sel:WORD_1 dst_unused:UNUSED_PRESERVE src0_sel:WORD_1
	v_exp_f16_sdwa v120, v116 dst_sel:WORD_1 dst_unused:UNUSED_PRESERVE src0_sel:WORD_1
	v_exp_f16_sdwa v121, v117 dst_sel:WORD_1 dst_unused:UNUSED_PRESERVE src0_sel:WORD_1
	v_pk_add_f16 v114, v222, v211 neg_lo:[0,1] neg_hi:[0,1]
	v_pk_add_f16 v97, v97, v118
	v_pk_add_f16 v96, v96, v119
	v_pk_add_f16 v95, v95, v120
	v_pk_add_f16 v94, v94, v121
	v_pk_fma_f16 v70, v90, v118, v70
	v_pk_fma_f16 v71, v91, v119, v71
	v_pk_fma_f16 v72, v92, v120, v72
	v_pk_fma_f16 v73, v93, v121, v73
	s_mov_b64 exec, s[78:79]
	buffer_load_dwordx4 v[6:9], v250, s[12:15], 0 offen offset:2048
	buffer_load_dwordx4 v[2:5], v250, s[12:15], 0 offen offset:2560
	s_mov_b64 exec, -1
	v_pk_add_f16 v115, v221, v212 neg_lo:[0,1] neg_hi:[0,1]
	v_pk_add_f16 v116, v220, v213 neg_lo:[0,1] neg_hi:[0,1]
	v_pk_add_f16 v117, v219, v214 neg_lo:[0,1] neg_hi:[0,1]
	v_exp_f16_sdwa v118, v114 dst_sel:WORD_0 dst_unused:UNUSED_PAD src0_sel:WORD_0
	v_exp_f16_sdwa v119, v115 dst_sel:WORD_0 dst_unused:UNUSED_PAD src0_sel:WORD_0
	v_exp_f16_sdwa v120, v116 dst_sel:WORD_0 dst_unused:UNUSED_PAD src0_sel:WORD_0
	v_exp_f16_sdwa v121, v117 dst_sel:WORD_0 dst_unused:UNUSED_PAD src0_sel:WORD_0
	v_exp_f16_sdwa v118, v114 dst_sel:WORD_1 dst_unused:UNUSED_PRESERVE src0_sel:WORD_1
	v_exp_f16_sdwa v119, v115 dst_sel:WORD_1 dst_unused:UNUSED_PRESERVE src0_sel:WORD_1
	v_exp_f16_sdwa v120, v116 dst_sel:WORD_1 dst_unused:UNUSED_PRESERVE src0_sel:WORD_1
	v_exp_f16_sdwa v121, v117 dst_sel:WORD_1 dst_unused:UNUSED_PRESERVE src0_sel:WORD_1
	v_pk_add_f16 v114, v226, v211 neg_lo:[0,1] neg_hi:[0,1]
	v_pk_add_f16 v97, v97, v118
	v_pk_add_f16 v94, v94, v121
	v_pk_add_f16 v95, v95, v120
	v_pk_add_f16 v96, v96, v119
	v_pk_fma_f16 v73, v25, v121, v73
	v_pk_fma_f16 v72, v24, v120, v72
	v_pk_fma_f16 v71, v23, v119, v71
	v_pk_fma_f16 v70, v22, v118, v70
	v_pk_add_f16 v115, v225, v212 neg_lo:[0,1] neg_hi:[0,1]
	v_pk_add_f16 v116, v224, v213 neg_lo:[0,1] neg_hi:[0,1]
	v_pk_add_f16 v117, v223, v214 neg_lo:[0,1] neg_hi:[0,1]
	v_exp_f16_sdwa v118, v114 dst_sel:WORD_0 dst_unused:UNUSED_PAD src0_sel:WORD_0
	v_exp_f16_sdwa v119, v115 dst_sel:WORD_0 dst_unused:UNUSED_PAD src0_sel:WORD_0
	v_exp_f16_sdwa v120, v116 dst_sel:WORD_0 dst_unused:UNUSED_PAD src0_sel:WORD_0
	v_exp_f16_sdwa v121, v117 dst_sel:WORD_0 dst_unused:UNUSED_PAD src0_sel:WORD_0
	v_exp_f16_sdwa v118, v114 dst_sel:WORD_1 dst_unused:UNUSED_PRESERVE src0_sel:WORD_1
	v_exp_f16_sdwa v119, v115 dst_sel:WORD_1 dst_unused:UNUSED_PRESERVE src0_sel:WORD_1
	v_exp_f16_sdwa v120, v116 dst_sel:WORD_1 dst_unused:UNUSED_PRESERVE src0_sel:WORD_1
	v_exp_f16_sdwa v121, v117 dst_sel:WORD_1 dst_unused:UNUSED_PRESERVE src0_sel:WORD_1
	v_pk_add_f16 v114, v162, v211 neg_lo:[0,1] neg_hi:[0,1]
	v_pk_add_f16 v97, v97, v118
	v_pk_add_f16 v96, v96, v119
	v_pk_add_f16 v95, v95, v120
	v_pk_add_f16 v94, v94, v121
	v_pk_fma_f16 v70, v34, v118, v70
	v_pk_fma_f16 v71, v35, v119, v71
	v_pk_fma_f16 v72, v36, v120, v72
	v_pk_fma_f16 v73, v37, v121, v73
	v_pk_add_f16 v115, v163, v212 neg_lo:[0,1] neg_hi:[0,1]
	v_pk_add_f16 v116, v164, v213 neg_lo:[0,1] neg_hi:[0,1]
	v_pk_add_f16 v117, v165, v214 neg_lo:[0,1] neg_hi:[0,1]
	v_exp_f16_sdwa v118, v114 dst_sel:WORD_0 dst_unused:UNUSED_PAD src0_sel:WORD_0
	v_exp_f16_sdwa v119, v115 dst_sel:WORD_0 dst_unused:UNUSED_PAD src0_sel:WORD_0
	v_exp_f16_sdwa v120, v116 dst_sel:WORD_0 dst_unused:UNUSED_PAD src0_sel:WORD_0
	v_exp_f16_sdwa v121, v117 dst_sel:WORD_0 dst_unused:UNUSED_PAD src0_sel:WORD_0
	v_exp_f16_sdwa v118, v114 dst_sel:WORD_1 dst_unused:UNUSED_PRESERVE src0_sel:WORD_1
	v_exp_f16_sdwa v119, v115 dst_sel:WORD_1 dst_unused:UNUSED_PRESERVE src0_sel:WORD_1
	v_exp_f16_sdwa v120, v116 dst_sel:WORD_1 dst_unused:UNUSED_PRESERVE src0_sel:WORD_1
	v_exp_f16_sdwa v121, v117 dst_sel:WORD_1 dst_unused:UNUSED_PRESERVE src0_sel:WORD_1
	v_pk_add_f16 v97, v97, v118
	v_pk_add_f16 v96, v96, v119
	v_rcp_f16_e32 v114, v97
	v_rcp_f16_sdwa v97, v97 dst_sel:DWORD dst_unused:UNUSED_PAD src0_sel:WORD_1
	v_pk_add_f16 v95, v95, v120
	v_rcp_f16_e32 v115, v96
	v_rcp_f16_sdwa v96, v96 dst_sel:DWORD dst_unused:UNUSED_PAD src0_sel:WORD_1
	v_pk_add_f16 v94, v94, v121
	v_rcp_f16_e32 v116, v95
	v_rcp_f16_sdwa v95, v95 dst_sel:DWORD dst_unused:UNUSED_PAD src0_sel:WORD_1
	v_rcp_f16_e32 v117, v94
	v_rcp_f16_sdwa v94, v94 dst_sel:DWORD dst_unused:UNUSED_PAD src0_sel:WORD_1
	v_pk_fma_f16 v70, v50, v118, v70
	v_pack_b32_f16 v97, v114, v97
	v_pk_fma_f16 v71, v51, v119, v71
	v_pk_mul_f16 v141, v70, v97
	v_pack_b32_f16 v70, v115, v96
	v_pk_fma_f16 v72, v52, v120, v72
	v_pk_mul_f16 v140, v71, v70
	v_pack_b32_f16 v70, v116, v95
	v_pk_fma_f16 v73, v53, v121, v73
	v_pk_mul_f16 v139, v72, v70
	v_pack_b32_f16 v70, v117, v94
	v_pk_mul_f16 v138, v73, v70
	s_waitcnt vmcnt(12)
	v_pk_mul_f16 v70, v160, v154 op_sel_hi:[0,1]
	v_pk_mul_f16 v73, v160, v157 op_sel_hi:[0,1]
	v_pk_mul_f16 v97, v158, v157 op_sel_hi:[0,1]
	v_pk_mul_f16 v117, v159, v157 op_sel_hi:[0,1]
	v_pk_mul_f16 v71, v160, v155 op_sel_hi:[0,1]
	v_pk_mul_f16 v72, v160, v156 op_sel_hi:[0,1]
	v_pk_mul_f16 v94, v158, v154 op_sel_hi:[0,1]
	v_pk_mul_f16 v95, v158, v155 op_sel_hi:[0,1]
	v_pk_mul_f16 v96, v158, v156 op_sel_hi:[0,1]
	v_pk_mul_f16 v114, v159, v154 op_sel_hi:[0,1]
	v_pk_mul_f16 v115, v159, v155 op_sel_hi:[0,1]
	v_pk_mul_f16 v116, v159, v156 op_sel_hi:[0,1]
	v_pk_fma_f16 v89, v89, v157, v73
	v_pk_fma_f16 v86, v86, v154, v70
	v_pk_fma_f16 v113, v113, v157, v73
	v_pk_fma_f16 v110, v110, v154, v70
	v_pk_fma_f16 v73, v129, v157, v73
	v_pk_fma_f16 v70, v126, v154, v70
	v_pk_fma_f16 v118, v57, v157, v97
	v_pk_fma_f16 v126, v77, v157, v97
	v_pk_fma_f16 v97, v101, v157, v97
	v_pk_fma_f16 v130, v29, v157, v117
	v_pk_fma_f16 v161, v41, v157, v117
	v_pk_fma_f16 v117, v61, v157, v117
	v_pk_maximum3_f16 v157, v89, v113, v73
	v_pk_fma_f16 v88, v88, v156, v72
	v_pk_fma_f16 v87, v87, v155, v71
	v_pk_fma_f16 v112, v112, v156, v72
	v_pk_fma_f16 v111, v111, v155, v71
	v_pk_fma_f16 v72, v128, v156, v72
	v_pk_fma_f16 v71, v127, v155, v71
	v_pk_fma_f16 v119, v56, v156, v96
	v_pk_fma_f16 v120, v55, v155, v95
	v_pk_fma_f16 v121, v54, v154, v94
	v_pk_fma_f16 v127, v76, v156, v96
	v_pk_fma_f16 v128, v75, v155, v95
	v_pk_fma_f16 v129, v74, v154, v94
	v_pk_fma_f16 v96, v100, v156, v96
	v_pk_fma_f16 v95, v99, v155, v95
	v_pk_fma_f16 v94, v98, v154, v94
	v_pk_fma_f16 v131, v28, v156, v116
	v_pk_fma_f16 v132, v27, v155, v115
	v_pk_fma_f16 v133, v26, v154, v114
	v_pk_fma_f16 v162, v40, v156, v116
	v_pk_fma_f16 v163, v39, v155, v115
	v_pk_fma_f16 v164, v38, v154, v114
	v_pk_fma_f16 v116, v60, v156, v116
	v_pk_fma_f16 v115, v59, v155, v115
	v_pk_fma_f16 v114, v58, v154, v114
	v_pk_maximum3_f16 v154, v86, v110, v70
	v_pk_maximum3_f16 v155, v87, v111, v71
	v_pk_maximum3_f16 v156, v88, v112, v72
	v_pk_maximum3_f16 v206, v118, v126, v97
	v_pk_maximum3_f16 v210, v130, v161, v117
	v_pk_maximum3_f16 v165, v121, v129, v94
	v_pk_maximum3_f16 v200, v120, v128, v95
	v_pk_maximum3_f16 v201, v119, v127, v96
	v_pk_maximum3_f16 v207, v133, v164, v114
	v_pk_maximum3_f16 v208, v132, v163, v115
	v_pk_maximum3_f16 v157, v157, v206, v210
	v_pk_maximum3_f16 v209, v131, v162, v116
	v_pk_maximum3_f16 v154, v154, v165, v207
	v_pk_maximum3_f16 v155, v155, v200, v208
	v_pk_maximum3_f16 v156, v156, v201, v209
	v_pk_add_f16 v89, v89, v157 neg_lo:[0,1] neg_hi:[0,1]
	v_pk_add_f16 v86, v86, v154 neg_lo:[0,1] neg_hi:[0,1]
	v_pk_add_f16 v87, v87, v155 neg_lo:[0,1] neg_hi:[0,1]
	v_pk_add_f16 v88, v88, v156 neg_lo:[0,1] neg_hi:[0,1]
	v_pk_add_f16 v110, v110, v154 neg_lo:[0,1] neg_hi:[0,1]
	v_exp_f16_sdwa v165, v86 dst_sel:WORD_0 dst_unused:UNUSED_PAD src0_sel:WORD_0
	v_exp_f16_sdwa v200, v87 dst_sel:WORD_0 dst_unused:UNUSED_PAD src0_sel:WORD_0
	v_exp_f16_sdwa v201, v88 dst_sel:WORD_0 dst_unused:UNUSED_PAD src0_sel:WORD_0
	v_exp_f16_sdwa v206, v89 dst_sel:WORD_0 dst_unused:UNUSED_PAD src0_sel:WORD_0
	v_exp_f16_sdwa v165, v86 dst_sel:WORD_1 dst_unused:UNUSED_PRESERVE src0_sel:WORD_1
	v_exp_f16_sdwa v200, v87 dst_sel:WORD_1 dst_unused:UNUSED_PRESERVE src0_sel:WORD_1
	v_exp_f16_sdwa v201, v88 dst_sel:WORD_1 dst_unused:UNUSED_PRESERVE src0_sel:WORD_1
	v_exp_f16_sdwa v206, v89 dst_sel:WORD_1 dst_unused:UNUSED_PRESERVE src0_sel:WORD_1
	v_pk_add_f16 v111, v111, v155 neg_lo:[0,1] neg_hi:[0,1]
	v_pk_add_f16 v89, v165, 0
	v_pk_fma_f16 v45, v45, v206, 0
	v_pk_add_f16 v86, v206, 0
	v_pk_add_f16 v87, v201, 0
	v_pk_add_f16 v88, v200, 0
	v_pk_fma_f16 v44, v44, v201, 0
	v_pk_fma_f16 v43, v43, v200, 0
	v_pk_fma_f16 v42, v42, v165, 0
	v_pk_add_f16 v112, v112, v156 neg_lo:[0,1] neg_hi:[0,1]
	v_pk_add_f16 v113, v113, v157 neg_lo:[0,1] neg_hi:[0,1]
	v_exp_f16_sdwa v165, v110 dst_sel:WORD_0 dst_unused:UNUSED_PAD src0_sel:WORD_0
	v_exp_f16_sdwa v200, v111 dst_sel:WORD_0 dst_unused:UNUSED_PAD src0_sel:WORD_0
	v_exp_f16_sdwa v201, v112 dst_sel:WORD_0 dst_unused:UNUSED_PAD src0_sel:WORD_0
	v_exp_f16_sdwa v206, v113 dst_sel:WORD_0 dst_unused:UNUSED_PAD src0_sel:WORD_0
	v_exp_f16_sdwa v165, v110 dst_sel:WORD_1 dst_unused:UNUSED_PRESERVE src0_sel:WORD_1
	v_exp_f16_sdwa v200, v111 dst_sel:WORD_1 dst_unused:UNUSED_PRESERVE src0_sel:WORD_1
	v_exp_f16_sdwa v201, v112 dst_sel:WORD_1 dst_unused:UNUSED_PRESERVE src0_sel:WORD_1
	v_exp_f16_sdwa v206, v113 dst_sel:WORD_1 dst_unused:UNUSED_PRESERVE src0_sel:WORD_1
	v_pk_add_f16 v89, v89, v165
	v_pk_fma_f16 v45, v69, v206, v45
	v_pk_add_f16 v69, v73, v157 neg_lo:[0,1] neg_hi:[0,1]
	v_pk_add_f16 v88, v88, v200
	v_pk_add_f16 v87, v87, v201
	v_pk_add_f16 v86, v86, v206
	v_pk_fma_f16 v42, v66, v165, v42
	v_pk_fma_f16 v43, v67, v200, v43
	v_pk_fma_f16 v44, v68, v201, v44
	v_pk_add_f16 v66, v70, v154 neg_lo:[0,1] neg_hi:[0,1]
	v_pk_add_f16 v67, v71, v155 neg_lo:[0,1] neg_hi:[0,1]
	v_pk_add_f16 v68, v72, v156 neg_lo:[0,1] neg_hi:[0,1]
	v_exp_f16_sdwa v70, v66 dst_sel:WORD_0 dst_unused:UNUSED_PAD src0_sel:WORD_0
	v_exp_f16_sdwa v71, v67 dst_sel:WORD_0 dst_unused:UNUSED_PAD src0_sel:WORD_0
	v_exp_f16_sdwa v72, v68 dst_sel:WORD_0 dst_unused:UNUSED_PAD src0_sel:WORD_0
	v_exp_f16_sdwa v73, v69 dst_sel:WORD_0 dst_unused:UNUSED_PAD src0_sel:WORD_0
	v_exp_f16_sdwa v70, v66 dst_sel:WORD_1 dst_unused:UNUSED_PRESERVE src0_sel:WORD_1
	v_exp_f16_sdwa v71, v67 dst_sel:WORD_1 dst_unused:UNUSED_PRESERVE src0_sel:WORD_1
	v_exp_f16_sdwa v72, v68 dst_sel:WORD_1 dst_unused:UNUSED_PRESERVE src0_sel:WORD_1
	v_exp_f16_sdwa v73, v69 dst_sel:WORD_1 dst_unused:UNUSED_PRESERVE src0_sel:WORD_1
	v_pk_add_f16 v69, v89, v70
	v_pk_add_f16 v66, v86, v73
	v_pk_add_f16 v67, v87, v72
	v_pk_add_f16 v68, v88, v71
	v_pk_fma_f16 v45, v93, v73, v45
	v_pk_fma_f16 v44, v92, v72, v44
	v_pk_fma_f16 v43, v91, v71, v43
	v_pk_fma_f16 v42, v90, v70, v42
	v_pk_add_f16 v70, v121, v154 neg_lo:[0,1] neg_hi:[0,1]
	v_pk_add_f16 v71, v120, v155 neg_lo:[0,1] neg_hi:[0,1]
	v_pk_add_f16 v72, v119, v156 neg_lo:[0,1] neg_hi:[0,1]
	v_pk_add_f16 v73, v118, v157 neg_lo:[0,1] neg_hi:[0,1]
	v_exp_f16_sdwa v86, v70 dst_sel:WORD_0 dst_unused:UNUSED_PAD src0_sel:WORD_0
	v_exp_f16_sdwa v87, v71 dst_sel:WORD_0 dst_unused:UNUSED_PAD src0_sel:WORD_0
	v_exp_f16_sdwa v88, v72 dst_sel:WORD_0 dst_unused:UNUSED_PAD src0_sel:WORD_0
	v_exp_f16_sdwa v89, v73 dst_sel:WORD_0 dst_unused:UNUSED_PAD src0_sel:WORD_0
	v_exp_f16_sdwa v86, v70 dst_sel:WORD_1 dst_unused:UNUSED_PRESERVE src0_sel:WORD_1
	v_exp_f16_sdwa v87, v71 dst_sel:WORD_1 dst_unused:UNUSED_PRESERVE src0_sel:WORD_1
	v_exp_f16_sdwa v88, v72 dst_sel:WORD_1 dst_unused:UNUSED_PRESERVE src0_sel:WORD_1
	v_exp_f16_sdwa v89, v73 dst_sel:WORD_1 dst_unused:UNUSED_PRESERVE src0_sel:WORD_1
	v_pk_add_f16 v70, v129, v154 neg_lo:[0,1] neg_hi:[0,1]
	v_pk_add_f16 v69, v69, v86
	v_pk_add_f16 v68, v68, v87
	v_pk_add_f16 v67, v67, v88
	v_pk_add_f16 v66, v66, v89
	v_pk_fma_f16 v42, v22, v86, v42
	v_pk_fma_f16 v43, v23, v87, v43
	v_pk_fma_f16 v44, v24, v88, v44
	v_pk_fma_f16 v45, v25, v89, v45
	v_pk_add_f16 v71, v128, v155 neg_lo:[0,1] neg_hi:[0,1]
	v_pk_add_f16 v72, v127, v156 neg_lo:[0,1] neg_hi:[0,1]
	v_pk_add_f16 v73, v126, v157 neg_lo:[0,1] neg_hi:[0,1]
	v_exp_f16_sdwa v86, v70 dst_sel:WORD_0 dst_unused:UNUSED_PAD src0_sel:WORD_0
	v_exp_f16_sdwa v87, v71 dst_sel:WORD_0 dst_unused:UNUSED_PAD src0_sel:WORD_0
	v_exp_f16_sdwa v88, v72 dst_sel:WORD_0 dst_unused:UNUSED_PAD src0_sel:WORD_0
	v_exp_f16_sdwa v89, v73 dst_sel:WORD_0 dst_unused:UNUSED_PAD src0_sel:WORD_0
	v_exp_f16_sdwa v86, v70 dst_sel:WORD_1 dst_unused:UNUSED_PRESERVE src0_sel:WORD_1
	v_exp_f16_sdwa v87, v71 dst_sel:WORD_1 dst_unused:UNUSED_PRESERVE src0_sel:WORD_1
	v_exp_f16_sdwa v88, v72 dst_sel:WORD_1 dst_unused:UNUSED_PRESERVE src0_sel:WORD_1
	v_exp_f16_sdwa v89, v73 dst_sel:WORD_1 dst_unused:UNUSED_PRESERVE src0_sel:WORD_1
	v_pk_add_f16 v70, v94, v154 neg_lo:[0,1] neg_hi:[0,1]
	v_pk_add_f16 v69, v69, v86
	v_pk_add_f16 v66, v66, v89
	v_pk_add_f16 v67, v67, v88
	v_pk_add_f16 v68, v68, v87
	v_pk_fma_f16 v45, v37, v89, v45
	v_pk_fma_f16 v44, v36, v88, v44
	v_pk_fma_f16 v43, v35, v87, v43
	v_pk_fma_f16 v42, v34, v86, v42
	v_pk_add_f16 v71, v95, v155 neg_lo:[0,1] neg_hi:[0,1]
	v_pk_add_f16 v72, v96, v156 neg_lo:[0,1] neg_hi:[0,1]
	v_pk_add_f16 v73, v97, v157 neg_lo:[0,1] neg_hi:[0,1]
	v_exp_f16_sdwa v86, v70 dst_sel:WORD_0 dst_unused:UNUSED_PAD src0_sel:WORD_0
	v_exp_f16_sdwa v87, v71 dst_sel:WORD_0 dst_unused:UNUSED_PAD src0_sel:WORD_0
	v_exp_f16_sdwa v88, v72 dst_sel:WORD_0 dst_unused:UNUSED_PAD src0_sel:WORD_0
	v_exp_f16_sdwa v89, v73 dst_sel:WORD_0 dst_unused:UNUSED_PAD src0_sel:WORD_0
	v_exp_f16_sdwa v86, v70 dst_sel:WORD_1 dst_unused:UNUSED_PRESERVE src0_sel:WORD_1
	v_exp_f16_sdwa v87, v71 dst_sel:WORD_1 dst_unused:UNUSED_PRESERVE src0_sel:WORD_1
	v_exp_f16_sdwa v88, v72 dst_sel:WORD_1 dst_unused:UNUSED_PRESERVE src0_sel:WORD_1
	v_exp_f16_sdwa v89, v73 dst_sel:WORD_1 dst_unused:UNUSED_PRESERVE src0_sel:WORD_1
	v_pk_add_f16 v70, v133, v154 neg_lo:[0,1] neg_hi:[0,1]
	v_pk_add_f16 v69, v69, v86
	v_pk_add_f16 v68, v68, v87
	v_pk_add_f16 v67, v67, v88
	v_pk_add_f16 v66, v66, v89
	v_pk_fma_f16 v42, v50, v86, v42
	v_pk_fma_f16 v43, v51, v87, v43
	v_pk_fma_f16 v44, v52, v88, v44
	v_pk_fma_f16 v45, v53, v89, v45
	v_pk_add_f16 v71, v132, v155 neg_lo:[0,1] neg_hi:[0,1]
	v_pk_add_f16 v72, v131, v156 neg_lo:[0,1] neg_hi:[0,1]
	v_pk_add_f16 v73, v130, v157 neg_lo:[0,1] neg_hi:[0,1]
	v_exp_f16_sdwa v86, v70 dst_sel:WORD_0 dst_unused:UNUSED_PAD src0_sel:WORD_0
	v_exp_f16_sdwa v87, v71 dst_sel:WORD_0 dst_unused:UNUSED_PAD src0_sel:WORD_0
	v_exp_f16_sdwa v88, v72 dst_sel:WORD_0 dst_unused:UNUSED_PAD src0_sel:WORD_0
	v_exp_f16_sdwa v89, v73 dst_sel:WORD_0 dst_unused:UNUSED_PAD src0_sel:WORD_0
	v_exp_f16_sdwa v86, v70 dst_sel:WORD_1 dst_unused:UNUSED_PRESERVE src0_sel:WORD_1
	v_exp_f16_sdwa v87, v71 dst_sel:WORD_1 dst_unused:UNUSED_PRESERVE src0_sel:WORD_1
	v_exp_f16_sdwa v88, v72 dst_sel:WORD_1 dst_unused:UNUSED_PRESERVE src0_sel:WORD_1
	v_exp_f16_sdwa v89, v73 dst_sel:WORD_1 dst_unused:UNUSED_PRESERVE src0_sel:WORD_1
	v_pk_add_f16 v70, v164, v154 neg_lo:[0,1] neg_hi:[0,1]
	v_pk_add_f16 v69, v69, v86
	v_pk_add_f16 v66, v66, v89
	v_pk_add_f16 v67, v67, v88
	v_pk_add_f16 v68, v68, v87
	v_pk_fma_f16 v45, v13, v89, v45
	v_pk_fma_f16 v44, v12, v88, v44
	v_pk_fma_f16 v43, v11, v87, v43
	v_pk_fma_f16 v42, v10, v86, v42
	v_pk_add_f16 v71, v163, v155 neg_lo:[0,1] neg_hi:[0,1]
	v_pk_add_f16 v72, v162, v156 neg_lo:[0,1] neg_hi:[0,1]
	v_pk_add_f16 v73, v161, v157 neg_lo:[0,1] neg_hi:[0,1]
	v_exp_f16_sdwa v86, v70 dst_sel:WORD_0 dst_unused:UNUSED_PAD src0_sel:WORD_0
	v_exp_f16_sdwa v87, v71 dst_sel:WORD_0 dst_unused:UNUSED_PAD src0_sel:WORD_0
	v_exp_f16_sdwa v88, v72 dst_sel:WORD_0 dst_unused:UNUSED_PAD src0_sel:WORD_0
	v_exp_f16_sdwa v89, v73 dst_sel:WORD_0 dst_unused:UNUSED_PAD src0_sel:WORD_0
	v_exp_f16_sdwa v86, v70 dst_sel:WORD_1 dst_unused:UNUSED_PRESERVE src0_sel:WORD_1
	v_exp_f16_sdwa v87, v71 dst_sel:WORD_1 dst_unused:UNUSED_PRESERVE src0_sel:WORD_1
	v_exp_f16_sdwa v88, v72 dst_sel:WORD_1 dst_unused:UNUSED_PRESERVE src0_sel:WORD_1
	v_exp_f16_sdwa v89, v73 dst_sel:WORD_1 dst_unused:UNUSED_PRESERVE src0_sel:WORD_1
	v_pk_add_f16 v70, v114, v154 neg_lo:[0,1] neg_hi:[0,1]
	v_pk_add_f16 v69, v69, v86
	v_pk_add_f16 v68, v68, v87
	v_pk_add_f16 v67, v67, v88
	v_pk_add_f16 v66, v66, v89
	v_pk_fma_f16 v42, v14, v86, v42
	v_pk_fma_f16 v43, v15, v87, v43
	v_pk_fma_f16 v44, v16, v88, v44
	v_pk_fma_f16 v45, v17, v89, v45
	v_pk_add_f16 v71, v115, v155 neg_lo:[0,1] neg_hi:[0,1]
	v_pk_add_f16 v72, v116, v156 neg_lo:[0,1] neg_hi:[0,1]
	v_pk_add_f16 v73, v117, v157 neg_lo:[0,1] neg_hi:[0,1]
	v_exp_f16_sdwa v86, v70 dst_sel:WORD_0 dst_unused:UNUSED_PAD src0_sel:WORD_0
	v_exp_f16_sdwa v87, v71 dst_sel:WORD_0 dst_unused:UNUSED_PAD src0_sel:WORD_0
	v_exp_f16_sdwa v88, v72 dst_sel:WORD_0 dst_unused:UNUSED_PAD src0_sel:WORD_0
	v_exp_f16_sdwa v89, v73 dst_sel:WORD_0 dst_unused:UNUSED_PAD src0_sel:WORD_0
	v_exp_f16_sdwa v86, v70 dst_sel:WORD_1 dst_unused:UNUSED_PRESERVE src0_sel:WORD_1
	v_exp_f16_sdwa v87, v71 dst_sel:WORD_1 dst_unused:UNUSED_PRESERVE src0_sel:WORD_1
	v_exp_f16_sdwa v88, v72 dst_sel:WORD_1 dst_unused:UNUSED_PRESERVE src0_sel:WORD_1
	v_exp_f16_sdwa v89, v73 dst_sel:WORD_1 dst_unused:UNUSED_PRESERVE src0_sel:WORD_1
	v_pk_add_f16 v69, v69, v86
	v_pk_add_f16 v68, v68, v87
	v_rcp_f16_e32 v70, v69
	v_rcp_f16_sdwa v69, v69 dst_sel:DWORD dst_unused:UNUSED_PAD src0_sel:WORD_1
	v_pk_add_f16 v67, v67, v88
	v_rcp_f16_e32 v71, v68
	v_rcp_f16_sdwa v68, v68 dst_sel:DWORD dst_unused:UNUSED_PAD src0_sel:WORD_1
	v_pk_add_f16 v66, v66, v89
	v_rcp_f16_e32 v72, v67
	v_rcp_f16_sdwa v67, v67 dst_sel:DWORD dst_unused:UNUSED_PAD src0_sel:WORD_1
	v_rcp_f16_e32 v73, v66
	v_rcp_f16_sdwa v66, v66 dst_sel:DWORD dst_unused:UNUSED_PAD src0_sel:WORD_1
	v_pk_fma_f16 v42, v18, v86, v42
	v_pack_b32_f16 v69, v70, v69
	v_pk_fma_f16 v43, v19, v87, v43
	v_pk_mul_f16 v97, v42, v69
	v_pack_b32_f16 v42, v71, v68
	v_pk_fma_f16 v44, v20, v88, v44
	v_pk_mul_f16 v96, v43, v42
	v_pack_b32_f16 v42, v72, v67
	v_pk_fma_f16 v45, v21, v89, v45
	v_pk_mul_f16 v95, v44, v42
	v_pack_b32_f16 v42, v73, v66
	v_pk_mul_f16 v94, v45, v42
	s_waitcnt vmcnt(6)
	v_pk_mul_f16 v45, v160, v153 op_sel_hi:[0,1]
	v_pk_mul_f16 v42, v160, v150 op_sel_hi:[0,1]
	v_pk_mul_f16 v43, v160, v151 op_sel_hi:[0,1]
	v_pk_mul_f16 v44, v160, v152 op_sel_hi:[0,1]
	v_pk_mul_f16 v69, v158, v153 op_sel_hi:[0,1]
	v_pk_mul_f16 v73, v159, v153 op_sel_hi:[0,1]
	v_pk_fma_f16 v57, v57, v153, v45
	v_pk_fma_f16 v77, v77, v153, v45
	v_pk_fma_f16 v45, v101, v153, v45
	v_pk_mul_f16 v66, v158, v150 op_sel_hi:[0,1]
	v_pk_maximum3_f16 v117, v57, v77, v45
	v_pk_mul_f16 v67, v158, v151 op_sel_hi:[0,1]
	v_pk_mul_f16 v68, v158, v152 op_sel_hi:[0,1]
	v_pk_mul_f16 v70, v159, v150 op_sel_hi:[0,1]
	v_pk_mul_f16 v71, v159, v151 op_sel_hi:[0,1]
	v_pk_mul_f16 v72, v159, v152 op_sel_hi:[0,1]
	v_pk_fma_f16 v56, v56, v152, v44
	v_pk_fma_f16 v55, v55, v151, v43
	v_pk_fma_f16 v54, v54, v150, v42
	v_pk_fma_f16 v76, v76, v152, v44
	v_pk_fma_f16 v75, v75, v151, v43
	v_pk_fma_f16 v74, v74, v150, v42
	v_pk_fma_f16 v44, v100, v152, v44
	v_pk_fma_f16 v43, v99, v151, v43
	v_pk_fma_f16 v42, v98, v150, v42
	v_pk_fma_f16 v86, v29, v153, v69
	v_pk_fma_f16 v90, v41, v153, v69
	v_pk_fma_f16 v69, v61, v153, v69
	v_pk_fma_f16 v98, v81, v153, v73
	v_pk_fma_f16 v110, v109, v153, v73
	v_pk_fma_f16 v73, v125, v153, v73
	v_pk_maximum3_f16 v114, v54, v74, v42
	v_pk_maximum3_f16 v115, v55, v75, v43
	v_pk_maximum3_f16 v116, v56, v76, v44
	v_pk_maximum3_f16 v121, v86, v90, v69
	v_pk_fma_f16 v87, v28, v152, v68
	v_pk_maximum3_f16 v129, v98, v110, v73
	v_pk_fma_f16 v88, v27, v151, v67
	v_pk_maximum3_f16 v117, v117, v121, v129
	v_pk_fma_f16 v89, v26, v150, v66
	v_pk_fma_f16 v91, v40, v152, v68
	v_pk_fma_f16 v92, v39, v151, v67
	v_pk_fma_f16 v93, v38, v150, v66
	v_pk_fma_f16 v68, v60, v152, v68
	v_pk_fma_f16 v67, v59, v151, v67
	v_pk_fma_f16 v66, v58, v150, v66
	v_pk_fma_f16 v99, v80, v152, v72
	v_pk_fma_f16 v100, v79, v151, v71
	v_pk_fma_f16 v101, v78, v150, v70
	v_pk_fma_f16 v111, v108, v152, v72
	v_pk_fma_f16 v112, v107, v151, v71
	v_pk_fma_f16 v113, v106, v150, v70
	v_pk_fma_f16 v72, v124, v152, v72
	v_pk_fma_f16 v71, v123, v151, v71
	v_pk_fma_f16 v70, v122, v150, v70
	v_pk_maximum3_f16 v118, v89, v93, v66
	v_pk_maximum3_f16 v119, v88, v92, v67
	v_pk_maximum3_f16 v120, v87, v91, v68
	v_pk_maximum3_f16 v127, v100, v112, v71
	v_pk_maximum3_f16 v128, v99, v111, v72
	v_pk_maximum3_f16 v126, v101, v113, v70
	v_pk_maximum3_f16 v114, v114, v118, v126
	v_pk_maximum3_f16 v115, v115, v119, v127
	v_pk_maximum3_f16 v116, v116, v120, v128
	v_pk_add_f16 v57, v57, v117 neg_lo:[0,1] neg_hi:[0,1]
	v_pk_add_f16 v54, v54, v114 neg_lo:[0,1] neg_hi:[0,1]
	v_pk_add_f16 v55, v55, v115 neg_lo:[0,1] neg_hi:[0,1]
	v_pk_add_f16 v56, v56, v116 neg_lo:[0,1] neg_hi:[0,1]
	v_pk_add_f16 v74, v74, v114 neg_lo:[0,1] neg_hi:[0,1]
	v_exp_f16_sdwa v118, v54 dst_sel:WORD_0 dst_unused:UNUSED_PAD src0_sel:WORD_0
	v_exp_f16_sdwa v119, v55 dst_sel:WORD_0 dst_unused:UNUSED_PAD src0_sel:WORD_0
	v_exp_f16_sdwa v120, v56 dst_sel:WORD_0 dst_unused:UNUSED_PAD src0_sel:WORD_0
	v_exp_f16_sdwa v121, v57 dst_sel:WORD_0 dst_unused:UNUSED_PAD src0_sel:WORD_0
	v_exp_f16_sdwa v118, v54 dst_sel:WORD_1 dst_unused:UNUSED_PRESERVE src0_sel:WORD_1
	v_exp_f16_sdwa v119, v55 dst_sel:WORD_1 dst_unused:UNUSED_PRESERVE src0_sel:WORD_1
	v_exp_f16_sdwa v120, v56 dst_sel:WORD_1 dst_unused:UNUSED_PRESERVE src0_sel:WORD_1
	v_exp_f16_sdwa v121, v57 dst_sel:WORD_1 dst_unused:UNUSED_PRESERVE src0_sel:WORD_1
	v_pk_add_f16 v75, v75, v115 neg_lo:[0,1] neg_hi:[0,1]
	v_pk_add_f16 v57, v118, 0
	v_pk_fma_f16 v25, v25, v121, 0
	v_pk_add_f16 v54, v121, 0
	v_pk_add_f16 v55, v120, 0
	v_pk_add_f16 v56, v119, 0
	v_pk_fma_f16 v24, v24, v120, 0
	v_pk_fma_f16 v23, v23, v119, 0
	v_pk_fma_f16 v22, v22, v118, 0
	v_pk_add_f16 v76, v76, v116 neg_lo:[0,1] neg_hi:[0,1]
	v_pk_add_f16 v77, v77, v117 neg_lo:[0,1] neg_hi:[0,1]
	v_exp_f16_sdwa v118, v74 dst_sel:WORD_0 dst_unused:UNUSED_PAD src0_sel:WORD_0
	v_exp_f16_sdwa v119, v75 dst_sel:WORD_0 dst_unused:UNUSED_PAD src0_sel:WORD_0
	v_exp_f16_sdwa v120, v76 dst_sel:WORD_0 dst_unused:UNUSED_PAD src0_sel:WORD_0
	v_exp_f16_sdwa v121, v77 dst_sel:WORD_0 dst_unused:UNUSED_PAD src0_sel:WORD_0
	v_exp_f16_sdwa v118, v74 dst_sel:WORD_1 dst_unused:UNUSED_PRESERVE src0_sel:WORD_1
	v_exp_f16_sdwa v119, v75 dst_sel:WORD_1 dst_unused:UNUSED_PRESERVE src0_sel:WORD_1
	v_exp_f16_sdwa v120, v76 dst_sel:WORD_1 dst_unused:UNUSED_PRESERVE src0_sel:WORD_1
	v_exp_f16_sdwa v121, v77 dst_sel:WORD_1 dst_unused:UNUSED_PRESERVE src0_sel:WORD_1
	v_pk_add_f16 v57, v57, v118
	v_pk_fma_f16 v25, v37, v121, v25
	v_pk_add_f16 v37, v45, v117 neg_lo:[0,1] neg_hi:[0,1]
	v_pk_add_f16 v56, v56, v119
	v_pk_add_f16 v55, v55, v120
	v_pk_add_f16 v54, v54, v121
	v_pk_fma_f16 v22, v34, v118, v22
	v_pk_fma_f16 v23, v35, v119, v23
	v_pk_fma_f16 v24, v36, v120, v24
	v_pk_add_f16 v34, v42, v114 neg_lo:[0,1] neg_hi:[0,1]
	v_pk_add_f16 v35, v43, v115 neg_lo:[0,1] neg_hi:[0,1]
	v_pk_add_f16 v36, v44, v116 neg_lo:[0,1] neg_hi:[0,1]
	v_exp_f16_sdwa v42, v34 dst_sel:WORD_0 dst_unused:UNUSED_PAD src0_sel:WORD_0
	v_exp_f16_sdwa v43, v35 dst_sel:WORD_0 dst_unused:UNUSED_PAD src0_sel:WORD_0
	v_exp_f16_sdwa v44, v36 dst_sel:WORD_0 dst_unused:UNUSED_PAD src0_sel:WORD_0
	v_exp_f16_sdwa v45, v37 dst_sel:WORD_0 dst_unused:UNUSED_PAD src0_sel:WORD_0
	v_exp_f16_sdwa v42, v34 dst_sel:WORD_1 dst_unused:UNUSED_PRESERVE src0_sel:WORD_1
	v_exp_f16_sdwa v43, v35 dst_sel:WORD_1 dst_unused:UNUSED_PRESERVE src0_sel:WORD_1
	v_exp_f16_sdwa v44, v36 dst_sel:WORD_1 dst_unused:UNUSED_PRESERVE src0_sel:WORD_1
	v_exp_f16_sdwa v45, v37 dst_sel:WORD_1 dst_unused:UNUSED_PRESERVE src0_sel:WORD_1
	v_pk_add_f16 v37, v57, v42
	v_pk_add_f16 v34, v54, v45
	v_pk_add_f16 v35, v55, v44
	v_pk_add_f16 v36, v56, v43
	v_pk_fma_f16 v25, v53, v45, v25
	v_pk_fma_f16 v24, v52, v44, v24
	v_pk_fma_f16 v23, v51, v43, v23
	v_pk_fma_f16 v22, v50, v42, v22
	v_pk_add_f16 v42, v89, v114 neg_lo:[0,1] neg_hi:[0,1]
	v_pk_add_f16 v43, v88, v115 neg_lo:[0,1] neg_hi:[0,1]
	v_pk_add_f16 v44, v87, v116 neg_lo:[0,1] neg_hi:[0,1]
	v_pk_add_f16 v45, v86, v117 neg_lo:[0,1] neg_hi:[0,1]
	v_exp_f16_sdwa v50, v42 dst_sel:WORD_0 dst_unused:UNUSED_PAD src0_sel:WORD_0
	v_exp_f16_sdwa v51, v43 dst_sel:WORD_0 dst_unused:UNUSED_PAD src0_sel:WORD_0
	v_exp_f16_sdwa v52, v44 dst_sel:WORD_0 dst_unused:UNUSED_PAD src0_sel:WORD_0
	v_exp_f16_sdwa v53, v45 dst_sel:WORD_0 dst_unused:UNUSED_PAD src0_sel:WORD_0
	v_exp_f16_sdwa v50, v42 dst_sel:WORD_1 dst_unused:UNUSED_PRESERVE src0_sel:WORD_1
	v_exp_f16_sdwa v51, v43 dst_sel:WORD_1 dst_unused:UNUSED_PRESERVE src0_sel:WORD_1
	v_exp_f16_sdwa v52, v44 dst_sel:WORD_1 dst_unused:UNUSED_PRESERVE src0_sel:WORD_1
	v_exp_f16_sdwa v53, v45 dst_sel:WORD_1 dst_unused:UNUSED_PRESERVE src0_sel:WORD_1
	v_pk_add_f16 v42, v93, v114 neg_lo:[0,1] neg_hi:[0,1]
	v_pk_add_f16 v37, v37, v50
	v_pk_add_f16 v36, v36, v51
	v_pk_add_f16 v35, v35, v52
	v_pk_add_f16 v34, v34, v53
	v_pk_fma_f16 v22, v10, v50, v22
	v_pk_fma_f16 v23, v11, v51, v23
	v_pk_fma_f16 v24, v12, v52, v24
	v_pk_fma_f16 v25, v13, v53, v25
	v_pk_add_f16 v43, v92, v115 neg_lo:[0,1] neg_hi:[0,1]
	v_pk_add_f16 v44, v91, v116 neg_lo:[0,1] neg_hi:[0,1]
	v_pk_add_f16 v45, v90, v117 neg_lo:[0,1] neg_hi:[0,1]
	v_exp_f16_sdwa v50, v42 dst_sel:WORD_0 dst_unused:UNUSED_PAD src0_sel:WORD_0
	v_exp_f16_sdwa v51, v43 dst_sel:WORD_0 dst_unused:UNUSED_PAD src0_sel:WORD_0
	v_exp_f16_sdwa v52, v44 dst_sel:WORD_0 dst_unused:UNUSED_PAD src0_sel:WORD_0
	v_exp_f16_sdwa v53, v45 dst_sel:WORD_0 dst_unused:UNUSED_PAD src0_sel:WORD_0
	v_exp_f16_sdwa v50, v42 dst_sel:WORD_1 dst_unused:UNUSED_PRESERVE src0_sel:WORD_1
	v_exp_f16_sdwa v51, v43 dst_sel:WORD_1 dst_unused:UNUSED_PRESERVE src0_sel:WORD_1
	v_exp_f16_sdwa v52, v44 dst_sel:WORD_1 dst_unused:UNUSED_PRESERVE src0_sel:WORD_1
	v_exp_f16_sdwa v53, v45 dst_sel:WORD_1 dst_unused:UNUSED_PRESERVE src0_sel:WORD_1
	v_pk_add_f16 v42, v66, v114 neg_lo:[0,1] neg_hi:[0,1]
	v_pk_add_f16 v37, v37, v50
	v_pk_add_f16 v34, v34, v53
	v_pk_add_f16 v35, v35, v52
	v_pk_add_f16 v36, v36, v51
	v_pk_fma_f16 v25, v17, v53, v25
	v_pk_fma_f16 v24, v16, v52, v24
	v_pk_fma_f16 v23, v15, v51, v23
	v_pk_fma_f16 v22, v14, v50, v22
	v_pk_add_f16 v43, v67, v115 neg_lo:[0,1] neg_hi:[0,1]
	v_pk_add_f16 v44, v68, v116 neg_lo:[0,1] neg_hi:[0,1]
	v_pk_add_f16 v45, v69, v117 neg_lo:[0,1] neg_hi:[0,1]
	v_exp_f16_sdwa v50, v42 dst_sel:WORD_0 dst_unused:UNUSED_PAD src0_sel:WORD_0
	v_exp_f16_sdwa v51, v43 dst_sel:WORD_0 dst_unused:UNUSED_PAD src0_sel:WORD_0
	v_exp_f16_sdwa v52, v44 dst_sel:WORD_0 dst_unused:UNUSED_PAD src0_sel:WORD_0
	v_exp_f16_sdwa v53, v45 dst_sel:WORD_0 dst_unused:UNUSED_PAD src0_sel:WORD_0
	v_exp_f16_sdwa v50, v42 dst_sel:WORD_1 dst_unused:UNUSED_PRESERVE src0_sel:WORD_1
	v_exp_f16_sdwa v51, v43 dst_sel:WORD_1 dst_unused:UNUSED_PRESERVE src0_sel:WORD_1
	v_exp_f16_sdwa v52, v44 dst_sel:WORD_1 dst_unused:UNUSED_PRESERVE src0_sel:WORD_1
	v_exp_f16_sdwa v53, v45 dst_sel:WORD_1 dst_unused:UNUSED_PRESERVE src0_sel:WORD_1
	v_pk_add_f16 v42, v101, v114 neg_lo:[0,1] neg_hi:[0,1]
	v_pk_add_f16 v37, v37, v50
	v_pk_add_f16 v36, v36, v51
	v_pk_add_f16 v35, v35, v52
	v_pk_add_f16 v34, v34, v53
	v_pk_fma_f16 v22, v18, v50, v22
	v_pk_fma_f16 v23, v19, v51, v23
	v_pk_fma_f16 v24, v20, v52, v24
	v_pk_fma_f16 v25, v21, v53, v25
	v_pk_add_f16 v43, v100, v115 neg_lo:[0,1] neg_hi:[0,1]
	v_pk_add_f16 v44, v99, v116 neg_lo:[0,1] neg_hi:[0,1]
	v_pk_add_f16 v45, v98, v117 neg_lo:[0,1] neg_hi:[0,1]
	v_exp_f16_sdwa v50, v42 dst_sel:WORD_0 dst_unused:UNUSED_PAD src0_sel:WORD_0
	v_exp_f16_sdwa v51, v43 dst_sel:WORD_0 dst_unused:UNUSED_PAD src0_sel:WORD_0
	v_exp_f16_sdwa v52, v44 dst_sel:WORD_0 dst_unused:UNUSED_PAD src0_sel:WORD_0
	v_exp_f16_sdwa v53, v45 dst_sel:WORD_0 dst_unused:UNUSED_PAD src0_sel:WORD_0
	v_exp_f16_sdwa v50, v42 dst_sel:WORD_1 dst_unused:UNUSED_PRESERVE src0_sel:WORD_1
	v_exp_f16_sdwa v51, v43 dst_sel:WORD_1 dst_unused:UNUSED_PRESERVE src0_sel:WORD_1
	v_exp_f16_sdwa v52, v44 dst_sel:WORD_1 dst_unused:UNUSED_PRESERVE src0_sel:WORD_1
	v_exp_f16_sdwa v53, v45 dst_sel:WORD_1 dst_unused:UNUSED_PRESERVE src0_sel:WORD_1
	v_pk_add_f16 v42, v113, v114 neg_lo:[0,1] neg_hi:[0,1]
	v_pk_add_f16 v37, v37, v50
	v_pk_add_f16 v34, v34, v53
	v_pk_add_f16 v35, v35, v52
	v_pk_add_f16 v36, v36, v51
	v_pk_fma_f16 v25, v33, v53, v25
	v_pk_fma_f16 v24, v32, v52, v24
	v_pk_fma_f16 v23, v31, v51, v23
	v_pk_fma_f16 v22, v30, v50, v22
	v_pk_add_f16 v43, v112, v115 neg_lo:[0,1] neg_hi:[0,1]
	v_pk_add_f16 v44, v111, v116 neg_lo:[0,1] neg_hi:[0,1]
	v_pk_add_f16 v45, v110, v117 neg_lo:[0,1] neg_hi:[0,1]
	v_exp_f16_sdwa v50, v42 dst_sel:WORD_0 dst_unused:UNUSED_PAD src0_sel:WORD_0
	v_exp_f16_sdwa v51, v43 dst_sel:WORD_0 dst_unused:UNUSED_PAD src0_sel:WORD_0
	v_exp_f16_sdwa v52, v44 dst_sel:WORD_0 dst_unused:UNUSED_PAD src0_sel:WORD_0
	v_exp_f16_sdwa v53, v45 dst_sel:WORD_0 dst_unused:UNUSED_PAD src0_sel:WORD_0
	v_exp_f16_sdwa v50, v42 dst_sel:WORD_1 dst_unused:UNUSED_PRESERVE src0_sel:WORD_1
	v_exp_f16_sdwa v51, v43 dst_sel:WORD_1 dst_unused:UNUSED_PRESERVE src0_sel:WORD_1
	v_exp_f16_sdwa v52, v44 dst_sel:WORD_1 dst_unused:UNUSED_PRESERVE src0_sel:WORD_1
	v_exp_f16_sdwa v53, v45 dst_sel:WORD_1 dst_unused:UNUSED_PRESERVE src0_sel:WORD_1
	v_pk_add_f16 v42, v70, v114 neg_lo:[0,1] neg_hi:[0,1]
	v_pk_add_f16 v37, v37, v50
	v_pk_add_f16 v36, v36, v51
	v_pk_add_f16 v35, v35, v52
	v_pk_add_f16 v34, v34, v53
	v_pk_fma_f16 v22, v46, v50, v22
	v_pk_fma_f16 v23, v47, v51, v23
	v_pk_fma_f16 v24, v48, v52, v24
	v_pk_fma_f16 v25, v49, v53, v25
	v_pk_add_f16 v43, v71, v115 neg_lo:[0,1] neg_hi:[0,1]
	v_pk_add_f16 v44, v72, v116 neg_lo:[0,1] neg_hi:[0,1]
	v_pk_add_f16 v45, v73, v117 neg_lo:[0,1] neg_hi:[0,1]
	v_exp_f16_sdwa v50, v42 dst_sel:WORD_0 dst_unused:UNUSED_PAD src0_sel:WORD_0
	v_exp_f16_sdwa v51, v43 dst_sel:WORD_0 dst_unused:UNUSED_PAD src0_sel:WORD_0
	v_exp_f16_sdwa v52, v44 dst_sel:WORD_0 dst_unused:UNUSED_PAD src0_sel:WORD_0
	v_exp_f16_sdwa v53, v45 dst_sel:WORD_0 dst_unused:UNUSED_PAD src0_sel:WORD_0
	v_exp_f16_sdwa v50, v42 dst_sel:WORD_1 dst_unused:UNUSED_PRESERVE src0_sel:WORD_1
	v_exp_f16_sdwa v51, v43 dst_sel:WORD_1 dst_unused:UNUSED_PRESERVE src0_sel:WORD_1
	v_exp_f16_sdwa v52, v44 dst_sel:WORD_1 dst_unused:UNUSED_PRESERVE src0_sel:WORD_1
	v_exp_f16_sdwa v53, v45 dst_sel:WORD_1 dst_unused:UNUSED_PRESERVE src0_sel:WORD_1
	v_pk_add_f16 v37, v37, v50
	v_pk_add_f16 v36, v36, v51
	v_rcp_f16_e32 v42, v37
	v_rcp_f16_sdwa v37, v37 dst_sel:DWORD dst_unused:UNUSED_PAD src0_sel:WORD_1
	v_pk_add_f16 v35, v35, v52
	v_rcp_f16_e32 v43, v36
	v_rcp_f16_sdwa v36, v36 dst_sel:DWORD dst_unused:UNUSED_PAD src0_sel:WORD_1
	v_pk_add_f16 v34, v34, v53
	v_pk_fma_f16 v22, v62, v50, v22
	v_rcp_f16_e32 v50, v35
	v_rcp_f16_sdwa v35, v35 dst_sel:DWORD dst_unused:UNUSED_PAD src0_sel:WORD_1
	v_pk_fma_f16 v23, v63, v51, v23
	v_rcp_f16_e32 v51, v34
	v_rcp_f16_sdwa v34, v34 dst_sel:DWORD dst_unused:UNUSED_PAD src0_sel:WORD_1
	v_pack_b32_f16 v37, v42, v37
	v_pk_mul_f16 v45, v22, v37
	v_pack_b32_f16 v22, v43, v36
	v_pk_fma_f16 v24, v64, v52, v24
	v_pk_mul_f16 v44, v23, v22
	v_pack_b32_f16 v22, v50, v35
	v_pk_fma_f16 v25, v65, v53, v25
	v_pk_mul_f16 v43, v24, v22
	v_pack_b32_f16 v22, v51, v34
	v_pk_mul_f16 v42, v25, v22
	s_waitcnt vmcnt(0)
	v_pk_mul_f16 v22, v160, v146 op_sel_hi:[0,1]
	v_pk_mul_f16 v23, v160, v147 op_sel_hi:[0,1]
	v_pk_mul_f16 v24, v160, v148 op_sel_hi:[0,1]
	v_pk_mul_f16 v25, v160, v149 op_sel_hi:[0,1]
	v_pk_mul_f16 v50, v159, v146 op_sel_hi:[0,1]
	v_pk_mul_f16 v51, v159, v147 op_sel_hi:[0,1]
	v_pk_mul_f16 v52, v159, v148 op_sel_hi:[0,1]
	v_pk_mul_f16 v53, v159, v149 op_sel_hi:[0,1]
	v_pk_mul_f16 v34, v158, v146 op_sel_hi:[0,1]
	v_pk_mul_f16 v35, v158, v147 op_sel_hi:[0,1]
	v_pk_mul_f16 v36, v158, v148 op_sel_hi:[0,1]
	v_pk_mul_f16 v37, v158, v149 op_sel_hi:[0,1]
	v_pk_fma_f16 v29, v29, v149, v25
	v_pk_fma_f16 v28, v28, v148, v24
	v_pk_fma_f16 v27, v27, v147, v23
	v_pk_fma_f16 v26, v26, v146, v22
	v_pk_fma_f16 v41, v41, v149, v25
	v_pk_fma_f16 v40, v40, v148, v24
	v_pk_fma_f16 v39, v39, v147, v23
	v_pk_fma_f16 v38, v38, v146, v22
	v_pk_fma_f16 v25, v61, v149, v25
	v_pk_fma_f16 v24, v60, v148, v24
	v_pk_fma_f16 v23, v59, v147, v23
	v_pk_fma_f16 v22, v58, v146, v22
	v_pk_fma_f16 v66, v137, v149, v53
	v_pk_fma_f16 v67, v136, v148, v52
	v_pk_fma_f16 v68, v135, v147, v51
	v_pk_fma_f16 v69, v134, v146, v50
	v_pk_fma_f16 v70, v145, v149, v53
	v_pk_fma_f16 v71, v144, v148, v52
	v_pk_fma_f16 v72, v143, v147, v51
	v_pk_fma_f16 v73, v142, v146, v50
	v_pk_fma_f16 v9, v9, v149, v53
	v_pk_fma_f16 v8, v8, v148, v52
	v_pk_fma_f16 v7, v7, v147, v51
	v_pk_fma_f16 v6, v6, v146, v50
	v_pk_maximum3_f16 v50, v26, v38, v22
	v_pk_maximum3_f16 v51, v27, v39, v23
	v_pk_maximum3_f16 v52, v28, v40, v24
	v_pk_maximum3_f16 v53, v29, v41, v25
	v_pk_fma_f16 v54, v81, v149, v37
	v_pk_fma_f16 v55, v80, v148, v36
	v_pk_fma_f16 v56, v79, v147, v35
	v_pk_fma_f16 v57, v78, v146, v34
	v_pk_fma_f16 v58, v109, v149, v37
	v_pk_fma_f16 v59, v108, v148, v36
	v_pk_fma_f16 v60, v107, v147, v35
	v_pk_fma_f16 v61, v106, v146, v34
	v_pk_fma_f16 v37, v125, v149, v37
	v_pk_fma_f16 v36, v124, v148, v36
	v_pk_fma_f16 v35, v123, v147, v35
	v_pk_fma_f16 v34, v122, v146, v34
	v_pk_maximum3_f16 v75, v56, v60, v35
	v_pk_maximum3_f16 v76, v55, v59, v36
	v_pk_maximum3_f16 v77, v54, v58, v37
	v_pk_maximum3_f16 v78, v69, v73, v6
	v_pk_maximum3_f16 v79, v68, v72, v7
	v_pk_maximum3_f16 v74, v57, v61, v34
	v_pk_maximum3_f16 v80, v67, v71, v8
	v_pk_maximum3_f16 v81, v66, v70, v9
	v_pk_maximum3_f16 v50, v50, v74, v78
	v_pk_maximum3_f16 v51, v51, v75, v79
	v_pk_maximum3_f16 v52, v52, v76, v80
	v_pk_maximum3_f16 v53, v53, v77, v81
	s_nop 0
	v_pk_add_f16 v26, v26, v50 neg_lo:[0,1] neg_hi:[0,1]
	v_pk_add_f16 v27, v27, v51 neg_lo:[0,1] neg_hi:[0,1]
	v_pk_add_f16 v28, v28, v52 neg_lo:[0,1] neg_hi:[0,1]
	v_pk_add_f16 v29, v29, v53 neg_lo:[0,1] neg_hi:[0,1]
	v_pk_add_f16 v38, v38, v50 neg_lo:[0,1] neg_hi:[0,1]
	v_exp_f16_sdwa v74, v26 dst_sel:WORD_0 dst_unused:UNUSED_PAD src0_sel:WORD_0
	v_exp_f16_sdwa v75, v27 dst_sel:WORD_0 dst_unused:UNUSED_PAD src0_sel:WORD_0
	v_exp_f16_sdwa v76, v28 dst_sel:WORD_0 dst_unused:UNUSED_PAD src0_sel:WORD_0
	v_exp_f16_sdwa v77, v29 dst_sel:WORD_0 dst_unused:UNUSED_PAD src0_sel:WORD_0
	v_exp_f16_sdwa v74, v26 dst_sel:WORD_1 dst_unused:UNUSED_PRESERVE src0_sel:WORD_1
	v_exp_f16_sdwa v75, v27 dst_sel:WORD_1 dst_unused:UNUSED_PRESERVE src0_sel:WORD_1
	v_exp_f16_sdwa v76, v28 dst_sel:WORD_1 dst_unused:UNUSED_PRESERVE src0_sel:WORD_1
	v_exp_f16_sdwa v77, v29 dst_sel:WORD_1 dst_unused:UNUSED_PRESERVE src0_sel:WORD_1
	v_pk_add_f16 v39, v39, v51 neg_lo:[0,1] neg_hi:[0,1]
	v_pk_add_f16 v26, v74, 0
	v_pk_add_f16 v27, v75, 0
	v_pk_add_f16 v28, v76, 0
	v_pk_add_f16 v29, v77, 0
	v_pk_fma_f16 v10, v10, v74, 0
	v_pk_fma_f16 v11, v11, v75, 0
	v_pk_fma_f16 v12, v12, v76, 0
	v_pk_fma_f16 v13, v13, v77, 0
	v_pk_add_f16 v40, v40, v52 neg_lo:[0,1] neg_hi:[0,1]
	v_pk_add_f16 v41, v41, v53 neg_lo:[0,1] neg_hi:[0,1]
	v_pk_add_f16 v6, v6, v50 neg_lo:[0,1] neg_hi:[0,1]
	v_exp_f16_sdwa v74, v38 dst_sel:WORD_0 dst_unused:UNUSED_PAD src0_sel:WORD_0
	v_exp_f16_sdwa v75, v39 dst_sel:WORD_0 dst_unused:UNUSED_PAD src0_sel:WORD_0
	v_exp_f16_sdwa v76, v40 dst_sel:WORD_0 dst_unused:UNUSED_PAD src0_sel:WORD_0
	v_exp_f16_sdwa v77, v41 dst_sel:WORD_0 dst_unused:UNUSED_PAD src0_sel:WORD_0
	v_exp_f16_sdwa v74, v38 dst_sel:WORD_1 dst_unused:UNUSED_PRESERVE src0_sel:WORD_1
	v_exp_f16_sdwa v75, v39 dst_sel:WORD_1 dst_unused:UNUSED_PRESERVE src0_sel:WORD_1
	v_exp_f16_sdwa v76, v40 dst_sel:WORD_1 dst_unused:UNUSED_PRESERVE src0_sel:WORD_1
	v_exp_f16_sdwa v77, v41 dst_sel:WORD_1 dst_unused:UNUSED_PRESERVE src0_sel:WORD_1
	v_pk_add_f16 v7, v7, v51 neg_lo:[0,1] neg_hi:[0,1]
	v_pk_add_f16 v29, v29, v77
	v_pk_add_f16 v28, v28, v76
	v_pk_add_f16 v27, v27, v75
	v_pk_add_f16 v26, v26, v74
	v_pk_fma_f16 v13, v17, v77, v13
	v_pk_fma_f16 v12, v16, v76, v12
	v_pk_fma_f16 v11, v15, v75, v11
	v_pk_fma_f16 v10, v14, v74, v10
	v_pk_add_f16 v14, v22, v50 neg_lo:[0,1] neg_hi:[0,1]
	v_pk_add_f16 v15, v23, v51 neg_lo:[0,1] neg_hi:[0,1]
	v_pk_add_f16 v16, v24, v52 neg_lo:[0,1] neg_hi:[0,1]
	v_pk_add_f16 v17, v25, v53 neg_lo:[0,1] neg_hi:[0,1]
	v_pk_add_f16 v8, v8, v52 neg_lo:[0,1] neg_hi:[0,1]
	v_exp_f16_sdwa v22, v14 dst_sel:WORD_0 dst_unused:UNUSED_PAD src0_sel:WORD_0
	v_exp_f16_sdwa v23, v15 dst_sel:WORD_0 dst_unused:UNUSED_PAD src0_sel:WORD_0
	v_exp_f16_sdwa v24, v16 dst_sel:WORD_0 dst_unused:UNUSED_PAD src0_sel:WORD_0
	v_exp_f16_sdwa v25, v17 dst_sel:WORD_0 dst_unused:UNUSED_PAD src0_sel:WORD_0
	v_exp_f16_sdwa v22, v14 dst_sel:WORD_1 dst_unused:UNUSED_PRESERVE src0_sel:WORD_1
	v_exp_f16_sdwa v23, v15 dst_sel:WORD_1 dst_unused:UNUSED_PRESERVE src0_sel:WORD_1
	v_exp_f16_sdwa v24, v16 dst_sel:WORD_1 dst_unused:UNUSED_PRESERVE src0_sel:WORD_1
	v_exp_f16_sdwa v25, v17 dst_sel:WORD_1 dst_unused:UNUSED_PRESERVE src0_sel:WORD_1
	v_pk_add_f16 v9, v9, v53 neg_lo:[0,1] neg_hi:[0,1]
	v_pk_add_f16 v14, v26, v22
	v_pk_add_f16 v15, v27, v23
	v_pk_add_f16 v16, v28, v24
	v_pk_add_f16 v17, v29, v25
	v_pk_fma_f16 v10, v18, v22, v10
	v_pk_fma_f16 v11, v19, v23, v11
	v_pk_fma_f16 v12, v20, v24, v12
	v_pk_fma_f16 v13, v21, v25, v13
	v_pk_add_f16 v18, v57, v50 neg_lo:[0,1] neg_hi:[0,1]
	v_pk_add_f16 v19, v56, v51 neg_lo:[0,1] neg_hi:[0,1]
	v_pk_add_f16 v20, v55, v52 neg_lo:[0,1] neg_hi:[0,1]
	v_pk_add_f16 v21, v54, v53 neg_lo:[0,1] neg_hi:[0,1]
	v_exp_f16_sdwa v22, v18 dst_sel:WORD_0 dst_unused:UNUSED_PAD src0_sel:WORD_0
	v_exp_f16_sdwa v23, v19 dst_sel:WORD_0 dst_unused:UNUSED_PAD src0_sel:WORD_0
	v_exp_f16_sdwa v24, v20 dst_sel:WORD_0 dst_unused:UNUSED_PAD src0_sel:WORD_0
	v_exp_f16_sdwa v25, v21 dst_sel:WORD_0 dst_unused:UNUSED_PAD src0_sel:WORD_0
	v_exp_f16_sdwa v22, v18 dst_sel:WORD_1 dst_unused:UNUSED_PRESERVE src0_sel:WORD_1
	v_exp_f16_sdwa v23, v19 dst_sel:WORD_1 dst_unused:UNUSED_PRESERVE src0_sel:WORD_1
	v_exp_f16_sdwa v24, v20 dst_sel:WORD_1 dst_unused:UNUSED_PRESERVE src0_sel:WORD_1
	v_exp_f16_sdwa v25, v21 dst_sel:WORD_1 dst_unused:UNUSED_PRESERVE src0_sel:WORD_1
	v_pk_add_f16 v18, v61, v50 neg_lo:[0,1] neg_hi:[0,1]
	v_pk_add_f16 v17, v17, v25
	v_pk_add_f16 v16, v16, v24
	v_pk_add_f16 v15, v15, v23
	v_pk_add_f16 v14, v14, v22
	v_pk_fma_f16 v13, v33, v25, v13
	v_pk_fma_f16 v12, v32, v24, v12
	v_pk_fma_f16 v11, v31, v23, v11
	v_pk_fma_f16 v10, v30, v22, v10
	v_pk_add_f16 v19, v60, v51 neg_lo:[0,1] neg_hi:[0,1]
	v_pk_add_f16 v20, v59, v52 neg_lo:[0,1] neg_hi:[0,1]
	v_pk_add_f16 v21, v58, v53 neg_lo:[0,1] neg_hi:[0,1]
	v_exp_f16_sdwa v22, v18 dst_sel:WORD_0 dst_unused:UNUSED_PAD src0_sel:WORD_0
	v_exp_f16_sdwa v23, v19 dst_sel:WORD_0 dst_unused:UNUSED_PAD src0_sel:WORD_0
	v_exp_f16_sdwa v24, v20 dst_sel:WORD_0 dst_unused:UNUSED_PAD src0_sel:WORD_0
	v_exp_f16_sdwa v25, v21 dst_sel:WORD_0 dst_unused:UNUSED_PAD src0_sel:WORD_0
	v_exp_f16_sdwa v22, v18 dst_sel:WORD_1 dst_unused:UNUSED_PRESERVE src0_sel:WORD_1
	v_exp_f16_sdwa v23, v19 dst_sel:WORD_1 dst_unused:UNUSED_PRESERVE src0_sel:WORD_1
	v_exp_f16_sdwa v24, v20 dst_sel:WORD_1 dst_unused:UNUSED_PRESERVE src0_sel:WORD_1
	v_exp_f16_sdwa v25, v21 dst_sel:WORD_1 dst_unused:UNUSED_PRESERVE src0_sel:WORD_1
	v_pk_add_f16 v18, v34, v50 neg_lo:[0,1] neg_hi:[0,1]
	v_pk_add_f16 v14, v14, v22
	v_pk_add_f16 v15, v15, v23
	v_pk_add_f16 v16, v16, v24
	v_pk_add_f16 v17, v17, v25
	v_pk_fma_f16 v10, v46, v22, v10
	v_pk_fma_f16 v11, v47, v23, v11
	v_pk_fma_f16 v12, v48, v24, v12
	v_pk_fma_f16 v13, v49, v25, v13
	v_pk_add_f16 v19, v35, v51 neg_lo:[0,1] neg_hi:[0,1]
	v_pk_add_f16 v20, v36, v52 neg_lo:[0,1] neg_hi:[0,1]
	v_pk_add_f16 v21, v37, v53 neg_lo:[0,1] neg_hi:[0,1]
	v_exp_f16_sdwa v22, v18 dst_sel:WORD_0 dst_unused:UNUSED_PAD src0_sel:WORD_0
	v_exp_f16_sdwa v23, v19 dst_sel:WORD_0 dst_unused:UNUSED_PAD src0_sel:WORD_0
	v_exp_f16_sdwa v24, v20 dst_sel:WORD_0 dst_unused:UNUSED_PAD src0_sel:WORD_0
	v_exp_f16_sdwa v25, v21 dst_sel:WORD_0 dst_unused:UNUSED_PAD src0_sel:WORD_0
	v_exp_f16_sdwa v22, v18 dst_sel:WORD_1 dst_unused:UNUSED_PRESERVE src0_sel:WORD_1
	v_exp_f16_sdwa v23, v19 dst_sel:WORD_1 dst_unused:UNUSED_PRESERVE src0_sel:WORD_1
	v_exp_f16_sdwa v24, v20 dst_sel:WORD_1 dst_unused:UNUSED_PRESERVE src0_sel:WORD_1
	v_exp_f16_sdwa v25, v21 dst_sel:WORD_1 dst_unused:UNUSED_PRESERVE src0_sel:WORD_1
	v_pk_add_f16 v18, v69, v50 neg_lo:[0,1] neg_hi:[0,1]
	v_pk_add_f16 v17, v17, v25
	v_pk_add_f16 v16, v16, v24
	v_pk_add_f16 v15, v15, v23
	v_pk_add_f16 v14, v14, v22
	v_pk_fma_f16 v13, v65, v25, v13
	v_pk_fma_f16 v12, v64, v24, v12
	v_pk_fma_f16 v11, v63, v23, v11
	v_pk_fma_f16 v10, v62, v22, v10
	v_pk_add_f16 v19, v68, v51 neg_lo:[0,1] neg_hi:[0,1]
	v_pk_add_f16 v20, v67, v52 neg_lo:[0,1] neg_hi:[0,1]
	v_pk_add_f16 v21, v66, v53 neg_lo:[0,1] neg_hi:[0,1]
	v_exp_f16_sdwa v22, v18 dst_sel:WORD_0 dst_unused:UNUSED_PAD src0_sel:WORD_0
	v_exp_f16_sdwa v23, v19 dst_sel:WORD_0 dst_unused:UNUSED_PAD src0_sel:WORD_0
	v_exp_f16_sdwa v24, v20 dst_sel:WORD_0 dst_unused:UNUSED_PAD src0_sel:WORD_0
	v_exp_f16_sdwa v25, v21 dst_sel:WORD_0 dst_unused:UNUSED_PAD src0_sel:WORD_0
	v_exp_f16_sdwa v22, v18 dst_sel:WORD_1 dst_unused:UNUSED_PRESERVE src0_sel:WORD_1
	v_exp_f16_sdwa v23, v19 dst_sel:WORD_1 dst_unused:UNUSED_PRESERVE src0_sel:WORD_1
	v_exp_f16_sdwa v24, v20 dst_sel:WORD_1 dst_unused:UNUSED_PRESERVE src0_sel:WORD_1
	v_exp_f16_sdwa v25, v21 dst_sel:WORD_1 dst_unused:UNUSED_PRESERVE src0_sel:WORD_1
	v_pk_add_f16 v18, v73, v50 neg_lo:[0,1] neg_hi:[0,1]
	v_pk_add_f16 v14, v14, v22
	v_pk_add_f16 v15, v15, v23
	v_pk_add_f16 v16, v16, v24
	v_pk_add_f16 v17, v17, v25
	v_pk_fma_f16 v10, v82, v22, v10
	v_pk_fma_f16 v11, v83, v23, v11
	v_pk_fma_f16 v12, v84, v24, v12
	v_pk_fma_f16 v13, v85, v25, v13
	v_pk_add_f16 v19, v72, v51 neg_lo:[0,1] neg_hi:[0,1]
	v_pk_add_f16 v20, v71, v52 neg_lo:[0,1] neg_hi:[0,1]
	v_pk_add_f16 v21, v70, v53 neg_lo:[0,1] neg_hi:[0,1]
	v_exp_f16_sdwa v22, v18 dst_sel:WORD_0 dst_unused:UNUSED_PAD src0_sel:WORD_0
	v_exp_f16_sdwa v23, v19 dst_sel:WORD_0 dst_unused:UNUSED_PAD src0_sel:WORD_0
	v_exp_f16_sdwa v24, v20 dst_sel:WORD_0 dst_unused:UNUSED_PAD src0_sel:WORD_0
	v_exp_f16_sdwa v25, v21 dst_sel:WORD_0 dst_unused:UNUSED_PAD src0_sel:WORD_0
	v_exp_f16_sdwa v22, v18 dst_sel:WORD_1 dst_unused:UNUSED_PRESERVE src0_sel:WORD_1
	v_exp_f16_sdwa v23, v19 dst_sel:WORD_1 dst_unused:UNUSED_PRESERVE src0_sel:WORD_1
	v_exp_f16_sdwa v24, v20 dst_sel:WORD_1 dst_unused:UNUSED_PRESERVE src0_sel:WORD_1
	v_exp_f16_sdwa v25, v21 dst_sel:WORD_1 dst_unused:UNUSED_PRESERVE src0_sel:WORD_1
	s_nop 0
	v_pk_add_f16 v17, v17, v25
	v_pk_add_f16 v16, v16, v24
	v_pk_add_f16 v15, v15, v23
	v_pk_add_f16 v14, v14, v22
	v_pk_fma_f16 v21, v105, v25, v13
	v_pk_fma_f16 v20, v104, v24, v12
	v_pk_fma_f16 v19, v103, v23, v11
	v_pk_fma_f16 v18, v102, v22, v10
	v_mov_b32_e32 v13, v5
	v_mov_b32_e32 v12, v4
	v_mov_b32_e32 v11, v3
	v_mov_b32_e32 v10, v2
	v_exp_f16_sdwa v22, v6 dst_sel:WORD_0 dst_unused:UNUSED_PAD src0_sel:WORD_0
	v_exp_f16_sdwa v23, v7 dst_sel:WORD_0 dst_unused:UNUSED_PAD src0_sel:WORD_0
	v_exp_f16_sdwa v24, v8 dst_sel:WORD_0 dst_unused:UNUSED_PAD src0_sel:WORD_0
	v_exp_f16_sdwa v25, v9 dst_sel:WORD_0 dst_unused:UNUSED_PAD src0_sel:WORD_0
	v_exp_f16_sdwa v22, v6 dst_sel:WORD_1 dst_unused:UNUSED_PRESERVE src0_sel:WORD_1
	v_exp_f16_sdwa v23, v7 dst_sel:WORD_1 dst_unused:UNUSED_PRESERVE src0_sel:WORD_1
	v_exp_f16_sdwa v24, v8 dst_sel:WORD_1 dst_unused:UNUSED_PRESERVE src0_sel:WORD_1
	v_exp_f16_sdwa v25, v9 dst_sel:WORD_1 dst_unused:UNUSED_PRESERVE src0_sel:WORD_1
	s_nop 0
.LBB4_3:
	v_pk_add_f16 v2, v17, v25
	v_pk_add_f16 v5, v14, v22
	v_pk_add_f16 v3, v16, v24
	v_pk_fma_f16 v6, v10, v22, v18
	v_pk_fma_f16 v7, v11, v23, v19
	v_rcp_f16_e32 v10, v5
	v_rcp_f16_sdwa v11, v5 dst_sel:DWORD dst_unused:UNUSED_PAD src0_sel:WORD_1
	v_rcp_f16_e32 v5, v2
	v_rcp_f16_sdwa v2, v2 dst_sel:DWORD dst_unused:UNUSED_PAD src0_sel:WORD_1
	v_pk_fma_f16 v9, v13, v25, v21
	v_rcp_f16_e32 v13, v3
	v_rcp_f16_sdwa v3, v3 dst_sel:DWORD dst_unused:UNUSED_PAD src0_sel:WORD_1
	v_pk_add_f16 v4, v15, v23
	v_pack_b32_f16 v2, v5, v2
	v_pk_fma_f16 v8, v12, v24, v20
	v_rcp_f16_e32 v12, v4
	v_rcp_f16_sdwa v14, v4 dst_sel:DWORD dst_unused:UNUSED_PAD src0_sel:WORD_1
	v_pk_mul_f16 v18, v9, v2
	v_pack_b32_f16 v2, v13, v3
	v_pk_mul_f16 v19, v8, v2
	ds_read_b128 v[2:5], v203
	v_pack_b32_f16 v8, v12, v14
	v_pk_mul_f16 v20, v7, v8
	v_pack_b32_f16 v7, v10, v11
	v_pk_mul_f16 v21, v6, v7
	s_waitcnt lgkmcnt(0)
	v_cvt_f32_f16_e32 v6, v2
	v_cvt_f32_f16_sdwa v7, v2 dst_sel:DWORD dst_unused:UNUSED_PAD src0_sel:WORD_1
	v_cvt_f32_f16_sdwa v9, v141 dst_sel:DWORD dst_unused:UNUSED_PAD src0_sel:WORD_1
	v_cvt_f32_f16_e32 v8, v141
	v_cvt_f32_f16_e32 v2, v3
	v_cvt_f32_f16_sdwa v3, v3 dst_sel:DWORD dst_unused:UNUSED_PAD src0_sel:WORD_1
	v_cvt_f32_f16_sdwa v11, v140 dst_sel:DWORD dst_unused:UNUSED_PAD src0_sel:WORD_1
	v_cvt_f32_f16_e32 v10, v140
	v_pk_add_f32 v[6:7], v[6:7], v[8:9]
	v_cvt_f32_f16_sdwa v13, v138 dst_sel:DWORD dst_unused:UNUSED_PAD src0_sel:WORD_1
	v_cvt_f32_f16_e32 v12, v138
	v_pk_add_f32 v[8:9], v[2:3], v[10:11]
	v_cvt_f32_f16_e32 v2, v4
	v_cvt_f32_f16_sdwa v3, v4 dst_sel:DWORD dst_unused:UNUSED_PAD src0_sel:WORD_1
	v_cvt_f32_f16_sdwa v11, v139 dst_sel:DWORD dst_unused:UNUSED_PAD src0_sel:WORD_1
	v_cvt_f32_f16_e32 v10, v139
	v_cvt_f32_f16_e32 v4, v5
	v_cvt_f32_f16_sdwa v5, v5 dst_sel:DWORD dst_unused:UNUSED_PAD src0_sel:WORD_1
	v_max_f32_e32 v14, 0, v6
	v_pk_add_f32 v[10:11], v[2:3], v[10:11]
	v_max_f32_e32 v15, 0, v7
	v_pk_add_f32 v[12:13], v[4:5], v[12:13]
	v_max_f32_e32 v16, 0, v8
	v_max_f32_e32 v17, 0, v9
	v_max_f32_e32 v2, 0, v10
	v_max_f32_e32 v3, 0, v11
	v_max_f32_e32 v4, 0, v12
	v_max_f32_e32 v5, 0, v13
	v_cvt_pk_f16_f32 v5, v4, v5
	v_cvt_pk_f16_f32 v4, v2, v3
	v_cvt_pk_f16_f32 v3, v16, v17
	v_cvt_pk_f16_f32 v2, v14, v15
	ds_write_b128 v203, v[2:5]
	v_add_u32_e32 v16, v205, v204
	ds_read_b128 v[2:5], v16
	v_cvt_pk_f16_f32 v6, v6, v7
	v_cvt_pk_f16_f32 v7, v8, v9
	v_cvt_pk_f16_f32 v8, v10, v11
	v_cvt_pk_f16_f32 v9, v12, v13
	s_waitcnt lgkmcnt(0)
	v_cvt_f32_f16_e32 v10, v2
	v_cvt_f32_f16_sdwa v11, v2 dst_sel:DWORD dst_unused:UNUSED_PAD src0_sel:WORD_1
	v_cvt_f32_f16_sdwa v13, v97 dst_sel:DWORD dst_unused:UNUSED_PAD src0_sel:WORD_1
	v_cvt_f32_f16_e32 v12, v97
	v_lshl_or_b32 v22, v199, 9, v194
	v_add_u32_e32 v2, v193, v22
	buffer_store_dwordx4 v[6:9], v2, s[40:43], 0 offen sc1
	s_add_i32 s46, s46, 1
	s_cmp_eq_u32 s46, s33
	v_pk_add_f32 v[6:7], v[10:11], v[12:13]
	v_cvt_f32_f16_e32 v8, v3
	v_cvt_f32_f16_sdwa v9, v3 dst_sel:DWORD dst_unused:UNUSED_PAD src0_sel:WORD_1
	v_cvt_f32_f16_sdwa v11, v96 dst_sel:DWORD dst_unused:UNUSED_PAD src0_sel:WORD_1
	v_cvt_f32_f16_e32 v10, v96
	v_cvt_pk_f16_f32 v2, v6, v7
	v_max_f32_e32 v3, 0, v6
	v_max_f32_e32 v17, 0, v7
	v_pk_add_f32 v[10:11], v[8:9], v[10:11]
	v_cvt_f32_f16_e32 v6, v4
	v_cvt_f32_f16_sdwa v7, v4 dst_sel:DWORD dst_unused:UNUSED_PAD src0_sel:WORD_1
	v_cvt_f32_f16_sdwa v9, v95 dst_sel:DWORD dst_unused:UNUSED_PAD src0_sel:WORD_1
	v_cvt_f32_f16_e32 v8, v95
	v_cvt_f32_f16_e32 v4, v5
	v_cvt_f32_f16_sdwa v5, v5 dst_sel:DWORD dst_unused:UNUSED_PAD src0_sel:WORD_1
	v_cvt_f32_f16_sdwa v13, v94 dst_sel:DWORD dst_unused:UNUSED_PAD src0_sel:WORD_1
	v_cvt_f32_f16_e32 v12, v94
	v_pk_add_f32 v[14:15], v[6:7], v[8:9]
	v_max_f32_e32 v23, 0, v10
	v_max_f32_e32 v24, 0, v11
	v_pk_add_f32 v[12:13], v[4:5], v[12:13]
	v_max_f32_e32 v6, 0, v14
	v_max_f32_e32 v8, 0, v15
	v_max_f32_e32 v4, 0, v12
	v_max_f32_e32 v5, 0, v13
	v_cvt_pk_f16_f32 v7, v4, v5
	v_cvt_pk_f16_f32 v6, v6, v8
	v_cvt_pk_f16_f32 v5, v23, v24
	v_cvt_pk_f16_f32 v4, v3, v17
	ds_write_b128 v16, v[4:7]
	v_add_u32_e32 v23, v189, v202
	ds_read_b128 v[6:9], v23
	v_cvt_pk_f16_f32 v3, v10, v11
	v_cvt_pk_f16_f32 v4, v14, v15
	v_cvt_pk_f16_f32 v5, v12, v13
	v_cvt_f32_f16_sdwa v13, v45 dst_sel:DWORD dst_unused:UNUSED_PAD src0_sel:WORD_1
	s_waitcnt lgkmcnt(0)
	v_cvt_f32_f16_e32 v10, v6
	v_cvt_f32_f16_sdwa v11, v6 dst_sel:DWORD dst_unused:UNUSED_PAD src0_sel:WORD_1
	v_cvt_f32_f16_e32 v12, v45
	v_cvt_f32_f16_e32 v6, v7
	v_cvt_f32_f16_sdwa v7, v7 dst_sel:DWORD dst_unused:UNUSED_PAD src0_sel:WORD_1
	v_cvt_f32_f16_sdwa v15, v44 dst_sel:DWORD dst_unused:UNUSED_PAD src0_sel:WORD_1
	v_cvt_f32_f16_e32 v14, v44
	v_pk_add_f32 v[10:11], v[10:11], v[12:13]
	v_cvt_f32_f16_sdwa v17, v42 dst_sel:DWORD dst_unused:UNUSED_PAD src0_sel:WORD_1
	v_cvt_f32_f16_e32 v16, v42
	v_pk_add_f32 v[12:13], v[6:7], v[14:15]
	v_cvt_f32_f16_e32 v6, v8
	v_cvt_f32_f16_sdwa v7, v8 dst_sel:DWORD dst_unused:UNUSED_PAD src0_sel:WORD_1
	v_cvt_f32_f16_sdwa v15, v43 dst_sel:DWORD dst_unused:UNUSED_PAD src0_sel:WORD_1
	v_cvt_f32_f16_e32 v14, v43
	v_cvt_f32_f16_e32 v8, v9
	v_cvt_f32_f16_sdwa v9, v9 dst_sel:DWORD dst_unused:UNUSED_PAD src0_sel:WORD_1
	v_max_f32_e32 v25, 0, v10
	v_pk_add_f32 v[14:15], v[6:7], v[14:15]
	v_max_f32_e32 v26, 0, v11
	v_pk_add_f32 v[16:17], v[8:9], v[16:17]
	v_max_f32_e32 v27, 0, v12
	v_max_f32_e32 v28, 0, v13
	v_max_f32_e32 v6, 0, v14
	v_max_f32_e32 v7, 0, v15
	v_max_f32_e32 v8, 0, v16
	v_max_f32_e32 v9, 0, v17
	v_cvt_pk_f16_f32 v9, v8, v9
	v_cvt_pk_f16_f32 v8, v6, v7
	v_cvt_pk_f16_f32 v7, v27, v28
	v_cvt_pk_f16_f32 v6, v25, v26
	ds_write_b128 v23, v[6:9]
	ds_read_b128 v[6:9], v168
	v_add_u32_e32 v24, v195, v22
	buffer_store_dwordx4 v[2:5], v24, s[40:43], 0 offen sc1
	s_nop 1
	v_cvt_pk_f16_f32 v2, v10, v11
	v_cvt_pk_f16_f32 v3, v12, v13
	s_waitcnt lgkmcnt(0)
	v_cvt_f32_f16_e32 v10, v6
	v_cvt_f32_f16_sdwa v11, v6 dst_sel:DWORD dst_unused:UNUSED_PAD src0_sel:WORD_1
	v_cvt_f32_f16_e32 v12, v21
	v_cvt_f32_f16_sdwa v13, v21 dst_sel:DWORD dst_unused:UNUSED_PAD src0_sel:WORD_1
	v_cvt_pk_f16_f32 v4, v14, v15
	v_cvt_pk_f16_f32 v5, v16, v17
	v_add_u32_e32 v6, v196, v22
	buffer_store_dwordx4 v[2:5], v6, s[40:43], 0 offen sc1
	v_cvt_f32_f16_e32 v6, v7
	v_cvt_f32_f16_sdwa v7, v7 dst_sel:DWORD dst_unused:UNUSED_PAD src0_sel:WORD_1
	v_pk_add_f32 v[4:5], v[10:11], v[12:13]
	v_cvt_f32_f16_e32 v10, v20
	v_cvt_f32_f16_sdwa v11, v20 dst_sel:DWORD dst_unused:UNUSED_PAD src0_sel:WORD_1
	v_cvt_pk_f16_f32 v2, v4, v5
	v_max_f32_e32 v12, 0, v4
	v_max_f32_e32 v13, 0, v5
	v_pk_add_f32 v[4:5], v[6:7], v[10:11]
	v_cvt_f32_f16_e32 v6, v8
	v_cvt_f32_f16_sdwa v7, v8 dst_sel:DWORD dst_unused:UNUSED_PAD src0_sel:WORD_1
	v_cvt_f32_f16_e32 v10, v19
	v_cvt_f32_f16_sdwa v11, v19 dst_sel:DWORD dst_unused:UNUSED_PAD src0_sel:WORD_1
	v_cvt_f32_f16_e32 v8, v9
	v_cvt_f32_f16_sdwa v9, v9 dst_sel:DWORD dst_unused:UNUSED_PAD src0_sel:WORD_1
	v_cvt_pk_f16_f32 v3, v4, v5
	v_pk_add_f32 v[6:7], v[6:7], v[10:11]
	v_cvt_f32_f16_e32 v10, v18
	v_cvt_f32_f16_sdwa v11, v18 dst_sel:DWORD dst_unused:UNUSED_PAD src0_sel:WORD_1
	v_max_f32_e32 v14, 0, v4
	v_cvt_pk_f16_f32 v4, v6, v7
	v_max_f32_e32 v16, 0, v6
	v_max_f32_e32 v17, 0, v7
	v_pk_add_f32 v[6:7], v[8:9], v[10:11]
	v_max_f32_e32 v15, 0, v5
	v_cvt_pk_f16_f32 v5, v6, v7
	v_max_f32_e32 v6, 0, v6
	v_max_f32_e32 v7, 0, v7
	v_cvt_pk_f16_f32 v9, v6, v7
	v_cvt_pk_f16_f32 v8, v16, v17
	v_cvt_pk_f16_f32 v7, v14, v15
	v_cvt_pk_f16_f32 v6, v12, v13
	v_add_u32_e32 v10, v197, v22
	buffer_store_dwordx4 v[2:5], v10, s[40:43], 0 offen sc1
	ds_write_b128 v168, v[6:9]
	s_cbranch_scc1 .LBB4_155
.LBB4_4:
	global_load_dwordx4 v[2:5], v[170:171], off
	global_load_dwordx4 v[8:11], v[172:173], off
	global_load_dwordx4 v[22:25], v[170:171], off offset:16
	global_load_dwordx4 v[26:29], v[172:173], off offset:16
	s_lshl_b32 s48, s46, 3
	s_add_i32 s48, s48, s44
	v_or_b32_e32 v199, s48, v178
	v_add_u32_e32 v168, v199, v181
	v_add_u32_e32 v201, -1, v199
	v_mul_lo_u32 v6, v168, s47
	v_or_b32_e32 v7, v201, v182
	v_or_b32_e32 v6, v6, v166
	s_mov_b64 s[4:5], -1
	s_and_b64 vcc, exec, s[26:27]
	v_cmp_gt_u32_e64 s[2:3], 64, v7
	v_lshlrev_b32_e32 v200, 1, v6
	s_waitcnt vmcnt(3)
	v_cvt_pk_f16_f32 v6, v2, v3
	s_waitcnt vmcnt(2)
	v_cvt_pk_f16_f32 v2, v8, v9
	v_cvt_pk_f16_f32 v7, v4, v5
	v_cvt_pk_f16_f32 v3, v10, v11
	s_waitcnt vmcnt(1)
	v_cvt_pk_f16_f32 v8, v22, v23
	s_waitcnt vmcnt(0)
	v_cvt_pk_f16_f32 v4, v26, v27
	v_cvt_pk_f16_f32 v9, v24, v25
	v_cvt_pk_f16_f32 v5, v28, v29
	s_cbranch_vccz .LBB4_42
	global_load_dwordx3 v[154:156], v169, s[10:11]
	v_cmp_lt_u32_e64 s[64:65], 0, v199
	v_cmp_gt_u32_e64 s[66:67], 63, v199
	v_cmp_lt_u32_e64 s[68:69], 0, v180
	v_cmp_gt_u32_e64 s[70:71], 60, v180
	buffer_load_dwordx4 v[206:209], v200, s[36:39], 0 offen
	s_and_b64 s[72:73], s[68:69], s[64:65]
	s_and_b64 s[74:75], s[68:69], s[66:67]
	s_and_b64 s[76:77], s[70:71], s[64:65]
	s_and_b64 s[78:79], s[70:71], s[66:67]
	v_mov_b32_e32 v122, v6
	v_mov_b32_e32 v123, v7
	v_mov_b32_e32 v124, v8
	v_mov_b32_e32 v125, v9
	v_mov_b32_e32 v82, v2
	v_mov_b32_e32 v83, v3
	v_mov_b32_e32 v84, v4
	v_mov_b32_e32 v85, v5
	v_mov_b32_e32 v138, v6
	v_mov_b32_e32 v139, v7
	v_mov_b32_e32 v140, v8
	v_mov_b32_e32 v141, v9
	v_mov_b32_e32 v106, v2
	v_mov_b32_e32 v107, v3
	v_mov_b32_e32 v108, v4
	v_mov_b32_e32 v109, v5
	v_mov_b32_e32 v146, v6
	v_mov_b32_e32 v147, v7
	v_mov_b32_e32 v148, v8
	v_mov_b32_e32 v149, v9
	v_mov_b32_e32 v126, v2
	v_mov_b32_e32 v127, v3
	v_mov_b32_e32 v128, v4
	v_mov_b32_e32 v129, v5
	v_mov_b32_e32 v94, v6
	v_mov_b32_e32 v95, v7
	v_mov_b32_e32 v96, v8
	v_mov_b32_e32 v97, v9
	v_mov_b32_e32 v54, v2
	v_mov_b32_e32 v55, v3
	v_mov_b32_e32 v56, v4
	v_mov_b32_e32 v57, v5
	v_mov_b32_e32 v134, v6
	v_mov_b32_e32 v135, v7
	v_mov_b32_e32 v136, v8
	v_mov_b32_e32 v137, v9
	v_mov_b32_e32 v98, v2
	v_mov_b32_e32 v99, v3
	v_mov_b32_e32 v100, v4
	v_mov_b32_e32 v101, v5
	v_mov_b32_e32 v62, v6
	v_mov_b32_e32 v63, v7
	v_mov_b32_e32 v64, v8
	v_mov_b32_e32 v65, v9
	v_mov_b32_e32 v30, v2
	v_mov_b32_e32 v31, v3
	v_mov_b32_e32 v32, v4
	v_mov_b32_e32 v33, v5
	v_mov_b32_e32 v102, v6
	v_mov_b32_e32 v103, v7
	v_mov_b32_e32 v104, v8
	v_mov_b32_e32 v105, v9
	v_mov_b32_e32 v58, v2
	v_mov_b32_e32 v59, v3
	v_mov_b32_e32 v60, v4
	v_mov_b32_e32 v61, v5
	v_mov_b32_e32 v34, v6
	v_mov_b32_e32 v35, v7
	v_mov_b32_e32 v36, v8
	v_mov_b32_e32 v37, v9
	v_mov_b32_e32 v18, v2
	v_mov_b32_e32 v19, v3
	v_mov_b32_e32 v20, v4
	v_mov_b32_e32 v21, v5
	v_mov_b32_e32 v66, v6
	v_mov_b32_e32 v67, v7
	v_mov_b32_e32 v68, v8
	v_mov_b32_e32 v69, v9
	v_mov_b32_e32 v26, v2
	v_mov_b32_e32 v27, v3
	v_mov_b32_e32 v28, v4
	v_mov_b32_e32 v29, v5
	v_mov_b32_e32 v86, v6
	v_mov_b32_e32 v87, v7
	v_mov_b32_e32 v88, v8
	v_mov_b32_e32 v89, v9
	v_mov_b32_e32 v38, v2
	v_mov_b32_e32 v39, v3
	v_mov_b32_e32 v40, v4
	v_mov_b32_e32 v41, v5
	v_mov_b32_e32 v130, v6
	v_mov_b32_e32 v131, v7
	v_mov_b32_e32 v132, v8
	v_mov_b32_e32 v133, v9
	v_mov_b32_e32 v70, v2
	v_mov_b32_e32 v71, v3
	v_mov_b32_e32 v72, v4
	v_mov_b32_e32 v73, v5
	v_mov_b32_e32 v142, v6
	v_mov_b32_e32 v143, v7
	v_mov_b32_e32 v144, v8
	v_mov_b32_e32 v145, v9
	v_mov_b32_e32 v90, v2
	v_mov_b32_e32 v91, v3
	v_mov_b32_e32 v92, v4
	v_mov_b32_e32 v93, v5
	v_mov_b32_e32 v150, v6
	v_mov_b32_e32 v151, v7
	v_mov_b32_e32 v152, v8
	v_mov_b32_e32 v153, v9
	v_mov_b32_e32 v110, v2
	v_mov_b32_e32 v111, v3
	v_mov_b32_e32 v112, v4
	v_mov_b32_e32 v113, v5
	v_mov_b32_e32 v14, v6
	v_mov_b32_e32 v15, v7
	v_mov_b32_e32 v16, v8
	v_mov_b32_e32 v17, v9
	v_mov_b32_e32 v10, v2
	v_mov_b32_e32 v11, v3
	v_mov_b32_e32 v12, v4
	v_mov_b32_e32 v13, v5
	v_add_u32_e32 v245, 0xfffe7c00, v200
	v_add_u32_e32 v246, 0xfffe8000, v200
	s_mov_b64 exec, s[72:73]
	buffer_load_dwordx4 v[122:125], v245, s[36:39], 0 offen
	buffer_load_dwordx4 v[82:85], v245, s[36:39], 0 offen offset:512
	s_mov_b64 exec, -1
	s_mov_b64 exec, s[68:69]
	buffer_load_dwordx4 v[138:141], v246, s[36:39], 0 offen offset:512
	buffer_load_dwordx4 v[106:109], v246, s[36:39], 0 offen offset:1024
	s_mov_b64 exec, -1
	s_mov_b64 exec, s[74:75]
	buffer_load_dwordx4 v[146:149], v246, s[36:39], 0 offen offset:2048
	buffer_load_dwordx4 v[126:129], v246, s[36:39], 0 offen offset:2560
	s_mov_b64 exec, -1
	v_add_u32_e32 v245, 0xfffffc00, v200
	s_mov_b64 exec, s[64:65]
	buffer_load_dwordx4 v[94:97], v245, s[36:39], 0 offen
	buffer_load_dwordx4 v[54:57], v245, s[36:39], 0 offen offset:512
	s_mov_b64 exec, -1
	buffer_load_dwordx4 v[118:121], v200, s[36:39], 0 offen offset:512
	buffer_load_dwordx4 v[74:77], v200, s[36:39], 0 offen offset:1024
	s_mov_b64 exec, s[66:67]
	buffer_load_dwordx4 v[134:137], v200, s[36:39], 0 offen offset:2048
	buffer_load_dwordx4 v[98:101], v200, s[36:39], 0 offen offset:2560
	s_mov_b64 exec, -1
	v_add_u32_e32 v245, 0x17c00, v200
	v_add_u32_e32 v246, 0x18000, v200
	s_mov_b64 exec, s[64:65]
	buffer_load_dwordx4 v[62:65], v245, s[36:39], 0 offen
	buffer_load_dwordx4 v[30:33], v245, s[36:39], 0 offen offset:512
	s_mov_b64 exec, -1
	buffer_load_dwordx4 v[78:81], v246, s[36:39], 0 offen offset:512
	buffer_load_dwordx4 v[42:45], v246, s[36:39], 0 offen offset:1024
	s_mov_b64 exec, s[66:67]
	buffer_load_dwordx4 v[102:105], v246, s[36:39], 0 offen offset:2048
	buffer_load_dwordx4 v[58:61], v246, s[36:39], 0 offen offset:2560
	s_mov_b64 exec, -1
	v_add_u32_e32 v245, 0x18000, v200
	buffer_load_dwordx4 v[162:165], v245, s[36:39], 0 offen
	v_add_u32_e32 v246, 0x30000, v200
	buffer_load_dwordx4 v[158:161], v246, s[36:39], 0 offen
	v_add_u32_e32 v245, 0x2fc00, v200
	v_add_u32_e32 v246, 0x30000, v200
	v_add_u32_e32 v247, 0x47c00, v200
	v_add_u32_e32 v248, 0x48000, v200
	v_add_u32_e32 v249, 0x5fc00, v200
	v_add_u32_e32 v250, 0x60000, v200
	s_waitcnt vmcnt(21)
	v_cvt_f16_f32_e32 v202, v155
	v_cvt_f16_f32_e32 v204, v154
	v_cvt_f16_f32_e32 v203, v156
	v_add_u32_e32 v251, 0x48000, v200
	buffer_load_dwordx4 v[154:157], v251, s[36:39], 0 offen
	s_mov_b64 s[4:5], 0
	s_waitcnt vmcnt(3)
	v_pk_mul_f16 v212, v204, v209 op_sel_hi:[0,1]
	v_pk_mul_f16 v216, v202, v209 op_sel_hi:[0,1]
	v_pk_mul_f16 v220, v203, v209 op_sel_hi:[0,1]
	v_pk_mul_f16 v205, v204, v206 op_sel_hi:[0,1]
	v_pk_mul_f16 v210, v204, v207 op_sel_hi:[0,1]
	v_pk_mul_f16 v211, v204, v208 op_sel_hi:[0,1]
	v_pk_mul_f16 v213, v202, v206 op_sel_hi:[0,1]
	s_mov_b64 exec, s[64:65]
	buffer_load_dwordx4 v[34:37], v245, s[36:39], 0 offen
	buffer_load_dwordx4 v[18:21], v245, s[36:39], 0 offen offset:512
	s_mov_b64 exec, -1
	v_pk_mul_f16 v214, v202, v207 op_sel_hi:[0,1]
	v_pk_mul_f16 v215, v202, v208 op_sel_hi:[0,1]
	v_pk_mul_f16 v217, v203, v206 op_sel_hi:[0,1]
	v_pk_mul_f16 v218, v203, v207 op_sel_hi:[0,1]
	v_pk_mul_f16 v219, v203, v208 op_sel_hi:[0,1]
	v_pk_fma_f16 v125, v125, v209, v212
	v_pk_fma_f16 v141, v141, v209, v216
	v_pk_fma_f16 v149, v149, v209, v220
	v_pk_fma_f16 v221, v97, v209, v212
	v_pk_fma_f16 v225, v121, v209, v216
	v_pk_fma_f16 v229, v137, v209, v220
	v_pk_fma_f16 v212, v65, v209, v212
	v_pk_fma_f16 v216, v81, v209, v216
	buffer_load_dwordx4 v[46:49], v246, s[36:39], 0 offen offset:512
	buffer_load_dwordx4 v[22:25], v246, s[36:39], 0 offen offset:1024
	v_pk_fma_f16 v209, v105, v209, v220
	v_pk_maximum3_f16 v220, v125, v141, v149
	v_pk_fma_f16 v124, v124, v208, v211
	v_pk_fma_f16 v123, v123, v207, v210
	v_pk_fma_f16 v122, v122, v206, v205
	v_pk_fma_f16 v140, v140, v208, v215
	v_pk_fma_f16 v139, v139, v207, v214
	v_pk_fma_f16 v138, v138, v206, v213
	v_pk_fma_f16 v148, v148, v208, v219
	v_pk_fma_f16 v147, v147, v207, v218
	v_pk_fma_f16 v146, v146, v206, v217
	v_pk_fma_f16 v222, v96, v208, v211
	v_pk_fma_f16 v223, v95, v207, v210
	v_pk_fma_f16 v224, v94, v206, v205
	v_pk_fma_f16 v226, v120, v208, v215
	v_pk_fma_f16 v227, v119, v207, v214
	s_mov_b64 exec, s[66:67]
	buffer_load_dwordx4 v[66:69], v246, s[36:39], 0 offen offset:2048
	buffer_load_dwordx4 v[26:29], v246, s[36:39], 0 offen offset:2560
	s_mov_b64 exec, -1
	v_pk_fma_f16 v228, v118, v206, v213
	v_pk_fma_f16 v230, v136, v208, v219
	v_pk_fma_f16 v231, v135, v207, v218
	v_pk_fma_f16 v232, v134, v206, v217
	v_pk_fma_f16 v211, v64, v208, v211
	v_pk_fma_f16 v210, v63, v207, v210
	v_pk_fma_f16 v205, v62, v206, v205
	v_pk_fma_f16 v215, v80, v208, v215
	v_pk_fma_f16 v214, v79, v207, v214
	v_pk_fma_f16 v213, v78, v206, v213
	v_pk_fma_f16 v208, v104, v208, v219
	v_pk_fma_f16 v207, v103, v207, v218
	v_pk_fma_f16 v206, v102, v206, v217
	v_pk_maximum3_f16 v217, v122, v138, v146
	v_pk_maximum3_f16 v218, v123, v139, v147
	v_pk_maximum3_f16 v219, v124, v140, v148
	v_pk_maximum3_f16 v236, v221, v225, v229
	v_pk_maximum3_f16 v240, v212, v216, v209
	v_pk_maximum3_f16 v233, v224, v228, v232
	v_pk_maximum3_f16 v234, v223, v227, v231
	v_pk_maximum3_f16 v235, v222, v226, v230
	v_pk_maximum3_f16 v237, v205, v213, v206
	v_pk_maximum3_f16 v238, v210, v214, v207
	v_pk_maximum3_f16 v220, v220, v236, v240
	v_pk_maximum3_f16 v239, v211, v215, v208
	v_pk_maximum3_f16 v217, v217, v233, v237
	v_pk_maximum3_f16 v218, v218, v234, v238
	v_pk_maximum3_f16 v219, v219, v235, v239
	v_pk_add_f16 v125, v125, v220 neg_lo:[0,1] neg_hi:[0,1]
	s_mov_b64 exec, s[64:65]
	buffer_load_dwordx4 v[86:89], v247, s[36:39], 0 offen
	buffer_load_dwordx4 v[38:41], v247, s[36:39], 0 offen offset:512
	s_mov_b64 exec, -1
	v_pk_add_f16 v122, v122, v217 neg_lo:[0,1] neg_hi:[0,1]
	v_pk_add_f16 v123, v123, v218 neg_lo:[0,1] neg_hi:[0,1]
	v_pk_add_f16 v124, v124, v219 neg_lo:[0,1] neg_hi:[0,1]
	v_pk_add_f16 v138, v138, v217 neg_lo:[0,1] neg_hi:[0,1]
	v_exp_f16_sdwa v233, v122 dst_sel:WORD_0 dst_unused:UNUSED_PAD src0_sel:WORD_0
	v_exp_f16_sdwa v234, v123 dst_sel:WORD_0 dst_unused:UNUSED_PAD src0_sel:WORD_0
	v_exp_f16_sdwa v235, v124 dst_sel:WORD_0 dst_unused:UNUSED_PAD src0_sel:WORD_0
	v_exp_f16_sdwa v236, v125 dst_sel:WORD_0 dst_unused:UNUSED_PAD src0_sel:WORD_0
	v_exp_f16_sdwa v233, v122 dst_sel:WORD_1 dst_unused:UNUSED_PRESERVE src0_sel:WORD_1
	v_exp_f16_sdwa v234, v123 dst_sel:WORD_1 dst_unused:UNUSED_PRESERVE src0_sel:WORD_1
	v_exp_f16_sdwa v235, v124 dst_sel:WORD_1 dst_unused:UNUSED_PRESERVE src0_sel:WORD_1
	v_exp_f16_sdwa v236, v125 dst_sel:WORD_1 dst_unused:UNUSED_PRESERVE src0_sel:WORD_1
	v_pk_add_f16 v139, v139, v218 neg_lo:[0,1] neg_hi:[0,1]
	v_pk_add_f16 v125, v233, 0
	v_pk_fma_f16 v85, v85, v236, 0
	v_pk_add_f16 v122, v236, 0
	v_pk_add_f16 v123, v235, 0
	v_pk_add_f16 v124, v234, 0
	v_pk_fma_f16 v84, v84, v235, 0
	v_pk_fma_f16 v83, v83, v234, 0
	v_pk_fma_f16 v82, v82, v233, 0
	v_pk_add_f16 v140, v140, v219 neg_lo:[0,1] neg_hi:[0,1]
	buffer_load_dwordx4 v[114:117], v248, s[36:39], 0 offen offset:512
	buffer_load_dwordx4 v[50:53], v248, s[36:39], 0 offen offset:1024
	v_pk_add_f16 v141, v141, v220 neg_lo:[0,1] neg_hi:[0,1]
	v_exp_f16_sdwa v233, v138 dst_sel:WORD_0 dst_unused:UNUSED_PAD src0_sel:WORD_0
	v_exp_f16_sdwa v234, v139 dst_sel:WORD_0 dst_unused:UNUSED_PAD src0_sel:WORD_0
	v_exp_f16_sdwa v235, v140 dst_sel:WORD_0 dst_unused:UNUSED_PAD src0_sel:WORD_0
	v_exp_f16_sdwa v236, v141 dst_sel:WORD_0 dst_unused:UNUSED_PAD src0_sel:WORD_0
	v_exp_f16_sdwa v233, v138 dst_sel:WORD_1 dst_unused:UNUSED_PRESERVE src0_sel:WORD_1
	v_exp_f16_sdwa v234, v139 dst_sel:WORD_1 dst_unused:UNUSED_PRESERVE src0_sel:WORD_1
	v_exp_f16_sdwa v235, v140 dst_sel:WORD_1 dst_unused:UNUSED_PRESERVE src0_sel:WORD_1
	v_exp_f16_sdwa v236, v141 dst_sel:WORD_1 dst_unused:UNUSED_PRESERVE src0_sel:WORD_1
	v_pk_add_f16 v125, v125, v233
	v_pk_fma_f16 v85, v109, v236, v85
	v_pk_add_f16 v109, v149, v220 neg_lo:[0,1] neg_hi:[0,1]
	v_pk_add_f16 v124, v124, v234
	v_pk_add_f16 v123, v123, v235
	v_pk_add_f16 v122, v122, v236
	v_pk_fma_f16 v82, v106, v233, v82
	v_pk_fma_f16 v83, v107, v234, v83
	v_pk_fma_f16 v84, v108, v235, v84
	v_pk_add_f16 v106, v146, v217 neg_lo:[0,1] neg_hi:[0,1]
	v_pk_add_f16 v107, v147, v218 neg_lo:[0,1] neg_hi:[0,1]
	v_pk_add_f16 v108, v148, v219 neg_lo:[0,1] neg_hi:[0,1]
	v_exp_f16_sdwa v138, v106 dst_sel:WORD_0 dst_unused:UNUSED_PAD src0_sel:WORD_0
	v_exp_f16_sdwa v139, v107 dst_sel:WORD_0 dst_unused:UNUSED_PAD src0_sel:WORD_0
	v_exp_f16_sdwa v140, v108 dst_sel:WORD_0 dst_unused:UNUSED_PAD src0_sel:WORD_0
	v_exp_f16_sdwa v141, v109 dst_sel:WORD_0 dst_unused:UNUSED_PAD src0_sel:WORD_0
	v_exp_f16_sdwa v138, v106 dst_sel:WORD_1 dst_unused:UNUSED_PRESERVE src0_sel:WORD_1
	v_exp_f16_sdwa v139, v107 dst_sel:WORD_1 dst_unused:UNUSED_PRESERVE src0_sel:WORD_1
	v_exp_f16_sdwa v140, v108 dst_sel:WORD_1 dst_unused:UNUSED_PRESERVE src0_sel:WORD_1
	v_exp_f16_sdwa v141, v109 dst_sel:WORD_1 dst_unused:UNUSED_PRESERVE src0_sel:WORD_1
	v_pk_add_f16 v109, v125, v138
	v_pk_add_f16 v106, v122, v141
	s_mov_b64 exec, s[66:67]
	buffer_load_dwordx4 v[130:133], v248, s[36:39], 0 offen offset:2048
	buffer_load_dwordx4 v[70:73], v248, s[36:39], 0 offen offset:2560
	s_mov_b64 exec, -1
	v_pk_add_f16 v107, v123, v140
	v_pk_add_f16 v108, v124, v139
	v_pk_fma_f16 v85, v129, v141, v85
	v_pk_fma_f16 v84, v128, v140, v84
	v_pk_fma_f16 v83, v127, v139, v83
	v_pk_fma_f16 v82, v126, v138, v82
	v_pk_add_f16 v122, v224, v217 neg_lo:[0,1] neg_hi:[0,1]
	v_pk_add_f16 v123, v223, v218 neg_lo:[0,1] neg_hi:[0,1]
	v_pk_add_f16 v124, v222, v219 neg_lo:[0,1] neg_hi:[0,1]
	v_pk_add_f16 v125, v221, v220 neg_lo:[0,1] neg_hi:[0,1]
	v_exp_f16_sdwa v126, v122 dst_sel:WORD_0 dst_unused:UNUSED_PAD src0_sel:WORD_0
	v_exp_f16_sdwa v127, v123 dst_sel:WORD_0 dst_unused:UNUSED_PAD src0_sel:WORD_0
	v_exp_f16_sdwa v128, v124 dst_sel:WORD_0 dst_unused:UNUSED_PAD src0_sel:WORD_0
	v_exp_f16_sdwa v129, v125 dst_sel:WORD_0 dst_unused:UNUSED_PAD src0_sel:WORD_0
	v_exp_f16_sdwa v126, v122 dst_sel:WORD_1 dst_unused:UNUSED_PRESERVE src0_sel:WORD_1
	v_exp_f16_sdwa v127, v123 dst_sel:WORD_1 dst_unused:UNUSED_PRESERVE src0_sel:WORD_1
	v_exp_f16_sdwa v128, v124 dst_sel:WORD_1 dst_unused:UNUSED_PRESERVE src0_sel:WORD_1
	v_exp_f16_sdwa v129, v125 dst_sel:WORD_1 dst_unused:UNUSED_PRESERVE src0_sel:WORD_1
	v_pk_add_f16 v122, v228, v217 neg_lo:[0,1] neg_hi:[0,1]
	v_pk_add_f16 v109, v109, v126
	v_pk_add_f16 v108, v108, v127
	v_pk_add_f16 v107, v107, v128
	s_mov_b64 exec, s[76:77]
	buffer_load_dwordx4 v[142:145], v249, s[36:39], 0 offen
	buffer_load_dwordx4 v[90:93], v249, s[36:39], 0 offen offset:512
	s_mov_b64 exec, -1
	v_pk_add_f16 v106, v106, v129
	v_pk_fma_f16 v82, v54, v126, v82
	v_pk_fma_f16 v83, v55, v127, v83
	v_pk_fma_f16 v84, v56, v128, v84
	v_pk_fma_f16 v85, v57, v129, v85
	v_pk_add_f16 v123, v227, v218 neg_lo:[0,1] neg_hi:[0,1]
	v_pk_add_f16 v124, v226, v219 neg_lo:[0,1] neg_hi:[0,1]
	v_pk_add_f16 v125, v225, v220 neg_lo:[0,1] neg_hi:[0,1]
	v_exp_f16_sdwa v126, v122 dst_sel:WORD_0 dst_unused:UNUSED_PAD src0_sel:WORD_0
	v_exp_f16_sdwa v127, v123 dst_sel:WORD_0 dst_unused:UNUSED_PAD src0_sel:WORD_0
	v_exp_f16_sdwa v128, v124 dst_sel:WORD_0 dst_unused:UNUSED_PAD src0_sel:WORD_0
	v_exp_f16_sdwa v129, v125 dst_sel:WORD_0 dst_unused:UNUSED_PAD src0_sel:WORD_0
	v_exp_f16_sdwa v126, v122 dst_sel:WORD_1 dst_unused:UNUSED_PRESERVE src0_sel:WORD_1
	v_exp_f16_sdwa v127, v123 dst_sel:WORD_1 dst_unused:UNUSED_PRESERVE src0_sel:WORD_1
	v_exp_f16_sdwa v128, v124 dst_sel:WORD_1 dst_unused:UNUSED_PRESERVE src0_sel:WORD_1
	v_exp_f16_sdwa v129, v125 dst_sel:WORD_1 dst_unused:UNUSED_PRESERVE src0_sel:WORD_1
	v_pk_add_f16 v122, v232, v217 neg_lo:[0,1] neg_hi:[0,1]
	v_pk_add_f16 v109, v109, v126
	v_pk_add_f16 v106, v106, v129
	v_pk_add_f16 v107, v107, v128
	v_pk_add_f16 v108, v108, v127
	v_pk_fma_f16 v85, v77, v129, v85
	v_pk_fma_f16 v84, v76, v128, v84
	s_mov_b64 exec, s[70:71]
	buffer_load_dwordx4 v[150:153], v250, s[36:39], 0 offen offset:512
	buffer_load_dwordx4 v[110:113], v250, s[36:39], 0 offen offset:1024
	s_mov_b64 exec, -1
	v_pk_fma_f16 v83, v75, v127, v83
	v_pk_fma_f16 v82, v74, v126, v82
	v_pk_add_f16 v123, v231, v218 neg_lo:[0,1] neg_hi:[0,1]
	v_pk_add_f16 v124, v230, v219 neg_lo:[0,1] neg_hi:[0,1]
	v_pk_add_f16 v125, v229, v220 neg_lo:[0,1] neg_hi:[0,1]
	v_exp_f16_sdwa v126, v122 dst_sel:WORD_0 dst_unused:UNUSED_PAD src0_sel:WORD_0
	v_exp_f16_sdwa v127, v123 dst_sel:WORD_0 dst_unused:UNUSED_PAD src0_sel:WORD_0
	v_exp_f16_sdwa v128, v124 dst_sel:WORD_0 dst_unused:UNUSED_PAD src0_sel:WORD_0
	v_exp_f16_sdwa v129, v125 dst_sel:WORD_0 dst_unused:UNUSED_PAD src0_sel:WORD_0
	v_exp_f16_sdwa v126, v122 dst_sel:WORD_1 dst_unused:UNUSED_PRESERVE src0_sel:WORD_1
	v_exp_f16_sdwa v127, v123 dst_sel:WORD_1 dst_unused:UNUSED_PRESERVE src0_sel:WORD_1
	v_exp_f16_sdwa v128, v124 dst_sel:WORD_1 dst_unused:UNUSED_PRESERVE src0_sel:WORD_1
	v_exp_f16_sdwa v129, v125 dst_sel:WORD_1 dst_unused:UNUSED_PRESERVE src0_sel:WORD_1
	v_pk_add_f16 v122, v205, v217 neg_lo:[0,1] neg_hi:[0,1]
	v_pk_add_f16 v109, v109, v126
	v_pk_add_f16 v108, v108, v127
	v_pk_add_f16 v107, v107, v128
	v_pk_add_f16 v106, v106, v129
	v_pk_fma_f16 v82, v98, v126, v82
	v_pk_fma_f16 v83, v99, v127, v83
	v_pk_fma_f16 v84, v100, v128, v84
	v_pk_fma_f16 v85, v101, v129, v85
	s_mov_b64 exec, s[78:79]
	buffer_load_dwordx4 v[14:17], v250, s[36:39], 0 offen offset:2048
	buffer_load_dwordx4 v[10:13], v250, s[36:39], 0 offen offset:2560
	s_mov_b64 exec, -1
	v_pk_add_f16 v123, v210, v218 neg_lo:[0,1] neg_hi:[0,1]
	v_pk_add_f16 v124, v211, v219 neg_lo:[0,1] neg_hi:[0,1]
	v_pk_add_f16 v125, v212, v220 neg_lo:[0,1] neg_hi:[0,1]
	v_exp_f16_sdwa v126, v122 dst_sel:WORD_0 dst_unused:UNUSED_PAD src0_sel:WORD_0
	v_exp_f16_sdwa v127, v123 dst_sel:WORD_0 dst_unused:UNUSED_PAD src0_sel:WORD_0
	v_exp_f16_sdwa v128, v124 dst_sel:WORD_0 dst_unused:UNUSED_PAD src0_sel:WORD_0
	v_exp_f16_sdwa v129, v125 dst_sel:WORD_0 dst_unused:UNUSED_PAD src0_sel:WORD_0
	v_exp_f16_sdwa v126, v122 dst_sel:WORD_1 dst_unused:UNUSED_PRESERVE src0_sel:WORD_1
	v_exp_f16_sdwa v127, v123 dst_sel:WORD_1 dst_unused:UNUSED_PRESERVE src0_sel:WORD_1
	v_exp_f16_sdwa v128, v124 dst_sel:WORD_1 dst_unused:UNUSED_PRESERVE src0_sel:WORD_1
	v_exp_f16_sdwa v129, v125 dst_sel:WORD_1 dst_unused:UNUSED_PRESERVE src0_sel:WORD_1
	v_pk_add_f16 v122, v213, v217 neg_lo:[0,1] neg_hi:[0,1]
	v_pk_add_f16 v109, v109, v126
	v_pk_add_f16 v106, v106, v129
	v_pk_add_f16 v107, v107, v128
	v_pk_add_f16 v108, v108, v127
	v_pk_fma_f16 v85, v33, v129, v85
	v_pk_fma_f16 v84, v32, v128, v84
	v_pk_fma_f16 v83, v31, v127, v83
	v_pk_fma_f16 v82, v30, v126, v82
	v_pk_add_f16 v123, v214, v218 neg_lo:[0,1] neg_hi:[0,1]
	v_pk_add_f16 v124, v215, v219 neg_lo:[0,1] neg_hi:[0,1]
	v_pk_add_f16 v125, v216, v220 neg_lo:[0,1] neg_hi:[0,1]
	v_exp_f16_sdwa v126, v122 dst_sel:WORD_0 dst_unused:UNUSED_PAD src0_sel:WORD_0
	v_exp_f16_sdwa v127, v123 dst_sel:WORD_0 dst_unused:UNUSED_PAD src0_sel:WORD_0
	v_exp_f16_sdwa v128, v124 dst_sel:WORD_0 dst_unused:UNUSED_PAD src0_sel:WORD_0
	v_exp_f16_sdwa v129, v125 dst_sel:WORD_0 dst_unused:UNUSED_PAD src0_sel:WORD_0
	v_exp_f16_sdwa v126, v122 dst_sel:WORD_1 dst_unused:UNUSED_PRESERVE src0_sel:WORD_1
	v_exp_f16_sdwa v127, v123 dst_sel:WORD_1 dst_unused:UNUSED_PRESERVE src0_sel:WORD_1
	v_exp_f16_sdwa v128, v124 dst_sel:WORD_1 dst_unused:UNUSED_PRESERVE src0_sel:WORD_1
	v_exp_f16_sdwa v129, v125 dst_sel:WORD_1 dst_unused:UNUSED_PRESERVE src0_sel:WORD_1
	v_pk_add_f16 v122, v206, v217 neg_lo:[0,1] neg_hi:[0,1]
	v_pk_add_f16 v109, v109, v126
	v_pk_add_f16 v108, v108, v127
	v_pk_add_f16 v107, v107, v128
	v_pk_add_f16 v106, v106, v129
	v_pk_fma_f16 v82, v42, v126, v82
	v_pk_fma_f16 v83, v43, v127, v83
	v_pk_fma_f16 v84, v44, v128, v84
	v_pk_fma_f16 v85, v45, v129, v85
	v_pk_add_f16 v123, v207, v218 neg_lo:[0,1] neg_hi:[0,1]
	v_pk_add_f16 v124, v208, v219 neg_lo:[0,1] neg_hi:[0,1]
	v_pk_add_f16 v125, v209, v220 neg_lo:[0,1] neg_hi:[0,1]
	v_exp_f16_sdwa v126, v122 dst_sel:WORD_0 dst_unused:UNUSED_PAD src0_sel:WORD_0
	v_exp_f16_sdwa v127, v123 dst_sel:WORD_0 dst_unused:UNUSED_PAD src0_sel:WORD_0
	v_exp_f16_sdwa v128, v124 dst_sel:WORD_0 dst_unused:UNUSED_PAD src0_sel:WORD_0
	v_exp_f16_sdwa v129, v125 dst_sel:WORD_0 dst_unused:UNUSED_PAD src0_sel:WORD_0
	v_exp_f16_sdwa v126, v122 dst_sel:WORD_1 dst_unused:UNUSED_PRESERVE src0_sel:WORD_1
	v_exp_f16_sdwa v127, v123 dst_sel:WORD_1 dst_unused:UNUSED_PRESERVE src0_sel:WORD_1
	v_exp_f16_sdwa v128, v124 dst_sel:WORD_1 dst_unused:UNUSED_PRESERVE src0_sel:WORD_1
	v_exp_f16_sdwa v129, v125 dst_sel:WORD_1 dst_unused:UNUSED_PRESERVE src0_sel:WORD_1
	v_pk_add_f16 v109, v109, v126
	v_pk_add_f16 v108, v108, v127
	v_rcp_f16_e32 v122, v109
	v_rcp_f16_sdwa v109, v109 dst_sel:DWORD dst_unused:UNUSED_PAD src0_sel:WORD_1
	v_pk_add_f16 v107, v107, v128
	v_rcp_f16_e32 v123, v108
	v_rcp_f16_sdwa v108, v108 dst_sel:DWORD dst_unused:UNUSED_PAD src0_sel:WORD_1
	v_pk_add_f16 v106, v106, v129
	v_rcp_f16_e32 v124, v107
	v_rcp_f16_sdwa v107, v107 dst_sel:DWORD dst_unused:UNUSED_PAD src0_sel:WORD_1
	v_rcp_f16_e32 v125, v106
	v_rcp_f16_sdwa v106, v106 dst_sel:DWORD dst_unused:UNUSED_PAD src0_sel:WORD_1
	v_pk_fma_f16 v82, v58, v126, v82
	v_pack_b32_f16 v109, v122, v109
	v_pk_fma_f16 v83, v59, v127, v83
	v_pk_mul_f16 v138, v82, v109
	v_pack_b32_f16 v82, v123, v108
	v_pk_fma_f16 v84, v60, v128, v84
	v_pk_mul_f16 v139, v83, v82
	v_pack_b32_f16 v82, v124, v107
	v_pk_fma_f16 v85, v61, v129, v85
	v_pk_mul_f16 v140, v84, v82
	v_pack_b32_f16 v82, v125, v106
	v_pk_mul_f16 v141, v85, v82
	s_waitcnt vmcnt(12)
	v_pk_mul_f16 v85, v204, v165 op_sel_hi:[0,1]
	v_pk_mul_f16 v109, v202, v165 op_sel_hi:[0,1]
	v_pk_mul_f16 v122, v203, v162 op_sel_hi:[0,1]
	v_pk_mul_f16 v125, v203, v165 op_sel_hi:[0,1]
	v_pk_mul_f16 v82, v204, v162 op_sel_hi:[0,1]
	v_pk_mul_f16 v83, v204, v163 op_sel_hi:[0,1]
	v_pk_mul_f16 v84, v204, v164 op_sel_hi:[0,1]
	v_pk_mul_f16 v106, v202, v162 op_sel_hi:[0,1]
	v_pk_mul_f16 v107, v202, v163 op_sel_hi:[0,1]
	v_pk_mul_f16 v108, v202, v164 op_sel_hi:[0,1]
	v_pk_mul_f16 v123, v203, v163 op_sel_hi:[0,1]
	v_pk_mul_f16 v124, v203, v164 op_sel_hi:[0,1]
	v_pk_fma_f16 v97, v97, v165, v85
	v_pk_fma_f16 v121, v121, v165, v109
	v_pk_fma_f16 v126, v137, v165, v125
	v_pk_fma_f16 v129, v134, v162, v122
	v_pk_fma_f16 v134, v65, v165, v85
	v_pk_fma_f16 v146, v81, v165, v109
	v_pk_fma_f16 v205, v105, v165, v125
	v_pk_fma_f16 v85, v37, v165, v85
	v_pk_fma_f16 v109, v49, v165, v109
	v_pk_fma_f16 v125, v69, v165, v125
	v_pk_maximum3_f16 v165, v97, v121, v126
	v_pk_fma_f16 v96, v96, v164, v84
	v_pk_fma_f16 v95, v95, v163, v83
	v_pk_fma_f16 v94, v94, v162, v82
	v_pk_fma_f16 v120, v120, v164, v108
	v_pk_fma_f16 v119, v119, v163, v107
	v_pk_fma_f16 v118, v118, v162, v106
	v_pk_fma_f16 v127, v136, v164, v124
	v_pk_fma_f16 v128, v135, v163, v123
	v_pk_fma_f16 v135, v64, v164, v84
	v_pk_fma_f16 v136, v63, v163, v83
	v_pk_fma_f16 v137, v62, v162, v82
	v_pk_fma_f16 v147, v80, v164, v108
	v_pk_fma_f16 v148, v79, v163, v107
	v_pk_fma_f16 v149, v78, v162, v106
	v_pk_fma_f16 v206, v104, v164, v124
	v_pk_fma_f16 v207, v103, v163, v123
	v_pk_fma_f16 v208, v102, v162, v122
	v_pk_fma_f16 v84, v36, v164, v84
	v_pk_fma_f16 v83, v35, v163, v83
	v_pk_fma_f16 v82, v34, v162, v82
	v_pk_fma_f16 v108, v48, v164, v108
	v_pk_fma_f16 v107, v47, v163, v107
	v_pk_fma_f16 v106, v46, v162, v106
	v_pk_fma_f16 v124, v68, v164, v124
	v_pk_fma_f16 v123, v67, v163, v123
	v_pk_fma_f16 v122, v66, v162, v122
	v_pk_maximum3_f16 v162, v94, v118, v129
	v_pk_maximum3_f16 v163, v95, v119, v128
	v_pk_maximum3_f16 v164, v96, v120, v127
	v_pk_maximum3_f16 v212, v134, v146, v205
	v_pk_maximum3_f16 v216, v85, v109, v125
	v_pk_maximum3_f16 v209, v137, v149, v208
	v_pk_maximum3_f16 v210, v136, v148, v207
	v_pk_maximum3_f16 v211, v135, v147, v206
	v_pk_maximum3_f16 v213, v82, v106, v122
	v_pk_maximum3_f16 v214, v83, v107, v123
	v_pk_maximum3_f16 v165, v165, v212, v216
	v_pk_maximum3_f16 v215, v84, v108, v124
	v_pk_maximum3_f16 v162, v162, v209, v213
	v_pk_maximum3_f16 v163, v163, v210, v214
	v_pk_maximum3_f16 v164, v164, v211, v215
	v_pk_add_f16 v97, v97, v165 neg_lo:[0,1] neg_hi:[0,1]
	v_pk_add_f16 v94, v94, v162 neg_lo:[0,1] neg_hi:[0,1]
	v_pk_add_f16 v95, v95, v163 neg_lo:[0,1] neg_hi:[0,1]
	v_pk_add_f16 v96, v96, v164 neg_lo:[0,1] neg_hi:[0,1]
	v_pk_add_f16 v118, v118, v162 neg_lo:[0,1] neg_hi:[0,1]
	v_exp_f16_sdwa v209, v94 dst_sel:WORD_0 dst_unused:UNUSED_PAD src0_sel:WORD_0
	v_exp_f16_sdwa v210, v95 dst_sel:WORD_0 dst_unused:UNUSED_PAD src0_sel:WORD_0
	v_exp_f16_sdwa v211, v96 dst_sel:WORD_0 dst_unused:UNUSED_PAD src0_sel:WORD_0
	v_exp_f16_sdwa v212, v97 dst_sel:WORD_0 dst_unused:UNUSED_PAD src0_sel:WORD_0
	v_exp_f16_sdwa v209, v94 dst_sel:WORD_1 dst_unused:UNUSED_PRESERVE src0_sel:WORD_1
	v_exp_f16_sdwa v210, v95 dst_sel:WORD_1 dst_unused:UNUSED_PRESERVE src0_sel:WORD_1
	v_exp_f16_sdwa v211, v96 dst_sel:WORD_1 dst_unused:UNUSED_PRESERVE src0_sel:WORD_1
	v_exp_f16_sdwa v212, v97 dst_sel:WORD_1 dst_unused:UNUSED_PRESERVE src0_sel:WORD_1
	v_pk_add_f16 v119, v119, v163 neg_lo:[0,1] neg_hi:[0,1]
	v_pk_add_f16 v97, v209, 0
	v_pk_fma_f16 v57, v57, v212, 0
	v_pk_add_f16 v94, v212, 0
	v_pk_add_f16 v95, v211, 0
	v_pk_add_f16 v96, v210, 0
	v_pk_fma_f16 v56, v56, v211, 0
	v_pk_fma_f16 v55, v55, v210, 0
	v_pk_fma_f16 v54, v54, v209, 0
	v_pk_add_f16 v120, v120, v164 neg_lo:[0,1] neg_hi:[0,1]
	v_pk_add_f16 v121, v121, v165 neg_lo:[0,1] neg_hi:[0,1]
	v_pk_add_f16 v82, v82, v162 neg_lo:[0,1] neg_hi:[0,1]
	v_exp_f16_sdwa v209, v118 dst_sel:WORD_0 dst_unused:UNUSED_PAD src0_sel:WORD_0
	v_exp_f16_sdwa v210, v119 dst_sel:WORD_0 dst_unused:UNUSED_PAD src0_sel:WORD_0
	v_exp_f16_sdwa v211, v120 dst_sel:WORD_0 dst_unused:UNUSED_PAD src0_sel:WORD_0
	v_exp_f16_sdwa v212, v121 dst_sel:WORD_0 dst_unused:UNUSED_PAD src0_sel:WORD_0
	v_exp_f16_sdwa v209, v118 dst_sel:WORD_1 dst_unused:UNUSED_PRESERVE src0_sel:WORD_1
	v_exp_f16_sdwa v210, v119 dst_sel:WORD_1 dst_unused:UNUSED_PRESERVE src0_sel:WORD_1
	v_exp_f16_sdwa v211, v120 dst_sel:WORD_1 dst_unused:UNUSED_PRESERVE src0_sel:WORD_1
	v_exp_f16_sdwa v212, v121 dst_sel:WORD_1 dst_unused:UNUSED_PRESERVE src0_sel:WORD_1
	v_pk_add_f16 v83, v83, v163 neg_lo:[0,1] neg_hi:[0,1]
	v_pk_add_f16 v97, v97, v209
	v_pk_fma_f16 v57, v77, v212, v57
	v_pk_add_f16 v77, v126, v165 neg_lo:[0,1] neg_hi:[0,1]
	v_pk_add_f16 v96, v96, v210
	v_pk_add_f16 v95, v95, v211
	v_pk_add_f16 v94, v94, v212
	v_pk_fma_f16 v54, v74, v209, v54
	v_pk_fma_f16 v55, v75, v210, v55
	v_pk_fma_f16 v56, v76, v211, v56
	v_pk_add_f16 v74, v129, v162 neg_lo:[0,1] neg_hi:[0,1]
	v_pk_add_f16 v75, v128, v163 neg_lo:[0,1] neg_hi:[0,1]
	v_pk_add_f16 v76, v127, v164 neg_lo:[0,1] neg_hi:[0,1]
	v_pk_add_f16 v84, v84, v164 neg_lo:[0,1] neg_hi:[0,1]
	v_exp_f16_sdwa v118, v74 dst_sel:WORD_0 dst_unused:UNUSED_PAD src0_sel:WORD_0
	v_exp_f16_sdwa v119, v75 dst_sel:WORD_0 dst_unused:UNUSED_PAD src0_sel:WORD_0
	v_exp_f16_sdwa v120, v76 dst_sel:WORD_0 dst_unused:UNUSED_PAD src0_sel:WORD_0
	v_exp_f16_sdwa v121, v77 dst_sel:WORD_0 dst_unused:UNUSED_PAD src0_sel:WORD_0
	v_exp_f16_sdwa v118, v74 dst_sel:WORD_1 dst_unused:UNUSED_PRESERVE src0_sel:WORD_1
	v_exp_f16_sdwa v119, v75 dst_sel:WORD_1 dst_unused:UNUSED_PRESERVE src0_sel:WORD_1
	v_exp_f16_sdwa v120, v76 dst_sel:WORD_1 dst_unused:UNUSED_PRESERVE src0_sel:WORD_1
	v_exp_f16_sdwa v121, v77 dst_sel:WORD_1 dst_unused:UNUSED_PRESERVE src0_sel:WORD_1
	v_pk_add_f16 v85, v85, v165 neg_lo:[0,1] neg_hi:[0,1]
	v_pk_add_f16 v77, v97, v118
	v_pk_add_f16 v74, v94, v121
	v_pk_add_f16 v75, v95, v120
	v_pk_add_f16 v76, v96, v119
	v_pk_fma_f16 v57, v101, v121, v57
	v_pk_fma_f16 v56, v100, v120, v56
	v_pk_fma_f16 v55, v99, v119, v55
	v_pk_fma_f16 v54, v98, v118, v54
	v_pk_add_f16 v94, v137, v162 neg_lo:[0,1] neg_hi:[0,1]
	v_pk_add_f16 v95, v136, v163 neg_lo:[0,1] neg_hi:[0,1]
	v_pk_add_f16 v96, v135, v164 neg_lo:[0,1] neg_hi:[0,1]
	v_pk_add_f16 v97, v134, v165 neg_lo:[0,1] neg_hi:[0,1]
	v_exp_f16_sdwa v98, v94 dst_sel:WORD_0 dst_unused:UNUSED_PAD src0_sel:WORD_0
	v_exp_f16_sdwa v99, v95 dst_sel:WORD_0 dst_unused:UNUSED_PAD src0_sel:WORD_0
	v_exp_f16_sdwa v100, v96 dst_sel:WORD_0 dst_unused:UNUSED_PAD src0_sel:WORD_0
	v_exp_f16_sdwa v101, v97 dst_sel:WORD_0 dst_unused:UNUSED_PAD src0_sel:WORD_0
	v_exp_f16_sdwa v98, v94 dst_sel:WORD_1 dst_unused:UNUSED_PRESERVE src0_sel:WORD_1
	v_exp_f16_sdwa v99, v95 dst_sel:WORD_1 dst_unused:UNUSED_PRESERVE src0_sel:WORD_1
	v_exp_f16_sdwa v100, v96 dst_sel:WORD_1 dst_unused:UNUSED_PRESERVE src0_sel:WORD_1
	v_exp_f16_sdwa v101, v97 dst_sel:WORD_1 dst_unused:UNUSED_PRESERVE src0_sel:WORD_1
	v_pk_add_f16 v94, v149, v162 neg_lo:[0,1] neg_hi:[0,1]
	v_pk_add_f16 v77, v77, v98
	v_pk_add_f16 v76, v76, v99
	v_pk_add_f16 v75, v75, v100
	v_pk_add_f16 v74, v74, v101
	v_pk_fma_f16 v54, v30, v98, v54
	v_pk_fma_f16 v55, v31, v99, v55
	v_pk_fma_f16 v56, v32, v100, v56
	v_pk_fma_f16 v57, v33, v101, v57
	v_pk_add_f16 v95, v148, v163 neg_lo:[0,1] neg_hi:[0,1]
	v_pk_add_f16 v96, v147, v164 neg_lo:[0,1] neg_hi:[0,1]
	v_pk_add_f16 v97, v146, v165 neg_lo:[0,1] neg_hi:[0,1]
	v_exp_f16_sdwa v98, v94 dst_sel:WORD_0 dst_unused:UNUSED_PAD src0_sel:WORD_0
	v_exp_f16_sdwa v99, v95 dst_sel:WORD_0 dst_unused:UNUSED_PAD src0_sel:WORD_0
	v_exp_f16_sdwa v100, v96 dst_sel:WORD_0 dst_unused:UNUSED_PAD src0_sel:WORD_0
	v_exp_f16_sdwa v101, v97 dst_sel:WORD_0 dst_unused:UNUSED_PAD src0_sel:WORD_0
	v_exp_f16_sdwa v98, v94 dst_sel:WORD_1 dst_unused:UNUSED_PRESERVE src0_sel:WORD_1
	v_exp_f16_sdwa v99, v95 dst_sel:WORD_1 dst_unused:UNUSED_PRESERVE src0_sel:WORD_1
	v_exp_f16_sdwa v100, v96 dst_sel:WORD_1 dst_unused:UNUSED_PRESERVE src0_sel:WORD_1
	v_exp_f16_sdwa v101, v97 dst_sel:WORD_1 dst_unused:UNUSED_PRESERVE src0_sel:WORD_1
	v_pk_add_f16 v94, v208, v162 neg_lo:[0,1] neg_hi:[0,1]
	v_pk_add_f16 v77, v77, v98
	v_pk_add_f16 v74, v74, v101
	v_pk_add_f16 v75, v75, v100
	v_pk_add_f16 v76, v76, v99
	v_pk_fma_f16 v57, v45, v101, v57
	v_pk_fma_f16 v56, v44, v100, v56
	v_pk_fma_f16 v55, v43, v99, v55
	v_pk_fma_f16 v54, v42, v98, v54
	v_pk_add_f16 v95, v207, v163 neg_lo:[0,1] neg_hi:[0,1]
	v_pk_add_f16 v96, v206, v164 neg_lo:[0,1] neg_hi:[0,1]
	v_pk_add_f16 v97, v205, v165 neg_lo:[0,1] neg_hi:[0,1]
	v_exp_f16_sdwa v98, v94 dst_sel:WORD_0 dst_unused:UNUSED_PAD src0_sel:WORD_0
	v_exp_f16_sdwa v99, v95 dst_sel:WORD_0 dst_unused:UNUSED_PAD src0_sel:WORD_0
	v_exp_f16_sdwa v100, v96 dst_sel:WORD_0 dst_unused:UNUSED_PAD src0_sel:WORD_0
	v_exp_f16_sdwa v101, v97 dst_sel:WORD_0 dst_unused:UNUSED_PAD src0_sel:WORD_0
	v_exp_f16_sdwa v98, v94 dst_sel:WORD_1 dst_unused:UNUSED_PRESERVE src0_sel:WORD_1
	v_exp_f16_sdwa v99, v95 dst_sel:WORD_1 dst_unused:UNUSED_PRESERVE src0_sel:WORD_1
	v_exp_f16_sdwa v100, v96 dst_sel:WORD_1 dst_unused:UNUSED_PRESERVE src0_sel:WORD_1
	v_exp_f16_sdwa v101, v97 dst_sel:WORD_1 dst_unused:UNUSED_PRESERVE src0_sel:WORD_1
	v_exp_f16_sdwa v94, v82 dst_sel:WORD_0 dst_unused:UNUSED_PAD src0_sel:WORD_0
	v_exp_f16_sdwa v95, v83 dst_sel:WORD_0 dst_unused:UNUSED_PAD src0_sel:WORD_0
	v_exp_f16_sdwa v96, v84 dst_sel:WORD_0 dst_unused:UNUSED_PAD src0_sel:WORD_0
	v_exp_f16_sdwa v97, v85 dst_sel:WORD_0 dst_unused:UNUSED_PAD src0_sel:WORD_0
	v_exp_f16_sdwa v94, v82 dst_sel:WORD_1 dst_unused:UNUSED_PRESERVE src0_sel:WORD_1
	v_exp_f16_sdwa v95, v83 dst_sel:WORD_1 dst_unused:UNUSED_PRESERVE src0_sel:WORD_1
	v_exp_f16_sdwa v96, v84 dst_sel:WORD_1 dst_unused:UNUSED_PRESERVE src0_sel:WORD_1
	v_exp_f16_sdwa v97, v85 dst_sel:WORD_1 dst_unused:UNUSED_PRESERVE src0_sel:WORD_1
	v_pk_add_f16 v82, v106, v162 neg_lo:[0,1] neg_hi:[0,1]
	v_pk_add_f16 v77, v77, v98
	v_pk_add_f16 v76, v76, v99
	v_pk_add_f16 v75, v75, v100
	v_pk_add_f16 v74, v74, v101
	v_pk_fma_f16 v54, v58, v98, v54
	v_pk_fma_f16 v55, v59, v99, v55
	v_pk_fma_f16 v56, v60, v100, v56
	v_pk_fma_f16 v57, v61, v101, v57
	v_pk_add_f16 v77, v77, v94
	v_pk_add_f16 v74, v74, v97
	v_pk_add_f16 v75, v75, v96
	v_pk_add_f16 v76, v76, v95
	v_pk_fma_f16 v57, v21, v97, v57
	v_pk_fma_f16 v56, v20, v96, v56
	v_pk_fma_f16 v55, v19, v95, v55
	v_pk_fma_f16 v54, v18, v94, v54
	v_pk_add_f16 v83, v107, v163 neg_lo:[0,1] neg_hi:[0,1]
	v_pk_add_f16 v84, v108, v164 neg_lo:[0,1] neg_hi:[0,1]
	v_pk_add_f16 v85, v109, v165 neg_lo:[0,1] neg_hi:[0,1]
	v_exp_f16_sdwa v94, v82 dst_sel:WORD_0 dst_unused:UNUSED_PAD src0_sel:WORD_0
	v_exp_f16_sdwa v95, v83 dst_sel:WORD_0 dst_unused:UNUSED_PAD src0_sel:WORD_0
	v_exp_f16_sdwa v96, v84 dst_sel:WORD_0 dst_unused:UNUSED_PAD src0_sel:WORD_0
	v_exp_f16_sdwa v97, v85 dst_sel:WORD_0 dst_unused:UNUSED_PAD src0_sel:WORD_0
	v_exp_f16_sdwa v94, v82 dst_sel:WORD_1 dst_unused:UNUSED_PRESERVE src0_sel:WORD_1
	v_exp_f16_sdwa v95, v83 dst_sel:WORD_1 dst_unused:UNUSED_PRESERVE src0_sel:WORD_1
	v_exp_f16_sdwa v96, v84 dst_sel:WORD_1 dst_unused:UNUSED_PRESERVE src0_sel:WORD_1
	v_exp_f16_sdwa v97, v85 dst_sel:WORD_1 dst_unused:UNUSED_PRESERVE src0_sel:WORD_1
	v_pk_add_f16 v82, v122, v162 neg_lo:[0,1] neg_hi:[0,1]
	v_pk_add_f16 v77, v77, v94
	v_pk_add_f16 v76, v76, v95
	v_pk_add_f16 v75, v75, v96
	v_pk_add_f16 v74, v74, v97
	v_pk_fma_f16 v54, v22, v94, v54
	v_pk_fma_f16 v55, v23, v95, v55
	v_pk_fma_f16 v56, v24, v96, v56
	v_pk_fma_f16 v57, v25, v97, v57
	v_pk_add_f16 v83, v123, v163 neg_lo:[0,1] neg_hi:[0,1]
	v_pk_add_f16 v84, v124, v164 neg_lo:[0,1] neg_hi:[0,1]
	v_pk_add_f16 v85, v125, v165 neg_lo:[0,1] neg_hi:[0,1]
	v_exp_f16_sdwa v94, v82 dst_sel:WORD_0 dst_unused:UNUSED_PAD src0_sel:WORD_0
	v_exp_f16_sdwa v95, v83 dst_sel:WORD_0 dst_unused:UNUSED_PAD src0_sel:WORD_0
	v_exp_f16_sdwa v96, v84 dst_sel:WORD_0 dst_unused:UNUSED_PAD src0_sel:WORD_0
	v_exp_f16_sdwa v97, v85 dst_sel:WORD_0 dst_unused:UNUSED_PAD src0_sel:WORD_0
	v_exp_f16_sdwa v94, v82 dst_sel:WORD_1 dst_unused:UNUSED_PRESERVE src0_sel:WORD_1
	v_exp_f16_sdwa v95, v83 dst_sel:WORD_1 dst_unused:UNUSED_PRESERVE src0_sel:WORD_1
	v_exp_f16_sdwa v96, v84 dst_sel:WORD_1 dst_unused:UNUSED_PRESERVE src0_sel:WORD_1
	v_exp_f16_sdwa v97, v85 dst_sel:WORD_1 dst_unused:UNUSED_PRESERVE src0_sel:WORD_1
	v_pk_add_f16 v77, v77, v94
	v_pk_add_f16 v76, v76, v95
	v_rcp_f16_e32 v82, v77
	v_rcp_f16_sdwa v77, v77 dst_sel:DWORD dst_unused:UNUSED_PAD src0_sel:WORD_1
	v_pk_add_f16 v75, v75, v96
	v_rcp_f16_e32 v83, v76
	v_rcp_f16_sdwa v76, v76 dst_sel:DWORD dst_unused:UNUSED_PAD src0_sel:WORD_1
	v_pk_add_f16 v74, v74, v97
	v_rcp_f16_e32 v84, v75
	v_rcp_f16_sdwa v75, v75 dst_sel:DWORD dst_unused:UNUSED_PAD src0_sel:WORD_1
	v_rcp_f16_e32 v85, v74
	v_rcp_f16_sdwa v74, v74 dst_sel:DWORD dst_unused:UNUSED_PAD src0_sel:WORD_1
	v_pk_fma_f16 v54, v26, v94, v54
	v_pack_b32_f16 v77, v82, v77
	v_pk_fma_f16 v55, v27, v95, v55
	v_pk_mul_f16 v77, v54, v77
	v_pack_b32_f16 v54, v83, v76
	v_pk_fma_f16 v56, v28, v96, v56
	v_pk_mul_f16 v76, v55, v54
	v_pack_b32_f16 v54, v84, v75
	v_pk_fma_f16 v57, v29, v97, v57
	v_pk_mul_f16 v75, v56, v54
	v_pack_b32_f16 v54, v85, v74
	v_pk_mul_f16 v74, v57, v54
	s_waitcnt vmcnt(6)
	v_pk_mul_f16 v57, v204, v161 op_sel_hi:[0,1]
	v_pk_mul_f16 v85, v202, v161 op_sel_hi:[0,1]
	v_pk_mul_f16 v97, v203, v161 op_sel_hi:[0,1]
	v_pk_mul_f16 v54, v204, v158 op_sel_hi:[0,1]
	v_pk_mul_f16 v55, v204, v159 op_sel_hi:[0,1]
	v_pk_mul_f16 v56, v204, v160 op_sel_hi:[0,1]
	v_pk_mul_f16 v82, v202, v158 op_sel_hi:[0,1]
	v_pk_mul_f16 v83, v202, v159 op_sel_hi:[0,1]
	v_pk_mul_f16 v84, v202, v160 op_sel_hi:[0,1]
	v_pk_mul_f16 v94, v203, v158 op_sel_hi:[0,1]
	v_pk_mul_f16 v95, v203, v159 op_sel_hi:[0,1]
	v_pk_mul_f16 v96, v203, v160 op_sel_hi:[0,1]
	v_pk_fma_f16 v65, v65, v161, v57
	v_pk_fma_f16 v81, v81, v161, v85
	v_pk_fma_f16 v98, v105, v161, v97
	v_pk_fma_f16 v64, v64, v160, v56
	v_pk_maximum3_f16 v125, v65, v81, v98
	v_pk_fma_f16 v63, v63, v159, v55
	v_pk_fma_f16 v62, v62, v158, v54
	v_pk_fma_f16 v80, v80, v160, v84
	v_pk_fma_f16 v79, v79, v159, v83
	v_pk_fma_f16 v78, v78, v158, v82
	v_pk_fma_f16 v99, v104, v160, v96
	v_pk_fma_f16 v100, v103, v159, v95
	v_pk_fma_f16 v101, v102, v158, v94
	v_pk_fma_f16 v102, v37, v161, v57
	v_pk_fma_f16 v106, v49, v161, v85
	v_pk_fma_f16 v118, v69, v161, v97
	v_pk_fma_f16 v57, v89, v161, v57
	v_pk_fma_f16 v85, v117, v161, v85
	v_pk_fma_f16 v97, v133, v161, v97
	v_pk_maximum3_f16 v122, v62, v78, v101
	v_pk_maximum3_f16 v123, v63, v79, v100
	v_pk_maximum3_f16 v124, v64, v80, v99
	v_pk_maximum3_f16 v129, v102, v106, v118
	v_pk_fma_f16 v103, v36, v160, v56
	v_pk_maximum3_f16 v137, v57, v85, v97
	v_pk_fma_f16 v104, v35, v159, v55
	v_pk_maximum3_f16 v125, v125, v129, v137
	v_pk_fma_f16 v105, v34, v158, v54
	v_pk_fma_f16 v107, v48, v160, v84
	v_pk_fma_f16 v108, v47, v159, v83
	v_pk_fma_f16 v109, v46, v158, v82
	v_pk_fma_f16 v119, v68, v160, v96
	v_pk_fma_f16 v120, v67, v159, v95
	v_pk_fma_f16 v121, v66, v158, v94
	v_pk_fma_f16 v56, v88, v160, v56
	v_pk_fma_f16 v55, v87, v159, v55
	v_pk_fma_f16 v54, v86, v158, v54
	v_pk_fma_f16 v84, v116, v160, v84
	v_pk_fma_f16 v83, v115, v159, v83
	v_pk_fma_f16 v82, v114, v158, v82
	v_pk_fma_f16 v96, v132, v160, v96
	v_pk_fma_f16 v95, v131, v159, v95
	v_pk_fma_f16 v94, v130, v158, v94
	v_pk_maximum3_f16 v126, v105, v109, v121
	v_pk_maximum3_f16 v127, v104, v108, v120
	v_pk_maximum3_f16 v128, v103, v107, v119
	v_pk_maximum3_f16 v135, v55, v83, v95
	v_pk_maximum3_f16 v136, v56, v84, v96
	v_pk_maximum3_f16 v134, v54, v82, v94
	v_pk_maximum3_f16 v122, v122, v126, v134
	v_pk_maximum3_f16 v123, v123, v127, v135
	v_pk_maximum3_f16 v124, v124, v128, v136
	v_pk_add_f16 v65, v65, v125 neg_lo:[0,1] neg_hi:[0,1]
	v_pk_add_f16 v62, v62, v122 neg_lo:[0,1] neg_hi:[0,1]
	v_pk_add_f16 v63, v63, v123 neg_lo:[0,1] neg_hi:[0,1]
	v_pk_add_f16 v64, v64, v124 neg_lo:[0,1] neg_hi:[0,1]
	v_pk_add_f16 v78, v78, v122 neg_lo:[0,1] neg_hi:[0,1]
	v_exp_f16_sdwa v126, v62 dst_sel:WORD_0 dst_unused:UNUSED_PAD src0_sel:WORD_0
	v_exp_f16_sdwa v127, v63 dst_sel:WORD_0 dst_unused:UNUSED_PAD src0_sel:WORD_0
	v_exp_f16_sdwa v128, v64 dst_sel:WORD_0 dst_unused:UNUSED_PAD src0_sel:WORD_0
	v_exp_f16_sdwa v129, v65 dst_sel:WORD_0 dst_unused:UNUSED_PAD src0_sel:WORD_0
	v_exp_f16_sdwa v126, v62 dst_sel:WORD_1 dst_unused:UNUSED_PRESERVE src0_sel:WORD_1
	v_exp_f16_sdwa v127, v63 dst_sel:WORD_1 dst_unused:UNUSED_PRESERVE src0_sel:WORD_1
	v_exp_f16_sdwa v128, v64 dst_sel:WORD_1 dst_unused:UNUSED_PRESERVE src0_sel:WORD_1
	v_exp_f16_sdwa v129, v65 dst_sel:WORD_1 dst_unused:UNUSED_PRESERVE src0_sel:WORD_1
	v_pk_add_f16 v79, v79, v123 neg_lo:[0,1] neg_hi:[0,1]
	v_pk_add_f16 v65, v126, 0
	v_pk_fma_f16 v33, v33, v129, 0
	v_pk_add_f16 v62, v129, 0
	v_pk_add_f16 v63, v128, 0
	v_pk_add_f16 v64, v127, 0
	v_pk_fma_f16 v32, v32, v128, 0
	v_pk_fma_f16 v31, v31, v127, 0
	v_pk_fma_f16 v30, v30, v126, 0
	v_pk_add_f16 v80, v80, v124 neg_lo:[0,1] neg_hi:[0,1]
	v_pk_add_f16 v81, v81, v125 neg_lo:[0,1] neg_hi:[0,1]
	v_pk_add_f16 v54, v54, v122 neg_lo:[0,1] neg_hi:[0,1]
	v_exp_f16_sdwa v126, v78 dst_sel:WORD_0 dst_unused:UNUSED_PAD src0_sel:WORD_0
	v_exp_f16_sdwa v127, v79 dst_sel:WORD_0 dst_unused:UNUSED_PAD src0_sel:WORD_0
	v_exp_f16_sdwa v128, v80 dst_sel:WORD_0 dst_unused:UNUSED_PAD src0_sel:WORD_0
	v_exp_f16_sdwa v129, v81 dst_sel:WORD_0 dst_unused:UNUSED_PAD src0_sel:WORD_0
	v_exp_f16_sdwa v126, v78 dst_sel:WORD_1 dst_unused:UNUSED_PRESERVE src0_sel:WORD_1
	v_exp_f16_sdwa v127, v79 dst_sel:WORD_1 dst_unused:UNUSED_PRESERVE src0_sel:WORD_1
	v_exp_f16_sdwa v128, v80 dst_sel:WORD_1 dst_unused:UNUSED_PRESERVE src0_sel:WORD_1
	v_exp_f16_sdwa v129, v81 dst_sel:WORD_1 dst_unused:UNUSED_PRESERVE src0_sel:WORD_1
	v_pk_add_f16 v55, v55, v123 neg_lo:[0,1] neg_hi:[0,1]
	v_pk_add_f16 v65, v65, v126
	v_pk_fma_f16 v33, v45, v129, v33
	v_pk_add_f16 v45, v98, v125 neg_lo:[0,1] neg_hi:[0,1]
	v_pk_add_f16 v64, v64, v127
	v_pk_add_f16 v63, v63, v128
	v_pk_add_f16 v62, v62, v129
	v_pk_fma_f16 v30, v42, v126, v30
	v_pk_fma_f16 v31, v43, v127, v31
	v_pk_fma_f16 v32, v44, v128, v32
	v_pk_add_f16 v42, v101, v122 neg_lo:[0,1] neg_hi:[0,1]
	v_pk_add_f16 v43, v100, v123 neg_lo:[0,1] neg_hi:[0,1]
	v_pk_add_f16 v44, v99, v124 neg_lo:[0,1] neg_hi:[0,1]
	v_pk_add_f16 v56, v56, v124 neg_lo:[0,1] neg_hi:[0,1]
	v_exp_f16_sdwa v78, v42 dst_sel:WORD_0 dst_unused:UNUSED_PAD src0_sel:WORD_0
	v_exp_f16_sdwa v79, v43 dst_sel:WORD_0 dst_unused:UNUSED_PAD src0_sel:WORD_0
	v_exp_f16_sdwa v80, v44 dst_sel:WORD_0 dst_unused:UNUSED_PAD src0_sel:WORD_0
	v_exp_f16_sdwa v81, v45 dst_sel:WORD_0 dst_unused:UNUSED_PAD src0_sel:WORD_0
	v_exp_f16_sdwa v78, v42 dst_sel:WORD_1 dst_unused:UNUSED_PRESERVE src0_sel:WORD_1
	v_exp_f16_sdwa v79, v43 dst_sel:WORD_1 dst_unused:UNUSED_PRESERVE src0_sel:WORD_1
	v_exp_f16_sdwa v80, v44 dst_sel:WORD_1 dst_unused:UNUSED_PRESERVE src0_sel:WORD_1
	v_exp_f16_sdwa v81, v45 dst_sel:WORD_1 dst_unused:UNUSED_PRESERVE src0_sel:WORD_1
	v_pk_add_f16 v57, v57, v125 neg_lo:[0,1] neg_hi:[0,1]
	v_pk_add_f16 v45, v65, v78
	v_pk_add_f16 v42, v62, v81
	v_pk_add_f16 v43, v63, v80
	v_pk_add_f16 v44, v64, v79
	v_pk_fma_f16 v33, v61, v81, v33
	v_pk_fma_f16 v32, v60, v80, v32
	v_pk_fma_f16 v31, v59, v79, v31
	v_pk_fma_f16 v30, v58, v78, v30
	v_pk_add_f16 v58, v105, v122 neg_lo:[0,1] neg_hi:[0,1]
	v_pk_add_f16 v59, v104, v123 neg_lo:[0,1] neg_hi:[0,1]
	v_pk_add_f16 v60, v103, v124 neg_lo:[0,1] neg_hi:[0,1]
	v_pk_add_f16 v61, v102, v125 neg_lo:[0,1] neg_hi:[0,1]
	v_exp_f16_sdwa v62, v58 dst_sel:WORD_0 dst_unused:UNUSED_PAD src0_sel:WORD_0
	v_exp_f16_sdwa v63, v59 dst_sel:WORD_0 dst_unused:UNUSED_PAD src0_sel:WORD_0
	v_exp_f16_sdwa v64, v60 dst_sel:WORD_0 dst_unused:UNUSED_PAD src0_sel:WORD_0
	v_exp_f16_sdwa v65, v61 dst_sel:WORD_0 dst_unused:UNUSED_PAD src0_sel:WORD_0
	v_exp_f16_sdwa v62, v58 dst_sel:WORD_1 dst_unused:UNUSED_PRESERVE src0_sel:WORD_1
	v_exp_f16_sdwa v63, v59 dst_sel:WORD_1 dst_unused:UNUSED_PRESERVE src0_sel:WORD_1
	v_exp_f16_sdwa v64, v60 dst_sel:WORD_1 dst_unused:UNUSED_PRESERVE src0_sel:WORD_1
	v_exp_f16_sdwa v65, v61 dst_sel:WORD_1 dst_unused:UNUSED_PRESERVE src0_sel:WORD_1
	v_pk_add_f16 v58, v109, v122 neg_lo:[0,1] neg_hi:[0,1]
	v_pk_add_f16 v45, v45, v62
	v_pk_add_f16 v44, v44, v63
	v_pk_add_f16 v43, v43, v64
	v_pk_add_f16 v42, v42, v65
	v_pk_fma_f16 v30, v18, v62, v30
	v_pk_fma_f16 v31, v19, v63, v31
	v_pk_fma_f16 v32, v20, v64, v32
	v_pk_fma_f16 v33, v21, v65, v33
	v_pk_add_f16 v59, v108, v123 neg_lo:[0,1] neg_hi:[0,1]
	v_pk_add_f16 v60, v107, v124 neg_lo:[0,1] neg_hi:[0,1]
	v_pk_add_f16 v61, v106, v125 neg_lo:[0,1] neg_hi:[0,1]
	v_exp_f16_sdwa v62, v58 dst_sel:WORD_0 dst_unused:UNUSED_PAD src0_sel:WORD_0
	v_exp_f16_sdwa v63, v59 dst_sel:WORD_0 dst_unused:UNUSED_PAD src0_sel:WORD_0
	v_exp_f16_sdwa v64, v60 dst_sel:WORD_0 dst_unused:UNUSED_PAD src0_sel:WORD_0
	v_exp_f16_sdwa v65, v61 dst_sel:WORD_0 dst_unused:UNUSED_PAD src0_sel:WORD_0
	v_exp_f16_sdwa v62, v58 dst_sel:WORD_1 dst_unused:UNUSED_PRESERVE src0_sel:WORD_1
	v_exp_f16_sdwa v63, v59 dst_sel:WORD_1 dst_unused:UNUSED_PRESERVE src0_sel:WORD_1
	v_exp_f16_sdwa v64, v60 dst_sel:WORD_1 dst_unused:UNUSED_PRESERVE src0_sel:WORD_1
	v_exp_f16_sdwa v65, v61 dst_sel:WORD_1 dst_unused:UNUSED_PRESERVE src0_sel:WORD_1
	v_pk_add_f16 v58, v121, v122 neg_lo:[0,1] neg_hi:[0,1]
	v_pk_add_f16 v45, v45, v62
	v_pk_add_f16 v42, v42, v65
	v_pk_add_f16 v43, v43, v64
	v_pk_add_f16 v44, v44, v63
	v_pk_fma_f16 v33, v25, v65, v33
	v_pk_fma_f16 v32, v24, v64, v32
	v_pk_fma_f16 v31, v23, v63, v31
	v_pk_fma_f16 v30, v22, v62, v30
	v_pk_add_f16 v59, v120, v123 neg_lo:[0,1] neg_hi:[0,1]
	v_pk_add_f16 v60, v119, v124 neg_lo:[0,1] neg_hi:[0,1]
	v_pk_add_f16 v61, v118, v125 neg_lo:[0,1] neg_hi:[0,1]
	v_exp_f16_sdwa v62, v58 dst_sel:WORD_0 dst_unused:UNUSED_PAD src0_sel:WORD_0
	v_exp_f16_sdwa v63, v59 dst_sel:WORD_0 dst_unused:UNUSED_PAD src0_sel:WORD_0
	v_exp_f16_sdwa v64, v60 dst_sel:WORD_0 dst_unused:UNUSED_PAD src0_sel:WORD_0
	v_exp_f16_sdwa v65, v61 dst_sel:WORD_0 dst_unused:UNUSED_PAD src0_sel:WORD_0
	v_exp_f16_sdwa v62, v58 dst_sel:WORD_1 dst_unused:UNUSED_PRESERVE src0_sel:WORD_1
	v_exp_f16_sdwa v63, v59 dst_sel:WORD_1 dst_unused:UNUSED_PRESERVE src0_sel:WORD_1
	v_exp_f16_sdwa v64, v60 dst_sel:WORD_1 dst_unused:UNUSED_PRESERVE src0_sel:WORD_1
	v_exp_f16_sdwa v65, v61 dst_sel:WORD_1 dst_unused:UNUSED_PRESERVE src0_sel:WORD_1
	v_exp_f16_sdwa v58, v54 dst_sel:WORD_0 dst_unused:UNUSED_PAD src0_sel:WORD_0
	v_exp_f16_sdwa v59, v55 dst_sel:WORD_0 dst_unused:UNUSED_PAD src0_sel:WORD_0
	v_exp_f16_sdwa v60, v56 dst_sel:WORD_0 dst_unused:UNUSED_PAD src0_sel:WORD_0
	v_exp_f16_sdwa v61, v57 dst_sel:WORD_0 dst_unused:UNUSED_PAD src0_sel:WORD_0
	v_exp_f16_sdwa v58, v54 dst_sel:WORD_1 dst_unused:UNUSED_PRESERVE src0_sel:WORD_1
	v_exp_f16_sdwa v59, v55 dst_sel:WORD_1 dst_unused:UNUSED_PRESERVE src0_sel:WORD_1
	v_exp_f16_sdwa v60, v56 dst_sel:WORD_1 dst_unused:UNUSED_PRESERVE src0_sel:WORD_1
	v_exp_f16_sdwa v61, v57 dst_sel:WORD_1 dst_unused:UNUSED_PRESERVE src0_sel:WORD_1
	v_pk_add_f16 v54, v82, v122 neg_lo:[0,1] neg_hi:[0,1]
	v_pk_add_f16 v45, v45, v62
	v_pk_add_f16 v44, v44, v63
	v_pk_add_f16 v43, v43, v64
	v_pk_add_f16 v42, v42, v65
	v_pk_fma_f16 v30, v26, v62, v30
	v_pk_fma_f16 v31, v27, v63, v31
	v_pk_fma_f16 v32, v28, v64, v32
	v_pk_fma_f16 v33, v29, v65, v33
	v_pk_add_f16 v45, v45, v58
	v_pk_add_f16 v42, v42, v61
	v_pk_add_f16 v43, v43, v60
	v_pk_add_f16 v44, v44, v59
	v_pk_fma_f16 v33, v41, v61, v33
	v_pk_fma_f16 v32, v40, v60, v32
	v_pk_fma_f16 v31, v39, v59, v31
	v_pk_fma_f16 v30, v38, v58, v30
	v_pk_add_f16 v55, v83, v123 neg_lo:[0,1] neg_hi:[0,1]
	v_pk_add_f16 v56, v84, v124 neg_lo:[0,1] neg_hi:[0,1]
	v_pk_add_f16 v57, v85, v125 neg_lo:[0,1] neg_hi:[0,1]
	v_exp_f16_sdwa v58, v54 dst_sel:WORD_0 dst_unused:UNUSED_PAD src0_sel:WORD_0
	v_exp_f16_sdwa v59, v55 dst_sel:WORD_0 dst_unused:UNUSED_PAD src0_sel:WORD_0
	v_exp_f16_sdwa v60, v56 dst_sel:WORD_0 dst_unused:UNUSED_PAD src0_sel:WORD_0
	v_exp_f16_sdwa v61, v57 dst_sel:WORD_0 dst_unused:UNUSED_PAD src0_sel:WORD_0
	v_exp_f16_sdwa v58, v54 dst_sel:WORD_1 dst_unused:UNUSED_PRESERVE src0_sel:WORD_1
	v_exp_f16_sdwa v59, v55 dst_sel:WORD_1 dst_unused:UNUSED_PRESERVE src0_sel:WORD_1
	v_exp_f16_sdwa v60, v56 dst_sel:WORD_1 dst_unused:UNUSED_PRESERVE src0_sel:WORD_1
	v_exp_f16_sdwa v61, v57 dst_sel:WORD_1 dst_unused:UNUSED_PRESERVE src0_sel:WORD_1
	v_pk_add_f16 v54, v94, v122 neg_lo:[0,1] neg_hi:[0,1]
	v_pk_add_f16 v45, v45, v58
	v_pk_add_f16 v44, v44, v59
	v_pk_add_f16 v43, v43, v60
	v_pk_add_f16 v42, v42, v61
	v_pk_fma_f16 v30, v50, v58, v30
	v_pk_fma_f16 v31, v51, v59, v31
	v_pk_fma_f16 v32, v52, v60, v32
	v_pk_fma_f16 v33, v53, v61, v33
	v_pk_add_f16 v55, v95, v123 neg_lo:[0,1] neg_hi:[0,1]
	v_pk_add_f16 v56, v96, v124 neg_lo:[0,1] neg_hi:[0,1]
	v_pk_add_f16 v57, v97, v125 neg_lo:[0,1] neg_hi:[0,1]
	v_exp_f16_sdwa v58, v54 dst_sel:WORD_0 dst_unused:UNUSED_PAD src0_sel:WORD_0
	v_exp_f16_sdwa v59, v55 dst_sel:WORD_0 dst_unused:UNUSED_PAD src0_sel:WORD_0
	v_exp_f16_sdwa v60, v56 dst_sel:WORD_0 dst_unused:UNUSED_PAD src0_sel:WORD_0
	v_exp_f16_sdwa v61, v57 dst_sel:WORD_0 dst_unused:UNUSED_PAD src0_sel:WORD_0
	v_exp_f16_sdwa v58, v54 dst_sel:WORD_1 dst_unused:UNUSED_PRESERVE src0_sel:WORD_1
	v_exp_f16_sdwa v59, v55 dst_sel:WORD_1 dst_unused:UNUSED_PRESERVE src0_sel:WORD_1
	v_exp_f16_sdwa v60, v56 dst_sel:WORD_1 dst_unused:UNUSED_PRESERVE src0_sel:WORD_1
	v_exp_f16_sdwa v61, v57 dst_sel:WORD_1 dst_unused:UNUSED_PRESERVE src0_sel:WORD_1
	v_pk_add_f16 v45, v45, v58
	v_pk_add_f16 v44, v44, v59
	v_rcp_f16_e32 v54, v45
	v_rcp_f16_sdwa v45, v45 dst_sel:DWORD dst_unused:UNUSED_PAD src0_sel:WORD_1
	v_pk_add_f16 v43, v43, v60
	v_rcp_f16_e32 v55, v44
	v_rcp_f16_sdwa v44, v44 dst_sel:DWORD dst_unused:UNUSED_PAD src0_sel:WORD_1
	v_pk_add_f16 v42, v42, v61
	v_pk_fma_f16 v30, v70, v58, v30
	v_rcp_f16_e32 v58, v43
	v_rcp_f16_sdwa v43, v43 dst_sel:DWORD dst_unused:UNUSED_PAD src0_sel:WORD_1
	v_pk_fma_f16 v31, v71, v59, v31
	v_rcp_f16_e32 v59, v42
	v_rcp_f16_sdwa v42, v42 dst_sel:DWORD dst_unused:UNUSED_PAD src0_sel:WORD_1
	v_pack_b32_f16 v45, v54, v45
	v_pk_mul_f16 v57, v30, v45
	v_pack_b32_f16 v30, v55, v44
	v_pk_fma_f16 v32, v72, v60, v32
	v_pk_mul_f16 v56, v31, v30
	v_pack_b32_f16 v30, v58, v43
	v_pk_fma_f16 v33, v73, v61, v33
	v_pk_mul_f16 v55, v32, v30
	v_pack_b32_f16 v30, v59, v42
	v_pk_mul_f16 v54, v33, v30
	s_waitcnt vmcnt(0)
	v_pk_mul_f16 v30, v204, v154 op_sel_hi:[0,1]
	v_pk_mul_f16 v31, v204, v155 op_sel_hi:[0,1]
	v_pk_mul_f16 v32, v204, v156 op_sel_hi:[0,1]
	v_pk_mul_f16 v33, v204, v157 op_sel_hi:[0,1]
	v_pk_mul_f16 v42, v202, v154 op_sel_hi:[0,1]
	v_pk_mul_f16 v43, v202, v155 op_sel_hi:[0,1]
	v_pk_mul_f16 v44, v202, v156 op_sel_hi:[0,1]
	v_pk_mul_f16 v45, v202, v157 op_sel_hi:[0,1]
	v_pk_mul_f16 v58, v203, v154 op_sel_hi:[0,1]
	v_pk_mul_f16 v59, v203, v155 op_sel_hi:[0,1]
	v_pk_mul_f16 v60, v203, v156 op_sel_hi:[0,1]
	v_pk_mul_f16 v61, v203, v157 op_sel_hi:[0,1]
	v_pk_fma_f16 v37, v37, v157, v33
	v_pk_fma_f16 v36, v36, v156, v32
	v_pk_fma_f16 v35, v35, v155, v31
	v_pk_fma_f16 v34, v34, v154, v30
	v_pk_fma_f16 v49, v49, v157, v45
	v_pk_fma_f16 v48, v48, v156, v44
	v_pk_fma_f16 v47, v47, v155, v43
	v_pk_fma_f16 v46, v46, v154, v42
	v_pk_fma_f16 v62, v69, v157, v61
	v_pk_fma_f16 v63, v68, v156, v60
	v_pk_fma_f16 v64, v67, v155, v59
	v_pk_fma_f16 v65, v66, v154, v58
	v_pk_fma_f16 v66, v89, v157, v33
	v_pk_fma_f16 v67, v88, v156, v32
	v_pk_fma_f16 v68, v87, v155, v31
	v_pk_fma_f16 v69, v86, v154, v30
	v_pk_fma_f16 v78, v117, v157, v45
	v_pk_fma_f16 v79, v116, v156, v44
	v_pk_fma_f16 v80, v115, v155, v43
	v_pk_fma_f16 v81, v114, v154, v42
	v_pk_fma_f16 v82, v133, v157, v61
	v_pk_fma_f16 v83, v132, v156, v60
	v_pk_fma_f16 v84, v131, v155, v59
	v_pk_fma_f16 v85, v130, v154, v58
	v_pk_fma_f16 v61, v17, v157, v61
	v_pk_fma_f16 v60, v16, v156, v60
	v_pk_fma_f16 v59, v15, v155, v59
	v_pk_fma_f16 v58, v14, v154, v58
	v_pk_maximum3_f16 v14, v34, v46, v65
	v_pk_maximum3_f16 v15, v35, v47, v64
	v_pk_maximum3_f16 v16, v36, v48, v63
	v_pk_maximum3_f16 v17, v37, v49, v62
	v_pk_maximum3_f16 v86, v69, v81, v85
	v_pk_maximum3_f16 v87, v68, v80, v84
	v_pk_maximum3_f16 v88, v67, v79, v83
	v_pk_maximum3_f16 v89, v66, v78, v82
	v_pk_fma_f16 v33, v145, v157, v33
	v_pk_fma_f16 v32, v144, v156, v32
	v_pk_fma_f16 v31, v143, v155, v31
	v_pk_fma_f16 v30, v142, v154, v30
	v_pk_fma_f16 v45, v153, v157, v45
	v_pk_fma_f16 v44, v152, v156, v44
	v_pk_fma_f16 v43, v151, v155, v43
	v_pk_fma_f16 v42, v150, v154, v42
	v_pk_maximum3_f16 v95, v31, v43, v59
	v_pk_maximum3_f16 v96, v32, v44, v60
	v_pk_maximum3_f16 v97, v33, v45, v61
	v_pk_maximum3_f16 v94, v30, v42, v58
	v_pk_maximum3_f16 v15, v15, v87, v95
	v_pk_maximum3_f16 v16, v16, v88, v96
	v_pk_maximum3_f16 v17, v17, v89, v97
	v_pk_maximum3_f16 v14, v14, v86, v94
	v_xor_b32_e32 v86, 0x80008000, v17
	v_xor_b32_e32 v87, 0x80008000, v16
	v_xor_b32_e32 v88, 0x80008000, v15
	v_xor_b32_e32 v89, 0x80008000, v14
	v_pk_add_f16 v14, v34, v89
	v_pk_add_f16 v15, v35, v88
	v_pk_add_f16 v16, v36, v87
	v_pk_add_f16 v17, v37, v86
	v_exp_f16_sdwa v34, v14 dst_sel:WORD_0 dst_unused:UNUSED_PAD src0_sel:WORD_0
	v_exp_f16_sdwa v35, v15 dst_sel:WORD_0 dst_unused:UNUSED_PAD src0_sel:WORD_0
	v_exp_f16_sdwa v36, v16 dst_sel:WORD_0 dst_unused:UNUSED_PAD src0_sel:WORD_0
	v_exp_f16_sdwa v37, v17 dst_sel:WORD_0 dst_unused:UNUSED_PAD src0_sel:WORD_0
	v_exp_f16_sdwa v34, v14 dst_sel:WORD_1 dst_unused:UNUSED_PRESERVE src0_sel:WORD_1
	v_exp_f16_sdwa v35, v15 dst_sel:WORD_1 dst_unused:UNUSED_PRESERVE src0_sel:WORD_1
	v_exp_f16_sdwa v36, v16 dst_sel:WORD_1 dst_unused:UNUSED_PRESERVE src0_sel:WORD_1
	v_exp_f16_sdwa v37, v17 dst_sel:WORD_1 dst_unused:UNUSED_PRESERVE src0_sel:WORD_1
	v_pk_add_f16 v14, v34, 0
	v_pk_add_f16 v15, v35, 0
	v_pk_add_f16 v16, v36, 0
	v_pk_add_f16 v17, v37, 0
	v_pk_fma_f16 v18, v18, v34, 0
	v_pk_fma_f16 v19, v19, v35, 0
	v_pk_fma_f16 v20, v20, v36, 0
	v_pk_fma_f16 v21, v21, v37, 0
	v_pk_add_f16 v34, v46, v89
	v_pk_add_f16 v35, v47, v88
	v_pk_add_f16 v36, v48, v87
	v_pk_add_f16 v37, v49, v86
	v_exp_f16_sdwa v46, v34 dst_sel:WORD_0 dst_unused:UNUSED_PAD src0_sel:WORD_0
	v_exp_f16_sdwa v47, v35 dst_sel:WORD_0 dst_unused:UNUSED_PAD src0_sel:WORD_0
	v_exp_f16_sdwa v48, v36 dst_sel:WORD_0 dst_unused:UNUSED_PAD src0_sel:WORD_0
	v_exp_f16_sdwa v49, v37 dst_sel:WORD_0 dst_unused:UNUSED_PAD src0_sel:WORD_0
	v_exp_f16_sdwa v46, v34 dst_sel:WORD_1 dst_unused:UNUSED_PRESERVE src0_sel:WORD_1
	v_exp_f16_sdwa v47, v35 dst_sel:WORD_1 dst_unused:UNUSED_PRESERVE src0_sel:WORD_1
	v_exp_f16_sdwa v48, v36 dst_sel:WORD_1 dst_unused:UNUSED_PRESERVE src0_sel:WORD_1
	v_exp_f16_sdwa v49, v37 dst_sel:WORD_1 dst_unused:UNUSED_PRESERVE src0_sel:WORD_1
	s_nop 0
	v_pk_add_f16 v17, v17, v49
	v_pk_add_f16 v16, v16, v48
	v_pk_add_f16 v15, v15, v47
	v_pk_add_f16 v14, v14, v46
	v_pk_fma_f16 v21, v25, v49, v21
	v_pk_fma_f16 v20, v24, v48, v20
	v_pk_fma_f16 v19, v23, v47, v19
	v_pk_fma_f16 v18, v22, v46, v18
	v_pk_add_f16 v22, v65, v89
	v_pk_add_f16 v23, v64, v88
	v_pk_add_f16 v24, v63, v87
	v_pk_add_f16 v25, v62, v86
	v_exp_f16_sdwa v34, v22 dst_sel:WORD_0 dst_unused:UNUSED_PAD src0_sel:WORD_0
	v_exp_f16_sdwa v35, v23 dst_sel:WORD_0 dst_unused:UNUSED_PAD src0_sel:WORD_0
	v_exp_f16_sdwa v36, v24 dst_sel:WORD_0 dst_unused:UNUSED_PAD src0_sel:WORD_0
	v_exp_f16_sdwa v37, v25 dst_sel:WORD_0 dst_unused:UNUSED_PAD src0_sel:WORD_0
	v_exp_f16_sdwa v34, v22 dst_sel:WORD_1 dst_unused:UNUSED_PRESERVE src0_sel:WORD_1
	v_exp_f16_sdwa v35, v23 dst_sel:WORD_1 dst_unused:UNUSED_PRESERVE src0_sel:WORD_1
	v_exp_f16_sdwa v36, v24 dst_sel:WORD_1 dst_unused:UNUSED_PRESERVE src0_sel:WORD_1
	v_exp_f16_sdwa v37, v25 dst_sel:WORD_1 dst_unused:UNUSED_PRESERVE src0_sel:WORD_1
	v_pk_add_f16 v22, v69, v89
	v_pk_add_f16 v14, v14, v34
	v_pk_add_f16 v15, v15, v35
	v_pk_add_f16 v16, v16, v36
	v_pk_add_f16 v17, v17, v37
	v_pk_fma_f16 v18, v26, v34, v18
	v_pk_fma_f16 v19, v27, v35, v19
	v_pk_fma_f16 v20, v28, v36, v20
	v_pk_fma_f16 v21, v29, v37, v21
	v_pk_add_f16 v23, v68, v88
	v_pk_add_f16 v24, v67, v87
	v_pk_add_f16 v25, v66, v86
	v_exp_f16_sdwa v26, v22 dst_sel:WORD_0 dst_unused:UNUSED_PAD src0_sel:WORD_0
	v_exp_f16_sdwa v27, v23 dst_sel:WORD_0 dst_unused:UNUSED_PAD src0_sel:WORD_0
	v_exp_f16_sdwa v28, v24 dst_sel:WORD_0 dst_unused:UNUSED_PAD src0_sel:WORD_0
	v_exp_f16_sdwa v29, v25 dst_sel:WORD_0 dst_unused:UNUSED_PAD src0_sel:WORD_0
	v_exp_f16_sdwa v26, v22 dst_sel:WORD_1 dst_unused:UNUSED_PRESERVE src0_sel:WORD_1
	v_exp_f16_sdwa v27, v23 dst_sel:WORD_1 dst_unused:UNUSED_PRESERVE src0_sel:WORD_1
	v_exp_f16_sdwa v28, v24 dst_sel:WORD_1 dst_unused:UNUSED_PRESERVE src0_sel:WORD_1
	v_exp_f16_sdwa v29, v25 dst_sel:WORD_1 dst_unused:UNUSED_PRESERVE src0_sel:WORD_1
	v_pk_add_f16 v22, v81, v89
	v_pk_add_f16 v17, v17, v29
	v_pk_add_f16 v16, v16, v28
	v_pk_add_f16 v15, v15, v27
	v_pk_add_f16 v14, v14, v26
	v_pk_fma_f16 v21, v41, v29, v21
	v_pk_fma_f16 v20, v40, v28, v20
	v_pk_fma_f16 v19, v39, v27, v19
	v_pk_fma_f16 v18, v38, v26, v18
	v_pk_add_f16 v23, v80, v88
	v_pk_add_f16 v24, v79, v87
	v_pk_add_f16 v25, v78, v86
	v_exp_f16_sdwa v26, v22 dst_sel:WORD_0 dst_unused:UNUSED_PAD src0_sel:WORD_0
	v_exp_f16_sdwa v27, v23 dst_sel:WORD_0 dst_unused:UNUSED_PAD src0_sel:WORD_0
	v_exp_f16_sdwa v28, v24 dst_sel:WORD_0 dst_unused:UNUSED_PAD src0_sel:WORD_0
	v_exp_f16_sdwa v29, v25 dst_sel:WORD_0 dst_unused:UNUSED_PAD src0_sel:WORD_0
	v_exp_f16_sdwa v26, v22 dst_sel:WORD_1 dst_unused:UNUSED_PRESERVE src0_sel:WORD_1
	v_exp_f16_sdwa v27, v23 dst_sel:WORD_1 dst_unused:UNUSED_PRESERVE src0_sel:WORD_1
	v_exp_f16_sdwa v28, v24 dst_sel:WORD_1 dst_unused:UNUSED_PRESERVE src0_sel:WORD_1
	v_exp_f16_sdwa v29, v25 dst_sel:WORD_1 dst_unused:UNUSED_PRESERVE src0_sel:WORD_1
	v_pk_add_f16 v22, v85, v89
	v_pk_add_f16 v14, v14, v26
	v_pk_add_f16 v15, v15, v27
	v_pk_add_f16 v16, v16, v28
	v_pk_add_f16 v17, v17, v29
	v_pk_fma_f16 v18, v50, v26, v18
	v_pk_fma_f16 v19, v51, v27, v19
	v_pk_fma_f16 v20, v52, v28, v20
	v_pk_fma_f16 v21, v53, v29, v21
	v_pk_add_f16 v23, v84, v88
	v_pk_add_f16 v24, v83, v87
	v_pk_add_f16 v25, v82, v86
	v_exp_f16_sdwa v26, v22 dst_sel:WORD_0 dst_unused:UNUSED_PAD src0_sel:WORD_0
	v_exp_f16_sdwa v27, v23 dst_sel:WORD_0 dst_unused:UNUSED_PAD src0_sel:WORD_0
	v_exp_f16_sdwa v28, v24 dst_sel:WORD_0 dst_unused:UNUSED_PAD src0_sel:WORD_0
	v_exp_f16_sdwa v29, v25 dst_sel:WORD_0 dst_unused:UNUSED_PAD src0_sel:WORD_0
	v_exp_f16_sdwa v26, v22 dst_sel:WORD_1 dst_unused:UNUSED_PRESERVE src0_sel:WORD_1
	v_exp_f16_sdwa v27, v23 dst_sel:WORD_1 dst_unused:UNUSED_PRESERVE src0_sel:WORD_1
	v_exp_f16_sdwa v28, v24 dst_sel:WORD_1 dst_unused:UNUSED_PRESERVE src0_sel:WORD_1
	v_exp_f16_sdwa v29, v25 dst_sel:WORD_1 dst_unused:UNUSED_PRESERVE src0_sel:WORD_1
	v_pk_add_f16 v22, v30, v89
	v_pk_add_f16 v17, v17, v29
	v_pk_add_f16 v16, v16, v28
	v_pk_add_f16 v15, v15, v27
	v_pk_add_f16 v14, v14, v26
	v_pk_fma_f16 v21, v73, v29, v21
	v_pk_fma_f16 v20, v72, v28, v20
	v_pk_fma_f16 v19, v71, v27, v19
	v_pk_fma_f16 v18, v70, v26, v18
	v_pk_add_f16 v23, v31, v88
	v_pk_add_f16 v24, v32, v87
	v_pk_add_f16 v25, v33, v86
	v_exp_f16_sdwa v26, v22 dst_sel:WORD_0 dst_unused:UNUSED_PAD src0_sel:WORD_0
	v_exp_f16_sdwa v27, v23 dst_sel:WORD_0 dst_unused:UNUSED_PAD src0_sel:WORD_0
	v_exp_f16_sdwa v28, v24 dst_sel:WORD_0 dst_unused:UNUSED_PAD src0_sel:WORD_0
	v_exp_f16_sdwa v29, v25 dst_sel:WORD_0 dst_unused:UNUSED_PAD src0_sel:WORD_0
	v_exp_f16_sdwa v26, v22 dst_sel:WORD_1 dst_unused:UNUSED_PRESERVE src0_sel:WORD_1
	v_exp_f16_sdwa v27, v23 dst_sel:WORD_1 dst_unused:UNUSED_PRESERVE src0_sel:WORD_1
	v_exp_f16_sdwa v28, v24 dst_sel:WORD_1 dst_unused:UNUSED_PRESERVE src0_sel:WORD_1
	v_exp_f16_sdwa v29, v25 dst_sel:WORD_1 dst_unused:UNUSED_PRESERVE src0_sel:WORD_1
	v_pk_add_f16 v22, v42, v89
	v_pk_add_f16 v14, v14, v26
	v_pk_add_f16 v15, v15, v27
	v_pk_add_f16 v16, v16, v28
	v_pk_add_f16 v17, v17, v29
	v_pk_fma_f16 v18, v90, v26, v18
	v_pk_fma_f16 v19, v91, v27, v19
	v_pk_fma_f16 v20, v92, v28, v20
	v_pk_fma_f16 v21, v93, v29, v21
	v_pk_add_f16 v23, v43, v88
	v_pk_add_f16 v24, v44, v87
	v_pk_add_f16 v25, v45, v86
	v_exp_f16_sdwa v26, v22 dst_sel:WORD_0 dst_unused:UNUSED_PAD src0_sel:WORD_0
	v_exp_f16_sdwa v27, v23 dst_sel:WORD_0 dst_unused:UNUSED_PAD src0_sel:WORD_0
	v_exp_f16_sdwa v28, v24 dst_sel:WORD_0 dst_unused:UNUSED_PAD src0_sel:WORD_0
	v_exp_f16_sdwa v29, v25 dst_sel:WORD_0 dst_unused:UNUSED_PAD src0_sel:WORD_0
	v_exp_f16_sdwa v26, v22 dst_sel:WORD_1 dst_unused:UNUSED_PRESERVE src0_sel:WORD_1
	v_exp_f16_sdwa v27, v23 dst_sel:WORD_1 dst_unused:UNUSED_PRESERVE src0_sel:WORD_1
	v_exp_f16_sdwa v28, v24 dst_sel:WORD_1 dst_unused:UNUSED_PRESERVE src0_sel:WORD_1
	v_exp_f16_sdwa v29, v25 dst_sel:WORD_1 dst_unused:UNUSED_PRESERVE src0_sel:WORD_1
	v_pk_add_f16 v22, v58, v89
	v_pk_add_f16 v17, v17, v29
	v_pk_add_f16 v16, v16, v28
	v_pk_add_f16 v15, v15, v27
	v_pk_add_f16 v14, v14, v26
	v_pk_fma_f16 v21, v113, v29, v21
	v_pk_fma_f16 v20, v112, v28, v20
	v_pk_fma_f16 v19, v111, v27, v19
	v_pk_fma_f16 v18, v110, v26, v18
	v_pk_add_f16 v23, v59, v88
	v_pk_add_f16 v24, v60, v87
	v_pk_add_f16 v25, v61, v86
	v_exp_f16_sdwa v30, v22 dst_sel:WORD_0 dst_unused:UNUSED_PAD src0_sel:WORD_0
	v_exp_f16_sdwa v31, v23 dst_sel:WORD_0 dst_unused:UNUSED_PAD src0_sel:WORD_0
	v_exp_f16_sdwa v32, v24 dst_sel:WORD_0 dst_unused:UNUSED_PAD src0_sel:WORD_0
	v_exp_f16_sdwa v33, v25 dst_sel:WORD_0 dst_unused:UNUSED_PAD src0_sel:WORD_0
	v_exp_f16_sdwa v30, v22 dst_sel:WORD_1 dst_unused:UNUSED_PRESERVE src0_sel:WORD_1
	v_exp_f16_sdwa v31, v23 dst_sel:WORD_1 dst_unused:UNUSED_PRESERVE src0_sel:WORD_1
	v_exp_f16_sdwa v32, v24 dst_sel:WORD_1 dst_unused:UNUSED_PRESERVE src0_sel:WORD_1
	v_exp_f16_sdwa v33, v25 dst_sel:WORD_1 dst_unused:UNUSED_PRESERVE src0_sel:WORD_1
	s_nop 0
.LBB4_42:
	s_and_b64 vcc, exec, s[4:5]
	s_cbranch_vccz .LBB4_80
	global_load_dwordx3 v[146:148], v169, s[8:9]
	v_cmp_lt_u32_e64 s[64:65], 0, v199
	v_cmp_gt_u32_e64 s[66:67], 63, v199
	v_cmp_lt_u32_e64 s[68:69], 0, v180
	v_cmp_gt_u32_e64 s[70:71], 60, v180
	buffer_load_dwordx4 v[162:165], v200, s[36:39], 0 offen
	s_and_b64 s[72:73], s[68:69], s[64:65]
	s_and_b64 s[74:75], s[68:69], s[66:67]
	s_and_b64 s[76:77], s[70:71], s[64:65]
	s_and_b64 s[78:79], s[70:71], s[66:67]
	v_mov_b32_e32 v114, v6
	v_mov_b32_e32 v115, v7
	v_mov_b32_e32 v116, v8
	v_mov_b32_e32 v117, v9
	v_mov_b32_e32 v74, v2
	v_mov_b32_e32 v75, v3
	v_mov_b32_e32 v76, v4
	v_mov_b32_e32 v77, v5
	v_mov_b32_e32 v130, v6
	v_mov_b32_e32 v131, v7
	v_mov_b32_e32 v132, v8
	v_mov_b32_e32 v133, v9
	v_mov_b32_e32 v98, v2
	v_mov_b32_e32 v99, v3
	v_mov_b32_e32 v100, v4
	v_mov_b32_e32 v101, v5
	v_mov_b32_e32 v138, v6
	v_mov_b32_e32 v139, v7
	v_mov_b32_e32 v140, v8
	v_mov_b32_e32 v141, v9
	v_mov_b32_e32 v118, v2
	v_mov_b32_e32 v119, v3
	v_mov_b32_e32 v120, v4
	v_mov_b32_e32 v121, v5
	v_mov_b32_e32 v86, v6
	v_mov_b32_e32 v87, v7
	v_mov_b32_e32 v88, v8
	v_mov_b32_e32 v89, v9
	v_mov_b32_e32 v46, v2
	v_mov_b32_e32 v47, v3
	v_mov_b32_e32 v48, v4
	v_mov_b32_e32 v49, v5
	v_mov_b32_e32 v126, v6
	v_mov_b32_e32 v127, v7
	v_mov_b32_e32 v128, v8
	v_mov_b32_e32 v129, v9
	v_mov_b32_e32 v90, v2
	v_mov_b32_e32 v91, v3
	v_mov_b32_e32 v92, v4
	v_mov_b32_e32 v93, v5
	v_mov_b32_e32 v54, v6
	v_mov_b32_e32 v55, v7
	v_mov_b32_e32 v56, v8
	v_mov_b32_e32 v57, v9
	v_mov_b32_e32 v22, v2
	v_mov_b32_e32 v23, v3
	v_mov_b32_e32 v24, v4
	v_mov_b32_e32 v25, v5
	v_mov_b32_e32 v94, v6
	v_mov_b32_e32 v95, v7
	v_mov_b32_e32 v96, v8
	v_mov_b32_e32 v97, v9
	v_mov_b32_e32 v50, v2
	v_mov_b32_e32 v51, v3
	v_mov_b32_e32 v52, v4
	v_mov_b32_e32 v53, v5
	v_mov_b32_e32 v26, v6
	v_mov_b32_e32 v27, v7
	v_mov_b32_e32 v28, v8
	v_mov_b32_e32 v29, v9
	v_mov_b32_e32 v10, v2
	v_mov_b32_e32 v11, v3
	v_mov_b32_e32 v12, v4
	v_mov_b32_e32 v13, v5
	v_mov_b32_e32 v58, v6
	v_mov_b32_e32 v59, v7
	v_mov_b32_e32 v60, v8
	v_mov_b32_e32 v61, v9
	v_mov_b32_e32 v18, v2
	v_mov_b32_e32 v19, v3
	v_mov_b32_e32 v20, v4
	v_mov_b32_e32 v21, v5
	v_mov_b32_e32 v78, v6
	v_mov_b32_e32 v79, v7
	v_mov_b32_e32 v80, v8
	v_mov_b32_e32 v81, v9
	v_mov_b32_e32 v30, v2
	v_mov_b32_e32 v31, v3
	v_mov_b32_e32 v32, v4
	v_mov_b32_e32 v33, v5
	v_mov_b32_e32 v122, v6
	v_mov_b32_e32 v123, v7
	v_mov_b32_e32 v124, v8
	v_mov_b32_e32 v125, v9
	v_mov_b32_e32 v62, v2
	v_mov_b32_e32 v63, v3
	v_mov_b32_e32 v64, v4
	v_mov_b32_e32 v65, v5
	v_mov_b32_e32 v134, v6
	v_mov_b32_e32 v135, v7
	v_mov_b32_e32 v136, v8
	v_mov_b32_e32 v137, v9
	v_mov_b32_e32 v82, v2
	v_mov_b32_e32 v83, v3
	v_mov_b32_e32 v84, v4
	v_mov_b32_e32 v85, v5
	v_mov_b32_e32 v142, v6
	v_mov_b32_e32 v143, v7
	v_mov_b32_e32 v144, v8
	v_mov_b32_e32 v145, v9
	v_mov_b32_e32 v102, v2
	v_mov_b32_e32 v103, v3
	v_mov_b32_e32 v104, v4
	v_mov_b32_e32 v105, v5
	v_add_u32_e32 v245, 0xfffe7c00, v200
	v_add_u32_e32 v246, 0xfffe8000, v200
	s_mov_b64 exec, s[72:73]
	buffer_load_dwordx4 v[114:117], v245, s[36:39], 0 offen
	buffer_load_dwordx4 v[74:77], v245, s[36:39], 0 offen offset:512
	s_mov_b64 exec, -1
	s_mov_b64 exec, s[68:69]
	buffer_load_dwordx4 v[130:133], v246, s[36:39], 0 offen offset:512
	buffer_load_dwordx4 v[98:101], v246, s[36:39], 0 offen offset:1024
	s_mov_b64 exec, -1
	s_mov_b64 exec, s[74:75]
	buffer_load_dwordx4 v[138:141], v246, s[36:39], 0 offen offset:2048
	buffer_load_dwordx4 v[118:121], v246, s[36:39], 0 offen offset:2560
	s_mov_b64 exec, -1
	v_add_u32_e32 v245, 0xfffffc00, v200
	s_mov_b64 exec, s[64:65]
	buffer_load_dwordx4 v[86:89], v245, s[36:39], 0 offen
	buffer_load_dwordx4 v[46:49], v245, s[36:39], 0 offen offset:512
	s_mov_b64 exec, -1
	buffer_load_dwordx4 v[110:113], v200, s[36:39], 0 offen offset:512
	buffer_load_dwordx4 v[66:69], v200, s[36:39], 0 offen offset:1024
	s_mov_b64 exec, s[66:67]
	buffer_load_dwordx4 v[126:129], v200, s[36:39], 0 offen offset:2048
	buffer_load_dwordx4 v[90:93], v200, s[36:39], 0 offen offset:2560
	s_mov_b64 exec, -1
	v_add_u32_e32 v245, 0x17c00, v200
	v_add_u32_e32 v246, 0x18000, v200
	s_mov_b64 exec, s[64:65]
	buffer_load_dwordx4 v[54:57], v245, s[36:39], 0 offen
	buffer_load_dwordx4 v[22:25], v245, s[36:39], 0 offen offset:512
	s_mov_b64 exec, -1
	buffer_load_dwordx4 v[70:73], v246, s[36:39], 0 offen offset:512
	buffer_load_dwordx4 v[34:37], v246, s[36:39], 0 offen offset:1024
	s_mov_b64 exec, s[66:67]
	buffer_load_dwordx4 v[94:97], v246, s[36:39], 0 offen offset:2048
	buffer_load_dwordx4 v[50:53], v246, s[36:39], 0 offen offset:2560
	s_mov_b64 exec, -1
	v_add_u32_e32 v245, 0x18000, v200
	buffer_load_dwordx4 v[154:157], v245, s[36:39], 0 offen
	v_add_u32_e32 v246, 0x30000, v200
	buffer_load_dwordx4 v[150:153], v246, s[36:39], 0 offen
	v_add_u32_e32 v245, 0x2fc00, v200
	v_add_u32_e32 v246, 0x30000, v200
	v_add_u32_e32 v247, 0x47c00, v200
	v_add_u32_e32 v248, 0x48000, v200
	v_add_u32_e32 v249, 0x5fc00, v200
	v_add_u32_e32 v250, 0x60000, v200
	s_waitcnt vmcnt(21)
	v_cvt_f16_f32_e32 v158, v147
	v_cvt_f16_f32_e32 v160, v146
	v_cvt_f16_f32_e32 v159, v148
	v_add_u32_e32 v251, 0x48000, v200
	buffer_load_dwordx4 v[146:149], v251, s[36:39], 0 offen
	s_waitcnt vmcnt(3)
	v_pk_mul_f16 v161, v160, v162 op_sel_hi:[0,1]
	v_pk_mul_f16 v204, v160, v165 op_sel_hi:[0,1]
	v_pk_mul_f16 v208, v158, v165 op_sel_hi:[0,1]
	v_pk_mul_f16 v212, v159, v165 op_sel_hi:[0,1]
	v_pk_mul_f16 v202, v160, v163 op_sel_hi:[0,1]
	v_pk_mul_f16 v203, v160, v164 op_sel_hi:[0,1]
	v_pk_mul_f16 v205, v158, v162 op_sel_hi:[0,1]
	s_mov_b64 exec, s[64:65]
	buffer_load_dwordx4 v[26:29], v245, s[36:39], 0 offen
	buffer_load_dwordx4 v[10:13], v245, s[36:39], 0 offen offset:512
	s_mov_b64 exec, -1
	v_pk_mul_f16 v206, v158, v163 op_sel_hi:[0,1]
	v_pk_mul_f16 v207, v158, v164 op_sel_hi:[0,1]
	v_pk_mul_f16 v209, v159, v162 op_sel_hi:[0,1]
	v_pk_mul_f16 v210, v159, v163 op_sel_hi:[0,1]
	v_pk_mul_f16 v211, v159, v164 op_sel_hi:[0,1]
	v_pk_fma_f16 v117, v117, v165, v204
	v_pk_fma_f16 v114, v114, v162, v161
	v_pk_fma_f16 v133, v133, v165, v204
	v_pk_fma_f16 v130, v130, v162, v161
	v_pk_fma_f16 v141, v141, v165, v204
	v_pk_fma_f16 v138, v138, v162, v161
	v_pk_fma_f16 v161, v89, v165, v208
	v_pk_fma_f16 v213, v113, v165, v208
	buffer_load_dwordx4 v[38:41], v246, s[36:39], 0 offen offset:512
	buffer_load_dwordx4 v[14:17], v246, s[36:39], 0 offen offset:1024
	v_pk_fma_f16 v208, v129, v165, v208
	v_pk_fma_f16 v217, v57, v165, v212
	v_pk_fma_f16 v221, v73, v165, v212
	v_pk_fma_f16 v165, v97, v165, v212
	v_pk_maximum3_f16 v212, v117, v133, v141
	v_pk_fma_f16 v116, v116, v164, v203
	v_pk_fma_f16 v115, v115, v163, v202
	v_pk_fma_f16 v132, v132, v164, v203
	v_pk_fma_f16 v131, v131, v163, v202
	v_pk_fma_f16 v140, v140, v164, v203
	v_pk_fma_f16 v139, v139, v163, v202
	v_pk_fma_f16 v202, v88, v164, v207
	v_pk_fma_f16 v203, v87, v163, v206
	v_pk_fma_f16 v204, v86, v162, v205
	v_pk_fma_f16 v214, v112, v164, v207
	v_pk_fma_f16 v215, v111, v163, v206
	s_mov_b64 exec, s[66:67]
	buffer_load_dwordx4 v[58:61], v246, s[36:39], 0 offen offset:2048
	buffer_load_dwordx4 v[18:21], v246, s[36:39], 0 offen offset:2560
	s_mov_b64 exec, -1
	v_pk_fma_f16 v216, v110, v162, v205
	v_pk_fma_f16 v207, v128, v164, v207
	v_pk_fma_f16 v206, v127, v163, v206
	v_pk_fma_f16 v205, v126, v162, v205
	v_pk_fma_f16 v218, v56, v164, v211
	v_pk_fma_f16 v219, v55, v163, v210
	v_pk_fma_f16 v220, v54, v162, v209
	v_pk_fma_f16 v222, v72, v164, v211
	v_pk_fma_f16 v223, v71, v163, v210
	v_pk_fma_f16 v224, v70, v162, v209
	v_pk_fma_f16 v164, v96, v164, v211
	v_pk_fma_f16 v163, v95, v163, v210
	v_pk_fma_f16 v162, v94, v162, v209
	v_pk_maximum3_f16 v209, v114, v130, v138
	v_pk_maximum3_f16 v210, v115, v131, v139
	v_pk_maximum3_f16 v211, v116, v132, v140
	v_pk_maximum3_f16 v228, v161, v213, v208
	v_pk_maximum3_f16 v232, v217, v221, v165
	v_pk_maximum3_f16 v225, v204, v216, v205
	v_pk_maximum3_f16 v226, v203, v215, v206
	v_pk_maximum3_f16 v227, v202, v214, v207
	v_pk_maximum3_f16 v229, v220, v224, v162
	v_pk_maximum3_f16 v230, v219, v223, v163
	v_pk_maximum3_f16 v212, v212, v228, v232
	v_pk_maximum3_f16 v231, v218, v222, v164
	v_pk_maximum3_f16 v209, v209, v225, v229
	v_pk_maximum3_f16 v210, v210, v226, v230
	v_pk_maximum3_f16 v211, v211, v227, v231
	v_pk_add_f16 v117, v117, v212 neg_lo:[0,1] neg_hi:[0,1]
	s_mov_b64 exec, s[64:65]
	buffer_load_dwordx4 v[78:81], v247, s[36:39], 0 offen
	buffer_load_dwordx4 v[30:33], v247, s[36:39], 0 offen offset:512
	s_mov_b64 exec, -1
	v_pk_add_f16 v114, v114, v209 neg_lo:[0,1] neg_hi:[0,1]
	v_pk_add_f16 v115, v115, v210 neg_lo:[0,1] neg_hi:[0,1]
	v_pk_add_f16 v116, v116, v211 neg_lo:[0,1] neg_hi:[0,1]
	v_pk_add_f16 v130, v130, v209 neg_lo:[0,1] neg_hi:[0,1]
	v_exp_f16_sdwa v225, v114 dst_sel:WORD_0 dst_unused:UNUSED_PAD src0_sel:WORD_0
	v_exp_f16_sdwa v226, v115 dst_sel:WORD_0 dst_unused:UNUSED_PAD src0_sel:WORD_0
	v_exp_f16_sdwa v227, v116 dst_sel:WORD_0 dst_unused:UNUSED_PAD src0_sel:WORD_0
	v_exp_f16_sdwa v228, v117 dst_sel:WORD_0 dst_unused:UNUSED_PAD src0_sel:WORD_0
	v_exp_f16_sdwa v225, v114 dst_sel:WORD_1 dst_unused:UNUSED_PRESERVE src0_sel:WORD_1
	v_exp_f16_sdwa v226, v115 dst_sel:WORD_1 dst_unused:UNUSED_PRESERVE src0_sel:WORD_1
	v_exp_f16_sdwa v227, v116 dst_sel:WORD_1 dst_unused:UNUSED_PRESERVE src0_sel:WORD_1
	v_exp_f16_sdwa v228, v117 dst_sel:WORD_1 dst_unused:UNUSED_PRESERVE src0_sel:WORD_1
	v_pk_add_f16 v131, v131, v210 neg_lo:[0,1] neg_hi:[0,1]
	v_pk_add_f16 v117, v225, 0
	v_pk_fma_f16 v77, v77, v228, 0
	v_pk_add_f16 v114, v228, 0
	v_pk_add_f16 v115, v227, 0
	v_pk_add_f16 v116, v226, 0
	v_pk_fma_f16 v76, v76, v227, 0
	v_pk_fma_f16 v75, v75, v226, 0
	v_pk_fma_f16 v74, v74, v225, 0
	v_pk_add_f16 v132, v132, v211 neg_lo:[0,1] neg_hi:[0,1]
	buffer_load_dwordx4 v[106:109], v248, s[36:39], 0 offen offset:512
	buffer_load_dwordx4 v[42:45], v248, s[36:39], 0 offen offset:1024
	v_pk_add_f16 v133, v133, v212 neg_lo:[0,1] neg_hi:[0,1]
	v_exp_f16_sdwa v225, v130 dst_sel:WORD_0 dst_unused:UNUSED_PAD src0_sel:WORD_0
	v_exp_f16_sdwa v226, v131 dst_sel:WORD_0 dst_unused:UNUSED_PAD src0_sel:WORD_0
	v_exp_f16_sdwa v227, v132 dst_sel:WORD_0 dst_unused:UNUSED_PAD src0_sel:WORD_0
	v_exp_f16_sdwa v228, v133 dst_sel:WORD_0 dst_unused:UNUSED_PAD src0_sel:WORD_0
	v_exp_f16_sdwa v225, v130 dst_sel:WORD_1 dst_unused:UNUSED_PRESERVE src0_sel:WORD_1
	v_exp_f16_sdwa v226, v131 dst_sel:WORD_1 dst_unused:UNUSED_PRESERVE src0_sel:WORD_1
	v_exp_f16_sdwa v227, v132 dst_sel:WORD_1 dst_unused:UNUSED_PRESERVE src0_sel:WORD_1
	v_exp_f16_sdwa v228, v133 dst_sel:WORD_1 dst_unused:UNUSED_PRESERVE src0_sel:WORD_1
	v_pk_add_f16 v117, v117, v225
	v_pk_fma_f16 v77, v101, v228, v77
	v_pk_add_f16 v101, v141, v212 neg_lo:[0,1] neg_hi:[0,1]
	v_pk_add_f16 v116, v116, v226
	v_pk_add_f16 v115, v115, v227
	v_pk_add_f16 v114, v114, v228
	v_pk_fma_f16 v74, v98, v225, v74
	v_pk_fma_f16 v75, v99, v226, v75
	v_pk_fma_f16 v76, v100, v227, v76
	v_pk_add_f16 v98, v138, v209 neg_lo:[0,1] neg_hi:[0,1]
	v_pk_add_f16 v99, v139, v210 neg_lo:[0,1] neg_hi:[0,1]
	v_pk_add_f16 v100, v140, v211 neg_lo:[0,1] neg_hi:[0,1]
	v_exp_f16_sdwa v130, v98 dst_sel:WORD_0 dst_unused:UNUSED_PAD src0_sel:WORD_0
	v_exp_f16_sdwa v131, v99 dst_sel:WORD_0 dst_unused:UNUSED_PAD src0_sel:WORD_0
	v_exp_f16_sdwa v132, v100 dst_sel:WORD_0 dst_unused:UNUSED_PAD src0_sel:WORD_0
	v_exp_f16_sdwa v133, v101 dst_sel:WORD_0 dst_unused:UNUSED_PAD src0_sel:WORD_0
	v_exp_f16_sdwa v130, v98 dst_sel:WORD_1 dst_unused:UNUSED_PRESERVE src0_sel:WORD_1
	v_exp_f16_sdwa v131, v99 dst_sel:WORD_1 dst_unused:UNUSED_PRESERVE src0_sel:WORD_1
	v_exp_f16_sdwa v132, v100 dst_sel:WORD_1 dst_unused:UNUSED_PRESERVE src0_sel:WORD_1
	v_exp_f16_sdwa v133, v101 dst_sel:WORD_1 dst_unused:UNUSED_PRESERVE src0_sel:WORD_1
	v_pk_add_f16 v101, v117, v130
	v_pk_add_f16 v98, v114, v133
	s_mov_b64 exec, s[66:67]
	buffer_load_dwordx4 v[122:125], v248, s[36:39], 0 offen offset:2048
	buffer_load_dwordx4 v[62:65], v248, s[36:39], 0 offen offset:2560
	s_mov_b64 exec, -1
	v_pk_add_f16 v99, v115, v132
	v_pk_add_f16 v100, v116, v131
	v_pk_fma_f16 v77, v121, v133, v77
	v_pk_fma_f16 v76, v120, v132, v76
	v_pk_fma_f16 v75, v119, v131, v75
	v_pk_fma_f16 v74, v118, v130, v74
	v_pk_add_f16 v114, v204, v209 neg_lo:[0,1] neg_hi:[0,1]
	v_pk_add_f16 v115, v203, v210 neg_lo:[0,1] neg_hi:[0,1]
	v_pk_add_f16 v116, v202, v211 neg_lo:[0,1] neg_hi:[0,1]
	v_pk_add_f16 v117, v161, v212 neg_lo:[0,1] neg_hi:[0,1]
	v_exp_f16_sdwa v118, v114 dst_sel:WORD_0 dst_unused:UNUSED_PAD src0_sel:WORD_0
	v_exp_f16_sdwa v119, v115 dst_sel:WORD_0 dst_unused:UNUSED_PAD src0_sel:WORD_0
	v_exp_f16_sdwa v120, v116 dst_sel:WORD_0 dst_unused:UNUSED_PAD src0_sel:WORD_0
	v_exp_f16_sdwa v121, v117 dst_sel:WORD_0 dst_unused:UNUSED_PAD src0_sel:WORD_0
	v_exp_f16_sdwa v118, v114 dst_sel:WORD_1 dst_unused:UNUSED_PRESERVE src0_sel:WORD_1
	v_exp_f16_sdwa v119, v115 dst_sel:WORD_1 dst_unused:UNUSED_PRESERVE src0_sel:WORD_1
	v_exp_f16_sdwa v120, v116 dst_sel:WORD_1 dst_unused:UNUSED_PRESERVE src0_sel:WORD_1
	v_exp_f16_sdwa v121, v117 dst_sel:WORD_1 dst_unused:UNUSED_PRESERVE src0_sel:WORD_1
	v_pk_add_f16 v114, v216, v209 neg_lo:[0,1] neg_hi:[0,1]
	v_pk_add_f16 v101, v101, v118
	v_pk_add_f16 v100, v100, v119
	v_pk_add_f16 v99, v99, v120
	s_mov_b64 exec, s[76:77]
	buffer_load_dwordx4 v[134:137], v249, s[36:39], 0 offen
	buffer_load_dwordx4 v[82:85], v249, s[36:39], 0 offen offset:512
	s_mov_b64 exec, -1
	v_pk_add_f16 v98, v98, v121
	v_pk_fma_f16 v74, v46, v118, v74
	v_pk_fma_f16 v75, v47, v119, v75
	v_pk_fma_f16 v76, v48, v120, v76
	v_pk_fma_f16 v77, v49, v121, v77
	v_pk_add_f16 v115, v215, v210 neg_lo:[0,1] neg_hi:[0,1]
	v_pk_add_f16 v116, v214, v211 neg_lo:[0,1] neg_hi:[0,1]
	v_pk_add_f16 v117, v213, v212 neg_lo:[0,1] neg_hi:[0,1]
	v_exp_f16_sdwa v118, v114 dst_sel:WORD_0 dst_unused:UNUSED_PAD src0_sel:WORD_0
	v_exp_f16_sdwa v119, v115 dst_sel:WORD_0 dst_unused:UNUSED_PAD src0_sel:WORD_0
	v_exp_f16_sdwa v120, v116 dst_sel:WORD_0 dst_unused:UNUSED_PAD src0_sel:WORD_0
	v_exp_f16_sdwa v121, v117 dst_sel:WORD_0 dst_unused:UNUSED_PAD src0_sel:WORD_0
	v_exp_f16_sdwa v118, v114 dst_sel:WORD_1 dst_unused:UNUSED_PRESERVE src0_sel:WORD_1
	v_exp_f16_sdwa v119, v115 dst_sel:WORD_1 dst_unused:UNUSED_PRESERVE src0_sel:WORD_1
	v_exp_f16_sdwa v120, v116 dst_sel:WORD_1 dst_unused:UNUSED_PRESERVE src0_sel:WORD_1
	v_exp_f16_sdwa v121, v117 dst_sel:WORD_1 dst_unused:UNUSED_PRESERVE src0_sel:WORD_1
	v_pk_add_f16 v114, v205, v209 neg_lo:[0,1] neg_hi:[0,1]
	v_pk_add_f16 v101, v101, v118
	v_pk_add_f16 v98, v98, v121
	v_pk_add_f16 v99, v99, v120
	v_pk_add_f16 v100, v100, v119
	v_pk_fma_f16 v77, v69, v121, v77
	v_pk_fma_f16 v76, v68, v120, v76
	s_mov_b64 exec, s[70:71]
	buffer_load_dwordx4 v[142:145], v250, s[36:39], 0 offen offset:512
	buffer_load_dwordx4 v[102:105], v250, s[36:39], 0 offen offset:1024
	s_mov_b64 exec, -1
	v_pk_fma_f16 v75, v67, v119, v75
	v_pk_fma_f16 v74, v66, v118, v74
	v_pk_add_f16 v115, v206, v210 neg_lo:[0,1] neg_hi:[0,1]
	v_pk_add_f16 v116, v207, v211 neg_lo:[0,1] neg_hi:[0,1]
	v_pk_add_f16 v117, v208, v212 neg_lo:[0,1] neg_hi:[0,1]
	v_exp_f16_sdwa v118, v114 dst_sel:WORD_0 dst_unused:UNUSED_PAD src0_sel:WORD_0
	v_exp_f16_sdwa v119, v115 dst_sel:WORD_0 dst_unused:UNUSED_PAD src0_sel:WORD_0
	v_exp_f16_sdwa v120, v116 dst_sel:WORD_0 dst_unused:UNUSED_PAD src0_sel:WORD_0
	v_exp_f16_sdwa v121, v117 dst_sel:WORD_0 dst_unused:UNUSED_PAD src0_sel:WORD_0
	v_exp_f16_sdwa v118, v114 dst_sel:WORD_1 dst_unused:UNUSED_PRESERVE src0_sel:WORD_1
	v_exp_f16_sdwa v119, v115 dst_sel:WORD_1 dst_unused:UNUSED_PRESERVE src0_sel:WORD_1
	v_exp_f16_sdwa v120, v116 dst_sel:WORD_1 dst_unused:UNUSED_PRESERVE src0_sel:WORD_1
	v_exp_f16_sdwa v121, v117 dst_sel:WORD_1 dst_unused:UNUSED_PRESERVE src0_sel:WORD_1
	v_pk_add_f16 v114, v220, v209 neg_lo:[0,1] neg_hi:[0,1]
	v_pk_add_f16 v101, v101, v118
	v_pk_add_f16 v100, v100, v119
	v_pk_add_f16 v99, v99, v120
	v_pk_add_f16 v98, v98, v121
	v_pk_fma_f16 v74, v90, v118, v74
	v_pk_fma_f16 v75, v91, v119, v75
	v_pk_fma_f16 v76, v92, v120, v76
	v_pk_fma_f16 v77, v93, v121, v77
	s_mov_b64 exec, s[78:79]
	buffer_load_dwordx4 v[6:9], v250, s[36:39], 0 offen offset:2048
	buffer_load_dwordx4 v[2:5], v250, s[36:39], 0 offen offset:2560
	s_mov_b64 exec, -1
	v_pk_add_f16 v115, v219, v210 neg_lo:[0,1] neg_hi:[0,1]
	v_pk_add_f16 v116, v218, v211 neg_lo:[0,1] neg_hi:[0,1]
	v_pk_add_f16 v117, v217, v212 neg_lo:[0,1] neg_hi:[0,1]
	v_exp_f16_sdwa v118, v114 dst_sel:WORD_0 dst_unused:UNUSED_PAD src0_sel:WORD_0
	v_exp_f16_sdwa v119, v115 dst_sel:WORD_0 dst_unused:UNUSED_PAD src0_sel:WORD_0
	v_exp_f16_sdwa v120, v116 dst_sel:WORD_0 dst_unused:UNUSED_PAD src0_sel:WORD_0
	v_exp_f16_sdwa v121, v117 dst_sel:WORD_0 dst_unused:UNUSED_PAD src0_sel:WORD_0
	v_exp_f16_sdwa v118, v114 dst_sel:WORD_1 dst_unused:UNUSED_PRESERVE src0_sel:WORD_1
	v_exp_f16_sdwa v119, v115 dst_sel:WORD_1 dst_unused:UNUSED_PRESERVE src0_sel:WORD_1
	v_exp_f16_sdwa v120, v116 dst_sel:WORD_1 dst_unused:UNUSED_PRESERVE src0_sel:WORD_1
	v_exp_f16_sdwa v121, v117 dst_sel:WORD_1 dst_unused:UNUSED_PRESERVE src0_sel:WORD_1
	v_pk_add_f16 v114, v224, v209 neg_lo:[0,1] neg_hi:[0,1]
	v_pk_add_f16 v101, v101, v118
	v_pk_add_f16 v98, v98, v121
	v_pk_add_f16 v99, v99, v120
	v_pk_add_f16 v100, v100, v119
	v_pk_fma_f16 v77, v25, v121, v77
	v_pk_fma_f16 v76, v24, v120, v76
	v_pk_fma_f16 v75, v23, v119, v75
	v_pk_fma_f16 v74, v22, v118, v74
	v_pk_add_f16 v115, v223, v210 neg_lo:[0,1] neg_hi:[0,1]
	v_pk_add_f16 v116, v222, v211 neg_lo:[0,1] neg_hi:[0,1]
	v_pk_add_f16 v117, v221, v212 neg_lo:[0,1] neg_hi:[0,1]
	v_exp_f16_sdwa v118, v114 dst_sel:WORD_0 dst_unused:UNUSED_PAD src0_sel:WORD_0
	v_exp_f16_sdwa v119, v115 dst_sel:WORD_0 dst_unused:UNUSED_PAD src0_sel:WORD_0
	v_exp_f16_sdwa v120, v116 dst_sel:WORD_0 dst_unused:UNUSED_PAD src0_sel:WORD_0
	v_exp_f16_sdwa v121, v117 dst_sel:WORD_0 dst_unused:UNUSED_PAD src0_sel:WORD_0
	v_exp_f16_sdwa v118, v114 dst_sel:WORD_1 dst_unused:UNUSED_PRESERVE src0_sel:WORD_1
	v_exp_f16_sdwa v119, v115 dst_sel:WORD_1 dst_unused:UNUSED_PRESERVE src0_sel:WORD_1
	v_exp_f16_sdwa v120, v116 dst_sel:WORD_1 dst_unused:UNUSED_PRESERVE src0_sel:WORD_1
	v_exp_f16_sdwa v121, v117 dst_sel:WORD_1 dst_unused:UNUSED_PRESERVE src0_sel:WORD_1
	v_pk_add_f16 v114, v162, v209 neg_lo:[0,1] neg_hi:[0,1]
	v_pk_add_f16 v101, v101, v118
	v_pk_add_f16 v100, v100, v119
	v_pk_add_f16 v99, v99, v120
	v_pk_add_f16 v98, v98, v121
	v_pk_fma_f16 v74, v34, v118, v74
	v_pk_fma_f16 v75, v35, v119, v75
	v_pk_fma_f16 v76, v36, v120, v76
	v_pk_fma_f16 v77, v37, v121, v77
	v_pk_add_f16 v115, v163, v210 neg_lo:[0,1] neg_hi:[0,1]
	v_pk_add_f16 v116, v164, v211 neg_lo:[0,1] neg_hi:[0,1]
	v_pk_add_f16 v117, v165, v212 neg_lo:[0,1] neg_hi:[0,1]
	v_exp_f16_sdwa v118, v114 dst_sel:WORD_0 dst_unused:UNUSED_PAD src0_sel:WORD_0
	v_exp_f16_sdwa v119, v115 dst_sel:WORD_0 dst_unused:UNUSED_PAD src0_sel:WORD_0
	v_exp_f16_sdwa v120, v116 dst_sel:WORD_0 dst_unused:UNUSED_PAD src0_sel:WORD_0
	v_exp_f16_sdwa v121, v117 dst_sel:WORD_0 dst_unused:UNUSED_PAD src0_sel:WORD_0
	v_exp_f16_sdwa v118, v114 dst_sel:WORD_1 dst_unused:UNUSED_PRESERVE src0_sel:WORD_1
	v_exp_f16_sdwa v119, v115 dst_sel:WORD_1 dst_unused:UNUSED_PRESERVE src0_sel:WORD_1
	v_exp_f16_sdwa v120, v116 dst_sel:WORD_1 dst_unused:UNUSED_PRESERVE src0_sel:WORD_1
	v_exp_f16_sdwa v121, v117 dst_sel:WORD_1 dst_unused:UNUSED_PRESERVE src0_sel:WORD_1
	v_pk_add_f16 v101, v101, v118
	v_pk_add_f16 v100, v100, v119
	v_rcp_f16_e32 v114, v101
	v_rcp_f16_sdwa v101, v101 dst_sel:DWORD dst_unused:UNUSED_PAD src0_sel:WORD_1
	v_pk_add_f16 v99, v99, v120
	v_rcp_f16_e32 v115, v100
	v_rcp_f16_sdwa v100, v100 dst_sel:DWORD dst_unused:UNUSED_PAD src0_sel:WORD_1
	v_pk_add_f16 v98, v98, v121
	v_rcp_f16_e32 v116, v99
	v_rcp_f16_sdwa v99, v99 dst_sel:DWORD dst_unused:UNUSED_PAD src0_sel:WORD_1
	v_rcp_f16_e32 v117, v98
	v_rcp_f16_sdwa v98, v98 dst_sel:DWORD dst_unused:UNUSED_PAD src0_sel:WORD_1
	v_pk_fma_f16 v74, v50, v118, v74
	v_pack_b32_f16 v101, v114, v101
	v_pk_fma_f16 v75, v51, v119, v75
	v_pk_mul_f16 v138, v74, v101
	v_pack_b32_f16 v74, v115, v100
	v_pk_fma_f16 v76, v52, v120, v76
	v_pk_mul_f16 v139, v75, v74
	v_pack_b32_f16 v74, v116, v99
	v_pk_fma_f16 v77, v53, v121, v77
	v_pk_mul_f16 v140, v76, v74
	v_pack_b32_f16 v74, v117, v98
	v_pk_mul_f16 v141, v77, v74
	s_waitcnt vmcnt(12)
	v_pk_mul_f16 v74, v160, v154 op_sel_hi:[0,1]
	v_pk_mul_f16 v77, v160, v157 op_sel_hi:[0,1]
	v_pk_mul_f16 v101, v158, v157 op_sel_hi:[0,1]
	v_pk_mul_f16 v117, v159, v157 op_sel_hi:[0,1]
	v_pk_mul_f16 v75, v160, v155 op_sel_hi:[0,1]
	v_pk_mul_f16 v76, v160, v156 op_sel_hi:[0,1]
	v_pk_mul_f16 v98, v158, v154 op_sel_hi:[0,1]
	v_pk_mul_f16 v99, v158, v155 op_sel_hi:[0,1]
	v_pk_mul_f16 v100, v158, v156 op_sel_hi:[0,1]
	v_pk_mul_f16 v114, v159, v154 op_sel_hi:[0,1]
	v_pk_mul_f16 v115, v159, v155 op_sel_hi:[0,1]
	v_pk_mul_f16 v116, v159, v156 op_sel_hi:[0,1]
	v_pk_fma_f16 v89, v89, v157, v77
	v_pk_fma_f16 v86, v86, v154, v74
	v_pk_fma_f16 v113, v113, v157, v77
	v_pk_fma_f16 v110, v110, v154, v74
	v_pk_fma_f16 v77, v129, v157, v77
	v_pk_fma_f16 v74, v126, v154, v74
	v_pk_fma_f16 v118, v57, v157, v101
	v_pk_fma_f16 v126, v73, v157, v101
	v_pk_fma_f16 v101, v97, v157, v101
	v_pk_fma_f16 v130, v29, v157, v117
	v_pk_fma_f16 v161, v41, v157, v117
	v_pk_fma_f16 v117, v61, v157, v117
	v_pk_maximum3_f16 v157, v89, v113, v77
	v_pk_fma_f16 v88, v88, v156, v76
	v_pk_fma_f16 v87, v87, v155, v75
	v_pk_fma_f16 v112, v112, v156, v76
	v_pk_fma_f16 v111, v111, v155, v75
	v_pk_fma_f16 v76, v128, v156, v76
	v_pk_fma_f16 v75, v127, v155, v75
	v_pk_fma_f16 v119, v56, v156, v100
	v_pk_fma_f16 v120, v55, v155, v99
	v_pk_fma_f16 v121, v54, v154, v98
	v_pk_fma_f16 v127, v72, v156, v100
	v_pk_fma_f16 v128, v71, v155, v99
	v_pk_fma_f16 v129, v70, v154, v98
	v_pk_fma_f16 v100, v96, v156, v100
	v_pk_fma_f16 v99, v95, v155, v99
	v_pk_fma_f16 v98, v94, v154, v98
	v_pk_fma_f16 v131, v28, v156, v116
	v_pk_fma_f16 v132, v27, v155, v115
	v_pk_fma_f16 v133, v26, v154, v114
	v_pk_fma_f16 v162, v40, v156, v116
	v_pk_fma_f16 v163, v39, v155, v115
	v_pk_fma_f16 v164, v38, v154, v114
	v_pk_fma_f16 v116, v60, v156, v116
	v_pk_fma_f16 v115, v59, v155, v115
	v_pk_fma_f16 v114, v58, v154, v114
	v_pk_maximum3_f16 v154, v86, v110, v74
	v_pk_maximum3_f16 v155, v87, v111, v75
	v_pk_maximum3_f16 v156, v88, v112, v76
	v_pk_maximum3_f16 v204, v118, v126, v101
	v_pk_maximum3_f16 v208, v130, v161, v117
	v_pk_maximum3_f16 v165, v121, v129, v98
	v_pk_maximum3_f16 v202, v120, v128, v99
	v_pk_maximum3_f16 v203, v119, v127, v100
	v_pk_maximum3_f16 v205, v133, v164, v114
	v_pk_maximum3_f16 v206, v132, v163, v115
	v_pk_maximum3_f16 v157, v157, v204, v208
	v_pk_maximum3_f16 v207, v131, v162, v116
	v_pk_maximum3_f16 v154, v154, v165, v205
	v_pk_maximum3_f16 v155, v155, v202, v206
	v_pk_maximum3_f16 v156, v156, v203, v207
	v_pk_add_f16 v89, v89, v157 neg_lo:[0,1] neg_hi:[0,1]
	v_pk_add_f16 v86, v86, v154 neg_lo:[0,1] neg_hi:[0,1]
	v_pk_add_f16 v87, v87, v155 neg_lo:[0,1] neg_hi:[0,1]
	v_pk_add_f16 v88, v88, v156 neg_lo:[0,1] neg_hi:[0,1]
	v_pk_add_f16 v110, v110, v154 neg_lo:[0,1] neg_hi:[0,1]
	v_exp_f16_sdwa v165, v86 dst_sel:WORD_0 dst_unused:UNUSED_PAD src0_sel:WORD_0
	v_exp_f16_sdwa v202, v87 dst_sel:WORD_0 dst_unused:UNUSED_PAD src0_sel:WORD_0
	v_exp_f16_sdwa v203, v88 dst_sel:WORD_0 dst_unused:UNUSED_PAD src0_sel:WORD_0
	v_exp_f16_sdwa v204, v89 dst_sel:WORD_0 dst_unused:UNUSED_PAD src0_sel:WORD_0
	v_exp_f16_sdwa v165, v86 dst_sel:WORD_1 dst_unused:UNUSED_PRESERVE src0_sel:WORD_1
	v_exp_f16_sdwa v202, v87 dst_sel:WORD_1 dst_unused:UNUSED_PRESERVE src0_sel:WORD_1
	v_exp_f16_sdwa v203, v88 dst_sel:WORD_1 dst_unused:UNUSED_PRESERVE src0_sel:WORD_1
	v_exp_f16_sdwa v204, v89 dst_sel:WORD_1 dst_unused:UNUSED_PRESERVE src0_sel:WORD_1
	v_pk_add_f16 v111, v111, v155 neg_lo:[0,1] neg_hi:[0,1]
	v_pk_add_f16 v89, v165, 0
	v_pk_fma_f16 v49, v49, v204, 0
	v_pk_add_f16 v86, v204, 0
	v_pk_add_f16 v87, v203, 0
	v_pk_add_f16 v88, v202, 0
	v_pk_fma_f16 v48, v48, v203, 0
	v_pk_fma_f16 v47, v47, v202, 0
	v_pk_fma_f16 v46, v46, v165, 0
	v_pk_add_f16 v112, v112, v156 neg_lo:[0,1] neg_hi:[0,1]
	v_pk_add_f16 v113, v113, v157 neg_lo:[0,1] neg_hi:[0,1]
	v_exp_f16_sdwa v165, v110 dst_sel:WORD_0 dst_unused:UNUSED_PAD src0_sel:WORD_0
	v_exp_f16_sdwa v202, v111 dst_sel:WORD_0 dst_unused:UNUSED_PAD src0_sel:WORD_0
	v_exp_f16_sdwa v203, v112 dst_sel:WORD_0 dst_unused:UNUSED_PAD src0_sel:WORD_0
	v_exp_f16_sdwa v204, v113 dst_sel:WORD_0 dst_unused:UNUSED_PAD src0_sel:WORD_0
	v_exp_f16_sdwa v165, v110 dst_sel:WORD_1 dst_unused:UNUSED_PRESERVE src0_sel:WORD_1
	v_exp_f16_sdwa v202, v111 dst_sel:WORD_1 dst_unused:UNUSED_PRESERVE src0_sel:WORD_1
	v_exp_f16_sdwa v203, v112 dst_sel:WORD_1 dst_unused:UNUSED_PRESERVE src0_sel:WORD_1
	v_exp_f16_sdwa v204, v113 dst_sel:WORD_1 dst_unused:UNUSED_PRESERVE src0_sel:WORD_1
	v_pk_add_f16 v89, v89, v165
	v_pk_fma_f16 v49, v69, v204, v49
	v_pk_add_f16 v69, v77, v157 neg_lo:[0,1] neg_hi:[0,1]
	v_pk_add_f16 v88, v88, v202
	v_pk_add_f16 v87, v87, v203
	v_pk_add_f16 v86, v86, v204
	v_pk_fma_f16 v46, v66, v165, v46
	v_pk_fma_f16 v47, v67, v202, v47
	v_pk_fma_f16 v48, v68, v203, v48
	v_pk_add_f16 v66, v74, v154 neg_lo:[0,1] neg_hi:[0,1]
	v_pk_add_f16 v67, v75, v155 neg_lo:[0,1] neg_hi:[0,1]
	v_pk_add_f16 v68, v76, v156 neg_lo:[0,1] neg_hi:[0,1]
	v_exp_f16_sdwa v74, v66 dst_sel:WORD_0 dst_unused:UNUSED_PAD src0_sel:WORD_0
	v_exp_f16_sdwa v75, v67 dst_sel:WORD_0 dst_unused:UNUSED_PAD src0_sel:WORD_0
	v_exp_f16_sdwa v76, v68 dst_sel:WORD_0 dst_unused:UNUSED_PAD src0_sel:WORD_0
	v_exp_f16_sdwa v77, v69 dst_sel:WORD_0 dst_unused:UNUSED_PAD src0_sel:WORD_0
	v_exp_f16_sdwa v74, v66 dst_sel:WORD_1 dst_unused:UNUSED_PRESERVE src0_sel:WORD_1
	v_exp_f16_sdwa v75, v67 dst_sel:WORD_1 dst_unused:UNUSED_PRESERVE src0_sel:WORD_1
	v_exp_f16_sdwa v76, v68 dst_sel:WORD_1 dst_unused:UNUSED_PRESERVE src0_sel:WORD_1
	v_exp_f16_sdwa v77, v69 dst_sel:WORD_1 dst_unused:UNUSED_PRESERVE src0_sel:WORD_1
	v_pk_add_f16 v69, v89, v74
	v_pk_add_f16 v66, v86, v77
	v_pk_add_f16 v67, v87, v76
	v_pk_add_f16 v68, v88, v75
	v_pk_fma_f16 v49, v93, v77, v49
	v_pk_fma_f16 v48, v92, v76, v48
	v_pk_fma_f16 v47, v91, v75, v47
	v_pk_fma_f16 v46, v90, v74, v46
	v_pk_add_f16 v74, v121, v154 neg_lo:[0,1] neg_hi:[0,1]
	v_pk_add_f16 v75, v120, v155 neg_lo:[0,1] neg_hi:[0,1]
	v_pk_add_f16 v76, v119, v156 neg_lo:[0,1] neg_hi:[0,1]
	v_pk_add_f16 v77, v118, v157 neg_lo:[0,1] neg_hi:[0,1]
	v_exp_f16_sdwa v86, v74 dst_sel:WORD_0 dst_unused:UNUSED_PAD src0_sel:WORD_0
	v_exp_f16_sdwa v87, v75 dst_sel:WORD_0 dst_unused:UNUSED_PAD src0_sel:WORD_0
	v_exp_f16_sdwa v88, v76 dst_sel:WORD_0 dst_unused:UNUSED_PAD src0_sel:WORD_0
	v_exp_f16_sdwa v89, v77 dst_sel:WORD_0 dst_unused:UNUSED_PAD src0_sel:WORD_0
	v_exp_f16_sdwa v86, v74 dst_sel:WORD_1 dst_unused:UNUSED_PRESERVE src0_sel:WORD_1
	v_exp_f16_sdwa v87, v75 dst_sel:WORD_1 dst_unused:UNUSED_PRESERVE src0_sel:WORD_1
	v_exp_f16_sdwa v88, v76 dst_sel:WORD_1 dst_unused:UNUSED_PRESERVE src0_sel:WORD_1
	v_exp_f16_sdwa v89, v77 dst_sel:WORD_1 dst_unused:UNUSED_PRESERVE src0_sel:WORD_1
	v_pk_add_f16 v74, v129, v154 neg_lo:[0,1] neg_hi:[0,1]
	v_pk_add_f16 v69, v69, v86
	v_pk_add_f16 v68, v68, v87
	v_pk_add_f16 v67, v67, v88
	v_pk_add_f16 v66, v66, v89
	v_pk_fma_f16 v46, v22, v86, v46
	v_pk_fma_f16 v47, v23, v87, v47
	v_pk_fma_f16 v48, v24, v88, v48
	v_pk_fma_f16 v49, v25, v89, v49
	v_pk_add_f16 v75, v128, v155 neg_lo:[0,1] neg_hi:[0,1]
	v_pk_add_f16 v76, v127, v156 neg_lo:[0,1] neg_hi:[0,1]
	v_pk_add_f16 v77, v126, v157 neg_lo:[0,1] neg_hi:[0,1]
	v_exp_f16_sdwa v86, v74 dst_sel:WORD_0 dst_unused:UNUSED_PAD src0_sel:WORD_0
	v_exp_f16_sdwa v87, v75 dst_sel:WORD_0 dst_unused:UNUSED_PAD src0_sel:WORD_0
	v_exp_f16_sdwa v88, v76 dst_sel:WORD_0 dst_unused:UNUSED_PAD src0_sel:WORD_0
	v_exp_f16_sdwa v89, v77 dst_sel:WORD_0 dst_unused:UNUSED_PAD src0_sel:WORD_0
	v_exp_f16_sdwa v86, v74 dst_sel:WORD_1 dst_unused:UNUSED_PRESERVE src0_sel:WORD_1
	v_exp_f16_sdwa v87, v75 dst_sel:WORD_1 dst_unused:UNUSED_PRESERVE src0_sel:WORD_1
	v_exp_f16_sdwa v88, v76 dst_sel:WORD_1 dst_unused:UNUSED_PRESERVE src0_sel:WORD_1
	v_exp_f16_sdwa v89, v77 dst_sel:WORD_1 dst_unused:UNUSED_PRESERVE src0_sel:WORD_1
	v_pk_add_f16 v74, v98, v154 neg_lo:[0,1] neg_hi:[0,1]
	v_pk_add_f16 v69, v69, v86
	v_pk_add_f16 v66, v66, v89
	v_pk_add_f16 v67, v67, v88
	v_pk_add_f16 v68, v68, v87
	v_pk_fma_f16 v49, v37, v89, v49
	v_pk_fma_f16 v48, v36, v88, v48
	v_pk_fma_f16 v47, v35, v87, v47
	v_pk_fma_f16 v46, v34, v86, v46
	v_pk_add_f16 v75, v99, v155 neg_lo:[0,1] neg_hi:[0,1]
	v_pk_add_f16 v76, v100, v156 neg_lo:[0,1] neg_hi:[0,1]
	v_pk_add_f16 v77, v101, v157 neg_lo:[0,1] neg_hi:[0,1]
	v_exp_f16_sdwa v86, v74 dst_sel:WORD_0 dst_unused:UNUSED_PAD src0_sel:WORD_0
	v_exp_f16_sdwa v87, v75 dst_sel:WORD_0 dst_unused:UNUSED_PAD src0_sel:WORD_0
	v_exp_f16_sdwa v88, v76 dst_sel:WORD_0 dst_unused:UNUSED_PAD src0_sel:WORD_0
	v_exp_f16_sdwa v89, v77 dst_sel:WORD_0 dst_unused:UNUSED_PAD src0_sel:WORD_0
	v_exp_f16_sdwa v86, v74 dst_sel:WORD_1 dst_unused:UNUSED_PRESERVE src0_sel:WORD_1
	v_exp_f16_sdwa v87, v75 dst_sel:WORD_1 dst_unused:UNUSED_PRESERVE src0_sel:WORD_1
	v_exp_f16_sdwa v88, v76 dst_sel:WORD_1 dst_unused:UNUSED_PRESERVE src0_sel:WORD_1
	v_exp_f16_sdwa v89, v77 dst_sel:WORD_1 dst_unused:UNUSED_PRESERVE src0_sel:WORD_1
	v_pk_add_f16 v74, v133, v154 neg_lo:[0,1] neg_hi:[0,1]
	v_pk_add_f16 v69, v69, v86
	v_pk_add_f16 v68, v68, v87
	v_pk_add_f16 v67, v67, v88
	v_pk_add_f16 v66, v66, v89
	v_pk_fma_f16 v46, v50, v86, v46
	v_pk_fma_f16 v47, v51, v87, v47
	v_pk_fma_f16 v48, v52, v88, v48
	v_pk_fma_f16 v49, v53, v89, v49
	v_pk_add_f16 v75, v132, v155 neg_lo:[0,1] neg_hi:[0,1]
	v_pk_add_f16 v76, v131, v156 neg_lo:[0,1] neg_hi:[0,1]
	v_pk_add_f16 v77, v130, v157 neg_lo:[0,1] neg_hi:[0,1]
	v_exp_f16_sdwa v86, v74 dst_sel:WORD_0 dst_unused:UNUSED_PAD src0_sel:WORD_0
	v_exp_f16_sdwa v87, v75 dst_sel:WORD_0 dst_unused:UNUSED_PAD src0_sel:WORD_0
	v_exp_f16_sdwa v88, v76 dst_sel:WORD_0 dst_unused:UNUSED_PAD src0_sel:WORD_0
	v_exp_f16_sdwa v89, v77 dst_sel:WORD_0 dst_unused:UNUSED_PAD src0_sel:WORD_0
	v_exp_f16_sdwa v86, v74 dst_sel:WORD_1 dst_unused:UNUSED_PRESERVE src0_sel:WORD_1
	v_exp_f16_sdwa v87, v75 dst_sel:WORD_1 dst_unused:UNUSED_PRESERVE src0_sel:WORD_1
	v_exp_f16_sdwa v88, v76 dst_sel:WORD_1 dst_unused:UNUSED_PRESERVE src0_sel:WORD_1
	v_exp_f16_sdwa v89, v77 dst_sel:WORD_1 dst_unused:UNUSED_PRESERVE src0_sel:WORD_1
	v_pk_add_f16 v74, v164, v154 neg_lo:[0,1] neg_hi:[0,1]
	v_pk_add_f16 v69, v69, v86
	v_pk_add_f16 v66, v66, v89
	v_pk_add_f16 v67, v67, v88
	v_pk_add_f16 v68, v68, v87
	v_pk_fma_f16 v49, v13, v89, v49
	v_pk_fma_f16 v48, v12, v88, v48
	v_pk_fma_f16 v47, v11, v87, v47
	v_pk_fma_f16 v46, v10, v86, v46
	v_pk_add_f16 v75, v163, v155 neg_lo:[0,1] neg_hi:[0,1]
	v_pk_add_f16 v76, v162, v156 neg_lo:[0,1] neg_hi:[0,1]
	v_pk_add_f16 v77, v161, v157 neg_lo:[0,1] neg_hi:[0,1]
	v_exp_f16_sdwa v86, v74 dst_sel:WORD_0 dst_unused:UNUSED_PAD src0_sel:WORD_0
	v_exp_f16_sdwa v87, v75 dst_sel:WORD_0 dst_unused:UNUSED_PAD src0_sel:WORD_0
	v_exp_f16_sdwa v88, v76 dst_sel:WORD_0 dst_unused:UNUSED_PAD src0_sel:WORD_0
	v_exp_f16_sdwa v89, v77 dst_sel:WORD_0 dst_unused:UNUSED_PAD src0_sel:WORD_0
	v_exp_f16_sdwa v86, v74 dst_sel:WORD_1 dst_unused:UNUSED_PRESERVE src0_sel:WORD_1
	v_exp_f16_sdwa v87, v75 dst_sel:WORD_1 dst_unused:UNUSED_PRESERVE src0_sel:WORD_1
	v_exp_f16_sdwa v88, v76 dst_sel:WORD_1 dst_unused:UNUSED_PRESERVE src0_sel:WORD_1
	v_exp_f16_sdwa v89, v77 dst_sel:WORD_1 dst_unused:UNUSED_PRESERVE src0_sel:WORD_1
	v_pk_add_f16 v74, v114, v154 neg_lo:[0,1] neg_hi:[0,1]
	v_pk_add_f16 v69, v69, v86
	v_pk_add_f16 v68, v68, v87
	v_pk_add_f16 v67, v67, v88
	v_pk_add_f16 v66, v66, v89
	v_pk_fma_f16 v46, v14, v86, v46
	v_pk_fma_f16 v47, v15, v87, v47
	v_pk_fma_f16 v48, v16, v88, v48
	v_pk_fma_f16 v49, v17, v89, v49
	v_pk_add_f16 v75, v115, v155 neg_lo:[0,1] neg_hi:[0,1]
	v_pk_add_f16 v76, v116, v156 neg_lo:[0,1] neg_hi:[0,1]
	v_pk_add_f16 v77, v117, v157 neg_lo:[0,1] neg_hi:[0,1]
	v_exp_f16_sdwa v86, v74 dst_sel:WORD_0 dst_unused:UNUSED_PAD src0_sel:WORD_0
	v_exp_f16_sdwa v87, v75 dst_sel:WORD_0 dst_unused:UNUSED_PAD src0_sel:WORD_0
	v_exp_f16_sdwa v88, v76 dst_sel:WORD_0 dst_unused:UNUSED_PAD src0_sel:WORD_0
	v_exp_f16_sdwa v89, v77 dst_sel:WORD_0 dst_unused:UNUSED_PAD src0_sel:WORD_0
	v_exp_f16_sdwa v86, v74 dst_sel:WORD_1 dst_unused:UNUSED_PRESERVE src0_sel:WORD_1
	v_exp_f16_sdwa v87, v75 dst_sel:WORD_1 dst_unused:UNUSED_PRESERVE src0_sel:WORD_1
	v_exp_f16_sdwa v88, v76 dst_sel:WORD_1 dst_unused:UNUSED_PRESERVE src0_sel:WORD_1
	v_exp_f16_sdwa v89, v77 dst_sel:WORD_1 dst_unused:UNUSED_PRESERVE src0_sel:WORD_1
	v_pk_add_f16 v69, v69, v86
	v_pk_add_f16 v68, v68, v87
	v_rcp_f16_e32 v74, v69
	v_rcp_f16_sdwa v69, v69 dst_sel:DWORD dst_unused:UNUSED_PAD src0_sel:WORD_1
	v_pk_add_f16 v67, v67, v88
	v_rcp_f16_e32 v75, v68
	v_rcp_f16_sdwa v68, v68 dst_sel:DWORD dst_unused:UNUSED_PAD src0_sel:WORD_1
	v_pk_add_f16 v66, v66, v89
	v_pk_fma_f16 v46, v18, v86, v46
	v_rcp_f16_e32 v86, v67
	v_rcp_f16_sdwa v67, v67 dst_sel:DWORD dst_unused:UNUSED_PAD src0_sel:WORD_1
	v_pk_fma_f16 v47, v19, v87, v47
	v_rcp_f16_e32 v87, v66
	v_rcp_f16_sdwa v66, v66 dst_sel:DWORD dst_unused:UNUSED_PAD src0_sel:WORD_1
	v_pack_b32_f16 v69, v74, v69
	v_pk_mul_f16 v77, v46, v69
	v_pack_b32_f16 v46, v75, v68
	v_pk_fma_f16 v48, v20, v88, v48
	v_pk_mul_f16 v76, v47, v46
	v_pack_b32_f16 v46, v86, v67
	v_pk_fma_f16 v49, v21, v89, v49
	v_pk_mul_f16 v75, v48, v46
	v_pack_b32_f16 v46, v87, v66
	v_pk_mul_f16 v74, v49, v46
	s_waitcnt vmcnt(6)
	v_pk_mul_f16 v49, v160, v153 op_sel_hi:[0,1]
	v_pk_mul_f16 v46, v160, v150 op_sel_hi:[0,1]
	v_pk_mul_f16 v47, v160, v151 op_sel_hi:[0,1]
	v_pk_mul_f16 v48, v160, v152 op_sel_hi:[0,1]
	v_pk_mul_f16 v69, v158, v153 op_sel_hi:[0,1]
	v_pk_mul_f16 v89, v159, v153 op_sel_hi:[0,1]
	v_pk_fma_f16 v57, v57, v153, v49
	v_pk_fma_f16 v73, v73, v153, v49
	v_pk_fma_f16 v49, v97, v153, v49
	v_pk_mul_f16 v66, v158, v150 op_sel_hi:[0,1]
	v_pk_maximum3_f16 v117, v57, v73, v49
	v_pk_mul_f16 v67, v158, v151 op_sel_hi:[0,1]
	v_pk_mul_f16 v68, v158, v152 op_sel_hi:[0,1]
	v_pk_mul_f16 v86, v159, v150 op_sel_hi:[0,1]
	v_pk_mul_f16 v87, v159, v151 op_sel_hi:[0,1]
	v_pk_mul_f16 v88, v159, v152 op_sel_hi:[0,1]
	v_pk_fma_f16 v56, v56, v152, v48
	v_pk_fma_f16 v55, v55, v151, v47
	v_pk_fma_f16 v54, v54, v150, v46
	v_pk_fma_f16 v72, v72, v152, v48
	v_pk_fma_f16 v71, v71, v151, v47
	v_pk_fma_f16 v70, v70, v150, v46
	v_pk_fma_f16 v48, v96, v152, v48
	v_pk_fma_f16 v47, v95, v151, v47
	v_pk_fma_f16 v46, v94, v150, v46
	v_pk_fma_f16 v90, v29, v153, v69
	v_pk_fma_f16 v94, v41, v153, v69
	v_pk_fma_f16 v69, v61, v153, v69
	v_pk_fma_f16 v98, v81, v153, v89
	v_pk_fma_f16 v110, v109, v153, v89
	v_pk_fma_f16 v89, v125, v153, v89
	v_pk_maximum3_f16 v114, v54, v70, v46
	v_pk_maximum3_f16 v115, v55, v71, v47
	v_pk_maximum3_f16 v116, v56, v72, v48
	v_pk_maximum3_f16 v121, v90, v94, v69
	v_pk_fma_f16 v91, v28, v152, v68
	v_pk_maximum3_f16 v129, v98, v110, v89
	v_pk_fma_f16 v92, v27, v151, v67
	v_pk_maximum3_f16 v117, v117, v121, v129
	v_pk_fma_f16 v93, v26, v150, v66
	v_pk_fma_f16 v95, v40, v152, v68
	v_pk_fma_f16 v96, v39, v151, v67
	v_pk_fma_f16 v97, v38, v150, v66
	v_pk_fma_f16 v68, v60, v152, v68
	v_pk_fma_f16 v67, v59, v151, v67
	v_pk_fma_f16 v66, v58, v150, v66
	v_pk_fma_f16 v99, v80, v152, v88
	v_pk_fma_f16 v100, v79, v151, v87
	v_pk_fma_f16 v101, v78, v150, v86
	v_pk_fma_f16 v111, v108, v152, v88
	v_pk_fma_f16 v112, v107, v151, v87
	v_pk_fma_f16 v113, v106, v150, v86
	v_pk_fma_f16 v88, v124, v152, v88
	v_pk_fma_f16 v87, v123, v151, v87
	v_pk_fma_f16 v86, v122, v150, v86
	v_pk_maximum3_f16 v118, v93, v97, v66
	v_pk_maximum3_f16 v119, v92, v96, v67
	v_pk_maximum3_f16 v120, v91, v95, v68
	v_pk_maximum3_f16 v127, v100, v112, v87
	v_pk_maximum3_f16 v128, v99, v111, v88
	v_pk_maximum3_f16 v126, v101, v113, v86
	v_pk_maximum3_f16 v114, v114, v118, v126
	v_pk_maximum3_f16 v115, v115, v119, v127
	v_pk_maximum3_f16 v116, v116, v120, v128
	v_pk_add_f16 v57, v57, v117 neg_lo:[0,1] neg_hi:[0,1]
	v_pk_add_f16 v54, v54, v114 neg_lo:[0,1] neg_hi:[0,1]
	v_pk_add_f16 v55, v55, v115 neg_lo:[0,1] neg_hi:[0,1]
	v_pk_add_f16 v56, v56, v116 neg_lo:[0,1] neg_hi:[0,1]
	v_pk_add_f16 v70, v70, v114 neg_lo:[0,1] neg_hi:[0,1]
	v_exp_f16_sdwa v118, v54 dst_sel:WORD_0 dst_unused:UNUSED_PAD src0_sel:WORD_0
	v_exp_f16_sdwa v119, v55 dst_sel:WORD_0 dst_unused:UNUSED_PAD src0_sel:WORD_0
	v_exp_f16_sdwa v120, v56 dst_sel:WORD_0 dst_unused:UNUSED_PAD src0_sel:WORD_0
	v_exp_f16_sdwa v121, v57 dst_sel:WORD_0 dst_unused:UNUSED_PAD src0_sel:WORD_0
	v_exp_f16_sdwa v118, v54 dst_sel:WORD_1 dst_unused:UNUSED_PRESERVE src0_sel:WORD_1
	v_exp_f16_sdwa v119, v55 dst_sel:WORD_1 dst_unused:UNUSED_PRESERVE src0_sel:WORD_1
	v_exp_f16_sdwa v120, v56 dst_sel:WORD_1 dst_unused:UNUSED_PRESERVE src0_sel:WORD_1
	v_exp_f16_sdwa v121, v57 dst_sel:WORD_1 dst_unused:UNUSED_PRESERVE src0_sel:WORD_1
	v_pk_add_f16 v71, v71, v115 neg_lo:[0,1] neg_hi:[0,1]
	v_pk_add_f16 v57, v118, 0
	v_pk_fma_f16 v25, v25, v121, 0
	v_pk_add_f16 v54, v121, 0
	v_pk_add_f16 v55, v120, 0
	v_pk_add_f16 v56, v119, 0
	v_pk_fma_f16 v24, v24, v120, 0
	v_pk_fma_f16 v23, v23, v119, 0
	v_pk_fma_f16 v22, v22, v118, 0
	v_pk_add_f16 v72, v72, v116 neg_lo:[0,1] neg_hi:[0,1]
	v_pk_add_f16 v73, v73, v117 neg_lo:[0,1] neg_hi:[0,1]
	v_exp_f16_sdwa v118, v70 dst_sel:WORD_0 dst_unused:UNUSED_PAD src0_sel:WORD_0
	v_exp_f16_sdwa v119, v71 dst_sel:WORD_0 dst_unused:UNUSED_PAD src0_sel:WORD_0
	v_exp_f16_sdwa v120, v72 dst_sel:WORD_0 dst_unused:UNUSED_PAD src0_sel:WORD_0
	v_exp_f16_sdwa v121, v73 dst_sel:WORD_0 dst_unused:UNUSED_PAD src0_sel:WORD_0
	v_exp_f16_sdwa v118, v70 dst_sel:WORD_1 dst_unused:UNUSED_PRESERVE src0_sel:WORD_1
	v_exp_f16_sdwa v119, v71 dst_sel:WORD_1 dst_unused:UNUSED_PRESERVE src0_sel:WORD_1
	v_exp_f16_sdwa v120, v72 dst_sel:WORD_1 dst_unused:UNUSED_PRESERVE src0_sel:WORD_1
	v_exp_f16_sdwa v121, v73 dst_sel:WORD_1 dst_unused:UNUSED_PRESERVE src0_sel:WORD_1
	v_pk_add_f16 v57, v57, v118
	v_pk_fma_f16 v25, v37, v121, v25
	v_pk_add_f16 v37, v49, v117 neg_lo:[0,1] neg_hi:[0,1]
	v_pk_add_f16 v56, v56, v119
	v_pk_add_f16 v55, v55, v120
	v_pk_add_f16 v54, v54, v121
	v_pk_fma_f16 v22, v34, v118, v22
	v_pk_fma_f16 v23, v35, v119, v23
	v_pk_fma_f16 v24, v36, v120, v24
	v_pk_add_f16 v34, v46, v114 neg_lo:[0,1] neg_hi:[0,1]
	v_pk_add_f16 v35, v47, v115 neg_lo:[0,1] neg_hi:[0,1]
	v_pk_add_f16 v36, v48, v116 neg_lo:[0,1] neg_hi:[0,1]
	v_exp_f16_sdwa v46, v34 dst_sel:WORD_0 dst_unused:UNUSED_PAD src0_sel:WORD_0
	v_exp_f16_sdwa v47, v35 dst_sel:WORD_0 dst_unused:UNUSED_PAD src0_sel:WORD_0
	v_exp_f16_sdwa v48, v36 dst_sel:WORD_0 dst_unused:UNUSED_PAD src0_sel:WORD_0
	v_exp_f16_sdwa v49, v37 dst_sel:WORD_0 dst_unused:UNUSED_PAD src0_sel:WORD_0
	v_exp_f16_sdwa v46, v34 dst_sel:WORD_1 dst_unused:UNUSED_PRESERVE src0_sel:WORD_1
	v_exp_f16_sdwa v47, v35 dst_sel:WORD_1 dst_unused:UNUSED_PRESERVE src0_sel:WORD_1
	v_exp_f16_sdwa v48, v36 dst_sel:WORD_1 dst_unused:UNUSED_PRESERVE src0_sel:WORD_1
	v_exp_f16_sdwa v49, v37 dst_sel:WORD_1 dst_unused:UNUSED_PRESERVE src0_sel:WORD_1
	v_pk_add_f16 v37, v57, v46
	v_pk_add_f16 v34, v54, v49
	v_pk_add_f16 v35, v55, v48
	v_pk_add_f16 v36, v56, v47
	v_pk_fma_f16 v25, v53, v49, v25
	v_pk_fma_f16 v24, v52, v48, v24
	v_pk_fma_f16 v23, v51, v47, v23
	v_pk_fma_f16 v22, v50, v46, v22
	v_pk_add_f16 v46, v93, v114 neg_lo:[0,1] neg_hi:[0,1]
	v_pk_add_f16 v47, v92, v115 neg_lo:[0,1] neg_hi:[0,1]
	v_pk_add_f16 v48, v91, v116 neg_lo:[0,1] neg_hi:[0,1]
	v_pk_add_f16 v49, v90, v117 neg_lo:[0,1] neg_hi:[0,1]
	v_exp_f16_sdwa v50, v46 dst_sel:WORD_0 dst_unused:UNUSED_PAD src0_sel:WORD_0
	v_exp_f16_sdwa v51, v47 dst_sel:WORD_0 dst_unused:UNUSED_PAD src0_sel:WORD_0
	v_exp_f16_sdwa v52, v48 dst_sel:WORD_0 dst_unused:UNUSED_PAD src0_sel:WORD_0
	v_exp_f16_sdwa v53, v49 dst_sel:WORD_0 dst_unused:UNUSED_PAD src0_sel:WORD_0
	v_exp_f16_sdwa v50, v46 dst_sel:WORD_1 dst_unused:UNUSED_PRESERVE src0_sel:WORD_1
	v_exp_f16_sdwa v51, v47 dst_sel:WORD_1 dst_unused:UNUSED_PRESERVE src0_sel:WORD_1
	v_exp_f16_sdwa v52, v48 dst_sel:WORD_1 dst_unused:UNUSED_PRESERVE src0_sel:WORD_1
	v_exp_f16_sdwa v53, v49 dst_sel:WORD_1 dst_unused:UNUSED_PRESERVE src0_sel:WORD_1
	v_pk_add_f16 v46, v97, v114 neg_lo:[0,1] neg_hi:[0,1]
	v_pk_add_f16 v37, v37, v50
	v_pk_add_f16 v36, v36, v51
	v_pk_add_f16 v35, v35, v52
	v_pk_add_f16 v34, v34, v53
	v_pk_fma_f16 v22, v10, v50, v22
	v_pk_fma_f16 v23, v11, v51, v23
	v_pk_fma_f16 v24, v12, v52, v24
	v_pk_fma_f16 v25, v13, v53, v25
	v_pk_add_f16 v47, v96, v115 neg_lo:[0,1] neg_hi:[0,1]
	v_pk_add_f16 v48, v95, v116 neg_lo:[0,1] neg_hi:[0,1]
	v_pk_add_f16 v49, v94, v117 neg_lo:[0,1] neg_hi:[0,1]
	v_exp_f16_sdwa v50, v46 dst_sel:WORD_0 dst_unused:UNUSED_PAD src0_sel:WORD_0
	v_exp_f16_sdwa v51, v47 dst_sel:WORD_0 dst_unused:UNUSED_PAD src0_sel:WORD_0
	v_exp_f16_sdwa v52, v48 dst_sel:WORD_0 dst_unused:UNUSED_PAD src0_sel:WORD_0
	v_exp_f16_sdwa v53, v49 dst_sel:WORD_0 dst_unused:UNUSED_PAD src0_sel:WORD_0
	v_exp_f16_sdwa v50, v46 dst_sel:WORD_1 dst_unused:UNUSED_PRESERVE src0_sel:WORD_1
	v_exp_f16_sdwa v51, v47 dst_sel:WORD_1 dst_unused:UNUSED_PRESERVE src0_sel:WORD_1
	v_exp_f16_sdwa v52, v48 dst_sel:WORD_1 dst_unused:UNUSED_PRESERVE src0_sel:WORD_1
	v_exp_f16_sdwa v53, v49 dst_sel:WORD_1 dst_unused:UNUSED_PRESERVE src0_sel:WORD_1
	v_pk_add_f16 v46, v66, v114 neg_lo:[0,1] neg_hi:[0,1]
	v_pk_add_f16 v37, v37, v50
	v_pk_add_f16 v34, v34, v53
	v_pk_add_f16 v35, v35, v52
	v_pk_add_f16 v36, v36, v51
	v_pk_fma_f16 v25, v17, v53, v25
	v_pk_fma_f16 v24, v16, v52, v24
	v_pk_fma_f16 v23, v15, v51, v23
	v_pk_fma_f16 v22, v14, v50, v22
	v_pk_add_f16 v47, v67, v115 neg_lo:[0,1] neg_hi:[0,1]
	v_pk_add_f16 v48, v68, v116 neg_lo:[0,1] neg_hi:[0,1]
	v_pk_add_f16 v49, v69, v117 neg_lo:[0,1] neg_hi:[0,1]
	v_exp_f16_sdwa v50, v46 dst_sel:WORD_0 dst_unused:UNUSED_PAD src0_sel:WORD_0
	v_exp_f16_sdwa v51, v47 dst_sel:WORD_0 dst_unused:UNUSED_PAD src0_sel:WORD_0
	v_exp_f16_sdwa v52, v48 dst_sel:WORD_0 dst_unused:UNUSED_PAD src0_sel:WORD_0
	v_exp_f16_sdwa v53, v49 dst_sel:WORD_0 dst_unused:UNUSED_PAD src0_sel:WORD_0
	v_exp_f16_sdwa v50, v46 dst_sel:WORD_1 dst_unused:UNUSED_PRESERVE src0_sel:WORD_1
	v_exp_f16_sdwa v51, v47 dst_sel:WORD_1 dst_unused:UNUSED_PRESERVE src0_sel:WORD_1
	v_exp_f16_sdwa v52, v48 dst_sel:WORD_1 dst_unused:UNUSED_PRESERVE src0_sel:WORD_1
	v_exp_f16_sdwa v53, v49 dst_sel:WORD_1 dst_unused:UNUSED_PRESERVE src0_sel:WORD_1
	v_pk_add_f16 v46, v101, v114 neg_lo:[0,1] neg_hi:[0,1]
	v_pk_add_f16 v37, v37, v50
	v_pk_add_f16 v36, v36, v51
	v_pk_add_f16 v35, v35, v52
	v_pk_add_f16 v34, v34, v53
	v_pk_fma_f16 v22, v18, v50, v22
	v_pk_fma_f16 v23, v19, v51, v23
	v_pk_fma_f16 v24, v20, v52, v24
	v_pk_fma_f16 v25, v21, v53, v25
	v_pk_add_f16 v47, v100, v115 neg_lo:[0,1] neg_hi:[0,1]
	v_pk_add_f16 v48, v99, v116 neg_lo:[0,1] neg_hi:[0,1]
	v_pk_add_f16 v49, v98, v117 neg_lo:[0,1] neg_hi:[0,1]
	v_exp_f16_sdwa v50, v46 dst_sel:WORD_0 dst_unused:UNUSED_PAD src0_sel:WORD_0
	v_exp_f16_sdwa v51, v47 dst_sel:WORD_0 dst_unused:UNUSED_PAD src0_sel:WORD_0
	v_exp_f16_sdwa v52, v48 dst_sel:WORD_0 dst_unused:UNUSED_PAD src0_sel:WORD_0
	v_exp_f16_sdwa v53, v49 dst_sel:WORD_0 dst_unused:UNUSED_PAD src0_sel:WORD_0
	v_exp_f16_sdwa v50, v46 dst_sel:WORD_1 dst_unused:UNUSED_PRESERVE src0_sel:WORD_1
	v_exp_f16_sdwa v51, v47 dst_sel:WORD_1 dst_unused:UNUSED_PRESERVE src0_sel:WORD_1
	v_exp_f16_sdwa v52, v48 dst_sel:WORD_1 dst_unused:UNUSED_PRESERVE src0_sel:WORD_1
	v_exp_f16_sdwa v53, v49 dst_sel:WORD_1 dst_unused:UNUSED_PRESERVE src0_sel:WORD_1
	v_pk_add_f16 v46, v113, v114 neg_lo:[0,1] neg_hi:[0,1]
	v_pk_add_f16 v37, v37, v50
	v_pk_add_f16 v34, v34, v53
	v_pk_add_f16 v35, v35, v52
	v_pk_add_f16 v36, v36, v51
	v_pk_fma_f16 v25, v33, v53, v25
	v_pk_fma_f16 v24, v32, v52, v24
	v_pk_fma_f16 v23, v31, v51, v23
	v_pk_fma_f16 v22, v30, v50, v22
	v_pk_add_f16 v47, v112, v115 neg_lo:[0,1] neg_hi:[0,1]
	v_pk_add_f16 v48, v111, v116 neg_lo:[0,1] neg_hi:[0,1]
	v_pk_add_f16 v49, v110, v117 neg_lo:[0,1] neg_hi:[0,1]
	v_exp_f16_sdwa v50, v46 dst_sel:WORD_0 dst_unused:UNUSED_PAD src0_sel:WORD_0
	v_exp_f16_sdwa v51, v47 dst_sel:WORD_0 dst_unused:UNUSED_PAD src0_sel:WORD_0
	v_exp_f16_sdwa v52, v48 dst_sel:WORD_0 dst_unused:UNUSED_PAD src0_sel:WORD_0
	v_exp_f16_sdwa v53, v49 dst_sel:WORD_0 dst_unused:UNUSED_PAD src0_sel:WORD_0
	v_exp_f16_sdwa v50, v46 dst_sel:WORD_1 dst_unused:UNUSED_PRESERVE src0_sel:WORD_1
	v_exp_f16_sdwa v51, v47 dst_sel:WORD_1 dst_unused:UNUSED_PRESERVE src0_sel:WORD_1
	v_exp_f16_sdwa v52, v48 dst_sel:WORD_1 dst_unused:UNUSED_PRESERVE src0_sel:WORD_1
	v_exp_f16_sdwa v53, v49 dst_sel:WORD_1 dst_unused:UNUSED_PRESERVE src0_sel:WORD_1
	v_pk_add_f16 v46, v86, v114 neg_lo:[0,1] neg_hi:[0,1]
	v_pk_add_f16 v37, v37, v50
	v_pk_add_f16 v36, v36, v51
	v_pk_add_f16 v35, v35, v52
	v_pk_add_f16 v34, v34, v53
	v_pk_fma_f16 v22, v42, v50, v22
	v_pk_fma_f16 v23, v43, v51, v23
	v_pk_fma_f16 v24, v44, v52, v24
	v_pk_fma_f16 v25, v45, v53, v25
	v_pk_add_f16 v47, v87, v115 neg_lo:[0,1] neg_hi:[0,1]
	v_pk_add_f16 v48, v88, v116 neg_lo:[0,1] neg_hi:[0,1]
	v_pk_add_f16 v49, v89, v117 neg_lo:[0,1] neg_hi:[0,1]
	v_exp_f16_sdwa v50, v46 dst_sel:WORD_0 dst_unused:UNUSED_PAD src0_sel:WORD_0
	v_exp_f16_sdwa v51, v47 dst_sel:WORD_0 dst_unused:UNUSED_PAD src0_sel:WORD_0
	v_exp_f16_sdwa v52, v48 dst_sel:WORD_0 dst_unused:UNUSED_PAD src0_sel:WORD_0
	v_exp_f16_sdwa v53, v49 dst_sel:WORD_0 dst_unused:UNUSED_PAD src0_sel:WORD_0
	v_exp_f16_sdwa v50, v46 dst_sel:WORD_1 dst_unused:UNUSED_PRESERVE src0_sel:WORD_1
	v_exp_f16_sdwa v51, v47 dst_sel:WORD_1 dst_unused:UNUSED_PRESERVE src0_sel:WORD_1
	v_exp_f16_sdwa v52, v48 dst_sel:WORD_1 dst_unused:UNUSED_PRESERVE src0_sel:WORD_1
	v_exp_f16_sdwa v53, v49 dst_sel:WORD_1 dst_unused:UNUSED_PRESERVE src0_sel:WORD_1
	v_pk_add_f16 v37, v37, v50
	v_pk_add_f16 v36, v36, v51
	v_rcp_f16_e32 v46, v37
	v_rcp_f16_sdwa v37, v37 dst_sel:DWORD dst_unused:UNUSED_PAD src0_sel:WORD_1
	v_pk_add_f16 v35, v35, v52
	v_rcp_f16_e32 v47, v36
	v_rcp_f16_sdwa v36, v36 dst_sel:DWORD dst_unused:UNUSED_PAD src0_sel:WORD_1
	v_pk_add_f16 v34, v34, v53
	v_rcp_f16_e32 v48, v35
	v_rcp_f16_sdwa v35, v35 dst_sel:DWORD dst_unused:UNUSED_PAD src0_sel:WORD_1
	v_rcp_f16_e32 v49, v34
	v_rcp_f16_sdwa v34, v34 dst_sel:DWORD dst_unused:UNUSED_PAD src0_sel:WORD_1
	v_pk_fma_f16 v22, v62, v50, v22
	v_pack_b32_f16 v37, v46, v37
	v_pk_fma_f16 v23, v63, v51, v23
	v_pk_mul_f16 v57, v22, v37
	v_pack_b32_f16 v22, v47, v36
	v_pk_fma_f16 v24, v64, v52, v24
	v_pk_mul_f16 v56, v23, v22
	v_pack_b32_f16 v22, v48, v35
	v_pk_fma_f16 v25, v65, v53, v25
	v_pk_mul_f16 v55, v24, v22
	v_pack_b32_f16 v22, v49, v34
	v_pk_mul_f16 v54, v25, v22
	s_waitcnt vmcnt(0)
	v_pk_mul_f16 v22, v160, v146 op_sel_hi:[0,1]
	v_pk_mul_f16 v23, v160, v147 op_sel_hi:[0,1]
	v_pk_mul_f16 v24, v160, v148 op_sel_hi:[0,1]
	v_pk_mul_f16 v25, v160, v149 op_sel_hi:[0,1]
	v_pk_mul_f16 v46, v159, v146 op_sel_hi:[0,1]
	v_pk_mul_f16 v47, v159, v147 op_sel_hi:[0,1]
	v_pk_mul_f16 v48, v159, v148 op_sel_hi:[0,1]
	v_pk_mul_f16 v49, v159, v149 op_sel_hi:[0,1]
	v_pk_mul_f16 v34, v158, v146 op_sel_hi:[0,1]
	v_pk_mul_f16 v35, v158, v147 op_sel_hi:[0,1]
	v_pk_mul_f16 v36, v158, v148 op_sel_hi:[0,1]
	v_pk_mul_f16 v37, v158, v149 op_sel_hi:[0,1]
	v_pk_fma_f16 v29, v29, v149, v25
	v_pk_fma_f16 v28, v28, v148, v24
	v_pk_fma_f16 v27, v27, v147, v23
	v_pk_fma_f16 v26, v26, v146, v22
	v_pk_fma_f16 v41, v41, v149, v25
	v_pk_fma_f16 v40, v40, v148, v24
	v_pk_fma_f16 v39, v39, v147, v23
	v_pk_fma_f16 v38, v38, v146, v22
	v_pk_fma_f16 v25, v61, v149, v25
	v_pk_fma_f16 v24, v60, v148, v24
	v_pk_fma_f16 v23, v59, v147, v23
	v_pk_fma_f16 v22, v58, v146, v22
	v_pk_fma_f16 v66, v137, v149, v49
	v_pk_fma_f16 v67, v136, v148, v48
	v_pk_fma_f16 v68, v135, v147, v47
	v_pk_fma_f16 v69, v134, v146, v46
	v_pk_fma_f16 v70, v145, v149, v49
	v_pk_fma_f16 v71, v144, v148, v48
	v_pk_fma_f16 v72, v143, v147, v47
	v_pk_fma_f16 v73, v142, v146, v46
	v_pk_fma_f16 v9, v9, v149, v49
	v_pk_fma_f16 v8, v8, v148, v48
	v_pk_fma_f16 v7, v7, v147, v47
	v_pk_fma_f16 v6, v6, v146, v46
	v_pk_maximum3_f16 v46, v26, v38, v22
	v_pk_maximum3_f16 v47, v27, v39, v23
	v_pk_maximum3_f16 v48, v28, v40, v24
	v_pk_maximum3_f16 v49, v29, v41, v25
	v_pk_fma_f16 v50, v81, v149, v37
	v_pk_fma_f16 v51, v80, v148, v36
	v_pk_fma_f16 v52, v79, v147, v35
	v_pk_fma_f16 v53, v78, v146, v34
	v_pk_fma_f16 v58, v109, v149, v37
	v_pk_fma_f16 v59, v108, v148, v36
	v_pk_fma_f16 v60, v107, v147, v35
	v_pk_fma_f16 v61, v106, v146, v34
	v_pk_fma_f16 v37, v125, v149, v37
	v_pk_fma_f16 v36, v124, v148, v36
	v_pk_fma_f16 v35, v123, v147, v35
	v_pk_fma_f16 v34, v122, v146, v34
	v_pk_maximum3_f16 v79, v52, v60, v35
	v_pk_maximum3_f16 v80, v51, v59, v36
	v_pk_maximum3_f16 v81, v50, v58, v37
	v_pk_maximum3_f16 v86, v69, v73, v6
	v_pk_maximum3_f16 v87, v68, v72, v7
	v_pk_maximum3_f16 v78, v53, v61, v34
	v_pk_maximum3_f16 v88, v67, v71, v8
	v_pk_maximum3_f16 v89, v66, v70, v9
	v_pk_maximum3_f16 v46, v46, v78, v86
	v_pk_maximum3_f16 v47, v47, v79, v87
	v_pk_maximum3_f16 v48, v48, v80, v88
	v_pk_maximum3_f16 v49, v49, v81, v89
	s_nop 0
	v_pk_add_f16 v26, v26, v46 neg_lo:[0,1] neg_hi:[0,1]
	v_pk_add_f16 v27, v27, v47 neg_lo:[0,1] neg_hi:[0,1]
	v_pk_add_f16 v28, v28, v48 neg_lo:[0,1] neg_hi:[0,1]
	v_pk_add_f16 v29, v29, v49 neg_lo:[0,1] neg_hi:[0,1]
	v_pk_add_f16 v38, v38, v46 neg_lo:[0,1] neg_hi:[0,1]
	v_exp_f16_sdwa v78, v26 dst_sel:WORD_0 dst_unused:UNUSED_PAD src0_sel:WORD_0
	v_exp_f16_sdwa v79, v27 dst_sel:WORD_0 dst_unused:UNUSED_PAD src0_sel:WORD_0
	v_exp_f16_sdwa v80, v28 dst_sel:WORD_0 dst_unused:UNUSED_PAD src0_sel:WORD_0
	v_exp_f16_sdwa v81, v29 dst_sel:WORD_0 dst_unused:UNUSED_PAD src0_sel:WORD_0
	v_exp_f16_sdwa v78, v26 dst_sel:WORD_1 dst_unused:UNUSED_PRESERVE src0_sel:WORD_1
	v_exp_f16_sdwa v79, v27 dst_sel:WORD_1 dst_unused:UNUSED_PRESERVE src0_sel:WORD_1
	v_exp_f16_sdwa v80, v28 dst_sel:WORD_1 dst_unused:UNUSED_PRESERVE src0_sel:WORD_1
	v_exp_f16_sdwa v81, v29 dst_sel:WORD_1 dst_unused:UNUSED_PRESERVE src0_sel:WORD_1
	v_pk_add_f16 v39, v39, v47 neg_lo:[0,1] neg_hi:[0,1]
	v_pk_add_f16 v26, v78, 0
	v_pk_add_f16 v27, v79, 0
	v_pk_add_f16 v28, v80, 0
	v_pk_add_f16 v29, v81, 0
	v_pk_fma_f16 v10, v10, v78, 0
	v_pk_fma_f16 v11, v11, v79, 0
	v_pk_fma_f16 v12, v12, v80, 0
	v_pk_fma_f16 v13, v13, v81, 0
	v_pk_add_f16 v40, v40, v48 neg_lo:[0,1] neg_hi:[0,1]
	v_pk_add_f16 v41, v41, v49 neg_lo:[0,1] neg_hi:[0,1]
	v_pk_add_f16 v6, v6, v46 neg_lo:[0,1] neg_hi:[0,1]
	v_exp_f16_sdwa v78, v38 dst_sel:WORD_0 dst_unused:UNUSED_PAD src0_sel:WORD_0
	v_exp_f16_sdwa v79, v39 dst_sel:WORD_0 dst_unused:UNUSED_PAD src0_sel:WORD_0
	v_exp_f16_sdwa v80, v40 dst_sel:WORD_0 dst_unused:UNUSED_PAD src0_sel:WORD_0
	v_exp_f16_sdwa v81, v41 dst_sel:WORD_0 dst_unused:UNUSED_PAD src0_sel:WORD_0
	v_exp_f16_sdwa v78, v38 dst_sel:WORD_1 dst_unused:UNUSED_PRESERVE src0_sel:WORD_1
	v_exp_f16_sdwa v79, v39 dst_sel:WORD_1 dst_unused:UNUSED_PRESERVE src0_sel:WORD_1
	v_exp_f16_sdwa v80, v40 dst_sel:WORD_1 dst_unused:UNUSED_PRESERVE src0_sel:WORD_1
	v_exp_f16_sdwa v81, v41 dst_sel:WORD_1 dst_unused:UNUSED_PRESERVE src0_sel:WORD_1
	v_pk_add_f16 v7, v7, v47 neg_lo:[0,1] neg_hi:[0,1]
	v_pk_add_f16 v29, v29, v81
	v_pk_add_f16 v28, v28, v80
	v_pk_add_f16 v27, v27, v79
	v_pk_add_f16 v26, v26, v78
	v_pk_fma_f16 v13, v17, v81, v13
	v_pk_fma_f16 v12, v16, v80, v12
	v_pk_fma_f16 v11, v15, v79, v11
	v_pk_fma_f16 v10, v14, v78, v10
	v_pk_add_f16 v14, v22, v46 neg_lo:[0,1] neg_hi:[0,1]
	v_pk_add_f16 v15, v23, v47 neg_lo:[0,1] neg_hi:[0,1]
	v_pk_add_f16 v16, v24, v48 neg_lo:[0,1] neg_hi:[0,1]
	v_pk_add_f16 v17, v25, v49 neg_lo:[0,1] neg_hi:[0,1]
	v_pk_add_f16 v8, v8, v48 neg_lo:[0,1] neg_hi:[0,1]
	v_exp_f16_sdwa v22, v14 dst_sel:WORD_0 dst_unused:UNUSED_PAD src0_sel:WORD_0
	v_exp_f16_sdwa v23, v15 dst_sel:WORD_0 dst_unused:UNUSED_PAD src0_sel:WORD_0
	v_exp_f16_sdwa v24, v16 dst_sel:WORD_0 dst_unused:UNUSED_PAD src0_sel:WORD_0
	v_exp_f16_sdwa v25, v17 dst_sel:WORD_0 dst_unused:UNUSED_PAD src0_sel:WORD_0
	v_exp_f16_sdwa v22, v14 dst_sel:WORD_1 dst_unused:UNUSED_PRESERVE src0_sel:WORD_1
	v_exp_f16_sdwa v23, v15 dst_sel:WORD_1 dst_unused:UNUSED_PRESERVE src0_sel:WORD_1
	v_exp_f16_sdwa v24, v16 dst_sel:WORD_1 dst_unused:UNUSED_PRESERVE src0_sel:WORD_1
	v_exp_f16_sdwa v25, v17 dst_sel:WORD_1 dst_unused:UNUSED_PRESERVE src0_sel:WORD_1
	v_pk_add_f16 v9, v9, v49 neg_lo:[0,1] neg_hi:[0,1]
	v_pk_add_f16 v14, v26, v22
	v_pk_add_f16 v15, v27, v23
	v_pk_add_f16 v16, v28, v24
	v_pk_add_f16 v17, v29, v25
	v_pk_fma_f16 v10, v18, v22, v10
	v_pk_fma_f16 v11, v19, v23, v11
	v_pk_fma_f16 v12, v20, v24, v12
	v_pk_fma_f16 v13, v21, v25, v13
	v_pk_add_f16 v18, v53, v46 neg_lo:[0,1] neg_hi:[0,1]
	v_pk_add_f16 v19, v52, v47 neg_lo:[0,1] neg_hi:[0,1]
	v_pk_add_f16 v20, v51, v48 neg_lo:[0,1] neg_hi:[0,1]
	v_pk_add_f16 v21, v50, v49 neg_lo:[0,1] neg_hi:[0,1]
	v_exp_f16_sdwa v22, v18 dst_sel:WORD_0 dst_unused:UNUSED_PAD src0_sel:WORD_0
	v_exp_f16_sdwa v23, v19 dst_sel:WORD_0 dst_unused:UNUSED_PAD src0_sel:WORD_0
	v_exp_f16_sdwa v24, v20 dst_sel:WORD_0 dst_unused:UNUSED_PAD src0_sel:WORD_0
	v_exp_f16_sdwa v25, v21 dst_sel:WORD_0 dst_unused:UNUSED_PAD src0_sel:WORD_0
	v_exp_f16_sdwa v22, v18 dst_sel:WORD_1 dst_unused:UNUSED_PRESERVE src0_sel:WORD_1
	v_exp_f16_sdwa v23, v19 dst_sel:WORD_1 dst_unused:UNUSED_PRESERVE src0_sel:WORD_1
	v_exp_f16_sdwa v24, v20 dst_sel:WORD_1 dst_unused:UNUSED_PRESERVE src0_sel:WORD_1
	v_exp_f16_sdwa v25, v21 dst_sel:WORD_1 dst_unused:UNUSED_PRESERVE src0_sel:WORD_1
	v_pk_add_f16 v18, v61, v46 neg_lo:[0,1] neg_hi:[0,1]
	v_pk_add_f16 v17, v17, v25
	v_pk_add_f16 v16, v16, v24
	v_pk_add_f16 v15, v15, v23
	v_pk_add_f16 v14, v14, v22
	v_pk_fma_f16 v13, v33, v25, v13
	v_pk_fma_f16 v12, v32, v24, v12
	v_pk_fma_f16 v11, v31, v23, v11
	v_pk_fma_f16 v10, v30, v22, v10
	v_pk_add_f16 v19, v60, v47 neg_lo:[0,1] neg_hi:[0,1]
	v_pk_add_f16 v20, v59, v48 neg_lo:[0,1] neg_hi:[0,1]
	v_pk_add_f16 v21, v58, v49 neg_lo:[0,1] neg_hi:[0,1]
	v_exp_f16_sdwa v30, v6 dst_sel:WORD_0 dst_unused:UNUSED_PAD src0_sel:WORD_0
	v_exp_f16_sdwa v31, v7 dst_sel:WORD_0 dst_unused:UNUSED_PAD src0_sel:WORD_0
	v_exp_f16_sdwa v32, v8 dst_sel:WORD_0 dst_unused:UNUSED_PAD src0_sel:WORD_0
	v_exp_f16_sdwa v33, v9 dst_sel:WORD_0 dst_unused:UNUSED_PAD src0_sel:WORD_0
	v_exp_f16_sdwa v30, v6 dst_sel:WORD_1 dst_unused:UNUSED_PRESERVE src0_sel:WORD_1
	v_exp_f16_sdwa v31, v7 dst_sel:WORD_1 dst_unused:UNUSED_PRESERVE src0_sel:WORD_1
	v_exp_f16_sdwa v32, v8 dst_sel:WORD_1 dst_unused:UNUSED_PRESERVE src0_sel:WORD_1
	v_exp_f16_sdwa v33, v9 dst_sel:WORD_1 dst_unused:UNUSED_PRESERVE src0_sel:WORD_1
	v_exp_f16_sdwa v22, v18 dst_sel:WORD_0 dst_unused:UNUSED_PAD src0_sel:WORD_0
	v_exp_f16_sdwa v23, v19 dst_sel:WORD_0 dst_unused:UNUSED_PAD src0_sel:WORD_0
	v_exp_f16_sdwa v24, v20 dst_sel:WORD_0 dst_unused:UNUSED_PAD src0_sel:WORD_0
	v_exp_f16_sdwa v25, v21 dst_sel:WORD_0 dst_unused:UNUSED_PAD src0_sel:WORD_0
	v_exp_f16_sdwa v22, v18 dst_sel:WORD_1 dst_unused:UNUSED_PRESERVE src0_sel:WORD_1
	v_exp_f16_sdwa v23, v19 dst_sel:WORD_1 dst_unused:UNUSED_PRESERVE src0_sel:WORD_1
	v_exp_f16_sdwa v24, v20 dst_sel:WORD_1 dst_unused:UNUSED_PRESERVE src0_sel:WORD_1
	v_exp_f16_sdwa v25, v21 dst_sel:WORD_1 dst_unused:UNUSED_PRESERVE src0_sel:WORD_1
	v_pk_add_f16 v18, v34, v46 neg_lo:[0,1] neg_hi:[0,1]
	v_pk_add_f16 v14, v14, v22
	v_pk_add_f16 v15, v15, v23
	v_pk_add_f16 v16, v16, v24
	v_pk_add_f16 v17, v17, v25
	v_pk_fma_f16 v10, v42, v22, v10
	v_pk_fma_f16 v11, v43, v23, v11
	v_pk_fma_f16 v12, v44, v24, v12
	v_pk_fma_f16 v13, v45, v25, v13
	v_pk_add_f16 v19, v35, v47 neg_lo:[0,1] neg_hi:[0,1]
	v_pk_add_f16 v20, v36, v48 neg_lo:[0,1] neg_hi:[0,1]
	v_pk_add_f16 v21, v37, v49 neg_lo:[0,1] neg_hi:[0,1]
	v_exp_f16_sdwa v22, v18 dst_sel:WORD_0 dst_unused:UNUSED_PAD src0_sel:WORD_0
	v_exp_f16_sdwa v23, v19 dst_sel:WORD_0 dst_unused:UNUSED_PAD src0_sel:WORD_0
	v_exp_f16_sdwa v24, v20 dst_sel:WORD_0 dst_unused:UNUSED_PAD src0_sel:WORD_0
	v_exp_f16_sdwa v25, v21 dst_sel:WORD_0 dst_unused:UNUSED_PAD src0_sel:WORD_0
	v_exp_f16_sdwa v22, v18 dst_sel:WORD_1 dst_unused:UNUSED_PRESERVE src0_sel:WORD_1
	v_exp_f16_sdwa v23, v19 dst_sel:WORD_1 dst_unused:UNUSED_PRESERVE src0_sel:WORD_1
	v_exp_f16_sdwa v24, v20 dst_sel:WORD_1 dst_unused:UNUSED_PRESERVE src0_sel:WORD_1
	v_exp_f16_sdwa v25, v21 dst_sel:WORD_1 dst_unused:UNUSED_PRESERVE src0_sel:WORD_1
	v_pk_add_f16 v18, v69, v46 neg_lo:[0,1] neg_hi:[0,1]
	v_pk_add_f16 v17, v17, v25
	v_pk_add_f16 v16, v16, v24
	v_pk_add_f16 v15, v15, v23
	v_pk_add_f16 v14, v14, v22
	v_pk_fma_f16 v13, v65, v25, v13
	v_pk_fma_f16 v12, v64, v24, v12
	v_pk_fma_f16 v11, v63, v23, v11
	v_pk_fma_f16 v10, v62, v22, v10
	v_pk_add_f16 v19, v68, v47 neg_lo:[0,1] neg_hi:[0,1]
	v_pk_add_f16 v20, v67, v48 neg_lo:[0,1] neg_hi:[0,1]
	v_pk_add_f16 v21, v66, v49 neg_lo:[0,1] neg_hi:[0,1]
	v_exp_f16_sdwa v22, v18 dst_sel:WORD_0 dst_unused:UNUSED_PAD src0_sel:WORD_0
	v_exp_f16_sdwa v23, v19 dst_sel:WORD_0 dst_unused:UNUSED_PAD src0_sel:WORD_0
	v_exp_f16_sdwa v24, v20 dst_sel:WORD_0 dst_unused:UNUSED_PAD src0_sel:WORD_0
	v_exp_f16_sdwa v25, v21 dst_sel:WORD_0 dst_unused:UNUSED_PAD src0_sel:WORD_0
	v_exp_f16_sdwa v22, v18 dst_sel:WORD_1 dst_unused:UNUSED_PRESERVE src0_sel:WORD_1
	v_exp_f16_sdwa v23, v19 dst_sel:WORD_1 dst_unused:UNUSED_PRESERVE src0_sel:WORD_1
	v_exp_f16_sdwa v24, v20 dst_sel:WORD_1 dst_unused:UNUSED_PRESERVE src0_sel:WORD_1
	v_exp_f16_sdwa v25, v21 dst_sel:WORD_1 dst_unused:UNUSED_PRESERVE src0_sel:WORD_1
	v_pk_add_f16 v18, v73, v46 neg_lo:[0,1] neg_hi:[0,1]
	v_pk_add_f16 v14, v14, v22
	v_pk_add_f16 v15, v15, v23
	v_pk_add_f16 v16, v16, v24
	v_pk_add_f16 v17, v17, v25
	v_pk_fma_f16 v10, v82, v22, v10
	v_pk_fma_f16 v11, v83, v23, v11
	v_pk_fma_f16 v12, v84, v24, v12
	v_pk_fma_f16 v13, v85, v25, v13
	v_pk_add_f16 v19, v72, v47 neg_lo:[0,1] neg_hi:[0,1]
	v_pk_add_f16 v20, v71, v48 neg_lo:[0,1] neg_hi:[0,1]
	v_pk_add_f16 v21, v70, v49 neg_lo:[0,1] neg_hi:[0,1]
	v_exp_f16_sdwa v22, v18 dst_sel:WORD_0 dst_unused:UNUSED_PAD src0_sel:WORD_0
	v_exp_f16_sdwa v23, v19 dst_sel:WORD_0 dst_unused:UNUSED_PAD src0_sel:WORD_0
	v_exp_f16_sdwa v24, v20 dst_sel:WORD_0 dst_unused:UNUSED_PAD src0_sel:WORD_0
	v_exp_f16_sdwa v25, v21 dst_sel:WORD_0 dst_unused:UNUSED_PAD src0_sel:WORD_0
	v_exp_f16_sdwa v22, v18 dst_sel:WORD_1 dst_unused:UNUSED_PRESERVE src0_sel:WORD_1
	v_exp_f16_sdwa v23, v19 dst_sel:WORD_1 dst_unused:UNUSED_PRESERVE src0_sel:WORD_1
	v_exp_f16_sdwa v24, v20 dst_sel:WORD_1 dst_unused:UNUSED_PRESERVE src0_sel:WORD_1
	v_exp_f16_sdwa v25, v21 dst_sel:WORD_1 dst_unused:UNUSED_PRESERVE src0_sel:WORD_1
	s_nop 0
	v_pk_add_f16 v17, v17, v25
	v_pk_add_f16 v16, v16, v24
	v_pk_add_f16 v15, v15, v23
	v_pk_add_f16 v14, v14, v22
	v_pk_fma_f16 v21, v105, v25, v13
	v_pk_fma_f16 v20, v104, v24, v12
	v_pk_fma_f16 v19, v103, v23, v11
	v_pk_fma_f16 v18, v102, v22, v10
	v_mov_b32_e32 v13, v5
	v_mov_b32_e32 v12, v4
	v_mov_b32_e32 v11, v3
	v_mov_b32_e32 v10, v2
.LBB4_80:
	v_lshlrev_b64 v[6:7], 9, v[168:169]
	v_or_b32_e32 v6, v6, v198
	v_lshl_add_u64 v[2:3], s[20:21], 0, v[6:7]
	global_load_dwordx4 v[2:5], v[2:3], off nt
	v_lshl_add_u64 v[6:7], s[22:23], 0, v[6:7]
	global_load_dwordx4 v[6:9], v[6:7], off nt
	v_add_u32_e32 v168, v185, v199
	v_lshlrev_b64 v[26:27], 9, v[168:169]
	v_or_b32_e32 v26, v26, v198
	v_lshl_add_u64 v[22:23], s[20:21], 0, v[26:27]
	global_load_dwordx4 v[22:25], v[22:23], off nt
	v_lshl_add_u64 v[26:27], s[22:23], 0, v[26:27]
	global_load_dwordx4 v[26:29], v[26:27], off nt
	v_pk_add_f16 v17, v17, v33
	v_pk_add_f16 v16, v16, v32
	v_pk_add_f16 v15, v15, v31
	v_pk_add_f16 v14, v14, v30
	v_pk_fma_f16 v42, v13, v33, v21
	v_pk_fma_f16 v43, v12, v32, v20
	v_rcp_f16_e32 v12, v14
	v_rcp_f16_sdwa v13, v14 dst_sel:DWORD dst_unused:UNUSED_PAD src0_sel:WORD_1
	v_rcp_f16_e32 v14, v15
	v_rcp_f16_sdwa v15, v15 dst_sel:DWORD dst_unused:UNUSED_PAD src0_sel:WORD_1
	v_rcp_f16_e32 v46, v16
	v_rcp_f16_sdwa v16, v16 dst_sel:DWORD dst_unused:UNUSED_PAD src0_sel:WORD_1
	v_rcp_f16_e32 v47, v17
	v_rcp_f16_sdwa v17, v17 dst_sel:DWORD dst_unused:UNUSED_PAD src0_sel:WORD_1
	v_add_u32_e32 v168, v187, v199
	v_pk_fma_f16 v44, v10, v30, v18
	v_pk_fma_f16 v45, v11, v31, v19
	v_lshlrev_b64 v[10:11], 9, v[168:169]
	v_or_b32_e32 v10, v10, v198
	v_lshl_add_u64 v[38:39], s[20:21], 0, v[10:11]
	v_lshl_add_u64 v[40:41], s[22:23], 0, v[10:11]
	v_pack_b32_f16 v48, v14, v15
	v_pack_b32_f16 v49, v12, v13
	v_pack_b32_f16 v46, v46, v16
	v_pack_b32_f16 v47, v47, v17
	global_load_dwordx4 v[10:13], v[38:39], off nt
	global_load_dwordx4 v[14:17], v[40:41], off nt
	v_cvt_f32_f16_sdwa v21, v139 dst_sel:DWORD dst_unused:UNUSED_PAD src0_sel:WORD_1
	v_cvt_f32_f16_e32 v20, v139
	v_cvt_f32_f16_sdwa v19, v138 dst_sel:DWORD dst_unused:UNUSED_PAD src0_sel:WORD_1
	v_cvt_f32_f16_e32 v18, v138
	v_cvt_f32_f16_sdwa v33, v141 dst_sel:DWORD dst_unused:UNUSED_PAD src0_sel:WORD_1
	v_cvt_f32_f16_e32 v32, v141
	v_pk_mul_f16 v58, v43, v46
	v_pk_mul_f16 v59, v42, v47
	v_cvt_f32_f16_sdwa v31, v140 dst_sel:DWORD dst_unused:UNUSED_PAD src0_sel:WORD_1
	v_cvt_f32_f16_e32 v30, v140
	v_pk_mul_f16 v52, v45, v48
	v_pk_mul_f16 v53, v44, v49
	v_add_u32_e32 v168, v190, v199
	v_lshlrev_b64 v[36:37], 9, v[168:169]
	v_or_b32_e32 v36, v36, v198
	v_lshl_or_b32 v50, s46, 6, v178
	v_lshlrev_b32_e32 v51, 9, v50
	v_add_u32_e32 v203, v184, v51
	v_cvt_f32_f16_sdwa v35, v77 dst_sel:DWORD dst_unused:UNUSED_PAD src0_sel:WORD_1
	v_cvt_f32_f16_e32 v34, v77
	v_add_lshl_u32 v202, v188, v50, 9
	s_mov_b64 s[4:5], -1
	s_and_b64 vcc, exec, s[26:27]
	s_waitcnt vmcnt(5)
	v_cvt_f32_f16_e32 v38, v2
	v_cvt_f32_f16_sdwa v39, v2 dst_sel:DWORD dst_unused:UNUSED_PAD src0_sel:WORD_1
	v_cvt_f32_f16_e32 v2, v3
	v_cvt_f32_f16_sdwa v3, v3 dst_sel:DWORD dst_unused:UNUSED_PAD src0_sel:WORD_1
	s_waitcnt vmcnt(4)
	v_cvt_f32_f16_e32 v40, v6
	v_cvt_f32_f16_sdwa v41, v6 dst_sel:DWORD dst_unused:UNUSED_PAD src0_sel:WORD_1
	v_cvt_f32_f16_e32 v6, v7
	v_cvt_f32_f16_sdwa v7, v7 dst_sel:DWORD dst_unused:UNUSED_PAD src0_sel:WORD_1
	v_cvt_f32_f16_e32 v42, v4
	v_cvt_f32_f16_sdwa v43, v4 dst_sel:DWORD dst_unused:UNUSED_PAD src0_sel:WORD_1
	v_cvt_f32_f16_e32 v4, v5
	v_cvt_f32_f16_sdwa v5, v5 dst_sel:DWORD dst_unused:UNUSED_PAD src0_sel:WORD_1
	v_cvt_f32_f16_e32 v44, v8
	v_cvt_f32_f16_sdwa v45, v8 dst_sel:DWORD dst_unused:UNUSED_PAD src0_sel:WORD_1
	v_cvt_f32_f16_e32 v8, v9
	v_cvt_f32_f16_sdwa v9, v9 dst_sel:DWORD dst_unused:UNUSED_PAD src0_sel:WORD_1
	v_pk_add_f32 v[2:3], v[20:21], v[2:3]
	v_pk_add_f32 v[18:19], v[18:19], v[38:39]
	v_pk_add_f32 v[4:5], v[32:33], v[4:5]
	v_pk_add_f32 v[6:7], v[2:3], v[6:7]
	v_pk_add_f32 v[20:21], v[30:31], v[42:43]
	v_pk_add_f32 v[18:19], v[18:19], v[40:41]
	v_pk_add_f32 v[8:9], v[4:5], v[8:9]
	v_cvt_pk_f16_f32 v3, v6, v7
	v_lshl_add_u64 v[6:7], s[20:21], 0, v[36:37]
	v_pk_add_f32 v[20:21], v[20:21], v[44:45]
	v_cvt_pk_f16_f32 v2, v18, v19
	v_cvt_pk_f16_f32 v5, v8, v9
	global_load_dwordx4 v[6:9], v[6:7], off nt
	v_lshl_add_u64 v[18:19], s[22:23], 0, v[36:37]
	v_cvt_pk_f16_f32 v4, v20, v21
	global_load_dwordx4 v[18:21], v[18:19], off nt
	s_waitcnt vmcnt(5)
	v_cvt_f32_f16_e32 v46, v22
	v_cvt_f32_f16_sdwa v47, v22 dst_sel:DWORD dst_unused:UNUSED_PAD src0_sel:WORD_1
	ds_write_b128 v203, v[2:5]
	v_cvt_f32_f16_sdwa v5, v76 dst_sel:DWORD dst_unused:UNUSED_PAD src0_sel:WORD_1
	v_cvt_f32_f16_e32 v4, v76
	v_cvt_f32_f16_e32 v22, v23
	v_cvt_f32_f16_sdwa v23, v23 dst_sel:DWORD dst_unused:UNUSED_PAD src0_sel:WORD_1
	s_waitcnt vmcnt(4)
	v_cvt_f32_f16_e32 v48, v26
	v_cvt_f32_f16_sdwa v49, v26 dst_sel:DWORD dst_unused:UNUSED_PAD src0_sel:WORD_1
	v_cvt_f32_f16_e32 v26, v27
	v_cvt_f32_f16_sdwa v27, v27 dst_sel:DWORD dst_unused:UNUSED_PAD src0_sel:WORD_1
	v_cvt_f32_f16_sdwa v31, v75 dst_sel:DWORD dst_unused:UNUSED_PAD src0_sel:WORD_1
	v_cvt_f32_f16_e32 v30, v75
	v_cvt_f32_f16_e32 v32, v24
	v_cvt_f32_f16_sdwa v33, v24 dst_sel:DWORD dst_unused:UNUSED_PAD src0_sel:WORD_1
	v_pk_add_f32 v[4:5], v[4:5], v[22:23]
	v_cvt_f32_f16_e32 v22, v28
	v_pk_add_f32 v[4:5], v[4:5], v[26:27]
	v_cvt_f32_f16_sdwa v23, v28 dst_sel:DWORD dst_unused:UNUSED_PAD src0_sel:WORD_1
	v_cvt_f32_f16_sdwa v27, v74 dst_sel:DWORD dst_unused:UNUSED_PAD src0_sel:WORD_1
	v_cvt_f32_f16_e32 v26, v74
	v_cvt_f32_f16_e32 v24, v25
	v_cvt_f32_f16_sdwa v25, v25 dst_sel:DWORD dst_unused:UNUSED_PAD src0_sel:WORD_1
	v_pk_add_f32 v[2:3], v[34:35], v[46:47]
	v_cvt_f32_f16_e32 v28, v29
	v_cvt_f32_f16_sdwa v29, v29 dst_sel:DWORD dst_unused:UNUSED_PAD src0_sel:WORD_1
	v_pk_add_f32 v[2:3], v[2:3], v[48:49]
	s_nop 0
	v_cvt_pk_f16_f32 v2, v2, v3
	v_cvt_pk_f16_f32 v3, v4, v5
	v_pk_add_f32 v[4:5], v[30:31], v[32:33]
	s_nop 0
	v_pk_add_f32 v[4:5], v[4:5], v[22:23]
	v_pk_add_f32 v[22:23], v[26:27], v[24:25]
	v_cvt_pk_f16_f32 v4, v4, v5
	v_pk_add_f32 v[22:23], v[22:23], v[28:29]
	s_waitcnt vmcnt(3)
	v_cvt_f32_f16_e32 v24, v10
	v_cvt_pk_f16_f32 v5, v22, v23
	v_add_u32_e32 v22, v186, v50
	v_lshlrev_b32_e32 v204, 9, v22
	v_bitop3_b32 v22, v22, v179, 15 bitop3:0x6c
	v_lshlrev_b32_e32 v205, 4, v22
	v_cvt_f32_f16_sdwa v25, v10 dst_sel:DWORD dst_unused:UNUSED_PAD src0_sel:WORD_1
	v_or_b32_e32 v10, v205, v204
	v_cvt_f32_f16_sdwa v23, v57 dst_sel:DWORD dst_unused:UNUSED_PAD src0_sel:WORD_1
	v_cvt_f32_f16_e32 v22, v57
	ds_write_b128 v10, v[2:5]
	v_cvt_f32_f16_sdwa v5, v56 dst_sel:DWORD dst_unused:UNUSED_PAD src0_sel:WORD_1
	v_cvt_f32_f16_e32 v4, v56
	v_cvt_f32_f16_e32 v10, v11
	v_cvt_f32_f16_sdwa v11, v11 dst_sel:DWORD dst_unused:UNUSED_PAD src0_sel:WORD_1
	s_waitcnt vmcnt(2)
	v_cvt_f32_f16_e32 v26, v14
	v_cvt_f32_f16_sdwa v27, v14 dst_sel:DWORD dst_unused:UNUSED_PAD src0_sel:WORD_1
	v_cvt_f32_f16_e32 v14, v15
	v_cvt_f32_f16_sdwa v15, v15 dst_sel:DWORD dst_unused:UNUSED_PAD src0_sel:WORD_1
	v_pk_add_f32 v[2:3], v[22:23], v[24:25]
	v_cvt_f32_f16_sdwa v23, v55 dst_sel:DWORD dst_unused:UNUSED_PAD src0_sel:WORD_1
	v_cvt_f32_f16_e32 v22, v55
	v_cvt_f32_f16_e32 v24, v12
	v_cvt_f32_f16_sdwa v25, v12 dst_sel:DWORD dst_unused:UNUSED_PAD src0_sel:WORD_1
	v_pk_add_f32 v[4:5], v[4:5], v[10:11]
	v_cvt_f32_f16_e32 v10, v16
	v_pk_add_f32 v[4:5], v[4:5], v[14:15]
	v_cvt_f32_f16_sdwa v11, v16 dst_sel:DWORD dst_unused:UNUSED_PAD src0_sel:WORD_1
	v_cvt_f32_f16_sdwa v15, v54 dst_sel:DWORD dst_unused:UNUSED_PAD src0_sel:WORD_1
	v_cvt_f32_f16_e32 v14, v54
	v_cvt_f32_f16_e32 v12, v13
	v_cvt_f32_f16_sdwa v13, v13 dst_sel:DWORD dst_unused:UNUSED_PAD src0_sel:WORD_1
	v_cvt_f32_f16_e32 v16, v17
	v_cvt_f32_f16_sdwa v17, v17 dst_sel:DWORD dst_unused:UNUSED_PAD src0_sel:WORD_1
	v_pk_add_f32 v[2:3], v[2:3], v[26:27]
	s_nop 0
	v_cvt_pk_f16_f32 v2, v2, v3
	v_cvt_pk_f16_f32 v3, v4, v5
	v_pk_add_f32 v[4:5], v[22:23], v[24:25]
	s_nop 0
	v_pk_add_f32 v[4:5], v[4:5], v[10:11]
	v_pk_add_f32 v[10:11], v[14:15], v[12:13]
	v_cvt_pk_f16_f32 v4, v4, v5
	v_pk_add_f32 v[10:11], v[10:11], v[16:17]
	s_waitcnt vmcnt(1)
	v_cvt_f32_f16_e32 v12, v6
	v_cvt_pk_f16_f32 v5, v10, v11
	v_cvt_f32_f16_e32 v10, v53
	v_cvt_f32_f16_sdwa v11, v53 dst_sel:DWORD dst_unused:UNUSED_PAD src0_sel:WORD_1
	v_cvt_f32_f16_sdwa v13, v6 dst_sel:DWORD dst_unused:UNUSED_PAD src0_sel:WORD_1
	s_waitcnt vmcnt(0)
	v_cvt_f32_f16_e32 v14, v18
	v_cvt_f32_f16_sdwa v15, v18 dst_sel:DWORD dst_unused:UNUSED_PAD src0_sel:WORD_1
	v_or_b32_e32 v6, v189, v202
	ds_write_b128 v6, v[2:5]
	v_cvt_f32_f16_e32 v4, v52
	v_cvt_f32_f16_sdwa v5, v52 dst_sel:DWORD dst_unused:UNUSED_PAD src0_sel:WORD_1
	v_cvt_f32_f16_e32 v6, v7
	v_cvt_f32_f16_sdwa v7, v7 dst_sel:DWORD dst_unused:UNUSED_PAD src0_sel:WORD_1
	v_pk_add_f32 v[2:3], v[10:11], v[12:13]
	v_cvt_f32_f16_e32 v10, v19
	v_cvt_f32_f16_sdwa v11, v19 dst_sel:DWORD dst_unused:UNUSED_PAD src0_sel:WORD_1
	v_pk_add_f32 v[2:3], v[2:3], v[14:15]
	v_cvt_f32_f16_e32 v12, v58
	v_cvt_f32_f16_sdwa v13, v58 dst_sel:DWORD dst_unused:UNUSED_PAD src0_sel:WORD_1
	v_cvt_f32_f16_e32 v14, v8
	v_cvt_f32_f16_sdwa v15, v8 dst_sel:DWORD dst_unused:UNUSED_PAD src0_sel:WORD_1
	v_pk_add_f32 v[4:5], v[4:5], v[6:7]
	v_cvt_f32_f16_e32 v6, v20
	v_pk_add_f32 v[4:5], v[4:5], v[10:11]
	v_cvt_f32_f16_sdwa v7, v20 dst_sel:DWORD dst_unused:UNUSED_PAD src0_sel:WORD_1
	v_cvt_f32_f16_e32 v10, v59
	v_cvt_f32_f16_sdwa v11, v59 dst_sel:DWORD dst_unused:UNUSED_PAD src0_sel:WORD_1
	v_cvt_f32_f16_e32 v8, v9
	v_cvt_f32_f16_sdwa v9, v9 dst_sel:DWORD dst_unused:UNUSED_PAD src0_sel:WORD_1
	v_cvt_pk_f16_f32 v2, v2, v3
	v_cvt_pk_f16_f32 v3, v4, v5
	v_pk_add_f32 v[4:5], v[12:13], v[14:15]
	v_cvt_f32_f16_e32 v12, v21
	v_cvt_f32_f16_sdwa v13, v21 dst_sel:DWORD dst_unused:UNUSED_PAD src0_sel:WORD_1
	v_pk_add_f32 v[4:5], v[4:5], v[6:7]
	v_pk_add_f32 v[6:7], v[10:11], v[8:9]
	v_cvt_pk_f16_f32 v4, v4, v5
	v_pk_add_f32 v[6:7], v[6:7], v[12:13]
	s_nop 0
	v_cvt_pk_f16_f32 v5, v6, v7
	v_add_lshl_u32 v6, v191, v50, 9
	v_add_u32_e32 v168, v192, v6
	ds_write_b128 v168, v[2:5]
	global_load_dwordx4 v[2:5], v[174:175], off
	global_load_dwordx4 v[8:11], v[176:177], off
	global_load_dwordx4 v[12:15], v[174:175], off offset:16
	global_load_dwordx4 v[16:19], v[176:177], off offset:16
	s_waitcnt vmcnt(3)
	v_cvt_pk_f16_f32 v6, v2, v3
	s_waitcnt vmcnt(2)
	v_cvt_pk_f16_f32 v2, v8, v9
	v_cvt_pk_f16_f32 v7, v4, v5
	v_cvt_pk_f16_f32 v3, v10, v11
	s_waitcnt vmcnt(1)
	v_cvt_pk_f16_f32 v8, v12, v13
	s_waitcnt vmcnt(0)
	v_cvt_pk_f16_f32 v4, v16, v17
	v_cvt_pk_f16_f32 v9, v14, v15
	v_cvt_pk_f16_f32 v5, v18, v19
	s_cbranch_vccz .LBB4_118
	global_load_dwordx3 v[154:156], v169, s[18:19]
	s_mov_b32 s14, s38
	s_mov_b32 s15, s39
	v_cmp_lt_u32_e64 s[64:65], 0, v199
	v_cmp_gt_u32_e64 s[66:67], 63, v199
	v_cmp_lt_u32_e64 s[68:69], 0, v180
	v_cmp_gt_u32_e64 s[70:71], 60, v180
	buffer_load_dwordx4 v[210:213], v200, s[12:15], 0 offen
	s_and_b64 s[72:73], s[68:69], s[64:65]
	s_and_b64 s[74:75], s[68:69], s[66:67]
	s_and_b64 s[76:77], s[70:71], s[64:65]
	s_and_b64 s[78:79], s[70:71], s[66:67]
	v_mov_b32_e32 v122, v6
	v_mov_b32_e32 v123, v7
	v_mov_b32_e32 v124, v8
	v_mov_b32_e32 v125, v9
	v_mov_b32_e32 v82, v2
	v_mov_b32_e32 v83, v3
	v_mov_b32_e32 v84, v4
	v_mov_b32_e32 v85, v5
	v_mov_b32_e32 v138, v6
	v_mov_b32_e32 v139, v7
	v_mov_b32_e32 v140, v8
	v_mov_b32_e32 v141, v9
	v_mov_b32_e32 v106, v2
	v_mov_b32_e32 v107, v3
	v_mov_b32_e32 v108, v4
	v_mov_b32_e32 v109, v5
	v_mov_b32_e32 v146, v6
	v_mov_b32_e32 v147, v7
	v_mov_b32_e32 v148, v8
	v_mov_b32_e32 v149, v9
	v_mov_b32_e32 v126, v2
	v_mov_b32_e32 v127, v3
	v_mov_b32_e32 v128, v4
	v_mov_b32_e32 v129, v5
	v_mov_b32_e32 v94, v6
	v_mov_b32_e32 v95, v7
	v_mov_b32_e32 v96, v8
	v_mov_b32_e32 v97, v9
	v_mov_b32_e32 v54, v2
	v_mov_b32_e32 v55, v3
	v_mov_b32_e32 v56, v4
	v_mov_b32_e32 v57, v5
	v_mov_b32_e32 v134, v6
	v_mov_b32_e32 v135, v7
	v_mov_b32_e32 v136, v8
	v_mov_b32_e32 v137, v9
	v_mov_b32_e32 v98, v2
	v_mov_b32_e32 v99, v3
	v_mov_b32_e32 v100, v4
	v_mov_b32_e32 v101, v5
	v_mov_b32_e32 v62, v6
	v_mov_b32_e32 v63, v7
	v_mov_b32_e32 v64, v8
	v_mov_b32_e32 v65, v9
	v_mov_b32_e32 v30, v2
	v_mov_b32_e32 v31, v3
	v_mov_b32_e32 v32, v4
	v_mov_b32_e32 v33, v5
	v_mov_b32_e32 v102, v6
	v_mov_b32_e32 v103, v7
	v_mov_b32_e32 v104, v8
	v_mov_b32_e32 v105, v9
	v_mov_b32_e32 v58, v2
	v_mov_b32_e32 v59, v3
	v_mov_b32_e32 v60, v4
	v_mov_b32_e32 v61, v5
	v_mov_b32_e32 v34, v6
	v_mov_b32_e32 v35, v7
	v_mov_b32_e32 v36, v8
	v_mov_b32_e32 v37, v9
	v_mov_b32_e32 v18, v2
	v_mov_b32_e32 v19, v3
	v_mov_b32_e32 v20, v4
	v_mov_b32_e32 v21, v5
	v_mov_b32_e32 v66, v6
	v_mov_b32_e32 v67, v7
	v_mov_b32_e32 v68, v8
	v_mov_b32_e32 v69, v9
	v_mov_b32_e32 v26, v2
	v_mov_b32_e32 v27, v3
	v_mov_b32_e32 v28, v4
	v_mov_b32_e32 v29, v5
	v_mov_b32_e32 v86, v6
	v_mov_b32_e32 v87, v7
	v_mov_b32_e32 v88, v8
	v_mov_b32_e32 v89, v9
	v_mov_b32_e32 v38, v2
	v_mov_b32_e32 v39, v3
	v_mov_b32_e32 v40, v4
	v_mov_b32_e32 v41, v5
	v_mov_b32_e32 v130, v6
	v_mov_b32_e32 v131, v7
	v_mov_b32_e32 v132, v8
	v_mov_b32_e32 v133, v9
	v_mov_b32_e32 v70, v2
	v_mov_b32_e32 v71, v3
	v_mov_b32_e32 v72, v4
	v_mov_b32_e32 v73, v5
	v_mov_b32_e32 v142, v6
	v_mov_b32_e32 v143, v7
	v_mov_b32_e32 v144, v8
	v_mov_b32_e32 v145, v9
	v_mov_b32_e32 v90, v2
	v_mov_b32_e32 v91, v3
	v_mov_b32_e32 v92, v4
	v_mov_b32_e32 v93, v5
	v_mov_b32_e32 v150, v6
	v_mov_b32_e32 v151, v7
	v_mov_b32_e32 v152, v8
	v_mov_b32_e32 v153, v9
	v_mov_b32_e32 v110, v2
	v_mov_b32_e32 v111, v3
	v_mov_b32_e32 v112, v4
	v_mov_b32_e32 v113, v5
	v_mov_b32_e32 v14, v6
	v_mov_b32_e32 v15, v7
	v_mov_b32_e32 v16, v8
	v_mov_b32_e32 v17, v9
	v_mov_b32_e32 v10, v2
	v_mov_b32_e32 v11, v3
	v_mov_b32_e32 v12, v4
	v_mov_b32_e32 v13, v5
	v_add_u32_e32 v245, 0xfffe7c00, v200
	v_add_u32_e32 v246, 0xfffe8000, v200
	s_mov_b64 exec, s[72:73]
	buffer_load_dwordx4 v[122:125], v245, s[12:15], 0 offen
	buffer_load_dwordx4 v[82:85], v245, s[12:15], 0 offen offset:512
	s_mov_b64 exec, -1
	s_mov_b64 exec, s[68:69]
	buffer_load_dwordx4 v[138:141], v246, s[12:15], 0 offen offset:512
	buffer_load_dwordx4 v[106:109], v246, s[12:15], 0 offen offset:1024
	s_mov_b64 exec, -1
	s_mov_b64 exec, s[74:75]
	buffer_load_dwordx4 v[146:149], v246, s[12:15], 0 offen offset:2048
	buffer_load_dwordx4 v[126:129], v246, s[12:15], 0 offen offset:2560
	s_mov_b64 exec, -1
	v_add_u32_e32 v245, 0xfffffc00, v200
	s_mov_b64 exec, s[64:65]
	buffer_load_dwordx4 v[94:97], v245, s[12:15], 0 offen
	buffer_load_dwordx4 v[54:57], v245, s[12:15], 0 offen offset:512
	s_mov_b64 exec, -1
	buffer_load_dwordx4 v[118:121], v200, s[12:15], 0 offen offset:512
	buffer_load_dwordx4 v[74:77], v200, s[12:15], 0 offen offset:1024
	s_mov_b64 exec, s[66:67]
	buffer_load_dwordx4 v[134:137], v200, s[12:15], 0 offen offset:2048
	buffer_load_dwordx4 v[98:101], v200, s[12:15], 0 offen offset:2560
	s_mov_b64 exec, -1
	v_add_u32_e32 v245, 0x17c00, v200
	v_add_u32_e32 v246, 0x18000, v200
	s_mov_b64 exec, s[64:65]
	buffer_load_dwordx4 v[62:65], v245, s[12:15], 0 offen
	buffer_load_dwordx4 v[30:33], v245, s[12:15], 0 offen offset:512
	s_mov_b64 exec, -1
	buffer_load_dwordx4 v[78:81], v246, s[12:15], 0 offen offset:512
	buffer_load_dwordx4 v[42:45], v246, s[12:15], 0 offen offset:1024
	s_mov_b64 exec, s[66:67]
	buffer_load_dwordx4 v[102:105], v246, s[12:15], 0 offen offset:2048
	buffer_load_dwordx4 v[58:61], v246, s[12:15], 0 offen offset:2560
	s_mov_b64 exec, -1
	v_add_u32_e32 v245, 0x18000, v200
	buffer_load_dwordx4 v[162:165], v245, s[12:15], 0 offen
	v_add_u32_e32 v246, 0x30000, v200
	buffer_load_dwordx4 v[158:161], v246, s[12:15], 0 offen
	v_add_u32_e32 v245, 0x2fc00, v200
	v_add_u32_e32 v246, 0x30000, v200
	v_add_u32_e32 v247, 0x47c00, v200
	v_add_u32_e32 v248, 0x48000, v200
	v_add_u32_e32 v249, 0x5fc00, v200
	v_add_u32_e32 v250, 0x60000, v200
	s_waitcnt vmcnt(21)
	v_cvt_f16_f32_e32 v206, v155
	v_cvt_f16_f32_e32 v208, v154
	v_cvt_f16_f32_e32 v207, v156
	v_add_u32_e32 v251, 0x48000, v200
	buffer_load_dwordx4 v[154:157], v251, s[12:15], 0 offen
	s_mov_b64 s[4:5], 0
	s_waitcnt vmcnt(3)
	v_pk_mul_f16 v216, v208, v213 op_sel_hi:[0,1]
	v_pk_mul_f16 v220, v206, v213 op_sel_hi:[0,1]
	v_pk_mul_f16 v224, v207, v213 op_sel_hi:[0,1]
	v_pk_mul_f16 v209, v208, v210 op_sel_hi:[0,1]
	v_pk_mul_f16 v214, v208, v211 op_sel_hi:[0,1]
	v_pk_mul_f16 v215, v208, v212 op_sel_hi:[0,1]
	v_pk_mul_f16 v217, v206, v210 op_sel_hi:[0,1]
	s_mov_b64 exec, s[64:65]
	buffer_load_dwordx4 v[34:37], v245, s[12:15], 0 offen
	buffer_load_dwordx4 v[18:21], v245, s[12:15], 0 offen offset:512
	s_mov_b64 exec, -1
	v_pk_mul_f16 v218, v206, v211 op_sel_hi:[0,1]
	v_pk_mul_f16 v219, v206, v212 op_sel_hi:[0,1]
	v_pk_mul_f16 v221, v207, v210 op_sel_hi:[0,1]
	v_pk_mul_f16 v222, v207, v211 op_sel_hi:[0,1]
	v_pk_mul_f16 v223, v207, v212 op_sel_hi:[0,1]
	v_pk_fma_f16 v125, v125, v213, v216
	v_pk_fma_f16 v141, v141, v213, v220
	v_pk_fma_f16 v149, v149, v213, v224
	v_pk_fma_f16 v225, v97, v213, v216
	v_pk_fma_f16 v229, v121, v213, v220
	v_pk_fma_f16 v233, v137, v213, v224
	v_pk_fma_f16 v216, v65, v213, v216
	v_pk_fma_f16 v220, v81, v213, v220
	buffer_load_dwordx4 v[46:49], v246, s[12:15], 0 offen offset:512
	buffer_load_dwordx4 v[22:25], v246, s[12:15], 0 offen offset:1024
	v_pk_fma_f16 v213, v105, v213, v224
	v_pk_maximum3_f16 v224, v125, v141, v149
	v_pk_fma_f16 v124, v124, v212, v215
	v_pk_fma_f16 v123, v123, v211, v214
	v_pk_fma_f16 v122, v122, v210, v209
	v_pk_fma_f16 v140, v140, v212, v219
	v_pk_fma_f16 v139, v139, v211, v218
	v_pk_fma_f16 v138, v138, v210, v217
	v_pk_fma_f16 v148, v148, v212, v223
	v_pk_fma_f16 v147, v147, v211, v222
	v_pk_fma_f16 v146, v146, v210, v221
	v_pk_fma_f16 v226, v96, v212, v215
	v_pk_fma_f16 v227, v95, v211, v214
	v_pk_fma_f16 v228, v94, v210, v209
	v_pk_fma_f16 v230, v120, v212, v219
	v_pk_fma_f16 v231, v119, v211, v218
	s_mov_b64 exec, s[66:67]
	buffer_load_dwordx4 v[66:69], v246, s[12:15], 0 offen offset:2048
	buffer_load_dwordx4 v[26:29], v246, s[12:15], 0 offen offset:2560
	s_mov_b64 exec, -1
	v_pk_fma_f16 v232, v118, v210, v217
	v_pk_fma_f16 v234, v136, v212, v223
	v_pk_fma_f16 v235, v135, v211, v222
	v_pk_fma_f16 v236, v134, v210, v221
	v_pk_fma_f16 v215, v64, v212, v215
	v_pk_fma_f16 v214, v63, v211, v214
	v_pk_fma_f16 v209, v62, v210, v209
	v_pk_fma_f16 v219, v80, v212, v219
	v_pk_fma_f16 v218, v79, v211, v218
	v_pk_fma_f16 v217, v78, v210, v217
	v_pk_fma_f16 v212, v104, v212, v223
	v_pk_fma_f16 v211, v103, v211, v222
	v_pk_fma_f16 v210, v102, v210, v221
	v_pk_maximum3_f16 v221, v122, v138, v146
	v_pk_maximum3_f16 v222, v123, v139, v147
	v_pk_maximum3_f16 v223, v124, v140, v148
	v_pk_maximum3_f16 v240, v225, v229, v233
	v_pk_maximum3_f16 v244, v216, v220, v213
	v_pk_maximum3_f16 v237, v228, v232, v236
	v_pk_maximum3_f16 v238, v227, v231, v235
	v_pk_maximum3_f16 v239, v226, v230, v234
	v_pk_maximum3_f16 v241, v209, v217, v210
	v_pk_maximum3_f16 v242, v214, v218, v211
	v_pk_maximum3_f16 v224, v224, v240, v244
	v_pk_maximum3_f16 v243, v215, v219, v212
	v_pk_maximum3_f16 v221, v221, v237, v241
	v_pk_maximum3_f16 v222, v222, v238, v242
	v_pk_maximum3_f16 v223, v223, v239, v243
	v_pk_add_f16 v125, v125, v224 neg_lo:[0,1] neg_hi:[0,1]
	s_mov_b64 exec, s[64:65]
	buffer_load_dwordx4 v[86:89], v247, s[12:15], 0 offen
	buffer_load_dwordx4 v[38:41], v247, s[12:15], 0 offen offset:512
	s_mov_b64 exec, -1
	v_pk_add_f16 v122, v122, v221 neg_lo:[0,1] neg_hi:[0,1]
	v_pk_add_f16 v123, v123, v222 neg_lo:[0,1] neg_hi:[0,1]
	v_pk_add_f16 v124, v124, v223 neg_lo:[0,1] neg_hi:[0,1]
	v_pk_add_f16 v138, v138, v221 neg_lo:[0,1] neg_hi:[0,1]
	v_exp_f16_sdwa v237, v122 dst_sel:WORD_0 dst_unused:UNUSED_PAD src0_sel:WORD_0
	v_exp_f16_sdwa v238, v123 dst_sel:WORD_0 dst_unused:UNUSED_PAD src0_sel:WORD_0
	v_exp_f16_sdwa v239, v124 dst_sel:WORD_0 dst_unused:UNUSED_PAD src0_sel:WORD_0
	v_exp_f16_sdwa v240, v125 dst_sel:WORD_0 dst_unused:UNUSED_PAD src0_sel:WORD_0
	v_exp_f16_sdwa v237, v122 dst_sel:WORD_1 dst_unused:UNUSED_PRESERVE src0_sel:WORD_1
	v_exp_f16_sdwa v238, v123 dst_sel:WORD_1 dst_unused:UNUSED_PRESERVE src0_sel:WORD_1
	v_exp_f16_sdwa v239, v124 dst_sel:WORD_1 dst_unused:UNUSED_PRESERVE src0_sel:WORD_1
	v_exp_f16_sdwa v240, v125 dst_sel:WORD_1 dst_unused:UNUSED_PRESERVE src0_sel:WORD_1
	v_pk_add_f16 v139, v139, v222 neg_lo:[0,1] neg_hi:[0,1]
	v_pk_add_f16 v125, v237, 0
	v_pk_fma_f16 v85, v85, v240, 0
	v_pk_add_f16 v122, v240, 0
	v_pk_add_f16 v123, v239, 0
	v_pk_add_f16 v124, v238, 0
	v_pk_fma_f16 v84, v84, v239, 0
	v_pk_fma_f16 v83, v83, v238, 0
	v_pk_fma_f16 v82, v82, v237, 0
	v_pk_add_f16 v140, v140, v223 neg_lo:[0,1] neg_hi:[0,1]
	buffer_load_dwordx4 v[114:117], v248, s[12:15], 0 offen offset:512
	buffer_load_dwordx4 v[50:53], v248, s[12:15], 0 offen offset:1024
	v_pk_add_f16 v141, v141, v224 neg_lo:[0,1] neg_hi:[0,1]
	v_exp_f16_sdwa v237, v138 dst_sel:WORD_0 dst_unused:UNUSED_PAD src0_sel:WORD_0
	v_exp_f16_sdwa v238, v139 dst_sel:WORD_0 dst_unused:UNUSED_PAD src0_sel:WORD_0
	v_exp_f16_sdwa v239, v140 dst_sel:WORD_0 dst_unused:UNUSED_PAD src0_sel:WORD_0
	v_exp_f16_sdwa v240, v141 dst_sel:WORD_0 dst_unused:UNUSED_PAD src0_sel:WORD_0
	v_exp_f16_sdwa v237, v138 dst_sel:WORD_1 dst_unused:UNUSED_PRESERVE src0_sel:WORD_1
	v_exp_f16_sdwa v238, v139 dst_sel:WORD_1 dst_unused:UNUSED_PRESERVE src0_sel:WORD_1
	v_exp_f16_sdwa v239, v140 dst_sel:WORD_1 dst_unused:UNUSED_PRESERVE src0_sel:WORD_1
	v_exp_f16_sdwa v240, v141 dst_sel:WORD_1 dst_unused:UNUSED_PRESERVE src0_sel:WORD_1
	v_pk_add_f16 v125, v125, v237
	v_pk_fma_f16 v85, v109, v240, v85
	v_pk_add_f16 v109, v149, v224 neg_lo:[0,1] neg_hi:[0,1]
	v_pk_add_f16 v124, v124, v238
	v_pk_add_f16 v123, v123, v239
	v_pk_add_f16 v122, v122, v240
	v_pk_fma_f16 v82, v106, v237, v82
	v_pk_fma_f16 v83, v107, v238, v83
	v_pk_fma_f16 v84, v108, v239, v84
	v_pk_add_f16 v106, v146, v221 neg_lo:[0,1] neg_hi:[0,1]
	v_pk_add_f16 v107, v147, v222 neg_lo:[0,1] neg_hi:[0,1]
	v_pk_add_f16 v108, v148, v223 neg_lo:[0,1] neg_hi:[0,1]
	v_exp_f16_sdwa v138, v106 dst_sel:WORD_0 dst_unused:UNUSED_PAD src0_sel:WORD_0
	v_exp_f16_sdwa v139, v107 dst_sel:WORD_0 dst_unused:UNUSED_PAD src0_sel:WORD_0
	v_exp_f16_sdwa v140, v108 dst_sel:WORD_0 dst_unused:UNUSED_PAD src0_sel:WORD_0
	v_exp_f16_sdwa v141, v109 dst_sel:WORD_0 dst_unused:UNUSED_PAD src0_sel:WORD_0
	v_exp_f16_sdwa v138, v106 dst_sel:WORD_1 dst_unused:UNUSED_PRESERVE src0_sel:WORD_1
	v_exp_f16_sdwa v139, v107 dst_sel:WORD_1 dst_unused:UNUSED_PRESERVE src0_sel:WORD_1
	v_exp_f16_sdwa v140, v108 dst_sel:WORD_1 dst_unused:UNUSED_PRESERVE src0_sel:WORD_1
	v_exp_f16_sdwa v141, v109 dst_sel:WORD_1 dst_unused:UNUSED_PRESERVE src0_sel:WORD_1
	v_pk_add_f16 v109, v125, v138
	v_pk_add_f16 v106, v122, v141
	s_mov_b64 exec, s[66:67]
	buffer_load_dwordx4 v[130:133], v248, s[12:15], 0 offen offset:2048
	buffer_load_dwordx4 v[70:73], v248, s[12:15], 0 offen offset:2560
	s_mov_b64 exec, -1
	v_pk_add_f16 v107, v123, v140
	v_pk_add_f16 v108, v124, v139
	v_pk_fma_f16 v85, v129, v141, v85
	v_pk_fma_f16 v84, v128, v140, v84
	v_pk_fma_f16 v83, v127, v139, v83
	v_pk_fma_f16 v82, v126, v138, v82
	v_pk_add_f16 v122, v228, v221 neg_lo:[0,1] neg_hi:[0,1]
	v_pk_add_f16 v123, v227, v222 neg_lo:[0,1] neg_hi:[0,1]
	v_pk_add_f16 v124, v226, v223 neg_lo:[0,1] neg_hi:[0,1]
	v_pk_add_f16 v125, v225, v224 neg_lo:[0,1] neg_hi:[0,1]
	v_exp_f16_sdwa v126, v122 dst_sel:WORD_0 dst_unused:UNUSED_PAD src0_sel:WORD_0
	v_exp_f16_sdwa v127, v123 dst_sel:WORD_0 dst_unused:UNUSED_PAD src0_sel:WORD_0
	v_exp_f16_sdwa v128, v124 dst_sel:WORD_0 dst_unused:UNUSED_PAD src0_sel:WORD_0
	v_exp_f16_sdwa v129, v125 dst_sel:WORD_0 dst_unused:UNUSED_PAD src0_sel:WORD_0
	v_exp_f16_sdwa v126, v122 dst_sel:WORD_1 dst_unused:UNUSED_PRESERVE src0_sel:WORD_1
	v_exp_f16_sdwa v127, v123 dst_sel:WORD_1 dst_unused:UNUSED_PRESERVE src0_sel:WORD_1
	v_exp_f16_sdwa v128, v124 dst_sel:WORD_1 dst_unused:UNUSED_PRESERVE src0_sel:WORD_1
	v_exp_f16_sdwa v129, v125 dst_sel:WORD_1 dst_unused:UNUSED_PRESERVE src0_sel:WORD_1
	v_pk_add_f16 v122, v232, v221 neg_lo:[0,1] neg_hi:[0,1]
	v_pk_add_f16 v109, v109, v126
	v_pk_add_f16 v108, v108, v127
	v_pk_add_f16 v107, v107, v128
	s_mov_b64 exec, s[76:77]
	buffer_load_dwordx4 v[142:145], v249, s[12:15], 0 offen
	buffer_load_dwordx4 v[90:93], v249, s[12:15], 0 offen offset:512
	s_mov_b64 exec, -1
	v_pk_add_f16 v106, v106, v129
	v_pk_fma_f16 v82, v54, v126, v82
	v_pk_fma_f16 v83, v55, v127, v83
	v_pk_fma_f16 v84, v56, v128, v84
	v_pk_fma_f16 v85, v57, v129, v85
	v_pk_add_f16 v123, v231, v222 neg_lo:[0,1] neg_hi:[0,1]
	v_pk_add_f16 v124, v230, v223 neg_lo:[0,1] neg_hi:[0,1]
	v_pk_add_f16 v125, v229, v224 neg_lo:[0,1] neg_hi:[0,1]
	v_exp_f16_sdwa v126, v122 dst_sel:WORD_0 dst_unused:UNUSED_PAD src0_sel:WORD_0
	v_exp_f16_sdwa v127, v123 dst_sel:WORD_0 dst_unused:UNUSED_PAD src0_sel:WORD_0
	v_exp_f16_sdwa v128, v124 dst_sel:WORD_0 dst_unused:UNUSED_PAD src0_sel:WORD_0
	v_exp_f16_sdwa v129, v125 dst_sel:WORD_0 dst_unused:UNUSED_PAD src0_sel:WORD_0
	v_exp_f16_sdwa v126, v122 dst_sel:WORD_1 dst_unused:UNUSED_PRESERVE src0_sel:WORD_1
	v_exp_f16_sdwa v127, v123 dst_sel:WORD_1 dst_unused:UNUSED_PRESERVE src0_sel:WORD_1
	v_exp_f16_sdwa v128, v124 dst_sel:WORD_1 dst_unused:UNUSED_PRESERVE src0_sel:WORD_1
	v_exp_f16_sdwa v129, v125 dst_sel:WORD_1 dst_unused:UNUSED_PRESERVE src0_sel:WORD_1
	v_pk_add_f16 v122, v236, v221 neg_lo:[0,1] neg_hi:[0,1]
	v_pk_add_f16 v109, v109, v126
	v_pk_add_f16 v106, v106, v129
	v_pk_add_f16 v107, v107, v128
	v_pk_add_f16 v108, v108, v127
	v_pk_fma_f16 v85, v77, v129, v85
	v_pk_fma_f16 v84, v76, v128, v84
	s_mov_b64 exec, s[70:71]
	buffer_load_dwordx4 v[150:153], v250, s[12:15], 0 offen offset:512
	buffer_load_dwordx4 v[110:113], v250, s[12:15], 0 offen offset:1024
	s_mov_b64 exec, -1
	v_pk_fma_f16 v83, v75, v127, v83
	v_pk_fma_f16 v82, v74, v126, v82
	v_pk_add_f16 v123, v235, v222 neg_lo:[0,1] neg_hi:[0,1]
	v_pk_add_f16 v124, v234, v223 neg_lo:[0,1] neg_hi:[0,1]
	v_pk_add_f16 v125, v233, v224 neg_lo:[0,1] neg_hi:[0,1]
	v_exp_f16_sdwa v126, v122 dst_sel:WORD_0 dst_unused:UNUSED_PAD src0_sel:WORD_0
	v_exp_f16_sdwa v127, v123 dst_sel:WORD_0 dst_unused:UNUSED_PAD src0_sel:WORD_0
	v_exp_f16_sdwa v128, v124 dst_sel:WORD_0 dst_unused:UNUSED_PAD src0_sel:WORD_0
	v_exp_f16_sdwa v129, v125 dst_sel:WORD_0 dst_unused:UNUSED_PAD src0_sel:WORD_0
	v_exp_f16_sdwa v126, v122 dst_sel:WORD_1 dst_unused:UNUSED_PRESERVE src0_sel:WORD_1
	v_exp_f16_sdwa v127, v123 dst_sel:WORD_1 dst_unused:UNUSED_PRESERVE src0_sel:WORD_1
	v_exp_f16_sdwa v128, v124 dst_sel:WORD_1 dst_unused:UNUSED_PRESERVE src0_sel:WORD_1
	v_exp_f16_sdwa v129, v125 dst_sel:WORD_1 dst_unused:UNUSED_PRESERVE src0_sel:WORD_1
	v_pk_add_f16 v122, v209, v221 neg_lo:[0,1] neg_hi:[0,1]
	v_pk_add_f16 v109, v109, v126
	v_pk_add_f16 v108, v108, v127
	v_pk_add_f16 v107, v107, v128
	v_pk_add_f16 v106, v106, v129
	v_pk_fma_f16 v82, v98, v126, v82
	v_pk_fma_f16 v83, v99, v127, v83
	v_pk_fma_f16 v84, v100, v128, v84
	v_pk_fma_f16 v85, v101, v129, v85
	s_mov_b64 exec, s[78:79]
	buffer_load_dwordx4 v[14:17], v250, s[12:15], 0 offen offset:2048
	buffer_load_dwordx4 v[10:13], v250, s[12:15], 0 offen offset:2560
	s_mov_b64 exec, -1
	v_pk_add_f16 v123, v214, v222 neg_lo:[0,1] neg_hi:[0,1]
	v_pk_add_f16 v124, v215, v223 neg_lo:[0,1] neg_hi:[0,1]
	v_pk_add_f16 v125, v216, v224 neg_lo:[0,1] neg_hi:[0,1]
	v_exp_f16_sdwa v126, v122 dst_sel:WORD_0 dst_unused:UNUSED_PAD src0_sel:WORD_0
	v_exp_f16_sdwa v127, v123 dst_sel:WORD_0 dst_unused:UNUSED_PAD src0_sel:WORD_0
	v_exp_f16_sdwa v128, v124 dst_sel:WORD_0 dst_unused:UNUSED_PAD src0_sel:WORD_0
	v_exp_f16_sdwa v129, v125 dst_sel:WORD_0 dst_unused:UNUSED_PAD src0_sel:WORD_0
	v_exp_f16_sdwa v126, v122 dst_sel:WORD_1 dst_unused:UNUSED_PRESERVE src0_sel:WORD_1
	v_exp_f16_sdwa v127, v123 dst_sel:WORD_1 dst_unused:UNUSED_PRESERVE src0_sel:WORD_1
	v_exp_f16_sdwa v128, v124 dst_sel:WORD_1 dst_unused:UNUSED_PRESERVE src0_sel:WORD_1
	v_exp_f16_sdwa v129, v125 dst_sel:WORD_1 dst_unused:UNUSED_PRESERVE src0_sel:WORD_1
	v_pk_add_f16 v122, v217, v221 neg_lo:[0,1] neg_hi:[0,1]
	v_pk_add_f16 v109, v109, v126
	v_pk_add_f16 v106, v106, v129
	v_pk_add_f16 v107, v107, v128
	v_pk_add_f16 v108, v108, v127
	v_pk_fma_f16 v85, v33, v129, v85
	v_pk_fma_f16 v84, v32, v128, v84
	v_pk_fma_f16 v83, v31, v127, v83
	v_pk_fma_f16 v82, v30, v126, v82
	v_pk_add_f16 v123, v218, v222 neg_lo:[0,1] neg_hi:[0,1]
	v_pk_add_f16 v124, v219, v223 neg_lo:[0,1] neg_hi:[0,1]
	v_pk_add_f16 v125, v220, v224 neg_lo:[0,1] neg_hi:[0,1]
	v_exp_f16_sdwa v126, v122 dst_sel:WORD_0 dst_unused:UNUSED_PAD src0_sel:WORD_0
	v_exp_f16_sdwa v127, v123 dst_sel:WORD_0 dst_unused:UNUSED_PAD src0_sel:WORD_0
	v_exp_f16_sdwa v128, v124 dst_sel:WORD_0 dst_unused:UNUSED_PAD src0_sel:WORD_0
	v_exp_f16_sdwa v129, v125 dst_sel:WORD_0 dst_unused:UNUSED_PAD src0_sel:WORD_0
	v_exp_f16_sdwa v126, v122 dst_sel:WORD_1 dst_unused:UNUSED_PRESERVE src0_sel:WORD_1
	v_exp_f16_sdwa v127, v123 dst_sel:WORD_1 dst_unused:UNUSED_PRESERVE src0_sel:WORD_1
	v_exp_f16_sdwa v128, v124 dst_sel:WORD_1 dst_unused:UNUSED_PRESERVE src0_sel:WORD_1
	v_exp_f16_sdwa v129, v125 dst_sel:WORD_1 dst_unused:UNUSED_PRESERVE src0_sel:WORD_1
	v_pk_add_f16 v122, v210, v221 neg_lo:[0,1] neg_hi:[0,1]
	v_pk_add_f16 v109, v109, v126
	v_pk_add_f16 v108, v108, v127
	v_pk_add_f16 v107, v107, v128
	v_pk_add_f16 v106, v106, v129
	v_pk_fma_f16 v82, v42, v126, v82
	v_pk_fma_f16 v83, v43, v127, v83
	v_pk_fma_f16 v84, v44, v128, v84
	v_pk_fma_f16 v85, v45, v129, v85
	v_pk_add_f16 v123, v211, v222 neg_lo:[0,1] neg_hi:[0,1]
	v_pk_add_f16 v124, v212, v223 neg_lo:[0,1] neg_hi:[0,1]
	v_pk_add_f16 v125, v213, v224 neg_lo:[0,1] neg_hi:[0,1]
	v_exp_f16_sdwa v126, v122 dst_sel:WORD_0 dst_unused:UNUSED_PAD src0_sel:WORD_0
	v_exp_f16_sdwa v127, v123 dst_sel:WORD_0 dst_unused:UNUSED_PAD src0_sel:WORD_0
	v_exp_f16_sdwa v128, v124 dst_sel:WORD_0 dst_unused:UNUSED_PAD src0_sel:WORD_0
	v_exp_f16_sdwa v129, v125 dst_sel:WORD_0 dst_unused:UNUSED_PAD src0_sel:WORD_0
	v_exp_f16_sdwa v126, v122 dst_sel:WORD_1 dst_unused:UNUSED_PRESERVE src0_sel:WORD_1
	v_exp_f16_sdwa v127, v123 dst_sel:WORD_1 dst_unused:UNUSED_PRESERVE src0_sel:WORD_1
	v_exp_f16_sdwa v128, v124 dst_sel:WORD_1 dst_unused:UNUSED_PRESERVE src0_sel:WORD_1
	v_exp_f16_sdwa v129, v125 dst_sel:WORD_1 dst_unused:UNUSED_PRESERVE src0_sel:WORD_1
	v_pk_add_f16 v109, v109, v126
	v_pk_add_f16 v108, v108, v127
	v_rcp_f16_e32 v122, v109
	v_rcp_f16_sdwa v109, v109 dst_sel:DWORD dst_unused:UNUSED_PAD src0_sel:WORD_1
	v_pk_add_f16 v107, v107, v128
	v_rcp_f16_e32 v123, v108
	v_rcp_f16_sdwa v108, v108 dst_sel:DWORD dst_unused:UNUSED_PAD src0_sel:WORD_1
	v_pk_add_f16 v106, v106, v129
	v_rcp_f16_e32 v124, v107
	v_rcp_f16_sdwa v107, v107 dst_sel:DWORD dst_unused:UNUSED_PAD src0_sel:WORD_1
	v_rcp_f16_e32 v125, v106
	v_rcp_f16_sdwa v106, v106 dst_sel:DWORD dst_unused:UNUSED_PAD src0_sel:WORD_1
	v_pk_fma_f16 v82, v58, v126, v82
	v_pack_b32_f16 v109, v122, v109
	v_pk_fma_f16 v83, v59, v127, v83
	v_pk_mul_f16 v141, v82, v109
	v_pack_b32_f16 v82, v123, v108
	v_pk_fma_f16 v84, v60, v128, v84
	v_pk_mul_f16 v140, v83, v82
	v_pack_b32_f16 v82, v124, v107
	v_pk_fma_f16 v85, v61, v129, v85
	v_pk_mul_f16 v139, v84, v82
	v_pack_b32_f16 v82, v125, v106
	v_pk_mul_f16 v138, v85, v82
	s_waitcnt vmcnt(12)
	v_pk_mul_f16 v85, v208, v165 op_sel_hi:[0,1]
	v_pk_mul_f16 v109, v206, v165 op_sel_hi:[0,1]
	v_pk_mul_f16 v122, v207, v162 op_sel_hi:[0,1]
	v_pk_mul_f16 v125, v207, v165 op_sel_hi:[0,1]
	v_pk_mul_f16 v82, v208, v162 op_sel_hi:[0,1]
	v_pk_mul_f16 v83, v208, v163 op_sel_hi:[0,1]
	v_pk_mul_f16 v84, v208, v164 op_sel_hi:[0,1]
	v_pk_mul_f16 v106, v206, v162 op_sel_hi:[0,1]
	v_pk_mul_f16 v107, v206, v163 op_sel_hi:[0,1]
	v_pk_mul_f16 v108, v206, v164 op_sel_hi:[0,1]
	v_pk_mul_f16 v123, v207, v163 op_sel_hi:[0,1]
	v_pk_mul_f16 v124, v207, v164 op_sel_hi:[0,1]
	v_pk_fma_f16 v97, v97, v165, v85
	v_pk_fma_f16 v121, v121, v165, v109
	v_pk_fma_f16 v126, v137, v165, v125
	v_pk_fma_f16 v129, v134, v162, v122
	v_pk_fma_f16 v134, v65, v165, v85
	v_pk_fma_f16 v146, v81, v165, v109
	v_pk_fma_f16 v209, v105, v165, v125
	v_pk_fma_f16 v85, v37, v165, v85
	v_pk_fma_f16 v109, v49, v165, v109
	v_pk_fma_f16 v125, v69, v165, v125
	v_pk_maximum3_f16 v165, v97, v121, v126
	v_pk_fma_f16 v96, v96, v164, v84
	v_pk_fma_f16 v95, v95, v163, v83
	v_pk_fma_f16 v94, v94, v162, v82
	v_pk_fma_f16 v120, v120, v164, v108
	v_pk_fma_f16 v119, v119, v163, v107
	v_pk_fma_f16 v118, v118, v162, v106
	v_pk_fma_f16 v127, v136, v164, v124
	v_pk_fma_f16 v128, v135, v163, v123
	v_pk_fma_f16 v135, v64, v164, v84
	v_pk_fma_f16 v136, v63, v163, v83
	v_pk_fma_f16 v137, v62, v162, v82
	v_pk_fma_f16 v147, v80, v164, v108
	v_pk_fma_f16 v148, v79, v163, v107
	v_pk_fma_f16 v149, v78, v162, v106
	v_pk_fma_f16 v210, v104, v164, v124
	v_pk_fma_f16 v211, v103, v163, v123
	v_pk_fma_f16 v212, v102, v162, v122
	v_pk_fma_f16 v84, v36, v164, v84
	v_pk_fma_f16 v83, v35, v163, v83
	v_pk_fma_f16 v82, v34, v162, v82
	v_pk_fma_f16 v108, v48, v164, v108
	v_pk_fma_f16 v107, v47, v163, v107
	v_pk_fma_f16 v106, v46, v162, v106
	v_pk_fma_f16 v124, v68, v164, v124
	v_pk_fma_f16 v123, v67, v163, v123
	v_pk_fma_f16 v122, v66, v162, v122
	v_pk_maximum3_f16 v162, v94, v118, v129
	v_pk_maximum3_f16 v163, v95, v119, v128
	v_pk_maximum3_f16 v164, v96, v120, v127
	v_pk_maximum3_f16 v216, v134, v146, v209
	v_pk_maximum3_f16 v220, v85, v109, v125
	v_pk_maximum3_f16 v213, v137, v149, v212
	v_pk_maximum3_f16 v214, v136, v148, v211
	v_pk_maximum3_f16 v215, v135, v147, v210
	v_pk_maximum3_f16 v217, v82, v106, v122
	v_pk_maximum3_f16 v218, v83, v107, v123
	v_pk_maximum3_f16 v165, v165, v216, v220
	v_pk_maximum3_f16 v219, v84, v108, v124
	v_pk_maximum3_f16 v162, v162, v213, v217
	v_pk_maximum3_f16 v163, v163, v214, v218
	v_pk_maximum3_f16 v164, v164, v215, v219
	v_pk_add_f16 v97, v97, v165 neg_lo:[0,1] neg_hi:[0,1]
	v_pk_add_f16 v94, v94, v162 neg_lo:[0,1] neg_hi:[0,1]
	v_pk_add_f16 v95, v95, v163 neg_lo:[0,1] neg_hi:[0,1]
	v_pk_add_f16 v96, v96, v164 neg_lo:[0,1] neg_hi:[0,1]
	v_pk_add_f16 v118, v118, v162 neg_lo:[0,1] neg_hi:[0,1]
	v_exp_f16_sdwa v213, v94 dst_sel:WORD_0 dst_unused:UNUSED_PAD src0_sel:WORD_0
	v_exp_f16_sdwa v214, v95 dst_sel:WORD_0 dst_unused:UNUSED_PAD src0_sel:WORD_0
	v_exp_f16_sdwa v215, v96 dst_sel:WORD_0 dst_unused:UNUSED_PAD src0_sel:WORD_0
	v_exp_f16_sdwa v216, v97 dst_sel:WORD_0 dst_unused:UNUSED_PAD src0_sel:WORD_0
	v_exp_f16_sdwa v213, v94 dst_sel:WORD_1 dst_unused:UNUSED_PRESERVE src0_sel:WORD_1
	v_exp_f16_sdwa v214, v95 dst_sel:WORD_1 dst_unused:UNUSED_PRESERVE src0_sel:WORD_1
	v_exp_f16_sdwa v215, v96 dst_sel:WORD_1 dst_unused:UNUSED_PRESERVE src0_sel:WORD_1
	v_exp_f16_sdwa v216, v97 dst_sel:WORD_1 dst_unused:UNUSED_PRESERVE src0_sel:WORD_1
	v_pk_add_f16 v119, v119, v163 neg_lo:[0,1] neg_hi:[0,1]
	v_pk_add_f16 v97, v213, 0
	v_pk_fma_f16 v57, v57, v216, 0
	v_pk_add_f16 v94, v216, 0
	v_pk_add_f16 v95, v215, 0
	v_pk_add_f16 v96, v214, 0
	v_pk_fma_f16 v56, v56, v215, 0
	v_pk_fma_f16 v55, v55, v214, 0
	v_pk_fma_f16 v54, v54, v213, 0
	v_pk_add_f16 v120, v120, v164 neg_lo:[0,1] neg_hi:[0,1]
	v_pk_add_f16 v121, v121, v165 neg_lo:[0,1] neg_hi:[0,1]
	v_pk_add_f16 v82, v82, v162 neg_lo:[0,1] neg_hi:[0,1]
	v_exp_f16_sdwa v213, v118 dst_sel:WORD_0 dst_unused:UNUSED_PAD src0_sel:WORD_0
	v_exp_f16_sdwa v214, v119 dst_sel:WORD_0 dst_unused:UNUSED_PAD src0_sel:WORD_0
	v_exp_f16_sdwa v215, v120 dst_sel:WORD_0 dst_unused:UNUSED_PAD src0_sel:WORD_0
	v_exp_f16_sdwa v216, v121 dst_sel:WORD_0 dst_unused:UNUSED_PAD src0_sel:WORD_0
	v_exp_f16_sdwa v213, v118 dst_sel:WORD_1 dst_unused:UNUSED_PRESERVE src0_sel:WORD_1
	v_exp_f16_sdwa v214, v119 dst_sel:WORD_1 dst_unused:UNUSED_PRESERVE src0_sel:WORD_1
	v_exp_f16_sdwa v215, v120 dst_sel:WORD_1 dst_unused:UNUSED_PRESERVE src0_sel:WORD_1
	v_exp_f16_sdwa v216, v121 dst_sel:WORD_1 dst_unused:UNUSED_PRESERVE src0_sel:WORD_1
	v_pk_add_f16 v83, v83, v163 neg_lo:[0,1] neg_hi:[0,1]
	v_pk_add_f16 v97, v97, v213
	v_pk_fma_f16 v57, v77, v216, v57
	v_pk_add_f16 v77, v126, v165 neg_lo:[0,1] neg_hi:[0,1]
	v_pk_add_f16 v96, v96, v214
	v_pk_add_f16 v95, v95, v215
	v_pk_add_f16 v94, v94, v216
	v_pk_fma_f16 v54, v74, v213, v54
	v_pk_fma_f16 v55, v75, v214, v55
	v_pk_fma_f16 v56, v76, v215, v56
	v_pk_add_f16 v74, v129, v162 neg_lo:[0,1] neg_hi:[0,1]
	v_pk_add_f16 v75, v128, v163 neg_lo:[0,1] neg_hi:[0,1]
	v_pk_add_f16 v76, v127, v164 neg_lo:[0,1] neg_hi:[0,1]
	v_pk_add_f16 v84, v84, v164 neg_lo:[0,1] neg_hi:[0,1]
	v_exp_f16_sdwa v118, v74 dst_sel:WORD_0 dst_unused:UNUSED_PAD src0_sel:WORD_0
	v_exp_f16_sdwa v119, v75 dst_sel:WORD_0 dst_unused:UNUSED_PAD src0_sel:WORD_0
	v_exp_f16_sdwa v120, v76 dst_sel:WORD_0 dst_unused:UNUSED_PAD src0_sel:WORD_0
	v_exp_f16_sdwa v121, v77 dst_sel:WORD_0 dst_unused:UNUSED_PAD src0_sel:WORD_0
	v_exp_f16_sdwa v118, v74 dst_sel:WORD_1 dst_unused:UNUSED_PRESERVE src0_sel:WORD_1
	v_exp_f16_sdwa v119, v75 dst_sel:WORD_1 dst_unused:UNUSED_PRESERVE src0_sel:WORD_1
	v_exp_f16_sdwa v120, v76 dst_sel:WORD_1 dst_unused:UNUSED_PRESERVE src0_sel:WORD_1
	v_exp_f16_sdwa v121, v77 dst_sel:WORD_1 dst_unused:UNUSED_PRESERVE src0_sel:WORD_1
	v_pk_add_f16 v85, v85, v165 neg_lo:[0,1] neg_hi:[0,1]
	v_pk_add_f16 v77, v97, v118
	v_pk_add_f16 v74, v94, v121
	v_pk_add_f16 v75, v95, v120
	v_pk_add_f16 v76, v96, v119
	v_pk_fma_f16 v57, v101, v121, v57
	v_pk_fma_f16 v56, v100, v120, v56
	v_pk_fma_f16 v55, v99, v119, v55
	v_pk_fma_f16 v54, v98, v118, v54
	v_pk_add_f16 v94, v137, v162 neg_lo:[0,1] neg_hi:[0,1]
	v_pk_add_f16 v95, v136, v163 neg_lo:[0,1] neg_hi:[0,1]
	v_pk_add_f16 v96, v135, v164 neg_lo:[0,1] neg_hi:[0,1]
	v_pk_add_f16 v97, v134, v165 neg_lo:[0,1] neg_hi:[0,1]
	v_exp_f16_sdwa v98, v94 dst_sel:WORD_0 dst_unused:UNUSED_PAD src0_sel:WORD_0
	v_exp_f16_sdwa v99, v95 dst_sel:WORD_0 dst_unused:UNUSED_PAD src0_sel:WORD_0
	v_exp_f16_sdwa v100, v96 dst_sel:WORD_0 dst_unused:UNUSED_PAD src0_sel:WORD_0
	v_exp_f16_sdwa v101, v97 dst_sel:WORD_0 dst_unused:UNUSED_PAD src0_sel:WORD_0
	v_exp_f16_sdwa v98, v94 dst_sel:WORD_1 dst_unused:UNUSED_PRESERVE src0_sel:WORD_1
	v_exp_f16_sdwa v99, v95 dst_sel:WORD_1 dst_unused:UNUSED_PRESERVE src0_sel:WORD_1
	v_exp_f16_sdwa v100, v96 dst_sel:WORD_1 dst_unused:UNUSED_PRESERVE src0_sel:WORD_1
	v_exp_f16_sdwa v101, v97 dst_sel:WORD_1 dst_unused:UNUSED_PRESERVE src0_sel:WORD_1
	v_pk_add_f16 v94, v149, v162 neg_lo:[0,1] neg_hi:[0,1]
	v_pk_add_f16 v77, v77, v98
	v_pk_add_f16 v76, v76, v99
	v_pk_add_f16 v75, v75, v100
	v_pk_add_f16 v74, v74, v101
	v_pk_fma_f16 v54, v30, v98, v54
	v_pk_fma_f16 v55, v31, v99, v55
	v_pk_fma_f16 v56, v32, v100, v56
	v_pk_fma_f16 v57, v33, v101, v57
	v_pk_add_f16 v95, v148, v163 neg_lo:[0,1] neg_hi:[0,1]
	v_pk_add_f16 v96, v147, v164 neg_lo:[0,1] neg_hi:[0,1]
	v_pk_add_f16 v97, v146, v165 neg_lo:[0,1] neg_hi:[0,1]
	v_exp_f16_sdwa v98, v94 dst_sel:WORD_0 dst_unused:UNUSED_PAD src0_sel:WORD_0
	v_exp_f16_sdwa v99, v95 dst_sel:WORD_0 dst_unused:UNUSED_PAD src0_sel:WORD_0
	v_exp_f16_sdwa v100, v96 dst_sel:WORD_0 dst_unused:UNUSED_PAD src0_sel:WORD_0
	v_exp_f16_sdwa v101, v97 dst_sel:WORD_0 dst_unused:UNUSED_PAD src0_sel:WORD_0
	v_exp_f16_sdwa v98, v94 dst_sel:WORD_1 dst_unused:UNUSED_PRESERVE src0_sel:WORD_1
	v_exp_f16_sdwa v99, v95 dst_sel:WORD_1 dst_unused:UNUSED_PRESERVE src0_sel:WORD_1
	v_exp_f16_sdwa v100, v96 dst_sel:WORD_1 dst_unused:UNUSED_PRESERVE src0_sel:WORD_1
	v_exp_f16_sdwa v101, v97 dst_sel:WORD_1 dst_unused:UNUSED_PRESERVE src0_sel:WORD_1
	v_pk_add_f16 v94, v212, v162 neg_lo:[0,1] neg_hi:[0,1]
	v_pk_add_f16 v77, v77, v98
	v_pk_add_f16 v74, v74, v101
	v_pk_add_f16 v75, v75, v100
	v_pk_add_f16 v76, v76, v99
	v_pk_fma_f16 v57, v45, v101, v57
	v_pk_fma_f16 v56, v44, v100, v56
	v_pk_fma_f16 v55, v43, v99, v55
	v_pk_fma_f16 v54, v42, v98, v54
	v_pk_add_f16 v95, v211, v163 neg_lo:[0,1] neg_hi:[0,1]
	v_pk_add_f16 v96, v210, v164 neg_lo:[0,1] neg_hi:[0,1]
	v_pk_add_f16 v97, v209, v165 neg_lo:[0,1] neg_hi:[0,1]
	v_exp_f16_sdwa v98, v94 dst_sel:WORD_0 dst_unused:UNUSED_PAD src0_sel:WORD_0
	v_exp_f16_sdwa v99, v95 dst_sel:WORD_0 dst_unused:UNUSED_PAD src0_sel:WORD_0
	v_exp_f16_sdwa v100, v96 dst_sel:WORD_0 dst_unused:UNUSED_PAD src0_sel:WORD_0
	v_exp_f16_sdwa v101, v97 dst_sel:WORD_0 dst_unused:UNUSED_PAD src0_sel:WORD_0
	v_exp_f16_sdwa v98, v94 dst_sel:WORD_1 dst_unused:UNUSED_PRESERVE src0_sel:WORD_1
	v_exp_f16_sdwa v99, v95 dst_sel:WORD_1 dst_unused:UNUSED_PRESERVE src0_sel:WORD_1
	v_exp_f16_sdwa v100, v96 dst_sel:WORD_1 dst_unused:UNUSED_PRESERVE src0_sel:WORD_1
	v_exp_f16_sdwa v101, v97 dst_sel:WORD_1 dst_unused:UNUSED_PRESERVE src0_sel:WORD_1
	v_exp_f16_sdwa v94, v82 dst_sel:WORD_0 dst_unused:UNUSED_PAD src0_sel:WORD_0
	v_exp_f16_sdwa v95, v83 dst_sel:WORD_0 dst_unused:UNUSED_PAD src0_sel:WORD_0
	v_exp_f16_sdwa v96, v84 dst_sel:WORD_0 dst_unused:UNUSED_PAD src0_sel:WORD_0
	v_exp_f16_sdwa v97, v85 dst_sel:WORD_0 dst_unused:UNUSED_PAD src0_sel:WORD_0
	v_exp_f16_sdwa v94, v82 dst_sel:WORD_1 dst_unused:UNUSED_PRESERVE src0_sel:WORD_1
	v_exp_f16_sdwa v95, v83 dst_sel:WORD_1 dst_unused:UNUSED_PRESERVE src0_sel:WORD_1
	v_exp_f16_sdwa v96, v84 dst_sel:WORD_1 dst_unused:UNUSED_PRESERVE src0_sel:WORD_1
	v_exp_f16_sdwa v97, v85 dst_sel:WORD_1 dst_unused:UNUSED_PRESERVE src0_sel:WORD_1
	v_pk_add_f16 v82, v106, v162 neg_lo:[0,1] neg_hi:[0,1]
	v_pk_add_f16 v77, v77, v98
	v_pk_add_f16 v76, v76, v99
	v_pk_add_f16 v75, v75, v100
	v_pk_add_f16 v74, v74, v101
	v_pk_fma_f16 v54, v58, v98, v54
	v_pk_fma_f16 v55, v59, v99, v55
	v_pk_fma_f16 v56, v60, v100, v56
	v_pk_fma_f16 v57, v61, v101, v57
	v_pk_add_f16 v77, v77, v94
	v_pk_add_f16 v74, v74, v97
	v_pk_add_f16 v75, v75, v96
	v_pk_add_f16 v76, v76, v95
	v_pk_fma_f16 v57, v21, v97, v57
	v_pk_fma_f16 v56, v20, v96, v56
	v_pk_fma_f16 v55, v19, v95, v55
	v_pk_fma_f16 v54, v18, v94, v54
	v_pk_add_f16 v83, v107, v163 neg_lo:[0,1] neg_hi:[0,1]
	v_pk_add_f16 v84, v108, v164 neg_lo:[0,1] neg_hi:[0,1]
	v_pk_add_f16 v85, v109, v165 neg_lo:[0,1] neg_hi:[0,1]
	v_exp_f16_sdwa v94, v82 dst_sel:WORD_0 dst_unused:UNUSED_PAD src0_sel:WORD_0
	v_exp_f16_sdwa v95, v83 dst_sel:WORD_0 dst_unused:UNUSED_PAD src0_sel:WORD_0
	v_exp_f16_sdwa v96, v84 dst_sel:WORD_0 dst_unused:UNUSED_PAD src0_sel:WORD_0
	v_exp_f16_sdwa v97, v85 dst_sel:WORD_0 dst_unused:UNUSED_PAD src0_sel:WORD_0
	v_exp_f16_sdwa v94, v82 dst_sel:WORD_1 dst_unused:UNUSED_PRESERVE src0_sel:WORD_1
	v_exp_f16_sdwa v95, v83 dst_sel:WORD_1 dst_unused:UNUSED_PRESERVE src0_sel:WORD_1
	v_exp_f16_sdwa v96, v84 dst_sel:WORD_1 dst_unused:UNUSED_PRESERVE src0_sel:WORD_1
	v_exp_f16_sdwa v97, v85 dst_sel:WORD_1 dst_unused:UNUSED_PRESERVE src0_sel:WORD_1
	v_pk_add_f16 v82, v122, v162 neg_lo:[0,1] neg_hi:[0,1]
	v_pk_add_f16 v77, v77, v94
	v_pk_add_f16 v76, v76, v95
	v_pk_add_f16 v75, v75, v96
	v_pk_add_f16 v74, v74, v97
	v_pk_fma_f16 v54, v22, v94, v54
	v_pk_fma_f16 v55, v23, v95, v55
	v_pk_fma_f16 v56, v24, v96, v56
	v_pk_fma_f16 v57, v25, v97, v57
	v_pk_add_f16 v83, v123, v163 neg_lo:[0,1] neg_hi:[0,1]
	v_pk_add_f16 v84, v124, v164 neg_lo:[0,1] neg_hi:[0,1]
	v_pk_add_f16 v85, v125, v165 neg_lo:[0,1] neg_hi:[0,1]
	v_exp_f16_sdwa v94, v82 dst_sel:WORD_0 dst_unused:UNUSED_PAD src0_sel:WORD_0
	v_exp_f16_sdwa v95, v83 dst_sel:WORD_0 dst_unused:UNUSED_PAD src0_sel:WORD_0
	v_exp_f16_sdwa v96, v84 dst_sel:WORD_0 dst_unused:UNUSED_PAD src0_sel:WORD_0
	v_exp_f16_sdwa v97, v85 dst_sel:WORD_0 dst_unused:UNUSED_PAD src0_sel:WORD_0
	v_exp_f16_sdwa v94, v82 dst_sel:WORD_1 dst_unused:UNUSED_PRESERVE src0_sel:WORD_1
	v_exp_f16_sdwa v95, v83 dst_sel:WORD_1 dst_unused:UNUSED_PRESERVE src0_sel:WORD_1
	v_exp_f16_sdwa v96, v84 dst_sel:WORD_1 dst_unused:UNUSED_PRESERVE src0_sel:WORD_1
	v_exp_f16_sdwa v97, v85 dst_sel:WORD_1 dst_unused:UNUSED_PRESERVE src0_sel:WORD_1
	v_pk_add_f16 v77, v77, v94
	v_pk_add_f16 v76, v76, v95
	v_rcp_f16_e32 v82, v77
	v_rcp_f16_sdwa v77, v77 dst_sel:DWORD dst_unused:UNUSED_PAD src0_sel:WORD_1
	v_pk_add_f16 v75, v75, v96
	v_rcp_f16_e32 v83, v76
	v_rcp_f16_sdwa v76, v76 dst_sel:DWORD dst_unused:UNUSED_PAD src0_sel:WORD_1
	v_pk_add_f16 v74, v74, v97
	v_rcp_f16_e32 v84, v75
	v_rcp_f16_sdwa v75, v75 dst_sel:DWORD dst_unused:UNUSED_PAD src0_sel:WORD_1
	v_rcp_f16_e32 v85, v74
	v_rcp_f16_sdwa v74, v74 dst_sel:DWORD dst_unused:UNUSED_PAD src0_sel:WORD_1
	v_pk_fma_f16 v54, v26, v94, v54
	v_pack_b32_f16 v77, v82, v77
	v_pk_fma_f16 v57, v29, v97, v57
	v_pk_fma_f16 v55, v27, v95, v55
	v_pk_mul_f16 v97, v54, v77
	v_pack_b32_f16 v54, v83, v76
	v_pk_fma_f16 v56, v28, v96, v56
	v_pk_mul_f16 v96, v55, v54
	v_pack_b32_f16 v54, v84, v75
	v_pk_mul_f16 v95, v56, v54
	v_pack_b32_f16 v54, v85, v74
	v_pk_mul_f16 v94, v57, v54
	s_waitcnt vmcnt(6)
	v_pk_mul_f16 v57, v208, v161 op_sel_hi:[0,1]
	v_pk_mul_f16 v77, v206, v161 op_sel_hi:[0,1]
	v_pk_mul_f16 v85, v207, v161 op_sel_hi:[0,1]
	v_pk_mul_f16 v54, v208, v158 op_sel_hi:[0,1]
	v_pk_mul_f16 v55, v208, v159 op_sel_hi:[0,1]
	v_pk_mul_f16 v56, v208, v160 op_sel_hi:[0,1]
	v_pk_mul_f16 v74, v206, v158 op_sel_hi:[0,1]
	v_pk_mul_f16 v75, v206, v159 op_sel_hi:[0,1]
	v_pk_mul_f16 v76, v206, v160 op_sel_hi:[0,1]
	v_pk_mul_f16 v82, v207, v158 op_sel_hi:[0,1]
	v_pk_mul_f16 v83, v207, v159 op_sel_hi:[0,1]
	v_pk_mul_f16 v84, v207, v160 op_sel_hi:[0,1]
	v_pk_fma_f16 v65, v65, v161, v57
	v_pk_fma_f16 v81, v81, v161, v77
	v_pk_fma_f16 v98, v105, v161, v85
	v_pk_fma_f16 v64, v64, v160, v56
	v_pk_maximum3_f16 v125, v65, v81, v98
	v_pk_fma_f16 v63, v63, v159, v55
	v_pk_fma_f16 v62, v62, v158, v54
	v_pk_fma_f16 v80, v80, v160, v76
	v_pk_fma_f16 v79, v79, v159, v75
	v_pk_fma_f16 v78, v78, v158, v74
	v_pk_fma_f16 v99, v104, v160, v84
	v_pk_fma_f16 v100, v103, v159, v83
	v_pk_fma_f16 v101, v102, v158, v82
	v_pk_fma_f16 v102, v37, v161, v57
	v_pk_fma_f16 v106, v49, v161, v77
	v_pk_fma_f16 v118, v69, v161, v85
	v_pk_fma_f16 v57, v89, v161, v57
	v_pk_fma_f16 v77, v117, v161, v77
	v_pk_fma_f16 v85, v133, v161, v85
	v_pk_maximum3_f16 v122, v62, v78, v101
	v_pk_maximum3_f16 v123, v63, v79, v100
	v_pk_maximum3_f16 v124, v64, v80, v99
	v_pk_maximum3_f16 v129, v102, v106, v118
	v_pk_fma_f16 v103, v36, v160, v56
	v_pk_maximum3_f16 v137, v57, v77, v85
	v_pk_fma_f16 v104, v35, v159, v55
	v_pk_maximum3_f16 v125, v125, v129, v137
	v_pk_fma_f16 v105, v34, v158, v54
	v_pk_fma_f16 v107, v48, v160, v76
	v_pk_fma_f16 v108, v47, v159, v75
	v_pk_fma_f16 v109, v46, v158, v74
	v_pk_fma_f16 v119, v68, v160, v84
	v_pk_fma_f16 v120, v67, v159, v83
	v_pk_fma_f16 v121, v66, v158, v82
	v_pk_fma_f16 v56, v88, v160, v56
	v_pk_fma_f16 v55, v87, v159, v55
	v_pk_fma_f16 v54, v86, v158, v54
	v_pk_fma_f16 v76, v116, v160, v76
	v_pk_fma_f16 v75, v115, v159, v75
	v_pk_fma_f16 v74, v114, v158, v74
	v_pk_fma_f16 v84, v132, v160, v84
	v_pk_fma_f16 v83, v131, v159, v83
	v_pk_fma_f16 v82, v130, v158, v82
	v_pk_maximum3_f16 v126, v105, v109, v121
	v_pk_maximum3_f16 v127, v104, v108, v120
	v_pk_maximum3_f16 v128, v103, v107, v119
	v_pk_maximum3_f16 v135, v55, v75, v83
	v_pk_maximum3_f16 v136, v56, v76, v84
	v_pk_maximum3_f16 v134, v54, v74, v82
	v_pk_maximum3_f16 v122, v122, v126, v134
	v_pk_maximum3_f16 v123, v123, v127, v135
	v_pk_maximum3_f16 v124, v124, v128, v136
	v_pk_add_f16 v65, v65, v125 neg_lo:[0,1] neg_hi:[0,1]
	v_pk_add_f16 v62, v62, v122 neg_lo:[0,1] neg_hi:[0,1]
	v_pk_add_f16 v63, v63, v123 neg_lo:[0,1] neg_hi:[0,1]
	v_pk_add_f16 v64, v64, v124 neg_lo:[0,1] neg_hi:[0,1]
	v_pk_add_f16 v78, v78, v122 neg_lo:[0,1] neg_hi:[0,1]
	v_exp_f16_sdwa v126, v62 dst_sel:WORD_0 dst_unused:UNUSED_PAD src0_sel:WORD_0
	v_exp_f16_sdwa v127, v63 dst_sel:WORD_0 dst_unused:UNUSED_PAD src0_sel:WORD_0
	v_exp_f16_sdwa v128, v64 dst_sel:WORD_0 dst_unused:UNUSED_PAD src0_sel:WORD_0
	v_exp_f16_sdwa v129, v65 dst_sel:WORD_0 dst_unused:UNUSED_PAD src0_sel:WORD_0
	v_exp_f16_sdwa v126, v62 dst_sel:WORD_1 dst_unused:UNUSED_PRESERVE src0_sel:WORD_1
	v_exp_f16_sdwa v127, v63 dst_sel:WORD_1 dst_unused:UNUSED_PRESERVE src0_sel:WORD_1
	v_exp_f16_sdwa v128, v64 dst_sel:WORD_1 dst_unused:UNUSED_PRESERVE src0_sel:WORD_1
	v_exp_f16_sdwa v129, v65 dst_sel:WORD_1 dst_unused:UNUSED_PRESERVE src0_sel:WORD_1
	v_pk_add_f16 v79, v79, v123 neg_lo:[0,1] neg_hi:[0,1]
	v_pk_add_f16 v65, v126, 0
	v_pk_fma_f16 v33, v33, v129, 0
	v_pk_add_f16 v62, v129, 0
	v_pk_add_f16 v63, v128, 0
	v_pk_add_f16 v64, v127, 0
	v_pk_fma_f16 v32, v32, v128, 0
	v_pk_fma_f16 v31, v31, v127, 0
	v_pk_fma_f16 v30, v30, v126, 0
	v_pk_add_f16 v80, v80, v124 neg_lo:[0,1] neg_hi:[0,1]
	v_pk_add_f16 v81, v81, v125 neg_lo:[0,1] neg_hi:[0,1]
	v_pk_add_f16 v54, v54, v122 neg_lo:[0,1] neg_hi:[0,1]
	v_exp_f16_sdwa v126, v78 dst_sel:WORD_0 dst_unused:UNUSED_PAD src0_sel:WORD_0
	v_exp_f16_sdwa v127, v79 dst_sel:WORD_0 dst_unused:UNUSED_PAD src0_sel:WORD_0
	v_exp_f16_sdwa v128, v80 dst_sel:WORD_0 dst_unused:UNUSED_PAD src0_sel:WORD_0
	v_exp_f16_sdwa v129, v81 dst_sel:WORD_0 dst_unused:UNUSED_PAD src0_sel:WORD_0
	v_exp_f16_sdwa v126, v78 dst_sel:WORD_1 dst_unused:UNUSED_PRESERVE src0_sel:WORD_1
	v_exp_f16_sdwa v127, v79 dst_sel:WORD_1 dst_unused:UNUSED_PRESERVE src0_sel:WORD_1
	v_exp_f16_sdwa v128, v80 dst_sel:WORD_1 dst_unused:UNUSED_PRESERVE src0_sel:WORD_1
	v_exp_f16_sdwa v129, v81 dst_sel:WORD_1 dst_unused:UNUSED_PRESERVE src0_sel:WORD_1
	v_pk_add_f16 v55, v55, v123 neg_lo:[0,1] neg_hi:[0,1]
	v_pk_add_f16 v65, v65, v126
	v_pk_fma_f16 v33, v45, v129, v33
	v_pk_add_f16 v45, v98, v125 neg_lo:[0,1] neg_hi:[0,1]
	v_pk_add_f16 v64, v64, v127
	v_pk_add_f16 v63, v63, v128
	v_pk_add_f16 v62, v62, v129
	v_pk_fma_f16 v30, v42, v126, v30
	v_pk_fma_f16 v31, v43, v127, v31
	v_pk_fma_f16 v32, v44, v128, v32
	v_pk_add_f16 v42, v101, v122 neg_lo:[0,1] neg_hi:[0,1]
	v_pk_add_f16 v43, v100, v123 neg_lo:[0,1] neg_hi:[0,1]
	v_pk_add_f16 v44, v99, v124 neg_lo:[0,1] neg_hi:[0,1]
	v_pk_add_f16 v56, v56, v124 neg_lo:[0,1] neg_hi:[0,1]
	v_exp_f16_sdwa v78, v42 dst_sel:WORD_0 dst_unused:UNUSED_PAD src0_sel:WORD_0
	v_exp_f16_sdwa v79, v43 dst_sel:WORD_0 dst_unused:UNUSED_PAD src0_sel:WORD_0
	v_exp_f16_sdwa v80, v44 dst_sel:WORD_0 dst_unused:UNUSED_PAD src0_sel:WORD_0
	v_exp_f16_sdwa v81, v45 dst_sel:WORD_0 dst_unused:UNUSED_PAD src0_sel:WORD_0
	v_exp_f16_sdwa v78, v42 dst_sel:WORD_1 dst_unused:UNUSED_PRESERVE src0_sel:WORD_1
	v_exp_f16_sdwa v79, v43 dst_sel:WORD_1 dst_unused:UNUSED_PRESERVE src0_sel:WORD_1
	v_exp_f16_sdwa v80, v44 dst_sel:WORD_1 dst_unused:UNUSED_PRESERVE src0_sel:WORD_1
	v_exp_f16_sdwa v81, v45 dst_sel:WORD_1 dst_unused:UNUSED_PRESERVE src0_sel:WORD_1
	v_pk_add_f16 v57, v57, v125 neg_lo:[0,1] neg_hi:[0,1]
	v_pk_add_f16 v45, v65, v78
	v_pk_add_f16 v42, v62, v81
	v_pk_add_f16 v43, v63, v80
	v_pk_add_f16 v44, v64, v79
	v_pk_fma_f16 v33, v61, v81, v33
	v_pk_fma_f16 v32, v60, v80, v32
	v_pk_fma_f16 v31, v59, v79, v31
	v_pk_fma_f16 v30, v58, v78, v30
	v_pk_add_f16 v58, v105, v122 neg_lo:[0,1] neg_hi:[0,1]
	v_pk_add_f16 v59, v104, v123 neg_lo:[0,1] neg_hi:[0,1]
	v_pk_add_f16 v60, v103, v124 neg_lo:[0,1] neg_hi:[0,1]
	v_pk_add_f16 v61, v102, v125 neg_lo:[0,1] neg_hi:[0,1]
	v_exp_f16_sdwa v62, v58 dst_sel:WORD_0 dst_unused:UNUSED_PAD src0_sel:WORD_0
	v_exp_f16_sdwa v63, v59 dst_sel:WORD_0 dst_unused:UNUSED_PAD src0_sel:WORD_0
	v_exp_f16_sdwa v64, v60 dst_sel:WORD_0 dst_unused:UNUSED_PAD src0_sel:WORD_0
	v_exp_f16_sdwa v65, v61 dst_sel:WORD_0 dst_unused:UNUSED_PAD src0_sel:WORD_0
	v_exp_f16_sdwa v62, v58 dst_sel:WORD_1 dst_unused:UNUSED_PRESERVE src0_sel:WORD_1
	v_exp_f16_sdwa v63, v59 dst_sel:WORD_1 dst_unused:UNUSED_PRESERVE src0_sel:WORD_1
	v_exp_f16_sdwa v64, v60 dst_sel:WORD_1 dst_unused:UNUSED_PRESERVE src0_sel:WORD_1
	v_exp_f16_sdwa v65, v61 dst_sel:WORD_1 dst_unused:UNUSED_PRESERVE src0_sel:WORD_1
	v_pk_add_f16 v58, v109, v122 neg_lo:[0,1] neg_hi:[0,1]
	v_pk_add_f16 v45, v45, v62
	v_pk_add_f16 v44, v44, v63
	v_pk_add_f16 v43, v43, v64
	v_pk_add_f16 v42, v42, v65
	v_pk_fma_f16 v30, v18, v62, v30
	v_pk_fma_f16 v31, v19, v63, v31
	v_pk_fma_f16 v32, v20, v64, v32
	v_pk_fma_f16 v33, v21, v65, v33
	v_pk_add_f16 v59, v108, v123 neg_lo:[0,1] neg_hi:[0,1]
	v_pk_add_f16 v60, v107, v124 neg_lo:[0,1] neg_hi:[0,1]
	v_pk_add_f16 v61, v106, v125 neg_lo:[0,1] neg_hi:[0,1]
	v_exp_f16_sdwa v62, v58 dst_sel:WORD_0 dst_unused:UNUSED_PAD src0_sel:WORD_0
	v_exp_f16_sdwa v63, v59 dst_sel:WORD_0 dst_unused:UNUSED_PAD src0_sel:WORD_0
	v_exp_f16_sdwa v64, v60 dst_sel:WORD_0 dst_unused:UNUSED_PAD src0_sel:WORD_0
	v_exp_f16_sdwa v65, v61 dst_sel:WORD_0 dst_unused:UNUSED_PAD src0_sel:WORD_0
	v_exp_f16_sdwa v62, v58 dst_sel:WORD_1 dst_unused:UNUSED_PRESERVE src0_sel:WORD_1
	v_exp_f16_sdwa v63, v59 dst_sel:WORD_1 dst_unused:UNUSED_PRESERVE src0_sel:WORD_1
	v_exp_f16_sdwa v64, v60 dst_sel:WORD_1 dst_unused:UNUSED_PRESERVE src0_sel:WORD_1
	v_exp_f16_sdwa v65, v61 dst_sel:WORD_1 dst_unused:UNUSED_PRESERVE src0_sel:WORD_1
	v_pk_add_f16 v58, v121, v122 neg_lo:[0,1] neg_hi:[0,1]
	v_pk_add_f16 v45, v45, v62
	v_pk_add_f16 v42, v42, v65
	v_pk_add_f16 v43, v43, v64
	v_pk_add_f16 v44, v44, v63
	v_pk_fma_f16 v33, v25, v65, v33
	v_pk_fma_f16 v32, v24, v64, v32
	v_pk_fma_f16 v31, v23, v63, v31
	v_pk_fma_f16 v30, v22, v62, v30
	v_pk_add_f16 v59, v120, v123 neg_lo:[0,1] neg_hi:[0,1]
	v_pk_add_f16 v60, v119, v124 neg_lo:[0,1] neg_hi:[0,1]
	v_pk_add_f16 v61, v118, v125 neg_lo:[0,1] neg_hi:[0,1]
	v_exp_f16_sdwa v62, v58 dst_sel:WORD_0 dst_unused:UNUSED_PAD src0_sel:WORD_0
	v_exp_f16_sdwa v63, v59 dst_sel:WORD_0 dst_unused:UNUSED_PAD src0_sel:WORD_0
	v_exp_f16_sdwa v64, v60 dst_sel:WORD_0 dst_unused:UNUSED_PAD src0_sel:WORD_0
	v_exp_f16_sdwa v65, v61 dst_sel:WORD_0 dst_unused:UNUSED_PAD src0_sel:WORD_0
	v_exp_f16_sdwa v62, v58 dst_sel:WORD_1 dst_unused:UNUSED_PRESERVE src0_sel:WORD_1
	v_exp_f16_sdwa v63, v59 dst_sel:WORD_1 dst_unused:UNUSED_PRESERVE src0_sel:WORD_1
	v_exp_f16_sdwa v64, v60 dst_sel:WORD_1 dst_unused:UNUSED_PRESERVE src0_sel:WORD_1
	v_exp_f16_sdwa v65, v61 dst_sel:WORD_1 dst_unused:UNUSED_PRESERVE src0_sel:WORD_1
	v_exp_f16_sdwa v58, v54 dst_sel:WORD_0 dst_unused:UNUSED_PAD src0_sel:WORD_0
	v_exp_f16_sdwa v59, v55 dst_sel:WORD_0 dst_unused:UNUSED_PAD src0_sel:WORD_0
	v_exp_f16_sdwa v60, v56 dst_sel:WORD_0 dst_unused:UNUSED_PAD src0_sel:WORD_0
	v_exp_f16_sdwa v61, v57 dst_sel:WORD_0 dst_unused:UNUSED_PAD src0_sel:WORD_0
	v_exp_f16_sdwa v58, v54 dst_sel:WORD_1 dst_unused:UNUSED_PRESERVE src0_sel:WORD_1
	v_exp_f16_sdwa v59, v55 dst_sel:WORD_1 dst_unused:UNUSED_PRESERVE src0_sel:WORD_1
	v_exp_f16_sdwa v60, v56 dst_sel:WORD_1 dst_unused:UNUSED_PRESERVE src0_sel:WORD_1
	v_exp_f16_sdwa v61, v57 dst_sel:WORD_1 dst_unused:UNUSED_PRESERVE src0_sel:WORD_1
	v_pk_add_f16 v54, v74, v122 neg_lo:[0,1] neg_hi:[0,1]
	v_pk_add_f16 v45, v45, v62
	v_pk_add_f16 v44, v44, v63
	v_pk_add_f16 v43, v43, v64
	v_pk_add_f16 v42, v42, v65
	v_pk_fma_f16 v30, v26, v62, v30
	v_pk_fma_f16 v31, v27, v63, v31
	v_pk_fma_f16 v32, v28, v64, v32
	v_pk_fma_f16 v33, v29, v65, v33
	v_pk_add_f16 v45, v45, v58
	v_pk_add_f16 v42, v42, v61
	v_pk_add_f16 v43, v43, v60
	v_pk_add_f16 v44, v44, v59
	v_pk_fma_f16 v33, v41, v61, v33
	v_pk_fma_f16 v32, v40, v60, v32
	v_pk_fma_f16 v31, v39, v59, v31
	v_pk_fma_f16 v30, v38, v58, v30
	v_pk_add_f16 v55, v75, v123 neg_lo:[0,1] neg_hi:[0,1]
	v_pk_add_f16 v56, v76, v124 neg_lo:[0,1] neg_hi:[0,1]
	v_pk_add_f16 v57, v77, v125 neg_lo:[0,1] neg_hi:[0,1]
	v_exp_f16_sdwa v58, v54 dst_sel:WORD_0 dst_unused:UNUSED_PAD src0_sel:WORD_0
	v_exp_f16_sdwa v59, v55 dst_sel:WORD_0 dst_unused:UNUSED_PAD src0_sel:WORD_0
	v_exp_f16_sdwa v60, v56 dst_sel:WORD_0 dst_unused:UNUSED_PAD src0_sel:WORD_0
	v_exp_f16_sdwa v61, v57 dst_sel:WORD_0 dst_unused:UNUSED_PAD src0_sel:WORD_0
	v_exp_f16_sdwa v58, v54 dst_sel:WORD_1 dst_unused:UNUSED_PRESERVE src0_sel:WORD_1
	v_exp_f16_sdwa v59, v55 dst_sel:WORD_1 dst_unused:UNUSED_PRESERVE src0_sel:WORD_1
	v_exp_f16_sdwa v60, v56 dst_sel:WORD_1 dst_unused:UNUSED_PRESERVE src0_sel:WORD_1
	v_exp_f16_sdwa v61, v57 dst_sel:WORD_1 dst_unused:UNUSED_PRESERVE src0_sel:WORD_1
	v_pk_add_f16 v54, v82, v122 neg_lo:[0,1] neg_hi:[0,1]
	v_pk_add_f16 v45, v45, v58
	v_pk_add_f16 v44, v44, v59
	v_pk_add_f16 v43, v43, v60
	v_pk_add_f16 v42, v42, v61
	v_pk_fma_f16 v30, v50, v58, v30
	v_pk_fma_f16 v31, v51, v59, v31
	v_pk_fma_f16 v32, v52, v60, v32
	v_pk_fma_f16 v33, v53, v61, v33
	v_pk_add_f16 v55, v83, v123 neg_lo:[0,1] neg_hi:[0,1]
	v_pk_add_f16 v56, v84, v124 neg_lo:[0,1] neg_hi:[0,1]
	v_pk_add_f16 v57, v85, v125 neg_lo:[0,1] neg_hi:[0,1]
	v_exp_f16_sdwa v58, v54 dst_sel:WORD_0 dst_unused:UNUSED_PAD src0_sel:WORD_0
	v_exp_f16_sdwa v59, v55 dst_sel:WORD_0 dst_unused:UNUSED_PAD src0_sel:WORD_0
	v_exp_f16_sdwa v60, v56 dst_sel:WORD_0 dst_unused:UNUSED_PAD src0_sel:WORD_0
	v_exp_f16_sdwa v61, v57 dst_sel:WORD_0 dst_unused:UNUSED_PAD src0_sel:WORD_0
	v_exp_f16_sdwa v58, v54 dst_sel:WORD_1 dst_unused:UNUSED_PRESERVE src0_sel:WORD_1
	v_exp_f16_sdwa v59, v55 dst_sel:WORD_1 dst_unused:UNUSED_PRESERVE src0_sel:WORD_1
	v_exp_f16_sdwa v60, v56 dst_sel:WORD_1 dst_unused:UNUSED_PRESERVE src0_sel:WORD_1
	v_exp_f16_sdwa v61, v57 dst_sel:WORD_1 dst_unused:UNUSED_PRESERVE src0_sel:WORD_1
	v_pk_add_f16 v45, v45, v58
	v_pk_add_f16 v44, v44, v59
	v_rcp_f16_e32 v54, v45
	v_rcp_f16_sdwa v45, v45 dst_sel:DWORD dst_unused:UNUSED_PAD src0_sel:WORD_1
	v_pk_add_f16 v43, v43, v60
	v_rcp_f16_e32 v55, v44
	v_rcp_f16_sdwa v44, v44 dst_sel:DWORD dst_unused:UNUSED_PAD src0_sel:WORD_1
	v_pk_add_f16 v42, v42, v61
	v_rcp_f16_e32 v56, v43
	v_rcp_f16_sdwa v43, v43 dst_sel:DWORD dst_unused:UNUSED_PAD src0_sel:WORD_1
	v_rcp_f16_e32 v57, v42
	v_rcp_f16_sdwa v42, v42 dst_sel:DWORD dst_unused:UNUSED_PAD src0_sel:WORD_1
	v_pk_fma_f16 v30, v70, v58, v30
	v_pack_b32_f16 v45, v54, v45
	v_pk_fma_f16 v31, v71, v59, v31
	v_pk_mul_f16 v45, v30, v45
	v_pack_b32_f16 v30, v55, v44
	v_pk_fma_f16 v32, v72, v60, v32
	v_pk_mul_f16 v44, v31, v30
	v_pack_b32_f16 v30, v56, v43
	v_pk_fma_f16 v33, v73, v61, v33
	v_pk_mul_f16 v43, v32, v30
	v_pack_b32_f16 v30, v57, v42
	v_pk_mul_f16 v42, v33, v30
	s_waitcnt vmcnt(0)
	v_pk_mul_f16 v30, v208, v154 op_sel_hi:[0,1]
	v_pk_mul_f16 v31, v208, v155 op_sel_hi:[0,1]
	v_pk_mul_f16 v32, v208, v156 op_sel_hi:[0,1]
	v_pk_mul_f16 v33, v208, v157 op_sel_hi:[0,1]
	v_pk_mul_f16 v54, v206, v154 op_sel_hi:[0,1]
	v_pk_mul_f16 v55, v206, v155 op_sel_hi:[0,1]
	v_pk_mul_f16 v56, v206, v156 op_sel_hi:[0,1]
	v_pk_mul_f16 v57, v206, v157 op_sel_hi:[0,1]
	v_pk_mul_f16 v58, v207, v154 op_sel_hi:[0,1]
	v_pk_mul_f16 v59, v207, v155 op_sel_hi:[0,1]
	v_pk_mul_f16 v60, v207, v156 op_sel_hi:[0,1]
	v_pk_mul_f16 v61, v207, v157 op_sel_hi:[0,1]
	v_pk_fma_f16 v37, v37, v157, v33
	v_pk_fma_f16 v36, v36, v156, v32
	v_pk_fma_f16 v35, v35, v155, v31
	v_pk_fma_f16 v34, v34, v154, v30
	v_pk_fma_f16 v49, v49, v157, v57
	v_pk_fma_f16 v48, v48, v156, v56
	v_pk_fma_f16 v47, v47, v155, v55
	v_pk_fma_f16 v46, v46, v154, v54
	v_pk_fma_f16 v62, v69, v157, v61
	v_pk_fma_f16 v63, v68, v156, v60
	v_pk_fma_f16 v64, v67, v155, v59
	v_pk_fma_f16 v65, v66, v154, v58
	v_pk_fma_f16 v66, v89, v157, v33
	v_pk_fma_f16 v67, v88, v156, v32
	v_pk_fma_f16 v68, v87, v155, v31
	v_pk_fma_f16 v69, v86, v154, v30
	v_pk_fma_f16 v74, v117, v157, v57
	v_pk_fma_f16 v75, v116, v156, v56
	v_pk_fma_f16 v76, v115, v155, v55
	v_pk_fma_f16 v77, v114, v154, v54
	v_pk_fma_f16 v78, v133, v157, v61
	v_pk_fma_f16 v79, v132, v156, v60
	v_pk_fma_f16 v80, v131, v155, v59
	v_pk_fma_f16 v81, v130, v154, v58
	v_pk_fma_f16 v61, v17, v157, v61
	v_pk_fma_f16 v60, v16, v156, v60
	v_pk_fma_f16 v59, v15, v155, v59
	v_pk_fma_f16 v58, v14, v154, v58
	v_pk_maximum3_f16 v14, v34, v46, v65
	v_pk_maximum3_f16 v15, v35, v47, v64
	v_pk_maximum3_f16 v16, v36, v48, v63
	v_pk_maximum3_f16 v17, v37, v49, v62
	v_pk_maximum3_f16 v82, v69, v77, v81
	v_pk_maximum3_f16 v83, v68, v76, v80
	v_pk_maximum3_f16 v84, v67, v75, v79
	v_pk_maximum3_f16 v85, v66, v74, v78
	v_pk_fma_f16 v33, v145, v157, v33
	v_pk_fma_f16 v32, v144, v156, v32
	v_pk_fma_f16 v31, v143, v155, v31
	v_pk_fma_f16 v30, v142, v154, v30
	v_pk_fma_f16 v57, v153, v157, v57
	v_pk_fma_f16 v56, v152, v156, v56
	v_pk_fma_f16 v55, v151, v155, v55
	v_pk_fma_f16 v54, v150, v154, v54
	v_pk_maximum3_f16 v87, v31, v55, v59
	v_pk_maximum3_f16 v88, v32, v56, v60
	v_pk_maximum3_f16 v89, v33, v57, v61
	v_pk_maximum3_f16 v86, v30, v54, v58
	v_pk_maximum3_f16 v15, v15, v83, v87
	v_pk_maximum3_f16 v16, v16, v84, v88
	v_pk_maximum3_f16 v17, v17, v85, v89
	v_pk_maximum3_f16 v14, v14, v82, v86
	v_xor_b32_e32 v82, 0x80008000, v17
	v_xor_b32_e32 v83, 0x80008000, v16
	v_xor_b32_e32 v84, 0x80008000, v15
	v_xor_b32_e32 v85, 0x80008000, v14
	v_pk_add_f16 v14, v34, v85
	v_pk_add_f16 v15, v35, v84
	v_pk_add_f16 v16, v36, v83
	v_pk_add_f16 v17, v37, v82
	v_exp_f16_sdwa v34, v14 dst_sel:WORD_0 dst_unused:UNUSED_PAD src0_sel:WORD_0
	v_exp_f16_sdwa v35, v15 dst_sel:WORD_0 dst_unused:UNUSED_PAD src0_sel:WORD_0
	v_exp_f16_sdwa v36, v16 dst_sel:WORD_0 dst_unused:UNUSED_PAD src0_sel:WORD_0
	v_exp_f16_sdwa v37, v17 dst_sel:WORD_0 dst_unused:UNUSED_PAD src0_sel:WORD_0
	v_exp_f16_sdwa v34, v14 dst_sel:WORD_1 dst_unused:UNUSED_PRESERVE src0_sel:WORD_1
	v_exp_f16_sdwa v35, v15 dst_sel:WORD_1 dst_unused:UNUSED_PRESERVE src0_sel:WORD_1
	v_exp_f16_sdwa v36, v16 dst_sel:WORD_1 dst_unused:UNUSED_PRESERVE src0_sel:WORD_1
	v_exp_f16_sdwa v37, v17 dst_sel:WORD_1 dst_unused:UNUSED_PRESERVE src0_sel:WORD_1
	v_pk_add_f16 v14, v34, 0
	v_pk_add_f16 v15, v35, 0
	v_pk_add_f16 v16, v36, 0
	v_pk_add_f16 v17, v37, 0
	v_pk_fma_f16 v18, v18, v34, 0
	v_pk_fma_f16 v19, v19, v35, 0
	v_pk_fma_f16 v20, v20, v36, 0
	v_pk_fma_f16 v21, v21, v37, 0
	v_pk_add_f16 v34, v46, v85
	v_pk_add_f16 v35, v47, v84
	v_pk_add_f16 v36, v48, v83
	v_pk_add_f16 v37, v49, v82
	v_exp_f16_sdwa v46, v34 dst_sel:WORD_0 dst_unused:UNUSED_PAD src0_sel:WORD_0
	v_exp_f16_sdwa v47, v35 dst_sel:WORD_0 dst_unused:UNUSED_PAD src0_sel:WORD_0
	v_exp_f16_sdwa v48, v36 dst_sel:WORD_0 dst_unused:UNUSED_PAD src0_sel:WORD_0
	v_exp_f16_sdwa v49, v37 dst_sel:WORD_0 dst_unused:UNUSED_PAD src0_sel:WORD_0
	v_exp_f16_sdwa v46, v34 dst_sel:WORD_1 dst_unused:UNUSED_PRESERVE src0_sel:WORD_1
	v_exp_f16_sdwa v47, v35 dst_sel:WORD_1 dst_unused:UNUSED_PRESERVE src0_sel:WORD_1
	v_exp_f16_sdwa v48, v36 dst_sel:WORD_1 dst_unused:UNUSED_PRESERVE src0_sel:WORD_1
	v_exp_f16_sdwa v49, v37 dst_sel:WORD_1 dst_unused:UNUSED_PRESERVE src0_sel:WORD_1
	s_nop 0
	v_pk_add_f16 v17, v17, v49
	v_pk_add_f16 v16, v16, v48
	v_pk_add_f16 v15, v15, v47
	v_pk_add_f16 v14, v14, v46
	v_pk_fma_f16 v21, v25, v49, v21
	v_pk_fma_f16 v20, v24, v48, v20
	v_pk_fma_f16 v19, v23, v47, v19
	v_pk_fma_f16 v18, v22, v46, v18
	v_pk_add_f16 v22, v65, v85
	v_pk_add_f16 v23, v64, v84
	v_pk_add_f16 v24, v63, v83
	v_pk_add_f16 v25, v62, v82
	v_exp_f16_sdwa v34, v22 dst_sel:WORD_0 dst_unused:UNUSED_PAD src0_sel:WORD_0
	v_exp_f16_sdwa v35, v23 dst_sel:WORD_0 dst_unused:UNUSED_PAD src0_sel:WORD_0
	v_exp_f16_sdwa v36, v24 dst_sel:WORD_0 dst_unused:UNUSED_PAD src0_sel:WORD_0
	v_exp_f16_sdwa v37, v25 dst_sel:WORD_0 dst_unused:UNUSED_PAD src0_sel:WORD_0
	v_exp_f16_sdwa v34, v22 dst_sel:WORD_1 dst_unused:UNUSED_PRESERVE src0_sel:WORD_1
	v_exp_f16_sdwa v35, v23 dst_sel:WORD_1 dst_unused:UNUSED_PRESERVE src0_sel:WORD_1
	v_exp_f16_sdwa v36, v24 dst_sel:WORD_1 dst_unused:UNUSED_PRESERVE src0_sel:WORD_1
	v_exp_f16_sdwa v37, v25 dst_sel:WORD_1 dst_unused:UNUSED_PRESERVE src0_sel:WORD_1
	v_pk_add_f16 v22, v69, v85
	v_pk_add_f16 v14, v14, v34
	v_pk_add_f16 v15, v15, v35
	v_pk_add_f16 v16, v16, v36
	v_pk_add_f16 v17, v17, v37
	v_pk_fma_f16 v18, v26, v34, v18
	v_pk_fma_f16 v19, v27, v35, v19
	v_pk_fma_f16 v20, v28, v36, v20
	v_pk_fma_f16 v21, v29, v37, v21
	v_pk_add_f16 v23, v68, v84
	v_pk_add_f16 v24, v67, v83
	v_pk_add_f16 v25, v66, v82
	v_exp_f16_sdwa v26, v22 dst_sel:WORD_0 dst_unused:UNUSED_PAD src0_sel:WORD_0
	v_exp_f16_sdwa v27, v23 dst_sel:WORD_0 dst_unused:UNUSED_PAD src0_sel:WORD_0
	v_exp_f16_sdwa v28, v24 dst_sel:WORD_0 dst_unused:UNUSED_PAD src0_sel:WORD_0
	v_exp_f16_sdwa v29, v25 dst_sel:WORD_0 dst_unused:UNUSED_PAD src0_sel:WORD_0
	v_exp_f16_sdwa v26, v22 dst_sel:WORD_1 dst_unused:UNUSED_PRESERVE src0_sel:WORD_1
	v_exp_f16_sdwa v27, v23 dst_sel:WORD_1 dst_unused:UNUSED_PRESERVE src0_sel:WORD_1
	v_exp_f16_sdwa v28, v24 dst_sel:WORD_1 dst_unused:UNUSED_PRESERVE src0_sel:WORD_1
	v_exp_f16_sdwa v29, v25 dst_sel:WORD_1 dst_unused:UNUSED_PRESERVE src0_sel:WORD_1
	v_pk_add_f16 v22, v77, v85
	v_pk_add_f16 v17, v17, v29
	v_pk_add_f16 v16, v16, v28
	v_pk_add_f16 v15, v15, v27
	v_pk_add_f16 v14, v14, v26
	v_pk_fma_f16 v21, v41, v29, v21
	v_pk_fma_f16 v20, v40, v28, v20
	v_pk_fma_f16 v19, v39, v27, v19
	v_pk_fma_f16 v18, v38, v26, v18
	v_pk_add_f16 v23, v76, v84
	v_pk_add_f16 v24, v75, v83
	v_pk_add_f16 v25, v74, v82
	v_exp_f16_sdwa v26, v22 dst_sel:WORD_0 dst_unused:UNUSED_PAD src0_sel:WORD_0
	v_exp_f16_sdwa v27, v23 dst_sel:WORD_0 dst_unused:UNUSED_PAD src0_sel:WORD_0
	v_exp_f16_sdwa v28, v24 dst_sel:WORD_0 dst_unused:UNUSED_PAD src0_sel:WORD_0
	v_exp_f16_sdwa v29, v25 dst_sel:WORD_0 dst_unused:UNUSED_PAD src0_sel:WORD_0
	v_exp_f16_sdwa v26, v22 dst_sel:WORD_1 dst_unused:UNUSED_PRESERVE src0_sel:WORD_1
	v_exp_f16_sdwa v27, v23 dst_sel:WORD_1 dst_unused:UNUSED_PRESERVE src0_sel:WORD_1
	v_exp_f16_sdwa v28, v24 dst_sel:WORD_1 dst_unused:UNUSED_PRESERVE src0_sel:WORD_1
	v_exp_f16_sdwa v29, v25 dst_sel:WORD_1 dst_unused:UNUSED_PRESERVE src0_sel:WORD_1
	v_pk_add_f16 v22, v81, v85
	v_pk_add_f16 v14, v14, v26
	v_pk_add_f16 v15, v15, v27
	v_pk_add_f16 v16, v16, v28
	v_pk_add_f16 v17, v17, v29
	v_pk_fma_f16 v18, v50, v26, v18
	v_pk_fma_f16 v19, v51, v27, v19
	v_pk_fma_f16 v20, v52, v28, v20
	v_pk_fma_f16 v21, v53, v29, v21
	v_pk_add_f16 v23, v80, v84
	v_pk_add_f16 v24, v79, v83
	v_pk_add_f16 v25, v78, v82
	v_exp_f16_sdwa v26, v22 dst_sel:WORD_0 dst_unused:UNUSED_PAD src0_sel:WORD_0
	v_exp_f16_sdwa v27, v23 dst_sel:WORD_0 dst_unused:UNUSED_PAD src0_sel:WORD_0
	v_exp_f16_sdwa v28, v24 dst_sel:WORD_0 dst_unused:UNUSED_PAD src0_sel:WORD_0
	v_exp_f16_sdwa v29, v25 dst_sel:WORD_0 dst_unused:UNUSED_PAD src0_sel:WORD_0
	v_exp_f16_sdwa v26, v22 dst_sel:WORD_1 dst_unused:UNUSED_PRESERVE src0_sel:WORD_1
	v_exp_f16_sdwa v27, v23 dst_sel:WORD_1 dst_unused:UNUSED_PRESERVE src0_sel:WORD_1
	v_exp_f16_sdwa v28, v24 dst_sel:WORD_1 dst_unused:UNUSED_PRESERVE src0_sel:WORD_1
	v_exp_f16_sdwa v29, v25 dst_sel:WORD_1 dst_unused:UNUSED_PRESERVE src0_sel:WORD_1
	v_pk_add_f16 v22, v30, v85
	v_pk_add_f16 v17, v17, v29
	v_pk_add_f16 v16, v16, v28
	v_pk_add_f16 v15, v15, v27
	v_pk_add_f16 v14, v14, v26
	v_pk_fma_f16 v21, v73, v29, v21
	v_pk_fma_f16 v20, v72, v28, v20
	v_pk_fma_f16 v19, v71, v27, v19
	v_pk_fma_f16 v18, v70, v26, v18
	v_pk_add_f16 v23, v31, v84
	v_pk_add_f16 v24, v32, v83
	v_pk_add_f16 v25, v33, v82
	v_exp_f16_sdwa v26, v22 dst_sel:WORD_0 dst_unused:UNUSED_PAD src0_sel:WORD_0
	v_exp_f16_sdwa v27, v23 dst_sel:WORD_0 dst_unused:UNUSED_PAD src0_sel:WORD_0
	v_exp_f16_sdwa v28, v24 dst_sel:WORD_0 dst_unused:UNUSED_PAD src0_sel:WORD_0
	v_exp_f16_sdwa v29, v25 dst_sel:WORD_0 dst_unused:UNUSED_PAD src0_sel:WORD_0
	v_exp_f16_sdwa v26, v22 dst_sel:WORD_1 dst_unused:UNUSED_PRESERVE src0_sel:WORD_1
	v_exp_f16_sdwa v27, v23 dst_sel:WORD_1 dst_unused:UNUSED_PRESERVE src0_sel:WORD_1
	v_exp_f16_sdwa v28, v24 dst_sel:WORD_1 dst_unused:UNUSED_PRESERVE src0_sel:WORD_1
	v_exp_f16_sdwa v29, v25 dst_sel:WORD_1 dst_unused:UNUSED_PRESERVE src0_sel:WORD_1
	v_pk_add_f16 v22, v54, v85
	v_pk_add_f16 v14, v14, v26
	v_pk_add_f16 v15, v15, v27
	v_pk_add_f16 v16, v16, v28
	v_pk_add_f16 v17, v17, v29
	v_pk_fma_f16 v18, v90, v26, v18
	v_pk_fma_f16 v19, v91, v27, v19
	v_pk_fma_f16 v20, v92, v28, v20
	v_pk_fma_f16 v21, v93, v29, v21
	v_pk_add_f16 v23, v55, v84
	v_pk_add_f16 v24, v56, v83
	v_pk_add_f16 v25, v57, v82
	v_exp_f16_sdwa v26, v22 dst_sel:WORD_0 dst_unused:UNUSED_PAD src0_sel:WORD_0
	v_exp_f16_sdwa v27, v23 dst_sel:WORD_0 dst_unused:UNUSED_PAD src0_sel:WORD_0
	v_exp_f16_sdwa v28, v24 dst_sel:WORD_0 dst_unused:UNUSED_PAD src0_sel:WORD_0
	v_exp_f16_sdwa v29, v25 dst_sel:WORD_0 dst_unused:UNUSED_PAD src0_sel:WORD_0
	v_exp_f16_sdwa v26, v22 dst_sel:WORD_1 dst_unused:UNUSED_PRESERVE src0_sel:WORD_1
	v_exp_f16_sdwa v27, v23 dst_sel:WORD_1 dst_unused:UNUSED_PRESERVE src0_sel:WORD_1
	v_exp_f16_sdwa v28, v24 dst_sel:WORD_1 dst_unused:UNUSED_PRESERVE src0_sel:WORD_1
	v_exp_f16_sdwa v29, v25 dst_sel:WORD_1 dst_unused:UNUSED_PRESERVE src0_sel:WORD_1
	s_nop 0
	v_pk_add_f16 v17, v17, v29
	v_pk_add_f16 v16, v16, v28
	v_pk_add_f16 v15, v15, v27
	v_pk_add_f16 v14, v14, v26
	v_pk_fma_f16 v21, v113, v29, v21
	v_pk_fma_f16 v20, v112, v28, v20
	v_pk_fma_f16 v19, v111, v27, v19
	v_pk_fma_f16 v18, v110, v26, v18
	v_pk_add_f16 v26, v58, v85
	v_pk_add_f16 v27, v59, v84
	v_pk_add_f16 v28, v60, v83
	v_pk_add_f16 v29, v61, v82
	v_exp_f16_sdwa v22, v26 dst_sel:WORD_0 dst_unused:UNUSED_PAD src0_sel:WORD_0
	v_exp_f16_sdwa v23, v27 dst_sel:WORD_0 dst_unused:UNUSED_PAD src0_sel:WORD_0
	v_exp_f16_sdwa v24, v28 dst_sel:WORD_0 dst_unused:UNUSED_PAD src0_sel:WORD_0
	v_exp_f16_sdwa v25, v29 dst_sel:WORD_0 dst_unused:UNUSED_PAD src0_sel:WORD_0
	v_exp_f16_sdwa v22, v26 dst_sel:WORD_1 dst_unused:UNUSED_PRESERVE src0_sel:WORD_1
	v_exp_f16_sdwa v23, v27 dst_sel:WORD_1 dst_unused:UNUSED_PRESERVE src0_sel:WORD_1
	v_exp_f16_sdwa v24, v28 dst_sel:WORD_1 dst_unused:UNUSED_PRESERVE src0_sel:WORD_1
	v_exp_f16_sdwa v25, v29 dst_sel:WORD_1 dst_unused:UNUSED_PRESERVE src0_sel:WORD_1
	s_nop 0
.LBB4_118:
	s_and_b64 vcc, exec, s[4:5]
	s_cbranch_vccz .LBB4_3
	global_load_dwordx3 v[146:148], v169, s[16:17]
	s_mov_b32 s14, s38
	s_mov_b32 s15, s39
	v_cmp_lt_u32_e64 s[64:65], 0, v199
	v_cmp_gt_u32_e64 s[66:67], 63, v199
	v_cmp_lt_u32_e64 s[68:69], 0, v180
	v_cmp_gt_u32_e64 s[70:71], 60, v180
	buffer_load_dwordx4 v[162:165], v200, s[12:15], 0 offen
	s_and_b64 s[72:73], s[68:69], s[64:65]
	s_and_b64 s[74:75], s[68:69], s[66:67]
	s_and_b64 s[76:77], s[70:71], s[64:65]
	s_and_b64 s[78:79], s[70:71], s[66:67]
	v_mov_b32_e32 v114, v6
	v_mov_b32_e32 v115, v7
	v_mov_b32_e32 v116, v8
	v_mov_b32_e32 v117, v9
	v_mov_b32_e32 v70, v2
	v_mov_b32_e32 v71, v3
	v_mov_b32_e32 v72, v4
	v_mov_b32_e32 v73, v5
	v_mov_b32_e32 v130, v6
	v_mov_b32_e32 v131, v7
	v_mov_b32_e32 v132, v8
	v_mov_b32_e32 v133, v9
	v_mov_b32_e32 v94, v2
	v_mov_b32_e32 v95, v3
	v_mov_b32_e32 v96, v4
	v_mov_b32_e32 v97, v5
	v_mov_b32_e32 v138, v6
	v_mov_b32_e32 v139, v7
	v_mov_b32_e32 v140, v8
	v_mov_b32_e32 v141, v9
	v_mov_b32_e32 v118, v2
	v_mov_b32_e32 v119, v3
	v_mov_b32_e32 v120, v4
	v_mov_b32_e32 v121, v5
	v_mov_b32_e32 v86, v6
	v_mov_b32_e32 v87, v7
	v_mov_b32_e32 v88, v8
	v_mov_b32_e32 v89, v9
	v_mov_b32_e32 v42, v2
	v_mov_b32_e32 v43, v3
	v_mov_b32_e32 v44, v4
	v_mov_b32_e32 v45, v5
	v_mov_b32_e32 v126, v6
	v_mov_b32_e32 v127, v7
	v_mov_b32_e32 v128, v8
	v_mov_b32_e32 v129, v9
	v_mov_b32_e32 v90, v2
	v_mov_b32_e32 v91, v3
	v_mov_b32_e32 v92, v4
	v_mov_b32_e32 v93, v5
	v_mov_b32_e32 v54, v6
	v_mov_b32_e32 v55, v7
	v_mov_b32_e32 v56, v8
	v_mov_b32_e32 v57, v9
	v_mov_b32_e32 v22, v2
	v_mov_b32_e32 v23, v3
	v_mov_b32_e32 v24, v4
	v_mov_b32_e32 v25, v5
	v_mov_b32_e32 v98, v6
	v_mov_b32_e32 v99, v7
	v_mov_b32_e32 v100, v8
	v_mov_b32_e32 v101, v9
	v_mov_b32_e32 v50, v2
	v_mov_b32_e32 v51, v3
	v_mov_b32_e32 v52, v4
	v_mov_b32_e32 v53, v5
	v_mov_b32_e32 v26, v6
	v_mov_b32_e32 v27, v7
	v_mov_b32_e32 v28, v8
	v_mov_b32_e32 v29, v9
	v_mov_b32_e32 v10, v2
	v_mov_b32_e32 v11, v3
	v_mov_b32_e32 v12, v4
	v_mov_b32_e32 v13, v5
	v_mov_b32_e32 v58, v6
	v_mov_b32_e32 v59, v7
	v_mov_b32_e32 v60, v8
	v_mov_b32_e32 v61, v9
	v_mov_b32_e32 v18, v2
	v_mov_b32_e32 v19, v3
	v_mov_b32_e32 v20, v4
	v_mov_b32_e32 v21, v5
	v_mov_b32_e32 v78, v6
	v_mov_b32_e32 v79, v7
	v_mov_b32_e32 v80, v8
	v_mov_b32_e32 v81, v9
	v_mov_b32_e32 v30, v2
	v_mov_b32_e32 v31, v3
	v_mov_b32_e32 v32, v4
	v_mov_b32_e32 v33, v5
	v_mov_b32_e32 v122, v6
	v_mov_b32_e32 v123, v7
	v_mov_b32_e32 v124, v8
	v_mov_b32_e32 v125, v9
	v_mov_b32_e32 v62, v2
	v_mov_b32_e32 v63, v3
	v_mov_b32_e32 v64, v4
	v_mov_b32_e32 v65, v5
	v_mov_b32_e32 v134, v6
	v_mov_b32_e32 v135, v7
	v_mov_b32_e32 v136, v8
	v_mov_b32_e32 v137, v9
	v_mov_b32_e32 v82, v2
	v_mov_b32_e32 v83, v3
	v_mov_b32_e32 v84, v4
	v_mov_b32_e32 v85, v5
	v_mov_b32_e32 v142, v6
	v_mov_b32_e32 v143, v7
	v_mov_b32_e32 v144, v8
	v_mov_b32_e32 v145, v9
	v_mov_b32_e32 v102, v2
	v_mov_b32_e32 v103, v3
	v_mov_b32_e32 v104, v4
	v_mov_b32_e32 v105, v5
	v_add_u32_e32 v245, 0xfffe7c00, v200
	v_add_u32_e32 v246, 0xfffe8000, v200
	s_mov_b64 exec, s[72:73]
	buffer_load_dwordx4 v[114:117], v245, s[12:15], 0 offen
	buffer_load_dwordx4 v[70:73], v245, s[12:15], 0 offen offset:512
	s_mov_b64 exec, -1
	s_mov_b64 exec, s[68:69]
	buffer_load_dwordx4 v[130:133], v246, s[12:15], 0 offen offset:512
	buffer_load_dwordx4 v[94:97], v246, s[12:15], 0 offen offset:1024
	s_mov_b64 exec, -1
	s_mov_b64 exec, s[74:75]
	buffer_load_dwordx4 v[138:141], v246, s[12:15], 0 offen offset:2048
	buffer_load_dwordx4 v[118:121], v246, s[12:15], 0 offen offset:2560
	s_mov_b64 exec, -1
	v_add_u32_e32 v245, 0xfffffc00, v200
	s_mov_b64 exec, s[64:65]
	buffer_load_dwordx4 v[86:89], v245, s[12:15], 0 offen
	buffer_load_dwordx4 v[42:45], v245, s[12:15], 0 offen offset:512
	s_mov_b64 exec, -1
	buffer_load_dwordx4 v[110:113], v200, s[12:15], 0 offen offset:512
	buffer_load_dwordx4 v[66:69], v200, s[12:15], 0 offen offset:1024
	s_mov_b64 exec, s[66:67]
	buffer_load_dwordx4 v[126:129], v200, s[12:15], 0 offen offset:2048
	buffer_load_dwordx4 v[90:93], v200, s[12:15], 0 offen offset:2560
	s_mov_b64 exec, -1
	v_add_u32_e32 v245, 0x17c00, v200
	v_add_u32_e32 v246, 0x18000, v200
	s_mov_b64 exec, s[64:65]
	buffer_load_dwordx4 v[54:57], v245, s[12:15], 0 offen
	buffer_load_dwordx4 v[22:25], v245, s[12:15], 0 offen offset:512
	s_mov_b64 exec, -1
	buffer_load_dwordx4 v[74:77], v246, s[12:15], 0 offen offset:512
	buffer_load_dwordx4 v[34:37], v246, s[12:15], 0 offen offset:1024
	s_mov_b64 exec, s[66:67]
	buffer_load_dwordx4 v[98:101], v246, s[12:15], 0 offen offset:2048
	buffer_load_dwordx4 v[50:53], v246, s[12:15], 0 offen offset:2560
	s_mov_b64 exec, -1
	v_add_u32_e32 v245, 0x18000, v200
	buffer_load_dwordx4 v[154:157], v245, s[12:15], 0 offen
	v_add_u32_e32 v246, 0x30000, v200
	buffer_load_dwordx4 v[150:153], v246, s[12:15], 0 offen
	v_add_u32_e32 v245, 0x2fc00, v200
	v_add_u32_e32 v246, 0x30000, v200
	v_add_u32_e32 v247, 0x47c00, v200
	v_add_u32_e32 v248, 0x48000, v200
	v_add_u32_e32 v249, 0x5fc00, v200
	v_add_u32_e32 v250, 0x60000, v200
	s_waitcnt vmcnt(21)
	v_cvt_f16_f32_e32 v158, v147
	v_cvt_f16_f32_e32 v160, v146
	v_cvt_f16_f32_e32 v159, v148
	v_add_u32_e32 v251, 0x48000, v200
	buffer_load_dwordx4 v[146:149], v251, s[12:15], 0 offen
	s_branch .LBB4_2

	.amdhsa_kernel _Z7k_stageILi1ELi4EEv8AttnArgsPKDF16_PKfPDF16_iii
		.amdhsa_group_segment_fixed_size 82944
		.amdhsa_private_segment_fixed_size 0
		.amdhsa_kernarg_size 148
		.amdhsa_user_sgpr_count 2
		.amdhsa_user_sgpr_dispatch_ptr 0
		.amdhsa_user_sgpr_queue_ptr 0
		.amdhsa_user_sgpr_kernarg_segment_ptr 1
		.amdhsa_user_sgpr_dispatch_id 0
		.amdhsa_user_sgpr_kernarg_preload_length 0
		.amdhsa_user_sgpr_kernarg_preload_offset 0
		.amdhsa_user_sgpr_private_segment_size 0
		.amdhsa_uses_dynamic_stack 0
		.amdhsa_enable_private_segment 0
		.amdhsa_system_sgpr_workgroup_id_x 1
		.amdhsa_system_sgpr_workgroup_id_y 0
		.amdhsa_system_sgpr_workgroup_id_z 0
		.amdhsa_system_sgpr_workgroup_info 0
		.amdhsa_system_vgpr_workitem_id 0
		.amdhsa_next_free_vgpr 252
		.amdhsa_next_free_sgpr 96
		.amdhsa_accum_offset 252
		.amdhsa_reserve_vcc 1
		.amdhsa_float_round_mode_32 0
		.amdhsa_float_round_mode_16_64 0
		.amdhsa_float_denorm_mode_32 3
		.amdhsa_float_denorm_mode_16_64 3
		.amdhsa_dx10_clamp 1
		.amdhsa_ieee_mode 1
		.amdhsa_fp16_overflow 0
		.amdhsa_tg_split 0
		.amdhsa_exception_fp_ieee_invalid_op 0
		.amdhsa_exception_fp_denorm_src 0
		.amdhsa_exception_fp_ieee_div_zero 0
		.amdhsa_exception_fp_ieee_overflow 0
		.amdhsa_exception_fp_ieee_underflow 0
		.amdhsa_exception_fp_ieee_inexact 0
		.amdhsa_exception_int_div_zero 0
	.end_amdhsa_kernel

.LBB5_2:
	s_waitcnt lgkmcnt(0)
	v_cvt_f16_f32_e32 v180, s7
	v_cvt_f16_f32_e32 v182, s6
	v_cvt_f16_f32_e32 v181, s28
	s_waitcnt vmcnt(3)
	v_pk_mul_f16 v183, v182, v184 op_sel_hi:[0,1]
	v_pk_mul_f16 v190, v182, v187 op_sel_hi:[0,1]
	v_pk_mul_f16 v194, v180, v187 op_sel_hi:[0,1]
	v_pk_mul_f16 v198, v181, v187 op_sel_hi:[0,1]
	v_pk_mul_f16 v188, v182, v185 op_sel_hi:[0,1]
	v_pk_mul_f16 v189, v182, v186 op_sel_hi:[0,1]
	v_pk_mul_f16 v191, v180, v184 op_sel_hi:[0,1]
	s_mov_b64 exec, s[64:65]
	buffer_load_dwordx4 v[18:21], v224, s[16:19], 0 offen
	buffer_load_dwordx4 v[6:9], v224, s[16:19], 0 offen offset:512
	s_mov_b64 exec, -1
	v_pk_mul_f16 v192, v180, v185 op_sel_hi:[0,1]
	v_pk_mul_f16 v193, v180, v186 op_sel_hi:[0,1]
	v_pk_mul_f16 v195, v181, v184 op_sel_hi:[0,1]
	v_pk_mul_f16 v196, v181, v185 op_sel_hi:[0,1]
	v_pk_mul_f16 v197, v181, v186 op_sel_hi:[0,1]
	v_pk_fma_f16 v113, v113, v187, v190
	v_pk_fma_f16 v110, v110, v184, v183
	v_pk_fma_f16 v129, v129, v187, v190
	v_pk_fma_f16 v126, v126, v184, v183
	v_pk_fma_f16 v137, v137, v187, v190
	v_pk_fma_f16 v134, v134, v184, v183
	v_pk_fma_f16 v183, v85, v187, v194
	v_pk_fma_f16 v199, v109, v187, v194
	buffer_load_dwordx4 v[30:33], v225, s[16:19], 0 offen offset:512
	buffer_load_dwordx4 v[10:13], v225, s[16:19], 0 offen offset:1024
	v_pk_fma_f16 v194, v125, v187, v194
	v_pk_fma_f16 v203, v53, v187, v198
	v_pk_fma_f16 v207, v69, v187, v198
	v_pk_fma_f16 v187, v97, v187, v198
	v_pk_maximum3_f16 v198, v113, v129, v137
	v_pk_fma_f16 v112, v112, v186, v189
	v_pk_fma_f16 v111, v111, v185, v188
	v_pk_fma_f16 v128, v128, v186, v189
	v_pk_fma_f16 v127, v127, v185, v188
	v_pk_fma_f16 v136, v136, v186, v189
	v_pk_fma_f16 v135, v135, v185, v188
	v_pk_fma_f16 v188, v84, v186, v193
	v_pk_fma_f16 v189, v83, v185, v192
	v_pk_fma_f16 v190, v82, v184, v191
	v_pk_fma_f16 v200, v108, v186, v193
	v_pk_fma_f16 v201, v107, v185, v192
	s_mov_b64 exec, s[66:67]
	buffer_load_dwordx4 v[54:57], v225, s[16:19], 0 offen offset:2048
	buffer_load_dwordx4 v[14:17], v225, s[16:19], 0 offen offset:2560
	s_mov_b64 exec, -1
	v_pk_fma_f16 v202, v106, v184, v191
	v_pk_fma_f16 v193, v124, v186, v193
	v_pk_fma_f16 v192, v123, v185, v192
	v_pk_fma_f16 v191, v122, v184, v191
	v_pk_fma_f16 v204, v52, v186, v197
	v_pk_fma_f16 v205, v51, v185, v196
	v_pk_fma_f16 v206, v50, v184, v195
	v_pk_fma_f16 v208, v68, v186, v197
	v_pk_fma_f16 v209, v67, v185, v196
	v_pk_fma_f16 v210, v66, v184, v195
	v_pk_fma_f16 v186, v96, v186, v197
	v_pk_fma_f16 v185, v95, v185, v196
	v_pk_fma_f16 v184, v94, v184, v195
	v_pk_maximum3_f16 v195, v110, v126, v134
	v_pk_maximum3_f16 v196, v111, v127, v135
	v_pk_maximum3_f16 v197, v112, v128, v136
	v_pk_maximum3_f16 v214, v183, v199, v194
	v_pk_maximum3_f16 v218, v203, v207, v187
	v_pk_maximum3_f16 v211, v190, v202, v191
	v_pk_maximum3_f16 v212, v189, v201, v192
	v_pk_maximum3_f16 v213, v188, v200, v193
	v_pk_maximum3_f16 v215, v206, v210, v184
	v_pk_maximum3_f16 v216, v205, v209, v185
	v_pk_maximum3_f16 v198, v198, v214, v218
	v_pk_maximum3_f16 v217, v204, v208, v186
	v_pk_maximum3_f16 v195, v195, v211, v215
	v_pk_maximum3_f16 v196, v196, v212, v216
	v_pk_maximum3_f16 v197, v197, v213, v217
	v_pk_add_f16 v113, v113, v198 neg_lo:[0,1] neg_hi:[0,1]
	s_mov_b64 exec, s[64:65]
	buffer_load_dwordx4 v[74:77], v226, s[16:19], 0 offen
	buffer_load_dwordx4 v[26:29], v226, s[16:19], 0 offen offset:512
	s_mov_b64 exec, -1
	v_pk_add_f16 v110, v110, v195 neg_lo:[0,1] neg_hi:[0,1]
	v_pk_add_f16 v111, v111, v196 neg_lo:[0,1] neg_hi:[0,1]
	v_pk_add_f16 v112, v112, v197 neg_lo:[0,1] neg_hi:[0,1]
	v_pk_add_f16 v126, v126, v195 neg_lo:[0,1] neg_hi:[0,1]
	v_exp_f16_sdwa v211, v110 dst_sel:WORD_0 dst_unused:UNUSED_PAD src0_sel:WORD_0
	v_exp_f16_sdwa v212, v111 dst_sel:WORD_0 dst_unused:UNUSED_PAD src0_sel:WORD_0
	v_exp_f16_sdwa v213, v112 dst_sel:WORD_0 dst_unused:UNUSED_PAD src0_sel:WORD_0
	v_exp_f16_sdwa v214, v113 dst_sel:WORD_0 dst_unused:UNUSED_PAD src0_sel:WORD_0
	v_exp_f16_sdwa v211, v110 dst_sel:WORD_1 dst_unused:UNUSED_PRESERVE src0_sel:WORD_1
	v_exp_f16_sdwa v212, v111 dst_sel:WORD_1 dst_unused:UNUSED_PRESERVE src0_sel:WORD_1
	v_exp_f16_sdwa v213, v112 dst_sel:WORD_1 dst_unused:UNUSED_PRESERVE src0_sel:WORD_1
	v_exp_f16_sdwa v214, v113 dst_sel:WORD_1 dst_unused:UNUSED_PRESERVE src0_sel:WORD_1
	v_pk_add_f16 v127, v127, v196 neg_lo:[0,1] neg_hi:[0,1]
	v_pk_add_f16 v113, v211, 0
	v_pk_fma_f16 v81, v81, v214, 0
	v_pk_add_f16 v110, v214, 0
	v_pk_add_f16 v111, v213, 0
	v_pk_add_f16 v112, v212, 0
	v_pk_fma_f16 v80, v80, v213, 0
	v_pk_fma_f16 v79, v79, v212, 0
	v_pk_fma_f16 v78, v78, v211, 0
	v_pk_add_f16 v128, v128, v197 neg_lo:[0,1] neg_hi:[0,1]
	buffer_load_dwordx4 v[98:101], v227, s[16:19], 0 offen offset:512
	buffer_load_dwordx4 v[38:41], v227, s[16:19], 0 offen offset:1024
	v_pk_add_f16 v129, v129, v198 neg_lo:[0,1] neg_hi:[0,1]
	v_exp_f16_sdwa v211, v126 dst_sel:WORD_0 dst_unused:UNUSED_PAD src0_sel:WORD_0
	v_exp_f16_sdwa v212, v127 dst_sel:WORD_0 dst_unused:UNUSED_PAD src0_sel:WORD_0
	v_exp_f16_sdwa v213, v128 dst_sel:WORD_0 dst_unused:UNUSED_PAD src0_sel:WORD_0
	v_exp_f16_sdwa v214, v129 dst_sel:WORD_0 dst_unused:UNUSED_PAD src0_sel:WORD_0
	v_exp_f16_sdwa v211, v126 dst_sel:WORD_1 dst_unused:UNUSED_PRESERVE src0_sel:WORD_1
	v_exp_f16_sdwa v212, v127 dst_sel:WORD_1 dst_unused:UNUSED_PRESERVE src0_sel:WORD_1
	v_exp_f16_sdwa v213, v128 dst_sel:WORD_1 dst_unused:UNUSED_PRESERVE src0_sel:WORD_1
	v_exp_f16_sdwa v214, v129 dst_sel:WORD_1 dst_unused:UNUSED_PRESERVE src0_sel:WORD_1
	v_pk_add_f16 v113, v113, v211
	v_pk_fma_f16 v81, v105, v214, v81
	v_pk_add_f16 v105, v137, v198 neg_lo:[0,1] neg_hi:[0,1]
	v_pk_add_f16 v112, v112, v212
	v_pk_add_f16 v111, v111, v213
	v_pk_add_f16 v110, v110, v214
	v_pk_fma_f16 v78, v102, v211, v78
	v_pk_fma_f16 v79, v103, v212, v79
	v_pk_fma_f16 v80, v104, v213, v80
	v_pk_add_f16 v102, v134, v195 neg_lo:[0,1] neg_hi:[0,1]
	v_pk_add_f16 v103, v135, v196 neg_lo:[0,1] neg_hi:[0,1]
	v_pk_add_f16 v104, v136, v197 neg_lo:[0,1] neg_hi:[0,1]
	v_exp_f16_sdwa v126, v102 dst_sel:WORD_0 dst_unused:UNUSED_PAD src0_sel:WORD_0
	v_exp_f16_sdwa v127, v103 dst_sel:WORD_0 dst_unused:UNUSED_PAD src0_sel:WORD_0
	v_exp_f16_sdwa v128, v104 dst_sel:WORD_0 dst_unused:UNUSED_PAD src0_sel:WORD_0
	v_exp_f16_sdwa v129, v105 dst_sel:WORD_0 dst_unused:UNUSED_PAD src0_sel:WORD_0
	v_exp_f16_sdwa v126, v102 dst_sel:WORD_1 dst_unused:UNUSED_PRESERVE src0_sel:WORD_1
	v_exp_f16_sdwa v127, v103 dst_sel:WORD_1 dst_unused:UNUSED_PRESERVE src0_sel:WORD_1
	v_exp_f16_sdwa v128, v104 dst_sel:WORD_1 dst_unused:UNUSED_PRESERVE src0_sel:WORD_1
	v_exp_f16_sdwa v129, v105 dst_sel:WORD_1 dst_unused:UNUSED_PRESERVE src0_sel:WORD_1
	v_pk_add_f16 v105, v113, v126
	v_pk_add_f16 v102, v110, v129
	s_mov_b64 exec, s[66:67]
	buffer_load_dwordx4 v[118:121], v227, s[16:19], 0 offen offset:2048
	buffer_load_dwordx4 v[58:61], v227, s[16:19], 0 offen offset:2560
	s_mov_b64 exec, -1
	v_pk_add_f16 v103, v111, v128
	v_pk_add_f16 v104, v112, v127
	v_pk_fma_f16 v81, v117, v129, v81
	v_pk_fma_f16 v80, v116, v128, v80
	v_pk_fma_f16 v79, v115, v127, v79
	v_pk_fma_f16 v78, v114, v126, v78
	v_pk_add_f16 v110, v190, v195 neg_lo:[0,1] neg_hi:[0,1]
	v_pk_add_f16 v111, v189, v196 neg_lo:[0,1] neg_hi:[0,1]
	v_pk_add_f16 v112, v188, v197 neg_lo:[0,1] neg_hi:[0,1]
	v_pk_add_f16 v113, v183, v198 neg_lo:[0,1] neg_hi:[0,1]
	v_exp_f16_sdwa v114, v110 dst_sel:WORD_0 dst_unused:UNUSED_PAD src0_sel:WORD_0
	v_exp_f16_sdwa v115, v111 dst_sel:WORD_0 dst_unused:UNUSED_PAD src0_sel:WORD_0
	v_exp_f16_sdwa v116, v112 dst_sel:WORD_0 dst_unused:UNUSED_PAD src0_sel:WORD_0
	v_exp_f16_sdwa v117, v113 dst_sel:WORD_0 dst_unused:UNUSED_PAD src0_sel:WORD_0
	v_exp_f16_sdwa v114, v110 dst_sel:WORD_1 dst_unused:UNUSED_PRESERVE src0_sel:WORD_1
	v_exp_f16_sdwa v115, v111 dst_sel:WORD_1 dst_unused:UNUSED_PRESERVE src0_sel:WORD_1
	v_exp_f16_sdwa v116, v112 dst_sel:WORD_1 dst_unused:UNUSED_PRESERVE src0_sel:WORD_1
	v_exp_f16_sdwa v117, v113 dst_sel:WORD_1 dst_unused:UNUSED_PRESERVE src0_sel:WORD_1
	v_pk_add_f16 v110, v202, v195 neg_lo:[0,1] neg_hi:[0,1]
	v_pk_add_f16 v105, v105, v114
	v_pk_add_f16 v104, v104, v115
	v_pk_add_f16 v103, v103, v116
	s_mov_b64 exec, s[76:77]
	buffer_load_dwordx4 v[130:133], v228, s[16:19], 0 offen
	buffer_load_dwordx4 v[70:73], v228, s[16:19], 0 offen offset:512
	s_mov_b64 exec, -1
	v_pk_add_f16 v102, v102, v117
	v_pk_fma_f16 v78, v42, v114, v78
	v_pk_fma_f16 v79, v43, v115, v79
	v_pk_fma_f16 v80, v44, v116, v80
	v_pk_fma_f16 v81, v45, v117, v81
	v_pk_add_f16 v111, v201, v196 neg_lo:[0,1] neg_hi:[0,1]
	v_pk_add_f16 v112, v200, v197 neg_lo:[0,1] neg_hi:[0,1]
	v_pk_add_f16 v113, v199, v198 neg_lo:[0,1] neg_hi:[0,1]
	v_exp_f16_sdwa v114, v110 dst_sel:WORD_0 dst_unused:UNUSED_PAD src0_sel:WORD_0
	v_exp_f16_sdwa v115, v111 dst_sel:WORD_0 dst_unused:UNUSED_PAD src0_sel:WORD_0
	v_exp_f16_sdwa v116, v112 dst_sel:WORD_0 dst_unused:UNUSED_PAD src0_sel:WORD_0
	v_exp_f16_sdwa v117, v113 dst_sel:WORD_0 dst_unused:UNUSED_PAD src0_sel:WORD_0
	v_exp_f16_sdwa v114, v110 dst_sel:WORD_1 dst_unused:UNUSED_PRESERVE src0_sel:WORD_1
	v_exp_f16_sdwa v115, v111 dst_sel:WORD_1 dst_unused:UNUSED_PRESERVE src0_sel:WORD_1
	v_exp_f16_sdwa v116, v112 dst_sel:WORD_1 dst_unused:UNUSED_PRESERVE src0_sel:WORD_1
	v_exp_f16_sdwa v117, v113 dst_sel:WORD_1 dst_unused:UNUSED_PRESERVE src0_sel:WORD_1
	v_pk_add_f16 v110, v191, v195 neg_lo:[0,1] neg_hi:[0,1]
	v_pk_add_f16 v105, v105, v114
	v_pk_add_f16 v102, v102, v117
	v_pk_add_f16 v103, v103, v116
	v_pk_add_f16 v104, v104, v115
	v_pk_fma_f16 v81, v65, v117, v81
	v_pk_fma_f16 v80, v64, v116, v80
	s_mov_b64 exec, s[70:71]
	buffer_load_dwordx4 v[138:141], v229, s[16:19], 0 offen offset:512
	buffer_load_dwordx4 v[90:93], v229, s[16:19], 0 offen offset:1024
	s_mov_b64 exec, -1
	v_pk_fma_f16 v79, v63, v115, v79
	v_pk_fma_f16 v78, v62, v114, v78
	v_pk_add_f16 v111, v192, v196 neg_lo:[0,1] neg_hi:[0,1]
	v_pk_add_f16 v112, v193, v197 neg_lo:[0,1] neg_hi:[0,1]
	v_pk_add_f16 v113, v194, v198 neg_lo:[0,1] neg_hi:[0,1]
	v_exp_f16_sdwa v114, v110 dst_sel:WORD_0 dst_unused:UNUSED_PAD src0_sel:WORD_0
	v_exp_f16_sdwa v115, v111 dst_sel:WORD_0 dst_unused:UNUSED_PAD src0_sel:WORD_0
	v_exp_f16_sdwa v116, v112 dst_sel:WORD_0 dst_unused:UNUSED_PAD src0_sel:WORD_0
	v_exp_f16_sdwa v117, v113 dst_sel:WORD_0 dst_unused:UNUSED_PAD src0_sel:WORD_0
	v_exp_f16_sdwa v114, v110 dst_sel:WORD_1 dst_unused:UNUSED_PRESERVE src0_sel:WORD_1
	v_exp_f16_sdwa v115, v111 dst_sel:WORD_1 dst_unused:UNUSED_PRESERVE src0_sel:WORD_1
	v_exp_f16_sdwa v116, v112 dst_sel:WORD_1 dst_unused:UNUSED_PRESERVE src0_sel:WORD_1
	v_exp_f16_sdwa v117, v113 dst_sel:WORD_1 dst_unused:UNUSED_PRESERVE src0_sel:WORD_1
	v_pk_add_f16 v110, v206, v195 neg_lo:[0,1] neg_hi:[0,1]
	v_pk_add_f16 v105, v105, v114
	v_pk_add_f16 v104, v104, v115
	v_pk_add_f16 v103, v103, v116
	v_pk_add_f16 v102, v102, v117
	v_pk_fma_f16 v78, v86, v114, v78
	v_pk_fma_f16 v79, v87, v115, v79
	v_pk_fma_f16 v80, v88, v116, v80
	v_pk_fma_f16 v81, v89, v117, v81
	s_mov_b64 exec, s[78:79]
	buffer_load_dwordx4 v[142:145], v229, s[16:19], 0 offen offset:2048
	buffer_load_dwordx4 v[2:5], v229, s[16:19], 0 offen offset:2560
	s_mov_b64 exec, -1
	v_pk_add_f16 v111, v205, v196 neg_lo:[0,1] neg_hi:[0,1]
	v_pk_add_f16 v112, v204, v197 neg_lo:[0,1] neg_hi:[0,1]
	v_pk_add_f16 v113, v203, v198 neg_lo:[0,1] neg_hi:[0,1]
	v_exp_f16_sdwa v114, v110 dst_sel:WORD_0 dst_unused:UNUSED_PAD src0_sel:WORD_0
	v_exp_f16_sdwa v115, v111 dst_sel:WORD_0 dst_unused:UNUSED_PAD src0_sel:WORD_0
	v_exp_f16_sdwa v116, v112 dst_sel:WORD_0 dst_unused:UNUSED_PAD src0_sel:WORD_0
	v_exp_f16_sdwa v117, v113 dst_sel:WORD_0 dst_unused:UNUSED_PAD src0_sel:WORD_0
	v_exp_f16_sdwa v114, v110 dst_sel:WORD_1 dst_unused:UNUSED_PRESERVE src0_sel:WORD_1
	v_exp_f16_sdwa v115, v111 dst_sel:WORD_1 dst_unused:UNUSED_PRESERVE src0_sel:WORD_1
	v_exp_f16_sdwa v116, v112 dst_sel:WORD_1 dst_unused:UNUSED_PRESERVE src0_sel:WORD_1
	v_exp_f16_sdwa v117, v113 dst_sel:WORD_1 dst_unused:UNUSED_PRESERVE src0_sel:WORD_1
	v_pk_add_f16 v110, v210, v195 neg_lo:[0,1] neg_hi:[0,1]
	v_pk_add_f16 v105, v105, v114
	v_pk_add_f16 v102, v102, v117
	v_pk_add_f16 v103, v103, v116
	v_pk_add_f16 v104, v104, v115
	v_pk_fma_f16 v81, v25, v117, v81
	v_pk_fma_f16 v80, v24, v116, v80
	v_pk_fma_f16 v79, v23, v115, v79
	v_pk_fma_f16 v78, v22, v114, v78
	v_pk_add_f16 v111, v209, v196 neg_lo:[0,1] neg_hi:[0,1]
	v_pk_add_f16 v112, v208, v197 neg_lo:[0,1] neg_hi:[0,1]
	v_pk_add_f16 v113, v207, v198 neg_lo:[0,1] neg_hi:[0,1]
	v_exp_f16_sdwa v114, v110 dst_sel:WORD_0 dst_unused:UNUSED_PAD src0_sel:WORD_0
	v_exp_f16_sdwa v115, v111 dst_sel:WORD_0 dst_unused:UNUSED_PAD src0_sel:WORD_0
	v_exp_f16_sdwa v116, v112 dst_sel:WORD_0 dst_unused:UNUSED_PAD src0_sel:WORD_0
	v_exp_f16_sdwa v117, v113 dst_sel:WORD_0 dst_unused:UNUSED_PAD src0_sel:WORD_0
	v_exp_f16_sdwa v114, v110 dst_sel:WORD_1 dst_unused:UNUSED_PRESERVE src0_sel:WORD_1
	v_exp_f16_sdwa v115, v111 dst_sel:WORD_1 dst_unused:UNUSED_PRESERVE src0_sel:WORD_1
	v_exp_f16_sdwa v116, v112 dst_sel:WORD_1 dst_unused:UNUSED_PRESERVE src0_sel:WORD_1
	v_exp_f16_sdwa v117, v113 dst_sel:WORD_1 dst_unused:UNUSED_PRESERVE src0_sel:WORD_1
	v_pk_add_f16 v110, v184, v195 neg_lo:[0,1] neg_hi:[0,1]
	v_pk_add_f16 v105, v105, v114
	v_pk_add_f16 v104, v104, v115
	v_pk_add_f16 v103, v103, v116
	v_pk_add_f16 v102, v102, v117
	v_pk_fma_f16 v78, v34, v114, v78
	v_pk_fma_f16 v79, v35, v115, v79
	v_pk_fma_f16 v80, v36, v116, v80
	v_pk_fma_f16 v81, v37, v117, v81
	v_pk_add_f16 v111, v185, v196 neg_lo:[0,1] neg_hi:[0,1]
	v_pk_add_f16 v112, v186, v197 neg_lo:[0,1] neg_hi:[0,1]
	v_pk_add_f16 v113, v187, v198 neg_lo:[0,1] neg_hi:[0,1]
	v_exp_f16_sdwa v114, v110 dst_sel:WORD_0 dst_unused:UNUSED_PAD src0_sel:WORD_0
	v_exp_f16_sdwa v115, v111 dst_sel:WORD_0 dst_unused:UNUSED_PAD src0_sel:WORD_0
	v_exp_f16_sdwa v116, v112 dst_sel:WORD_0 dst_unused:UNUSED_PAD src0_sel:WORD_0
	v_exp_f16_sdwa v117, v113 dst_sel:WORD_0 dst_unused:UNUSED_PAD src0_sel:WORD_0
	v_exp_f16_sdwa v114, v110 dst_sel:WORD_1 dst_unused:UNUSED_PRESERVE src0_sel:WORD_1
	v_exp_f16_sdwa v115, v111 dst_sel:WORD_1 dst_unused:UNUSED_PRESERVE src0_sel:WORD_1
	v_exp_f16_sdwa v116, v112 dst_sel:WORD_1 dst_unused:UNUSED_PRESERVE src0_sel:WORD_1
	v_exp_f16_sdwa v117, v113 dst_sel:WORD_1 dst_unused:UNUSED_PRESERVE src0_sel:WORD_1
	v_pk_add_f16 v105, v105, v114
	v_pk_add_f16 v104, v104, v115
	v_rcp_f16_e32 v110, v105
	v_rcp_f16_sdwa v105, v105 dst_sel:DWORD dst_unused:UNUSED_PAD src0_sel:WORD_1
	v_pk_add_f16 v103, v103, v116
	v_rcp_f16_e32 v111, v104
	v_rcp_f16_sdwa v104, v104 dst_sel:DWORD dst_unused:UNUSED_PAD src0_sel:WORD_1
	v_pk_add_f16 v102, v102, v117
	v_rcp_f16_e32 v112, v103
	v_rcp_f16_sdwa v103, v103 dst_sel:DWORD dst_unused:UNUSED_PAD src0_sel:WORD_1
	v_rcp_f16_e32 v113, v102
	v_rcp_f16_sdwa v102, v102 dst_sel:DWORD dst_unused:UNUSED_PAD src0_sel:WORD_1
	v_pk_fma_f16 v78, v46, v114, v78
	v_pack_b32_f16 v105, v110, v105
	v_pk_fma_f16 v79, v47, v115, v79
	v_pk_mul_f16 v110, v78, v105
	v_pack_b32_f16 v78, v111, v104
	v_pk_fma_f16 v80, v48, v116, v80
	v_pk_mul_f16 v111, v79, v78
	v_pack_b32_f16 v78, v112, v103
	v_pk_fma_f16 v81, v49, v117, v81
	v_pk_mul_f16 v112, v80, v78
	v_pack_b32_f16 v78, v113, v102
	v_pk_mul_f16 v113, v81, v78
	s_waitcnt vmcnt(12)
	v_pk_mul_f16 v78, v182, v154 op_sel_hi:[0,1]
	v_pk_mul_f16 v81, v182, v157 op_sel_hi:[0,1]
	v_pk_mul_f16 v102, v180, v154 op_sel_hi:[0,1]
	v_pk_mul_f16 v114, v181, v154 op_sel_hi:[0,1]
	v_pk_mul_f16 v79, v182, v155 op_sel_hi:[0,1]
	v_pk_mul_f16 v80, v182, v156 op_sel_hi:[0,1]
	v_pk_mul_f16 v103, v180, v155 op_sel_hi:[0,1]
	v_pk_mul_f16 v104, v180, v156 op_sel_hi:[0,1]
	v_pk_mul_f16 v105, v180, v157 op_sel_hi:[0,1]
	v_pk_mul_f16 v115, v181, v155 op_sel_hi:[0,1]
	v_pk_mul_f16 v116, v181, v156 op_sel_hi:[0,1]
	v_pk_mul_f16 v117, v181, v157 op_sel_hi:[0,1]
	v_pk_fma_f16 v85, v85, v157, v81
	v_pk_fma_f16 v82, v82, v154, v78
	v_pk_fma_f16 v109, v109, v157, v81
	v_pk_fma_f16 v106, v106, v154, v78
	v_pk_fma_f16 v81, v125, v157, v81
	v_pk_fma_f16 v78, v122, v154, v78
	v_pk_fma_f16 v125, v50, v154, v102
	v_pk_fma_f16 v129, v66, v154, v102
	v_pk_fma_f16 v102, v94, v154, v102
	v_pk_fma_f16 v137, v18, v154, v114
	v_pk_fma_f16 v186, v30, v154, v114
	v_pk_fma_f16 v114, v54, v154, v114
	v_pk_maximum3_f16 v154, v82, v106, v78
	v_pk_fma_f16 v84, v84, v156, v80
	v_pk_fma_f16 v83, v83, v155, v79
	v_pk_fma_f16 v108, v108, v156, v80
	v_pk_fma_f16 v107, v107, v155, v79
	v_pk_fma_f16 v80, v124, v156, v80
	v_pk_fma_f16 v79, v123, v155, v79
	v_pk_fma_f16 v122, v53, v157, v105
	v_pk_fma_f16 v123, v52, v156, v104
	v_pk_fma_f16 v124, v51, v155, v103
	v_pk_fma_f16 v126, v69, v157, v105
	v_pk_fma_f16 v127, v68, v156, v104
	v_pk_fma_f16 v128, v67, v155, v103
	v_pk_fma_f16 v105, v97, v157, v105
	v_pk_fma_f16 v104, v96, v156, v104
	v_pk_fma_f16 v103, v95, v155, v103
	v_pk_fma_f16 v134, v21, v157, v117
	v_pk_fma_f16 v135, v20, v156, v116
	v_pk_fma_f16 v136, v19, v155, v115
	v_pk_fma_f16 v183, v33, v157, v117
	v_pk_fma_f16 v184, v32, v156, v116
	v_pk_fma_f16 v185, v31, v155, v115
	v_pk_fma_f16 v117, v57, v157, v117
	v_pk_fma_f16 v116, v56, v156, v116
	v_pk_fma_f16 v115, v55, v155, v115
	v_pk_maximum3_f16 v155, v83, v107, v79
	v_pk_maximum3_f16 v156, v84, v108, v80
	v_pk_maximum3_f16 v157, v85, v109, v81
	v_pk_maximum3_f16 v187, v125, v129, v102
	v_pk_maximum3_f16 v191, v137, v186, v114
	v_pk_maximum3_f16 v188, v124, v128, v103
	v_pk_maximum3_f16 v189, v123, v127, v104
	v_pk_maximum3_f16 v190, v122, v126, v105
	v_pk_maximum3_f16 v192, v136, v185, v115
	v_pk_maximum3_f16 v193, v135, v184, v116
	v_pk_maximum3_f16 v154, v154, v187, v191
	v_pk_maximum3_f16 v194, v134, v183, v117
	v_pk_maximum3_f16 v155, v155, v188, v192
	v_pk_maximum3_f16 v156, v156, v189, v193
	v_pk_maximum3_f16 v157, v157, v190, v194
	v_pk_add_f16 v82, v82, v154 neg_lo:[0,1] neg_hi:[0,1]
	v_pk_add_f16 v83, v83, v155 neg_lo:[0,1] neg_hi:[0,1]
	v_pk_add_f16 v84, v84, v156 neg_lo:[0,1] neg_hi:[0,1]
	v_pk_add_f16 v85, v85, v157 neg_lo:[0,1] neg_hi:[0,1]
	v_pk_add_f16 v106, v106, v154 neg_lo:[0,1] neg_hi:[0,1]
	v_exp_f16_sdwa v187, v82 dst_sel:WORD_0 dst_unused:UNUSED_PAD src0_sel:WORD_0
	v_exp_f16_sdwa v188, v83 dst_sel:WORD_0 dst_unused:UNUSED_PAD src0_sel:WORD_0
	v_exp_f16_sdwa v189, v84 dst_sel:WORD_0 dst_unused:UNUSED_PAD src0_sel:WORD_0
	v_exp_f16_sdwa v190, v85 dst_sel:WORD_0 dst_unused:UNUSED_PAD src0_sel:WORD_0
	v_exp_f16_sdwa v187, v82 dst_sel:WORD_1 dst_unused:UNUSED_PRESERVE src0_sel:WORD_1
	v_exp_f16_sdwa v188, v83 dst_sel:WORD_1 dst_unused:UNUSED_PRESERVE src0_sel:WORD_1
	v_exp_f16_sdwa v189, v84 dst_sel:WORD_1 dst_unused:UNUSED_PRESERVE src0_sel:WORD_1
	v_exp_f16_sdwa v190, v85 dst_sel:WORD_1 dst_unused:UNUSED_PRESERVE src0_sel:WORD_1
	v_pk_add_f16 v107, v107, v155 neg_lo:[0,1] neg_hi:[0,1]
	v_pk_add_f16 v82, v190, 0
	v_pk_fma_f16 v42, v42, v187, 0
	v_pk_add_f16 v83, v189, 0
	v_pk_add_f16 v84, v188, 0
	v_pk_add_f16 v85, v187, 0
	v_pk_fma_f16 v45, v45, v190, 0
	v_pk_fma_f16 v44, v44, v189, 0
	v_pk_fma_f16 v43, v43, v188, 0
	v_pk_add_f16 v108, v108, v156 neg_lo:[0,1] neg_hi:[0,1]
	v_pk_add_f16 v109, v109, v157 neg_lo:[0,1] neg_hi:[0,1]
	v_exp_f16_sdwa v187, v106 dst_sel:WORD_0 dst_unused:UNUSED_PAD src0_sel:WORD_0
	v_exp_f16_sdwa v188, v107 dst_sel:WORD_0 dst_unused:UNUSED_PAD src0_sel:WORD_0
	v_exp_f16_sdwa v189, v108 dst_sel:WORD_0 dst_unused:UNUSED_PAD src0_sel:WORD_0
	v_exp_f16_sdwa v190, v109 dst_sel:WORD_0 dst_unused:UNUSED_PAD src0_sel:WORD_0
	v_exp_f16_sdwa v187, v106 dst_sel:WORD_1 dst_unused:UNUSED_PRESERVE src0_sel:WORD_1
	v_exp_f16_sdwa v188, v107 dst_sel:WORD_1 dst_unused:UNUSED_PRESERVE src0_sel:WORD_1
	v_exp_f16_sdwa v189, v108 dst_sel:WORD_1 dst_unused:UNUSED_PRESERVE src0_sel:WORD_1
	v_exp_f16_sdwa v190, v109 dst_sel:WORD_1 dst_unused:UNUSED_PRESERVE src0_sel:WORD_1
	s_nop 0
	v_pk_add_f16 v82, v82, v190
	v_pk_fma_f16 v42, v62, v187, v42
	v_pk_add_f16 v62, v78, v154 neg_lo:[0,1] neg_hi:[0,1]
	v_pk_add_f16 v85, v85, v187
	v_pk_add_f16 v84, v84, v188
	v_pk_add_f16 v83, v83, v189
	v_pk_fma_f16 v43, v63, v188, v43
	v_pk_fma_f16 v44, v64, v189, v44
	v_pk_fma_f16 v45, v65, v190, v45
	v_pk_add_f16 v63, v79, v155 neg_lo:[0,1] neg_hi:[0,1]
	v_pk_add_f16 v64, v80, v156 neg_lo:[0,1] neg_hi:[0,1]
	v_pk_add_f16 v65, v81, v157 neg_lo:[0,1] neg_hi:[0,1]
	v_exp_f16_sdwa v78, v62 dst_sel:WORD_0 dst_unused:UNUSED_PAD src0_sel:WORD_0
	v_exp_f16_sdwa v79, v63 dst_sel:WORD_0 dst_unused:UNUSED_PAD src0_sel:WORD_0
	v_exp_f16_sdwa v80, v64 dst_sel:WORD_0 dst_unused:UNUSED_PAD src0_sel:WORD_0
	v_exp_f16_sdwa v81, v65 dst_sel:WORD_0 dst_unused:UNUSED_PAD src0_sel:WORD_0
	v_exp_f16_sdwa v78, v62 dst_sel:WORD_1 dst_unused:UNUSED_PRESERVE src0_sel:WORD_1
	v_exp_f16_sdwa v79, v63 dst_sel:WORD_1 dst_unused:UNUSED_PRESERVE src0_sel:WORD_1
	v_exp_f16_sdwa v80, v64 dst_sel:WORD_1 dst_unused:UNUSED_PRESERVE src0_sel:WORD_1
	v_exp_f16_sdwa v81, v65 dst_sel:WORD_1 dst_unused:UNUSED_PRESERVE src0_sel:WORD_1
	s_nop 0
	v_pk_add_f16 v62, v82, v81
	v_pk_add_f16 v63, v83, v80
	v_pk_add_f16 v64, v84, v79
	v_pk_add_f16 v65, v85, v78
	v_pk_fma_f16 v45, v89, v81, v45
	v_pk_fma_f16 v44, v88, v80, v44
	v_pk_fma_f16 v43, v87, v79, v43
	v_pk_fma_f16 v42, v86, v78, v42
	v_pk_add_f16 v78, v125, v154 neg_lo:[0,1] neg_hi:[0,1]
	v_pk_add_f16 v79, v124, v155 neg_lo:[0,1] neg_hi:[0,1]
	v_pk_add_f16 v80, v123, v156 neg_lo:[0,1] neg_hi:[0,1]
	v_pk_add_f16 v81, v122, v157 neg_lo:[0,1] neg_hi:[0,1]
	v_exp_f16_sdwa v82, v78 dst_sel:WORD_0 dst_unused:UNUSED_PAD src0_sel:WORD_0
	v_exp_f16_sdwa v83, v79 dst_sel:WORD_0 dst_unused:UNUSED_PAD src0_sel:WORD_0
	v_exp_f16_sdwa v84, v80 dst_sel:WORD_0 dst_unused:UNUSED_PAD src0_sel:WORD_0
	v_exp_f16_sdwa v85, v81 dst_sel:WORD_0 dst_unused:UNUSED_PAD src0_sel:WORD_0
	v_exp_f16_sdwa v82, v78 dst_sel:WORD_1 dst_unused:UNUSED_PRESERVE src0_sel:WORD_1
	v_exp_f16_sdwa v83, v79 dst_sel:WORD_1 dst_unused:UNUSED_PRESERVE src0_sel:WORD_1
	v_exp_f16_sdwa v84, v80 dst_sel:WORD_1 dst_unused:UNUSED_PRESERVE src0_sel:WORD_1
	v_exp_f16_sdwa v85, v81 dst_sel:WORD_1 dst_unused:UNUSED_PRESERVE src0_sel:WORD_1
	v_pk_add_f16 v78, v129, v154 neg_lo:[0,1] neg_hi:[0,1]
	v_pk_add_f16 v62, v62, v85
	v_pk_add_f16 v65, v65, v82
	v_pk_add_f16 v64, v64, v83
	v_pk_add_f16 v63, v63, v84
	v_pk_fma_f16 v42, v22, v82, v42
	v_pk_fma_f16 v43, v23, v83, v43
	v_pk_fma_f16 v44, v24, v84, v44
	v_pk_fma_f16 v45, v25, v85, v45
	v_pk_add_f16 v79, v128, v155 neg_lo:[0,1] neg_hi:[0,1]
	v_pk_add_f16 v80, v127, v156 neg_lo:[0,1] neg_hi:[0,1]
	v_pk_add_f16 v81, v126, v157 neg_lo:[0,1] neg_hi:[0,1]
	v_exp_f16_sdwa v82, v78 dst_sel:WORD_0 dst_unused:UNUSED_PAD src0_sel:WORD_0
	v_exp_f16_sdwa v83, v79 dst_sel:WORD_0 dst_unused:UNUSED_PAD src0_sel:WORD_0
	v_exp_f16_sdwa v84, v80 dst_sel:WORD_0 dst_unused:UNUSED_PAD src0_sel:WORD_0
	v_exp_f16_sdwa v85, v81 dst_sel:WORD_0 dst_unused:UNUSED_PAD src0_sel:WORD_0
	v_exp_f16_sdwa v82, v78 dst_sel:WORD_1 dst_unused:UNUSED_PRESERVE src0_sel:WORD_1
	v_exp_f16_sdwa v83, v79 dst_sel:WORD_1 dst_unused:UNUSED_PRESERVE src0_sel:WORD_1
	v_exp_f16_sdwa v84, v80 dst_sel:WORD_1 dst_unused:UNUSED_PRESERVE src0_sel:WORD_1
	v_exp_f16_sdwa v85, v81 dst_sel:WORD_1 dst_unused:UNUSED_PRESERVE src0_sel:WORD_1
	v_pk_add_f16 v78, v102, v154 neg_lo:[0,1] neg_hi:[0,1]
	v_pk_add_f16 v62, v62, v85
	v_pk_add_f16 v63, v63, v84
	v_pk_add_f16 v64, v64, v83
	v_pk_add_f16 v65, v65, v82
	v_pk_fma_f16 v45, v37, v85, v45
	v_pk_fma_f16 v44, v36, v84, v44
	v_pk_fma_f16 v43, v35, v83, v43
	v_pk_fma_f16 v42, v34, v82, v42
	v_pk_add_f16 v79, v103, v155 neg_lo:[0,1] neg_hi:[0,1]
	v_pk_add_f16 v80, v104, v156 neg_lo:[0,1] neg_hi:[0,1]
	v_pk_add_f16 v81, v105, v157 neg_lo:[0,1] neg_hi:[0,1]
	v_exp_f16_sdwa v82, v78 dst_sel:WORD_0 dst_unused:UNUSED_PAD src0_sel:WORD_0
	v_exp_f16_sdwa v83, v79 dst_sel:WORD_0 dst_unused:UNUSED_PAD src0_sel:WORD_0
	v_exp_f16_sdwa v84, v80 dst_sel:WORD_0 dst_unused:UNUSED_PAD src0_sel:WORD_0
	v_exp_f16_sdwa v85, v81 dst_sel:WORD_0 dst_unused:UNUSED_PAD src0_sel:WORD_0
	v_exp_f16_sdwa v82, v78 dst_sel:WORD_1 dst_unused:UNUSED_PRESERVE src0_sel:WORD_1
	v_exp_f16_sdwa v83, v79 dst_sel:WORD_1 dst_unused:UNUSED_PRESERVE src0_sel:WORD_1
	v_exp_f16_sdwa v84, v80 dst_sel:WORD_1 dst_unused:UNUSED_PRESERVE src0_sel:WORD_1
	v_exp_f16_sdwa v85, v81 dst_sel:WORD_1 dst_unused:UNUSED_PRESERVE src0_sel:WORD_1
	v_pk_add_f16 v78, v137, v154 neg_lo:[0,1] neg_hi:[0,1]
	v_pk_add_f16 v62, v62, v85
	v_pk_add_f16 v65, v65, v82
	v_pk_add_f16 v64, v64, v83
	v_pk_add_f16 v63, v63, v84
	v_pk_fma_f16 v42, v46, v82, v42
	v_pk_fma_f16 v43, v47, v83, v43
	v_pk_fma_f16 v44, v48, v84, v44
	v_pk_fma_f16 v45, v49, v85, v45
	v_pk_add_f16 v79, v136, v155 neg_lo:[0,1] neg_hi:[0,1]
	v_pk_add_f16 v80, v135, v156 neg_lo:[0,1] neg_hi:[0,1]
	v_pk_add_f16 v81, v134, v157 neg_lo:[0,1] neg_hi:[0,1]
	v_exp_f16_sdwa v82, v78 dst_sel:WORD_0 dst_unused:UNUSED_PAD src0_sel:WORD_0
	v_exp_f16_sdwa v83, v79 dst_sel:WORD_0 dst_unused:UNUSED_PAD src0_sel:WORD_0
	v_exp_f16_sdwa v84, v80 dst_sel:WORD_0 dst_unused:UNUSED_PAD src0_sel:WORD_0
	v_exp_f16_sdwa v85, v81 dst_sel:WORD_0 dst_unused:UNUSED_PAD src0_sel:WORD_0
	v_exp_f16_sdwa v82, v78 dst_sel:WORD_1 dst_unused:UNUSED_PRESERVE src0_sel:WORD_1
	v_exp_f16_sdwa v83, v79 dst_sel:WORD_1 dst_unused:UNUSED_PRESERVE src0_sel:WORD_1
	v_exp_f16_sdwa v84, v80 dst_sel:WORD_1 dst_unused:UNUSED_PRESERVE src0_sel:WORD_1
	v_exp_f16_sdwa v85, v81 dst_sel:WORD_1 dst_unused:UNUSED_PRESERVE src0_sel:WORD_1
	v_pk_add_f16 v78, v186, v154 neg_lo:[0,1] neg_hi:[0,1]
	v_pk_add_f16 v62, v62, v85
	v_pk_add_f16 v63, v63, v84
	v_pk_add_f16 v64, v64, v83
	v_pk_add_f16 v65, v65, v82
	v_pk_fma_f16 v45, v9, v85, v45
	v_pk_fma_f16 v44, v8, v84, v44
	v_pk_fma_f16 v43, v7, v83, v43
	v_pk_fma_f16 v42, v6, v82, v42
	v_pk_add_f16 v79, v185, v155 neg_lo:[0,1] neg_hi:[0,1]
	v_pk_add_f16 v80, v184, v156 neg_lo:[0,1] neg_hi:[0,1]
	v_pk_add_f16 v81, v183, v157 neg_lo:[0,1] neg_hi:[0,1]
	v_exp_f16_sdwa v82, v78 dst_sel:WORD_0 dst_unused:UNUSED_PAD src0_sel:WORD_0
	v_exp_f16_sdwa v83, v79 dst_sel:WORD_0 dst_unused:UNUSED_PAD src0_sel:WORD_0
	v_exp_f16_sdwa v84, v80 dst_sel:WORD_0 dst_unused:UNUSED_PAD src0_sel:WORD_0
	v_exp_f16_sdwa v85, v81 dst_sel:WORD_0 dst_unused:UNUSED_PAD src0_sel:WORD_0
	v_exp_f16_sdwa v82, v78 dst_sel:WORD_1 dst_unused:UNUSED_PRESERVE src0_sel:WORD_1
	v_exp_f16_sdwa v83, v79 dst_sel:WORD_1 dst_unused:UNUSED_PRESERVE src0_sel:WORD_1
	v_exp_f16_sdwa v84, v80 dst_sel:WORD_1 dst_unused:UNUSED_PRESERVE src0_sel:WORD_1
	v_exp_f16_sdwa v85, v81 dst_sel:WORD_1 dst_unused:UNUSED_PRESERVE src0_sel:WORD_1
	v_pk_add_f16 v78, v114, v154 neg_lo:[0,1] neg_hi:[0,1]
	v_pk_add_f16 v62, v62, v85
	v_pk_add_f16 v65, v65, v82
	v_pk_add_f16 v64, v64, v83
	v_pk_add_f16 v63, v63, v84
	v_pk_fma_f16 v42, v10, v82, v42
	v_pk_fma_f16 v43, v11, v83, v43
	v_pk_fma_f16 v44, v12, v84, v44
	v_pk_fma_f16 v45, v13, v85, v45
	v_pk_add_f16 v79, v115, v155 neg_lo:[0,1] neg_hi:[0,1]
	v_pk_add_f16 v80, v116, v156 neg_lo:[0,1] neg_hi:[0,1]
	v_pk_add_f16 v81, v117, v157 neg_lo:[0,1] neg_hi:[0,1]
	v_exp_f16_sdwa v82, v78 dst_sel:WORD_0 dst_unused:UNUSED_PAD src0_sel:WORD_0
	v_exp_f16_sdwa v83, v79 dst_sel:WORD_0 dst_unused:UNUSED_PAD src0_sel:WORD_0
	v_exp_f16_sdwa v84, v80 dst_sel:WORD_0 dst_unused:UNUSED_PAD src0_sel:WORD_0
	v_exp_f16_sdwa v85, v81 dst_sel:WORD_0 dst_unused:UNUSED_PAD src0_sel:WORD_0
	v_exp_f16_sdwa v82, v78 dst_sel:WORD_1 dst_unused:UNUSED_PRESERVE src0_sel:WORD_1
	v_exp_f16_sdwa v83, v79 dst_sel:WORD_1 dst_unused:UNUSED_PRESERVE src0_sel:WORD_1
	v_exp_f16_sdwa v84, v80 dst_sel:WORD_1 dst_unused:UNUSED_PRESERVE src0_sel:WORD_1
	v_exp_f16_sdwa v85, v81 dst_sel:WORD_1 dst_unused:UNUSED_PRESERVE src0_sel:WORD_1
	s_nop 0
	v_pk_add_f16 v62, v62, v85
	v_pk_add_f16 v63, v63, v84
	v_pk_add_f16 v64, v64, v83
	v_pk_add_f16 v65, v65, v82
	v_rcp_f16_e32 v81, v62
	v_rcp_f16_sdwa v62, v62 dst_sel:DWORD dst_unused:UNUSED_PAD src0_sel:WORD_1
	v_rcp_f16_e32 v78, v65
	v_rcp_f16_sdwa v65, v65 dst_sel:DWORD dst_unused:UNUSED_PAD src0_sel:WORD_1
	v_rcp_f16_e32 v79, v64
	v_rcp_f16_sdwa v64, v64 dst_sel:DWORD dst_unused:UNUSED_PAD src0_sel:WORD_1
	v_rcp_f16_e32 v80, v63
	v_rcp_f16_sdwa v63, v63 dst_sel:DWORD dst_unused:UNUSED_PAD src0_sel:WORD_1
	v_pk_fma_f16 v45, v17, v85, v45
	v_pack_b32_f16 v62, v81, v62
	v_pk_fma_f16 v44, v16, v84, v44
	v_pk_fma_f16 v43, v15, v83, v43
	v_pk_fma_f16 v42, v14, v82, v42
	v_pack_b32_f16 v65, v78, v65
	v_pack_b32_f16 v64, v79, v64
	v_pack_b32_f16 v63, v80, v63
	v_pk_mul_f16 v45, v45, v62
	s_waitcnt vmcnt(6)
	v_pk_mul_f16 v62, v182, v150 op_sel_hi:[0,1]
	v_pk_mul_f16 v42, v42, v65
	v_pk_mul_f16 v43, v43, v64
	v_pk_mul_f16 v44, v44, v63
	v_pk_mul_f16 v63, v182, v151 op_sel_hi:[0,1]
	v_pk_mul_f16 v64, v182, v152 op_sel_hi:[0,1]
	v_pk_mul_f16 v65, v182, v153 op_sel_hi:[0,1]
	v_pk_mul_f16 v78, v180, v150 op_sel_hi:[0,1]
	v_pk_mul_f16 v82, v181, v150 op_sel_hi:[0,1]
	v_pk_fma_f16 v50, v50, v150, v62
	v_pk_fma_f16 v66, v66, v150, v62
	v_pk_fma_f16 v62, v94, v150, v62
	v_pk_mul_f16 v79, v180, v151 op_sel_hi:[0,1]
	v_pk_maximum3_f16 v114, v50, v66, v62
	v_pk_mul_f16 v80, v180, v152 op_sel_hi:[0,1]
	v_pk_mul_f16 v81, v180, v153 op_sel_hi:[0,1]
	v_pk_mul_f16 v83, v181, v151 op_sel_hi:[0,1]
	v_pk_mul_f16 v84, v181, v152 op_sel_hi:[0,1]
	v_pk_mul_f16 v85, v181, v153 op_sel_hi:[0,1]
	v_pk_fma_f16 v53, v53, v153, v65
	v_pk_fma_f16 v52, v52, v152, v64
	v_pk_fma_f16 v51, v51, v151, v63
	v_pk_fma_f16 v69, v69, v153, v65
	v_pk_fma_f16 v68, v68, v152, v64
	v_pk_fma_f16 v67, v67, v151, v63
	v_pk_fma_f16 v65, v97, v153, v65
	v_pk_fma_f16 v64, v96, v152, v64
	v_pk_fma_f16 v63, v95, v151, v63
	v_pk_fma_f16 v89, v18, v150, v78
	v_pk_fma_f16 v97, v30, v150, v78
	v_pk_fma_f16 v78, v54, v150, v78
	v_pk_fma_f16 v105, v74, v150, v82
	v_pk_fma_f16 v109, v98, v150, v82
	v_pk_fma_f16 v82, v118, v150, v82
	v_pk_maximum3_f16 v115, v51, v67, v63
	v_pk_maximum3_f16 v116, v52, v68, v64
	v_pk_maximum3_f16 v117, v53, v69, v65
	v_pk_maximum3_f16 v122, v89, v97, v78
	v_pk_fma_f16 v86, v21, v153, v81
	v_pk_maximum3_f16 v126, v105, v109, v82
	v_pk_fma_f16 v87, v20, v152, v80
	v_pk_maximum3_f16 v114, v114, v122, v126
	v_pk_fma_f16 v88, v19, v151, v79
	v_pk_fma_f16 v94, v33, v153, v81
	v_pk_fma_f16 v95, v32, v152, v80
	v_pk_fma_f16 v96, v31, v151, v79
	v_pk_fma_f16 v81, v57, v153, v81
	v_pk_fma_f16 v80, v56, v152, v80
	v_pk_fma_f16 v79, v55, v151, v79
	v_pk_fma_f16 v102, v77, v153, v85
	v_pk_fma_f16 v103, v76, v152, v84
	v_pk_fma_f16 v104, v75, v151, v83
	v_pk_fma_f16 v106, v101, v153, v85
	v_pk_fma_f16 v107, v100, v152, v84
	v_pk_fma_f16 v108, v99, v151, v83
	v_pk_fma_f16 v85, v121, v153, v85
	v_pk_fma_f16 v84, v120, v152, v84
	v_pk_fma_f16 v83, v119, v151, v83
	v_pk_maximum3_f16 v123, v88, v96, v79
	v_pk_maximum3_f16 v124, v87, v95, v80
	v_pk_maximum3_f16 v125, v86, v94, v81
	v_pk_maximum3_f16 v128, v103, v107, v84
	v_pk_maximum3_f16 v129, v102, v106, v85
	v_pk_maximum3_f16 v127, v104, v108, v83
	v_pk_maximum3_f16 v115, v115, v123, v127
	v_pk_maximum3_f16 v116, v116, v124, v128
	v_pk_maximum3_f16 v117, v117, v125, v129
	v_pk_add_f16 v50, v50, v114 neg_lo:[0,1] neg_hi:[0,1]
	v_pk_add_f16 v51, v51, v115 neg_lo:[0,1] neg_hi:[0,1]
	v_pk_add_f16 v52, v52, v116 neg_lo:[0,1] neg_hi:[0,1]
	v_pk_add_f16 v53, v53, v117 neg_lo:[0,1] neg_hi:[0,1]
	v_pk_add_f16 v66, v66, v114 neg_lo:[0,1] neg_hi:[0,1]
	v_exp_f16_sdwa v122, v50 dst_sel:WORD_0 dst_unused:UNUSED_PAD src0_sel:WORD_0
	v_exp_f16_sdwa v123, v51 dst_sel:WORD_0 dst_unused:UNUSED_PAD src0_sel:WORD_0
	v_exp_f16_sdwa v124, v52 dst_sel:WORD_0 dst_unused:UNUSED_PAD src0_sel:WORD_0
	v_exp_f16_sdwa v125, v53 dst_sel:WORD_0 dst_unused:UNUSED_PAD src0_sel:WORD_0
	v_exp_f16_sdwa v122, v50 dst_sel:WORD_1 dst_unused:UNUSED_PRESERVE src0_sel:WORD_1
	v_exp_f16_sdwa v123, v51 dst_sel:WORD_1 dst_unused:UNUSED_PRESERVE src0_sel:WORD_1
	v_exp_f16_sdwa v124, v52 dst_sel:WORD_1 dst_unused:UNUSED_PRESERVE src0_sel:WORD_1
	v_exp_f16_sdwa v125, v53 dst_sel:WORD_1 dst_unused:UNUSED_PRESERVE src0_sel:WORD_1
	v_pk_add_f16 v67, v67, v115 neg_lo:[0,1] neg_hi:[0,1]
	v_pk_add_f16 v50, v125, 0
	v_pk_fma_f16 v22, v22, v122, 0
	v_pk_add_f16 v51, v124, 0
	v_pk_add_f16 v52, v123, 0
	v_pk_add_f16 v53, v122, 0
	v_pk_fma_f16 v23, v23, v123, 0
	v_pk_fma_f16 v24, v24, v124, 0
	v_pk_fma_f16 v25, v25, v125, 0
	v_pk_add_f16 v68, v68, v116 neg_lo:[0,1] neg_hi:[0,1]
	v_pk_add_f16 v69, v69, v117 neg_lo:[0,1] neg_hi:[0,1]
	v_exp_f16_sdwa v122, v66 dst_sel:WORD_0 dst_unused:UNUSED_PAD src0_sel:WORD_0
	v_exp_f16_sdwa v123, v67 dst_sel:WORD_0 dst_unused:UNUSED_PAD src0_sel:WORD_0
	v_exp_f16_sdwa v124, v68 dst_sel:WORD_0 dst_unused:UNUSED_PAD src0_sel:WORD_0
	v_exp_f16_sdwa v125, v69 dst_sel:WORD_0 dst_unused:UNUSED_PAD src0_sel:WORD_0
	v_exp_f16_sdwa v122, v66 dst_sel:WORD_1 dst_unused:UNUSED_PRESERVE src0_sel:WORD_1
	v_exp_f16_sdwa v123, v67 dst_sel:WORD_1 dst_unused:UNUSED_PRESERVE src0_sel:WORD_1
	v_exp_f16_sdwa v124, v68 dst_sel:WORD_1 dst_unused:UNUSED_PRESERVE src0_sel:WORD_1
	v_exp_f16_sdwa v125, v69 dst_sel:WORD_1 dst_unused:UNUSED_PRESERVE src0_sel:WORD_1
	s_nop 0
	v_pk_add_f16 v50, v50, v125
	v_pk_fma_f16 v22, v34, v122, v22
	v_pk_add_f16 v34, v62, v114 neg_lo:[0,1] neg_hi:[0,1]
	v_pk_add_f16 v53, v53, v122
	v_pk_add_f16 v52, v52, v123
	v_pk_add_f16 v51, v51, v124
	v_pk_fma_f16 v25, v37, v125, v25
	v_pk_fma_f16 v24, v36, v124, v24
	v_pk_fma_f16 v23, v35, v123, v23
	v_pk_add_f16 v35, v63, v115 neg_lo:[0,1] neg_hi:[0,1]
	v_pk_add_f16 v36, v64, v116 neg_lo:[0,1] neg_hi:[0,1]
	v_pk_add_f16 v37, v65, v117 neg_lo:[0,1] neg_hi:[0,1]
	v_exp_f16_sdwa v62, v34 dst_sel:WORD_0 dst_unused:UNUSED_PAD src0_sel:WORD_0
	v_exp_f16_sdwa v63, v35 dst_sel:WORD_0 dst_unused:UNUSED_PAD src0_sel:WORD_0
	v_exp_f16_sdwa v64, v36 dst_sel:WORD_0 dst_unused:UNUSED_PAD src0_sel:WORD_0
	v_exp_f16_sdwa v65, v37 dst_sel:WORD_0 dst_unused:UNUSED_PAD src0_sel:WORD_0
	v_exp_f16_sdwa v62, v34 dst_sel:WORD_1 dst_unused:UNUSED_PRESERVE src0_sel:WORD_1
	v_exp_f16_sdwa v63, v35 dst_sel:WORD_1 dst_unused:UNUSED_PRESERVE src0_sel:WORD_1
	v_exp_f16_sdwa v64, v36 dst_sel:WORD_1 dst_unused:UNUSED_PRESERVE src0_sel:WORD_1
	v_exp_f16_sdwa v65, v37 dst_sel:WORD_1 dst_unused:UNUSED_PRESERVE src0_sel:WORD_1
	s_nop 0
	v_pk_add_f16 v34, v50, v65
	v_pk_add_f16 v35, v51, v64
	v_pk_add_f16 v36, v52, v63
	v_pk_add_f16 v37, v53, v62
	v_pk_fma_f16 v22, v46, v62, v22
	v_pk_fma_f16 v23, v47, v63, v23
	v_pk_fma_f16 v24, v48, v64, v24
	v_pk_fma_f16 v25, v49, v65, v25
	v_pk_add_f16 v46, v89, v114 neg_lo:[0,1] neg_hi:[0,1]
	v_pk_add_f16 v47, v88, v115 neg_lo:[0,1] neg_hi:[0,1]
	v_pk_add_f16 v48, v87, v116 neg_lo:[0,1] neg_hi:[0,1]
	v_pk_add_f16 v49, v86, v117 neg_lo:[0,1] neg_hi:[0,1]
	v_exp_f16_sdwa v50, v46 dst_sel:WORD_0 dst_unused:UNUSED_PAD src0_sel:WORD_0
	v_exp_f16_sdwa v51, v47 dst_sel:WORD_0 dst_unused:UNUSED_PAD src0_sel:WORD_0
	v_exp_f16_sdwa v52, v48 dst_sel:WORD_0 dst_unused:UNUSED_PAD src0_sel:WORD_0
	v_exp_f16_sdwa v53, v49 dst_sel:WORD_0 dst_unused:UNUSED_PAD src0_sel:WORD_0
	v_exp_f16_sdwa v50, v46 dst_sel:WORD_1 dst_unused:UNUSED_PRESERVE src0_sel:WORD_1
	v_exp_f16_sdwa v51, v47 dst_sel:WORD_1 dst_unused:UNUSED_PRESERVE src0_sel:WORD_1
	v_exp_f16_sdwa v52, v48 dst_sel:WORD_1 dst_unused:UNUSED_PRESERVE src0_sel:WORD_1
	v_exp_f16_sdwa v53, v49 dst_sel:WORD_1 dst_unused:UNUSED_PRESERVE src0_sel:WORD_1
	v_pk_add_f16 v46, v97, v114 neg_lo:[0,1] neg_hi:[0,1]
	v_pk_add_f16 v34, v34, v53
	v_pk_add_f16 v37, v37, v50
	v_pk_add_f16 v36, v36, v51
	v_pk_add_f16 v35, v35, v52
	v_pk_fma_f16 v25, v9, v53, v25
	v_pk_fma_f16 v24, v8, v52, v24
	v_pk_fma_f16 v23, v7, v51, v23
	v_pk_fma_f16 v22, v6, v50, v22
	v_pk_add_f16 v47, v96, v115 neg_lo:[0,1] neg_hi:[0,1]
	v_pk_add_f16 v48, v95, v116 neg_lo:[0,1] neg_hi:[0,1]
	v_pk_add_f16 v49, v94, v117 neg_lo:[0,1] neg_hi:[0,1]
	v_exp_f16_sdwa v50, v46 dst_sel:WORD_0 dst_unused:UNUSED_PAD src0_sel:WORD_0
	v_exp_f16_sdwa v51, v47 dst_sel:WORD_0 dst_unused:UNUSED_PAD src0_sel:WORD_0
	v_exp_f16_sdwa v52, v48 dst_sel:WORD_0 dst_unused:UNUSED_PAD src0_sel:WORD_0
	v_exp_f16_sdwa v53, v49 dst_sel:WORD_0 dst_unused:UNUSED_PAD src0_sel:WORD_0
	v_exp_f16_sdwa v50, v46 dst_sel:WORD_1 dst_unused:UNUSED_PRESERVE src0_sel:WORD_1
	v_exp_f16_sdwa v51, v47 dst_sel:WORD_1 dst_unused:UNUSED_PRESERVE src0_sel:WORD_1
	v_exp_f16_sdwa v52, v48 dst_sel:WORD_1 dst_unused:UNUSED_PRESERVE src0_sel:WORD_1
	v_exp_f16_sdwa v53, v49 dst_sel:WORD_1 dst_unused:UNUSED_PRESERVE src0_sel:WORD_1
	v_pk_add_f16 v46, v78, v114 neg_lo:[0,1] neg_hi:[0,1]
	v_pk_add_f16 v34, v34, v53
	v_pk_add_f16 v35, v35, v52
	v_pk_add_f16 v36, v36, v51
	v_pk_add_f16 v37, v37, v50
	v_pk_fma_f16 v22, v10, v50, v22
	v_pk_fma_f16 v23, v11, v51, v23
	v_pk_fma_f16 v24, v12, v52, v24
	v_pk_fma_f16 v25, v13, v53, v25
	v_pk_add_f16 v47, v79, v115 neg_lo:[0,1] neg_hi:[0,1]
	v_pk_add_f16 v48, v80, v116 neg_lo:[0,1] neg_hi:[0,1]
	v_pk_add_f16 v49, v81, v117 neg_lo:[0,1] neg_hi:[0,1]
	v_exp_f16_sdwa v50, v46 dst_sel:WORD_0 dst_unused:UNUSED_PAD src0_sel:WORD_0
	v_exp_f16_sdwa v51, v47 dst_sel:WORD_0 dst_unused:UNUSED_PAD src0_sel:WORD_0
	v_exp_f16_sdwa v52, v48 dst_sel:WORD_0 dst_unused:UNUSED_PAD src0_sel:WORD_0
	v_exp_f16_sdwa v53, v49 dst_sel:WORD_0 dst_unused:UNUSED_PAD src0_sel:WORD_0
	v_exp_f16_sdwa v50, v46 dst_sel:WORD_1 dst_unused:UNUSED_PRESERVE src0_sel:WORD_1
	v_exp_f16_sdwa v51, v47 dst_sel:WORD_1 dst_unused:UNUSED_PRESERVE src0_sel:WORD_1
	v_exp_f16_sdwa v52, v48 dst_sel:WORD_1 dst_unused:UNUSED_PRESERVE src0_sel:WORD_1
	v_exp_f16_sdwa v53, v49 dst_sel:WORD_1 dst_unused:UNUSED_PRESERVE src0_sel:WORD_1
	v_pk_add_f16 v46, v105, v114 neg_lo:[0,1] neg_hi:[0,1]
	v_pk_add_f16 v34, v34, v53
	v_pk_add_f16 v37, v37, v50
	v_pk_add_f16 v36, v36, v51
	v_pk_add_f16 v35, v35, v52
	v_pk_fma_f16 v25, v17, v53, v25
	v_pk_fma_f16 v24, v16, v52, v24
	v_pk_fma_f16 v23, v15, v51, v23
	v_pk_fma_f16 v22, v14, v50, v22
	v_pk_add_f16 v47, v104, v115 neg_lo:[0,1] neg_hi:[0,1]
	v_pk_add_f16 v48, v103, v116 neg_lo:[0,1] neg_hi:[0,1]
	v_pk_add_f16 v49, v102, v117 neg_lo:[0,1] neg_hi:[0,1]
	v_exp_f16_sdwa v50, v46 dst_sel:WORD_0 dst_unused:UNUSED_PAD src0_sel:WORD_0
	v_exp_f16_sdwa v51, v47 dst_sel:WORD_0 dst_unused:UNUSED_PAD src0_sel:WORD_0
	v_exp_f16_sdwa v52, v48 dst_sel:WORD_0 dst_unused:UNUSED_PAD src0_sel:WORD_0
	v_exp_f16_sdwa v53, v49 dst_sel:WORD_0 dst_unused:UNUSED_PAD src0_sel:WORD_0
	v_exp_f16_sdwa v50, v46 dst_sel:WORD_1 dst_unused:UNUSED_PRESERVE src0_sel:WORD_1
	v_exp_f16_sdwa v51, v47 dst_sel:WORD_1 dst_unused:UNUSED_PRESERVE src0_sel:WORD_1
	v_exp_f16_sdwa v52, v48 dst_sel:WORD_1 dst_unused:UNUSED_PRESERVE src0_sel:WORD_1
	v_exp_f16_sdwa v53, v49 dst_sel:WORD_1 dst_unused:UNUSED_PRESERVE src0_sel:WORD_1
	v_pk_add_f16 v46, v109, v114 neg_lo:[0,1] neg_hi:[0,1]
	v_pk_add_f16 v34, v34, v53
	v_pk_add_f16 v35, v35, v52
	v_pk_add_f16 v36, v36, v51
	v_pk_add_f16 v37, v37, v50
	v_pk_fma_f16 v22, v26, v50, v22
	v_pk_fma_f16 v23, v27, v51, v23
	v_pk_fma_f16 v24, v28, v52, v24
	v_pk_fma_f16 v25, v29, v53, v25
	v_pk_add_f16 v47, v108, v115 neg_lo:[0,1] neg_hi:[0,1]
	v_pk_add_f16 v48, v107, v116 neg_lo:[0,1] neg_hi:[0,1]
	v_pk_add_f16 v49, v106, v117 neg_lo:[0,1] neg_hi:[0,1]
	v_exp_f16_sdwa v50, v46 dst_sel:WORD_0 dst_unused:UNUSED_PAD src0_sel:WORD_0
	v_exp_f16_sdwa v51, v47 dst_sel:WORD_0 dst_unused:UNUSED_PAD src0_sel:WORD_0
	v_exp_f16_sdwa v52, v48 dst_sel:WORD_0 dst_unused:UNUSED_PAD src0_sel:WORD_0
	v_exp_f16_sdwa v53, v49 dst_sel:WORD_0 dst_unused:UNUSED_PAD src0_sel:WORD_0
	v_exp_f16_sdwa v50, v46 dst_sel:WORD_1 dst_unused:UNUSED_PRESERVE src0_sel:WORD_1
	v_exp_f16_sdwa v51, v47 dst_sel:WORD_1 dst_unused:UNUSED_PRESERVE src0_sel:WORD_1
	v_exp_f16_sdwa v52, v48 dst_sel:WORD_1 dst_unused:UNUSED_PRESERVE src0_sel:WORD_1
	v_exp_f16_sdwa v53, v49 dst_sel:WORD_1 dst_unused:UNUSED_PRESERVE src0_sel:WORD_1
	v_pk_add_f16 v46, v82, v114 neg_lo:[0,1] neg_hi:[0,1]
	v_pk_add_f16 v34, v34, v53
	v_pk_add_f16 v37, v37, v50
	v_pk_add_f16 v36, v36, v51
	v_pk_add_f16 v35, v35, v52
	v_pk_fma_f16 v25, v41, v53, v25
	v_pk_fma_f16 v24, v40, v52, v24
	v_pk_fma_f16 v23, v39, v51, v23
	v_pk_fma_f16 v22, v38, v50, v22
	v_pk_add_f16 v47, v83, v115 neg_lo:[0,1] neg_hi:[0,1]
	v_pk_add_f16 v48, v84, v116 neg_lo:[0,1] neg_hi:[0,1]
	v_pk_add_f16 v49, v85, v117 neg_lo:[0,1] neg_hi:[0,1]
	v_exp_f16_sdwa v50, v46 dst_sel:WORD_0 dst_unused:UNUSED_PAD src0_sel:WORD_0
	v_exp_f16_sdwa v51, v47 dst_sel:WORD_0 dst_unused:UNUSED_PAD src0_sel:WORD_0
	v_exp_f16_sdwa v52, v48 dst_sel:WORD_0 dst_unused:UNUSED_PAD src0_sel:WORD_0
	v_exp_f16_sdwa v53, v49 dst_sel:WORD_0 dst_unused:UNUSED_PAD src0_sel:WORD_0
	v_exp_f16_sdwa v50, v46 dst_sel:WORD_1 dst_unused:UNUSED_PRESERVE src0_sel:WORD_1
	v_exp_f16_sdwa v51, v47 dst_sel:WORD_1 dst_unused:UNUSED_PRESERVE src0_sel:WORD_1
	v_exp_f16_sdwa v52, v48 dst_sel:WORD_1 dst_unused:UNUSED_PRESERVE src0_sel:WORD_1
	v_exp_f16_sdwa v53, v49 dst_sel:WORD_1 dst_unused:UNUSED_PRESERVE src0_sel:WORD_1
	s_nop 0
	v_pk_add_f16 v34, v34, v53
	v_pk_add_f16 v35, v35, v52
	v_rcp_f16_e32 v48, v34
	v_rcp_f16_sdwa v34, v34 dst_sel:DWORD dst_unused:UNUSED_PAD src0_sel:WORD_1
	v_pk_add_f16 v36, v36, v51
	v_rcp_f16_e32 v49, v35
	v_rcp_f16_sdwa v35, v35 dst_sel:DWORD dst_unused:UNUSED_PAD src0_sel:WORD_1
	v_pk_add_f16 v37, v37, v50
	v_rcp_f16_e32 v47, v36
	v_rcp_f16_sdwa v36, v36 dst_sel:DWORD dst_unused:UNUSED_PAD src0_sel:WORD_1
	v_rcp_f16_e32 v46, v37
	v_rcp_f16_sdwa v37, v37 dst_sel:DWORD dst_unused:UNUSED_PAD src0_sel:WORD_1
	v_pk_fma_f16 v25, v61, v53, v25
	v_pack_b32_f16 v34, v48, v34
	v_pk_fma_f16 v24, v60, v52, v24
	v_pk_mul_f16 v25, v25, v34
	v_pack_b32_f16 v34, v49, v35
	v_pk_fma_f16 v23, v59, v51, v23
	v_pk_mul_f16 v24, v24, v34
	v_pack_b32_f16 v34, v47, v36
	v_pk_fma_f16 v22, v58, v50, v22
	v_pk_mul_f16 v23, v23, v34
	v_pack_b32_f16 v34, v46, v37
	v_pk_mul_f16 v22, v22, v34
	s_waitcnt vmcnt(0)
	v_pk_mul_f16 v34, v182, v146 op_sel_hi:[0,1]
	v_pk_mul_f16 v35, v182, v147 op_sel_hi:[0,1]
	v_pk_mul_f16 v36, v182, v148 op_sel_hi:[0,1]
	v_pk_mul_f16 v37, v182, v149 op_sel_hi:[0,1]
	v_pk_mul_f16 v46, v180, v146 op_sel_hi:[0,1]
	v_pk_mul_f16 v47, v180, v147 op_sel_hi:[0,1]
	v_pk_mul_f16 v48, v180, v148 op_sel_hi:[0,1]
	v_pk_mul_f16 v49, v180, v149 op_sel_hi:[0,1]
	v_pk_mul_f16 v50, v181, v146 op_sel_hi:[0,1]
	v_pk_mul_f16 v51, v181, v147 op_sel_hi:[0,1]
	v_pk_mul_f16 v52, v181, v148 op_sel_hi:[0,1]
	v_pk_mul_f16 v53, v181, v149 op_sel_hi:[0,1]
	v_pk_fma_f16 v21, v21, v149, v37
	v_pk_fma_f16 v20, v20, v148, v36
	v_pk_fma_f16 v19, v19, v147, v35
	v_pk_fma_f16 v18, v18, v146, v34
	v_pk_fma_f16 v33, v33, v149, v37
	v_pk_fma_f16 v32, v32, v148, v36
	v_pk_fma_f16 v31, v31, v147, v35
	v_pk_fma_f16 v30, v30, v146, v34
	v_pk_fma_f16 v37, v57, v149, v37
	v_pk_fma_f16 v36, v56, v148, v36
	v_pk_fma_f16 v35, v55, v147, v35
	v_pk_fma_f16 v34, v54, v146, v34
	v_pk_maximum3_f16 v79, v19, v31, v35
	v_pk_maximum3_f16 v80, v20, v32, v36
	v_pk_maximum3_f16 v81, v21, v33, v37
	v_pk_fma_f16 v54, v77, v149, v49
	v_pk_maximum3_f16 v78, v18, v30, v34
	v_pk_fma_f16 v55, v76, v148, v48
	v_pk_fma_f16 v56, v75, v147, v47
	v_pk_fma_f16 v57, v74, v146, v46
	v_pk_fma_f16 v62, v101, v149, v49
	v_pk_fma_f16 v63, v100, v148, v48
	v_pk_fma_f16 v64, v99, v147, v47
	v_pk_fma_f16 v65, v98, v146, v46
	v_pk_fma_f16 v49, v121, v149, v49
	v_pk_fma_f16 v48, v120, v148, v48
	v_pk_fma_f16 v47, v119, v147, v47
	v_pk_fma_f16 v46, v118, v146, v46
	v_pk_fma_f16 v66, v133, v149, v53
	v_pk_fma_f16 v67, v132, v148, v52
	v_pk_fma_f16 v68, v131, v147, v51
	v_pk_fma_f16 v69, v130, v146, v50
	v_pk_fma_f16 v74, v141, v149, v53
	v_pk_fma_f16 v75, v140, v148, v52
	v_pk_fma_f16 v76, v139, v147, v51
	v_pk_fma_f16 v77, v138, v146, v50
	v_pk_fma_f16 v53, v145, v149, v53
	v_pk_fma_f16 v52, v144, v148, v52
	v_pk_fma_f16 v51, v143, v147, v51
	v_pk_fma_f16 v50, v142, v146, v50
	v_pk_maximum3_f16 v82, v57, v65, v46
	v_pk_maximum3_f16 v83, v56, v64, v47
	v_pk_maximum3_f16 v84, v55, v63, v48
	v_pk_maximum3_f16 v85, v54, v62, v49
	v_pk_maximum3_f16 v87, v68, v76, v51
	v_pk_maximum3_f16 v86, v69, v77, v50
	v_pk_maximum3_f16 v88, v67, v75, v52
	v_pk_maximum3_f16 v89, v66, v74, v53
	v_pk_maximum3_f16 v78, v78, v82, v86
	v_pk_maximum3_f16 v79, v79, v83, v87
	v_pk_maximum3_f16 v80, v80, v84, v88
	v_pk_maximum3_f16 v81, v81, v85, v89
	s_nop 0
	v_pk_add_f16 v18, v18, v78 neg_lo:[0,1] neg_hi:[0,1]
	v_pk_add_f16 v19, v19, v79 neg_lo:[0,1] neg_hi:[0,1]
	v_pk_add_f16 v20, v20, v80 neg_lo:[0,1] neg_hi:[0,1]
	v_pk_add_f16 v21, v21, v81 neg_lo:[0,1] neg_hi:[0,1]
	v_pk_add_f16 v30, v30, v78 neg_lo:[0,1] neg_hi:[0,1]
	v_exp_f16_sdwa v82, v18 dst_sel:WORD_0 dst_unused:UNUSED_PAD src0_sel:WORD_0
	v_exp_f16_sdwa v83, v19 dst_sel:WORD_0 dst_unused:UNUSED_PAD src0_sel:WORD_0
	v_exp_f16_sdwa v84, v20 dst_sel:WORD_0 dst_unused:UNUSED_PAD src0_sel:WORD_0
	v_exp_f16_sdwa v85, v21 dst_sel:WORD_0 dst_unused:UNUSED_PAD src0_sel:WORD_0
	v_exp_f16_sdwa v82, v18 dst_sel:WORD_1 dst_unused:UNUSED_PRESERVE src0_sel:WORD_1
	v_exp_f16_sdwa v83, v19 dst_sel:WORD_1 dst_unused:UNUSED_PRESERVE src0_sel:WORD_1
	v_exp_f16_sdwa v84, v20 dst_sel:WORD_1 dst_unused:UNUSED_PRESERVE src0_sel:WORD_1
	v_exp_f16_sdwa v85, v21 dst_sel:WORD_1 dst_unused:UNUSED_PRESERVE src0_sel:WORD_1
	v_pk_add_f16 v31, v31, v79 neg_lo:[0,1] neg_hi:[0,1]
	v_pk_add_f16 v18, v82, 0
	v_pk_add_f16 v19, v83, 0
	v_pk_add_f16 v20, v84, 0
	v_pk_add_f16 v21, v85, 0
	v_pk_fma_f16 v6, v6, v82, 0
	v_pk_fma_f16 v7, v7, v83, 0
	v_pk_fma_f16 v8, v8, v84, 0
	v_pk_fma_f16 v9, v9, v85, 0
	v_pk_add_f16 v32, v32, v80 neg_lo:[0,1] neg_hi:[0,1]
	v_pk_add_f16 v33, v33, v81 neg_lo:[0,1] neg_hi:[0,1]
	v_exp_f16_sdwa v82, v30 dst_sel:WORD_0 dst_unused:UNUSED_PAD src0_sel:WORD_0
	v_exp_f16_sdwa v83, v31 dst_sel:WORD_0 dst_unused:UNUSED_PAD src0_sel:WORD_0
	v_exp_f16_sdwa v84, v32 dst_sel:WORD_0 dst_unused:UNUSED_PAD src0_sel:WORD_0
	v_exp_f16_sdwa v85, v33 dst_sel:WORD_0 dst_unused:UNUSED_PAD src0_sel:WORD_0
	v_exp_f16_sdwa v82, v30 dst_sel:WORD_1 dst_unused:UNUSED_PRESERVE src0_sel:WORD_1
	v_exp_f16_sdwa v83, v31 dst_sel:WORD_1 dst_unused:UNUSED_PRESERVE src0_sel:WORD_1
	v_exp_f16_sdwa v84, v32 dst_sel:WORD_1 dst_unused:UNUSED_PRESERVE src0_sel:WORD_1
	v_exp_f16_sdwa v85, v33 dst_sel:WORD_1 dst_unused:UNUSED_PRESERVE src0_sel:WORD_1
	s_nop 0
	v_pk_add_f16 v21, v21, v85
	v_pk_add_f16 v20, v20, v84
	v_pk_add_f16 v19, v19, v83
	v_pk_add_f16 v18, v18, v82
	v_pk_fma_f16 v9, v13, v85, v9
	v_pk_fma_f16 v8, v12, v84, v8
	v_pk_fma_f16 v7, v11, v83, v7
	v_pk_fma_f16 v6, v10, v82, v6
	v_pk_add_f16 v10, v34, v78 neg_lo:[0,1] neg_hi:[0,1]
	v_pk_add_f16 v11, v35, v79 neg_lo:[0,1] neg_hi:[0,1]
	v_pk_add_f16 v12, v36, v80 neg_lo:[0,1] neg_hi:[0,1]
	v_pk_add_f16 v13, v37, v81 neg_lo:[0,1] neg_hi:[0,1]
	v_exp_f16_sdwa v30, v10 dst_sel:WORD_0 dst_unused:UNUSED_PAD src0_sel:WORD_0
	v_exp_f16_sdwa v31, v11 dst_sel:WORD_0 dst_unused:UNUSED_PAD src0_sel:WORD_0
	v_exp_f16_sdwa v32, v12 dst_sel:WORD_0 dst_unused:UNUSED_PAD src0_sel:WORD_0
	v_exp_f16_sdwa v33, v13 dst_sel:WORD_0 dst_unused:UNUSED_PAD src0_sel:WORD_0
	v_exp_f16_sdwa v30, v10 dst_sel:WORD_1 dst_unused:UNUSED_PRESERVE src0_sel:WORD_1
	v_exp_f16_sdwa v31, v11 dst_sel:WORD_1 dst_unused:UNUSED_PRESERVE src0_sel:WORD_1
	v_exp_f16_sdwa v32, v12 dst_sel:WORD_1 dst_unused:UNUSED_PRESERVE src0_sel:WORD_1
	v_exp_f16_sdwa v33, v13 dst_sel:WORD_1 dst_unused:UNUSED_PRESERVE src0_sel:WORD_1
	v_pk_add_f16 v10, v18, v30
	v_pk_add_f16 v11, v19, v31
	v_pk_add_f16 v12, v20, v32
	v_pk_add_f16 v13, v21, v33
	v_pk_fma_f16 v6, v14, v30, v6
	v_pk_fma_f16 v7, v15, v31, v7
	v_pk_fma_f16 v8, v16, v32, v8
	v_pk_fma_f16 v9, v17, v33, v9
	v_pk_add_f16 v14, v57, v78 neg_lo:[0,1] neg_hi:[0,1]
	v_pk_add_f16 v15, v56, v79 neg_lo:[0,1] neg_hi:[0,1]
	v_pk_add_f16 v16, v55, v80 neg_lo:[0,1] neg_hi:[0,1]
	v_pk_add_f16 v17, v54, v81 neg_lo:[0,1] neg_hi:[0,1]
	v_exp_f16_sdwa v18, v14 dst_sel:WORD_0 dst_unused:UNUSED_PAD src0_sel:WORD_0
	v_exp_f16_sdwa v19, v15 dst_sel:WORD_0 dst_unused:UNUSED_PAD src0_sel:WORD_0
	v_exp_f16_sdwa v20, v16 dst_sel:WORD_0 dst_unused:UNUSED_PAD src0_sel:WORD_0
	v_exp_f16_sdwa v21, v17 dst_sel:WORD_0 dst_unused:UNUSED_PAD src0_sel:WORD_0
	v_exp_f16_sdwa v18, v14 dst_sel:WORD_1 dst_unused:UNUSED_PRESERVE src0_sel:WORD_1
	v_exp_f16_sdwa v19, v15 dst_sel:WORD_1 dst_unused:UNUSED_PRESERVE src0_sel:WORD_1
	v_exp_f16_sdwa v20, v16 dst_sel:WORD_1 dst_unused:UNUSED_PRESERVE src0_sel:WORD_1
	v_exp_f16_sdwa v21, v17 dst_sel:WORD_1 dst_unused:UNUSED_PRESERVE src0_sel:WORD_1
	v_pk_add_f16 v14, v65, v78 neg_lo:[0,1] neg_hi:[0,1]
	v_pk_add_f16 v13, v13, v21
	v_pk_add_f16 v12, v12, v20
	v_pk_add_f16 v11, v11, v19
	v_pk_add_f16 v10, v10, v18
	v_pk_fma_f16 v9, v29, v21, v9
	v_pk_fma_f16 v8, v28, v20, v8
	v_pk_fma_f16 v7, v27, v19, v7
	v_pk_fma_f16 v6, v26, v18, v6
	v_pk_add_f16 v15, v64, v79 neg_lo:[0,1] neg_hi:[0,1]
	v_pk_add_f16 v16, v63, v80 neg_lo:[0,1] neg_hi:[0,1]
	v_pk_add_f16 v17, v62, v81 neg_lo:[0,1] neg_hi:[0,1]
	v_exp_f16_sdwa v18, v14 dst_sel:WORD_0 dst_unused:UNUSED_PAD src0_sel:WORD_0
	v_exp_f16_sdwa v19, v15 dst_sel:WORD_0 dst_unused:UNUSED_PAD src0_sel:WORD_0
	v_exp_f16_sdwa v20, v16 dst_sel:WORD_0 dst_unused:UNUSED_PAD src0_sel:WORD_0
	v_exp_f16_sdwa v21, v17 dst_sel:WORD_0 dst_unused:UNUSED_PAD src0_sel:WORD_0
	v_exp_f16_sdwa v18, v14 dst_sel:WORD_1 dst_unused:UNUSED_PRESERVE src0_sel:WORD_1
	v_exp_f16_sdwa v19, v15 dst_sel:WORD_1 dst_unused:UNUSED_PRESERVE src0_sel:WORD_1
	v_exp_f16_sdwa v20, v16 dst_sel:WORD_1 dst_unused:UNUSED_PRESERVE src0_sel:WORD_1
	v_exp_f16_sdwa v21, v17 dst_sel:WORD_1 dst_unused:UNUSED_PRESERVE src0_sel:WORD_1
	v_pk_add_f16 v14, v46, v78 neg_lo:[0,1] neg_hi:[0,1]
	v_pk_add_f16 v10, v10, v18
	v_pk_add_f16 v11, v11, v19
	v_pk_add_f16 v12, v12, v20
	v_pk_add_f16 v13, v13, v21
	v_pk_fma_f16 v6, v38, v18, v6
	v_pk_fma_f16 v7, v39, v19, v7
	v_pk_fma_f16 v8, v40, v20, v8
	v_pk_fma_f16 v9, v41, v21, v9
	v_pk_add_f16 v15, v47, v79 neg_lo:[0,1] neg_hi:[0,1]
	v_pk_add_f16 v16, v48, v80 neg_lo:[0,1] neg_hi:[0,1]
	v_pk_add_f16 v17, v49, v81 neg_lo:[0,1] neg_hi:[0,1]
	v_exp_f16_sdwa v18, v14 dst_sel:WORD_0 dst_unused:UNUSED_PAD src0_sel:WORD_0
	v_exp_f16_sdwa v19, v15 dst_sel:WORD_0 dst_unused:UNUSED_PAD src0_sel:WORD_0
	v_exp_f16_sdwa v20, v16 dst_sel:WORD_0 dst_unused:UNUSED_PAD src0_sel:WORD_0
	v_exp_f16_sdwa v21, v17 dst_sel:WORD_0 dst_unused:UNUSED_PAD src0_sel:WORD_0
	v_exp_f16_sdwa v18, v14 dst_sel:WORD_1 dst_unused:UNUSED_PRESERVE src0_sel:WORD_1
	v_exp_f16_sdwa v19, v15 dst_sel:WORD_1 dst_unused:UNUSED_PRESERVE src0_sel:WORD_1
	v_exp_f16_sdwa v20, v16 dst_sel:WORD_1 dst_unused:UNUSED_PRESERVE src0_sel:WORD_1
	v_exp_f16_sdwa v21, v17 dst_sel:WORD_1 dst_unused:UNUSED_PRESERVE src0_sel:WORD_1
	v_pk_add_f16 v14, v69, v78 neg_lo:[0,1] neg_hi:[0,1]
	v_pk_add_f16 v13, v13, v21
	v_pk_add_f16 v12, v12, v20
	v_pk_add_f16 v11, v11, v19
	v_pk_add_f16 v10, v10, v18
	v_pk_fma_f16 v9, v61, v21, v9
	v_pk_fma_f16 v8, v60, v20, v8
	v_pk_fma_f16 v7, v59, v19, v7
	v_pk_fma_f16 v6, v58, v18, v6
	v_pk_add_f16 v15, v68, v79 neg_lo:[0,1] neg_hi:[0,1]
	v_pk_add_f16 v16, v67, v80 neg_lo:[0,1] neg_hi:[0,1]
	v_pk_add_f16 v17, v66, v81 neg_lo:[0,1] neg_hi:[0,1]
	v_exp_f16_sdwa v18, v14 dst_sel:WORD_0 dst_unused:UNUSED_PAD src0_sel:WORD_0
	v_exp_f16_sdwa v19, v15 dst_sel:WORD_0 dst_unused:UNUSED_PAD src0_sel:WORD_0
	v_exp_f16_sdwa v20, v16 dst_sel:WORD_0 dst_unused:UNUSED_PAD src0_sel:WORD_0
	v_exp_f16_sdwa v21, v17 dst_sel:WORD_0 dst_unused:UNUSED_PAD src0_sel:WORD_0
	v_exp_f16_sdwa v18, v14 dst_sel:WORD_1 dst_unused:UNUSED_PRESERVE src0_sel:WORD_1
	v_exp_f16_sdwa v19, v15 dst_sel:WORD_1 dst_unused:UNUSED_PRESERVE src0_sel:WORD_1
	v_exp_f16_sdwa v20, v16 dst_sel:WORD_1 dst_unused:UNUSED_PRESERVE src0_sel:WORD_1
	v_exp_f16_sdwa v21, v17 dst_sel:WORD_1 dst_unused:UNUSED_PRESERVE src0_sel:WORD_1
	v_pk_add_f16 v10, v10, v18
	v_pk_add_f16 v11, v11, v19
	v_pk_add_f16 v12, v12, v20
	v_pk_add_f16 v13, v13, v21
	v_pk_fma_f16 v14, v70, v18, v6
	v_pk_fma_f16 v15, v71, v19, v7
	v_pk_fma_f16 v16, v72, v20, v8
	v_pk_fma_f16 v17, v73, v21, v9
	v_pk_add_f16 v6, v77, v78 neg_lo:[0,1] neg_hi:[0,1]
	v_pk_add_f16 v7, v76, v79 neg_lo:[0,1] neg_hi:[0,1]
	v_pk_add_f16 v8, v75, v80 neg_lo:[0,1] neg_hi:[0,1]
	v_pk_add_f16 v9, v74, v81 neg_lo:[0,1] neg_hi:[0,1]
	v_exp_f16_sdwa v18, v6 dst_sel:WORD_0 dst_unused:UNUSED_PAD src0_sel:WORD_0
	v_exp_f16_sdwa v19, v7 dst_sel:WORD_0 dst_unused:UNUSED_PAD src0_sel:WORD_0
	v_exp_f16_sdwa v20, v8 dst_sel:WORD_0 dst_unused:UNUSED_PAD src0_sel:WORD_0
	v_exp_f16_sdwa v21, v9 dst_sel:WORD_0 dst_unused:UNUSED_PAD src0_sel:WORD_0
	v_exp_f16_sdwa v18, v6 dst_sel:WORD_1 dst_unused:UNUSED_PRESERVE src0_sel:WORD_1
	v_exp_f16_sdwa v19, v7 dst_sel:WORD_1 dst_unused:UNUSED_PRESERVE src0_sel:WORD_1
	v_exp_f16_sdwa v20, v8 dst_sel:WORD_1 dst_unused:UNUSED_PRESERVE src0_sel:WORD_1
	v_exp_f16_sdwa v21, v9 dst_sel:WORD_1 dst_unused:UNUSED_PRESERVE src0_sel:WORD_1
	s_nop 0
	v_pk_add_f16 v9, v13, v21
	v_pk_add_f16 v8, v12, v20
	v_pk_add_f16 v7, v11, v19
	v_pk_add_f16 v6, v10, v18
	v_pk_fma_f16 v13, v93, v21, v17
	v_pk_fma_f16 v12, v92, v20, v16
	v_pk_fma_f16 v11, v91, v19, v15
	v_pk_fma_f16 v10, v90, v18, v14
	v_pk_add_f16 v18, v50, v78 neg_lo:[0,1] neg_hi:[0,1]
	v_pk_add_f16 v19, v51, v79 neg_lo:[0,1] neg_hi:[0,1]
	v_pk_add_f16 v20, v52, v80 neg_lo:[0,1] neg_hi:[0,1]
	v_pk_add_f16 v21, v53, v81 neg_lo:[0,1] neg_hi:[0,1]
	v_exp_f16_sdwa v14, v18 dst_sel:WORD_0 dst_unused:UNUSED_PAD src0_sel:WORD_0
	v_exp_f16_sdwa v17, v19 dst_sel:WORD_0 dst_unused:UNUSED_PAD src0_sel:WORD_0
	v_exp_f16_sdwa v15, v20 dst_sel:WORD_0 dst_unused:UNUSED_PAD src0_sel:WORD_0
	v_exp_f16_sdwa v16, v21 dst_sel:WORD_0 dst_unused:UNUSED_PAD src0_sel:WORD_0
	v_exp_f16_sdwa v14, v18 dst_sel:WORD_1 dst_unused:UNUSED_PRESERVE src0_sel:WORD_1
	v_exp_f16_sdwa v17, v19 dst_sel:WORD_1 dst_unused:UNUSED_PRESERVE src0_sel:WORD_1
	v_exp_f16_sdwa v15, v20 dst_sel:WORD_1 dst_unused:UNUSED_PRESERVE src0_sel:WORD_1
	v_exp_f16_sdwa v16, v21 dst_sel:WORD_1 dst_unused:UNUSED_PRESERVE src0_sel:WORD_1
	s_nop 0
.LBB5_3:
	v_pk_add_f16 v9, v9, v16
	v_pk_add_f16 v8, v8, v15
	v_pk_fma_f16 v4, v4, v15, v12
	v_rcp_f16_e32 v12, v9
	v_rcp_f16_sdwa v9, v9 dst_sel:DWORD dst_unused:UNUSED_PAD src0_sel:WORD_1
	v_pk_add_f16 v6, v6, v14
	v_pk_fma_f16 v5, v5, v16, v13
	v_rcp_f16_e32 v13, v8
	v_rcp_f16_sdwa v8, v8 dst_sel:DWORD dst_unused:UNUSED_PAD src0_sel:WORD_1
	v_pk_add_f16 v7, v7, v17
	v_pk_fma_f16 v2, v2, v14, v10
	v_rcp_f16_e32 v10, v6
	v_rcp_f16_sdwa v6, v6 dst_sel:DWORD dst_unused:UNUSED_PAD src0_sel:WORD_1
	v_pk_fma_f16 v3, v3, v17, v11
	v_rcp_f16_e32 v11, v7
	v_rcp_f16_sdwa v7, v7 dst_sel:DWORD dst_unused:UNUSED_PAD src0_sel:WORD_1
	v_pack_b32_f16 v9, v12, v9
	v_pk_mul_f16 v9, v5, v9
	v_pack_b32_f16 v5, v13, v8
	v_pk_mul_f16 v8, v4, v5
	v_pack_b32_f16 v4, v10, v6
	v_pk_mul_f16 v6, v2, v4
	v_pack_b32_f16 v2, v11, v7
	v_pk_mul_f16 v7, v3, v2
	v_pk_max_f16 v2, v113, v113
	v_add_u32_e32 v10, v168, v160
	v_pk_max_f16 v5, v2, 0
	v_pk_max_f16 v2, v112, v112
	s_add_i32 s14, s14, -1
	v_pk_max_f16 v4, v2, 0
	v_pk_max_f16 v2, v111, v111
	s_add_i32 s30, s30, 8
	v_pk_max_f16 v3, v2, 0
	v_pk_max_f16 v2, v110, v110
	v_add_u32_e32 v168, 0x8000, v168
	v_pk_max_f16 v2, v2, 0
	ds_write_b128 v10, v[2:5]
	v_pk_max_f16 v2, v45, v45
	v_bitop3_b32 v10, v166, v159, 15 bitop3:0x6c
	v_pk_max_f16 v5, v2, 0
	v_pk_max_f16 v2, v44, v44
	v_lshlrev_b32_e32 v10, 4, v10
	v_pk_max_f16 v4, v2, 0
	v_pk_max_f16 v2, v43, v43
	v_add3_u32 v10, v160, v10, v167
	v_pk_max_f16 v3, v2, 0
	v_pk_max_f16 v2, v42, v42
	v_add_u32_e32 v166, 64, v166
	v_pk_max_f16 v2, v2, 0
	ds_write_b128 v10, v[2:5]
	v_pk_max_f16 v2, v25, v25
	v_add_u32_e32 v10, v170, v160
	v_pk_max_f16 v5, v2, 0
	v_pk_max_f16 v2, v24, v24
	v_add_u32_e32 v170, 0x8000, v170
	v_pk_max_f16 v4, v2, 0
	v_pk_max_f16 v2, v23, v23
	v_add_u32_e32 v167, 0x8000, v167
	v_pk_max_f16 v3, v2, 0
	v_pk_max_f16 v2, v22, v22
	s_cmp_eq_u32 s14, 0
	v_pk_max_f16 v2, v2, 0
	ds_write_b128 v10, v[2:5]
	v_pk_max_f16 v3, v7, 0
	v_pk_max_f16 v2, v6, 0
	v_pk_max_f16 v4, v8, 0
	v_pk_max_f16 v5, v9, 0
	v_add_u32_e32 v6, v169, v163
	v_add_u32_e32 v163, 0x8000, v163
	v_add_u32_e32 v171, 0x3000, v171
	ds_write_b128 v6, v[2:5]
	s_cbranch_scc1 .LBB5_79
.LBB5_4:
	v_add_u32_e32 v182, s30, v161
	v_add_u32_e32 v181, -1, v182
	v_or_b32_e32 v2, v181, v164
	v_add_u32_e32 v180, 0x18400, v171
	v_cmp_gt_u32_e64 s[0:1], 64, v2
	s_mov_b64 s[4:5], -1
	s_and_b64 vcc, exec, s[24:25]
	s_cbranch_vccz .LBB5_42
	s_load_dwordx2 s[4:5], s[22:23], 0x20
	s_waitcnt lgkmcnt(0)
	s_load_dwordx2 s[26:27], s[4:5], 0x0
	s_load_dword s31, s[4:5], 0x8
	v_cmp_lt_u32_e64 s[64:65], 0, v182
	v_cmp_gt_u32_e64 s[66:67], 63, v182
	v_cmp_lt_u32_e64 s[68:69], 0, v162
	v_cmp_gt_u32_e64 s[70:71], 60, v162
	buffer_load_dwordx4 v[186:189], v180, s[16:19], 0 offen
	s_and_b64 s[72:73], s[68:69], s[64:65]
	s_and_b64 s[74:75], s[68:69], s[66:67]
	s_and_b64 s[76:77], s[70:71], s[64:65]
	s_and_b64 s[78:79], s[70:71], s[66:67]
	v_mov_b32_e32 v110, v172
	v_mov_b32_e32 v111, v174
	v_mov_b32_e32 v112, v176
	v_mov_b32_e32 v113, v178
	v_mov_b32_e32 v70, v173
	v_mov_b32_e32 v71, v175
	v_mov_b32_e32 v72, v177
	v_mov_b32_e32 v73, v179
	v_mov_b32_e32 v126, v172
	v_mov_b32_e32 v127, v174
	v_mov_b32_e32 v128, v176
	v_mov_b32_e32 v129, v178
	v_mov_b32_e32 v98, v173
	v_mov_b32_e32 v99, v175
	v_mov_b32_e32 v100, v177
	v_mov_b32_e32 v101, v179
	v_mov_b32_e32 v134, v172
	v_mov_b32_e32 v135, v174
	v_mov_b32_e32 v136, v176
	v_mov_b32_e32 v137, v178
	v_mov_b32_e32 v114, v173
	v_mov_b32_e32 v115, v175
	v_mov_b32_e32 v116, v177
	v_mov_b32_e32 v117, v179
	v_mov_b32_e32 v82, v172
	v_mov_b32_e32 v83, v174
	v_mov_b32_e32 v84, v176
	v_mov_b32_e32 v85, v178
	v_mov_b32_e32 v42, v173
	v_mov_b32_e32 v43, v175
	v_mov_b32_e32 v44, v177
	v_mov_b32_e32 v45, v179
	v_mov_b32_e32 v122, v172
	v_mov_b32_e32 v123, v174
	v_mov_b32_e32 v124, v176
	v_mov_b32_e32 v125, v178
	v_mov_b32_e32 v86, v173
	v_mov_b32_e32 v87, v175
	v_mov_b32_e32 v88, v177
	v_mov_b32_e32 v89, v179
	v_mov_b32_e32 v50, v172
	v_mov_b32_e32 v51, v174
	v_mov_b32_e32 v52, v176
	v_mov_b32_e32 v53, v178
	v_mov_b32_e32 v22, v173
	v_mov_b32_e32 v23, v175
	v_mov_b32_e32 v24, v177
	v_mov_b32_e32 v25, v179
	v_mov_b32_e32 v94, v172
	v_mov_b32_e32 v95, v174
	v_mov_b32_e32 v96, v176
	v_mov_b32_e32 v97, v178
	v_mov_b32_e32 v46, v173
	v_mov_b32_e32 v47, v175
	v_mov_b32_e32 v48, v177
	v_mov_b32_e32 v49, v179
	v_mov_b32_e32 v18, v172
	v_mov_b32_e32 v19, v174
	v_mov_b32_e32 v20, v176
	v_mov_b32_e32 v21, v178
	v_mov_b32_e32 v6, v173
	v_mov_b32_e32 v7, v175
	v_mov_b32_e32 v8, v177
	v_mov_b32_e32 v9, v179
	v_mov_b32_e32 v54, v172
	v_mov_b32_e32 v55, v174
	v_mov_b32_e32 v56, v176
	v_mov_b32_e32 v57, v178
	v_mov_b32_e32 v14, v173
	v_mov_b32_e32 v15, v175
	v_mov_b32_e32 v16, v177
	v_mov_b32_e32 v17, v179
	v_mov_b32_e32 v74, v172
	v_mov_b32_e32 v75, v174
	v_mov_b32_e32 v76, v176
	v_mov_b32_e32 v77, v178
	v_mov_b32_e32 v26, v173
	v_mov_b32_e32 v27, v175
	v_mov_b32_e32 v28, v177
	v_mov_b32_e32 v29, v179
	v_mov_b32_e32 v118, v172
	v_mov_b32_e32 v119, v174
	v_mov_b32_e32 v120, v176
	v_mov_b32_e32 v121, v178
	v_mov_b32_e32 v58, v173
	v_mov_b32_e32 v59, v175
	v_mov_b32_e32 v60, v177
	v_mov_b32_e32 v61, v179
	v_mov_b32_e32 v130, v172
	v_mov_b32_e32 v131, v174
	v_mov_b32_e32 v132, v176
	v_mov_b32_e32 v133, v178
	v_mov_b32_e32 v78, v173
	v_mov_b32_e32 v79, v175
	v_mov_b32_e32 v80, v177
	v_mov_b32_e32 v81, v179
	v_mov_b32_e32 v138, v172
	v_mov_b32_e32 v139, v174
	v_mov_b32_e32 v140, v176
	v_mov_b32_e32 v141, v178
	v_mov_b32_e32 v90, v173
	v_mov_b32_e32 v91, v175
	v_mov_b32_e32 v92, v177
	v_mov_b32_e32 v93, v179
	v_mov_b32_e32 v142, v172
	v_mov_b32_e32 v143, v174
	v_mov_b32_e32 v144, v176
	v_mov_b32_e32 v145, v178
	v_mov_b32_e32 v2, v173
	v_mov_b32_e32 v3, v175
	v_mov_b32_e32 v4, v177
	v_mov_b32_e32 v5, v179
	v_add_u32_e32 v224, 0xfffe7c00, v180
	v_add_u32_e32 v225, 0xfffe8000, v180
	s_mov_b64 exec, s[72:73]
	buffer_load_dwordx4 v[110:113], v224, s[16:19], 0 offen
	buffer_load_dwordx4 v[70:73], v224, s[16:19], 0 offen offset:512
	s_mov_b64 exec, -1
	s_mov_b64 exec, s[68:69]
	buffer_load_dwordx4 v[126:129], v225, s[16:19], 0 offen offset:512
	buffer_load_dwordx4 v[98:101], v225, s[16:19], 0 offen offset:1024
	s_mov_b64 exec, -1
	s_mov_b64 exec, s[74:75]
	buffer_load_dwordx4 v[134:137], v225, s[16:19], 0 offen offset:2048
	buffer_load_dwordx4 v[114:117], v225, s[16:19], 0 offen offset:2560
	s_mov_b64 exec, -1
	v_add_u32_e32 v224, 0xfffffc00, v180
	s_mov_b64 exec, s[64:65]
	buffer_load_dwordx4 v[82:85], v224, s[16:19], 0 offen
	buffer_load_dwordx4 v[42:45], v224, s[16:19], 0 offen offset:512
	s_mov_b64 exec, -1
	buffer_load_dwordx4 v[106:109], v180, s[16:19], 0 offen offset:512
	buffer_load_dwordx4 v[62:65], v180, s[16:19], 0 offen offset:1024
	s_mov_b64 exec, s[66:67]
	buffer_load_dwordx4 v[122:125], v180, s[16:19], 0 offen offset:2048
	buffer_load_dwordx4 v[86:89], v180, s[16:19], 0 offen offset:2560
	s_mov_b64 exec, -1
	v_add_u32_e32 v224, 0x17c00, v180
	v_add_u32_e32 v225, 0x18000, v180
	s_mov_b64 exec, s[64:65]
	buffer_load_dwordx4 v[50:53], v224, s[16:19], 0 offen
	buffer_load_dwordx4 v[22:25], v224, s[16:19], 0 offen offset:512
	s_mov_b64 exec, -1
	buffer_load_dwordx4 v[66:69], v225, s[16:19], 0 offen offset:512
	buffer_load_dwordx4 v[30:33], v225, s[16:19], 0 offen offset:1024
	s_mov_b64 exec, s[66:67]
	buffer_load_dwordx4 v[94:97], v225, s[16:19], 0 offen offset:2048
	buffer_load_dwordx4 v[46:49], v225, s[16:19], 0 offen offset:2560
	s_mov_b64 exec, -1
	v_add_u32_e32 v224, 0x18000, v180
	buffer_load_dwordx4 v[154:157], v224, s[16:19], 0 offen
	v_add_u32_e32 v225, 0x30000, v180
	buffer_load_dwordx4 v[150:153], v225, s[16:19], 0 offen
	v_add_u32_e32 v224, 0x48000, v180
	buffer_load_dwordx4 v[146:149], v224, s[16:19], 0 offen
	v_add_u32_e32 v224, 0x2fc00, v180
	v_add_u32_e32 v225, 0x30000, v180
	v_add_u32_e32 v226, 0x47c00, v180
	v_add_u32_e32 v227, 0x48000, v180
	v_add_u32_e32 v228, 0x5fc00, v180
	v_add_u32_e32 v229, 0x60000, v180
	s_waitcnt lgkmcnt(0)
	v_cvt_f16_f32_e32 v183, s27
	v_cvt_f16_f32_e32 v185, s26
	v_cvt_f16_f32_e32 v184, s31
	s_mov_b64 s[4:5], 0
	s_waitcnt vmcnt(3)
	v_pk_mul_f16 v193, v185, v189 op_sel_hi:[0,1]
	v_pk_mul_f16 v197, v183, v189 op_sel_hi:[0,1]
	v_pk_mul_f16 v201, v184, v189 op_sel_hi:[0,1]
	v_pk_mul_f16 v190, v185, v186 op_sel_hi:[0,1]
	v_pk_mul_f16 v191, v185, v187 op_sel_hi:[0,1]
	v_pk_mul_f16 v192, v185, v188 op_sel_hi:[0,1]
	v_pk_mul_f16 v194, v183, v186 op_sel_hi:[0,1]
	s_mov_b64 exec, s[64:65]
	buffer_load_dwordx4 v[18:21], v224, s[16:19], 0 offen
	buffer_load_dwordx4 v[6:9], v224, s[16:19], 0 offen offset:512
	s_mov_b64 exec, -1
	v_pk_mul_f16 v195, v183, v187 op_sel_hi:[0,1]
	v_pk_mul_f16 v196, v183, v188 op_sel_hi:[0,1]
	v_pk_mul_f16 v198, v184, v186 op_sel_hi:[0,1]
	v_pk_mul_f16 v199, v184, v187 op_sel_hi:[0,1]
	v_pk_mul_f16 v200, v184, v188 op_sel_hi:[0,1]
	v_pk_fma_f16 v113, v113, v189, v193
	v_pk_fma_f16 v129, v129, v189, v197
	v_pk_fma_f16 v137, v137, v189, v201
	v_pk_fma_f16 v202, v85, v189, v193
	v_pk_fma_f16 v206, v109, v189, v197
	v_pk_fma_f16 v210, v125, v189, v201
	v_pk_fma_f16 v193, v53, v189, v193
	v_pk_fma_f16 v197, v69, v189, v197
	buffer_load_dwordx4 v[34:37], v225, s[16:19], 0 offen offset:512
	buffer_load_dwordx4 v[10:13], v225, s[16:19], 0 offen offset:1024
	v_pk_fma_f16 v189, v97, v189, v201
	v_pk_maximum3_f16 v201, v113, v129, v137
	v_pk_fma_f16 v112, v112, v188, v192
	v_pk_fma_f16 v111, v111, v187, v191
	v_pk_fma_f16 v110, v110, v186, v190
	v_pk_fma_f16 v128, v128, v188, v196
	v_pk_fma_f16 v127, v127, v187, v195
	v_pk_fma_f16 v126, v126, v186, v194
	v_pk_fma_f16 v136, v136, v188, v200
	v_pk_fma_f16 v135, v135, v187, v199
	v_pk_fma_f16 v134, v134, v186, v198
	v_pk_fma_f16 v203, v84, v188, v192
	v_pk_fma_f16 v204, v83, v187, v191
	v_pk_fma_f16 v205, v82, v186, v190
	v_pk_fma_f16 v207, v108, v188, v196
	v_pk_fma_f16 v208, v107, v187, v195
	s_mov_b64 exec, s[66:67]
	buffer_load_dwordx4 v[54:57], v225, s[16:19], 0 offen offset:2048
	buffer_load_dwordx4 v[14:17], v225, s[16:19], 0 offen offset:2560
	s_mov_b64 exec, -1
	v_pk_fma_f16 v209, v106, v186, v194
	v_pk_fma_f16 v211, v124, v188, v200
	v_pk_fma_f16 v212, v123, v187, v199
	v_pk_fma_f16 v213, v122, v186, v198
	v_pk_fma_f16 v192, v52, v188, v192
	v_pk_fma_f16 v191, v51, v187, v191
	v_pk_fma_f16 v190, v50, v186, v190
	v_pk_fma_f16 v196, v68, v188, v196
	v_pk_fma_f16 v195, v67, v187, v195
	v_pk_fma_f16 v194, v66, v186, v194
	v_pk_fma_f16 v188, v96, v188, v200
	v_pk_fma_f16 v187, v95, v187, v199
	v_pk_fma_f16 v186, v94, v186, v198
	v_pk_maximum3_f16 v198, v110, v126, v134
	v_pk_maximum3_f16 v199, v111, v127, v135
	v_pk_maximum3_f16 v200, v112, v128, v136
	v_pk_maximum3_f16 v217, v202, v206, v210
	v_pk_maximum3_f16 v221, v193, v197, v189
	v_pk_maximum3_f16 v214, v205, v209, v213
	v_pk_maximum3_f16 v215, v204, v208, v212
	v_pk_maximum3_f16 v216, v203, v207, v211
	v_pk_maximum3_f16 v218, v190, v194, v186
	v_pk_maximum3_f16 v219, v191, v195, v187
	v_pk_maximum3_f16 v201, v201, v217, v221
	v_pk_maximum3_f16 v220, v192, v196, v188
	v_pk_maximum3_f16 v198, v198, v214, v218
	v_pk_maximum3_f16 v199, v199, v215, v219
	v_pk_maximum3_f16 v200, v200, v216, v220
	v_pk_add_f16 v113, v113, v201 neg_lo:[0,1] neg_hi:[0,1]
	s_mov_b64 exec, s[64:65]
	buffer_load_dwordx4 v[74:77], v226, s[16:19], 0 offen
	buffer_load_dwordx4 v[26:29], v226, s[16:19], 0 offen offset:512
	s_mov_b64 exec, -1
	v_pk_add_f16 v110, v110, v198 neg_lo:[0,1] neg_hi:[0,1]
	v_pk_add_f16 v111, v111, v199 neg_lo:[0,1] neg_hi:[0,1]
	v_pk_add_f16 v112, v112, v200 neg_lo:[0,1] neg_hi:[0,1]
	v_pk_add_f16 v126, v126, v198 neg_lo:[0,1] neg_hi:[0,1]
	v_exp_f16_sdwa v214, v110 dst_sel:WORD_0 dst_unused:UNUSED_PAD src0_sel:WORD_0
	v_exp_f16_sdwa v215, v111 dst_sel:WORD_0 dst_unused:UNUSED_PAD src0_sel:WORD_0
	v_exp_f16_sdwa v216, v112 dst_sel:WORD_0 dst_unused:UNUSED_PAD src0_sel:WORD_0
	v_exp_f16_sdwa v217, v113 dst_sel:WORD_0 dst_unused:UNUSED_PAD src0_sel:WORD_0
	v_exp_f16_sdwa v214, v110 dst_sel:WORD_1 dst_unused:UNUSED_PRESERVE src0_sel:WORD_1
	v_exp_f16_sdwa v215, v111 dst_sel:WORD_1 dst_unused:UNUSED_PRESERVE src0_sel:WORD_1
	v_exp_f16_sdwa v216, v112 dst_sel:WORD_1 dst_unused:UNUSED_PRESERVE src0_sel:WORD_1
	v_exp_f16_sdwa v217, v113 dst_sel:WORD_1 dst_unused:UNUSED_PRESERVE src0_sel:WORD_1
	v_pk_add_f16 v127, v127, v199 neg_lo:[0,1] neg_hi:[0,1]
	v_pk_add_f16 v113, v214, 0
	v_pk_fma_f16 v73, v73, v217, 0
	v_pk_add_f16 v110, v217, 0
	v_pk_add_f16 v111, v216, 0
	v_pk_add_f16 v112, v215, 0
	v_pk_fma_f16 v72, v72, v216, 0
	v_pk_fma_f16 v71, v71, v215, 0
	v_pk_fma_f16 v70, v70, v214, 0
	v_pk_add_f16 v128, v128, v200 neg_lo:[0,1] neg_hi:[0,1]
	buffer_load_dwordx4 v[102:105], v227, s[16:19], 0 offen offset:512
	buffer_load_dwordx4 v[38:41], v227, s[16:19], 0 offen offset:1024
	v_pk_add_f16 v129, v129, v201 neg_lo:[0,1] neg_hi:[0,1]
	v_exp_f16_sdwa v214, v126 dst_sel:WORD_0 dst_unused:UNUSED_PAD src0_sel:WORD_0
	v_exp_f16_sdwa v215, v127 dst_sel:WORD_0 dst_unused:UNUSED_PAD src0_sel:WORD_0
	v_exp_f16_sdwa v216, v128 dst_sel:WORD_0 dst_unused:UNUSED_PAD src0_sel:WORD_0
	v_exp_f16_sdwa v217, v129 dst_sel:WORD_0 dst_unused:UNUSED_PAD src0_sel:WORD_0
	v_exp_f16_sdwa v214, v126 dst_sel:WORD_1 dst_unused:UNUSED_PRESERVE src0_sel:WORD_1
	v_exp_f16_sdwa v215, v127 dst_sel:WORD_1 dst_unused:UNUSED_PRESERVE src0_sel:WORD_1
	v_exp_f16_sdwa v216, v128 dst_sel:WORD_1 dst_unused:UNUSED_PRESERVE src0_sel:WORD_1
	v_exp_f16_sdwa v217, v129 dst_sel:WORD_1 dst_unused:UNUSED_PRESERVE src0_sel:WORD_1
	v_pk_add_f16 v113, v113, v214
	v_pk_fma_f16 v73, v101, v217, v73
	v_pk_add_f16 v101, v137, v201 neg_lo:[0,1] neg_hi:[0,1]
	v_pk_add_f16 v112, v112, v215
	v_pk_add_f16 v111, v111, v216
	v_pk_add_f16 v110, v110, v217
	v_pk_fma_f16 v70, v98, v214, v70
	v_pk_fma_f16 v71, v99, v215, v71
	v_pk_fma_f16 v72, v100, v216, v72
	v_pk_add_f16 v98, v134, v198 neg_lo:[0,1] neg_hi:[0,1]
	v_pk_add_f16 v99, v135, v199 neg_lo:[0,1] neg_hi:[0,1]
	v_pk_add_f16 v100, v136, v200 neg_lo:[0,1] neg_hi:[0,1]
	v_exp_f16_sdwa v126, v98 dst_sel:WORD_0 dst_unused:UNUSED_PAD src0_sel:WORD_0
	v_exp_f16_sdwa v127, v99 dst_sel:WORD_0 dst_unused:UNUSED_PAD src0_sel:WORD_0
	v_exp_f16_sdwa v128, v100 dst_sel:WORD_0 dst_unused:UNUSED_PAD src0_sel:WORD_0
	v_exp_f16_sdwa v129, v101 dst_sel:WORD_0 dst_unused:UNUSED_PAD src0_sel:WORD_0
	v_exp_f16_sdwa v126, v98 dst_sel:WORD_1 dst_unused:UNUSED_PRESERVE src0_sel:WORD_1
	v_exp_f16_sdwa v127, v99 dst_sel:WORD_1 dst_unused:UNUSED_PRESERVE src0_sel:WORD_1
	v_exp_f16_sdwa v128, v100 dst_sel:WORD_1 dst_unused:UNUSED_PRESERVE src0_sel:WORD_1
	v_exp_f16_sdwa v129, v101 dst_sel:WORD_1 dst_unused:UNUSED_PRESERVE src0_sel:WORD_1
	v_pk_add_f16 v101, v113, v126
	v_pk_add_f16 v98, v110, v129
	s_mov_b64 exec, s[66:67]
	buffer_load_dwordx4 v[118:121], v227, s[16:19], 0 offen offset:2048
	buffer_load_dwordx4 v[58:61], v227, s[16:19], 0 offen offset:2560
	s_mov_b64 exec, -1
	v_pk_add_f16 v99, v111, v128
	v_pk_add_f16 v100, v112, v127
	v_pk_fma_f16 v73, v117, v129, v73
	v_pk_fma_f16 v72, v116, v128, v72
	v_pk_fma_f16 v71, v115, v127, v71
	v_pk_fma_f16 v70, v114, v126, v70
	v_pk_add_f16 v110, v205, v198 neg_lo:[0,1] neg_hi:[0,1]
	v_pk_add_f16 v111, v204, v199 neg_lo:[0,1] neg_hi:[0,1]
	v_pk_add_f16 v112, v203, v200 neg_lo:[0,1] neg_hi:[0,1]
	v_pk_add_f16 v113, v202, v201 neg_lo:[0,1] neg_hi:[0,1]
	v_exp_f16_sdwa v114, v110 dst_sel:WORD_0 dst_unused:UNUSED_PAD src0_sel:WORD_0
	v_exp_f16_sdwa v115, v111 dst_sel:WORD_0 dst_unused:UNUSED_PAD src0_sel:WORD_0
	v_exp_f16_sdwa v116, v112 dst_sel:WORD_0 dst_unused:UNUSED_PAD src0_sel:WORD_0
	v_exp_f16_sdwa v117, v113 dst_sel:WORD_0 dst_unused:UNUSED_PAD src0_sel:WORD_0
	v_exp_f16_sdwa v114, v110 dst_sel:WORD_1 dst_unused:UNUSED_PRESERVE src0_sel:WORD_1
	v_exp_f16_sdwa v115, v111 dst_sel:WORD_1 dst_unused:UNUSED_PRESERVE src0_sel:WORD_1
	v_exp_f16_sdwa v116, v112 dst_sel:WORD_1 dst_unused:UNUSED_PRESERVE src0_sel:WORD_1
	v_exp_f16_sdwa v117, v113 dst_sel:WORD_1 dst_unused:UNUSED_PRESERVE src0_sel:WORD_1
	v_pk_add_f16 v110, v209, v198 neg_lo:[0,1] neg_hi:[0,1]
	v_pk_add_f16 v101, v101, v114
	v_pk_add_f16 v100, v100, v115
	v_pk_add_f16 v99, v99, v116
	s_mov_b64 exec, s[76:77]
	buffer_load_dwordx4 v[130:133], v228, s[16:19], 0 offen
	buffer_load_dwordx4 v[78:81], v228, s[16:19], 0 offen offset:512
	s_mov_b64 exec, -1
	v_pk_add_f16 v98, v98, v117
	v_pk_fma_f16 v70, v42, v114, v70
	v_pk_fma_f16 v71, v43, v115, v71
	v_pk_fma_f16 v72, v44, v116, v72
	v_pk_fma_f16 v73, v45, v117, v73
	v_pk_add_f16 v111, v208, v199 neg_lo:[0,1] neg_hi:[0,1]
	v_pk_add_f16 v112, v207, v200 neg_lo:[0,1] neg_hi:[0,1]
	v_pk_add_f16 v113, v206, v201 neg_lo:[0,1] neg_hi:[0,1]
	v_exp_f16_sdwa v114, v110 dst_sel:WORD_0 dst_unused:UNUSED_PAD src0_sel:WORD_0
	v_exp_f16_sdwa v115, v111 dst_sel:WORD_0 dst_unused:UNUSED_PAD src0_sel:WORD_0
	v_exp_f16_sdwa v116, v112 dst_sel:WORD_0 dst_unused:UNUSED_PAD src0_sel:WORD_0
	v_exp_f16_sdwa v117, v113 dst_sel:WORD_0 dst_unused:UNUSED_PAD src0_sel:WORD_0
	v_exp_f16_sdwa v114, v110 dst_sel:WORD_1 dst_unused:UNUSED_PRESERVE src0_sel:WORD_1
	v_exp_f16_sdwa v115, v111 dst_sel:WORD_1 dst_unused:UNUSED_PRESERVE src0_sel:WORD_1
	v_exp_f16_sdwa v116, v112 dst_sel:WORD_1 dst_unused:UNUSED_PRESERVE src0_sel:WORD_1
	v_exp_f16_sdwa v117, v113 dst_sel:WORD_1 dst_unused:UNUSED_PRESERVE src0_sel:WORD_1
	v_pk_add_f16 v110, v213, v198 neg_lo:[0,1] neg_hi:[0,1]
	v_pk_add_f16 v101, v101, v114
	v_pk_add_f16 v98, v98, v117
	v_pk_add_f16 v99, v99, v116
	v_pk_add_f16 v100, v100, v115
	v_pk_fma_f16 v73, v65, v117, v73
	v_pk_fma_f16 v72, v64, v116, v72
	s_mov_b64 exec, s[70:71]
	buffer_load_dwordx4 v[138:141], v229, s[16:19], 0 offen offset:512
	buffer_load_dwordx4 v[90:93], v229, s[16:19], 0 offen offset:1024
	s_mov_b64 exec, -1
	v_pk_fma_f16 v71, v63, v115, v71
	v_pk_fma_f16 v70, v62, v114, v70
	v_pk_add_f16 v111, v212, v199 neg_lo:[0,1] neg_hi:[0,1]
	v_pk_add_f16 v112, v211, v200 neg_lo:[0,1] neg_hi:[0,1]
	v_pk_add_f16 v113, v210, v201 neg_lo:[0,1] neg_hi:[0,1]
	v_exp_f16_sdwa v114, v110 dst_sel:WORD_0 dst_unused:UNUSED_PAD src0_sel:WORD_0
	v_exp_f16_sdwa v115, v111 dst_sel:WORD_0 dst_unused:UNUSED_PAD src0_sel:WORD_0
	v_exp_f16_sdwa v116, v112 dst_sel:WORD_0 dst_unused:UNUSED_PAD src0_sel:WORD_0
	v_exp_f16_sdwa v117, v113 dst_sel:WORD_0 dst_unused:UNUSED_PAD src0_sel:WORD_0
	v_exp_f16_sdwa v114, v110 dst_sel:WORD_1 dst_unused:UNUSED_PRESERVE src0_sel:WORD_1
	v_exp_f16_sdwa v115, v111 dst_sel:WORD_1 dst_unused:UNUSED_PRESERVE src0_sel:WORD_1
	v_exp_f16_sdwa v116, v112 dst_sel:WORD_1 dst_unused:UNUSED_PRESERVE src0_sel:WORD_1
	v_exp_f16_sdwa v117, v113 dst_sel:WORD_1 dst_unused:UNUSED_PRESERVE src0_sel:WORD_1
	v_pk_add_f16 v110, v190, v198 neg_lo:[0,1] neg_hi:[0,1]
	v_pk_add_f16 v101, v101, v114
	v_pk_add_f16 v100, v100, v115
	v_pk_add_f16 v99, v99, v116
	v_pk_add_f16 v98, v98, v117
	v_pk_fma_f16 v70, v86, v114, v70
	v_pk_fma_f16 v71, v87, v115, v71
	v_pk_fma_f16 v72, v88, v116, v72
	v_pk_fma_f16 v73, v89, v117, v73
	s_mov_b64 exec, s[78:79]
	buffer_load_dwordx4 v[142:145], v229, s[16:19], 0 offen offset:2048
	buffer_load_dwordx4 v[2:5], v229, s[16:19], 0 offen offset:2560
	s_mov_b64 exec, -1
	v_pk_add_f16 v111, v191, v199 neg_lo:[0,1] neg_hi:[0,1]
	v_pk_add_f16 v112, v192, v200 neg_lo:[0,1] neg_hi:[0,1]
	v_pk_add_f16 v113, v193, v201 neg_lo:[0,1] neg_hi:[0,1]
	v_exp_f16_sdwa v114, v110 dst_sel:WORD_0 dst_unused:UNUSED_PAD src0_sel:WORD_0
	v_exp_f16_sdwa v115, v111 dst_sel:WORD_0 dst_unused:UNUSED_PAD src0_sel:WORD_0
	v_exp_f16_sdwa v116, v112 dst_sel:WORD_0 dst_unused:UNUSED_PAD src0_sel:WORD_0
	v_exp_f16_sdwa v117, v113 dst_sel:WORD_0 dst_unused:UNUSED_PAD src0_sel:WORD_0
	v_exp_f16_sdwa v114, v110 dst_sel:WORD_1 dst_unused:UNUSED_PRESERVE src0_sel:WORD_1
	v_exp_f16_sdwa v115, v111 dst_sel:WORD_1 dst_unused:UNUSED_PRESERVE src0_sel:WORD_1
	v_exp_f16_sdwa v116, v112 dst_sel:WORD_1 dst_unused:UNUSED_PRESERVE src0_sel:WORD_1
	v_exp_f16_sdwa v117, v113 dst_sel:WORD_1 dst_unused:UNUSED_PRESERVE src0_sel:WORD_1
	v_pk_add_f16 v110, v194, v198 neg_lo:[0,1] neg_hi:[0,1]
	v_pk_add_f16 v101, v101, v114
	v_pk_add_f16 v98, v98, v117
	v_pk_add_f16 v99, v99, v116
	v_pk_add_f16 v100, v100, v115
	v_pk_fma_f16 v73, v25, v117, v73
	v_pk_fma_f16 v72, v24, v116, v72
	v_pk_fma_f16 v71, v23, v115, v71
	v_pk_fma_f16 v70, v22, v114, v70
	v_pk_add_f16 v111, v195, v199 neg_lo:[0,1] neg_hi:[0,1]
	v_pk_add_f16 v112, v196, v200 neg_lo:[0,1] neg_hi:[0,1]
	v_pk_add_f16 v113, v197, v201 neg_lo:[0,1] neg_hi:[0,1]
	v_exp_f16_sdwa v114, v110 dst_sel:WORD_0 dst_unused:UNUSED_PAD src0_sel:WORD_0
	v_exp_f16_sdwa v115, v111 dst_sel:WORD_0 dst_unused:UNUSED_PAD src0_sel:WORD_0
	v_exp_f16_sdwa v116, v112 dst_sel:WORD_0 dst_unused:UNUSED_PAD src0_sel:WORD_0
	v_exp_f16_sdwa v117, v113 dst_sel:WORD_0 dst_unused:UNUSED_PAD src0_sel:WORD_0
	v_exp_f16_sdwa v114, v110 dst_sel:WORD_1 dst_unused:UNUSED_PRESERVE src0_sel:WORD_1
	v_exp_f16_sdwa v115, v111 dst_sel:WORD_1 dst_unused:UNUSED_PRESERVE src0_sel:WORD_1
	v_exp_f16_sdwa v116, v112 dst_sel:WORD_1 dst_unused:UNUSED_PRESERVE src0_sel:WORD_1
	v_exp_f16_sdwa v117, v113 dst_sel:WORD_1 dst_unused:UNUSED_PRESERVE src0_sel:WORD_1
	v_pk_add_f16 v110, v186, v198 neg_lo:[0,1] neg_hi:[0,1]
	v_pk_add_f16 v101, v101, v114
	v_pk_add_f16 v100, v100, v115
	v_pk_add_f16 v99, v99, v116
	v_pk_add_f16 v98, v98, v117
	v_pk_fma_f16 v70, v30, v114, v70
	v_pk_fma_f16 v71, v31, v115, v71
	v_pk_fma_f16 v72, v32, v116, v72
	v_pk_fma_f16 v73, v33, v117, v73
	v_pk_add_f16 v111, v187, v199 neg_lo:[0,1] neg_hi:[0,1]
	v_pk_add_f16 v112, v188, v200 neg_lo:[0,1] neg_hi:[0,1]
	v_pk_add_f16 v113, v189, v201 neg_lo:[0,1] neg_hi:[0,1]
	v_exp_f16_sdwa v114, v110 dst_sel:WORD_0 dst_unused:UNUSED_PAD src0_sel:WORD_0
	v_exp_f16_sdwa v115, v111 dst_sel:WORD_0 dst_unused:UNUSED_PAD src0_sel:WORD_0
	v_exp_f16_sdwa v116, v112 dst_sel:WORD_0 dst_unused:UNUSED_PAD src0_sel:WORD_0
	v_exp_f16_sdwa v117, v113 dst_sel:WORD_0 dst_unused:UNUSED_PAD src0_sel:WORD_0
	v_exp_f16_sdwa v114, v110 dst_sel:WORD_1 dst_unused:UNUSED_PRESERVE src0_sel:WORD_1
	v_exp_f16_sdwa v115, v111 dst_sel:WORD_1 dst_unused:UNUSED_PRESERVE src0_sel:WORD_1
	v_exp_f16_sdwa v116, v112 dst_sel:WORD_1 dst_unused:UNUSED_PRESERVE src0_sel:WORD_1
	v_exp_f16_sdwa v117, v113 dst_sel:WORD_1 dst_unused:UNUSED_PRESERVE src0_sel:WORD_1
	v_pk_add_f16 v101, v101, v114
	v_pk_add_f16 v100, v100, v115
	v_rcp_f16_e32 v110, v101
	v_rcp_f16_sdwa v101, v101 dst_sel:DWORD dst_unused:UNUSED_PAD src0_sel:WORD_1
	v_pk_add_f16 v99, v99, v116
	v_rcp_f16_e32 v111, v100
	v_rcp_f16_sdwa v100, v100 dst_sel:DWORD dst_unused:UNUSED_PAD src0_sel:WORD_1
	v_pk_add_f16 v98, v98, v117
	v_rcp_f16_e32 v112, v99
	v_rcp_f16_sdwa v99, v99 dst_sel:DWORD dst_unused:UNUSED_PAD src0_sel:WORD_1
	v_rcp_f16_e32 v113, v98
	v_rcp_f16_sdwa v98, v98 dst_sel:DWORD dst_unused:UNUSED_PAD src0_sel:WORD_1
	v_pk_fma_f16 v70, v46, v114, v70
	v_pack_b32_f16 v101, v110, v101
	v_pk_fma_f16 v71, v47, v115, v71
	v_pk_mul_f16 v110, v70, v101
	v_pack_b32_f16 v70, v111, v100
	v_pk_fma_f16 v72, v48, v116, v72
	v_pk_mul_f16 v111, v71, v70
	v_pack_b32_f16 v70, v112, v99
	v_pk_fma_f16 v73, v49, v117, v73
	v_pk_mul_f16 v112, v72, v70
	v_pack_b32_f16 v70, v113, v98
	v_pk_mul_f16 v113, v73, v70
	s_waitcnt vmcnt(12)
	v_pk_mul_f16 v70, v185, v154 op_sel_hi:[0,1]
	v_pk_mul_f16 v98, v183, v154 op_sel_hi:[0,1]
	v_pk_mul_f16 v114, v184, v154 op_sel_hi:[0,1]
	v_pk_mul_f16 v71, v185, v155 op_sel_hi:[0,1]
	v_pk_mul_f16 v72, v185, v156 op_sel_hi:[0,1]
	v_pk_mul_f16 v73, v185, v157 op_sel_hi:[0,1]
	v_pk_mul_f16 v99, v183, v155 op_sel_hi:[0,1]
	v_pk_mul_f16 v100, v183, v156 op_sel_hi:[0,1]
	v_pk_mul_f16 v101, v183, v157 op_sel_hi:[0,1]
	v_pk_mul_f16 v115, v184, v155 op_sel_hi:[0,1]
	v_pk_mul_f16 v116, v184, v156 op_sel_hi:[0,1]
	v_pk_mul_f16 v117, v184, v157 op_sel_hi:[0,1]
	v_pk_fma_f16 v82, v82, v154, v70
	v_pk_fma_f16 v106, v106, v154, v98
	v_pk_fma_f16 v122, v122, v154, v114
	v_pk_fma_f16 v129, v50, v154, v70
	v_pk_fma_f16 v137, v66, v154, v98
	v_pk_fma_f16 v189, v94, v154, v114
	v_pk_fma_f16 v70, v18, v154, v70
	v_pk_fma_f16 v98, v34, v154, v98
	v_pk_fma_f16 v114, v54, v154, v114
	v_pk_maximum3_f16 v154, v82, v106, v122
	v_pk_fma_f16 v85, v85, v157, v73
	v_pk_fma_f16 v84, v84, v156, v72
	v_pk_fma_f16 v83, v83, v155, v71
	v_pk_fma_f16 v109, v109, v157, v101
	v_pk_fma_f16 v108, v108, v156, v100
	v_pk_fma_f16 v107, v107, v155, v99
	v_pk_fma_f16 v125, v125, v157, v117
	v_pk_fma_f16 v124, v124, v156, v116
	v_pk_fma_f16 v123, v123, v155, v115
	v_pk_fma_f16 v126, v53, v157, v73
	v_pk_fma_f16 v127, v52, v156, v72
	v_pk_fma_f16 v128, v51, v155, v71
	v_pk_fma_f16 v134, v69, v157, v101
	v_pk_fma_f16 v135, v68, v156, v100
	v_pk_fma_f16 v136, v67, v155, v99
	v_pk_fma_f16 v186, v97, v157, v117
	v_pk_fma_f16 v187, v96, v156, v116
	v_pk_fma_f16 v188, v95, v155, v115
	v_pk_fma_f16 v73, v21, v157, v73
	v_pk_fma_f16 v72, v20, v156, v72
	v_pk_fma_f16 v71, v19, v155, v71
	v_pk_fma_f16 v101, v37, v157, v101
	v_pk_fma_f16 v100, v36, v156, v100
	v_pk_fma_f16 v99, v35, v155, v99
	v_pk_fma_f16 v117, v57, v157, v117
	v_pk_fma_f16 v116, v56, v156, v116
	v_pk_fma_f16 v115, v55, v155, v115
	v_pk_maximum3_f16 v155, v83, v107, v123
	v_pk_maximum3_f16 v156, v84, v108, v124
	v_pk_maximum3_f16 v157, v85, v109, v125
	v_pk_maximum3_f16 v190, v129, v137, v189
	v_pk_maximum3_f16 v194, v70, v98, v114
	v_pk_maximum3_f16 v191, v128, v136, v188
	v_pk_maximum3_f16 v192, v127, v135, v187
	v_pk_maximum3_f16 v193, v126, v134, v186
	v_pk_maximum3_f16 v195, v71, v99, v115
	v_pk_maximum3_f16 v196, v72, v100, v116
	v_pk_maximum3_f16 v154, v154, v190, v194
	v_pk_maximum3_f16 v197, v73, v101, v117
	v_pk_maximum3_f16 v155, v155, v191, v195
	v_pk_maximum3_f16 v156, v156, v192, v196
	v_pk_maximum3_f16 v157, v157, v193, v197
	v_pk_add_f16 v82, v82, v154 neg_lo:[0,1] neg_hi:[0,1]
	v_pk_add_f16 v83, v83, v155 neg_lo:[0,1] neg_hi:[0,1]
	v_pk_add_f16 v84, v84, v156 neg_lo:[0,1] neg_hi:[0,1]
	v_pk_add_f16 v85, v85, v157 neg_lo:[0,1] neg_hi:[0,1]
	v_pk_add_f16 v106, v106, v154 neg_lo:[0,1] neg_hi:[0,1]
	v_exp_f16_sdwa v190, v82 dst_sel:WORD_0 dst_unused:UNUSED_PAD src0_sel:WORD_0
	v_exp_f16_sdwa v191, v83 dst_sel:WORD_0 dst_unused:UNUSED_PAD src0_sel:WORD_0
	v_exp_f16_sdwa v192, v84 dst_sel:WORD_0 dst_unused:UNUSED_PAD src0_sel:WORD_0
	v_exp_f16_sdwa v193, v85 dst_sel:WORD_0 dst_unused:UNUSED_PAD src0_sel:WORD_0
	v_exp_f16_sdwa v190, v82 dst_sel:WORD_1 dst_unused:UNUSED_PRESERVE src0_sel:WORD_1
	v_exp_f16_sdwa v191, v83 dst_sel:WORD_1 dst_unused:UNUSED_PRESERVE src0_sel:WORD_1
	v_exp_f16_sdwa v192, v84 dst_sel:WORD_1 dst_unused:UNUSED_PRESERVE src0_sel:WORD_1
	v_exp_f16_sdwa v193, v85 dst_sel:WORD_1 dst_unused:UNUSED_PRESERVE src0_sel:WORD_1
	v_pk_add_f16 v107, v107, v155 neg_lo:[0,1] neg_hi:[0,1]
	v_pk_add_f16 v82, v193, 0
	v_pk_fma_f16 v42, v42, v190, 0
	v_pk_add_f16 v83, v192, 0
	v_pk_add_f16 v84, v191, 0
	v_pk_add_f16 v85, v190, 0
	v_pk_fma_f16 v45, v45, v193, 0
	v_pk_fma_f16 v44, v44, v192, 0
	v_pk_fma_f16 v43, v43, v191, 0
	v_pk_add_f16 v108, v108, v156 neg_lo:[0,1] neg_hi:[0,1]
	v_pk_add_f16 v109, v109, v157 neg_lo:[0,1] neg_hi:[0,1]
	v_pk_add_f16 v70, v70, v154 neg_lo:[0,1] neg_hi:[0,1]
	v_exp_f16_sdwa v190, v106 dst_sel:WORD_0 dst_unused:UNUSED_PAD src0_sel:WORD_0
	v_exp_f16_sdwa v191, v107 dst_sel:WORD_0 dst_unused:UNUSED_PAD src0_sel:WORD_0
	v_exp_f16_sdwa v192, v108 dst_sel:WORD_0 dst_unused:UNUSED_PAD src0_sel:WORD_0
	v_exp_f16_sdwa v193, v109 dst_sel:WORD_0 dst_unused:UNUSED_PAD src0_sel:WORD_0
	v_exp_f16_sdwa v190, v106 dst_sel:WORD_1 dst_unused:UNUSED_PRESERVE src0_sel:WORD_1
	v_exp_f16_sdwa v191, v107 dst_sel:WORD_1 dst_unused:UNUSED_PRESERVE src0_sel:WORD_1
	v_exp_f16_sdwa v192, v108 dst_sel:WORD_1 dst_unused:UNUSED_PRESERVE src0_sel:WORD_1
	v_exp_f16_sdwa v193, v109 dst_sel:WORD_1 dst_unused:UNUSED_PRESERVE src0_sel:WORD_1
	v_pk_add_f16 v71, v71, v155 neg_lo:[0,1] neg_hi:[0,1]
	v_pk_add_f16 v82, v82, v193
	v_pk_fma_f16 v42, v62, v190, v42
	v_pk_add_f16 v62, v122, v154 neg_lo:[0,1] neg_hi:[0,1]
	v_pk_add_f16 v85, v85, v190
	v_pk_add_f16 v84, v84, v191
	v_pk_add_f16 v83, v83, v192
	v_pk_fma_f16 v43, v63, v191, v43
	v_pk_fma_f16 v44, v64, v192, v44
	v_pk_fma_f16 v45, v65, v193, v45
	v_pk_add_f16 v63, v123, v155 neg_lo:[0,1] neg_hi:[0,1]
	v_pk_add_f16 v64, v124, v156 neg_lo:[0,1] neg_hi:[0,1]
	v_pk_add_f16 v65, v125, v157 neg_lo:[0,1] neg_hi:[0,1]
	v_pk_add_f16 v72, v72, v156 neg_lo:[0,1] neg_hi:[0,1]
	v_exp_f16_sdwa v106, v62 dst_sel:WORD_0 dst_unused:UNUSED_PAD src0_sel:WORD_0
	v_exp_f16_sdwa v107, v63 dst_sel:WORD_0 dst_unused:UNUSED_PAD src0_sel:WORD_0
	v_exp_f16_sdwa v108, v64 dst_sel:WORD_0 dst_unused:UNUSED_PAD src0_sel:WORD_0
	v_exp_f16_sdwa v109, v65 dst_sel:WORD_0 dst_unused:UNUSED_PAD src0_sel:WORD_0
	v_exp_f16_sdwa v106, v62 dst_sel:WORD_1 dst_unused:UNUSED_PRESERVE src0_sel:WORD_1
	v_exp_f16_sdwa v107, v63 dst_sel:WORD_1 dst_unused:UNUSED_PRESERVE src0_sel:WORD_1
	v_exp_f16_sdwa v108, v64 dst_sel:WORD_1 dst_unused:UNUSED_PRESERVE src0_sel:WORD_1
	v_exp_f16_sdwa v109, v65 dst_sel:WORD_1 dst_unused:UNUSED_PRESERVE src0_sel:WORD_1
	v_pk_add_f16 v73, v73, v157 neg_lo:[0,1] neg_hi:[0,1]
	v_pk_add_f16 v62, v82, v109
	v_pk_add_f16 v63, v83, v108
	v_pk_add_f16 v64, v84, v107
	v_pk_add_f16 v65, v85, v106
	v_pk_fma_f16 v45, v89, v109, v45
	v_pk_fma_f16 v44, v88, v108, v44
	v_pk_fma_f16 v43, v87, v107, v43
	v_pk_fma_f16 v42, v86, v106, v42
	v_pk_add_f16 v82, v129, v154 neg_lo:[0,1] neg_hi:[0,1]
	v_pk_add_f16 v83, v128, v155 neg_lo:[0,1] neg_hi:[0,1]
	v_pk_add_f16 v84, v127, v156 neg_lo:[0,1] neg_hi:[0,1]
	v_pk_add_f16 v85, v126, v157 neg_lo:[0,1] neg_hi:[0,1]
	v_exp_f16_sdwa v86, v82 dst_sel:WORD_0 dst_unused:UNUSED_PAD src0_sel:WORD_0
	v_exp_f16_sdwa v87, v83 dst_sel:WORD_0 dst_unused:UNUSED_PAD src0_sel:WORD_0
	v_exp_f16_sdwa v88, v84 dst_sel:WORD_0 dst_unused:UNUSED_PAD src0_sel:WORD_0
	v_exp_f16_sdwa v89, v85 dst_sel:WORD_0 dst_unused:UNUSED_PAD src0_sel:WORD_0
	v_exp_f16_sdwa v86, v82 dst_sel:WORD_1 dst_unused:UNUSED_PRESERVE src0_sel:WORD_1
	v_exp_f16_sdwa v87, v83 dst_sel:WORD_1 dst_unused:UNUSED_PRESERVE src0_sel:WORD_1
	v_exp_f16_sdwa v88, v84 dst_sel:WORD_1 dst_unused:UNUSED_PRESERVE src0_sel:WORD_1
	v_exp_f16_sdwa v89, v85 dst_sel:WORD_1 dst_unused:UNUSED_PRESERVE src0_sel:WORD_1
	v_pk_add_f16 v82, v137, v154 neg_lo:[0,1] neg_hi:[0,1]
	v_pk_add_f16 v62, v62, v89
	v_pk_add_f16 v65, v65, v86
	v_pk_add_f16 v64, v64, v87
	v_pk_add_f16 v63, v63, v88
	v_pk_fma_f16 v42, v22, v86, v42
	v_pk_fma_f16 v43, v23, v87, v43
	v_pk_fma_f16 v44, v24, v88, v44
	v_pk_fma_f16 v45, v25, v89, v45
	v_pk_add_f16 v83, v136, v155 neg_lo:[0,1] neg_hi:[0,1]
	v_pk_add_f16 v84, v135, v156 neg_lo:[0,1] neg_hi:[0,1]
	v_pk_add_f16 v85, v134, v157 neg_lo:[0,1] neg_hi:[0,1]
	v_exp_f16_sdwa v86, v82 dst_sel:WORD_0 dst_unused:UNUSED_PAD src0_sel:WORD_0
	v_exp_f16_sdwa v87, v83 dst_sel:WORD_0 dst_unused:UNUSED_PAD src0_sel:WORD_0
	v_exp_f16_sdwa v88, v84 dst_sel:WORD_0 dst_unused:UNUSED_PAD src0_sel:WORD_0
	v_exp_f16_sdwa v89, v85 dst_sel:WORD_0 dst_unused:UNUSED_PAD src0_sel:WORD_0
	v_exp_f16_sdwa v86, v82 dst_sel:WORD_1 dst_unused:UNUSED_PRESERVE src0_sel:WORD_1
	v_exp_f16_sdwa v87, v83 dst_sel:WORD_1 dst_unused:UNUSED_PRESERVE src0_sel:WORD_1
	v_exp_f16_sdwa v88, v84 dst_sel:WORD_1 dst_unused:UNUSED_PRESERVE src0_sel:WORD_1
	v_exp_f16_sdwa v89, v85 dst_sel:WORD_1 dst_unused:UNUSED_PRESERVE src0_sel:WORD_1
	v_pk_add_f16 v82, v189, v154 neg_lo:[0,1] neg_hi:[0,1]
	v_pk_add_f16 v62, v62, v89
	v_pk_add_f16 v63, v63, v88
	v_pk_add_f16 v64, v64, v87
	v_pk_add_f16 v65, v65, v86
	v_pk_fma_f16 v45, v33, v89, v45
	v_pk_fma_f16 v44, v32, v88, v44
	v_pk_fma_f16 v43, v31, v87, v43
	v_pk_fma_f16 v42, v30, v86, v42
	v_pk_add_f16 v83, v188, v155 neg_lo:[0,1] neg_hi:[0,1]
	v_pk_add_f16 v84, v187, v156 neg_lo:[0,1] neg_hi:[0,1]
	v_pk_add_f16 v85, v186, v157 neg_lo:[0,1] neg_hi:[0,1]
	v_exp_f16_sdwa v86, v82 dst_sel:WORD_0 dst_unused:UNUSED_PAD src0_sel:WORD_0
	v_exp_f16_sdwa v87, v83 dst_sel:WORD_0 dst_unused:UNUSED_PAD src0_sel:WORD_0
	v_exp_f16_sdwa v88, v84 dst_sel:WORD_0 dst_unused:UNUSED_PAD src0_sel:WORD_0
	v_exp_f16_sdwa v89, v85 dst_sel:WORD_0 dst_unused:UNUSED_PAD src0_sel:WORD_0
	v_exp_f16_sdwa v86, v82 dst_sel:WORD_1 dst_unused:UNUSED_PRESERVE src0_sel:WORD_1
	v_exp_f16_sdwa v87, v83 dst_sel:WORD_1 dst_unused:UNUSED_PRESERVE src0_sel:WORD_1
	v_exp_f16_sdwa v88, v84 dst_sel:WORD_1 dst_unused:UNUSED_PRESERVE src0_sel:WORD_1
	v_exp_f16_sdwa v89, v85 dst_sel:WORD_1 dst_unused:UNUSED_PRESERVE src0_sel:WORD_1
	v_exp_f16_sdwa v82, v70 dst_sel:WORD_0 dst_unused:UNUSED_PAD src0_sel:WORD_0
	v_exp_f16_sdwa v83, v71 dst_sel:WORD_0 dst_unused:UNUSED_PAD src0_sel:WORD_0
	v_exp_f16_sdwa v84, v72 dst_sel:WORD_0 dst_unused:UNUSED_PAD src0_sel:WORD_0
	v_exp_f16_sdwa v85, v73 dst_sel:WORD_0 dst_unused:UNUSED_PAD src0_sel:WORD_0
	v_exp_f16_sdwa v82, v70 dst_sel:WORD_1 dst_unused:UNUSED_PRESERVE src0_sel:WORD_1
	v_exp_f16_sdwa v83, v71 dst_sel:WORD_1 dst_unused:UNUSED_PRESERVE src0_sel:WORD_1
	v_exp_f16_sdwa v84, v72 dst_sel:WORD_1 dst_unused:UNUSED_PRESERVE src0_sel:WORD_1
	v_exp_f16_sdwa v85, v73 dst_sel:WORD_1 dst_unused:UNUSED_PRESERVE src0_sel:WORD_1
	v_pk_add_f16 v70, v98, v154 neg_lo:[0,1] neg_hi:[0,1]
	v_pk_add_f16 v62, v62, v89
	v_pk_add_f16 v65, v65, v86
	v_pk_add_f16 v64, v64, v87
	v_pk_add_f16 v63, v63, v88
	v_pk_fma_f16 v42, v46, v86, v42
	v_pk_fma_f16 v43, v47, v87, v43
	v_pk_fma_f16 v44, v48, v88, v44
	v_pk_fma_f16 v45, v49, v89, v45
	v_pk_add_f16 v62, v62, v85
	v_pk_add_f16 v63, v63, v84
	v_pk_add_f16 v64, v64, v83
	v_pk_add_f16 v65, v65, v82
	v_pk_fma_f16 v45, v9, v85, v45
	v_pk_fma_f16 v44, v8, v84, v44
	v_pk_fma_f16 v43, v7, v83, v43
	v_pk_fma_f16 v42, v6, v82, v42
	v_pk_add_f16 v71, v99, v155 neg_lo:[0,1] neg_hi:[0,1]
	v_pk_add_f16 v72, v100, v156 neg_lo:[0,1] neg_hi:[0,1]
	v_pk_add_f16 v73, v101, v157 neg_lo:[0,1] neg_hi:[0,1]
	v_exp_f16_sdwa v82, v70 dst_sel:WORD_0 dst_unused:UNUSED_PAD src0_sel:WORD_0
	v_exp_f16_sdwa v83, v71 dst_sel:WORD_0 dst_unused:UNUSED_PAD src0_sel:WORD_0
	v_exp_f16_sdwa v84, v72 dst_sel:WORD_0 dst_unused:UNUSED_PAD src0_sel:WORD_0
	v_exp_f16_sdwa v85, v73 dst_sel:WORD_0 dst_unused:UNUSED_PAD src0_sel:WORD_0
	v_exp_f16_sdwa v82, v70 dst_sel:WORD_1 dst_unused:UNUSED_PRESERVE src0_sel:WORD_1
	v_exp_f16_sdwa v83, v71 dst_sel:WORD_1 dst_unused:UNUSED_PRESERVE src0_sel:WORD_1
	v_exp_f16_sdwa v84, v72 dst_sel:WORD_1 dst_unused:UNUSED_PRESERVE src0_sel:WORD_1
	v_exp_f16_sdwa v85, v73 dst_sel:WORD_1 dst_unused:UNUSED_PRESERVE src0_sel:WORD_1
	v_pk_add_f16 v70, v114, v154 neg_lo:[0,1] neg_hi:[0,1]
	v_pk_add_f16 v62, v62, v85
	v_pk_add_f16 v65, v65, v82
	v_pk_add_f16 v64, v64, v83
	v_pk_add_f16 v63, v63, v84
	v_pk_fma_f16 v42, v10, v82, v42
	v_pk_fma_f16 v43, v11, v83, v43
	v_pk_fma_f16 v44, v12, v84, v44
	v_pk_fma_f16 v45, v13, v85, v45
	v_pk_add_f16 v71, v115, v155 neg_lo:[0,1] neg_hi:[0,1]
	v_pk_add_f16 v72, v116, v156 neg_lo:[0,1] neg_hi:[0,1]
	v_pk_add_f16 v73, v117, v157 neg_lo:[0,1] neg_hi:[0,1]
	v_exp_f16_sdwa v82, v70 dst_sel:WORD_0 dst_unused:UNUSED_PAD src0_sel:WORD_0
	v_exp_f16_sdwa v83, v71 dst_sel:WORD_0 dst_unused:UNUSED_PAD src0_sel:WORD_0
	v_exp_f16_sdwa v84, v72 dst_sel:WORD_0 dst_unused:UNUSED_PAD src0_sel:WORD_0
	v_exp_f16_sdwa v85, v73 dst_sel:WORD_0 dst_unused:UNUSED_PAD src0_sel:WORD_0
	v_exp_f16_sdwa v82, v70 dst_sel:WORD_1 dst_unused:UNUSED_PRESERVE src0_sel:WORD_1
	v_exp_f16_sdwa v83, v71 dst_sel:WORD_1 dst_unused:UNUSED_PRESERVE src0_sel:WORD_1
	v_exp_f16_sdwa v84, v72 dst_sel:WORD_1 dst_unused:UNUSED_PRESERVE src0_sel:WORD_1
	v_exp_f16_sdwa v85, v73 dst_sel:WORD_1 dst_unused:UNUSED_PRESERVE src0_sel:WORD_1
	s_nop 0
	v_pk_add_f16 v62, v62, v85
	v_pk_add_f16 v63, v63, v84
	v_pk_add_f16 v64, v64, v83
	v_pk_add_f16 v65, v65, v82
	v_rcp_f16_e32 v73, v62
	v_rcp_f16_sdwa v62, v62 dst_sel:DWORD dst_unused:UNUSED_PAD src0_sel:WORD_1
	v_rcp_f16_e32 v70, v65
	v_rcp_f16_sdwa v65, v65 dst_sel:DWORD dst_unused:UNUSED_PAD src0_sel:WORD_1
	v_rcp_f16_e32 v71, v64
	v_rcp_f16_sdwa v64, v64 dst_sel:DWORD dst_unused:UNUSED_PAD src0_sel:WORD_1
	v_rcp_f16_e32 v72, v63
	v_rcp_f16_sdwa v63, v63 dst_sel:DWORD dst_unused:UNUSED_PAD src0_sel:WORD_1
	v_pk_fma_f16 v45, v17, v85, v45
	v_pack_b32_f16 v62, v73, v62
	v_pk_fma_f16 v44, v16, v84, v44
	v_pk_fma_f16 v43, v15, v83, v43
	v_pk_fma_f16 v42, v14, v82, v42
	v_pack_b32_f16 v65, v70, v65
	v_pack_b32_f16 v64, v71, v64
	v_pack_b32_f16 v63, v72, v63
	v_pk_mul_f16 v45, v45, v62
	s_waitcnt vmcnt(6)
	v_pk_mul_f16 v62, v185, v150 op_sel_hi:[0,1]
	v_pk_mul_f16 v70, v183, v150 op_sel_hi:[0,1]
	v_pk_mul_f16 v82, v184, v150 op_sel_hi:[0,1]
	v_pk_mul_f16 v42, v42, v65
	v_pk_mul_f16 v43, v43, v64
	v_pk_mul_f16 v44, v44, v63
	v_pk_mul_f16 v63, v185, v151 op_sel_hi:[0,1]
	v_pk_mul_f16 v64, v185, v152 op_sel_hi:[0,1]
	v_pk_mul_f16 v65, v185, v153 op_sel_hi:[0,1]
	v_pk_mul_f16 v71, v183, v151 op_sel_hi:[0,1]
	v_pk_mul_f16 v72, v183, v152 op_sel_hi:[0,1]
	v_pk_mul_f16 v73, v183, v153 op_sel_hi:[0,1]
	v_pk_mul_f16 v83, v184, v151 op_sel_hi:[0,1]
	v_pk_mul_f16 v84, v184, v152 op_sel_hi:[0,1]
	v_pk_mul_f16 v85, v184, v153 op_sel_hi:[0,1]
	v_pk_fma_f16 v50, v50, v150, v62
	v_pk_fma_f16 v66, v66, v150, v70
	v_pk_fma_f16 v89, v94, v150, v82
	v_pk_fma_f16 v53, v53, v153, v65
	v_pk_maximum3_f16 v114, v50, v66, v89
	v_pk_fma_f16 v52, v52, v152, v64
	v_pk_fma_f16 v51, v51, v151, v63
	v_pk_fma_f16 v69, v69, v153, v73
	v_pk_fma_f16 v68, v68, v152, v72
	v_pk_fma_f16 v67, v67, v151, v71
	v_pk_fma_f16 v86, v97, v153, v85
	v_pk_fma_f16 v87, v96, v152, v84
	v_pk_fma_f16 v88, v95, v151, v83
	v_pk_fma_f16 v97, v18, v150, v62
	v_pk_fma_f16 v101, v34, v150, v70
	v_pk_fma_f16 v109, v54, v150, v82
	v_pk_fma_f16 v62, v74, v150, v62
	v_pk_fma_f16 v70, v102, v150, v70
	v_pk_fma_f16 v82, v118, v150, v82
	v_pk_maximum3_f16 v115, v51, v67, v88
	v_pk_maximum3_f16 v116, v52, v68, v87
	v_pk_maximum3_f16 v117, v53, v69, v86
	v_pk_maximum3_f16 v122, v97, v101, v109
	v_pk_fma_f16 v94, v21, v153, v65
	v_pk_maximum3_f16 v126, v62, v70, v82
	v_pk_fma_f16 v95, v20, v152, v64
	v_pk_maximum3_f16 v114, v114, v122, v126
	v_pk_fma_f16 v96, v19, v151, v63
	v_pk_fma_f16 v98, v37, v153, v73
	v_pk_fma_f16 v99, v36, v152, v72
	v_pk_fma_f16 v100, v35, v151, v71
	v_pk_fma_f16 v106, v57, v153, v85
	v_pk_fma_f16 v107, v56, v152, v84
	v_pk_fma_f16 v108, v55, v151, v83
	v_pk_fma_f16 v65, v77, v153, v65
	v_pk_fma_f16 v64, v76, v152, v64
	v_pk_fma_f16 v63, v75, v151, v63
	v_pk_fma_f16 v73, v105, v153, v73
	v_pk_fma_f16 v72, v104, v152, v72
	v_pk_fma_f16 v71, v103, v151, v71
	v_pk_fma_f16 v85, v121, v153, v85
	v_pk_fma_f16 v84, v120, v152, v84
	v_pk_fma_f16 v83, v119, v151, v83
	v_pk_maximum3_f16 v123, v96, v100, v108
	v_pk_maximum3_f16 v124, v95, v99, v107
	v_pk_maximum3_f16 v125, v94, v98, v106
	v_pk_maximum3_f16 v128, v64, v72, v84
	v_pk_maximum3_f16 v129, v65, v73, v85
	v_pk_maximum3_f16 v127, v63, v71, v83
	v_pk_maximum3_f16 v115, v115, v123, v127
	v_pk_maximum3_f16 v116, v116, v124, v128
	v_pk_maximum3_f16 v117, v117, v125, v129
	v_pk_add_f16 v50, v50, v114 neg_lo:[0,1] neg_hi:[0,1]
	v_pk_add_f16 v51, v51, v115 neg_lo:[0,1] neg_hi:[0,1]
	v_pk_add_f16 v52, v52, v116 neg_lo:[0,1] neg_hi:[0,1]
	v_pk_add_f16 v53, v53, v117 neg_lo:[0,1] neg_hi:[0,1]
	v_pk_add_f16 v66, v66, v114 neg_lo:[0,1] neg_hi:[0,1]
	v_exp_f16_sdwa v122, v50 dst_sel:WORD_0 dst_unused:UNUSED_PAD src0_sel:WORD_0
	v_exp_f16_sdwa v123, v51 dst_sel:WORD_0 dst_unused:UNUSED_PAD src0_sel:WORD_0
	v_exp_f16_sdwa v124, v52 dst_sel:WORD_0 dst_unused:UNUSED_PAD src0_sel:WORD_0
	v_exp_f16_sdwa v125, v53 dst_sel:WORD_0 dst_unused:UNUSED_PAD src0_sel:WORD_0
	v_exp_f16_sdwa v122, v50 dst_sel:WORD_1 dst_unused:UNUSED_PRESERVE src0_sel:WORD_1
	v_exp_f16_sdwa v123, v51 dst_sel:WORD_1 dst_unused:UNUSED_PRESERVE src0_sel:WORD_1
	v_exp_f16_sdwa v124, v52 dst_sel:WORD_1 dst_unused:UNUSED_PRESERVE src0_sel:WORD_1
	v_exp_f16_sdwa v125, v53 dst_sel:WORD_1 dst_unused:UNUSED_PRESERVE src0_sel:WORD_1
	v_pk_add_f16 v67, v67, v115 neg_lo:[0,1] neg_hi:[0,1]
	v_pk_add_f16 v50, v125, 0
	v_pk_fma_f16 v22, v22, v122, 0
	v_pk_add_f16 v51, v124, 0
	v_pk_add_f16 v52, v123, 0
	v_pk_add_f16 v53, v122, 0
	v_pk_fma_f16 v23, v23, v123, 0
	v_pk_fma_f16 v24, v24, v124, 0
	v_pk_fma_f16 v25, v25, v125, 0
	v_pk_add_f16 v68, v68, v116 neg_lo:[0,1] neg_hi:[0,1]
	v_pk_add_f16 v69, v69, v117 neg_lo:[0,1] neg_hi:[0,1]
	v_exp_f16_sdwa v122, v66 dst_sel:WORD_0 dst_unused:UNUSED_PAD src0_sel:WORD_0
	v_exp_f16_sdwa v123, v67 dst_sel:WORD_0 dst_unused:UNUSED_PAD src0_sel:WORD_0
	v_exp_f16_sdwa v124, v68 dst_sel:WORD_0 dst_unused:UNUSED_PAD src0_sel:WORD_0
	v_exp_f16_sdwa v125, v69 dst_sel:WORD_0 dst_unused:UNUSED_PAD src0_sel:WORD_0
	v_exp_f16_sdwa v122, v66 dst_sel:WORD_1 dst_unused:UNUSED_PRESERVE src0_sel:WORD_1
	v_exp_f16_sdwa v123, v67 dst_sel:WORD_1 dst_unused:UNUSED_PRESERVE src0_sel:WORD_1
	v_exp_f16_sdwa v124, v68 dst_sel:WORD_1 dst_unused:UNUSED_PRESERVE src0_sel:WORD_1
	v_exp_f16_sdwa v125, v69 dst_sel:WORD_1 dst_unused:UNUSED_PRESERVE src0_sel:WORD_1
	s_nop 0
	v_pk_add_f16 v50, v50, v125
	v_pk_fma_f16 v22, v30, v122, v22
	v_pk_add_f16 v30, v89, v114 neg_lo:[0,1] neg_hi:[0,1]
	v_pk_add_f16 v53, v53, v122
	v_pk_add_f16 v52, v52, v123
	v_pk_add_f16 v51, v51, v124
	v_pk_fma_f16 v25, v33, v125, v25
	v_pk_fma_f16 v24, v32, v124, v24
	v_pk_fma_f16 v23, v31, v123, v23
	v_pk_add_f16 v31, v88, v115 neg_lo:[0,1] neg_hi:[0,1]
	v_pk_add_f16 v32, v87, v116 neg_lo:[0,1] neg_hi:[0,1]
	v_pk_add_f16 v33, v86, v117 neg_lo:[0,1] neg_hi:[0,1]
	v_exp_f16_sdwa v66, v30 dst_sel:WORD_0 dst_unused:UNUSED_PAD src0_sel:WORD_0
	v_exp_f16_sdwa v67, v31 dst_sel:WORD_0 dst_unused:UNUSED_PAD src0_sel:WORD_0
	v_exp_f16_sdwa v68, v32 dst_sel:WORD_0 dst_unused:UNUSED_PAD src0_sel:WORD_0
	v_exp_f16_sdwa v69, v33 dst_sel:WORD_0 dst_unused:UNUSED_PAD src0_sel:WORD_0
	v_exp_f16_sdwa v66, v30 dst_sel:WORD_1 dst_unused:UNUSED_PRESERVE src0_sel:WORD_1
	v_exp_f16_sdwa v67, v31 dst_sel:WORD_1 dst_unused:UNUSED_PRESERVE src0_sel:WORD_1
	v_exp_f16_sdwa v68, v32 dst_sel:WORD_1 dst_unused:UNUSED_PRESERVE src0_sel:WORD_1
	v_exp_f16_sdwa v69, v33 dst_sel:WORD_1 dst_unused:UNUSED_PRESERVE src0_sel:WORD_1
	s_nop 0
	v_pk_add_f16 v30, v50, v69
	v_pk_add_f16 v31, v51, v68
	v_pk_add_f16 v32, v52, v67
	v_pk_add_f16 v33, v53, v66
	v_pk_fma_f16 v22, v46, v66, v22
	v_pk_fma_f16 v23, v47, v67, v23
	v_pk_fma_f16 v24, v48, v68, v24
	v_pk_fma_f16 v25, v49, v69, v25
	v_pk_add_f16 v46, v97, v114 neg_lo:[0,1] neg_hi:[0,1]
	v_pk_add_f16 v47, v96, v115 neg_lo:[0,1] neg_hi:[0,1]
	v_pk_add_f16 v48, v95, v116 neg_lo:[0,1] neg_hi:[0,1]
	v_pk_add_f16 v49, v94, v117 neg_lo:[0,1] neg_hi:[0,1]
	v_exp_f16_sdwa v50, v46 dst_sel:WORD_0 dst_unused:UNUSED_PAD src0_sel:WORD_0
	v_exp_f16_sdwa v51, v47 dst_sel:WORD_0 dst_unused:UNUSED_PAD src0_sel:WORD_0
	v_exp_f16_sdwa v52, v48 dst_sel:WORD_0 dst_unused:UNUSED_PAD src0_sel:WORD_0
	v_exp_f16_sdwa v53, v49 dst_sel:WORD_0 dst_unused:UNUSED_PAD src0_sel:WORD_0
	v_exp_f16_sdwa v50, v46 dst_sel:WORD_1 dst_unused:UNUSED_PRESERVE src0_sel:WORD_1
	v_exp_f16_sdwa v51, v47 dst_sel:WORD_1 dst_unused:UNUSED_PRESERVE src0_sel:WORD_1
	v_exp_f16_sdwa v52, v48 dst_sel:WORD_1 dst_unused:UNUSED_PRESERVE src0_sel:WORD_1
	v_exp_f16_sdwa v53, v49 dst_sel:WORD_1 dst_unused:UNUSED_PRESERVE src0_sel:WORD_1
	v_pk_add_f16 v46, v101, v114 neg_lo:[0,1] neg_hi:[0,1]
	v_pk_add_f16 v30, v30, v53
	v_pk_add_f16 v33, v33, v50
	v_pk_add_f16 v32, v32, v51
	v_pk_add_f16 v31, v31, v52
	v_pk_fma_f16 v25, v9, v53, v25
	v_pk_fma_f16 v24, v8, v52, v24
	v_pk_fma_f16 v23, v7, v51, v23
	v_pk_fma_f16 v22, v6, v50, v22
	v_pk_add_f16 v47, v100, v115 neg_lo:[0,1] neg_hi:[0,1]
	v_pk_add_f16 v48, v99, v116 neg_lo:[0,1] neg_hi:[0,1]
	v_pk_add_f16 v49, v98, v117 neg_lo:[0,1] neg_hi:[0,1]
	v_exp_f16_sdwa v50, v46 dst_sel:WORD_0 dst_unused:UNUSED_PAD src0_sel:WORD_0
	v_exp_f16_sdwa v51, v47 dst_sel:WORD_0 dst_unused:UNUSED_PAD src0_sel:WORD_0
	v_exp_f16_sdwa v52, v48 dst_sel:WORD_0 dst_unused:UNUSED_PAD src0_sel:WORD_0
	v_exp_f16_sdwa v53, v49 dst_sel:WORD_0 dst_unused:UNUSED_PAD src0_sel:WORD_0
	v_exp_f16_sdwa v50, v46 dst_sel:WORD_1 dst_unused:UNUSED_PRESERVE src0_sel:WORD_1
	v_exp_f16_sdwa v51, v47 dst_sel:WORD_1 dst_unused:UNUSED_PRESERVE src0_sel:WORD_1
	v_exp_f16_sdwa v52, v48 dst_sel:WORD_1 dst_unused:UNUSED_PRESERVE src0_sel:WORD_1
	v_exp_f16_sdwa v53, v49 dst_sel:WORD_1 dst_unused:UNUSED_PRESERVE src0_sel:WORD_1
	v_pk_add_f16 v46, v109, v114 neg_lo:[0,1] neg_hi:[0,1]
	v_pk_add_f16 v30, v30, v53
	v_pk_add_f16 v31, v31, v52
	v_pk_add_f16 v32, v32, v51
	v_pk_add_f16 v33, v33, v50
	v_pk_fma_f16 v22, v10, v50, v22
	v_pk_fma_f16 v23, v11, v51, v23
	v_pk_fma_f16 v24, v12, v52, v24
	v_pk_fma_f16 v25, v13, v53, v25
	v_pk_add_f16 v47, v108, v115 neg_lo:[0,1] neg_hi:[0,1]
	v_pk_add_f16 v48, v107, v116 neg_lo:[0,1] neg_hi:[0,1]
	v_pk_add_f16 v49, v106, v117 neg_lo:[0,1] neg_hi:[0,1]
	v_exp_f16_sdwa v50, v46 dst_sel:WORD_0 dst_unused:UNUSED_PAD src0_sel:WORD_0
	v_exp_f16_sdwa v51, v47 dst_sel:WORD_0 dst_unused:UNUSED_PAD src0_sel:WORD_0
	v_exp_f16_sdwa v52, v48 dst_sel:WORD_0 dst_unused:UNUSED_PAD src0_sel:WORD_0
	v_exp_f16_sdwa v53, v49 dst_sel:WORD_0 dst_unused:UNUSED_PAD src0_sel:WORD_0
	v_exp_f16_sdwa v50, v46 dst_sel:WORD_1 dst_unused:UNUSED_PRESERVE src0_sel:WORD_1
	v_exp_f16_sdwa v51, v47 dst_sel:WORD_1 dst_unused:UNUSED_PRESERVE src0_sel:WORD_1
	v_exp_f16_sdwa v52, v48 dst_sel:WORD_1 dst_unused:UNUSED_PRESERVE src0_sel:WORD_1
	v_exp_f16_sdwa v53, v49 dst_sel:WORD_1 dst_unused:UNUSED_PRESERVE src0_sel:WORD_1
	v_pk_add_f16 v46, v62, v114 neg_lo:[0,1] neg_hi:[0,1]
	v_pk_add_f16 v30, v30, v53
	v_pk_add_f16 v33, v33, v50
	v_pk_add_f16 v32, v32, v51
	v_pk_add_f16 v31, v31, v52
	v_pk_fma_f16 v25, v17, v53, v25
	v_pk_fma_f16 v24, v16, v52, v24
	v_pk_fma_f16 v23, v15, v51, v23
	v_pk_fma_f16 v22, v14, v50, v22
	v_pk_add_f16 v47, v63, v115 neg_lo:[0,1] neg_hi:[0,1]
	v_pk_add_f16 v48, v64, v116 neg_lo:[0,1] neg_hi:[0,1]
	v_pk_add_f16 v49, v65, v117 neg_lo:[0,1] neg_hi:[0,1]
	v_exp_f16_sdwa v50, v46 dst_sel:WORD_0 dst_unused:UNUSED_PAD src0_sel:WORD_0
	v_exp_f16_sdwa v51, v47 dst_sel:WORD_0 dst_unused:UNUSED_PAD src0_sel:WORD_0
	v_exp_f16_sdwa v52, v48 dst_sel:WORD_0 dst_unused:UNUSED_PAD src0_sel:WORD_0
	v_exp_f16_sdwa v53, v49 dst_sel:WORD_0 dst_unused:UNUSED_PAD src0_sel:WORD_0
	v_exp_f16_sdwa v50, v46 dst_sel:WORD_1 dst_unused:UNUSED_PRESERVE src0_sel:WORD_1
	v_exp_f16_sdwa v51, v47 dst_sel:WORD_1 dst_unused:UNUSED_PRESERVE src0_sel:WORD_1
	v_exp_f16_sdwa v52, v48 dst_sel:WORD_1 dst_unused:UNUSED_PRESERVE src0_sel:WORD_1
	v_exp_f16_sdwa v53, v49 dst_sel:WORD_1 dst_unused:UNUSED_PRESERVE src0_sel:WORD_1
	v_pk_add_f16 v46, v70, v114 neg_lo:[0,1] neg_hi:[0,1]
	v_pk_add_f16 v30, v30, v53
	v_pk_add_f16 v31, v31, v52
	v_pk_add_f16 v32, v32, v51
	v_pk_add_f16 v33, v33, v50
	v_pk_fma_f16 v22, v26, v50, v22
	v_pk_fma_f16 v23, v27, v51, v23
	v_pk_fma_f16 v24, v28, v52, v24
	v_pk_fma_f16 v25, v29, v53, v25
	v_pk_add_f16 v47, v71, v115 neg_lo:[0,1] neg_hi:[0,1]
	v_pk_add_f16 v48, v72, v116 neg_lo:[0,1] neg_hi:[0,1]
	v_pk_add_f16 v49, v73, v117 neg_lo:[0,1] neg_hi:[0,1]
	v_exp_f16_sdwa v50, v46 dst_sel:WORD_0 dst_unused:UNUSED_PAD src0_sel:WORD_0
	v_exp_f16_sdwa v51, v47 dst_sel:WORD_0 dst_unused:UNUSED_PAD src0_sel:WORD_0
	v_exp_f16_sdwa v52, v48 dst_sel:WORD_0 dst_unused:UNUSED_PAD src0_sel:WORD_0
	v_exp_f16_sdwa v53, v49 dst_sel:WORD_0 dst_unused:UNUSED_PAD src0_sel:WORD_0
	v_exp_f16_sdwa v50, v46 dst_sel:WORD_1 dst_unused:UNUSED_PRESERVE src0_sel:WORD_1
	v_exp_f16_sdwa v51, v47 dst_sel:WORD_1 dst_unused:UNUSED_PRESERVE src0_sel:WORD_1
	v_exp_f16_sdwa v52, v48 dst_sel:WORD_1 dst_unused:UNUSED_PRESERVE src0_sel:WORD_1
	v_exp_f16_sdwa v53, v49 dst_sel:WORD_1 dst_unused:UNUSED_PRESERVE src0_sel:WORD_1
	v_pk_add_f16 v46, v82, v114 neg_lo:[0,1] neg_hi:[0,1]
	v_pk_add_f16 v30, v30, v53
	v_pk_add_f16 v33, v33, v50
	v_pk_add_f16 v32, v32, v51
	v_pk_add_f16 v31, v31, v52
	v_pk_fma_f16 v25, v41, v53, v25
	v_pk_fma_f16 v24, v40, v52, v24
	v_pk_fma_f16 v23, v39, v51, v23
	v_pk_fma_f16 v22, v38, v50, v22
	v_pk_add_f16 v47, v83, v115 neg_lo:[0,1] neg_hi:[0,1]
	v_pk_add_f16 v48, v84, v116 neg_lo:[0,1] neg_hi:[0,1]
	v_pk_add_f16 v49, v85, v117 neg_lo:[0,1] neg_hi:[0,1]
	v_exp_f16_sdwa v50, v46 dst_sel:WORD_0 dst_unused:UNUSED_PAD src0_sel:WORD_0
	v_exp_f16_sdwa v51, v47 dst_sel:WORD_0 dst_unused:UNUSED_PAD src0_sel:WORD_0
	v_exp_f16_sdwa v52, v48 dst_sel:WORD_0 dst_unused:UNUSED_PAD src0_sel:WORD_0
	v_exp_f16_sdwa v53, v49 dst_sel:WORD_0 dst_unused:UNUSED_PAD src0_sel:WORD_0
	v_exp_f16_sdwa v50, v46 dst_sel:WORD_1 dst_unused:UNUSED_PRESERVE src0_sel:WORD_1
	v_exp_f16_sdwa v51, v47 dst_sel:WORD_1 dst_unused:UNUSED_PRESERVE src0_sel:WORD_1
	v_exp_f16_sdwa v52, v48 dst_sel:WORD_1 dst_unused:UNUSED_PRESERVE src0_sel:WORD_1
	v_exp_f16_sdwa v53, v49 dst_sel:WORD_1 dst_unused:UNUSED_PRESERVE src0_sel:WORD_1
	s_nop 0
	v_pk_add_f16 v30, v30, v53
	v_pk_add_f16 v31, v31, v52
	v_rcp_f16_e32 v48, v30
	v_rcp_f16_sdwa v30, v30 dst_sel:DWORD dst_unused:UNUSED_PAD src0_sel:WORD_1
	v_pk_add_f16 v32, v32, v51
	v_rcp_f16_e32 v49, v31
	v_rcp_f16_sdwa v31, v31 dst_sel:DWORD dst_unused:UNUSED_PAD src0_sel:WORD_1
	v_pk_add_f16 v33, v33, v50
	v_rcp_f16_e32 v47, v32
	v_rcp_f16_sdwa v32, v32 dst_sel:DWORD dst_unused:UNUSED_PAD src0_sel:WORD_1
	v_rcp_f16_e32 v46, v33
	v_rcp_f16_sdwa v33, v33 dst_sel:DWORD dst_unused:UNUSED_PAD src0_sel:WORD_1
	v_pk_fma_f16 v25, v61, v53, v25
	v_pack_b32_f16 v30, v48, v30
	v_pk_fma_f16 v24, v60, v52, v24
	v_pk_mul_f16 v25, v25, v30
	v_pack_b32_f16 v30, v49, v31
	v_pk_fma_f16 v23, v59, v51, v23
	v_pk_mul_f16 v24, v24, v30
	v_pack_b32_f16 v30, v47, v32
	v_pk_fma_f16 v22, v58, v50, v22
	v_pk_mul_f16 v23, v23, v30
	v_pack_b32_f16 v30, v46, v33
	v_pk_mul_f16 v22, v22, v30
	s_waitcnt vmcnt(0)
	v_pk_mul_f16 v30, v185, v146 op_sel_hi:[0,1]
	v_pk_mul_f16 v31, v185, v147 op_sel_hi:[0,1]
	v_pk_mul_f16 v32, v185, v148 op_sel_hi:[0,1]
	v_pk_mul_f16 v33, v185, v149 op_sel_hi:[0,1]
	v_pk_mul_f16 v46, v183, v146 op_sel_hi:[0,1]
	v_pk_mul_f16 v47, v183, v147 op_sel_hi:[0,1]
	v_pk_mul_f16 v48, v183, v148 op_sel_hi:[0,1]
	v_pk_mul_f16 v49, v183, v149 op_sel_hi:[0,1]
	v_pk_mul_f16 v50, v184, v146 op_sel_hi:[0,1]
	v_pk_mul_f16 v51, v184, v147 op_sel_hi:[0,1]
	v_pk_mul_f16 v52, v184, v148 op_sel_hi:[0,1]
	v_pk_mul_f16 v53, v184, v149 op_sel_hi:[0,1]
	v_pk_fma_f16 v21, v21, v149, v33
	v_pk_fma_f16 v20, v20, v148, v32
	v_pk_fma_f16 v19, v19, v147, v31
	v_pk_fma_f16 v18, v18, v146, v30
	v_pk_fma_f16 v37, v37, v149, v49
	v_pk_fma_f16 v36, v36, v148, v48
	v_pk_fma_f16 v35, v35, v147, v47
	v_pk_fma_f16 v34, v34, v146, v46
	v_pk_fma_f16 v57, v57, v149, v53
	v_pk_fma_f16 v56, v56, v148, v52
	v_pk_fma_f16 v55, v55, v147, v51
	v_pk_fma_f16 v54, v54, v146, v50
	v_pk_fma_f16 v62, v77, v149, v33
	v_pk_fma_f16 v63, v76, v148, v32
	v_pk_fma_f16 v64, v75, v147, v31
	v_pk_fma_f16 v65, v74, v146, v30
	v_pk_maximum3_f16 v74, v18, v34, v54
	v_pk_maximum3_f16 v75, v19, v35, v55
	v_pk_maximum3_f16 v76, v20, v36, v56
	v_pk_maximum3_f16 v77, v21, v37, v57
	v_pk_fma_f16 v66, v105, v149, v49
	v_pk_fma_f16 v67, v104, v148, v48
	v_pk_fma_f16 v68, v103, v147, v47
	v_pk_fma_f16 v69, v102, v146, v46
	v_pk_fma_f16 v70, v121, v149, v53
	v_pk_fma_f16 v71, v120, v148, v52
	v_pk_fma_f16 v72, v119, v147, v51
	v_pk_fma_f16 v73, v118, v146, v50
	v_pk_fma_f16 v33, v133, v149, v33
	v_pk_fma_f16 v32, v132, v148, v32
	v_pk_fma_f16 v31, v131, v147, v31
	v_pk_fma_f16 v30, v130, v146, v30
	v_pk_fma_f16 v49, v141, v149, v49
	v_pk_fma_f16 v48, v140, v148, v48
	v_pk_fma_f16 v47, v139, v147, v47
	v_pk_fma_f16 v46, v138, v146, v46
	v_pk_fma_f16 v53, v145, v149, v53
	v_pk_fma_f16 v52, v144, v148, v52
	v_pk_fma_f16 v51, v143, v147, v51
	v_pk_fma_f16 v50, v142, v146, v50
	v_pk_maximum3_f16 v82, v65, v69, v73
	v_pk_maximum3_f16 v83, v64, v68, v72
	v_pk_maximum3_f16 v84, v63, v67, v71
	v_pk_maximum3_f16 v85, v62, v66, v70
	v_pk_maximum3_f16 v87, v31, v47, v51
	v_pk_maximum3_f16 v86, v30, v46, v50
	v_pk_maximum3_f16 v88, v32, v48, v52
	v_pk_maximum3_f16 v89, v33, v49, v53
	v_pk_maximum3_f16 v74, v74, v82, v86
	v_pk_maximum3_f16 v75, v75, v83, v87
	v_pk_maximum3_f16 v76, v76, v84, v88
	v_pk_maximum3_f16 v77, v77, v85, v89
	s_nop 0
	v_pk_add_f16 v18, v18, v74 neg_lo:[0,1] neg_hi:[0,1]
	v_pk_add_f16 v19, v19, v75 neg_lo:[0,1] neg_hi:[0,1]
	v_pk_add_f16 v20, v20, v76 neg_lo:[0,1] neg_hi:[0,1]
	v_pk_add_f16 v21, v21, v77 neg_lo:[0,1] neg_hi:[0,1]
	v_pk_add_f16 v34, v34, v74 neg_lo:[0,1] neg_hi:[0,1]
	v_exp_f16_sdwa v82, v18 dst_sel:WORD_0 dst_unused:UNUSED_PAD src0_sel:WORD_0
	v_exp_f16_sdwa v83, v19 dst_sel:WORD_0 dst_unused:UNUSED_PAD src0_sel:WORD_0
	v_exp_f16_sdwa v84, v20 dst_sel:WORD_0 dst_unused:UNUSED_PAD src0_sel:WORD_0
	v_exp_f16_sdwa v85, v21 dst_sel:WORD_0 dst_unused:UNUSED_PAD src0_sel:WORD_0
	v_exp_f16_sdwa v82, v18 dst_sel:WORD_1 dst_unused:UNUSED_PRESERVE src0_sel:WORD_1
	v_exp_f16_sdwa v83, v19 dst_sel:WORD_1 dst_unused:UNUSED_PRESERVE src0_sel:WORD_1
	v_exp_f16_sdwa v84, v20 dst_sel:WORD_1 dst_unused:UNUSED_PRESERVE src0_sel:WORD_1
	v_exp_f16_sdwa v85, v21 dst_sel:WORD_1 dst_unused:UNUSED_PRESERVE src0_sel:WORD_1
	v_pk_add_f16 v35, v35, v75 neg_lo:[0,1] neg_hi:[0,1]
	v_pk_add_f16 v18, v82, 0
	v_pk_add_f16 v19, v83, 0
	v_pk_add_f16 v20, v84, 0
	v_pk_add_f16 v21, v85, 0
	v_pk_fma_f16 v6, v6, v82, 0
	v_pk_fma_f16 v7, v7, v83, 0
	v_pk_fma_f16 v8, v8, v84, 0
	v_pk_fma_f16 v9, v9, v85, 0
	v_pk_add_f16 v36, v36, v76 neg_lo:[0,1] neg_hi:[0,1]
	v_pk_add_f16 v37, v37, v77 neg_lo:[0,1] neg_hi:[0,1]
	v_exp_f16_sdwa v82, v34 dst_sel:WORD_0 dst_unused:UNUSED_PAD src0_sel:WORD_0
	v_exp_f16_sdwa v83, v35 dst_sel:WORD_0 dst_unused:UNUSED_PAD src0_sel:WORD_0
	v_exp_f16_sdwa v84, v36 dst_sel:WORD_0 dst_unused:UNUSED_PAD src0_sel:WORD_0
	v_exp_f16_sdwa v85, v37 dst_sel:WORD_0 dst_unused:UNUSED_PAD src0_sel:WORD_0
	v_exp_f16_sdwa v82, v34 dst_sel:WORD_1 dst_unused:UNUSED_PRESERVE src0_sel:WORD_1
	v_exp_f16_sdwa v83, v35 dst_sel:WORD_1 dst_unused:UNUSED_PRESERVE src0_sel:WORD_1
	v_exp_f16_sdwa v84, v36 dst_sel:WORD_1 dst_unused:UNUSED_PRESERVE src0_sel:WORD_1
	v_exp_f16_sdwa v85, v37 dst_sel:WORD_1 dst_unused:UNUSED_PRESERVE src0_sel:WORD_1
	s_nop 0
	v_pk_add_f16 v21, v21, v85
	v_pk_add_f16 v20, v20, v84
	v_pk_add_f16 v19, v19, v83
	v_pk_add_f16 v18, v18, v82
	v_pk_fma_f16 v9, v13, v85, v9
	v_pk_fma_f16 v8, v12, v84, v8
	v_pk_fma_f16 v7, v11, v83, v7
	v_pk_fma_f16 v6, v10, v82, v6
	v_pk_add_f16 v10, v54, v74 neg_lo:[0,1] neg_hi:[0,1]
	v_pk_add_f16 v11, v55, v75 neg_lo:[0,1] neg_hi:[0,1]
	v_pk_add_f16 v12, v56, v76 neg_lo:[0,1] neg_hi:[0,1]
	v_pk_add_f16 v13, v57, v77 neg_lo:[0,1] neg_hi:[0,1]
	v_exp_f16_sdwa v34, v10 dst_sel:WORD_0 dst_unused:UNUSED_PAD src0_sel:WORD_0
	v_exp_f16_sdwa v35, v11 dst_sel:WORD_0 dst_unused:UNUSED_PAD src0_sel:WORD_0
	v_exp_f16_sdwa v36, v12 dst_sel:WORD_0 dst_unused:UNUSED_PAD src0_sel:WORD_0
	v_exp_f16_sdwa v37, v13 dst_sel:WORD_0 dst_unused:UNUSED_PAD src0_sel:WORD_0
	v_exp_f16_sdwa v34, v10 dst_sel:WORD_1 dst_unused:UNUSED_PRESERVE src0_sel:WORD_1
	v_exp_f16_sdwa v35, v11 dst_sel:WORD_1 dst_unused:UNUSED_PRESERVE src0_sel:WORD_1
	v_exp_f16_sdwa v36, v12 dst_sel:WORD_1 dst_unused:UNUSED_PRESERVE src0_sel:WORD_1
	v_exp_f16_sdwa v37, v13 dst_sel:WORD_1 dst_unused:UNUSED_PRESERVE src0_sel:WORD_1
	v_pk_add_f16 v10, v18, v34
	v_pk_add_f16 v11, v19, v35
	v_pk_add_f16 v12, v20, v36
	v_pk_add_f16 v13, v21, v37
	v_pk_fma_f16 v6, v14, v34, v6
	v_pk_fma_f16 v7, v15, v35, v7
	v_pk_fma_f16 v8, v16, v36, v8
	v_pk_fma_f16 v9, v17, v37, v9
	v_pk_add_f16 v14, v65, v74 neg_lo:[0,1] neg_hi:[0,1]
	v_pk_add_f16 v15, v64, v75 neg_lo:[0,1] neg_hi:[0,1]
	v_pk_add_f16 v16, v63, v76 neg_lo:[0,1] neg_hi:[0,1]
	v_pk_add_f16 v17, v62, v77 neg_lo:[0,1] neg_hi:[0,1]
	v_exp_f16_sdwa v18, v14 dst_sel:WORD_0 dst_unused:UNUSED_PAD src0_sel:WORD_0
	v_exp_f16_sdwa v19, v15 dst_sel:WORD_0 dst_unused:UNUSED_PAD src0_sel:WORD_0
	v_exp_f16_sdwa v20, v16 dst_sel:WORD_0 dst_unused:UNUSED_PAD src0_sel:WORD_0
	v_exp_f16_sdwa v21, v17 dst_sel:WORD_0 dst_unused:UNUSED_PAD src0_sel:WORD_0
	v_exp_f16_sdwa v18, v14 dst_sel:WORD_1 dst_unused:UNUSED_PRESERVE src0_sel:WORD_1
	v_exp_f16_sdwa v19, v15 dst_sel:WORD_1 dst_unused:UNUSED_PRESERVE src0_sel:WORD_1
	v_exp_f16_sdwa v20, v16 dst_sel:WORD_1 dst_unused:UNUSED_PRESERVE src0_sel:WORD_1
	v_exp_f16_sdwa v21, v17 dst_sel:WORD_1 dst_unused:UNUSED_PRESERVE src0_sel:WORD_1
	v_pk_add_f16 v14, v69, v74 neg_lo:[0,1] neg_hi:[0,1]
	v_pk_add_f16 v13, v13, v21
	v_pk_add_f16 v12, v12, v20
	v_pk_add_f16 v11, v11, v19
	v_pk_add_f16 v10, v10, v18
	v_pk_fma_f16 v9, v29, v21, v9
	v_pk_fma_f16 v8, v28, v20, v8
	v_pk_fma_f16 v7, v27, v19, v7
	v_pk_fma_f16 v6, v26, v18, v6
	v_pk_add_f16 v15, v68, v75 neg_lo:[0,1] neg_hi:[0,1]
	v_pk_add_f16 v16, v67, v76 neg_lo:[0,1] neg_hi:[0,1]
	v_pk_add_f16 v17, v66, v77 neg_lo:[0,1] neg_hi:[0,1]
	v_exp_f16_sdwa v18, v14 dst_sel:WORD_0 dst_unused:UNUSED_PAD src0_sel:WORD_0
	v_exp_f16_sdwa v19, v15 dst_sel:WORD_0 dst_unused:UNUSED_PAD src0_sel:WORD_0
	v_exp_f16_sdwa v20, v16 dst_sel:WORD_0 dst_unused:UNUSED_PAD src0_sel:WORD_0
	v_exp_f16_sdwa v21, v17 dst_sel:WORD_0 dst_unused:UNUSED_PAD src0_sel:WORD_0
	v_exp_f16_sdwa v18, v14 dst_sel:WORD_1 dst_unused:UNUSED_PRESERVE src0_sel:WORD_1
	v_exp_f16_sdwa v19, v15 dst_sel:WORD_1 dst_unused:UNUSED_PRESERVE src0_sel:WORD_1
	v_exp_f16_sdwa v20, v16 dst_sel:WORD_1 dst_unused:UNUSED_PRESERVE src0_sel:WORD_1
	v_exp_f16_sdwa v21, v17 dst_sel:WORD_1 dst_unused:UNUSED_PRESERVE src0_sel:WORD_1
	v_pk_add_f16 v14, v73, v74 neg_lo:[0,1] neg_hi:[0,1]
	v_pk_add_f16 v10, v10, v18
	v_pk_add_f16 v11, v11, v19
	v_pk_add_f16 v12, v12, v20
	v_pk_add_f16 v13, v13, v21
	v_pk_fma_f16 v6, v38, v18, v6
	v_pk_fma_f16 v7, v39, v19, v7
	v_pk_fma_f16 v8, v40, v20, v8
	v_pk_fma_f16 v9, v41, v21, v9
	v_pk_add_f16 v15, v72, v75 neg_lo:[0,1] neg_hi:[0,1]
	v_pk_add_f16 v16, v71, v76 neg_lo:[0,1] neg_hi:[0,1]
	v_pk_add_f16 v17, v70, v77 neg_lo:[0,1] neg_hi:[0,1]
	v_exp_f16_sdwa v18, v14 dst_sel:WORD_0 dst_unused:UNUSED_PAD src0_sel:WORD_0
	v_exp_f16_sdwa v19, v15 dst_sel:WORD_0 dst_unused:UNUSED_PAD src0_sel:WORD_0
	v_exp_f16_sdwa v20, v16 dst_sel:WORD_0 dst_unused:UNUSED_PAD src0_sel:WORD_0
	v_exp_f16_sdwa v21, v17 dst_sel:WORD_0 dst_unused:UNUSED_PAD src0_sel:WORD_0
	v_exp_f16_sdwa v18, v14 dst_sel:WORD_1 dst_unused:UNUSED_PRESERVE src0_sel:WORD_1
	v_exp_f16_sdwa v19, v15 dst_sel:WORD_1 dst_unused:UNUSED_PRESERVE src0_sel:WORD_1
	v_exp_f16_sdwa v20, v16 dst_sel:WORD_1 dst_unused:UNUSED_PRESERVE src0_sel:WORD_1
	v_exp_f16_sdwa v21, v17 dst_sel:WORD_1 dst_unused:UNUSED_PRESERVE src0_sel:WORD_1
	v_pk_add_f16 v14, v30, v74 neg_lo:[0,1] neg_hi:[0,1]
	v_pk_add_f16 v13, v13, v21
	v_pk_add_f16 v12, v12, v20
	v_pk_add_f16 v11, v11, v19
	v_pk_add_f16 v10, v10, v18
	v_pk_fma_f16 v9, v61, v21, v9
	v_pk_fma_f16 v8, v60, v20, v8
	v_pk_fma_f16 v7, v59, v19, v7
	v_pk_fma_f16 v6, v58, v18, v6
	v_pk_add_f16 v15, v31, v75 neg_lo:[0,1] neg_hi:[0,1]
	v_pk_add_f16 v16, v32, v76 neg_lo:[0,1] neg_hi:[0,1]
	v_pk_add_f16 v17, v33, v77 neg_lo:[0,1] neg_hi:[0,1]
	v_exp_f16_sdwa v18, v14 dst_sel:WORD_0 dst_unused:UNUSED_PAD src0_sel:WORD_0
	v_exp_f16_sdwa v19, v15 dst_sel:WORD_0 dst_unused:UNUSED_PAD src0_sel:WORD_0
	v_exp_f16_sdwa v20, v16 dst_sel:WORD_0 dst_unused:UNUSED_PAD src0_sel:WORD_0
	v_exp_f16_sdwa v21, v17 dst_sel:WORD_0 dst_unused:UNUSED_PAD src0_sel:WORD_0
	v_exp_f16_sdwa v18, v14 dst_sel:WORD_1 dst_unused:UNUSED_PRESERVE src0_sel:WORD_1
	v_exp_f16_sdwa v19, v15 dst_sel:WORD_1 dst_unused:UNUSED_PRESERVE src0_sel:WORD_1
	v_exp_f16_sdwa v20, v16 dst_sel:WORD_1 dst_unused:UNUSED_PRESERVE src0_sel:WORD_1
	v_exp_f16_sdwa v21, v17 dst_sel:WORD_1 dst_unused:UNUSED_PRESERVE src0_sel:WORD_1
	v_pk_add_f16 v10, v10, v18
	v_pk_add_f16 v11, v11, v19
	v_pk_add_f16 v12, v12, v20
	v_pk_add_f16 v13, v13, v21
	v_pk_fma_f16 v14, v78, v18, v6
	v_pk_fma_f16 v15, v79, v19, v7
	v_pk_fma_f16 v16, v80, v20, v8
	v_pk_fma_f16 v17, v81, v21, v9
	v_pk_add_f16 v6, v46, v74 neg_lo:[0,1] neg_hi:[0,1]
	v_pk_add_f16 v7, v47, v75 neg_lo:[0,1] neg_hi:[0,1]
	v_pk_add_f16 v8, v48, v76 neg_lo:[0,1] neg_hi:[0,1]
	v_pk_add_f16 v9, v49, v77 neg_lo:[0,1] neg_hi:[0,1]
	v_exp_f16_sdwa v18, v6 dst_sel:WORD_0 dst_unused:UNUSED_PAD src0_sel:WORD_0
	v_exp_f16_sdwa v19, v7 dst_sel:WORD_0 dst_unused:UNUSED_PAD src0_sel:WORD_0
	v_exp_f16_sdwa v20, v8 dst_sel:WORD_0 dst_unused:UNUSED_PAD src0_sel:WORD_0
	v_exp_f16_sdwa v21, v9 dst_sel:WORD_0 dst_unused:UNUSED_PAD src0_sel:WORD_0
	v_exp_f16_sdwa v18, v6 dst_sel:WORD_1 dst_unused:UNUSED_PRESERVE src0_sel:WORD_1
	v_exp_f16_sdwa v19, v7 dst_sel:WORD_1 dst_unused:UNUSED_PRESERVE src0_sel:WORD_1
	v_exp_f16_sdwa v20, v8 dst_sel:WORD_1 dst_unused:UNUSED_PRESERVE src0_sel:WORD_1
	v_exp_f16_sdwa v21, v9 dst_sel:WORD_1 dst_unused:UNUSED_PRESERVE src0_sel:WORD_1
	s_nop 0
	v_pk_add_f16 v9, v13, v21
	v_pk_add_f16 v8, v12, v20
	v_pk_add_f16 v7, v11, v19
	v_pk_add_f16 v6, v10, v18
	v_pk_fma_f16 v13, v93, v21, v17
	v_pk_fma_f16 v12, v92, v20, v16
	v_pk_fma_f16 v11, v91, v19, v15
	v_pk_fma_f16 v10, v90, v18, v14
	v_pk_add_f16 v18, v50, v74 neg_lo:[0,1] neg_hi:[0,1]
	v_pk_add_f16 v19, v51, v75 neg_lo:[0,1] neg_hi:[0,1]
	v_pk_add_f16 v20, v52, v76 neg_lo:[0,1] neg_hi:[0,1]
	v_pk_add_f16 v21, v53, v77 neg_lo:[0,1] neg_hi:[0,1]
	v_exp_f16_sdwa v14, v18 dst_sel:WORD_0 dst_unused:UNUSED_PAD src0_sel:WORD_0
	v_exp_f16_sdwa v17, v19 dst_sel:WORD_0 dst_unused:UNUSED_PAD src0_sel:WORD_0
	v_exp_f16_sdwa v15, v20 dst_sel:WORD_0 dst_unused:UNUSED_PAD src0_sel:WORD_0
	v_exp_f16_sdwa v16, v21 dst_sel:WORD_0 dst_unused:UNUSED_PAD src0_sel:WORD_0
	v_exp_f16_sdwa v14, v18 dst_sel:WORD_1 dst_unused:UNUSED_PRESERVE src0_sel:WORD_1
	v_exp_f16_sdwa v17, v19 dst_sel:WORD_1 dst_unused:UNUSED_PRESERVE src0_sel:WORD_1
	v_exp_f16_sdwa v15, v20 dst_sel:WORD_1 dst_unused:UNUSED_PRESERVE src0_sel:WORD_1
	v_exp_f16_sdwa v16, v21 dst_sel:WORD_1 dst_unused:UNUSED_PRESERVE src0_sel:WORD_1
	s_nop 0
.LBB5_42:
	s_and_b64 vcc, exec, s[4:5]
	s_cbranch_vccz .LBB5_3
	s_load_dwordx2 s[0:1], s[22:23], 0x18
	s_waitcnt lgkmcnt(0)
	s_load_dwordx2 s[6:7], s[0:1], 0x0
	s_load_dword s28, s[0:1], 0x8
	v_cmp_lt_u32_e64 s[64:65], 0, v182
	v_cmp_gt_u32_e64 s[66:67], 63, v182
	v_cmp_lt_u32_e64 s[68:69], 0, v162
	v_cmp_gt_u32_e64 s[70:71], 60, v162
	buffer_load_dwordx4 v[184:187], v180, s[16:19], 0 offen
	s_and_b64 s[72:73], s[68:69], s[64:65]
	s_and_b64 s[74:75], s[68:69], s[66:67]
	s_and_b64 s[76:77], s[70:71], s[64:65]
	s_and_b64 s[78:79], s[70:71], s[66:67]
	v_mov_b32_e32 v110, v172
	v_mov_b32_e32 v111, v174
	v_mov_b32_e32 v112, v176
	v_mov_b32_e32 v113, v178
	v_mov_b32_e32 v78, v173
	v_mov_b32_e32 v79, v175
	v_mov_b32_e32 v80, v177
	v_mov_b32_e32 v81, v179
	v_mov_b32_e32 v126, v172
	v_mov_b32_e32 v127, v174
	v_mov_b32_e32 v128, v176
	v_mov_b32_e32 v129, v178
	v_mov_b32_e32 v102, v173
	v_mov_b32_e32 v103, v175
	v_mov_b32_e32 v104, v177
	v_mov_b32_e32 v105, v179
	v_mov_b32_e32 v134, v172
	v_mov_b32_e32 v135, v174
	v_mov_b32_e32 v136, v176
	v_mov_b32_e32 v137, v178
	v_mov_b32_e32 v114, v173
	v_mov_b32_e32 v115, v175
	v_mov_b32_e32 v116, v177
	v_mov_b32_e32 v117, v179
	v_mov_b32_e32 v82, v172
	v_mov_b32_e32 v83, v174
	v_mov_b32_e32 v84, v176
	v_mov_b32_e32 v85, v178
	v_mov_b32_e32 v42, v173
	v_mov_b32_e32 v43, v175
	v_mov_b32_e32 v44, v177
	v_mov_b32_e32 v45, v179
	v_mov_b32_e32 v122, v172
	v_mov_b32_e32 v123, v174
	v_mov_b32_e32 v124, v176
	v_mov_b32_e32 v125, v178
	v_mov_b32_e32 v86, v173
	v_mov_b32_e32 v87, v175
	v_mov_b32_e32 v88, v177
	v_mov_b32_e32 v89, v179
	v_mov_b32_e32 v50, v172
	v_mov_b32_e32 v51, v174
	v_mov_b32_e32 v52, v176
	v_mov_b32_e32 v53, v178
	v_mov_b32_e32 v22, v173
	v_mov_b32_e32 v23, v175
	v_mov_b32_e32 v24, v177
	v_mov_b32_e32 v25, v179
	v_mov_b32_e32 v94, v172
	v_mov_b32_e32 v95, v174
	v_mov_b32_e32 v96, v176
	v_mov_b32_e32 v97, v178
	v_mov_b32_e32 v46, v173
	v_mov_b32_e32 v47, v175
	v_mov_b32_e32 v48, v177
	v_mov_b32_e32 v49, v179
	v_mov_b32_e32 v18, v172
	v_mov_b32_e32 v19, v174
	v_mov_b32_e32 v20, v176
	v_mov_b32_e32 v21, v178
	v_mov_b32_e32 v6, v173
	v_mov_b32_e32 v7, v175
	v_mov_b32_e32 v8, v177
	v_mov_b32_e32 v9, v179
	v_mov_b32_e32 v54, v172
	v_mov_b32_e32 v55, v174
	v_mov_b32_e32 v56, v176
	v_mov_b32_e32 v57, v178
	v_mov_b32_e32 v14, v173
	v_mov_b32_e32 v15, v175
	v_mov_b32_e32 v16, v177
	v_mov_b32_e32 v17, v179
	v_mov_b32_e32 v74, v172
	v_mov_b32_e32 v75, v174
	v_mov_b32_e32 v76, v176
	v_mov_b32_e32 v77, v178
	v_mov_b32_e32 v26, v173
	v_mov_b32_e32 v27, v175
	v_mov_b32_e32 v28, v177
	v_mov_b32_e32 v29, v179
	v_mov_b32_e32 v118, v172
	v_mov_b32_e32 v119, v174
	v_mov_b32_e32 v120, v176
	v_mov_b32_e32 v121, v178
	v_mov_b32_e32 v58, v173
	v_mov_b32_e32 v59, v175
	v_mov_b32_e32 v60, v177
	v_mov_b32_e32 v61, v179
	v_mov_b32_e32 v130, v172
	v_mov_b32_e32 v131, v174
	v_mov_b32_e32 v132, v176
	v_mov_b32_e32 v133, v178
	v_mov_b32_e32 v70, v173
	v_mov_b32_e32 v71, v175
	v_mov_b32_e32 v72, v177
	v_mov_b32_e32 v73, v179
	v_mov_b32_e32 v138, v172
	v_mov_b32_e32 v139, v174
	v_mov_b32_e32 v140, v176
	v_mov_b32_e32 v141, v178
	v_mov_b32_e32 v90, v173
	v_mov_b32_e32 v91, v175
	v_mov_b32_e32 v92, v177
	v_mov_b32_e32 v93, v179
	v_mov_b32_e32 v142, v172
	v_mov_b32_e32 v143, v174
	v_mov_b32_e32 v144, v176
	v_mov_b32_e32 v145, v178
	v_mov_b32_e32 v2, v173
	v_mov_b32_e32 v3, v175
	v_mov_b32_e32 v4, v177
	v_mov_b32_e32 v5, v179
	v_add_u32_e32 v224, 0xfffe7c00, v180
	v_add_u32_e32 v225, 0xfffe8000, v180
	s_mov_b64 exec, s[72:73]
	buffer_load_dwordx4 v[110:113], v224, s[16:19], 0 offen
	buffer_load_dwordx4 v[78:81], v224, s[16:19], 0 offen offset:512
	s_mov_b64 exec, -1
	s_mov_b64 exec, s[68:69]
	buffer_load_dwordx4 v[126:129], v225, s[16:19], 0 offen offset:512
	buffer_load_dwordx4 v[102:105], v225, s[16:19], 0 offen offset:1024
	s_mov_b64 exec, -1
	s_mov_b64 exec, s[74:75]
	buffer_load_dwordx4 v[134:137], v225, s[16:19], 0 offen offset:2048
	buffer_load_dwordx4 v[114:117], v225, s[16:19], 0 offen offset:2560
	s_mov_b64 exec, -1
	v_add_u32_e32 v224, 0xfffffc00, v180
	s_mov_b64 exec, s[64:65]
	buffer_load_dwordx4 v[82:85], v224, s[16:19], 0 offen
	buffer_load_dwordx4 v[42:45], v224, s[16:19], 0 offen offset:512
	s_mov_b64 exec, -1
	buffer_load_dwordx4 v[106:109], v180, s[16:19], 0 offen offset:512
	buffer_load_dwordx4 v[62:65], v180, s[16:19], 0 offen offset:1024
	s_mov_b64 exec, s[66:67]
	buffer_load_dwordx4 v[122:125], v180, s[16:19], 0 offen offset:2048
	buffer_load_dwordx4 v[86:89], v180, s[16:19], 0 offen offset:2560
	s_mov_b64 exec, -1
	v_add_u32_e32 v224, 0x17c00, v180
	v_add_u32_e32 v225, 0x18000, v180
	s_mov_b64 exec, s[64:65]
	buffer_load_dwordx4 v[50:53], v224, s[16:19], 0 offen
	buffer_load_dwordx4 v[22:25], v224, s[16:19], 0 offen offset:512
	s_mov_b64 exec, -1
	buffer_load_dwordx4 v[66:69], v225, s[16:19], 0 offen offset:512
	buffer_load_dwordx4 v[34:37], v225, s[16:19], 0 offen offset:1024
	s_mov_b64 exec, s[66:67]
	buffer_load_dwordx4 v[94:97], v225, s[16:19], 0 offen offset:2048
	buffer_load_dwordx4 v[46:49], v225, s[16:19], 0 offen offset:2560
	s_mov_b64 exec, -1
	v_add_u32_e32 v224, 0x18000, v180
	buffer_load_dwordx4 v[154:157], v224, s[16:19], 0 offen
	v_add_u32_e32 v225, 0x30000, v180
	buffer_load_dwordx4 v[150:153], v225, s[16:19], 0 offen
	v_add_u32_e32 v224, 0x48000, v180
	buffer_load_dwordx4 v[146:149], v224, s[16:19], 0 offen
	v_add_u32_e32 v224, 0x2fc00, v180
	v_add_u32_e32 v225, 0x30000, v180
	v_add_u32_e32 v226, 0x47c00, v180
	v_add_u32_e32 v227, 0x48000, v180
	v_add_u32_e32 v228, 0x5fc00, v180
	v_add_u32_e32 v229, 0x60000, v180
	s_branch .LBB5_2

	.amdhsa_kernel _Z7k_stageILi0ELi4EEv8AttnArgsPKDF16_PKfPDF16_iii
		.amdhsa_group_segment_fixed_size 82944
		.amdhsa_private_segment_fixed_size 0
		.amdhsa_kernarg_size 148
		.amdhsa_user_sgpr_count 2
		.amdhsa_user_sgpr_dispatch_ptr 0
		.amdhsa_user_sgpr_queue_ptr 0
		.amdhsa_user_sgpr_kernarg_segment_ptr 1
		.amdhsa_user_sgpr_dispatch_id 0
		.amdhsa_user_sgpr_kernarg_preload_length 0
		.amdhsa_user_sgpr_kernarg_preload_offset 0
		.amdhsa_user_sgpr_private_segment_size 0
		.amdhsa_uses_dynamic_stack 0
		.amdhsa_enable_private_segment 0
		.amdhsa_system_sgpr_workgroup_id_x 1
		.amdhsa_system_sgpr_workgroup_id_y 1
		.amdhsa_system_sgpr_workgroup_id_z 0
		.amdhsa_system_sgpr_workgroup_info 0
		.amdhsa_system_vgpr_workitem_id 0
		.amdhsa_next_free_vgpr 230
		.amdhsa_next_free_sgpr 96
		.amdhsa_accum_offset 232
		.amdhsa_reserve_vcc 1
		.amdhsa_float_round_mode_32 0
		.amdhsa_float_round_mode_16_64 0
		.amdhsa_float_denorm_mode_32 3
		.amdhsa_float_denorm_mode_16_64 3
		.amdhsa_dx10_clamp 1
		.amdhsa_ieee_mode 1
		.amdhsa_fp16_overflow 0
		.amdhsa_tg_split 0
		.amdhsa_exception_fp_ieee_invalid_op 0
		.amdhsa_exception_fp_denorm_src 0
		.amdhsa_exception_fp_ieee_div_zero 0
		.amdhsa_exception_fp_ieee_overflow 0
		.amdhsa_exception_fp_ieee_underflow 0
		.amdhsa_exception_fp_ieee_inexact 0
		.amdhsa_exception_int_div_zero 0
	.end_amdhsa_kernel

_Z7k_attn2ILi2EEv8AttnArgs:
	v_readfirstlane_b32 s3, v0
	s_lshl_b32 s12, s3, 1
	v_lshlrev_b32_e32 v3, 3, v0
	s_and_b32 s12, s12, 0x80
	v_and_b32_e32 v3, 0x78, v3
	s_load_dwordx4 s[8:11], s[0:1], 0x0
	s_load_dwordx2 s[4:5], s[0:1], 0x10
	s_load_dwordx2 s[6:7], s[0:1], 0x50
	v_or_b32_e32 v180, s12, v3
	s_lshl_b32 s12, s2, 5
	v_lshrrev_b32_e32 v1, 5, v0
	v_bfe_u32 v2, v0, 4, 2
	s_and_b32 s14, s12, 0xe0
	s_lshr_b32 s12, s2, 3
	v_lshrrev_b32_e32 v0, 6, v0
	v_and_b32_e32 v1, 4, v1
	s_add_i32 s14, s14, s12
	s_and_b32 s2, s2, 56
	v_and_b32_e32 v0, 4, v0
	v_and_or_b32 v181, s14, 56, v0
	v_or3_b32 v182, v2, s2, v1
	s_and_b32 s2, s14, 0x3ffffc0
	v_or_b32_e32 v4, s2, v181
	v_lshlrev_b32_e32 v0, 1, v180
	v_mov_b32_e32 v1, 0
	s_waitcnt lgkmcnt(0)
	v_lshl_add_u64 v[2:3], s[6:7], 0, v[0:1]
	v_lshl_or_b32 v0, v4, 6, v182
	v_lshlrev_b64 v[4:5], 9, v[0:1]
	v_lshl_add_u64 v[8:9], v[2:3], 0, v[4:5]
	v_or_b32_e32 v4, 64, v0
	v_mov_b32_e32 v5, v1
	v_lshlrev_b64 v[4:5], 9, v[4:5]
	v_lshlrev_b32_e32 v20, 2, v180
	v_lshl_add_u64 v[10:11], v[2:3], 0, v[4:5]
	global_load_dwordx4 v[22:25], v20, s[10:11] offset:16
	global_load_dwordx4 v[16:19], v20, s[10:11]
	global_load_dwordx4 v[26:29], v20, s[4:5] offset:16
	global_load_dwordx4 v[30:33], v20, s[4:5]
	global_load_dwordx4 v[12:15], v[8:9], off nt
	global_load_dwordx4 v[4:7], v[10:11], off nt
	v_or_b32_e32 v8, 0x80, v0
	v_mov_b32_e32 v9, v1
	v_lshlrev_b64 v[8:9], 9, v[8:9]
	v_or_b32_e32 v0, 0xc0, v0
	v_lshl_add_u64 v[20:21], v[2:3], 0, v[8:9]
	v_lshlrev_b64 v[0:1], 9, v[0:1]
	v_lshl_add_u64 v[34:35], v[2:3], 0, v[0:1]
	global_load_dwordx4 v[8:11], v[20:21], off nt
	global_load_dwordx4 v[0:3], v[34:35], off nt
	s_bitcmp1_b32 s3, 6
	s_cselect_b64 s[4:5], -1, 0
	s_and_b32 s2, s14, 0x3ffc0
	v_or_b32_e32 v20, s2, v181
	v_lshl_or_b32 v20, v20, 6, v182
	v_add_u32_e32 v184, -1, v182
	v_add_u32_e32 v185, -1, v181
	v_mul_u32_u24_e32 v20, 0x300, v20
	v_or_b32_e32 v34, v185, v184
	v_or_b32_e32 v20, v180, v20
	s_mov_b32 s11, 0x20000
	s_mov_b32 s10, 0x1800000
	s_and_b32 s9, s9, 0xffff
	v_lshlrev_b32_e32 v183, 1, v20
	v_cmp_gt_u32_e64 s[2:3], 64, v34
	s_and_b64 vcc, exec, s[4:5]
	s_waitcnt vmcnt(7)
	v_cvt_pk_f16_f32 v22, v22, v23
	s_waitcnt vmcnt(6)
	v_cvt_pk_f16_f32 v20, v16, v17
	v_cvt_pk_f16_f32 v21, v18, v19
	s_waitcnt vmcnt(4)
	v_cvt_pk_f16_f32 v16, v30, v31
	v_cvt_pk_f16_f32 v17, v32, v33
	v_cvt_pk_f16_f32 v18, v26, v27
	v_cvt_pk_f16_f32 v23, v24, v25
	v_cvt_pk_f16_f32 v19, v28, v29
	s_cbranch_vccz .LBB6_38
	s_load_dwordx2 s[12:13], s[0:1], 0x20
	s_waitcnt lgkmcnt(0)
	s_load_dwordx2 s[4:5], s[12:13], 0x0
	s_load_dword s12, s[12:13], 0x8
	v_cmp_lt_u32_e64 s[64:65], 0, v182
	v_cmp_gt_u32_e64 s[66:67], 63, v182
	v_cmp_lt_u32_e64 s[68:69], 0, v181
	v_cmp_gt_u32_e64 s[70:71], 60, v181
	buffer_load_dwordx4 v[190:193], v183, s[8:11], 0 offen
	s_and_b64 s[72:73], s[68:69], s[64:65]
	s_and_b64 s[74:75], s[68:69], s[66:67]
	s_and_b64 s[76:77], s[70:71], s[64:65]
	s_and_b64 s[78:79], s[70:71], s[66:67]
	v_mov_b32_e32 v136, v20
	v_mov_b32_e32 v137, v21
	v_mov_b32_e32 v138, v22
	v_mov_b32_e32 v139, v23
	v_mov_b32_e32 v96, v16
	v_mov_b32_e32 v97, v17
	v_mov_b32_e32 v98, v18
	v_mov_b32_e32 v99, v19
	v_mov_b32_e32 v152, v20
	v_mov_b32_e32 v153, v21
	v_mov_b32_e32 v154, v22
	v_mov_b32_e32 v155, v23
	v_mov_b32_e32 v124, v16
	v_mov_b32_e32 v125, v17
	v_mov_b32_e32 v126, v18
	v_mov_b32_e32 v127, v19
	v_mov_b32_e32 v160, v20
	v_mov_b32_e32 v161, v21
	v_mov_b32_e32 v162, v22
	v_mov_b32_e32 v163, v23
	v_mov_b32_e32 v140, v16
	v_mov_b32_e32 v141, v17
	v_mov_b32_e32 v142, v18
	v_mov_b32_e32 v143, v19
	v_mov_b32_e32 v112, v20
	v_mov_b32_e32 v113, v21
	v_mov_b32_e32 v114, v22
	v_mov_b32_e32 v115, v23
	v_mov_b32_e32 v68, v16
	v_mov_b32_e32 v69, v17
	v_mov_b32_e32 v70, v18
	v_mov_b32_e32 v71, v19
	v_mov_b32_e32 v148, v20
	v_mov_b32_e32 v149, v21
	v_mov_b32_e32 v150, v22
	v_mov_b32_e32 v151, v23
	v_mov_b32_e32 v108, v16
	v_mov_b32_e32 v109, v17
	v_mov_b32_e32 v110, v18
	v_mov_b32_e32 v111, v19
	v_mov_b32_e32 v76, v20
	v_mov_b32_e32 v77, v21
	v_mov_b32_e32 v78, v22
	v_mov_b32_e32 v79, v23
	v_mov_b32_e32 v48, v16
	v_mov_b32_e32 v49, v17
	v_mov_b32_e32 v50, v18
	v_mov_b32_e32 v51, v19
	v_mov_b32_e32 v116, v20
	v_mov_b32_e32 v117, v21
	v_mov_b32_e32 v118, v22
	v_mov_b32_e32 v119, v23
	v_mov_b32_e32 v72, v16
	v_mov_b32_e32 v73, v17
	v_mov_b32_e32 v74, v18
	v_mov_b32_e32 v75, v19
	v_mov_b32_e32 v44, v20
	v_mov_b32_e32 v45, v21
	v_mov_b32_e32 v46, v22
	v_mov_b32_e32 v47, v23
	v_mov_b32_e32 v32, v16
	v_mov_b32_e32 v33, v17
	v_mov_b32_e32 v34, v18
	v_mov_b32_e32 v35, v19
	v_mov_b32_e32 v80, v20
	v_mov_b32_e32 v81, v21
	v_mov_b32_e32 v82, v22
	v_mov_b32_e32 v83, v23
	v_mov_b32_e32 v40, v16
	v_mov_b32_e32 v41, v17
	v_mov_b32_e32 v42, v18
	v_mov_b32_e32 v43, v19
	v_mov_b32_e32 v100, v20
	v_mov_b32_e32 v101, v21
	v_mov_b32_e32 v102, v22
	v_mov_b32_e32 v103, v23
	v_mov_b32_e32 v52, v16
	v_mov_b32_e32 v53, v17
	v_mov_b32_e32 v54, v18
	v_mov_b32_e32 v55, v19
	v_mov_b32_e32 v144, v20
	v_mov_b32_e32 v145, v21
	v_mov_b32_e32 v146, v22
	v_mov_b32_e32 v147, v23
	v_mov_b32_e32 v84, v16
	v_mov_b32_e32 v85, v17
	v_mov_b32_e32 v86, v18
	v_mov_b32_e32 v87, v19
	v_mov_b32_e32 v156, v20
	v_mov_b32_e32 v157, v21
	v_mov_b32_e32 v158, v22
	v_mov_b32_e32 v159, v23
	v_mov_b32_e32 v104, v16
	v_mov_b32_e32 v105, v17
	v_mov_b32_e32 v106, v18
	v_mov_b32_e32 v107, v19
	v_mov_b32_e32 v164, v20
	v_mov_b32_e32 v165, v21
	v_mov_b32_e32 v166, v22
	v_mov_b32_e32 v167, v23
	v_mov_b32_e32 v120, v16
	v_mov_b32_e32 v121, v17
	v_mov_b32_e32 v122, v18
	v_mov_b32_e32 v123, v19
	v_mov_b32_e32 v28, v20
	v_mov_b32_e32 v29, v21
	v_mov_b32_e32 v30, v22
	v_mov_b32_e32 v31, v23
	v_mov_b32_e32 v24, v16
	v_mov_b32_e32 v25, v17
	v_mov_b32_e32 v26, v18
	v_mov_b32_e32 v27, v19
	v_add_u32_e32 v228, 0xfffe7c00, v183
	v_add_u32_e32 v229, 0xfffe8000, v183
	s_mov_b64 exec, s[72:73]
	buffer_load_dwordx4 v[136:139], v228, s[8:11], 0 offen
	buffer_load_dwordx4 v[96:99], v228, s[8:11], 0 offen offset:512
	s_mov_b64 exec, -1
	s_mov_b64 exec, s[68:69]
	buffer_load_dwordx4 v[152:155], v229, s[8:11], 0 offen offset:512
	buffer_load_dwordx4 v[124:127], v229, s[8:11], 0 offen offset:1024
	s_mov_b64 exec, -1
	s_mov_b64 exec, s[74:75]
	buffer_load_dwordx4 v[160:163], v229, s[8:11], 0 offen offset:2048
	buffer_load_dwordx4 v[140:143], v229, s[8:11], 0 offen offset:2560
	s_mov_b64 exec, -1
	v_add_u32_e32 v228, 0xfffffc00, v183
	s_mov_b64 exec, s[64:65]
	buffer_load_dwordx4 v[112:115], v228, s[8:11], 0 offen
	buffer_load_dwordx4 v[68:71], v228, s[8:11], 0 offen offset:512
	s_mov_b64 exec, -1
	buffer_load_dwordx4 v[132:135], v183, s[8:11], 0 offen offset:512
	buffer_load_dwordx4 v[88:91], v183, s[8:11], 0 offen offset:1024
	s_mov_b64 exec, s[66:67]
	buffer_load_dwordx4 v[148:151], v183, s[8:11], 0 offen offset:2048
	buffer_load_dwordx4 v[108:111], v183, s[8:11], 0 offen offset:2560
	s_mov_b64 exec, -1
	v_add_u32_e32 v228, 0x17c00, v183
	v_add_u32_e32 v229, 0x18000, v183
	s_mov_b64 exec, s[64:65]
	buffer_load_dwordx4 v[76:79], v228, s[8:11], 0 offen
	buffer_load_dwordx4 v[48:51], v228, s[8:11], 0 offen offset:512
	s_mov_b64 exec, -1
	buffer_load_dwordx4 v[92:95], v229, s[8:11], 0 offen offset:512
	buffer_load_dwordx4 v[56:59], v229, s[8:11], 0 offen offset:1024
	s_mov_b64 exec, s[66:67]
	buffer_load_dwordx4 v[116:119], v229, s[8:11], 0 offen offset:2048
	buffer_load_dwordx4 v[72:75], v229, s[8:11], 0 offen offset:2560
	s_mov_b64 exec, -1
	v_add_u32_e32 v228, 0x18000, v183
	buffer_load_dwordx4 v[176:179], v228, s[8:11], 0 offen
	v_add_u32_e32 v229, 0x30000, v183
	buffer_load_dwordx4 v[172:175], v229, s[8:11], 0 offen
	v_add_u32_e32 v228, 0x48000, v183
	buffer_load_dwordx4 v[168:171], v228, s[8:11], 0 offen
	v_add_u32_e32 v228, 0x2fc00, v183
	v_add_u32_e32 v229, 0x30000, v183
	v_add_u32_e32 v230, 0x47c00, v183
	v_add_u32_e32 v231, 0x48000, v183
	v_add_u32_e32 v232, 0x5fc00, v183
	v_add_u32_e32 v233, 0x60000, v183
	s_waitcnt lgkmcnt(0)
	v_cvt_f16_f32_e32 v186, s5
	v_cvt_f16_f32_e32 v188, s4
	v_cvt_f16_f32_e32 v187, s12
	s_waitcnt vmcnt(3)
	v_pk_mul_f16 v196, v188, v193 op_sel_hi:[0,1]
	v_pk_mul_f16 v200, v186, v193 op_sel_hi:[0,1]
	v_pk_mul_f16 v204, v187, v193 op_sel_hi:[0,1]
	v_pk_mul_f16 v189, v188, v190 op_sel_hi:[0,1]
	v_pk_mul_f16 v194, v188, v191 op_sel_hi:[0,1]
	v_pk_mul_f16 v195, v188, v192 op_sel_hi:[0,1]
	v_pk_mul_f16 v197, v186, v190 op_sel_hi:[0,1]
	s_mov_b64 exec, s[64:65]
	buffer_load_dwordx4 v[44:47], v228, s[8:11], 0 offen
	buffer_load_dwordx4 v[32:35], v228, s[8:11], 0 offen offset:512
	s_mov_b64 exec, -1
	v_pk_mul_f16 v198, v186, v191 op_sel_hi:[0,1]
	v_pk_mul_f16 v199, v186, v192 op_sel_hi:[0,1]
	v_pk_mul_f16 v201, v187, v190 op_sel_hi:[0,1]
	v_pk_mul_f16 v202, v187, v191 op_sel_hi:[0,1]
	v_pk_mul_f16 v203, v187, v192 op_sel_hi:[0,1]
	v_pk_fma_f16 v139, v139, v193, v196
	v_pk_fma_f16 v155, v155, v193, v200
	v_pk_fma_f16 v163, v163, v193, v204
	v_pk_fma_f16 v205, v115, v193, v196
	v_pk_fma_f16 v209, v135, v193, v200
	v_pk_fma_f16 v213, v151, v193, v204
	v_pk_fma_f16 v196, v79, v193, v196
	v_pk_fma_f16 v200, v95, v193, v200
	buffer_load_dwordx4 v[60:63], v229, s[8:11], 0 offen offset:512
	buffer_load_dwordx4 v[36:39], v229, s[8:11], 0 offen offset:1024
	v_pk_fma_f16 v193, v119, v193, v204
	v_pk_maximum3_f16 v204, v139, v155, v163
	v_pk_fma_f16 v138, v138, v192, v195
	v_pk_fma_f16 v137, v137, v191, v194
	v_pk_fma_f16 v136, v136, v190, v189
	v_pk_fma_f16 v154, v154, v192, v199
	v_pk_fma_f16 v153, v153, v191, v198
	v_pk_fma_f16 v152, v152, v190, v197
	v_pk_fma_f16 v162, v162, v192, v203
	v_pk_fma_f16 v161, v161, v191, v202
	v_pk_fma_f16 v160, v160, v190, v201
	v_pk_fma_f16 v206, v114, v192, v195
	v_pk_fma_f16 v207, v113, v191, v194
	v_pk_fma_f16 v208, v112, v190, v189
	v_pk_fma_f16 v210, v134, v192, v199
	v_pk_fma_f16 v211, v133, v191, v198
	s_mov_b64 exec, s[66:67]
	buffer_load_dwordx4 v[80:83], v229, s[8:11], 0 offen offset:2048
	buffer_load_dwordx4 v[40:43], v229, s[8:11], 0 offen offset:2560
	s_mov_b64 exec, -1
	v_pk_fma_f16 v212, v132, v190, v197
	v_pk_fma_f16 v214, v150, v192, v203
	v_pk_fma_f16 v215, v149, v191, v202
	v_pk_fma_f16 v216, v148, v190, v201
	v_pk_fma_f16 v195, v78, v192, v195
	v_pk_fma_f16 v194, v77, v191, v194
	v_pk_fma_f16 v189, v76, v190, v189
	v_pk_fma_f16 v199, v94, v192, v199
	v_pk_fma_f16 v198, v93, v191, v198
	v_pk_fma_f16 v197, v92, v190, v197
	v_pk_fma_f16 v192, v118, v192, v203
	v_pk_fma_f16 v191, v117, v191, v202
	v_pk_fma_f16 v190, v116, v190, v201
	v_pk_maximum3_f16 v201, v136, v152, v160
	v_pk_maximum3_f16 v202, v137, v153, v161
	v_pk_maximum3_f16 v203, v138, v154, v162
	v_pk_maximum3_f16 v220, v205, v209, v213
	v_pk_maximum3_f16 v224, v196, v200, v193
	v_pk_maximum3_f16 v217, v208, v212, v216
	v_pk_maximum3_f16 v218, v207, v211, v215
	v_pk_maximum3_f16 v219, v206, v210, v214
	v_pk_maximum3_f16 v221, v189, v197, v190
	v_pk_maximum3_f16 v222, v194, v198, v191
	v_pk_maximum3_f16 v204, v204, v220, v224
	v_pk_maximum3_f16 v223, v195, v199, v192
	v_pk_maximum3_f16 v201, v201, v217, v221
	v_pk_maximum3_f16 v202, v202, v218, v222
	v_pk_maximum3_f16 v203, v203, v219, v223
	v_pk_add_f16 v139, v139, v204 neg_lo:[0,1] neg_hi:[0,1]
	s_mov_b64 exec, s[64:65]
	buffer_load_dwordx4 v[100:103], v230, s[8:11], 0 offen
	buffer_load_dwordx4 v[52:55], v230, s[8:11], 0 offen offset:512
	s_mov_b64 exec, -1
	v_pk_add_f16 v136, v136, v201 neg_lo:[0,1] neg_hi:[0,1]
	v_pk_add_f16 v137, v137, v202 neg_lo:[0,1] neg_hi:[0,1]
	v_pk_add_f16 v138, v138, v203 neg_lo:[0,1] neg_hi:[0,1]
	v_pk_add_f16 v152, v152, v201 neg_lo:[0,1] neg_hi:[0,1]
	v_exp_f16_sdwa v217, v136 dst_sel:WORD_0 dst_unused:UNUSED_PAD src0_sel:WORD_0
	v_exp_f16_sdwa v218, v137 dst_sel:WORD_0 dst_unused:UNUSED_PAD src0_sel:WORD_0
	v_exp_f16_sdwa v219, v138 dst_sel:WORD_0 dst_unused:UNUSED_PAD src0_sel:WORD_0
	v_exp_f16_sdwa v220, v139 dst_sel:WORD_0 dst_unused:UNUSED_PAD src0_sel:WORD_0
	v_exp_f16_sdwa v217, v136 dst_sel:WORD_1 dst_unused:UNUSED_PRESERVE src0_sel:WORD_1
	v_exp_f16_sdwa v218, v137 dst_sel:WORD_1 dst_unused:UNUSED_PRESERVE src0_sel:WORD_1
	v_exp_f16_sdwa v219, v138 dst_sel:WORD_1 dst_unused:UNUSED_PRESERVE src0_sel:WORD_1
	v_exp_f16_sdwa v220, v139 dst_sel:WORD_1 dst_unused:UNUSED_PRESERVE src0_sel:WORD_1
	v_pk_add_f16 v153, v153, v202 neg_lo:[0,1] neg_hi:[0,1]
	v_pk_add_f16 v139, v217, 0
	v_pk_fma_f16 v99, v99, v220, 0
	v_pk_add_f16 v136, v220, 0
	v_pk_add_f16 v137, v219, 0
	v_pk_add_f16 v138, v218, 0
	v_pk_fma_f16 v98, v98, v219, 0
	v_pk_fma_f16 v97, v97, v218, 0
	v_pk_fma_f16 v96, v96, v217, 0
	v_pk_add_f16 v154, v154, v203 neg_lo:[0,1] neg_hi:[0,1]
	buffer_load_dwordx4 v[128:131], v231, s[8:11], 0 offen offset:512
	buffer_load_dwordx4 v[64:67], v231, s[8:11], 0 offen offset:1024
	v_pk_add_f16 v155, v155, v204 neg_lo:[0,1] neg_hi:[0,1]
	v_exp_f16_sdwa v217, v152 dst_sel:WORD_0 dst_unused:UNUSED_PAD src0_sel:WORD_0
	v_exp_f16_sdwa v218, v153 dst_sel:WORD_0 dst_unused:UNUSED_PAD src0_sel:WORD_0
	v_exp_f16_sdwa v219, v154 dst_sel:WORD_0 dst_unused:UNUSED_PAD src0_sel:WORD_0
	v_exp_f16_sdwa v220, v155 dst_sel:WORD_0 dst_unused:UNUSED_PAD src0_sel:WORD_0
	v_exp_f16_sdwa v217, v152 dst_sel:WORD_1 dst_unused:UNUSED_PRESERVE src0_sel:WORD_1
	v_exp_f16_sdwa v218, v153 dst_sel:WORD_1 dst_unused:UNUSED_PRESERVE src0_sel:WORD_1
	v_exp_f16_sdwa v219, v154 dst_sel:WORD_1 dst_unused:UNUSED_PRESERVE src0_sel:WORD_1
	v_exp_f16_sdwa v220, v155 dst_sel:WORD_1 dst_unused:UNUSED_PRESERVE src0_sel:WORD_1
	v_pk_add_f16 v139, v139, v217
	v_pk_fma_f16 v99, v127, v220, v99
	v_pk_add_f16 v127, v163, v204 neg_lo:[0,1] neg_hi:[0,1]
	v_pk_add_f16 v138, v138, v218
	v_pk_add_f16 v137, v137, v219
	v_pk_add_f16 v136, v136, v220
	v_pk_fma_f16 v96, v124, v217, v96
	v_pk_fma_f16 v97, v125, v218, v97
	v_pk_fma_f16 v98, v126, v219, v98
	v_pk_add_f16 v124, v160, v201 neg_lo:[0,1] neg_hi:[0,1]
	v_pk_add_f16 v125, v161, v202 neg_lo:[0,1] neg_hi:[0,1]
	v_pk_add_f16 v126, v162, v203 neg_lo:[0,1] neg_hi:[0,1]
	v_exp_f16_sdwa v152, v124 dst_sel:WORD_0 dst_unused:UNUSED_PAD src0_sel:WORD_0
	v_exp_f16_sdwa v153, v125 dst_sel:WORD_0 dst_unused:UNUSED_PAD src0_sel:WORD_0
	v_exp_f16_sdwa v154, v126 dst_sel:WORD_0 dst_unused:UNUSED_PAD src0_sel:WORD_0
	v_exp_f16_sdwa v155, v127 dst_sel:WORD_0 dst_unused:UNUSED_PAD src0_sel:WORD_0
	v_exp_f16_sdwa v152, v124 dst_sel:WORD_1 dst_unused:UNUSED_PRESERVE src0_sel:WORD_1
	v_exp_f16_sdwa v153, v125 dst_sel:WORD_1 dst_unused:UNUSED_PRESERVE src0_sel:WORD_1
	v_exp_f16_sdwa v154, v126 dst_sel:WORD_1 dst_unused:UNUSED_PRESERVE src0_sel:WORD_1
	v_exp_f16_sdwa v155, v127 dst_sel:WORD_1 dst_unused:UNUSED_PRESERVE src0_sel:WORD_1
	v_pk_add_f16 v127, v139, v152
	v_pk_add_f16 v124, v136, v155
	s_mov_b64 exec, s[66:67]
	buffer_load_dwordx4 v[144:147], v231, s[8:11], 0 offen offset:2048
	buffer_load_dwordx4 v[84:87], v231, s[8:11], 0 offen offset:2560
	s_mov_b64 exec, -1
	v_pk_add_f16 v125, v137, v154
	v_pk_add_f16 v126, v138, v153
	v_pk_fma_f16 v99, v143, v155, v99
	v_pk_fma_f16 v98, v142, v154, v98
	v_pk_fma_f16 v97, v141, v153, v97
	v_pk_fma_f16 v96, v140, v152, v96
	v_pk_add_f16 v136, v208, v201 neg_lo:[0,1] neg_hi:[0,1]
	v_pk_add_f16 v137, v207, v202 neg_lo:[0,1] neg_hi:[0,1]
	v_pk_add_f16 v138, v206, v203 neg_lo:[0,1] neg_hi:[0,1]
	v_pk_add_f16 v139, v205, v204 neg_lo:[0,1] neg_hi:[0,1]
	v_exp_f16_sdwa v140, v136 dst_sel:WORD_0 dst_unused:UNUSED_PAD src0_sel:WORD_0
	v_exp_f16_sdwa v141, v137 dst_sel:WORD_0 dst_unused:UNUSED_PAD src0_sel:WORD_0
	v_exp_f16_sdwa v142, v138 dst_sel:WORD_0 dst_unused:UNUSED_PAD src0_sel:WORD_0
	v_exp_f16_sdwa v143, v139 dst_sel:WORD_0 dst_unused:UNUSED_PAD src0_sel:WORD_0
	v_exp_f16_sdwa v140, v136 dst_sel:WORD_1 dst_unused:UNUSED_PRESERVE src0_sel:WORD_1
	v_exp_f16_sdwa v141, v137 dst_sel:WORD_1 dst_unused:UNUSED_PRESERVE src0_sel:WORD_1
	v_exp_f16_sdwa v142, v138 dst_sel:WORD_1 dst_unused:UNUSED_PRESERVE src0_sel:WORD_1
	v_exp_f16_sdwa v143, v139 dst_sel:WORD_1 dst_unused:UNUSED_PRESERVE src0_sel:WORD_1
	v_pk_add_f16 v136, v212, v201 neg_lo:[0,1] neg_hi:[0,1]
	v_pk_add_f16 v127, v127, v140
	v_pk_add_f16 v126, v126, v141
	v_pk_add_f16 v125, v125, v142
	s_mov_b64 exec, s[76:77]
	buffer_load_dwordx4 v[156:159], v232, s[8:11], 0 offen
	buffer_load_dwordx4 v[104:107], v232, s[8:11], 0 offen offset:512
	s_mov_b64 exec, -1
	v_pk_add_f16 v124, v124, v143
	v_pk_fma_f16 v96, v68, v140, v96
	v_pk_fma_f16 v97, v69, v141, v97
	v_pk_fma_f16 v98, v70, v142, v98
	v_pk_fma_f16 v99, v71, v143, v99
	v_pk_add_f16 v137, v211, v202 neg_lo:[0,1] neg_hi:[0,1]
	v_pk_add_f16 v138, v210, v203 neg_lo:[0,1] neg_hi:[0,1]
	v_pk_add_f16 v139, v209, v204 neg_lo:[0,1] neg_hi:[0,1]
	v_exp_f16_sdwa v140, v136 dst_sel:WORD_0 dst_unused:UNUSED_PAD src0_sel:WORD_0
	v_exp_f16_sdwa v141, v137 dst_sel:WORD_0 dst_unused:UNUSED_PAD src0_sel:WORD_0
	v_exp_f16_sdwa v142, v138 dst_sel:WORD_0 dst_unused:UNUSED_PAD src0_sel:WORD_0
	v_exp_f16_sdwa v143, v139 dst_sel:WORD_0 dst_unused:UNUSED_PAD src0_sel:WORD_0
	v_exp_f16_sdwa v140, v136 dst_sel:WORD_1 dst_unused:UNUSED_PRESERVE src0_sel:WORD_1
	v_exp_f16_sdwa v141, v137 dst_sel:WORD_1 dst_unused:UNUSED_PRESERVE src0_sel:WORD_1
	v_exp_f16_sdwa v142, v138 dst_sel:WORD_1 dst_unused:UNUSED_PRESERVE src0_sel:WORD_1
	v_exp_f16_sdwa v143, v139 dst_sel:WORD_1 dst_unused:UNUSED_PRESERVE src0_sel:WORD_1
	v_pk_add_f16 v136, v216, v201 neg_lo:[0,1] neg_hi:[0,1]
	v_pk_add_f16 v127, v127, v140
	v_pk_add_f16 v124, v124, v143
	v_pk_add_f16 v125, v125, v142
	v_pk_add_f16 v126, v126, v141
	v_pk_fma_f16 v99, v91, v143, v99
	v_pk_fma_f16 v98, v90, v142, v98
	s_mov_b64 exec, s[70:71]
	buffer_load_dwordx4 v[164:167], v233, s[8:11], 0 offen offset:512
	buffer_load_dwordx4 v[120:123], v233, s[8:11], 0 offen offset:1024
	s_mov_b64 exec, -1
	v_pk_fma_f16 v97, v89, v141, v97
	v_pk_fma_f16 v96, v88, v140, v96
	v_pk_add_f16 v137, v215, v202 neg_lo:[0,1] neg_hi:[0,1]
	v_pk_add_f16 v138, v214, v203 neg_lo:[0,1] neg_hi:[0,1]
	v_pk_add_f16 v139, v213, v204 neg_lo:[0,1] neg_hi:[0,1]
	v_exp_f16_sdwa v140, v136 dst_sel:WORD_0 dst_unused:UNUSED_PAD src0_sel:WORD_0
	v_exp_f16_sdwa v141, v137 dst_sel:WORD_0 dst_unused:UNUSED_PAD src0_sel:WORD_0
	v_exp_f16_sdwa v142, v138 dst_sel:WORD_0 dst_unused:UNUSED_PAD src0_sel:WORD_0
	v_exp_f16_sdwa v143, v139 dst_sel:WORD_0 dst_unused:UNUSED_PAD src0_sel:WORD_0
	v_exp_f16_sdwa v140, v136 dst_sel:WORD_1 dst_unused:UNUSED_PRESERVE src0_sel:WORD_1
	v_exp_f16_sdwa v141, v137 dst_sel:WORD_1 dst_unused:UNUSED_PRESERVE src0_sel:WORD_1
	v_exp_f16_sdwa v142, v138 dst_sel:WORD_1 dst_unused:UNUSED_PRESERVE src0_sel:WORD_1
	v_exp_f16_sdwa v143, v139 dst_sel:WORD_1 dst_unused:UNUSED_PRESERVE src0_sel:WORD_1
	v_pk_add_f16 v136, v189, v201 neg_lo:[0,1] neg_hi:[0,1]
	v_pk_add_f16 v127, v127, v140
	v_pk_add_f16 v126, v126, v141
	v_pk_add_f16 v125, v125, v142
	v_pk_add_f16 v124, v124, v143
	v_pk_fma_f16 v96, v108, v140, v96
	v_pk_fma_f16 v97, v109, v141, v97
	v_pk_fma_f16 v98, v110, v142, v98
	v_pk_fma_f16 v99, v111, v143, v99
	s_mov_b64 exec, s[78:79]
	buffer_load_dwordx4 v[28:31], v233, s[8:11], 0 offen offset:2048
	buffer_load_dwordx4 v[24:27], v233, s[8:11], 0 offen offset:2560
	s_mov_b64 exec, -1
	v_pk_add_f16 v137, v194, v202 neg_lo:[0,1] neg_hi:[0,1]
	v_pk_add_f16 v138, v195, v203 neg_lo:[0,1] neg_hi:[0,1]
	v_pk_add_f16 v139, v196, v204 neg_lo:[0,1] neg_hi:[0,1]
	v_exp_f16_sdwa v140, v136 dst_sel:WORD_0 dst_unused:UNUSED_PAD src0_sel:WORD_0
	v_exp_f16_sdwa v141, v137 dst_sel:WORD_0 dst_unused:UNUSED_PAD src0_sel:WORD_0
	v_exp_f16_sdwa v142, v138 dst_sel:WORD_0 dst_unused:UNUSED_PAD src0_sel:WORD_0
	v_exp_f16_sdwa v143, v139 dst_sel:WORD_0 dst_unused:UNUSED_PAD src0_sel:WORD_0
	v_exp_f16_sdwa v140, v136 dst_sel:WORD_1 dst_unused:UNUSED_PRESERVE src0_sel:WORD_1
	v_exp_f16_sdwa v141, v137 dst_sel:WORD_1 dst_unused:UNUSED_PRESERVE src0_sel:WORD_1
	v_exp_f16_sdwa v142, v138 dst_sel:WORD_1 dst_unused:UNUSED_PRESERVE src0_sel:WORD_1
	v_exp_f16_sdwa v143, v139 dst_sel:WORD_1 dst_unused:UNUSED_PRESERVE src0_sel:WORD_1
	v_pk_add_f16 v136, v197, v201 neg_lo:[0,1] neg_hi:[0,1]
	v_pk_add_f16 v127, v127, v140
	v_pk_add_f16 v124, v124, v143
	v_pk_add_f16 v125, v125, v142
	v_pk_add_f16 v126, v126, v141
	v_pk_fma_f16 v99, v51, v143, v99
	v_pk_fma_f16 v98, v50, v142, v98
	v_pk_fma_f16 v97, v49, v141, v97
	v_pk_fma_f16 v96, v48, v140, v96
	v_pk_add_f16 v137, v198, v202 neg_lo:[0,1] neg_hi:[0,1]
	v_pk_add_f16 v138, v199, v203 neg_lo:[0,1] neg_hi:[0,1]
	v_pk_add_f16 v139, v200, v204 neg_lo:[0,1] neg_hi:[0,1]
	v_exp_f16_sdwa v140, v136 dst_sel:WORD_0 dst_unused:UNUSED_PAD src0_sel:WORD_0
	v_exp_f16_sdwa v141, v137 dst_sel:WORD_0 dst_unused:UNUSED_PAD src0_sel:WORD_0
	v_exp_f16_sdwa v142, v138 dst_sel:WORD_0 dst_unused:UNUSED_PAD src0_sel:WORD_0
	v_exp_f16_sdwa v143, v139 dst_sel:WORD_0 dst_unused:UNUSED_PAD src0_sel:WORD_0
	v_exp_f16_sdwa v140, v136 dst_sel:WORD_1 dst_unused:UNUSED_PRESERVE src0_sel:WORD_1
	v_exp_f16_sdwa v141, v137 dst_sel:WORD_1 dst_unused:UNUSED_PRESERVE src0_sel:WORD_1
	v_exp_f16_sdwa v142, v138 dst_sel:WORD_1 dst_unused:UNUSED_PRESERVE src0_sel:WORD_1
	v_exp_f16_sdwa v143, v139 dst_sel:WORD_1 dst_unused:UNUSED_PRESERVE src0_sel:WORD_1
	v_pk_add_f16 v136, v190, v201 neg_lo:[0,1] neg_hi:[0,1]
	v_pk_add_f16 v127, v127, v140
	v_pk_add_f16 v126, v126, v141
	v_pk_add_f16 v125, v125, v142
	v_pk_add_f16 v124, v124, v143
	v_pk_fma_f16 v96, v56, v140, v96
	v_pk_fma_f16 v97, v57, v141, v97
	v_pk_fma_f16 v98, v58, v142, v98
	v_pk_fma_f16 v99, v59, v143, v99
	v_pk_add_f16 v137, v191, v202 neg_lo:[0,1] neg_hi:[0,1]
	v_pk_add_f16 v138, v192, v203 neg_lo:[0,1] neg_hi:[0,1]
	v_pk_add_f16 v139, v193, v204 neg_lo:[0,1] neg_hi:[0,1]
	v_exp_f16_sdwa v140, v136 dst_sel:WORD_0 dst_unused:UNUSED_PAD src0_sel:WORD_0
	v_exp_f16_sdwa v141, v137 dst_sel:WORD_0 dst_unused:UNUSED_PAD src0_sel:WORD_0
	v_exp_f16_sdwa v142, v138 dst_sel:WORD_0 dst_unused:UNUSED_PAD src0_sel:WORD_0
	v_exp_f16_sdwa v143, v139 dst_sel:WORD_0 dst_unused:UNUSED_PAD src0_sel:WORD_0
	v_exp_f16_sdwa v140, v136 dst_sel:WORD_1 dst_unused:UNUSED_PRESERVE src0_sel:WORD_1
	v_exp_f16_sdwa v141, v137 dst_sel:WORD_1 dst_unused:UNUSED_PRESERVE src0_sel:WORD_1
	v_exp_f16_sdwa v142, v138 dst_sel:WORD_1 dst_unused:UNUSED_PRESERVE src0_sel:WORD_1
	v_exp_f16_sdwa v143, v139 dst_sel:WORD_1 dst_unused:UNUSED_PRESERVE src0_sel:WORD_1
	v_pk_add_f16 v127, v127, v140
	v_pk_add_f16 v126, v126, v141
	v_rcp_f16_e32 v136, v127
	v_rcp_f16_sdwa v127, v127 dst_sel:DWORD dst_unused:UNUSED_PAD src0_sel:WORD_1
	v_pk_add_f16 v125, v125, v142
	v_rcp_f16_e32 v137, v126
	v_rcp_f16_sdwa v126, v126 dst_sel:DWORD dst_unused:UNUSED_PAD src0_sel:WORD_1
	v_pk_add_f16 v124, v124, v143
	v_rcp_f16_e32 v138, v125
	v_rcp_f16_sdwa v139, v125 dst_sel:DWORD dst_unused:UNUSED_PAD src0_sel:WORD_1
	v_pk_fma_f16 v97, v73, v141, v97
	v_pk_fma_f16 v96, v72, v140, v96
	v_rcp_f16_e32 v140, v124
	v_rcp_f16_sdwa v141, v124 dst_sel:DWORD dst_unused:UNUSED_PAD src0_sel:WORD_1
	v_pack_b32_f16 v124, v136, v127
	v_pk_mul_f16 v124, v96, v124
	v_pack_b32_f16 v96, v137, v126
	v_pk_fma_f16 v98, v74, v142, v98
	v_pk_mul_f16 v125, v97, v96
	v_pack_b32_f16 v96, v138, v139
	v_pk_fma_f16 v99, v75, v143, v99
	v_pk_mul_f16 v126, v98, v96
	v_pack_b32_f16 v96, v140, v141
	v_pk_mul_f16 v127, v99, v96
	s_waitcnt vmcnt(12)
	v_pk_mul_f16 v99, v188, v179 op_sel_hi:[0,1]
	v_pk_mul_f16 v139, v186, v179 op_sel_hi:[0,1]
	v_pk_mul_f16 v143, v187, v179 op_sel_hi:[0,1]
	v_pk_mul_f16 v96, v188, v176 op_sel_hi:[0,1]
	v_pk_mul_f16 v97, v188, v177 op_sel_hi:[0,1]
	v_pk_mul_f16 v98, v188, v178 op_sel_hi:[0,1]
	v_pk_mul_f16 v136, v186, v176 op_sel_hi:[0,1]
	v_pk_mul_f16 v137, v186, v177 op_sel_hi:[0,1]
	v_pk_mul_f16 v138, v186, v178 op_sel_hi:[0,1]
	v_pk_mul_f16 v140, v187, v176 op_sel_hi:[0,1]
	v_pk_mul_f16 v141, v187, v177 op_sel_hi:[0,1]
	v_pk_mul_f16 v142, v187, v178 op_sel_hi:[0,1]
	v_pk_fma_f16 v115, v115, v179, v99
	v_pk_fma_f16 v135, v135, v179, v139
	v_pk_fma_f16 v151, v151, v179, v143
	v_pk_fma_f16 v152, v79, v179, v99
	v_pk_fma_f16 v160, v95, v179, v139
	v_pk_fma_f16 v189, v119, v179, v143
	v_pk_fma_f16 v99, v47, v179, v99
	v_pk_fma_f16 v139, v63, v179, v139
	v_pk_fma_f16 v143, v83, v179, v143
	v_pk_maximum3_f16 v179, v115, v135, v151
	v_pk_fma_f16 v114, v114, v178, v98
	v_pk_fma_f16 v113, v113, v177, v97
	v_pk_fma_f16 v112, v112, v176, v96
	v_pk_fma_f16 v134, v134, v178, v138
	v_pk_fma_f16 v133, v133, v177, v137
	v_pk_fma_f16 v132, v132, v176, v136
	v_pk_fma_f16 v150, v150, v178, v142
	v_pk_fma_f16 v149, v149, v177, v141
	v_pk_fma_f16 v148, v148, v176, v140
	v_pk_fma_f16 v153, v78, v178, v98
	v_pk_fma_f16 v154, v77, v177, v97
	v_pk_fma_f16 v155, v76, v176, v96
	v_pk_fma_f16 v161, v94, v178, v138
	v_pk_fma_f16 v162, v93, v177, v137
	v_pk_fma_f16 v163, v92, v176, v136
	v_pk_fma_f16 v190, v118, v178, v142
	v_pk_fma_f16 v191, v117, v177, v141
	v_pk_fma_f16 v192, v116, v176, v140
	v_pk_fma_f16 v98, v46, v178, v98
	v_pk_fma_f16 v97, v45, v177, v97
	v_pk_fma_f16 v96, v44, v176, v96
	v_pk_fma_f16 v138, v62, v178, v138
	v_pk_fma_f16 v137, v61, v177, v137
	v_pk_fma_f16 v136, v60, v176, v136
	v_pk_fma_f16 v142, v82, v178, v142
	v_pk_fma_f16 v141, v81, v177, v141
	v_pk_fma_f16 v140, v80, v176, v140
	v_pk_maximum3_f16 v176, v112, v132, v148
	v_pk_maximum3_f16 v177, v113, v133, v149
	v_pk_maximum3_f16 v178, v114, v134, v150
	v_pk_maximum3_f16 v196, v152, v160, v189
	v_pk_maximum3_f16 v200, v99, v139, v143
	v_pk_maximum3_f16 v193, v155, v163, v192
	v_pk_maximum3_f16 v194, v154, v162, v191
	v_pk_maximum3_f16 v195, v153, v161, v190
	v_pk_maximum3_f16 v197, v96, v136, v140
	v_pk_maximum3_f16 v198, v97, v137, v141
	v_pk_maximum3_f16 v179, v179, v196, v200
	v_pk_maximum3_f16 v199, v98, v138, v142
	v_pk_maximum3_f16 v176, v176, v193, v197
	v_pk_maximum3_f16 v177, v177, v194, v198
	v_pk_maximum3_f16 v178, v178, v195, v199
	v_pk_add_f16 v115, v115, v179 neg_lo:[0,1] neg_hi:[0,1]
	v_pk_add_f16 v112, v112, v176 neg_lo:[0,1] neg_hi:[0,1]
	v_pk_add_f16 v113, v113, v177 neg_lo:[0,1] neg_hi:[0,1]
	v_pk_add_f16 v114, v114, v178 neg_lo:[0,1] neg_hi:[0,1]
	v_pk_add_f16 v132, v132, v176 neg_lo:[0,1] neg_hi:[0,1]
	v_exp_f16_sdwa v193, v112 dst_sel:WORD_0 dst_unused:UNUSED_PAD src0_sel:WORD_0
	v_exp_f16_sdwa v194, v113 dst_sel:WORD_0 dst_unused:UNUSED_PAD src0_sel:WORD_0
	v_exp_f16_sdwa v195, v114 dst_sel:WORD_0 dst_unused:UNUSED_PAD src0_sel:WORD_0
	v_exp_f16_sdwa v196, v115 dst_sel:WORD_0 dst_unused:UNUSED_PAD src0_sel:WORD_0
	v_exp_f16_sdwa v193, v112 dst_sel:WORD_1 dst_unused:UNUSED_PRESERVE src0_sel:WORD_1
	v_exp_f16_sdwa v194, v113 dst_sel:WORD_1 dst_unused:UNUSED_PRESERVE src0_sel:WORD_1
	v_exp_f16_sdwa v195, v114 dst_sel:WORD_1 dst_unused:UNUSED_PRESERVE src0_sel:WORD_1
	v_exp_f16_sdwa v196, v115 dst_sel:WORD_1 dst_unused:UNUSED_PRESERVE src0_sel:WORD_1
	v_pk_add_f16 v133, v133, v177 neg_lo:[0,1] neg_hi:[0,1]
	v_pk_add_f16 v115, v193, 0
	v_pk_fma_f16 v71, v71, v196, 0
	v_pk_add_f16 v112, v196, 0
	v_pk_add_f16 v113, v195, 0
	v_pk_add_f16 v114, v194, 0
	v_pk_fma_f16 v70, v70, v195, 0
	v_pk_fma_f16 v69, v69, v194, 0
	v_pk_fma_f16 v68, v68, v193, 0
	v_pk_add_f16 v134, v134, v178 neg_lo:[0,1] neg_hi:[0,1]
	v_pk_add_f16 v135, v135, v179 neg_lo:[0,1] neg_hi:[0,1]
	v_pk_add_f16 v96, v96, v176 neg_lo:[0,1] neg_hi:[0,1]
	v_exp_f16_sdwa v193, v132 dst_sel:WORD_0 dst_unused:UNUSED_PAD src0_sel:WORD_0
	v_exp_f16_sdwa v194, v133 dst_sel:WORD_0 dst_unused:UNUSED_PAD src0_sel:WORD_0
	v_exp_f16_sdwa v195, v134 dst_sel:WORD_0 dst_unused:UNUSED_PAD src0_sel:WORD_0
	v_exp_f16_sdwa v196, v135 dst_sel:WORD_0 dst_unused:UNUSED_PAD src0_sel:WORD_0
	v_exp_f16_sdwa v193, v132 dst_sel:WORD_1 dst_unused:UNUSED_PRESERVE src0_sel:WORD_1
	v_exp_f16_sdwa v194, v133 dst_sel:WORD_1 dst_unused:UNUSED_PRESERVE src0_sel:WORD_1
	v_exp_f16_sdwa v195, v134 dst_sel:WORD_1 dst_unused:UNUSED_PRESERVE src0_sel:WORD_1
	v_exp_f16_sdwa v196, v135 dst_sel:WORD_1 dst_unused:UNUSED_PRESERVE src0_sel:WORD_1
	v_pk_add_f16 v97, v97, v177 neg_lo:[0,1] neg_hi:[0,1]
	v_pk_add_f16 v115, v115, v193
	v_pk_fma_f16 v71, v91, v196, v71
	v_pk_add_f16 v91, v151, v179 neg_lo:[0,1] neg_hi:[0,1]
	v_pk_add_f16 v114, v114, v194
	v_pk_add_f16 v113, v113, v195
	v_pk_add_f16 v112, v112, v196
	v_pk_fma_f16 v68, v88, v193, v68
	v_pk_fma_f16 v69, v89, v194, v69
	v_pk_fma_f16 v70, v90, v195, v70
	v_pk_add_f16 v88, v148, v176 neg_lo:[0,1] neg_hi:[0,1]
	v_pk_add_f16 v89, v149, v177 neg_lo:[0,1] neg_hi:[0,1]
	v_pk_add_f16 v90, v150, v178 neg_lo:[0,1] neg_hi:[0,1]
	v_pk_add_f16 v98, v98, v178 neg_lo:[0,1] neg_hi:[0,1]
	v_exp_f16_sdwa v132, v88 dst_sel:WORD_0 dst_unused:UNUSED_PAD src0_sel:WORD_0
	v_exp_f16_sdwa v133, v89 dst_sel:WORD_0 dst_unused:UNUSED_PAD src0_sel:WORD_0
	v_exp_f16_sdwa v134, v90 dst_sel:WORD_0 dst_unused:UNUSED_PAD src0_sel:WORD_0
	v_exp_f16_sdwa v135, v91 dst_sel:WORD_0 dst_unused:UNUSED_PAD src0_sel:WORD_0
	v_exp_f16_sdwa v132, v88 dst_sel:WORD_1 dst_unused:UNUSED_PRESERVE src0_sel:WORD_1
	v_exp_f16_sdwa v133, v89 dst_sel:WORD_1 dst_unused:UNUSED_PRESERVE src0_sel:WORD_1
	v_exp_f16_sdwa v134, v90 dst_sel:WORD_1 dst_unused:UNUSED_PRESERVE src0_sel:WORD_1
	v_exp_f16_sdwa v135, v91 dst_sel:WORD_1 dst_unused:UNUSED_PRESERVE src0_sel:WORD_1
	v_pk_add_f16 v99, v99, v179 neg_lo:[0,1] neg_hi:[0,1]
	v_pk_add_f16 v91, v115, v132
	v_pk_add_f16 v88, v112, v135
	v_pk_add_f16 v89, v113, v134
	v_pk_add_f16 v90, v114, v133
	v_pk_fma_f16 v71, v111, v135, v71
	v_pk_fma_f16 v70, v110, v134, v70
	v_pk_fma_f16 v69, v109, v133, v69
	v_pk_fma_f16 v68, v108, v132, v68
	v_pk_add_f16 v108, v155, v176 neg_lo:[0,1] neg_hi:[0,1]
	v_pk_add_f16 v109, v154, v177 neg_lo:[0,1] neg_hi:[0,1]
	v_pk_add_f16 v110, v153, v178 neg_lo:[0,1] neg_hi:[0,1]
	v_pk_add_f16 v111, v152, v179 neg_lo:[0,1] neg_hi:[0,1]
	v_exp_f16_sdwa v112, v108 dst_sel:WORD_0 dst_unused:UNUSED_PAD src0_sel:WORD_0
	v_exp_f16_sdwa v113, v109 dst_sel:WORD_0 dst_unused:UNUSED_PAD src0_sel:WORD_0
	v_exp_f16_sdwa v114, v110 dst_sel:WORD_0 dst_unused:UNUSED_PAD src0_sel:WORD_0
	v_exp_f16_sdwa v115, v111 dst_sel:WORD_0 dst_unused:UNUSED_PAD src0_sel:WORD_0
	v_exp_f16_sdwa v112, v108 dst_sel:WORD_1 dst_unused:UNUSED_PRESERVE src0_sel:WORD_1
	v_exp_f16_sdwa v113, v109 dst_sel:WORD_1 dst_unused:UNUSED_PRESERVE src0_sel:WORD_1
	v_exp_f16_sdwa v114, v110 dst_sel:WORD_1 dst_unused:UNUSED_PRESERVE src0_sel:WORD_1
	v_exp_f16_sdwa v115, v111 dst_sel:WORD_1 dst_unused:UNUSED_PRESERVE src0_sel:WORD_1
	v_pk_add_f16 v108, v163, v176 neg_lo:[0,1] neg_hi:[0,1]
	v_pk_add_f16 v91, v91, v112
	v_pk_add_f16 v90, v90, v113
	v_pk_add_f16 v89, v89, v114
	v_pk_add_f16 v88, v88, v115
	v_pk_fma_f16 v68, v48, v112, v68
	v_pk_fma_f16 v69, v49, v113, v69
	v_pk_fma_f16 v70, v50, v114, v70
	v_pk_fma_f16 v71, v51, v115, v71
	v_pk_add_f16 v109, v162, v177 neg_lo:[0,1] neg_hi:[0,1]
	v_pk_add_f16 v110, v161, v178 neg_lo:[0,1] neg_hi:[0,1]
	v_pk_add_f16 v111, v160, v179 neg_lo:[0,1] neg_hi:[0,1]
	v_exp_f16_sdwa v112, v108 dst_sel:WORD_0 dst_unused:UNUSED_PAD src0_sel:WORD_0
	v_exp_f16_sdwa v113, v109 dst_sel:WORD_0 dst_unused:UNUSED_PAD src0_sel:WORD_0
	v_exp_f16_sdwa v114, v110 dst_sel:WORD_0 dst_unused:UNUSED_PAD src0_sel:WORD_0
	v_exp_f16_sdwa v115, v111 dst_sel:WORD_0 dst_unused:UNUSED_PAD src0_sel:WORD_0
	v_exp_f16_sdwa v112, v108 dst_sel:WORD_1 dst_unused:UNUSED_PRESERVE src0_sel:WORD_1
	v_exp_f16_sdwa v113, v109 dst_sel:WORD_1 dst_unused:UNUSED_PRESERVE src0_sel:WORD_1
	v_exp_f16_sdwa v114, v110 dst_sel:WORD_1 dst_unused:UNUSED_PRESERVE src0_sel:WORD_1
	v_exp_f16_sdwa v115, v111 dst_sel:WORD_1 dst_unused:UNUSED_PRESERVE src0_sel:WORD_1
	v_pk_add_f16 v108, v192, v176 neg_lo:[0,1] neg_hi:[0,1]
	v_pk_add_f16 v91, v91, v112
	v_pk_add_f16 v88, v88, v115
	v_pk_add_f16 v89, v89, v114
	v_pk_add_f16 v90, v90, v113
	v_pk_fma_f16 v71, v59, v115, v71
	v_pk_fma_f16 v70, v58, v114, v70
	v_pk_fma_f16 v69, v57, v113, v69
	v_pk_fma_f16 v68, v56, v112, v68
	v_pk_add_f16 v109, v191, v177 neg_lo:[0,1] neg_hi:[0,1]
	v_pk_add_f16 v110, v190, v178 neg_lo:[0,1] neg_hi:[0,1]
	v_pk_add_f16 v111, v189, v179 neg_lo:[0,1] neg_hi:[0,1]
	v_exp_f16_sdwa v112, v108 dst_sel:WORD_0 dst_unused:UNUSED_PAD src0_sel:WORD_0
	v_exp_f16_sdwa v113, v109 dst_sel:WORD_0 dst_unused:UNUSED_PAD src0_sel:WORD_0
	v_exp_f16_sdwa v114, v110 dst_sel:WORD_0 dst_unused:UNUSED_PAD src0_sel:WORD_0
	v_exp_f16_sdwa v115, v111 dst_sel:WORD_0 dst_unused:UNUSED_PAD src0_sel:WORD_0
	v_exp_f16_sdwa v112, v108 dst_sel:WORD_1 dst_unused:UNUSED_PRESERVE src0_sel:WORD_1
	v_exp_f16_sdwa v113, v109 dst_sel:WORD_1 dst_unused:UNUSED_PRESERVE src0_sel:WORD_1
	v_exp_f16_sdwa v114, v110 dst_sel:WORD_1 dst_unused:UNUSED_PRESERVE src0_sel:WORD_1
	v_exp_f16_sdwa v115, v111 dst_sel:WORD_1 dst_unused:UNUSED_PRESERVE src0_sel:WORD_1
	v_exp_f16_sdwa v108, v96 dst_sel:WORD_0 dst_unused:UNUSED_PAD src0_sel:WORD_0
	v_exp_f16_sdwa v109, v97 dst_sel:WORD_0 dst_unused:UNUSED_PAD src0_sel:WORD_0
	v_exp_f16_sdwa v110, v98 dst_sel:WORD_0 dst_unused:UNUSED_PAD src0_sel:WORD_0
	v_exp_f16_sdwa v111, v99 dst_sel:WORD_0 dst_unused:UNUSED_PAD src0_sel:WORD_0
	v_exp_f16_sdwa v108, v96 dst_sel:WORD_1 dst_unused:UNUSED_PRESERVE src0_sel:WORD_1
	v_exp_f16_sdwa v109, v97 dst_sel:WORD_1 dst_unused:UNUSED_PRESERVE src0_sel:WORD_1
	v_exp_f16_sdwa v110, v98 dst_sel:WORD_1 dst_unused:UNUSED_PRESERVE src0_sel:WORD_1
	v_exp_f16_sdwa v111, v99 dst_sel:WORD_1 dst_unused:UNUSED_PRESERVE src0_sel:WORD_1
	v_pk_add_f16 v96, v136, v176 neg_lo:[0,1] neg_hi:[0,1]
	v_pk_add_f16 v91, v91, v112
	v_pk_add_f16 v90, v90, v113
	v_pk_add_f16 v89, v89, v114
	v_pk_add_f16 v88, v88, v115
	v_pk_fma_f16 v68, v72, v112, v68
	v_pk_fma_f16 v69, v73, v113, v69
	v_pk_fma_f16 v70, v74, v114, v70
	v_pk_fma_f16 v71, v75, v115, v71
	v_pk_add_f16 v91, v91, v108
	v_pk_add_f16 v88, v88, v111
	v_pk_add_f16 v89, v89, v110
	v_pk_add_f16 v90, v90, v109
	v_pk_fma_f16 v71, v35, v111, v71
	v_pk_fma_f16 v70, v34, v110, v70
	v_pk_fma_f16 v69, v33, v109, v69
	v_pk_fma_f16 v68, v32, v108, v68
	v_pk_add_f16 v97, v137, v177 neg_lo:[0,1] neg_hi:[0,1]
	v_pk_add_f16 v98, v138, v178 neg_lo:[0,1] neg_hi:[0,1]
	v_pk_add_f16 v99, v139, v179 neg_lo:[0,1] neg_hi:[0,1]
	v_exp_f16_sdwa v108, v96 dst_sel:WORD_0 dst_unused:UNUSED_PAD src0_sel:WORD_0
	v_exp_f16_sdwa v109, v97 dst_sel:WORD_0 dst_unused:UNUSED_PAD src0_sel:WORD_0
	v_exp_f16_sdwa v110, v98 dst_sel:WORD_0 dst_unused:UNUSED_PAD src0_sel:WORD_0
	v_exp_f16_sdwa v111, v99 dst_sel:WORD_0 dst_unused:UNUSED_PAD src0_sel:WORD_0
	v_exp_f16_sdwa v108, v96 dst_sel:WORD_1 dst_unused:UNUSED_PRESERVE src0_sel:WORD_1
	v_exp_f16_sdwa v109, v97 dst_sel:WORD_1 dst_unused:UNUSED_PRESERVE src0_sel:WORD_1
	v_exp_f16_sdwa v110, v98 dst_sel:WORD_1 dst_unused:UNUSED_PRESERVE src0_sel:WORD_1
	v_exp_f16_sdwa v111, v99 dst_sel:WORD_1 dst_unused:UNUSED_PRESERVE src0_sel:WORD_1
	v_pk_add_f16 v96, v140, v176 neg_lo:[0,1] neg_hi:[0,1]
	v_pk_add_f16 v91, v91, v108
	v_pk_add_f16 v90, v90, v109
	v_pk_add_f16 v89, v89, v110
	v_pk_add_f16 v88, v88, v111
	v_pk_fma_f16 v68, v36, v108, v68
	v_pk_fma_f16 v69, v37, v109, v69
	v_pk_fma_f16 v70, v38, v110, v70
	v_pk_fma_f16 v71, v39, v111, v71
	v_pk_add_f16 v97, v141, v177 neg_lo:[0,1] neg_hi:[0,1]
	v_pk_add_f16 v98, v142, v178 neg_lo:[0,1] neg_hi:[0,1]
	v_pk_add_f16 v99, v143, v179 neg_lo:[0,1] neg_hi:[0,1]
	v_exp_f16_sdwa v108, v96 dst_sel:WORD_0 dst_unused:UNUSED_PAD src0_sel:WORD_0
	v_exp_f16_sdwa v109, v97 dst_sel:WORD_0 dst_unused:UNUSED_PAD src0_sel:WORD_0
	v_exp_f16_sdwa v110, v98 dst_sel:WORD_0 dst_unused:UNUSED_PAD src0_sel:WORD_0
	v_exp_f16_sdwa v111, v99 dst_sel:WORD_0 dst_unused:UNUSED_PAD src0_sel:WORD_0
	v_exp_f16_sdwa v108, v96 dst_sel:WORD_1 dst_unused:UNUSED_PRESERVE src0_sel:WORD_1
	v_exp_f16_sdwa v109, v97 dst_sel:WORD_1 dst_unused:UNUSED_PRESERVE src0_sel:WORD_1
	v_exp_f16_sdwa v110, v98 dst_sel:WORD_1 dst_unused:UNUSED_PRESERVE src0_sel:WORD_1
	v_exp_f16_sdwa v111, v99 dst_sel:WORD_1 dst_unused:UNUSED_PRESERVE src0_sel:WORD_1
	v_pk_add_f16 v91, v91, v108
	v_pk_add_f16 v90, v90, v109
	v_rcp_f16_e32 v96, v91
	v_rcp_f16_sdwa v91, v91 dst_sel:DWORD dst_unused:UNUSED_PAD src0_sel:WORD_1
	v_pk_add_f16 v89, v89, v110
	v_rcp_f16_e32 v97, v90
	v_rcp_f16_sdwa v90, v90 dst_sel:DWORD dst_unused:UNUSED_PAD src0_sel:WORD_1
	v_pk_add_f16 v88, v88, v111
	v_rcp_f16_e32 v98, v89
	v_rcp_f16_sdwa v99, v89 dst_sel:DWORD dst_unused:UNUSED_PAD src0_sel:WORD_1
	v_pk_fma_f16 v69, v41, v109, v69
	v_pk_fma_f16 v68, v40, v108, v68
	v_rcp_f16_e32 v108, v88
	v_rcp_f16_sdwa v109, v88 dst_sel:DWORD dst_unused:UNUSED_PAD src0_sel:WORD_1
	v_pack_b32_f16 v88, v96, v91
	v_pk_mul_f16 v88, v68, v88
	v_pack_b32_f16 v68, v97, v90
	v_pk_fma_f16 v70, v42, v110, v70
	v_pk_mul_f16 v89, v69, v68
	v_pack_b32_f16 v68, v98, v99
	v_pk_fma_f16 v71, v43, v111, v71
	v_pk_mul_f16 v90, v70, v68
	v_pack_b32_f16 v68, v108, v109
	v_pk_mul_f16 v91, v71, v68
	s_waitcnt vmcnt(6)
	v_pk_mul_f16 v68, v188, v172 op_sel_hi:[0,1]
	v_pk_mul_f16 v96, v186, v172 op_sel_hi:[0,1]
	v_pk_mul_f16 v108, v187, v172 op_sel_hi:[0,1]
	v_pk_mul_f16 v69, v188, v173 op_sel_hi:[0,1]
	v_pk_mul_f16 v70, v188, v174 op_sel_hi:[0,1]
	v_pk_mul_f16 v71, v188, v175 op_sel_hi:[0,1]
	v_pk_mul_f16 v97, v186, v173 op_sel_hi:[0,1]
	v_pk_mul_f16 v98, v186, v174 op_sel_hi:[0,1]
	v_pk_mul_f16 v99, v186, v175 op_sel_hi:[0,1]
	v_pk_mul_f16 v109, v187, v173 op_sel_hi:[0,1]
	v_pk_mul_f16 v110, v187, v174 op_sel_hi:[0,1]
	v_pk_mul_f16 v111, v187, v175 op_sel_hi:[0,1]
	v_pk_fma_f16 v76, v76, v172, v68
	v_pk_fma_f16 v92, v92, v172, v96
	v_pk_fma_f16 v115, v116, v172, v108
	v_pk_fma_f16 v79, v79, v175, v71
	v_pk_maximum3_f16 v140, v76, v92, v115
	v_pk_fma_f16 v78, v78, v174, v70
	v_pk_fma_f16 v77, v77, v173, v69
	v_pk_fma_f16 v95, v95, v175, v99
	v_pk_fma_f16 v94, v94, v174, v98
	v_pk_fma_f16 v93, v93, v173, v97
	v_pk_fma_f16 v112, v119, v175, v111
	v_pk_fma_f16 v113, v118, v174, v110
	v_pk_fma_f16 v114, v117, v173, v109
	v_pk_fma_f16 v119, v44, v172, v68
	v_pk_fma_f16 v135, v60, v172, v96
	v_pk_fma_f16 v139, v80, v172, v108
	v_pk_fma_f16 v68, v100, v172, v68
	v_pk_fma_f16 v96, v128, v172, v96
	v_pk_fma_f16 v108, v144, v172, v108
	v_pk_maximum3_f16 v141, v77, v93, v114
	v_pk_maximum3_f16 v142, v78, v94, v113
	v_pk_maximum3_f16 v143, v79, v95, v112
	v_pk_maximum3_f16 v148, v119, v135, v139
	v_pk_fma_f16 v116, v47, v175, v71
	v_pk_maximum3_f16 v152, v68, v96, v108
	v_pk_fma_f16 v117, v46, v174, v70
	v_pk_maximum3_f16 v140, v140, v148, v152
	v_pk_fma_f16 v118, v45, v173, v69
	v_pk_fma_f16 v132, v63, v175, v99
	v_pk_fma_f16 v133, v62, v174, v98
	v_pk_fma_f16 v134, v61, v173, v97
	v_pk_fma_f16 v136, v83, v175, v111
	v_pk_fma_f16 v137, v82, v174, v110
	v_pk_fma_f16 v138, v81, v173, v109
	v_pk_fma_f16 v71, v103, v175, v71
	v_pk_fma_f16 v70, v102, v174, v70
	v_pk_fma_f16 v69, v101, v173, v69
	v_pk_fma_f16 v99, v131, v175, v99
	v_pk_fma_f16 v98, v130, v174, v98
	v_pk_fma_f16 v97, v129, v173, v97
	v_pk_fma_f16 v111, v147, v175, v111
	v_pk_fma_f16 v110, v146, v174, v110
	v_pk_fma_f16 v109, v145, v173, v109
	v_pk_maximum3_f16 v149, v118, v134, v138
	v_pk_maximum3_f16 v150, v117, v133, v137
	v_pk_maximum3_f16 v151, v116, v132, v136
	v_pk_maximum3_f16 v154, v70, v98, v110
	v_pk_maximum3_f16 v155, v71, v99, v111
	v_pk_maximum3_f16 v153, v69, v97, v109
	v_pk_maximum3_f16 v141, v141, v149, v153
	v_pk_maximum3_f16 v142, v142, v150, v154
	v_pk_maximum3_f16 v143, v143, v151, v155
	v_pk_add_f16 v76, v76, v140 neg_lo:[0,1] neg_hi:[0,1]
	v_pk_add_f16 v77, v77, v141 neg_lo:[0,1] neg_hi:[0,1]
	v_pk_add_f16 v78, v78, v142 neg_lo:[0,1] neg_hi:[0,1]
	v_pk_add_f16 v79, v79, v143 neg_lo:[0,1] neg_hi:[0,1]
	v_pk_add_f16 v92, v92, v140 neg_lo:[0,1] neg_hi:[0,1]
	v_exp_f16_sdwa v148, v76 dst_sel:WORD_0 dst_unused:UNUSED_PAD src0_sel:WORD_0
	v_exp_f16_sdwa v149, v77 dst_sel:WORD_0 dst_unused:UNUSED_PAD src0_sel:WORD_0
	v_exp_f16_sdwa v150, v78 dst_sel:WORD_0 dst_unused:UNUSED_PAD src0_sel:WORD_0
	v_exp_f16_sdwa v151, v79 dst_sel:WORD_0 dst_unused:UNUSED_PAD src0_sel:WORD_0
	v_exp_f16_sdwa v148, v76 dst_sel:WORD_1 dst_unused:UNUSED_PRESERVE src0_sel:WORD_1
	v_exp_f16_sdwa v149, v77 dst_sel:WORD_1 dst_unused:UNUSED_PRESERVE src0_sel:WORD_1
	v_exp_f16_sdwa v150, v78 dst_sel:WORD_1 dst_unused:UNUSED_PRESERVE src0_sel:WORD_1
	v_exp_f16_sdwa v151, v79 dst_sel:WORD_1 dst_unused:UNUSED_PRESERVE src0_sel:WORD_1
	v_pk_add_f16 v93, v93, v141 neg_lo:[0,1] neg_hi:[0,1]
	v_pk_add_f16 v76, v151, 0
	v_pk_fma_f16 v48, v48, v148, 0
	v_pk_add_f16 v77, v150, 0
	v_pk_add_f16 v78, v149, 0
	v_pk_add_f16 v79, v148, 0
	v_pk_fma_f16 v49, v49, v149, 0
	v_pk_fma_f16 v50, v50, v150, 0
	v_pk_fma_f16 v51, v51, v151, 0
	v_pk_add_f16 v94, v94, v142 neg_lo:[0,1] neg_hi:[0,1]
	v_pk_add_f16 v95, v95, v143 neg_lo:[0,1] neg_hi:[0,1]
	v_pk_add_f16 v68, v68, v140 neg_lo:[0,1] neg_hi:[0,1]
	v_exp_f16_sdwa v148, v92 dst_sel:WORD_0 dst_unused:UNUSED_PAD src0_sel:WORD_0
	v_exp_f16_sdwa v149, v93 dst_sel:WORD_0 dst_unused:UNUSED_PAD src0_sel:WORD_0
	v_exp_f16_sdwa v150, v94 dst_sel:WORD_0 dst_unused:UNUSED_PAD src0_sel:WORD_0
	v_exp_f16_sdwa v151, v95 dst_sel:WORD_0 dst_unused:UNUSED_PAD src0_sel:WORD_0
	v_exp_f16_sdwa v148, v92 dst_sel:WORD_1 dst_unused:UNUSED_PRESERVE src0_sel:WORD_1
	v_exp_f16_sdwa v149, v93 dst_sel:WORD_1 dst_unused:UNUSED_PRESERVE src0_sel:WORD_1
	v_exp_f16_sdwa v150, v94 dst_sel:WORD_1 dst_unused:UNUSED_PRESERVE src0_sel:WORD_1
	v_exp_f16_sdwa v151, v95 dst_sel:WORD_1 dst_unused:UNUSED_PRESERVE src0_sel:WORD_1
	v_pk_add_f16 v69, v69, v141 neg_lo:[0,1] neg_hi:[0,1]
	v_pk_add_f16 v76, v76, v151
	v_pk_fma_f16 v48, v56, v148, v48
	v_pk_add_f16 v56, v115, v140 neg_lo:[0,1] neg_hi:[0,1]
	v_pk_add_f16 v79, v79, v148
	v_pk_add_f16 v78, v78, v149
	v_pk_add_f16 v77, v77, v150
	v_pk_fma_f16 v51, v59, v151, v51
	v_pk_fma_f16 v50, v58, v150, v50
	v_pk_fma_f16 v49, v57, v149, v49
	v_pk_add_f16 v57, v114, v141 neg_lo:[0,1] neg_hi:[0,1]
	v_pk_add_f16 v58, v113, v142 neg_lo:[0,1] neg_hi:[0,1]
	v_pk_add_f16 v59, v112, v143 neg_lo:[0,1] neg_hi:[0,1]
	v_pk_add_f16 v70, v70, v142 neg_lo:[0,1] neg_hi:[0,1]
	v_exp_f16_sdwa v92, v56 dst_sel:WORD_0 dst_unused:UNUSED_PAD src0_sel:WORD_0
	v_exp_f16_sdwa v93, v57 dst_sel:WORD_0 dst_unused:UNUSED_PAD src0_sel:WORD_0
	v_exp_f16_sdwa v94, v58 dst_sel:WORD_0 dst_unused:UNUSED_PAD src0_sel:WORD_0
	v_exp_f16_sdwa v95, v59 dst_sel:WORD_0 dst_unused:UNUSED_PAD src0_sel:WORD_0
	v_exp_f16_sdwa v92, v56 dst_sel:WORD_1 dst_unused:UNUSED_PRESERVE src0_sel:WORD_1
	v_exp_f16_sdwa v93, v57 dst_sel:WORD_1 dst_unused:UNUSED_PRESERVE src0_sel:WORD_1
	v_exp_f16_sdwa v94, v58 dst_sel:WORD_1 dst_unused:UNUSED_PRESERVE src0_sel:WORD_1
	v_exp_f16_sdwa v95, v59 dst_sel:WORD_1 dst_unused:UNUSED_PRESERVE src0_sel:WORD_1
	v_pk_add_f16 v71, v71, v143 neg_lo:[0,1] neg_hi:[0,1]
	v_pk_add_f16 v56, v76, v95
	v_pk_add_f16 v57, v77, v94
	v_pk_add_f16 v58, v78, v93
	v_pk_add_f16 v59, v79, v92
	v_pk_fma_f16 v48, v72, v92, v48
	v_pk_fma_f16 v49, v73, v93, v49
	v_pk_fma_f16 v50, v74, v94, v50
	v_pk_fma_f16 v51, v75, v95, v51
	v_pk_add_f16 v72, v119, v140 neg_lo:[0,1] neg_hi:[0,1]
	v_pk_add_f16 v73, v118, v141 neg_lo:[0,1] neg_hi:[0,1]
	v_pk_add_f16 v74, v117, v142 neg_lo:[0,1] neg_hi:[0,1]
	v_pk_add_f16 v75, v116, v143 neg_lo:[0,1] neg_hi:[0,1]
	v_exp_f16_sdwa v76, v72 dst_sel:WORD_0 dst_unused:UNUSED_PAD src0_sel:WORD_0
	v_exp_f16_sdwa v77, v73 dst_sel:WORD_0 dst_unused:UNUSED_PAD src0_sel:WORD_0
	v_exp_f16_sdwa v78, v74 dst_sel:WORD_0 dst_unused:UNUSED_PAD src0_sel:WORD_0
	v_exp_f16_sdwa v79, v75 dst_sel:WORD_0 dst_unused:UNUSED_PAD src0_sel:WORD_0
	v_exp_f16_sdwa v76, v72 dst_sel:WORD_1 dst_unused:UNUSED_PRESERVE src0_sel:WORD_1
	v_exp_f16_sdwa v77, v73 dst_sel:WORD_1 dst_unused:UNUSED_PRESERVE src0_sel:WORD_1
	v_exp_f16_sdwa v78, v74 dst_sel:WORD_1 dst_unused:UNUSED_PRESERVE src0_sel:WORD_1
	v_exp_f16_sdwa v79, v75 dst_sel:WORD_1 dst_unused:UNUSED_PRESERVE src0_sel:WORD_1
	v_pk_add_f16 v72, v135, v140 neg_lo:[0,1] neg_hi:[0,1]
	v_pk_add_f16 v56, v56, v79
	v_pk_add_f16 v59, v59, v76
	v_pk_add_f16 v58, v58, v77
	v_pk_add_f16 v57, v57, v78
	v_pk_fma_f16 v51, v35, v79, v51
	v_pk_fma_f16 v50, v34, v78, v50
	v_pk_fma_f16 v49, v33, v77, v49
	v_pk_fma_f16 v48, v32, v76, v48
	v_pk_add_f16 v73, v134, v141 neg_lo:[0,1] neg_hi:[0,1]
	v_pk_add_f16 v74, v133, v142 neg_lo:[0,1] neg_hi:[0,1]
	v_pk_add_f16 v75, v132, v143 neg_lo:[0,1] neg_hi:[0,1]
	v_exp_f16_sdwa v76, v72 dst_sel:WORD_0 dst_unused:UNUSED_PAD src0_sel:WORD_0
	v_exp_f16_sdwa v77, v73 dst_sel:WORD_0 dst_unused:UNUSED_PAD src0_sel:WORD_0
	v_exp_f16_sdwa v78, v74 dst_sel:WORD_0 dst_unused:UNUSED_PAD src0_sel:WORD_0
	v_exp_f16_sdwa v79, v75 dst_sel:WORD_0 dst_unused:UNUSED_PAD src0_sel:WORD_0
	v_exp_f16_sdwa v76, v72 dst_sel:WORD_1 dst_unused:UNUSED_PRESERVE src0_sel:WORD_1
	v_exp_f16_sdwa v77, v73 dst_sel:WORD_1 dst_unused:UNUSED_PRESERVE src0_sel:WORD_1
	v_exp_f16_sdwa v78, v74 dst_sel:WORD_1 dst_unused:UNUSED_PRESERVE src0_sel:WORD_1
	v_exp_f16_sdwa v79, v75 dst_sel:WORD_1 dst_unused:UNUSED_PRESERVE src0_sel:WORD_1
	v_pk_add_f16 v72, v139, v140 neg_lo:[0,1] neg_hi:[0,1]
	v_pk_add_f16 v56, v56, v79
	v_pk_add_f16 v57, v57, v78
	v_pk_add_f16 v58, v58, v77
	v_pk_add_f16 v59, v59, v76
	v_pk_fma_f16 v48, v36, v76, v48
	v_pk_fma_f16 v49, v37, v77, v49
	v_pk_fma_f16 v50, v38, v78, v50
	v_pk_fma_f16 v51, v39, v79, v51
	v_pk_add_f16 v73, v138, v141 neg_lo:[0,1] neg_hi:[0,1]
	v_pk_add_f16 v74, v137, v142 neg_lo:[0,1] neg_hi:[0,1]
	v_pk_add_f16 v75, v136, v143 neg_lo:[0,1] neg_hi:[0,1]
	v_exp_f16_sdwa v76, v72 dst_sel:WORD_0 dst_unused:UNUSED_PAD src0_sel:WORD_0
	v_exp_f16_sdwa v77, v73 dst_sel:WORD_0 dst_unused:UNUSED_PAD src0_sel:WORD_0
	v_exp_f16_sdwa v78, v74 dst_sel:WORD_0 dst_unused:UNUSED_PAD src0_sel:WORD_0
	v_exp_f16_sdwa v79, v75 dst_sel:WORD_0 dst_unused:UNUSED_PAD src0_sel:WORD_0
	v_exp_f16_sdwa v76, v72 dst_sel:WORD_1 dst_unused:UNUSED_PRESERVE src0_sel:WORD_1
	v_exp_f16_sdwa v77, v73 dst_sel:WORD_1 dst_unused:UNUSED_PRESERVE src0_sel:WORD_1
	v_exp_f16_sdwa v78, v74 dst_sel:WORD_1 dst_unused:UNUSED_PRESERVE src0_sel:WORD_1
	v_exp_f16_sdwa v79, v75 dst_sel:WORD_1 dst_unused:UNUSED_PRESERVE src0_sel:WORD_1
	v_exp_f16_sdwa v72, v68 dst_sel:WORD_0 dst_unused:UNUSED_PAD src0_sel:WORD_0
	v_exp_f16_sdwa v73, v69 dst_sel:WORD_0 dst_unused:UNUSED_PAD src0_sel:WORD_0
	v_exp_f16_sdwa v74, v70 dst_sel:WORD_0 dst_unused:UNUSED_PAD src0_sel:WORD_0
	v_exp_f16_sdwa v75, v71 dst_sel:WORD_0 dst_unused:UNUSED_PAD src0_sel:WORD_0
	v_exp_f16_sdwa v72, v68 dst_sel:WORD_1 dst_unused:UNUSED_PRESERVE src0_sel:WORD_1
	v_exp_f16_sdwa v73, v69 dst_sel:WORD_1 dst_unused:UNUSED_PRESERVE src0_sel:WORD_1
	v_exp_f16_sdwa v74, v70 dst_sel:WORD_1 dst_unused:UNUSED_PRESERVE src0_sel:WORD_1
	v_exp_f16_sdwa v75, v71 dst_sel:WORD_1 dst_unused:UNUSED_PRESERVE src0_sel:WORD_1
	v_pk_add_f16 v68, v96, v140 neg_lo:[0,1] neg_hi:[0,1]
	v_pk_add_f16 v56, v56, v79
	v_pk_add_f16 v59, v59, v76
	v_pk_add_f16 v58, v58, v77
	v_pk_add_f16 v57, v57, v78
	v_pk_fma_f16 v51, v43, v79, v51
	v_pk_fma_f16 v50, v42, v78, v50
	v_pk_fma_f16 v49, v41, v77, v49
	v_pk_fma_f16 v48, v40, v76, v48
	v_pk_add_f16 v56, v56, v75
	v_pk_add_f16 v57, v57, v74
	v_pk_add_f16 v58, v58, v73
	v_pk_add_f16 v59, v59, v72
	v_pk_fma_f16 v48, v52, v72, v48
	v_pk_fma_f16 v49, v53, v73, v49
	v_pk_fma_f16 v50, v54, v74, v50
	v_pk_fma_f16 v51, v55, v75, v51
	v_pk_add_f16 v69, v97, v141 neg_lo:[0,1] neg_hi:[0,1]
	v_pk_add_f16 v70, v98, v142 neg_lo:[0,1] neg_hi:[0,1]
	v_pk_add_f16 v71, v99, v143 neg_lo:[0,1] neg_hi:[0,1]
	v_exp_f16_sdwa v72, v68 dst_sel:WORD_0 dst_unused:UNUSED_PAD src0_sel:WORD_0
	v_exp_f16_sdwa v73, v69 dst_sel:WORD_0 dst_unused:UNUSED_PAD src0_sel:WORD_0
	v_exp_f16_sdwa v74, v70 dst_sel:WORD_0 dst_unused:UNUSED_PAD src0_sel:WORD_0
	v_exp_f16_sdwa v75, v71 dst_sel:WORD_0 dst_unused:UNUSED_PAD src0_sel:WORD_0
	v_exp_f16_sdwa v72, v68 dst_sel:WORD_1 dst_unused:UNUSED_PRESERVE src0_sel:WORD_1
	v_exp_f16_sdwa v73, v69 dst_sel:WORD_1 dst_unused:UNUSED_PRESERVE src0_sel:WORD_1
	v_exp_f16_sdwa v74, v70 dst_sel:WORD_1 dst_unused:UNUSED_PRESERVE src0_sel:WORD_1
	v_exp_f16_sdwa v75, v71 dst_sel:WORD_1 dst_unused:UNUSED_PRESERVE src0_sel:WORD_1
	v_pk_add_f16 v68, v108, v140 neg_lo:[0,1] neg_hi:[0,1]
	v_pk_add_f16 v56, v56, v75
	v_pk_add_f16 v59, v59, v72
	v_pk_add_f16 v58, v58, v73
	v_pk_add_f16 v57, v57, v74
	v_pk_fma_f16 v51, v67, v75, v51
	v_pk_fma_f16 v50, v66, v74, v50
	v_pk_fma_f16 v49, v65, v73, v49
	v_pk_fma_f16 v48, v64, v72, v48
	v_pk_add_f16 v69, v109, v141 neg_lo:[0,1] neg_hi:[0,1]
	v_pk_add_f16 v70, v110, v142 neg_lo:[0,1] neg_hi:[0,1]
	v_pk_add_f16 v71, v111, v143 neg_lo:[0,1] neg_hi:[0,1]
	v_exp_f16_sdwa v72, v68 dst_sel:WORD_0 dst_unused:UNUSED_PAD src0_sel:WORD_0
	v_exp_f16_sdwa v73, v69 dst_sel:WORD_0 dst_unused:UNUSED_PAD src0_sel:WORD_0
	v_exp_f16_sdwa v74, v70 dst_sel:WORD_0 dst_unused:UNUSED_PAD src0_sel:WORD_0
	v_exp_f16_sdwa v75, v71 dst_sel:WORD_0 dst_unused:UNUSED_PAD src0_sel:WORD_0
	v_exp_f16_sdwa v72, v68 dst_sel:WORD_1 dst_unused:UNUSED_PRESERVE src0_sel:WORD_1
	v_exp_f16_sdwa v73, v69 dst_sel:WORD_1 dst_unused:UNUSED_PRESERVE src0_sel:WORD_1
	v_exp_f16_sdwa v74, v70 dst_sel:WORD_1 dst_unused:UNUSED_PRESERVE src0_sel:WORD_1
	v_exp_f16_sdwa v75, v71 dst_sel:WORD_1 dst_unused:UNUSED_PRESERVE src0_sel:WORD_1
	s_nop 0
	v_pk_add_f16 v56, v56, v75
	v_pk_add_f16 v57, v57, v74
	v_rcp_f16_e32 v70, v56
	v_rcp_f16_sdwa v56, v56 dst_sel:DWORD dst_unused:UNUSED_PAD src0_sel:WORD_1
	v_pk_add_f16 v58, v58, v73
	v_rcp_f16_e32 v71, v57
	v_rcp_f16_sdwa v57, v57 dst_sel:DWORD dst_unused:UNUSED_PAD src0_sel:WORD_1
	v_pk_add_f16 v59, v59, v72
	v_rcp_f16_e32 v69, v58
	v_rcp_f16_sdwa v58, v58 dst_sel:DWORD dst_unused:UNUSED_PAD src0_sel:WORD_1
	v_rcp_f16_e32 v68, v59
	v_rcp_f16_sdwa v59, v59 dst_sel:DWORD dst_unused:UNUSED_PAD src0_sel:WORD_1
	v_pk_fma_f16 v51, v87, v75, v51
	v_pack_b32_f16 v56, v70, v56
	v_pk_fma_f16 v50, v86, v74, v50
	v_pk_mul_f16 v51, v51, v56
	v_pack_b32_f16 v56, v71, v57
	v_pk_fma_f16 v49, v85, v73, v49
	v_pk_mul_f16 v50, v50, v56
	v_pack_b32_f16 v56, v69, v58
	v_pk_fma_f16 v48, v84, v72, v48
	v_pk_mul_f16 v49, v49, v56
	v_pack_b32_f16 v56, v68, v59
	v_pk_mul_f16 v48, v48, v56
	s_waitcnt vmcnt(0)
	v_pk_mul_f16 v56, v188, v168 op_sel_hi:[0,1]
	v_pk_mul_f16 v57, v188, v169 op_sel_hi:[0,1]
	v_pk_mul_f16 v58, v188, v170 op_sel_hi:[0,1]
	v_pk_mul_f16 v59, v188, v171 op_sel_hi:[0,1]
	v_pk_mul_f16 v68, v186, v168 op_sel_hi:[0,1]
	v_pk_mul_f16 v69, v186, v169 op_sel_hi:[0,1]
	v_pk_mul_f16 v70, v186, v170 op_sel_hi:[0,1]
	v_pk_mul_f16 v71, v186, v171 op_sel_hi:[0,1]
	v_pk_mul_f16 v72, v187, v168 op_sel_hi:[0,1]
	v_pk_mul_f16 v73, v187, v169 op_sel_hi:[0,1]
	v_pk_mul_f16 v74, v187, v170 op_sel_hi:[0,1]
	v_pk_mul_f16 v75, v187, v171 op_sel_hi:[0,1]
	v_pk_fma_f16 v47, v47, v171, v59
	v_pk_fma_f16 v46, v46, v170, v58
	v_pk_fma_f16 v45, v45, v169, v57
	v_pk_fma_f16 v44, v44, v168, v56
	v_pk_fma_f16 v63, v63, v171, v71
	v_pk_fma_f16 v62, v62, v170, v70
	v_pk_fma_f16 v61, v61, v169, v69
	v_pk_fma_f16 v60, v60, v168, v68
	v_pk_fma_f16 v76, v83, v171, v75
	v_pk_fma_f16 v77, v82, v170, v74
	v_pk_fma_f16 v78, v81, v169, v73
	v_pk_fma_f16 v79, v80, v168, v72
	v_pk_fma_f16 v80, v103, v171, v59
	v_pk_fma_f16 v81, v102, v170, v58
	v_pk_fma_f16 v82, v101, v169, v57
	v_pk_fma_f16 v83, v100, v168, v56
	v_pk_fma_f16 v92, v131, v171, v71
	v_pk_fma_f16 v93, v130, v170, v70
	v_pk_fma_f16 v94, v129, v169, v69
	v_pk_fma_f16 v95, v128, v168, v68
	v_pk_fma_f16 v96, v147, v171, v75
	v_pk_fma_f16 v97, v146, v170, v74
	v_pk_fma_f16 v98, v145, v169, v73
	v_pk_fma_f16 v99, v144, v168, v72
	v_pk_fma_f16 v75, v31, v171, v75
	v_pk_fma_f16 v74, v30, v170, v74
	v_pk_fma_f16 v73, v29, v169, v73
	v_pk_fma_f16 v72, v28, v168, v72
	v_pk_maximum3_f16 v28, v44, v60, v79
	v_pk_maximum3_f16 v29, v45, v61, v78
	v_pk_maximum3_f16 v30, v46, v62, v77
	v_pk_maximum3_f16 v31, v47, v63, v76
	v_pk_maximum3_f16 v100, v83, v95, v99
	v_pk_maximum3_f16 v101, v82, v94, v98
	v_pk_maximum3_f16 v102, v81, v93, v97
	v_pk_maximum3_f16 v103, v80, v92, v96
	v_pk_fma_f16 v59, v159, v171, v59
	v_pk_fma_f16 v58, v158, v170, v58
	v_pk_fma_f16 v57, v157, v169, v57
	v_pk_fma_f16 v56, v156, v168, v56
	v_pk_fma_f16 v71, v167, v171, v71
	v_pk_fma_f16 v70, v166, v170, v70
	v_pk_fma_f16 v69, v165, v169, v69
	v_pk_fma_f16 v68, v164, v168, v68
	v_pk_maximum3_f16 v109, v57, v69, v73
	v_pk_maximum3_f16 v110, v58, v70, v74
	v_pk_maximum3_f16 v111, v59, v71, v75
	v_pk_maximum3_f16 v108, v56, v68, v72
	v_pk_maximum3_f16 v29, v29, v101, v109
	v_pk_maximum3_f16 v30, v30, v102, v110
	v_pk_maximum3_f16 v31, v31, v103, v111
	v_pk_maximum3_f16 v28, v28, v100, v108
	v_xor_b32_e32 v100, 0x80008000, v31
	v_xor_b32_e32 v101, 0x80008000, v30
	v_xor_b32_e32 v102, 0x80008000, v29
	v_xor_b32_e32 v103, 0x80008000, v28
	v_pk_add_f16 v28, v44, v103
	v_pk_add_f16 v29, v45, v102
	v_pk_add_f16 v30, v46, v101
	v_pk_add_f16 v31, v47, v100
	v_exp_f16_sdwa v44, v28 dst_sel:WORD_0 dst_unused:UNUSED_PAD src0_sel:WORD_0
	v_exp_f16_sdwa v45, v29 dst_sel:WORD_0 dst_unused:UNUSED_PAD src0_sel:WORD_0
	v_exp_f16_sdwa v46, v30 dst_sel:WORD_0 dst_unused:UNUSED_PAD src0_sel:WORD_0
	v_exp_f16_sdwa v47, v31 dst_sel:WORD_0 dst_unused:UNUSED_PAD src0_sel:WORD_0
	v_exp_f16_sdwa v44, v28 dst_sel:WORD_1 dst_unused:UNUSED_PRESERVE src0_sel:WORD_1
	v_exp_f16_sdwa v45, v29 dst_sel:WORD_1 dst_unused:UNUSED_PRESERVE src0_sel:WORD_1
	v_exp_f16_sdwa v46, v30 dst_sel:WORD_1 dst_unused:UNUSED_PRESERVE src0_sel:WORD_1
	v_exp_f16_sdwa v47, v31 dst_sel:WORD_1 dst_unused:UNUSED_PRESERVE src0_sel:WORD_1
	v_pk_add_f16 v28, v44, 0
	v_pk_add_f16 v29, v45, 0
	v_pk_add_f16 v30, v46, 0
	v_pk_add_f16 v31, v47, 0
	v_pk_fma_f16 v32, v32, v44, 0
	v_pk_fma_f16 v33, v33, v45, 0
	v_pk_fma_f16 v34, v34, v46, 0
	v_pk_fma_f16 v35, v35, v47, 0
	v_pk_add_f16 v44, v60, v103
	v_pk_add_f16 v45, v61, v102
	v_pk_add_f16 v46, v62, v101
	v_pk_add_f16 v47, v63, v100
	v_exp_f16_sdwa v60, v44 dst_sel:WORD_0 dst_unused:UNUSED_PAD src0_sel:WORD_0
	v_exp_f16_sdwa v61, v45 dst_sel:WORD_0 dst_unused:UNUSED_PAD src0_sel:WORD_0
	v_exp_f16_sdwa v62, v46 dst_sel:WORD_0 dst_unused:UNUSED_PAD src0_sel:WORD_0
	v_exp_f16_sdwa v63, v47 dst_sel:WORD_0 dst_unused:UNUSED_PAD src0_sel:WORD_0
	v_exp_f16_sdwa v60, v44 dst_sel:WORD_1 dst_unused:UNUSED_PRESERVE src0_sel:WORD_1
	v_exp_f16_sdwa v61, v45 dst_sel:WORD_1 dst_unused:UNUSED_PRESERVE src0_sel:WORD_1
	v_exp_f16_sdwa v62, v46 dst_sel:WORD_1 dst_unused:UNUSED_PRESERVE src0_sel:WORD_1
	v_exp_f16_sdwa v63, v47 dst_sel:WORD_1 dst_unused:UNUSED_PRESERVE src0_sel:WORD_1
	s_nop 0
	v_pk_add_f16 v31, v31, v63
	v_pk_add_f16 v30, v30, v62
	v_pk_add_f16 v29, v29, v61
	v_pk_add_f16 v28, v28, v60
	v_pk_fma_f16 v35, v39, v63, v35
	v_pk_fma_f16 v34, v38, v62, v34
	v_pk_fma_f16 v33, v37, v61, v33
	v_pk_fma_f16 v32, v36, v60, v32
	v_pk_add_f16 v36, v79, v103
	v_pk_add_f16 v37, v78, v102
	v_pk_add_f16 v38, v77, v101
	v_pk_add_f16 v39, v76, v100
	v_exp_f16_sdwa v44, v36 dst_sel:WORD_0 dst_unused:UNUSED_PAD src0_sel:WORD_0
	v_exp_f16_sdwa v45, v37 dst_sel:WORD_0 dst_unused:UNUSED_PAD src0_sel:WORD_0
	v_exp_f16_sdwa v46, v38 dst_sel:WORD_0 dst_unused:UNUSED_PAD src0_sel:WORD_0
	v_exp_f16_sdwa v47, v39 dst_sel:WORD_0 dst_unused:UNUSED_PAD src0_sel:WORD_0
	v_exp_f16_sdwa v44, v36 dst_sel:WORD_1 dst_unused:UNUSED_PRESERVE src0_sel:WORD_1
	v_exp_f16_sdwa v45, v37 dst_sel:WORD_1 dst_unused:UNUSED_PRESERVE src0_sel:WORD_1
	v_exp_f16_sdwa v46, v38 dst_sel:WORD_1 dst_unused:UNUSED_PRESERVE src0_sel:WORD_1
	v_exp_f16_sdwa v47, v39 dst_sel:WORD_1 dst_unused:UNUSED_PRESERVE src0_sel:WORD_1
	v_pk_add_f16 v36, v83, v103
	v_pk_add_f16 v28, v28, v44
	v_pk_add_f16 v29, v29, v45
	v_pk_add_f16 v30, v30, v46
	v_pk_add_f16 v31, v31, v47
	v_pk_fma_f16 v32, v40, v44, v32
	v_pk_fma_f16 v33, v41, v45, v33
	v_pk_fma_f16 v34, v42, v46, v34
	v_pk_fma_f16 v35, v43, v47, v35
	v_pk_add_f16 v37, v82, v102
	v_pk_add_f16 v38, v81, v101
	v_pk_add_f16 v39, v80, v100
	v_exp_f16_sdwa v40, v36 dst_sel:WORD_0 dst_unused:UNUSED_PAD src0_sel:WORD_0
	v_exp_f16_sdwa v41, v37 dst_sel:WORD_0 dst_unused:UNUSED_PAD src0_sel:WORD_0
	v_exp_f16_sdwa v42, v38 dst_sel:WORD_0 dst_unused:UNUSED_PAD src0_sel:WORD_0
	v_exp_f16_sdwa v43, v39 dst_sel:WORD_0 dst_unused:UNUSED_PAD src0_sel:WORD_0
	v_exp_f16_sdwa v40, v36 dst_sel:WORD_1 dst_unused:UNUSED_PRESERVE src0_sel:WORD_1
	v_exp_f16_sdwa v41, v37 dst_sel:WORD_1 dst_unused:UNUSED_PRESERVE src0_sel:WORD_1
	v_exp_f16_sdwa v42, v38 dst_sel:WORD_1 dst_unused:UNUSED_PRESERVE src0_sel:WORD_1
	v_exp_f16_sdwa v43, v39 dst_sel:WORD_1 dst_unused:UNUSED_PRESERVE src0_sel:WORD_1
	v_pk_add_f16 v36, v95, v103
	v_pk_add_f16 v31, v31, v43
	v_pk_add_f16 v30, v30, v42
	v_pk_add_f16 v29, v29, v41
	v_pk_add_f16 v28, v28, v40
	v_pk_fma_f16 v35, v55, v43, v35
	v_pk_fma_f16 v34, v54, v42, v34
	v_pk_fma_f16 v33, v53, v41, v33
	v_pk_fma_f16 v32, v52, v40, v32
	v_pk_add_f16 v37, v94, v102
	v_pk_add_f16 v38, v93, v101
	v_pk_add_f16 v39, v92, v100
	v_exp_f16_sdwa v40, v36 dst_sel:WORD_0 dst_unused:UNUSED_PAD src0_sel:WORD_0
	v_exp_f16_sdwa v41, v37 dst_sel:WORD_0 dst_unused:UNUSED_PAD src0_sel:WORD_0
	v_exp_f16_sdwa v42, v38 dst_sel:WORD_0 dst_unused:UNUSED_PAD src0_sel:WORD_0
	v_exp_f16_sdwa v43, v39 dst_sel:WORD_0 dst_unused:UNUSED_PAD src0_sel:WORD_0
	v_exp_f16_sdwa v40, v36 dst_sel:WORD_1 dst_unused:UNUSED_PRESERVE src0_sel:WORD_1
	v_exp_f16_sdwa v41, v37 dst_sel:WORD_1 dst_unused:UNUSED_PRESERVE src0_sel:WORD_1
	v_exp_f16_sdwa v42, v38 dst_sel:WORD_1 dst_unused:UNUSED_PRESERVE src0_sel:WORD_1
	v_exp_f16_sdwa v43, v39 dst_sel:WORD_1 dst_unused:UNUSED_PRESERVE src0_sel:WORD_1
	v_pk_add_f16 v36, v99, v103
	v_pk_add_f16 v28, v28, v40
	v_pk_add_f16 v29, v29, v41
	v_pk_add_f16 v30, v30, v42
	v_pk_add_f16 v31, v31, v43
	v_pk_fma_f16 v32, v64, v40, v32
	v_pk_fma_f16 v33, v65, v41, v33
	v_pk_fma_f16 v34, v66, v42, v34
	v_pk_fma_f16 v35, v67, v43, v35
	v_pk_add_f16 v37, v98, v102
	v_pk_add_f16 v38, v97, v101
	v_pk_add_f16 v39, v96, v100
	v_exp_f16_sdwa v40, v36 dst_sel:WORD_0 dst_unused:UNUSED_PAD src0_sel:WORD_0
	v_exp_f16_sdwa v41, v37 dst_sel:WORD_0 dst_unused:UNUSED_PAD src0_sel:WORD_0
	v_exp_f16_sdwa v42, v38 dst_sel:WORD_0 dst_unused:UNUSED_PAD src0_sel:WORD_0
	v_exp_f16_sdwa v43, v39 dst_sel:WORD_0 dst_unused:UNUSED_PAD src0_sel:WORD_0
	v_exp_f16_sdwa v40, v36 dst_sel:WORD_1 dst_unused:UNUSED_PRESERVE src0_sel:WORD_1
	v_exp_f16_sdwa v41, v37 dst_sel:WORD_1 dst_unused:UNUSED_PRESERVE src0_sel:WORD_1
	v_exp_f16_sdwa v42, v38 dst_sel:WORD_1 dst_unused:UNUSED_PRESERVE src0_sel:WORD_1
	v_exp_f16_sdwa v43, v39 dst_sel:WORD_1 dst_unused:UNUSED_PRESERVE src0_sel:WORD_1
	v_pk_add_f16 v36, v56, v103
	v_pk_add_f16 v31, v31, v43
	v_pk_add_f16 v30, v30, v42
	v_pk_add_f16 v29, v29, v41
	v_pk_add_f16 v28, v28, v40
	v_pk_fma_f16 v35, v87, v43, v35
	v_pk_fma_f16 v34, v86, v42, v34
	v_pk_fma_f16 v33, v85, v41, v33
	v_pk_fma_f16 v32, v84, v40, v32
	v_pk_add_f16 v37, v57, v102
	v_pk_add_f16 v38, v58, v101
	v_pk_add_f16 v39, v59, v100
	v_exp_f16_sdwa v40, v36 dst_sel:WORD_0 dst_unused:UNUSED_PAD src0_sel:WORD_0
	v_exp_f16_sdwa v41, v37 dst_sel:WORD_0 dst_unused:UNUSED_PAD src0_sel:WORD_0
	v_exp_f16_sdwa v42, v38 dst_sel:WORD_0 dst_unused:UNUSED_PAD src0_sel:WORD_0
	v_exp_f16_sdwa v43, v39 dst_sel:WORD_0 dst_unused:UNUSED_PAD src0_sel:WORD_0
	v_exp_f16_sdwa v40, v36 dst_sel:WORD_1 dst_unused:UNUSED_PRESERVE src0_sel:WORD_1
	v_exp_f16_sdwa v41, v37 dst_sel:WORD_1 dst_unused:UNUSED_PRESERVE src0_sel:WORD_1
	v_exp_f16_sdwa v42, v38 dst_sel:WORD_1 dst_unused:UNUSED_PRESERVE src0_sel:WORD_1
	v_exp_f16_sdwa v43, v39 dst_sel:WORD_1 dst_unused:UNUSED_PRESERVE src0_sel:WORD_1
	v_pk_add_f16 v36, v68, v103
	v_pk_add_f16 v28, v28, v40
	v_pk_add_f16 v29, v29, v41
	v_pk_add_f16 v30, v30, v42
	v_pk_add_f16 v31, v31, v43
	v_pk_fma_f16 v32, v104, v40, v32
	v_pk_fma_f16 v33, v105, v41, v33
	v_pk_fma_f16 v34, v106, v42, v34
	v_pk_fma_f16 v35, v107, v43, v35
	v_pk_add_f16 v37, v69, v102
	v_pk_add_f16 v38, v70, v101
	v_pk_add_f16 v39, v71, v100
	v_exp_f16_sdwa v40, v36 dst_sel:WORD_0 dst_unused:UNUSED_PAD src0_sel:WORD_0
	v_exp_f16_sdwa v41, v37 dst_sel:WORD_0 dst_unused:UNUSED_PAD src0_sel:WORD_0
	v_exp_f16_sdwa v42, v38 dst_sel:WORD_0 dst_unused:UNUSED_PAD src0_sel:WORD_0
	v_exp_f16_sdwa v43, v39 dst_sel:WORD_0 dst_unused:UNUSED_PAD src0_sel:WORD_0
	v_exp_f16_sdwa v40, v36 dst_sel:WORD_1 dst_unused:UNUSED_PRESERVE src0_sel:WORD_1
	v_exp_f16_sdwa v41, v37 dst_sel:WORD_1 dst_unused:UNUSED_PRESERVE src0_sel:WORD_1
	v_exp_f16_sdwa v42, v38 dst_sel:WORD_1 dst_unused:UNUSED_PRESERVE src0_sel:WORD_1
	v_exp_f16_sdwa v43, v39 dst_sel:WORD_1 dst_unused:UNUSED_PRESERVE src0_sel:WORD_1
	s_nop 0
	v_pk_add_f16 v31, v31, v43
	v_pk_add_f16 v30, v30, v42
	v_pk_add_f16 v29, v29, v41
	v_pk_add_f16 v28, v28, v40
	v_pk_fma_f16 v35, v123, v43, v35
	v_pk_fma_f16 v34, v122, v42, v34
	v_pk_fma_f16 v33, v121, v41, v33
	v_pk_fma_f16 v32, v120, v40, v32
	v_pk_add_f16 v40, v72, v103
	v_pk_add_f16 v41, v73, v102
	v_pk_add_f16 v42, v74, v101
	v_pk_add_f16 v43, v75, v100
	v_exp_f16_sdwa v36, v40 dst_sel:WORD_0 dst_unused:UNUSED_PAD src0_sel:WORD_0
	v_exp_f16_sdwa v37, v41 dst_sel:WORD_0 dst_unused:UNUSED_PAD src0_sel:WORD_0
	v_exp_f16_sdwa v38, v42 dst_sel:WORD_0 dst_unused:UNUSED_PAD src0_sel:WORD_0
	v_exp_f16_sdwa v39, v43 dst_sel:WORD_0 dst_unused:UNUSED_PAD src0_sel:WORD_0
	v_exp_f16_sdwa v36, v40 dst_sel:WORD_1 dst_unused:UNUSED_PRESERVE src0_sel:WORD_1
	v_exp_f16_sdwa v37, v41 dst_sel:WORD_1 dst_unused:UNUSED_PRESERVE src0_sel:WORD_1
	v_exp_f16_sdwa v38, v42 dst_sel:WORD_1 dst_unused:UNUSED_PRESERVE src0_sel:WORD_1
	v_exp_f16_sdwa v39, v43 dst_sel:WORD_1 dst_unused:UNUSED_PRESERVE src0_sel:WORD_1
	s_nop 0
	s_load_dwordx2 s[12:13], s[0:1], 0x60
	s_branch .LBB6_76
.LBB6_38:
	s_load_dwordx2 s[12:13], s[0:1], 0x60
	s_cbranch_execz .LBB6_76
	s_load_dwordx2 s[2:3], s[0:1], 0x18
	s_waitcnt lgkmcnt(0)
	s_load_dwordx2 s[0:1], s[2:3], 0x0
	s_load_dword s4, s[2:3], 0x8
	v_cmp_lt_u32_e64 s[64:65], 0, v182
	v_cmp_gt_u32_e64 s[66:67], 63, v182
	v_cmp_lt_u32_e64 s[68:69], 0, v181
	v_cmp_gt_u32_e64 s[70:71], 60, v181
	buffer_load_dwordx4 v[168:171], v183, s[8:11], 0 offen
	s_and_b64 s[72:73], s[68:69], s[64:65]
	s_and_b64 s[74:75], s[68:69], s[66:67]
	s_and_b64 s[76:77], s[70:71], s[64:65]
	s_and_b64 s[78:79], s[70:71], s[66:67]
	v_mov_b32_e32 v140, v20
	v_mov_b32_e32 v141, v21
	v_mov_b32_e32 v142, v22
	v_mov_b32_e32 v143, v23
	v_mov_b32_e32 v120, v16
	v_mov_b32_e32 v121, v17
	v_mov_b32_e32 v122, v18
	v_mov_b32_e32 v123, v19
	v_mov_b32_e32 v152, v20
	v_mov_b32_e32 v153, v21
	v_mov_b32_e32 v154, v22
	v_mov_b32_e32 v155, v23
	v_mov_b32_e32 v132, v16
	v_mov_b32_e32 v133, v17
	v_mov_b32_e32 v134, v18
	v_mov_b32_e32 v135, v19
	v_mov_b32_e32 v156, v20
	v_mov_b32_e32 v157, v21
	v_mov_b32_e32 v158, v22
	v_mov_b32_e32 v159, v23
	v_mov_b32_e32 v144, v16
	v_mov_b32_e32 v145, v17
	v_mov_b32_e32 v146, v18
	v_mov_b32_e32 v147, v19
	v_mov_b32_e32 v124, v20
	v_mov_b32_e32 v125, v21
	v_mov_b32_e32 v126, v22
	v_mov_b32_e32 v127, v23
	v_mov_b32_e32 v104, v16
	v_mov_b32_e32 v105, v17
	v_mov_b32_e32 v106, v18
	v_mov_b32_e32 v107, v19
	v_mov_b32_e32 v148, v20
	v_mov_b32_e32 v149, v21
	v_mov_b32_e32 v150, v22
	v_mov_b32_e32 v151, v23
	v_mov_b32_e32 v88, v16
	v_mov_b32_e32 v89, v17
	v_mov_b32_e32 v90, v18
	v_mov_b32_e32 v91, v19
	v_mov_b32_e32 v64, v20
	v_mov_b32_e32 v65, v21
	v_mov_b32_e32 v66, v22
	v_mov_b32_e32 v67, v23
	v_mov_b32_e32 v40, v16
	v_mov_b32_e32 v41, v17
	v_mov_b32_e32 v42, v18
	v_mov_b32_e32 v43, v19
	v_mov_b32_e32 v92, v20
	v_mov_b32_e32 v93, v21
	v_mov_b32_e32 v94, v22
	v_mov_b32_e32 v95, v23
	v_mov_b32_e32 v60, v16
	v_mov_b32_e32 v61, v17
	v_mov_b32_e32 v62, v18
	v_mov_b32_e32 v63, v19
	v_mov_b32_e32 v36, v20
	v_mov_b32_e32 v37, v21
	v_mov_b32_e32 v38, v22
	v_mov_b32_e32 v39, v23
	v_mov_b32_e32 v24, v16
	v_mov_b32_e32 v25, v17
	v_mov_b32_e32 v26, v18
	v_mov_b32_e32 v27, v19
	v_mov_b32_e32 v68, v20
	v_mov_b32_e32 v69, v21
	v_mov_b32_e32 v70, v22
	v_mov_b32_e32 v71, v23
	v_mov_b32_e32 v32, v16
	v_mov_b32_e32 v33, v17
	v_mov_b32_e32 v34, v18
	v_mov_b32_e32 v35, v19
	v_mov_b32_e32 v80, v20
	v_mov_b32_e32 v81, v21
	v_mov_b32_e32 v82, v22
	v_mov_b32_e32 v83, v23
	v_mov_b32_e32 v44, v16
	v_mov_b32_e32 v45, v17
	v_mov_b32_e32 v46, v18
	v_mov_b32_e32 v47, v19
	v_mov_b32_e32 v112, v20
	v_mov_b32_e32 v113, v21
	v_mov_b32_e32 v114, v22
	v_mov_b32_e32 v115, v23
	v_mov_b32_e32 v72, v16
	v_mov_b32_e32 v73, v17
	v_mov_b32_e32 v74, v18
	v_mov_b32_e32 v75, v19
	v_mov_b32_e32 v116, v20
	v_mov_b32_e32 v117, v21
	v_mov_b32_e32 v118, v22
	v_mov_b32_e32 v119, v23
	v_mov_b32_e32 v84, v16
	v_mov_b32_e32 v85, v17
	v_mov_b32_e32 v86, v18
	v_mov_b32_e32 v87, v19
	v_mov_b32_e32 v128, v20
	v_mov_b32_e32 v129, v21
	v_mov_b32_e32 v130, v22
	v_mov_b32_e32 v131, v23
	v_mov_b32_e32 v96, v16
	v_mov_b32_e32 v97, v17
	v_mov_b32_e32 v98, v18
	v_mov_b32_e32 v99, v19
	v_add_u32_e32 v228, 0xfffe7c00, v183
	v_add_u32_e32 v229, 0xfffe8000, v183
	s_mov_b64 exec, s[72:73]
	buffer_load_dwordx4 v[140:143], v228, s[8:11], 0 offen
	buffer_load_dwordx4 v[120:123], v228, s[8:11], 0 offen offset:512
	s_mov_b64 exec, -1
	s_mov_b64 exec, s[68:69]
	buffer_load_dwordx4 v[152:155], v229, s[8:11], 0 offen offset:512
	buffer_load_dwordx4 v[132:135], v229, s[8:11], 0 offen offset:1024
	s_mov_b64 exec, -1
	s_mov_b64 exec, s[74:75]
	buffer_load_dwordx4 v[156:159], v229, s[8:11], 0 offen offset:2048
	buffer_load_dwordx4 v[144:147], v229, s[8:11], 0 offen offset:2560
	s_mov_b64 exec, -1
	v_add_u32_e32 v228, 0xfffffc00, v183
	s_mov_b64 exec, s[64:65]
	buffer_load_dwordx4 v[124:127], v228, s[8:11], 0 offen
	buffer_load_dwordx4 v[104:107], v228, s[8:11], 0 offen offset:512
	s_mov_b64 exec, -1
	buffer_load_dwordx4 v[136:139], v183, s[8:11], 0 offen offset:512
	buffer_load_dwordx4 v[108:111], v183, s[8:11], 0 offen offset:1024
	s_mov_b64 exec, s[66:67]
	buffer_load_dwordx4 v[148:151], v183, s[8:11], 0 offen offset:2048
	buffer_load_dwordx4 v[88:91], v183, s[8:11], 0 offen offset:2560
	s_mov_b64 exec, -1
	v_add_u32_e32 v228, 0x17c00, v183
	v_add_u32_e32 v229, 0x18000, v183
	s_mov_b64 exec, s[64:65]
	buffer_load_dwordx4 v[64:67], v228, s[8:11], 0 offen
	buffer_load_dwordx4 v[40:43], v228, s[8:11], 0 offen offset:512
	s_mov_b64 exec, -1
	buffer_load_dwordx4 v[76:79], v229, s[8:11], 0 offen offset:512
	buffer_load_dwordx4 v[48:51], v229, s[8:11], 0 offen offset:1024
	s_mov_b64 exec, s[66:67]
	buffer_load_dwordx4 v[92:95], v229, s[8:11], 0 offen offset:2048
	buffer_load_dwordx4 v[60:63], v229, s[8:11], 0 offen offset:2560
	s_mov_b64 exec, -1
	v_add_u32_e32 v228, 0x2fc00, v183
	v_add_u32_e32 v229, 0x30000, v183
	s_mov_b64 exec, s[64:65]
	buffer_load_dwordx4 v[36:39], v228, s[8:11], 0 offen
	buffer_load_dwordx4 v[24:27], v228, s[8:11], 0 offen offset:512
	s_mov_b64 exec, -1
	buffer_load_dwordx4 v[52:55], v229, s[8:11], 0 offen offset:512
	buffer_load_dwordx4 v[28:31], v229, s[8:11], 0 offen offset:1024
	s_mov_b64 exec, s[66:67]
	buffer_load_dwordx4 v[68:71], v229, s[8:11], 0 offen offset:2048
	buffer_load_dwordx4 v[32:35], v229, s[8:11], 0 offen offset:2560
	s_mov_b64 exec, -1
	v_add_u32_e32 v228, 0x18000, v183
	buffer_load_dwordx4 v[160:163], v228, s[8:11], 0 offen
	v_add_u32_e32 v228, 0x47c00, v183
	v_add_u32_e32 v229, 0x48000, v183
	v_add_u32_e32 v230, 0x5fc00, v183
	v_add_u32_e32 v231, 0x60000, v183
	s_waitcnt lgkmcnt(0)
	v_cvt_f16_f32_e32 v164, s0
	v_cvt_f16_f32_e32 v165, s1
	v_cvt_f16_f32_e32 v166, s4
	s_waitcnt vmcnt(7)
	v_pk_mul_f16 v167, v164, v168 op_sel_hi:[0,1]
	v_pk_mul_f16 v172, v164, v169 op_sel_hi:[0,1]
	v_pk_mul_f16 v173, v164, v170 op_sel_hi:[0,1]
	v_pk_mul_f16 v174, v164, v171 op_sel_hi:[0,1]
	v_pk_mul_f16 v175, v165, v170 op_sel_hi:[0,1]
	v_pk_mul_f16 v176, v165, v171 op_sel_hi:[0,1]
	v_pk_mul_f16 v177, v165, v169 op_sel_hi:[0,1]
	v_pk_mul_f16 v178, v165, v168 op_sel_hi:[0,1]
	v_pk_mul_f16 v179, v166, v171 op_sel_hi:[0,1]
	v_pk_mul_f16 v184, v166, v170 op_sel_hi:[0,1]
	v_pk_mul_f16 v185, v166, v169 op_sel_hi:[0,1]
	v_pk_mul_f16 v186, v166, v168 op_sel_hi:[0,1]
	v_pk_fma_f16 v143, v143, v171, v174
	v_pk_fma_f16 v142, v142, v170, v173
	v_pk_fma_f16 v141, v141, v169, v172
	v_pk_fma_f16 v140, v140, v168, v167
	v_pk_fma_f16 v155, v155, v171, v174
	v_pk_fma_f16 v154, v154, v170, v173
	v_pk_fma_f16 v153, v153, v169, v172
	v_pk_fma_f16 v152, v152, v168, v167
	v_pk_fma_f16 v159, v159, v171, v174
	v_pk_fma_f16 v158, v158, v170, v173
	v_pk_fma_f16 v157, v157, v169, v172
	v_pk_fma_f16 v156, v156, v168, v167
	v_pk_fma_f16 v167, v127, v171, v176
	v_pk_fma_f16 v172, v126, v170, v175
	v_pk_fma_f16 v173, v139, v171, v176
	v_pk_fma_f16 v174, v138, v170, v175
	v_pk_fma_f16 v176, v151, v171, v176
	v_pk_fma_f16 v175, v150, v170, v175
	v_pk_fma_f16 v187, v125, v169, v177
	v_pk_fma_f16 v188, v137, v169, v177
	v_pk_fma_f16 v177, v149, v169, v177
	v_pk_fma_f16 v189, v124, v168, v178
	v_pk_fma_f16 v190, v136, v168, v178
	v_pk_fma_f16 v178, v148, v168, v178
	v_pk_fma_f16 v191, v67, v171, v179
	v_pk_fma_f16 v192, v79, v171, v179
	v_pk_fma_f16 v171, v95, v171, v179
	v_pk_fma_f16 v179, v66, v170, v184
	v_pk_fma_f16 v193, v78, v170, v184
	v_pk_fma_f16 v170, v94, v170, v184
	v_pk_fma_f16 v184, v65, v169, v185
	v_pk_fma_f16 v194, v77, v169, v185
	v_pk_fma_f16 v169, v93, v169, v185
	v_pk_fma_f16 v185, v64, v168, v186
	v_pk_fma_f16 v195, v76, v168, v186
	v_pk_fma_f16 v168, v92, v168, v186
	v_pk_maximum3_f16 v186, v140, v152, v156
	v_pk_maximum3_f16 v196, v189, v190, v178
	v_pk_maximum3_f16 v198, v141, v153, v157
	v_pk_maximum3_f16 v199, v187, v188, v177
	v_pk_maximum3_f16 v200, v184, v194, v169
	v_pk_maximum3_f16 v197, v185, v195, v168
	v_pk_maximum3_f16 v201, v142, v154, v158
	v_pk_maximum3_f16 v202, v172, v174, v175
	v_pk_maximum3_f16 v203, v179, v193, v170
	v_pk_maximum3_f16 v204, v143, v155, v159
	v_pk_maximum3_f16 v205, v167, v173, v176
	v_pk_maximum3_f16 v206, v191, v192, v171
	v_pk_maximum3_f16 v186, v186, v196, v197
	v_pk_maximum3_f16 v196, v198, v199, v200
	v_pk_maximum3_f16 v197, v201, v202, v203
	s_waitcnt vmcnt(0)
	v_pk_mul_f16 v203, v166, v163 op_sel_hi:[0,1]
	v_pk_maximum3_f16 v198, v204, v205, v206
	v_pk_add_f16 v140, v140, v186 neg_lo:[0,1] neg_hi:[0,1]
	v_pk_add_f16 v141, v141, v196 neg_lo:[0,1] neg_hi:[0,1]
	v_pk_add_f16 v142, v142, v197 neg_lo:[0,1] neg_hi:[0,1]
	v_pk_add_f16 v143, v143, v198 neg_lo:[0,1] neg_hi:[0,1]
	v_pk_add_f16 v152, v152, v186 neg_lo:[0,1] neg_hi:[0,1]
	v_exp_f16_sdwa v199, v140 dst_sel:WORD_0 dst_unused:UNUSED_PAD src0_sel:WORD_0
	v_exp_f16_sdwa v200, v141 dst_sel:WORD_0 dst_unused:UNUSED_PAD src0_sel:WORD_0
	v_exp_f16_sdwa v201, v142 dst_sel:WORD_0 dst_unused:UNUSED_PAD src0_sel:WORD_0
	v_exp_f16_sdwa v202, v143 dst_sel:WORD_0 dst_unused:UNUSED_PAD src0_sel:WORD_0
	v_exp_f16_sdwa v199, v140 dst_sel:WORD_1 dst_unused:UNUSED_PRESERVE src0_sel:WORD_1
	v_exp_f16_sdwa v200, v141 dst_sel:WORD_1 dst_unused:UNUSED_PRESERVE src0_sel:WORD_1
	v_exp_f16_sdwa v201, v142 dst_sel:WORD_1 dst_unused:UNUSED_PRESERVE src0_sel:WORD_1
	v_exp_f16_sdwa v202, v143 dst_sel:WORD_1 dst_unused:UNUSED_PRESERVE src0_sel:WORD_1
	v_pk_add_f16 v153, v153, v196 neg_lo:[0,1] neg_hi:[0,1]
	v_pk_fma_f16 v123, v123, v202, 0
	v_pk_fma_f16 v120, v120, v199, 0
	v_pk_add_f16 v154, v154, v197 neg_lo:[0,1] neg_hi:[0,1]
	v_pk_add_f16 v155, v155, v198 neg_lo:[0,1] neg_hi:[0,1]
	v_pk_fma_f16 v122, v122, v201, 0
	v_exp_f16_sdwa v140, v152 dst_sel:WORD_0 dst_unused:UNUSED_PAD src0_sel:WORD_0
	v_exp_f16_sdwa v141, v153 dst_sel:WORD_0 dst_unused:UNUSED_PAD src0_sel:WORD_0
	v_exp_f16_sdwa v142, v154 dst_sel:WORD_0 dst_unused:UNUSED_PAD src0_sel:WORD_0
	v_exp_f16_sdwa v143, v155 dst_sel:WORD_0 dst_unused:UNUSED_PAD src0_sel:WORD_0
	v_exp_f16_sdwa v140, v152 dst_sel:WORD_1 dst_unused:UNUSED_PRESERVE src0_sel:WORD_1
	v_exp_f16_sdwa v141, v153 dst_sel:WORD_1 dst_unused:UNUSED_PRESERVE src0_sel:WORD_1
	v_exp_f16_sdwa v142, v154 dst_sel:WORD_1 dst_unused:UNUSED_PRESERVE src0_sel:WORD_1
	v_exp_f16_sdwa v143, v155 dst_sel:WORD_1 dst_unused:UNUSED_PRESERVE src0_sel:WORD_1
	v_pk_fma_f16 v121, v121, v200, 0
	v_pk_fma_f16 v120, v132, v140, v120
	v_pk_fma_f16 v123, v135, v143, v123
	s_mov_b64 exec, s[64:65]
	buffer_load_dwordx4 v[80:83], v228, s[8:11], 0 offen
	buffer_load_dwordx4 v[44:47], v228, s[8:11], 0 offen offset:512
	s_mov_b64 exec, -1
	v_pk_add_f16 v135, v159, v198 neg_lo:[0,1] neg_hi:[0,1]
	v_pk_fma_f16 v121, v133, v141, v121
	v_pk_fma_f16 v122, v134, v142, v122
	v_pk_add_f16 v132, v156, v186 neg_lo:[0,1] neg_hi:[0,1]
	v_pk_add_f16 v133, v157, v196 neg_lo:[0,1] neg_hi:[0,1]
	v_pk_add_f16 v134, v158, v197 neg_lo:[0,1] neg_hi:[0,1]
	v_pk_fma_f16 v204, v39, v163, v203
	v_exp_f16_sdwa v152, v132 dst_sel:WORD_0 dst_unused:UNUSED_PAD src0_sel:WORD_0
	v_exp_f16_sdwa v153, v133 dst_sel:WORD_0 dst_unused:UNUSED_PAD src0_sel:WORD_0
	v_exp_f16_sdwa v154, v134 dst_sel:WORD_0 dst_unused:UNUSED_PAD src0_sel:WORD_0
	v_exp_f16_sdwa v155, v135 dst_sel:WORD_0 dst_unused:UNUSED_PAD src0_sel:WORD_0
	v_exp_f16_sdwa v152, v132 dst_sel:WORD_1 dst_unused:UNUSED_PRESERVE src0_sel:WORD_1
	v_exp_f16_sdwa v153, v133 dst_sel:WORD_1 dst_unused:UNUSED_PRESERVE src0_sel:WORD_1
	v_exp_f16_sdwa v154, v134 dst_sel:WORD_1 dst_unused:UNUSED_PRESERVE src0_sel:WORD_1
	v_exp_f16_sdwa v155, v135 dst_sel:WORD_1 dst_unused:UNUSED_PRESERVE src0_sel:WORD_1
	v_pk_mul_f16 v135, v164, v163 op_sel_hi:[0,1]
	v_pk_fma_f16 v120, v144, v152, v120
	v_pk_mul_f16 v144, v165, v163 op_sel_hi:[0,1]
	v_pk_fma_f16 v123, v147, v155, v123
	v_pk_fma_f16 v122, v146, v154, v122
	v_pk_fma_f16 v121, v145, v153, v121
	v_pk_mul_f16 v132, v164, v160 op_sel_hi:[0,1]
	v_pk_mul_f16 v133, v164, v161 op_sel_hi:[0,1]
	v_pk_mul_f16 v134, v164, v162 op_sel_hi:[0,1]
	v_pk_fma_f16 v127, v127, v163, v135
	v_pk_fma_f16 v139, v139, v163, v135
	v_pk_fma_f16 v135, v151, v163, v135
	v_pk_fma_f16 v145, v67, v163, v144
	v_pk_fma_f16 v146, v79, v163, v144
	v_pk_fma_f16 v144, v95, v163, v144
	v_pk_mul_f16 v147, v165, v162 op_sel_hi:[0,1]
	v_pk_fma_f16 v205, v55, v163, v203
	buffer_load_dwordx4 v[100:103], v229, s[8:11], 0 offen offset:512
	buffer_load_dwordx4 v[56:59], v229, s[8:11], 0 offen offset:1024
	v_pk_fma_f16 v163, v71, v163, v203
	v_pk_mul_f16 v203, v166, v162 op_sel_hi:[0,1]
	v_pk_fma_f16 v126, v126, v162, v134
	v_pk_fma_f16 v125, v125, v161, v133
	v_pk_fma_f16 v124, v124, v160, v132
	v_pk_fma_f16 v138, v138, v162, v134
	v_pk_fma_f16 v137, v137, v161, v133
	v_pk_fma_f16 v136, v136, v160, v132
	v_pk_fma_f16 v134, v150, v162, v134
	v_pk_fma_f16 v133, v149, v161, v133
	v_pk_fma_f16 v132, v148, v160, v132
	v_pk_fma_f16 v148, v66, v162, v147
	v_pk_fma_f16 v149, v78, v162, v147
	v_pk_fma_f16 v147, v94, v162, v147
	v_pk_mul_f16 v150, v165, v161 op_sel_hi:[0,1]
	v_pk_fma_f16 v206, v38, v162, v203
	v_pk_fma_f16 v207, v54, v162, v203
	v_pk_fma_f16 v162, v70, v162, v203
	v_pk_mul_f16 v203, v166, v161 op_sel_hi:[0,1]
	v_pk_fma_f16 v151, v65, v161, v150
	v_pk_fma_f16 v156, v77, v161, v150
	v_pk_fma_f16 v150, v93, v161, v150
	v_pk_mul_f16 v157, v165, v160 op_sel_hi:[0,1]
	s_mov_b64 exec, s[66:67]
	buffer_load_dwordx4 v[112:115], v229, s[8:11], 0 offen offset:2048
	buffer_load_dwordx4 v[72:75], v229, s[8:11], 0 offen offset:2560
	s_mov_b64 exec, -1
	v_pk_fma_f16 v208, v37, v161, v203
	v_pk_fma_f16 v209, v53, v161, v203
	v_pk_fma_f16 v161, v69, v161, v203
	v_pk_mul_f16 v203, v166, v160 op_sel_hi:[0,1]
	v_pk_fma_f16 v158, v64, v160, v157
	v_pk_fma_f16 v159, v76, v160, v157
	v_pk_fma_f16 v157, v92, v160, v157
	v_pk_fma_f16 v210, v36, v160, v203
	v_pk_fma_f16 v211, v52, v160, v203
	v_pk_fma_f16 v160, v68, v160, v203
	v_pk_maximum3_f16 v203, v124, v136, v132
	v_pk_maximum3_f16 v212, v158, v159, v157
	v_pk_maximum3_f16 v214, v208, v209, v161
	v_pk_maximum3_f16 v215, v206, v207, v162
	v_pk_maximum3_f16 v216, v204, v205, v163
	v_pk_maximum3_f16 v213, v210, v211, v160
	v_pk_add_f16 v189, v189, v186 neg_lo:[0,1] neg_hi:[0,1]
	v_pk_maximum3_f16 v203, v203, v212, v213
	v_pk_maximum3_f16 v212, v125, v137, v133
	v_pk_maximum3_f16 v213, v151, v156, v150
	v_pk_add_f16 v187, v187, v196 neg_lo:[0,1] neg_hi:[0,1]
	v_pk_maximum3_f16 v212, v212, v213, v214
	v_pk_maximum3_f16 v213, v126, v138, v134
	v_pk_maximum3_f16 v214, v148, v149, v147
	v_pk_add_f16 v172, v172, v197 neg_lo:[0,1] neg_hi:[0,1]
	v_pk_maximum3_f16 v213, v213, v214, v215
	v_pk_maximum3_f16 v214, v127, v139, v135
	v_pk_maximum3_f16 v215, v145, v146, v144
	v_pk_add_f16 v167, v167, v198 neg_lo:[0,1] neg_hi:[0,1]
	v_pk_maximum3_f16 v214, v214, v215, v216
	v_exp_f16_sdwa v215, v189 dst_sel:WORD_0 dst_unused:UNUSED_PAD src0_sel:WORD_0
	v_exp_f16_sdwa v216, v187 dst_sel:WORD_0 dst_unused:UNUSED_PAD src0_sel:WORD_0
	v_exp_f16_sdwa v217, v172 dst_sel:WORD_0 dst_unused:UNUSED_PAD src0_sel:WORD_0
	v_exp_f16_sdwa v218, v167 dst_sel:WORD_0 dst_unused:UNUSED_PAD src0_sel:WORD_0
	v_exp_f16_sdwa v215, v189 dst_sel:WORD_1 dst_unused:UNUSED_PRESERVE src0_sel:WORD_1
	v_exp_f16_sdwa v216, v187 dst_sel:WORD_1 dst_unused:UNUSED_PRESERVE src0_sel:WORD_1
	v_exp_f16_sdwa v217, v172 dst_sel:WORD_1 dst_unused:UNUSED_PRESERVE src0_sel:WORD_1
	v_exp_f16_sdwa v218, v167 dst_sel:WORD_1 dst_unused:UNUSED_PRESERVE src0_sel:WORD_1
	v_xor_b32_e32 v167, 0x80008000, v214
	v_xor_b32_e32 v172, 0x80008000, v213
	v_xor_b32_e32 v187, 0x80008000, v212
	v_xor_b32_e32 v189, 0x80008000, v203
	v_pk_add_f16 v124, v124, v189
	v_pk_add_f16 v125, v125, v187
	v_pk_add_f16 v126, v126, v172
	v_pk_add_f16 v127, v127, v167
	v_pk_fma_f16 v120, v104, v215, v120
	v_pk_fma_f16 v121, v105, v216, v121
	v_exp_f16_sdwa v203, v124 dst_sel:WORD_0 dst_unused:UNUSED_PAD src0_sel:WORD_0
	v_exp_f16_sdwa v212, v125 dst_sel:WORD_0 dst_unused:UNUSED_PAD src0_sel:WORD_0
	v_exp_f16_sdwa v213, v126 dst_sel:WORD_0 dst_unused:UNUSED_PAD src0_sel:WORD_0
	v_exp_f16_sdwa v214, v127 dst_sel:WORD_0 dst_unused:UNUSED_PAD src0_sel:WORD_0
	v_exp_f16_sdwa v203, v124 dst_sel:WORD_1 dst_unused:UNUSED_PRESERVE src0_sel:WORD_1
	v_exp_f16_sdwa v212, v125 dst_sel:WORD_1 dst_unused:UNUSED_PRESERVE src0_sel:WORD_1
	v_exp_f16_sdwa v213, v126 dst_sel:WORD_1 dst_unused:UNUSED_PRESERVE src0_sel:WORD_1
	v_exp_f16_sdwa v214, v127 dst_sel:WORD_1 dst_unused:UNUSED_PRESERVE src0_sel:WORD_1
	v_pk_add_f16 v124, v190, v186 neg_lo:[0,1] neg_hi:[0,1]
	v_pk_fma_f16 v105, v105, v212, 0
	v_pk_fma_f16 v104, v104, v203, 0
	v_pk_add_f16 v125, v188, v196 neg_lo:[0,1] neg_hi:[0,1]
	v_pk_add_f16 v126, v174, v197 neg_lo:[0,1] neg_hi:[0,1]
	v_pk_add_f16 v127, v173, v198 neg_lo:[0,1] neg_hi:[0,1]
	v_pk_fma_f16 v122, v106, v217, v122
	v_pk_fma_f16 v123, v107, v218, v123
	s_mov_b64 exec, s[76:77]
	buffer_load_dwordx4 v[116:119], v230, s[8:11], 0 offen
	buffer_load_dwordx4 v[84:87], v230, s[8:11], 0 offen offset:512
	s_mov_b64 exec, -1
	v_pk_fma_f16 v107, v107, v214, 0
	v_pk_fma_f16 v106, v106, v213, 0
	v_exp_f16_sdwa v173, v124 dst_sel:WORD_0 dst_unused:UNUSED_PAD src0_sel:WORD_0
	v_exp_f16_sdwa v174, v125 dst_sel:WORD_0 dst_unused:UNUSED_PAD src0_sel:WORD_0
	v_exp_f16_sdwa v188, v126 dst_sel:WORD_0 dst_unused:UNUSED_PAD src0_sel:WORD_0
	v_exp_f16_sdwa v190, v127 dst_sel:WORD_0 dst_unused:UNUSED_PAD src0_sel:WORD_0
	v_exp_f16_sdwa v173, v124 dst_sel:WORD_1 dst_unused:UNUSED_PRESERVE src0_sel:WORD_1
	v_exp_f16_sdwa v174, v125 dst_sel:WORD_1 dst_unused:UNUSED_PRESERVE src0_sel:WORD_1
	v_exp_f16_sdwa v188, v126 dst_sel:WORD_1 dst_unused:UNUSED_PRESERVE src0_sel:WORD_1
	v_exp_f16_sdwa v190, v127 dst_sel:WORD_1 dst_unused:UNUSED_PRESERVE src0_sel:WORD_1
	v_pk_add_f16 v124, v136, v189
	v_pk_add_f16 v125, v137, v187
	v_pk_add_f16 v126, v138, v172
	v_pk_add_f16 v127, v139, v167
	v_pk_fma_f16 v123, v111, v190, v123
	v_exp_f16_sdwa v136, v124 dst_sel:WORD_0 dst_unused:UNUSED_PAD src0_sel:WORD_0
	v_exp_f16_sdwa v137, v125 dst_sel:WORD_0 dst_unused:UNUSED_PAD src0_sel:WORD_0
	v_exp_f16_sdwa v138, v126 dst_sel:WORD_0 dst_unused:UNUSED_PAD src0_sel:WORD_0
	v_exp_f16_sdwa v139, v127 dst_sel:WORD_0 dst_unused:UNUSED_PAD src0_sel:WORD_0
	v_exp_f16_sdwa v136, v124 dst_sel:WORD_1 dst_unused:UNUSED_PRESERVE src0_sel:WORD_1
	v_exp_f16_sdwa v137, v125 dst_sel:WORD_1 dst_unused:UNUSED_PRESERVE src0_sel:WORD_1
	v_exp_f16_sdwa v138, v126 dst_sel:WORD_1 dst_unused:UNUSED_PRESERVE src0_sel:WORD_1
	v_exp_f16_sdwa v139, v127 dst_sel:WORD_1 dst_unused:UNUSED_PRESERVE src0_sel:WORD_1
	v_pk_fma_f16 v122, v110, v188, v122
	v_pk_fma_f16 v219, v108, v136, v104
	v_pk_fma_f16 v220, v109, v137, v105
	v_pk_add_f16 v104, v199, 0
	v_pk_add_f16 v105, v200, 0
	v_pk_fma_f16 v221, v110, v138, v106
	v_pk_fma_f16 v222, v111, v139, v107
	v_pk_add_f16 v104, v104, v140
	v_pk_add_f16 v105, v105, v141
	v_pk_add_f16 v106, v201, 0
	v_pk_add_f16 v107, v202, 0
	v_pk_add_f16 v106, v106, v142
	v_pk_add_f16 v107, v107, v143
	v_pk_add_f16 v105, v105, v153
	v_pk_add_f16 v104, v104, v152
	v_pk_add_f16 v107, v107, v155
	v_pk_add_f16 v106, v106, v154
	v_pk_add_f16 v104, v104, v215
	s_mov_b64 exec, s[70:71]
	buffer_load_dwordx4 v[128:131], v231, s[8:11], 0 offen offset:512
	buffer_load_dwordx4 v[96:99], v231, s[8:11], 0 offen offset:1024
	s_mov_b64 exec, -1
	v_pk_add_f16 v105, v105, v216
	v_pk_add_f16 v106, v106, v217
	v_pk_add_f16 v107, v107, v218
	v_pk_add_f16 v105, v105, v174
	v_pk_add_f16 v104, v104, v173
	v_pk_fma_f16 v121, v109, v174, v121
	v_pk_fma_f16 v120, v108, v173, v120
	v_pk_add_f16 v107, v107, v190
	v_pk_add_f16 v106, v106, v188
	v_pk_add_f16 v108, v178, v186 neg_lo:[0,1] neg_hi:[0,1]
	v_pk_add_f16 v109, v177, v196 neg_lo:[0,1] neg_hi:[0,1]
	v_pk_add_f16 v110, v175, v197 neg_lo:[0,1] neg_hi:[0,1]
	v_pk_add_f16 v111, v176, v198 neg_lo:[0,1] neg_hi:[0,1]
	v_pk_add_f16 v132, v132, v189
	v_exp_f16_sdwa v124, v108 dst_sel:WORD_0 dst_unused:UNUSED_PAD src0_sel:WORD_0
	v_exp_f16_sdwa v125, v109 dst_sel:WORD_0 dst_unused:UNUSED_PAD src0_sel:WORD_0
	v_exp_f16_sdwa v126, v110 dst_sel:WORD_0 dst_unused:UNUSED_PAD src0_sel:WORD_0
	v_exp_f16_sdwa v127, v111 dst_sel:WORD_0 dst_unused:UNUSED_PAD src0_sel:WORD_0
	v_exp_f16_sdwa v124, v108 dst_sel:WORD_1 dst_unused:UNUSED_PRESERVE src0_sel:WORD_1
	v_exp_f16_sdwa v125, v109 dst_sel:WORD_1 dst_unused:UNUSED_PRESERVE src0_sel:WORD_1
	v_exp_f16_sdwa v126, v110 dst_sel:WORD_1 dst_unused:UNUSED_PRESERVE src0_sel:WORD_1
	v_exp_f16_sdwa v127, v111 dst_sel:WORD_1 dst_unused:UNUSED_PRESERVE src0_sel:WORD_1
	v_pk_add_f16 v133, v133, v187
	v_pk_add_f16 v104, v104, v124
	v_pk_add_f16 v105, v105, v125
	v_pk_fma_f16 v108, v88, v124, v120
	v_pk_fma_f16 v109, v89, v125, v121
	v_pk_add_f16 v106, v106, v126
	v_pk_fma_f16 v110, v90, v126, v122
	v_pk_add_f16 v107, v107, v127
	v_pk_fma_f16 v111, v91, v127, v123
	v_pk_add_f16 v120, v185, v186 neg_lo:[0,1] neg_hi:[0,1]
	s_mov_b64 exec, s[78:79]
	buffer_load_dwordx4 v[20:23], v231, s[8:11], 0 offen offset:2048
	buffer_load_dwordx4 v[16:19], v231, s[8:11], 0 offen offset:2560
	s_mov_b64 exec, -1
	v_pk_add_f16 v121, v184, v196 neg_lo:[0,1] neg_hi:[0,1]
	v_pk_add_f16 v122, v179, v197 neg_lo:[0,1] neg_hi:[0,1]
	v_pk_add_f16 v123, v191, v198 neg_lo:[0,1] neg_hi:[0,1]
	v_pk_add_f16 v134, v134, v172
	v_exp_f16_sdwa v124, v120 dst_sel:WORD_0 dst_unused:UNUSED_PAD src0_sel:WORD_0
	v_exp_f16_sdwa v125, v121 dst_sel:WORD_0 dst_unused:UNUSED_PAD src0_sel:WORD_0
	v_exp_f16_sdwa v126, v122 dst_sel:WORD_0 dst_unused:UNUSED_PAD src0_sel:WORD_0
	v_exp_f16_sdwa v127, v123 dst_sel:WORD_0 dst_unused:UNUSED_PAD src0_sel:WORD_0
	v_exp_f16_sdwa v124, v120 dst_sel:WORD_1 dst_unused:UNUSED_PRESERVE src0_sel:WORD_1
	v_exp_f16_sdwa v125, v121 dst_sel:WORD_1 dst_unused:UNUSED_PRESERVE src0_sel:WORD_1
	v_exp_f16_sdwa v126, v122 dst_sel:WORD_1 dst_unused:UNUSED_PRESERVE src0_sel:WORD_1
	v_exp_f16_sdwa v127, v123 dst_sel:WORD_1 dst_unused:UNUSED_PRESERVE src0_sel:WORD_1
	v_pk_add_f16 v120, v195, v186 neg_lo:[0,1] neg_hi:[0,1]
	v_pk_add_f16 v105, v105, v125
	v_pk_add_f16 v104, v104, v124
	v_pk_add_f16 v107, v107, v127
	v_pk_fma_f16 v111, v43, v127, v111
	v_pk_add_f16 v106, v106, v126
	v_pk_fma_f16 v110, v42, v126, v110
	v_pk_fma_f16 v109, v41, v125, v109
	v_pk_fma_f16 v108, v40, v124, v108
	v_pk_add_f16 v121, v194, v196 neg_lo:[0,1] neg_hi:[0,1]
	v_pk_add_f16 v122, v193, v197 neg_lo:[0,1] neg_hi:[0,1]
	v_pk_add_f16 v123, v192, v198 neg_lo:[0,1] neg_hi:[0,1]
	v_pk_add_f16 v135, v135, v167
	v_exp_f16_sdwa v124, v120 dst_sel:WORD_0 dst_unused:UNUSED_PAD src0_sel:WORD_0
	v_exp_f16_sdwa v125, v121 dst_sel:WORD_0 dst_unused:UNUSED_PAD src0_sel:WORD_0
	v_exp_f16_sdwa v126, v122 dst_sel:WORD_0 dst_unused:UNUSED_PAD src0_sel:WORD_0
	v_exp_f16_sdwa v127, v123 dst_sel:WORD_0 dst_unused:UNUSED_PAD src0_sel:WORD_0
	v_exp_f16_sdwa v124, v120 dst_sel:WORD_1 dst_unused:UNUSED_PRESERVE src0_sel:WORD_1
	v_exp_f16_sdwa v125, v121 dst_sel:WORD_1 dst_unused:UNUSED_PRESERVE src0_sel:WORD_1
	v_exp_f16_sdwa v126, v122 dst_sel:WORD_1 dst_unused:UNUSED_PRESERVE src0_sel:WORD_1
	v_exp_f16_sdwa v127, v123 dst_sel:WORD_1 dst_unused:UNUSED_PRESERVE src0_sel:WORD_1
	v_pk_add_f16 v120, v168, v186 neg_lo:[0,1] neg_hi:[0,1]
	v_pk_add_f16 v104, v104, v124
	v_pk_add_f16 v105, v105, v125
	v_pk_fma_f16 v108, v48, v124, v108
	v_pk_fma_f16 v109, v49, v125, v109
	v_pk_add_f16 v106, v106, v126
	v_pk_fma_f16 v110, v50, v126, v110
	v_pk_add_f16 v107, v107, v127
	v_pk_fma_f16 v111, v51, v127, v111
	v_pk_add_f16 v121, v169, v196 neg_lo:[0,1] neg_hi:[0,1]
	v_pk_add_f16 v122, v170, v197 neg_lo:[0,1] neg_hi:[0,1]
	v_pk_add_f16 v123, v171, v198 neg_lo:[0,1] neg_hi:[0,1]
	v_exp_f16_sdwa v124, v120 dst_sel:WORD_0 dst_unused:UNUSED_PAD src0_sel:WORD_0
	v_exp_f16_sdwa v125, v121 dst_sel:WORD_0 dst_unused:UNUSED_PAD src0_sel:WORD_0
	v_exp_f16_sdwa v126, v122 dst_sel:WORD_0 dst_unused:UNUSED_PAD src0_sel:WORD_0
	v_exp_f16_sdwa v127, v123 dst_sel:WORD_0 dst_unused:UNUSED_PAD src0_sel:WORD_0
	v_exp_f16_sdwa v124, v120 dst_sel:WORD_1 dst_unused:UNUSED_PRESERVE src0_sel:WORD_1
	v_exp_f16_sdwa v125, v121 dst_sel:WORD_1 dst_unused:UNUSED_PRESERVE src0_sel:WORD_1
	v_exp_f16_sdwa v126, v122 dst_sel:WORD_1 dst_unused:UNUSED_PRESERVE src0_sel:WORD_1
	v_exp_f16_sdwa v127, v123 dst_sel:WORD_1 dst_unused:UNUSED_PRESERVE src0_sel:WORD_1
	v_pk_add_f16 v123, v213, 0
	v_pk_add_f16 v105, v105, v125
	v_pk_add_f16 v104, v104, v124
	v_rcp_f16_e32 v121, v105
	v_rcp_f16_e32 v120, v104
	v_rcp_f16_sdwa v104, v104 dst_sel:DWORD dst_unused:UNUSED_PAD src0_sel:WORD_1
	v_rcp_f16_sdwa v105, v105 dst_sel:DWORD dst_unused:UNUSED_PAD src0_sel:WORD_1
	v_pk_add_f16 v107, v107, v127
	v_pk_add_f16 v106, v106, v126
	v_pk_fma_f16 v109, v61, v125, v109
	v_pk_fma_f16 v108, v60, v124, v108
	v_pack_b32_f16 v104, v120, v104
	v_pack_b32_f16 v105, v121, v105
	v_pk_mul_f16 v124, v108, v104
	v_rcp_f16_e32 v108, v106
	v_rcp_f16_sdwa v106, v106 dst_sel:DWORD dst_unused:UNUSED_PAD src0_sel:WORD_1
	v_pk_mul_f16 v125, v109, v105
	v_rcp_f16_e32 v105, v107
	v_rcp_f16_sdwa v107, v107 dst_sel:DWORD dst_unused:UNUSED_PAD src0_sel:WORD_1
	v_pk_fma_f16 v111, v63, v127, v111
	v_pk_fma_f16 v110, v62, v126, v110
	v_pack_b32_f16 v106, v108, v106
	v_pack_b32_f16 v105, v105, v107
	v_add_u32_e32 v104, 0x30000, v183
	v_pk_mul_f16 v126, v110, v106
	v_pk_mul_f16 v127, v111, v105
	v_pk_add_f16 v105, v212, 0
	v_pk_add_f16 v106, v203, 0
	v_add_u32_e32 v120, 0x48000, v183
	v_pk_add_f16 v121, v106, v136
	v_pk_add_f16 v122, v105, v137
	buffer_load_dwordx4 v[108:111], v104, s[8:11], 0 offen
	s_nop 0
	buffer_load_dwordx4 v[104:107], v120, s[8:11], 0 offen
	v_pk_add_f16 v120, v214, 0
	v_pk_add_f16 v123, v123, v138
	v_pk_add_f16 v120, v120, v139
	v_exp_f16_sdwa v136, v132 dst_sel:WORD_0 dst_unused:UNUSED_PAD src0_sel:WORD_0
	v_exp_f16_sdwa v137, v133 dst_sel:WORD_0 dst_unused:UNUSED_PAD src0_sel:WORD_0
	v_exp_f16_sdwa v138, v134 dst_sel:WORD_0 dst_unused:UNUSED_PAD src0_sel:WORD_0
	v_exp_f16_sdwa v139, v135 dst_sel:WORD_0 dst_unused:UNUSED_PAD src0_sel:WORD_0
	v_exp_f16_sdwa v136, v132 dst_sel:WORD_1 dst_unused:UNUSED_PRESERVE src0_sel:WORD_1
	v_exp_f16_sdwa v137, v133 dst_sel:WORD_1 dst_unused:UNUSED_PRESERVE src0_sel:WORD_1
	v_exp_f16_sdwa v138, v134 dst_sel:WORD_1 dst_unused:UNUSED_PRESERVE src0_sel:WORD_1
	v_exp_f16_sdwa v139, v135 dst_sel:WORD_1 dst_unused:UNUSED_PRESERVE src0_sel:WORD_1
	v_pk_add_f16 v132, v158, v189
	v_pk_add_f16 v121, v121, v136
	v_pk_add_f16 v120, v120, v139
	v_pk_add_f16 v123, v123, v138
	v_pk_add_f16 v122, v122, v137
	v_pk_fma_f16 v91, v91, v139, v222
	v_pk_fma_f16 v90, v90, v138, v221
	v_pk_fma_f16 v89, v89, v137, v220
	v_pk_fma_f16 v88, v88, v136, v219
	v_pk_add_f16 v133, v151, v187
	v_pk_add_f16 v134, v148, v172
	v_pk_add_f16 v135, v145, v167
	v_exp_f16_sdwa v136, v132 dst_sel:WORD_0 dst_unused:UNUSED_PAD src0_sel:WORD_0
	v_exp_f16_sdwa v137, v133 dst_sel:WORD_0 dst_unused:UNUSED_PAD src0_sel:WORD_0
	v_exp_f16_sdwa v138, v134 dst_sel:WORD_0 dst_unused:UNUSED_PAD src0_sel:WORD_0
	v_exp_f16_sdwa v139, v135 dst_sel:WORD_0 dst_unused:UNUSED_PAD src0_sel:WORD_0
	v_exp_f16_sdwa v136, v132 dst_sel:WORD_1 dst_unused:UNUSED_PRESERVE src0_sel:WORD_1
	v_exp_f16_sdwa v137, v133 dst_sel:WORD_1 dst_unused:UNUSED_PRESERVE src0_sel:WORD_1
	v_exp_f16_sdwa v138, v134 dst_sel:WORD_1 dst_unused:UNUSED_PRESERVE src0_sel:WORD_1
	v_exp_f16_sdwa v139, v135 dst_sel:WORD_1 dst_unused:UNUSED_PRESERVE src0_sel:WORD_1
	v_pk_add_f16 v132, v159, v189
	v_pk_add_f16 v121, v121, v136
	v_pk_add_f16 v122, v122, v137
	v_pk_add_f16 v123, v123, v138
	v_pk_add_f16 v120, v120, v139
	v_pk_fma_f16 v88, v40, v136, v88
	v_pk_fma_f16 v89, v41, v137, v89
	v_pk_fma_f16 v90, v42, v138, v90
	v_pk_fma_f16 v91, v43, v139, v91
	v_pk_add_f16 v133, v156, v187
	v_pk_add_f16 v134, v149, v172
	v_pk_add_f16 v135, v146, v167
	v_exp_f16_sdwa v136, v132 dst_sel:WORD_0 dst_unused:UNUSED_PAD src0_sel:WORD_0
	v_exp_f16_sdwa v137, v133 dst_sel:WORD_0 dst_unused:UNUSED_PAD src0_sel:WORD_0
	v_exp_f16_sdwa v138, v134 dst_sel:WORD_0 dst_unused:UNUSED_PAD src0_sel:WORD_0
	v_exp_f16_sdwa v139, v135 dst_sel:WORD_0 dst_unused:UNUSED_PAD src0_sel:WORD_0
	v_exp_f16_sdwa v136, v132 dst_sel:WORD_1 dst_unused:UNUSED_PRESERVE src0_sel:WORD_1
	v_exp_f16_sdwa v137, v133 dst_sel:WORD_1 dst_unused:UNUSED_PRESERVE src0_sel:WORD_1
	v_exp_f16_sdwa v138, v134 dst_sel:WORD_1 dst_unused:UNUSED_PRESERVE src0_sel:WORD_1
	v_exp_f16_sdwa v139, v135 dst_sel:WORD_1 dst_unused:UNUSED_PRESERVE src0_sel:WORD_1
	v_pk_add_f16 v132, v157, v189
	v_pk_add_f16 v121, v121, v136
	v_pk_add_f16 v120, v120, v139
	v_pk_add_f16 v123, v123, v138
	v_pk_add_f16 v122, v122, v137
	v_pk_fma_f16 v91, v51, v139, v91
	v_pk_fma_f16 v90, v50, v138, v90
	v_pk_fma_f16 v89, v49, v137, v89
	v_pk_fma_f16 v88, v48, v136, v88
	v_pk_add_f16 v133, v150, v187
	v_pk_add_f16 v134, v147, v172
	v_pk_add_f16 v135, v144, v167
	v_exp_f16_sdwa v136, v132 dst_sel:WORD_0 dst_unused:UNUSED_PAD src0_sel:WORD_0
	v_exp_f16_sdwa v137, v133 dst_sel:WORD_0 dst_unused:UNUSED_PAD src0_sel:WORD_0
	v_exp_f16_sdwa v138, v134 dst_sel:WORD_0 dst_unused:UNUSED_PAD src0_sel:WORD_0
	v_exp_f16_sdwa v139, v135 dst_sel:WORD_0 dst_unused:UNUSED_PAD src0_sel:WORD_0
	v_exp_f16_sdwa v136, v132 dst_sel:WORD_1 dst_unused:UNUSED_PRESERVE src0_sel:WORD_1
	v_exp_f16_sdwa v137, v133 dst_sel:WORD_1 dst_unused:UNUSED_PRESERVE src0_sel:WORD_1
	v_exp_f16_sdwa v138, v134 dst_sel:WORD_1 dst_unused:UNUSED_PRESERVE src0_sel:WORD_1
	v_exp_f16_sdwa v139, v135 dst_sel:WORD_1 dst_unused:UNUSED_PRESERVE src0_sel:WORD_1
	v_pk_add_f16 v132, v210, v189
	v_pk_add_f16 v121, v121, v136
	v_pk_add_f16 v122, v122, v137
	v_pk_add_f16 v123, v123, v138
	v_pk_add_f16 v120, v120, v139
	v_pk_fma_f16 v88, v60, v136, v88
	v_pk_fma_f16 v89, v61, v137, v89
	v_pk_fma_f16 v90, v62, v138, v90
	v_pk_fma_f16 v91, v63, v139, v91
	v_pk_add_f16 v133, v208, v187
	v_pk_add_f16 v134, v206, v172
	v_pk_add_f16 v135, v204, v167
	v_exp_f16_sdwa v136, v132 dst_sel:WORD_0 dst_unused:UNUSED_PAD src0_sel:WORD_0
	v_exp_f16_sdwa v137, v133 dst_sel:WORD_0 dst_unused:UNUSED_PAD src0_sel:WORD_0
	v_exp_f16_sdwa v138, v134 dst_sel:WORD_0 dst_unused:UNUSED_PAD src0_sel:WORD_0
	v_exp_f16_sdwa v139, v135 dst_sel:WORD_0 dst_unused:UNUSED_PAD src0_sel:WORD_0
	v_exp_f16_sdwa v136, v132 dst_sel:WORD_1 dst_unused:UNUSED_PRESERVE src0_sel:WORD_1
	v_exp_f16_sdwa v137, v133 dst_sel:WORD_1 dst_unused:UNUSED_PRESERVE src0_sel:WORD_1
	v_exp_f16_sdwa v138, v134 dst_sel:WORD_1 dst_unused:UNUSED_PRESERVE src0_sel:WORD_1
	v_exp_f16_sdwa v139, v135 dst_sel:WORD_1 dst_unused:UNUSED_PRESERVE src0_sel:WORD_1
	v_pk_add_f16 v132, v211, v189
	v_pk_add_f16 v121, v121, v136
	v_pk_add_f16 v120, v120, v139
	v_pk_add_f16 v123, v123, v138
	v_pk_add_f16 v122, v122, v137
	v_pk_fma_f16 v91, v27, v139, v91
	v_pk_fma_f16 v90, v26, v138, v90
	v_pk_fma_f16 v89, v25, v137, v89
	v_pk_fma_f16 v88, v24, v136, v88
	v_pk_add_f16 v133, v209, v187
	v_pk_add_f16 v134, v207, v172
	v_pk_add_f16 v135, v205, v167
	v_exp_f16_sdwa v136, v132 dst_sel:WORD_0 dst_unused:UNUSED_PAD src0_sel:WORD_0
	v_exp_f16_sdwa v137, v133 dst_sel:WORD_0 dst_unused:UNUSED_PAD src0_sel:WORD_0
	v_exp_f16_sdwa v138, v134 dst_sel:WORD_0 dst_unused:UNUSED_PAD src0_sel:WORD_0
	v_exp_f16_sdwa v139, v135 dst_sel:WORD_0 dst_unused:UNUSED_PAD src0_sel:WORD_0
	v_exp_f16_sdwa v136, v132 dst_sel:WORD_1 dst_unused:UNUSED_PRESERVE src0_sel:WORD_1
	v_exp_f16_sdwa v137, v133 dst_sel:WORD_1 dst_unused:UNUSED_PRESERVE src0_sel:WORD_1
	v_exp_f16_sdwa v138, v134 dst_sel:WORD_1 dst_unused:UNUSED_PRESERVE src0_sel:WORD_1
	v_exp_f16_sdwa v139, v135 dst_sel:WORD_1 dst_unused:UNUSED_PRESERVE src0_sel:WORD_1
	v_pk_add_f16 v132, v160, v189
	v_pk_add_f16 v121, v121, v136
	v_pk_add_f16 v122, v122, v137
	v_pk_add_f16 v123, v123, v138
	v_pk_add_f16 v120, v120, v139
	v_pk_fma_f16 v88, v28, v136, v88
	v_pk_fma_f16 v89, v29, v137, v89
	v_pk_fma_f16 v90, v30, v138, v90
	v_pk_fma_f16 v91, v31, v139, v91
	v_pk_add_f16 v133, v161, v187
	v_pk_add_f16 v134, v162, v172
	v_pk_add_f16 v135, v163, v167
	v_exp_f16_sdwa v136, v132 dst_sel:WORD_0 dst_unused:UNUSED_PAD src0_sel:WORD_0
	v_exp_f16_sdwa v137, v133 dst_sel:WORD_0 dst_unused:UNUSED_PAD src0_sel:WORD_0
	v_exp_f16_sdwa v138, v134 dst_sel:WORD_0 dst_unused:UNUSED_PAD src0_sel:WORD_0
	v_exp_f16_sdwa v139, v135 dst_sel:WORD_0 dst_unused:UNUSED_PAD src0_sel:WORD_0
	v_exp_f16_sdwa v136, v132 dst_sel:WORD_1 dst_unused:UNUSED_PRESERVE src0_sel:WORD_1
	v_exp_f16_sdwa v137, v133 dst_sel:WORD_1 dst_unused:UNUSED_PRESERVE src0_sel:WORD_1
	v_exp_f16_sdwa v138, v134 dst_sel:WORD_1 dst_unused:UNUSED_PRESERVE src0_sel:WORD_1
	v_exp_f16_sdwa v139, v135 dst_sel:WORD_1 dst_unused:UNUSED_PRESERVE src0_sel:WORD_1
	v_pk_add_f16 v121, v121, v136
	v_pk_add_f16 v120, v120, v139
	v_pk_add_f16 v122, v122, v137
	v_rcp_f16_e32 v132, v121
	v_rcp_f16_sdwa v121, v121 dst_sel:DWORD dst_unused:UNUSED_PAD src0_sel:WORD_1
	v_pk_add_f16 v123, v123, v138
	v_rcp_f16_e32 v133, v122
	v_rcp_f16_sdwa v122, v122 dst_sel:DWORD dst_unused:UNUSED_PAD src0_sel:WORD_1
	v_rcp_f16_e32 v135, v120
	v_rcp_f16_sdwa v120, v120 dst_sel:DWORD dst_unused:UNUSED_PAD src0_sel:WORD_1
	v_rcp_f16_e32 v134, v123
	v_rcp_f16_sdwa v123, v123 dst_sel:DWORD dst_unused:UNUSED_PAD src0_sel:WORD_1
	v_pk_fma_f16 v88, v32, v136, v88
	v_pack_b32_f16 v121, v132, v121
	v_pk_fma_f16 v91, v35, v139, v91
	v_pk_fma_f16 v89, v33, v137, v89
	v_pk_mul_f16 v88, v88, v121
	v_pack_b32_f16 v121, v133, v122
	v_pack_b32_f16 v120, v135, v120
	v_pk_fma_f16 v90, v34, v138, v90
	v_pk_mul_f16 v89, v89, v121
	v_pack_b32_f16 v121, v134, v123
	v_pk_mul_f16 v91, v91, v120
	s_waitcnt vmcnt(1)
	v_pk_mul_f16 v120, v164, v108 op_sel_hi:[0,1]
	v_pk_mul_f16 v123, v164, v111 op_sel_hi:[0,1]
	v_pk_mul_f16 v132, v165, v108 op_sel_hi:[0,1]
	v_pk_mul_f16 v135, v165, v111 op_sel_hi:[0,1]
	v_pk_mul_f16 v136, v166, v108 op_sel_hi:[0,1]
	v_pk_mul_f16 v139, v166, v111 op_sel_hi:[0,1]
	v_pk_mul_f16 v90, v90, v121
	v_pk_mul_f16 v121, v164, v109 op_sel_hi:[0,1]
	v_pk_mul_f16 v122, v164, v110 op_sel_hi:[0,1]
	v_pk_mul_f16 v133, v165, v109 op_sel_hi:[0,1]
	v_pk_mul_f16 v134, v165, v110 op_sel_hi:[0,1]
	v_pk_mul_f16 v137, v166, v109 op_sel_hi:[0,1]
	v_pk_mul_f16 v138, v166, v110 op_sel_hi:[0,1]
	v_pk_fma_f16 v67, v67, v111, v123
	v_pk_fma_f16 v64, v64, v108, v120
	v_pk_fma_f16 v79, v79, v111, v123
	v_pk_fma_f16 v76, v76, v108, v120
	v_pk_fma_f16 v95, v95, v111, v123
	v_pk_fma_f16 v92, v92, v108, v120
	v_pk_fma_f16 v120, v39, v111, v135
	v_pk_fma_f16 v123, v36, v108, v132
	v_pk_fma_f16 v140, v55, v111, v135
	v_pk_fma_f16 v143, v52, v108, v132
	v_pk_fma_f16 v135, v71, v111, v135
	v_pk_fma_f16 v132, v68, v108, v132
	v_pk_fma_f16 v144, v83, v111, v139
	v_pk_fma_f16 v147, v80, v108, v136
	v_pk_fma_f16 v148, v103, v111, v139
	v_pk_fma_f16 v151, v100, v108, v136
	v_pk_fma_f16 v111, v115, v111, v139
	v_pk_fma_f16 v108, v112, v108, v136
	v_pk_maximum3_f16 v136, v64, v76, v92
	v_pk_maximum3_f16 v139, v67, v79, v95
	v_pk_fma_f16 v66, v66, v110, v122
	v_pk_fma_f16 v65, v65, v109, v121
	v_pk_fma_f16 v78, v78, v110, v122
	v_pk_fma_f16 v77, v77, v109, v121
	v_pk_fma_f16 v94, v94, v110, v122
	v_pk_fma_f16 v93, v93, v109, v121
	v_pk_fma_f16 v121, v38, v110, v134
	v_pk_fma_f16 v122, v37, v109, v133
	v_pk_fma_f16 v141, v54, v110, v134
	v_pk_fma_f16 v142, v53, v109, v133
	v_pk_fma_f16 v134, v70, v110, v134
	v_pk_fma_f16 v133, v69, v109, v133
	v_pk_fma_f16 v145, v82, v110, v138
	v_pk_fma_f16 v146, v81, v109, v137
	v_pk_fma_f16 v149, v102, v110, v138
	v_pk_fma_f16 v150, v101, v109, v137
	v_pk_fma_f16 v110, v114, v110, v138
	v_pk_fma_f16 v109, v113, v109, v137
	v_pk_maximum3_f16 v137, v65, v77, v93
	v_pk_maximum3_f16 v138, v66, v78, v94
	v_pk_maximum3_f16 v152, v123, v143, v132
	v_pk_maximum3_f16 v155, v120, v140, v135
	v_pk_maximum3_f16 v156, v147, v151, v108
	v_pk_maximum3_f16 v159, v144, v148, v111
	v_pk_maximum3_f16 v153, v122, v142, v133
	v_pk_maximum3_f16 v154, v121, v141, v134
	v_pk_maximum3_f16 v157, v146, v150, v109
	v_pk_maximum3_f16 v158, v145, v149, v110
	v_pk_maximum3_f16 v136, v136, v152, v156
	v_pk_maximum3_f16 v139, v139, v155, v159
	v_pk_maximum3_f16 v137, v137, v153, v157
	v_pk_maximum3_f16 v138, v138, v154, v158
	v_pk_add_f16 v64, v64, v136 neg_lo:[0,1] neg_hi:[0,1]
	v_pk_add_f16 v67, v67, v139 neg_lo:[0,1] neg_hi:[0,1]
	v_pk_add_f16 v65, v65, v137 neg_lo:[0,1] neg_hi:[0,1]
	v_pk_add_f16 v66, v66, v138 neg_lo:[0,1] neg_hi:[0,1]
	v_pk_add_f16 v76, v76, v136 neg_lo:[0,1] neg_hi:[0,1]
	v_exp_f16_sdwa v152, v64 dst_sel:WORD_0 dst_unused:UNUSED_PAD src0_sel:WORD_0
	v_exp_f16_sdwa v153, v65 dst_sel:WORD_0 dst_unused:UNUSED_PAD src0_sel:WORD_0
	v_exp_f16_sdwa v154, v66 dst_sel:WORD_0 dst_unused:UNUSED_PAD src0_sel:WORD_0
	v_exp_f16_sdwa v155, v67 dst_sel:WORD_0 dst_unused:UNUSED_PAD src0_sel:WORD_0
	v_exp_f16_sdwa v152, v64 dst_sel:WORD_1 dst_unused:UNUSED_PRESERVE src0_sel:WORD_1
	v_exp_f16_sdwa v153, v65 dst_sel:WORD_1 dst_unused:UNUSED_PRESERVE src0_sel:WORD_1
	v_exp_f16_sdwa v154, v66 dst_sel:WORD_1 dst_unused:UNUSED_PRESERVE src0_sel:WORD_1
	v_exp_f16_sdwa v155, v67 dst_sel:WORD_1 dst_unused:UNUSED_PRESERVE src0_sel:WORD_1
	v_pk_add_f16 v77, v77, v137 neg_lo:[0,1] neg_hi:[0,1]
	v_pk_add_f16 v64, v155, 0
	v_pk_add_f16 v67, v152, 0
	v_pk_fma_f16 v40, v40, v152, 0
	v_pk_fma_f16 v43, v43, v155, 0
	v_pk_add_f16 v65, v154, 0
	v_pk_add_f16 v66, v153, 0
	v_pk_fma_f16 v41, v41, v153, 0
	v_pk_fma_f16 v42, v42, v154, 0
	v_pk_add_f16 v78, v78, v138 neg_lo:[0,1] neg_hi:[0,1]
	v_pk_add_f16 v79, v79, v139 neg_lo:[0,1] neg_hi:[0,1]
	v_exp_f16_sdwa v152, v76 dst_sel:WORD_0 dst_unused:UNUSED_PAD src0_sel:WORD_0
	v_exp_f16_sdwa v153, v77 dst_sel:WORD_0 dst_unused:UNUSED_PAD src0_sel:WORD_0
	v_exp_f16_sdwa v154, v78 dst_sel:WORD_0 dst_unused:UNUSED_PAD src0_sel:WORD_0
	v_exp_f16_sdwa v155, v79 dst_sel:WORD_0 dst_unused:UNUSED_PAD src0_sel:WORD_0
	v_exp_f16_sdwa v152, v76 dst_sel:WORD_1 dst_unused:UNUSED_PRESERVE src0_sel:WORD_1
	v_exp_f16_sdwa v153, v77 dst_sel:WORD_1 dst_unused:UNUSED_PRESERVE src0_sel:WORD_1
	v_exp_f16_sdwa v154, v78 dst_sel:WORD_1 dst_unused:UNUSED_PRESERVE src0_sel:WORD_1
	v_exp_f16_sdwa v155, v79 dst_sel:WORD_1 dst_unused:UNUSED_PRESERVE src0_sel:WORD_1
	v_pk_add_f16 v67, v67, v152
	v_pk_add_f16 v64, v64, v155
	v_pk_fma_f16 v43, v51, v155, v43
	v_pk_fma_f16 v40, v48, v152, v40
	v_pk_add_f16 v48, v92, v136 neg_lo:[0,1] neg_hi:[0,1]
	v_pk_add_f16 v51, v95, v139 neg_lo:[0,1] neg_hi:[0,1]
	v_pk_add_f16 v66, v66, v153
	v_pk_add_f16 v65, v65, v154
	v_pk_fma_f16 v42, v50, v154, v42
	v_pk_fma_f16 v41, v49, v153, v41
	v_pk_add_f16 v49, v93, v137 neg_lo:[0,1] neg_hi:[0,1]
	v_pk_add_f16 v50, v94, v138 neg_lo:[0,1] neg_hi:[0,1]
	v_exp_f16_sdwa v76, v48 dst_sel:WORD_0 dst_unused:UNUSED_PAD src0_sel:WORD_0
	v_exp_f16_sdwa v77, v49 dst_sel:WORD_0 dst_unused:UNUSED_PAD src0_sel:WORD_0
	v_exp_f16_sdwa v78, v50 dst_sel:WORD_0 dst_unused:UNUSED_PAD src0_sel:WORD_0
	v_exp_f16_sdwa v79, v51 dst_sel:WORD_0 dst_unused:UNUSED_PAD src0_sel:WORD_0
	v_exp_f16_sdwa v76, v48 dst_sel:WORD_1 dst_unused:UNUSED_PRESERVE src0_sel:WORD_1
	v_exp_f16_sdwa v77, v49 dst_sel:WORD_1 dst_unused:UNUSED_PRESERVE src0_sel:WORD_1
	v_exp_f16_sdwa v78, v50 dst_sel:WORD_1 dst_unused:UNUSED_PRESERVE src0_sel:WORD_1
	v_exp_f16_sdwa v79, v51 dst_sel:WORD_1 dst_unused:UNUSED_PRESERVE src0_sel:WORD_1
	s_nop 0
	v_pk_add_f16 v48, v64, v79
	v_pk_add_f16 v51, v67, v76
	v_pk_add_f16 v49, v65, v78
	v_pk_add_f16 v50, v66, v77
	v_pk_fma_f16 v40, v60, v76, v40
	v_pk_fma_f16 v41, v61, v77, v41
	v_pk_fma_f16 v42, v62, v78, v42
	v_pk_fma_f16 v43, v63, v79, v43
	v_pk_add_f16 v60, v123, v136 neg_lo:[0,1] neg_hi:[0,1]
	v_pk_add_f16 v61, v122, v137 neg_lo:[0,1] neg_hi:[0,1]
	v_pk_add_f16 v62, v121, v138 neg_lo:[0,1] neg_hi:[0,1]
	v_pk_add_f16 v63, v120, v139 neg_lo:[0,1] neg_hi:[0,1]
	v_exp_f16_sdwa v64, v60 dst_sel:WORD_0 dst_unused:UNUSED_PAD src0_sel:WORD_0
	v_exp_f16_sdwa v65, v61 dst_sel:WORD_0 dst_unused:UNUSED_PAD src0_sel:WORD_0
	v_exp_f16_sdwa v66, v62 dst_sel:WORD_0 dst_unused:UNUSED_PAD src0_sel:WORD_0
	v_exp_f16_sdwa v67, v63 dst_sel:WORD_0 dst_unused:UNUSED_PAD src0_sel:WORD_0
	v_exp_f16_sdwa v64, v60 dst_sel:WORD_1 dst_unused:UNUSED_PRESERVE src0_sel:WORD_1
	v_exp_f16_sdwa v65, v61 dst_sel:WORD_1 dst_unused:UNUSED_PRESERVE src0_sel:WORD_1
	v_exp_f16_sdwa v66, v62 dst_sel:WORD_1 dst_unused:UNUSED_PRESERVE src0_sel:WORD_1
	v_exp_f16_sdwa v67, v63 dst_sel:WORD_1 dst_unused:UNUSED_PRESERVE src0_sel:WORD_1
	v_pk_add_f16 v60, v143, v136 neg_lo:[0,1] neg_hi:[0,1]
	v_pk_add_f16 v51, v51, v64
	v_pk_add_f16 v48, v48, v67
	v_pk_add_f16 v50, v50, v65
	v_pk_add_f16 v49, v49, v66
	v_pk_fma_f16 v43, v27, v67, v43
	v_pk_fma_f16 v42, v26, v66, v42
	v_pk_fma_f16 v41, v25, v65, v41
	v_pk_fma_f16 v40, v24, v64, v40
	v_pk_add_f16 v61, v142, v137 neg_lo:[0,1] neg_hi:[0,1]
	v_pk_add_f16 v62, v141, v138 neg_lo:[0,1] neg_hi:[0,1]
	v_pk_add_f16 v63, v140, v139 neg_lo:[0,1] neg_hi:[0,1]
	v_exp_f16_sdwa v64, v60 dst_sel:WORD_0 dst_unused:UNUSED_PAD src0_sel:WORD_0
	v_exp_f16_sdwa v65, v61 dst_sel:WORD_0 dst_unused:UNUSED_PAD src0_sel:WORD_0
	v_exp_f16_sdwa v66, v62 dst_sel:WORD_0 dst_unused:UNUSED_PAD src0_sel:WORD_0
	v_exp_f16_sdwa v67, v63 dst_sel:WORD_0 dst_unused:UNUSED_PAD src0_sel:WORD_0
	v_exp_f16_sdwa v64, v60 dst_sel:WORD_1 dst_unused:UNUSED_PRESERVE src0_sel:WORD_1
	v_exp_f16_sdwa v65, v61 dst_sel:WORD_1 dst_unused:UNUSED_PRESERVE src0_sel:WORD_1
	v_exp_f16_sdwa v66, v62 dst_sel:WORD_1 dst_unused:UNUSED_PRESERVE src0_sel:WORD_1
	v_exp_f16_sdwa v67, v63 dst_sel:WORD_1 dst_unused:UNUSED_PRESERVE src0_sel:WORD_1
	v_pk_add_f16 v60, v132, v136 neg_lo:[0,1] neg_hi:[0,1]
	v_pk_add_f16 v48, v48, v67
	v_pk_add_f16 v51, v51, v64
	v_pk_add_f16 v49, v49, v66
	v_pk_add_f16 v50, v50, v65
	v_pk_fma_f16 v40, v28, v64, v40
	v_pk_fma_f16 v41, v29, v65, v41
	v_pk_fma_f16 v42, v30, v66, v42
	v_pk_fma_f16 v43, v31, v67, v43
	v_pk_add_f16 v61, v133, v137 neg_lo:[0,1] neg_hi:[0,1]
	v_pk_add_f16 v62, v134, v138 neg_lo:[0,1] neg_hi:[0,1]
	v_pk_add_f16 v63, v135, v139 neg_lo:[0,1] neg_hi:[0,1]
	v_exp_f16_sdwa v64, v60 dst_sel:WORD_0 dst_unused:UNUSED_PAD src0_sel:WORD_0
	v_exp_f16_sdwa v65, v61 dst_sel:WORD_0 dst_unused:UNUSED_PAD src0_sel:WORD_0
	v_exp_f16_sdwa v66, v62 dst_sel:WORD_0 dst_unused:UNUSED_PAD src0_sel:WORD_0
	v_exp_f16_sdwa v67, v63 dst_sel:WORD_0 dst_unused:UNUSED_PAD src0_sel:WORD_0
	v_exp_f16_sdwa v64, v60 dst_sel:WORD_1 dst_unused:UNUSED_PRESERVE src0_sel:WORD_1
	v_exp_f16_sdwa v65, v61 dst_sel:WORD_1 dst_unused:UNUSED_PRESERVE src0_sel:WORD_1
	v_exp_f16_sdwa v66, v62 dst_sel:WORD_1 dst_unused:UNUSED_PRESERVE src0_sel:WORD_1
	v_exp_f16_sdwa v67, v63 dst_sel:WORD_1 dst_unused:UNUSED_PRESERVE src0_sel:WORD_1
	v_pk_add_f16 v60, v147, v136 neg_lo:[0,1] neg_hi:[0,1]
	v_pk_add_f16 v51, v51, v64
	v_pk_add_f16 v48, v48, v67
	v_pk_add_f16 v50, v50, v65
	v_pk_add_f16 v49, v49, v66
	v_pk_fma_f16 v43, v35, v67, v43
	v_pk_fma_f16 v42, v34, v66, v42
	v_pk_fma_f16 v41, v33, v65, v41
	v_pk_fma_f16 v40, v32, v64, v40
	v_pk_add_f16 v61, v146, v137 neg_lo:[0,1] neg_hi:[0,1]
	v_pk_add_f16 v62, v145, v138 neg_lo:[0,1] neg_hi:[0,1]
	v_pk_add_f16 v63, v144, v139 neg_lo:[0,1] neg_hi:[0,1]
	v_exp_f16_sdwa v64, v60 dst_sel:WORD_0 dst_unused:UNUSED_PAD src0_sel:WORD_0
	v_exp_f16_sdwa v65, v61 dst_sel:WORD_0 dst_unused:UNUSED_PAD src0_sel:WORD_0
	v_exp_f16_sdwa v66, v62 dst_sel:WORD_0 dst_unused:UNUSED_PAD src0_sel:WORD_0
	v_exp_f16_sdwa v67, v63 dst_sel:WORD_0 dst_unused:UNUSED_PAD src0_sel:WORD_0
	v_exp_f16_sdwa v64, v60 dst_sel:WORD_1 dst_unused:UNUSED_PRESERVE src0_sel:WORD_1
	v_exp_f16_sdwa v65, v61 dst_sel:WORD_1 dst_unused:UNUSED_PRESERVE src0_sel:WORD_1
	v_exp_f16_sdwa v66, v62 dst_sel:WORD_1 dst_unused:UNUSED_PRESERVE src0_sel:WORD_1
	v_exp_f16_sdwa v67, v63 dst_sel:WORD_1 dst_unused:UNUSED_PRESERVE src0_sel:WORD_1
	v_pk_add_f16 v60, v151, v136 neg_lo:[0,1] neg_hi:[0,1]
	v_pk_add_f16 v48, v48, v67
	v_pk_add_f16 v51, v51, v64
	v_pk_add_f16 v49, v49, v66
	v_pk_add_f16 v50, v50, v65
	v_pk_fma_f16 v40, v44, v64, v40
	v_pk_fma_f16 v41, v45, v65, v41
	v_pk_fma_f16 v42, v46, v66, v42
	v_pk_fma_f16 v43, v47, v67, v43
	v_pk_add_f16 v61, v150, v137 neg_lo:[0,1] neg_hi:[0,1]
	v_pk_add_f16 v62, v149, v138 neg_lo:[0,1] neg_hi:[0,1]
	v_pk_add_f16 v63, v148, v139 neg_lo:[0,1] neg_hi:[0,1]
	v_exp_f16_sdwa v64, v60 dst_sel:WORD_0 dst_unused:UNUSED_PAD src0_sel:WORD_0
	v_exp_f16_sdwa v65, v61 dst_sel:WORD_0 dst_unused:UNUSED_PAD src0_sel:WORD_0
	v_exp_f16_sdwa v66, v62 dst_sel:WORD_0 dst_unused:UNUSED_PAD src0_sel:WORD_0
	v_exp_f16_sdwa v67, v63 dst_sel:WORD_0 dst_unused:UNUSED_PAD src0_sel:WORD_0
	v_exp_f16_sdwa v64, v60 dst_sel:WORD_1 dst_unused:UNUSED_PRESERVE src0_sel:WORD_1
	v_exp_f16_sdwa v65, v61 dst_sel:WORD_1 dst_unused:UNUSED_PRESERVE src0_sel:WORD_1
	v_exp_f16_sdwa v66, v62 dst_sel:WORD_1 dst_unused:UNUSED_PRESERVE src0_sel:WORD_1
	v_exp_f16_sdwa v67, v63 dst_sel:WORD_1 dst_unused:UNUSED_PRESERVE src0_sel:WORD_1
	v_pk_add_f16 v60, v108, v136 neg_lo:[0,1] neg_hi:[0,1]
	v_pk_add_f16 v51, v51, v64
	v_pk_add_f16 v48, v48, v67
	v_pk_add_f16 v50, v50, v65
	v_pk_add_f16 v49, v49, v66
	v_pk_fma_f16 v43, v59, v67, v43
	v_pk_fma_f16 v42, v58, v66, v42
	v_pk_fma_f16 v41, v57, v65, v41
	v_pk_fma_f16 v40, v56, v64, v40
	v_pk_add_f16 v61, v109, v137 neg_lo:[0,1] neg_hi:[0,1]
	v_pk_add_f16 v62, v110, v138 neg_lo:[0,1] neg_hi:[0,1]
	v_pk_add_f16 v63, v111, v139 neg_lo:[0,1] neg_hi:[0,1]
	v_exp_f16_sdwa v64, v60 dst_sel:WORD_0 dst_unused:UNUSED_PAD src0_sel:WORD_0
	v_exp_f16_sdwa v65, v61 dst_sel:WORD_0 dst_unused:UNUSED_PAD src0_sel:WORD_0
	v_exp_f16_sdwa v66, v62 dst_sel:WORD_0 dst_unused:UNUSED_PAD src0_sel:WORD_0
	v_exp_f16_sdwa v67, v63 dst_sel:WORD_0 dst_unused:UNUSED_PAD src0_sel:WORD_0
	v_exp_f16_sdwa v64, v60 dst_sel:WORD_1 dst_unused:UNUSED_PRESERVE src0_sel:WORD_1
	v_exp_f16_sdwa v65, v61 dst_sel:WORD_1 dst_unused:UNUSED_PRESERVE src0_sel:WORD_1
	v_exp_f16_sdwa v66, v62 dst_sel:WORD_1 dst_unused:UNUSED_PRESERVE src0_sel:WORD_1
	v_exp_f16_sdwa v67, v63 dst_sel:WORD_1 dst_unused:UNUSED_PRESERVE src0_sel:WORD_1
	s_nop 0
	v_pk_add_f16 v48, v48, v67
	v_pk_add_f16 v51, v51, v64
	v_pk_add_f16 v49, v49, v66
	v_rcp_f16_e32 v60, v51
	v_rcp_f16_sdwa v61, v51 dst_sel:DWORD dst_unused:UNUSED_PAD src0_sel:WORD_1
	v_rcp_f16_e32 v51, v48
	v_rcp_f16_sdwa v48, v48 dst_sel:DWORD dst_unused:UNUSED_PAD src0_sel:WORD_1
	v_pk_add_f16 v50, v50, v65
	v_rcp_f16_e32 v63, v49
	v_rcp_f16_sdwa v49, v49 dst_sel:DWORD dst_unused:UNUSED_PAD src0_sel:WORD_1
	v_pk_fma_f16 v40, v72, v64, v40
	v_rcp_f16_e32 v62, v50
	v_rcp_f16_sdwa v64, v50 dst_sel:DWORD dst_unused:UNUSED_PAD src0_sel:WORD_1
	v_pk_fma_f16 v43, v75, v67, v43
	v_pack_b32_f16 v48, v51, v48
	v_pk_fma_f16 v42, v74, v66, v42
	v_pk_mul_f16 v51, v43, v48
	v_pack_b32_f16 v43, v63, v49
	v_pk_fma_f16 v41, v73, v65, v41
	v_pk_mul_f16 v50, v42, v43
	v_pack_b32_f16 v42, v62, v64
	v_pk_mul_f16 v49, v41, v42
	v_pack_b32_f16 v41, v60, v61
	v_pk_mul_f16 v48, v40, v41
	s_waitcnt vmcnt(0)
	v_pk_mul_f16 v40, v164, v104 op_sel_hi:[0,1]
	v_pk_mul_f16 v41, v164, v105 op_sel_hi:[0,1]
	v_pk_mul_f16 v42, v164, v106 op_sel_hi:[0,1]
	v_pk_mul_f16 v43, v164, v107 op_sel_hi:[0,1]
	v_pk_mul_f16 v60, v165, v104 op_sel_hi:[0,1]
	v_pk_mul_f16 v61, v165, v105 op_sel_hi:[0,1]
	v_pk_mul_f16 v62, v165, v106 op_sel_hi:[0,1]
	v_pk_mul_f16 v63, v165, v107 op_sel_hi:[0,1]
	v_pk_mul_f16 v64, v166, v104 op_sel_hi:[0,1]
	v_pk_mul_f16 v65, v166, v105 op_sel_hi:[0,1]
	v_pk_mul_f16 v66, v166, v106 op_sel_hi:[0,1]
	v_pk_mul_f16 v67, v166, v107 op_sel_hi:[0,1]
	v_pk_fma_f16 v39, v39, v107, v43
	v_pk_fma_f16 v38, v38, v106, v42
	v_pk_fma_f16 v37, v37, v105, v41
	v_pk_fma_f16 v36, v36, v104, v40
	v_pk_fma_f16 v55, v55, v107, v43
	v_pk_fma_f16 v54, v54, v106, v42
	v_pk_fma_f16 v53, v53, v105, v41
	v_pk_fma_f16 v52, v52, v104, v40
	v_pk_fma_f16 v43, v71, v107, v43
	v_pk_fma_f16 v42, v70, v106, v42
	v_pk_fma_f16 v41, v69, v105, v41
	v_pk_fma_f16 v40, v68, v104, v40
	v_pk_fma_f16 v68, v83, v107, v63
	v_pk_fma_f16 v69, v82, v106, v62
	v_pk_fma_f16 v70, v81, v105, v61
	v_pk_fma_f16 v71, v80, v104, v60
	v_pk_fma_f16 v80, v119, v107, v67
	v_pk_fma_f16 v81, v118, v106, v66
	v_pk_fma_f16 v82, v117, v105, v65
	v_pk_fma_f16 v83, v116, v104, v64
	v_pk_fma_f16 v92, v131, v107, v67
	v_pk_fma_f16 v93, v130, v106, v66
	v_pk_fma_f16 v94, v129, v105, v65
	v_pk_fma_f16 v95, v128, v104, v64
	v_pk_fma_f16 v23, v23, v107, v67
	v_pk_fma_f16 v22, v22, v106, v66
	v_pk_fma_f16 v21, v21, v105, v65
	v_pk_fma_f16 v20, v20, v104, v64
	v_pk_maximum3_f16 v64, v36, v52, v40
	v_pk_maximum3_f16 v65, v37, v53, v41
	v_pk_maximum3_f16 v66, v38, v54, v42
	v_pk_maximum3_f16 v67, v39, v55, v43
	v_pk_fma_f16 v76, v103, v107, v63
	v_pk_fma_f16 v77, v102, v106, v62
	v_pk_fma_f16 v78, v101, v105, v61
	v_pk_fma_f16 v79, v100, v104, v60
	v_pk_fma_f16 v63, v115, v107, v63
	v_pk_fma_f16 v62, v114, v106, v62
	v_pk_fma_f16 v61, v113, v105, v61
	v_pk_fma_f16 v60, v112, v104, v60
	v_pk_maximum3_f16 v101, v70, v78, v61
	v_pk_maximum3_f16 v102, v69, v77, v62
	v_pk_maximum3_f16 v103, v68, v76, v63
	v_pk_maximum3_f16 v104, v83, v95, v20
	v_pk_maximum3_f16 v105, v82, v94, v21
	v_pk_maximum3_f16 v100, v71, v79, v60
	v_pk_maximum3_f16 v106, v81, v93, v22
	v_pk_maximum3_f16 v107, v80, v92, v23
	v_pk_maximum3_f16 v64, v64, v100, v104
	v_pk_maximum3_f16 v65, v65, v101, v105
	v_pk_maximum3_f16 v66, v66, v102, v106
	v_pk_maximum3_f16 v67, v67, v103, v107
	s_nop 0
	v_pk_add_f16 v36, v36, v64 neg_lo:[0,1] neg_hi:[0,1]
	v_pk_add_f16 v37, v37, v65 neg_lo:[0,1] neg_hi:[0,1]
	v_pk_add_f16 v38, v38, v66 neg_lo:[0,1] neg_hi:[0,1]
	v_pk_add_f16 v39, v39, v67 neg_lo:[0,1] neg_hi:[0,1]
	v_pk_add_f16 v52, v52, v64 neg_lo:[0,1] neg_hi:[0,1]
	v_exp_f16_sdwa v100, v36 dst_sel:WORD_0 dst_unused:UNUSED_PAD src0_sel:WORD_0
	v_exp_f16_sdwa v101, v37 dst_sel:WORD_0 dst_unused:UNUSED_PAD src0_sel:WORD_0
	v_exp_f16_sdwa v102, v38 dst_sel:WORD_0 dst_unused:UNUSED_PAD src0_sel:WORD_0
	v_exp_f16_sdwa v103, v39 dst_sel:WORD_0 dst_unused:UNUSED_PAD src0_sel:WORD_0
	v_exp_f16_sdwa v100, v36 dst_sel:WORD_1 dst_unused:UNUSED_PRESERVE src0_sel:WORD_1
	v_exp_f16_sdwa v101, v37 dst_sel:WORD_1 dst_unused:UNUSED_PRESERVE src0_sel:WORD_1
	v_exp_f16_sdwa v102, v38 dst_sel:WORD_1 dst_unused:UNUSED_PRESERVE src0_sel:WORD_1
	v_exp_f16_sdwa v103, v39 dst_sel:WORD_1 dst_unused:UNUSED_PRESERVE src0_sel:WORD_1
	v_pk_add_f16 v53, v53, v65 neg_lo:[0,1] neg_hi:[0,1]
	v_pk_add_f16 v36, v100, 0
	v_pk_add_f16 v37, v101, 0
	v_pk_add_f16 v38, v102, 0
	v_pk_add_f16 v39, v103, 0
	v_pk_fma_f16 v24, v24, v100, 0
	v_pk_fma_f16 v25, v25, v101, 0
	v_pk_fma_f16 v26, v26, v102, 0
	v_pk_fma_f16 v27, v27, v103, 0
	v_pk_add_f16 v54, v54, v66 neg_lo:[0,1] neg_hi:[0,1]
	v_pk_add_f16 v55, v55, v67 neg_lo:[0,1] neg_hi:[0,1]
	v_pk_add_f16 v20, v20, v64 neg_lo:[0,1] neg_hi:[0,1]
	v_exp_f16_sdwa v100, v52 dst_sel:WORD_0 dst_unused:UNUSED_PAD src0_sel:WORD_0
	v_exp_f16_sdwa v101, v53 dst_sel:WORD_0 dst_unused:UNUSED_PAD src0_sel:WORD_0
	v_exp_f16_sdwa v102, v54 dst_sel:WORD_0 dst_unused:UNUSED_PAD src0_sel:WORD_0
	v_exp_f16_sdwa v103, v55 dst_sel:WORD_0 dst_unused:UNUSED_PAD src0_sel:WORD_0
	v_exp_f16_sdwa v100, v52 dst_sel:WORD_1 dst_unused:UNUSED_PRESERVE src0_sel:WORD_1
	v_exp_f16_sdwa v101, v53 dst_sel:WORD_1 dst_unused:UNUSED_PRESERVE src0_sel:WORD_1
	v_exp_f16_sdwa v102, v54 dst_sel:WORD_1 dst_unused:UNUSED_PRESERVE src0_sel:WORD_1
	v_exp_f16_sdwa v103, v55 dst_sel:WORD_1 dst_unused:UNUSED_PRESERVE src0_sel:WORD_1
	v_pk_add_f16 v21, v21, v65 neg_lo:[0,1] neg_hi:[0,1]
	v_pk_add_f16 v39, v39, v103
	v_pk_add_f16 v38, v38, v102
	v_pk_add_f16 v37, v37, v101
	v_pk_add_f16 v36, v36, v100
	v_pk_fma_f16 v27, v31, v103, v27
	v_pk_fma_f16 v26, v30, v102, v26
	v_pk_fma_f16 v25, v29, v101, v25
	v_pk_fma_f16 v24, v28, v100, v24
	v_pk_add_f16 v28, v40, v64 neg_lo:[0,1] neg_hi:[0,1]
	v_pk_add_f16 v29, v41, v65 neg_lo:[0,1] neg_hi:[0,1]
	v_pk_add_f16 v30, v42, v66 neg_lo:[0,1] neg_hi:[0,1]
	v_pk_add_f16 v31, v43, v67 neg_lo:[0,1] neg_hi:[0,1]
	v_pk_add_f16 v22, v22, v66 neg_lo:[0,1] neg_hi:[0,1]
	v_exp_f16_sdwa v40, v28 dst_sel:WORD_0 dst_unused:UNUSED_PAD src0_sel:WORD_0
	v_exp_f16_sdwa v41, v29 dst_sel:WORD_0 dst_unused:UNUSED_PAD src0_sel:WORD_0
	v_exp_f16_sdwa v42, v30 dst_sel:WORD_0 dst_unused:UNUSED_PAD src0_sel:WORD_0
	v_exp_f16_sdwa v43, v31 dst_sel:WORD_0 dst_unused:UNUSED_PAD src0_sel:WORD_0
	v_exp_f16_sdwa v40, v28 dst_sel:WORD_1 dst_unused:UNUSED_PRESERVE src0_sel:WORD_1
	v_exp_f16_sdwa v41, v29 dst_sel:WORD_1 dst_unused:UNUSED_PRESERVE src0_sel:WORD_1
	v_exp_f16_sdwa v42, v30 dst_sel:WORD_1 dst_unused:UNUSED_PRESERVE src0_sel:WORD_1
	v_exp_f16_sdwa v43, v31 dst_sel:WORD_1 dst_unused:UNUSED_PRESERVE src0_sel:WORD_1
	v_pk_add_f16 v23, v23, v67 neg_lo:[0,1] neg_hi:[0,1]
	v_pk_add_f16 v28, v36, v40
	v_pk_add_f16 v29, v37, v41
	v_pk_add_f16 v30, v38, v42
	v_pk_add_f16 v31, v39, v43
	v_pk_fma_f16 v24, v32, v40, v24
	v_pk_fma_f16 v25, v33, v41, v25
	v_pk_fma_f16 v26, v34, v42, v26
	v_pk_fma_f16 v27, v35, v43, v27
	v_pk_add_f16 v32, v71, v64 neg_lo:[0,1] neg_hi:[0,1]
	v_pk_add_f16 v33, v70, v65 neg_lo:[0,1] neg_hi:[0,1]
	v_pk_add_f16 v34, v69, v66 neg_lo:[0,1] neg_hi:[0,1]
	v_pk_add_f16 v35, v68, v67 neg_lo:[0,1] neg_hi:[0,1]
	v_exp_f16_sdwa v36, v32 dst_sel:WORD_0 dst_unused:UNUSED_PAD src0_sel:WORD_0
	v_exp_f16_sdwa v37, v33 dst_sel:WORD_0 dst_unused:UNUSED_PAD src0_sel:WORD_0
	v_exp_f16_sdwa v38, v34 dst_sel:WORD_0 dst_unused:UNUSED_PAD src0_sel:WORD_0
	v_exp_f16_sdwa v39, v35 dst_sel:WORD_0 dst_unused:UNUSED_PAD src0_sel:WORD_0
	v_exp_f16_sdwa v36, v32 dst_sel:WORD_1 dst_unused:UNUSED_PRESERVE src0_sel:WORD_1
	v_exp_f16_sdwa v37, v33 dst_sel:WORD_1 dst_unused:UNUSED_PRESERVE src0_sel:WORD_1
	v_exp_f16_sdwa v38, v34 dst_sel:WORD_1 dst_unused:UNUSED_PRESERVE src0_sel:WORD_1
	v_exp_f16_sdwa v39, v35 dst_sel:WORD_1 dst_unused:UNUSED_PRESERVE src0_sel:WORD_1
	v_pk_add_f16 v32, v79, v64 neg_lo:[0,1] neg_hi:[0,1]
	v_pk_add_f16 v31, v31, v39
	v_pk_add_f16 v30, v30, v38
	v_pk_add_f16 v29, v29, v37
	v_pk_add_f16 v28, v28, v36
	v_pk_fma_f16 v27, v47, v39, v27
	v_pk_fma_f16 v26, v46, v38, v26
	v_pk_fma_f16 v25, v45, v37, v25
	v_pk_fma_f16 v24, v44, v36, v24
	v_pk_add_f16 v33, v78, v65 neg_lo:[0,1] neg_hi:[0,1]
	v_pk_add_f16 v34, v77, v66 neg_lo:[0,1] neg_hi:[0,1]
	v_pk_add_f16 v35, v76, v67 neg_lo:[0,1] neg_hi:[0,1]
	v_exp_f16_sdwa v36, v32 dst_sel:WORD_0 dst_unused:UNUSED_PAD src0_sel:WORD_0
	v_exp_f16_sdwa v37, v33 dst_sel:WORD_0 dst_unused:UNUSED_PAD src0_sel:WORD_0
	v_exp_f16_sdwa v38, v34 dst_sel:WORD_0 dst_unused:UNUSED_PAD src0_sel:WORD_0
	v_exp_f16_sdwa v39, v35 dst_sel:WORD_0 dst_unused:UNUSED_PAD src0_sel:WORD_0
	v_exp_f16_sdwa v36, v32 dst_sel:WORD_1 dst_unused:UNUSED_PRESERVE src0_sel:WORD_1
	v_exp_f16_sdwa v37, v33 dst_sel:WORD_1 dst_unused:UNUSED_PRESERVE src0_sel:WORD_1
	v_exp_f16_sdwa v38, v34 dst_sel:WORD_1 dst_unused:UNUSED_PRESERVE src0_sel:WORD_1
	v_exp_f16_sdwa v39, v35 dst_sel:WORD_1 dst_unused:UNUSED_PRESERVE src0_sel:WORD_1
	v_pk_add_f16 v32, v60, v64 neg_lo:[0,1] neg_hi:[0,1]
	v_pk_add_f16 v28, v28, v36
	v_pk_add_f16 v29, v29, v37
	v_pk_add_f16 v30, v30, v38
	v_pk_add_f16 v31, v31, v39
	v_pk_fma_f16 v24, v56, v36, v24
	v_pk_fma_f16 v25, v57, v37, v25
	v_pk_fma_f16 v26, v58, v38, v26
	v_pk_fma_f16 v27, v59, v39, v27
	v_pk_add_f16 v33, v61, v65 neg_lo:[0,1] neg_hi:[0,1]
	v_pk_add_f16 v34, v62, v66 neg_lo:[0,1] neg_hi:[0,1]
	v_pk_add_f16 v35, v63, v67 neg_lo:[0,1] neg_hi:[0,1]
	v_exp_f16_sdwa v36, v32 dst_sel:WORD_0 dst_unused:UNUSED_PAD src0_sel:WORD_0
	v_exp_f16_sdwa v37, v33 dst_sel:WORD_0 dst_unused:UNUSED_PAD src0_sel:WORD_0
	v_exp_f16_sdwa v38, v34 dst_sel:WORD_0 dst_unused:UNUSED_PAD src0_sel:WORD_0
	v_exp_f16_sdwa v39, v35 dst_sel:WORD_0 dst_unused:UNUSED_PAD src0_sel:WORD_0
	v_exp_f16_sdwa v36, v32 dst_sel:WORD_1 dst_unused:UNUSED_PRESERVE src0_sel:WORD_1
	v_exp_f16_sdwa v37, v33 dst_sel:WORD_1 dst_unused:UNUSED_PRESERVE src0_sel:WORD_1
	v_exp_f16_sdwa v38, v34 dst_sel:WORD_1 dst_unused:UNUSED_PRESERVE src0_sel:WORD_1
	v_exp_f16_sdwa v39, v35 dst_sel:WORD_1 dst_unused:UNUSED_PRESERVE src0_sel:WORD_1
	v_pk_add_f16 v32, v83, v64 neg_lo:[0,1] neg_hi:[0,1]
	v_pk_add_f16 v31, v31, v39
	v_pk_add_f16 v30, v30, v38
	v_pk_add_f16 v29, v29, v37
	v_pk_add_f16 v28, v28, v36
	v_pk_fma_f16 v27, v75, v39, v27
	v_pk_fma_f16 v26, v74, v38, v26
	v_pk_fma_f16 v25, v73, v37, v25
	v_pk_fma_f16 v24, v72, v36, v24
	v_pk_add_f16 v33, v82, v65 neg_lo:[0,1] neg_hi:[0,1]
	v_pk_add_f16 v34, v81, v66 neg_lo:[0,1] neg_hi:[0,1]
	v_pk_add_f16 v35, v80, v67 neg_lo:[0,1] neg_hi:[0,1]
	v_exp_f16_sdwa v36, v32 dst_sel:WORD_0 dst_unused:UNUSED_PAD src0_sel:WORD_0
	v_exp_f16_sdwa v37, v33 dst_sel:WORD_0 dst_unused:UNUSED_PAD src0_sel:WORD_0
	v_exp_f16_sdwa v38, v34 dst_sel:WORD_0 dst_unused:UNUSED_PAD src0_sel:WORD_0
	v_exp_f16_sdwa v39, v35 dst_sel:WORD_0 dst_unused:UNUSED_PAD src0_sel:WORD_0
	v_exp_f16_sdwa v36, v32 dst_sel:WORD_1 dst_unused:UNUSED_PRESERVE src0_sel:WORD_1
	v_exp_f16_sdwa v37, v33 dst_sel:WORD_1 dst_unused:UNUSED_PRESERVE src0_sel:WORD_1
	v_exp_f16_sdwa v38, v34 dst_sel:WORD_1 dst_unused:UNUSED_PRESERVE src0_sel:WORD_1
	v_exp_f16_sdwa v39, v35 dst_sel:WORD_1 dst_unused:UNUSED_PRESERVE src0_sel:WORD_1
	v_pk_add_f16 v32, v95, v64 neg_lo:[0,1] neg_hi:[0,1]
	v_pk_add_f16 v28, v28, v36
	v_pk_add_f16 v29, v29, v37
	v_pk_add_f16 v30, v30, v38
	v_pk_add_f16 v31, v31, v39
	v_pk_fma_f16 v24, v84, v36, v24
	v_pk_fma_f16 v25, v85, v37, v25
	v_pk_fma_f16 v26, v86, v38, v26
	v_pk_fma_f16 v27, v87, v39, v27
	v_pk_add_f16 v33, v94, v65 neg_lo:[0,1] neg_hi:[0,1]
	v_pk_add_f16 v34, v93, v66 neg_lo:[0,1] neg_hi:[0,1]
	v_pk_add_f16 v35, v92, v67 neg_lo:[0,1] neg_hi:[0,1]
	v_exp_f16_sdwa v36, v32 dst_sel:WORD_0 dst_unused:UNUSED_PAD src0_sel:WORD_0
	v_exp_f16_sdwa v37, v33 dst_sel:WORD_0 dst_unused:UNUSED_PAD src0_sel:WORD_0
	v_exp_f16_sdwa v38, v34 dst_sel:WORD_0 dst_unused:UNUSED_PAD src0_sel:WORD_0
	v_exp_f16_sdwa v39, v35 dst_sel:WORD_0 dst_unused:UNUSED_PAD src0_sel:WORD_0
	v_exp_f16_sdwa v36, v32 dst_sel:WORD_1 dst_unused:UNUSED_PRESERVE src0_sel:WORD_1
	v_exp_f16_sdwa v37, v33 dst_sel:WORD_1 dst_unused:UNUSED_PRESERVE src0_sel:WORD_1
	v_exp_f16_sdwa v38, v34 dst_sel:WORD_1 dst_unused:UNUSED_PRESERVE src0_sel:WORD_1
	v_exp_f16_sdwa v39, v35 dst_sel:WORD_1 dst_unused:UNUSED_PRESERVE src0_sel:WORD_1
	s_nop 0
	v_pk_add_f16 v31, v31, v39
	v_pk_add_f16 v30, v30, v38
	v_pk_add_f16 v29, v29, v37
	v_pk_add_f16 v28, v28, v36
	v_pk_fma_f16 v35, v99, v39, v27
	v_pk_fma_f16 v34, v98, v38, v26
	v_pk_fma_f16 v33, v97, v37, v25
	v_pk_fma_f16 v32, v96, v36, v24
	v_exp_f16_sdwa v36, v20 dst_sel:WORD_0 dst_unused:UNUSED_PAD src0_sel:WORD_0
	v_exp_f16_sdwa v37, v21 dst_sel:WORD_0 dst_unused:UNUSED_PAD src0_sel:WORD_0
	v_exp_f16_sdwa v38, v22 dst_sel:WORD_0 dst_unused:UNUSED_PAD src0_sel:WORD_0
	v_exp_f16_sdwa v39, v23 dst_sel:WORD_0 dst_unused:UNUSED_PAD src0_sel:WORD_0
	v_exp_f16_sdwa v36, v20 dst_sel:WORD_1 dst_unused:UNUSED_PRESERVE src0_sel:WORD_1
	v_exp_f16_sdwa v37, v21 dst_sel:WORD_1 dst_unused:UNUSED_PRESERVE src0_sel:WORD_1
	v_exp_f16_sdwa v38, v22 dst_sel:WORD_1 dst_unused:UNUSED_PRESERVE src0_sel:WORD_1
	v_exp_f16_sdwa v39, v23 dst_sel:WORD_1 dst_unused:UNUSED_PRESERVE src0_sel:WORD_1
	v_mov_b32_e32 v27, v19
	v_mov_b32_e32 v26, v18
	v_mov_b32_e32 v25, v17
	v_mov_b32_e32 v24, v16

	.amdhsa_kernel _Z7k_attn2ILi2EEv8AttnArgs
		.amdhsa_group_segment_fixed_size 0
		.amdhsa_private_segment_fixed_size 0
		.amdhsa_kernarg_size 112
		.amdhsa_user_sgpr_count 2
		.amdhsa_user_sgpr_dispatch_ptr 0
		.amdhsa_user_sgpr_queue_ptr 0
		.amdhsa_user_sgpr_kernarg_segment_ptr 1
		.amdhsa_user_sgpr_dispatch_id 0
		.amdhsa_user_sgpr_kernarg_preload_length 0
		.amdhsa_user_sgpr_kernarg_preload_offset 0
		.amdhsa_user_sgpr_private_segment_size 0
		.amdhsa_uses_dynamic_stack 0
		.amdhsa_enable_private_segment 0
		.amdhsa_system_sgpr_workgroup_id_x 1
		.amdhsa_system_sgpr_workgroup_id_y 0
		.amdhsa_system_sgpr_workgroup_id_z 0
		.amdhsa_system_sgpr_workgroup_info 0
		.amdhsa_system_vgpr_workitem_id 0
		.amdhsa_next_free_vgpr 236
		.amdhsa_next_free_sgpr 80
		.amdhsa_accum_offset 236
		.amdhsa_reserve_vcc 1
		.amdhsa_float_round_mode_32 0
		.amdhsa_float_round_mode_16_64 0
		.amdhsa_float_denorm_mode_32 3
		.amdhsa_float_denorm_mode_16_64 3
		.amdhsa_dx10_clamp 1
		.amdhsa_ieee_mode 1
		.amdhsa_fp16_overflow 0
		.amdhsa_tg_split 0
		.amdhsa_exception_fp_ieee_invalid_op 0
		.amdhsa_exception_fp_denorm_src 0
		.amdhsa_exception_fp_ieee_div_zero 0
		.amdhsa_exception_fp_ieee_overflow 0
		.amdhsa_exception_fp_ieee_underflow 0
		.amdhsa_exception_fp_ieee_inexact 0
		.amdhsa_exception_int_div_zero 0
	.end_amdhsa_kernel

amdhsa.kernels:
  - .agpr_count:     0
    .args:
      - .actual_access:  read_only
        .address_space:  global
        .offset:         0
        .size:           8
        .value_kind:     global_buffer
      - .actual_access:  read_only
        .address_space:  global
        .offset:         8
        .size:           8
        .value_kind:     global_buffer
      - .actual_access:  read_only
        .address_space:  global
        .offset:         16
        .size:           8
        .value_kind:     global_buffer
      - .actual_access:  read_only
        .address_space:  global
        .offset:         24
        .size:           8
        .value_kind:     global_buffer
      - .actual_access:  read_only
        .address_space:  global
        .offset:         32
        .size:           8
        .value_kind:     global_buffer
      - .actual_access:  read_only
        .address_space:  global
        .offset:         40
        .size:           8
        .value_kind:     global_buffer
      - .actual_access:  read_only
        .address_space:  global
        .offset:         48
        .size:           8
        .value_kind:     global_buffer
      - .actual_access:  read_only
        .address_space:  global
        .offset:         56
        .size:           8
        .value_kind:     global_buffer
      - .actual_access:  write_only
        .address_space:  global
        .offset:         64
        .size:           8
        .value_kind:     global_buffer
      - .actual_access:  write_only
        .address_space:  global
        .offset:         72
        .size:           8
        .value_kind:     global_buffer
      - .actual_access:  write_only
        .address_space:  global
        .offset:         80
        .size:           8
        .value_kind:     global_buffer
      - .actual_access:  write_only
        .address_space:  global
        .offset:         88
        .size:           8
        .value_kind:     global_buffer
    .group_segment_fixed_size: 0
    .kernarg_segment_align: 8
    .kernarg_segment_size: 96
    .language:       OpenCL C
    .language_version:
      - 2
      - 0
    .max_flat_workgroup_size: 256
    .name:           _Z8k_prep_wPKfS0_S0_S0_S0_S0_S0_S0_PDF16_PfS1_S1_
    .private_segment_fixed_size: 0
    .sgpr_count:     23
    .sgpr_spill_count: 0
    .symbol:         _Z8k_prep_wPKfS0_S0_S0_S0_S0_S0_S0_PDF16_PfS1_S1_.kd
    .uniform_work_group_size: 1
    .uses_dynamic_stack: false
    .vgpr_count:     15
    .vgpr_spill_count: 0
    .wavefront_size: 64
  - .agpr_count:     0
    .args:
      - .actual_access:  read_only
        .address_space:  global
        .offset:         0
        .size:           8
        .value_kind:     global_buffer
      - .actual_access:  read_only
        .address_space:  global
        .offset:         8
        .size:           8
        .value_kind:     global_buffer
      - .actual_access:  read_only
        .address_space:  global
        .offset:         16
        .size:           8
        .value_kind:     global_buffer
      - .actual_access:  read_only
        .address_space:  global
        .offset:         24
        .size:           8
        .value_kind:     global_buffer
      - .actual_access:  write_only
        .address_space:  global
        .offset:         32
        .size:           8
        .value_kind:     global_buffer
      - .actual_access:  read_only
        .address_space:  global
        .offset:         40
        .size:           8
        .value_kind:     global_buffer
      - .actual_access:  read_only
        .address_space:  global
        .offset:         48
        .size:           8
        .value_kind:     global_buffer
      - .actual_access:  write_only
        .address_space:  global
        .offset:         56
        .size:           8
        .value_kind:     global_buffer
      - .offset:         64
        .size:           4
        .value_kind:     by_value
      - .offset:         68
        .size:           4
        .value_kind:     by_value
    .group_segment_fixed_size: 115712
    .kernarg_segment_align: 8
    .kernarg_segment_size: 72
    .language:       OpenCL C
    .language_version:
      - 2
      - 0
    .max_flat_workgroup_size: 512
    .name:           _Z8k_stageAPKfS0_S0_S0_PDF16_PKDF16_S0_S1_ii
    .private_segment_fixed_size: 0
    .sgpr_count:     28
    .sgpr_spill_count: 0
    .symbol:         _Z8k_stageAPKfS0_S0_S0_PDF16_PKDF16_S0_S1_ii.kd
    .uniform_work_group_size: 1
    .uses_dynamic_stack: false
    .vgpr_count:     251
    .vgpr_spill_count: 0
    .wavefront_size: 64
  - .agpr_count:     112
    .args:
      - .actual_access:  read_only
        .address_space:  global
        .offset:         0
        .size:           8
        .value_kind:     global_buffer
      - .actual_access:  read_only
        .address_space:  global
        .offset:         8
        .size:           8
        .value_kind:     global_buffer
      - .actual_access:  read_only
        .address_space:  global
        .offset:         16
        .size:           8
        .value_kind:     global_buffer
      - .actual_access:  read_only
        .address_space:  global
        .offset:         24
        .size:           8
        .value_kind:     global_buffer
      - .actual_access:  read_only
        .address_space:  global
        .offset:         32
        .size:           8
        .value_kind:     global_buffer
      - .actual_access:  write_only
        .address_space:  global
        .offset:         40
        .size:           8
        .value_kind:     global_buffer
    .group_segment_fixed_size: 107712
    .kernarg_segment_align: 8
    .kernarg_segment_size: 48
    .language:       OpenCL C
    .language_version:
      - 2
      - 0
    .max_flat_workgroup_size: 256
    .name:           _Z7k_conv4PKDF16_S0_S0_PKfS2_Pf
    .private_segment_fixed_size: 0
    .sgpr_count:     36
    .sgpr_spill_count: 0
    .symbol:         _Z7k_conv4PKDF16_S0_S0_PKfS2_Pf.kd
    .uniform_work_group_size: 1
    .uses_dynamic_stack: false
    .vgpr_count:     328
    .vgpr_spill_count: 0
    .wavefront_size: 64
  - .agpr_count:     0
    .args:
      - .offset:         0
        .size:           112
        .value_kind:     by_value
      - .actual_access:  read_only
        .address_space:  global
        .offset:         112
        .size:           8
        .value_kind:     global_buffer
      - .actual_access:  read_only
        .address_space:  global
        .offset:         120
        .size:           8
        .value_kind:     global_buffer
      - .actual_access:  write_only
        .address_space:  global
        .offset:         128
        .size:           8
        .value_kind:     global_buffer
      - .offset:         136
        .size:           4
        .value_kind:     by_value
      - .offset:         140
        .size:           4
        .value_kind:     by_value
      - .offset:         144
        .size:           4
        .value_kind:     by_value
    .group_segment_fixed_size: 115712
    .kernarg_segment_align: 8
    .kernarg_segment_size: 148
    .language:       OpenCL C
    .language_version:
      - 2
      - 0
    .max_flat_workgroup_size: 512
    .name:           _Z7k_stageILi0ELi8EEv8AttnArgsPKDF16_PKfPDF16_iii
    .private_segment_fixed_size: 0
    .sgpr_count:     41
    .sgpr_spill_count: 0
    .symbol:         _Z7k_stageILi0ELi8EEv8AttnArgsPKDF16_PKfPDF16_iii.kd
    .uniform_work_group_size: 1
    .uses_dynamic_stack: false
    .vgpr_count:     255
    .vgpr_spill_count: 0
    .wavefront_size: 64
  - .agpr_count:     0
    .args:
      - .offset:         0
        .size:           112
        .value_kind:     by_value
      - .actual_access:  read_only
        .address_space:  global
        .offset:         112
        .size:           8
        .value_kind:     global_buffer
      - .actual_access:  read_only
        .address_space:  global
        .offset:         120
        .size:           8
        .value_kind:     global_buffer
      - .actual_access:  write_only
        .address_space:  global
        .offset:         128
        .size:           8
        .value_kind:     global_buffer
      - .offset:         136
        .size:           4
        .value_kind:     by_value
      - .offset:         140
        .size:           4
        .value_kind:     by_value
      - .offset:         144
        .size:           4
        .value_kind:     by_value
    .group_segment_fixed_size: 82944
    .kernarg_segment_align: 8
    .kernarg_segment_size: 148
    .language:       OpenCL C
    .language_version:
      - 2
      - 0
    .max_flat_workgroup_size: 512
    .name:           _Z7k_stageILi1ELi4EEv8AttnArgsPKDF16_PKfPDF16_iii
    .private_segment_fixed_size: 0
    .sgpr_count:     55
    .sgpr_spill_count: 0
    .symbol:         _Z7k_stageILi1ELi4EEv8AttnArgsPKDF16_PKfPDF16_iii.kd
    .uniform_work_group_size: 1
    .uses_dynamic_stack: false
    .vgpr_count:     252
    .vgpr_spill_count: 0
    .wavefront_size: 64
  - .agpr_count:     0
    .args:
      - .offset:         0
        .size:           112
        .value_kind:     by_value
      - .actual_access:  read_only
        .address_space:  global
        .offset:         112
        .size:           8
        .value_kind:     global_buffer
      - .actual_access:  read_only
        .address_space:  global
        .offset:         120
        .size:           8
        .value_kind:     global_buffer
      - .actual_access:  write_only
        .address_space:  global
        .offset:         128
        .size:           8
        .value_kind:     global_buffer
      - .offset:         136
        .size:           4
        .value_kind:     by_value
      - .offset:         140
        .size:           4
        .value_kind:     by_value
      - .offset:         144
        .size:           4
        .value_kind:     by_value
    .group_segment_fixed_size: 82944
    .kernarg_segment_align: 8
    .kernarg_segment_size: 148
    .language:       OpenCL C
    .language_version:
      - 2
      - 0
    .max_flat_workgroup_size: 512
    .name:           _Z7k_stageILi0ELi4EEv8AttnArgsPKDF16_PKfPDF16_iii
    .private_segment_fixed_size: 0
    .sgpr_count:     38
    .sgpr_spill_count: 0
    .symbol:         _Z7k_stageILi0ELi4EEv8AttnArgsPKDF16_PKfPDF16_iii.kd
    .uniform_work_group_size: 1
    .uses_dynamic_stack: false
    .vgpr_count:     230
    .vgpr_spill_count: 0
    .wavefront_size: 64
  - .agpr_count:     0
    .args:
      - .offset:         0
        .size:           112
        .value_kind:     by_value
    .group_segment_fixed_size: 0
    .kernarg_segment_align: 8
    .kernarg_segment_size: 112
    .language:       OpenCL C
    .language_version:
      - 2
      - 0
    .max_flat_workgroup_size: 512
    .name:           _Z7k_attn2ILi2EEv8AttnArgs
    .private_segment_fixed_size: 0
    .sgpr_count:     86
    .sgpr_spill_count: 0
    .symbol:         _Z7k_attn2ILi2EEv8AttnArgs.kd
    .uniform_work_group_size: 1
    .uses_dynamic_stack: false
    .vgpr_count:     236
    .vgpr_spill_count: 0
    .wavefront_size: 64
